# stack: v31 + counted LDS waits per PV MFMA + rcp-based division in SGU/up-proj/GLA-out/router + up-proj epilogue rope-load waits moved to first consumer
# baseline (speedup 1.0000x reference)
.LBB0_400:
	s_lshl_b32 s48, s8, 8
	s_cmp_lg_u32 s58, 0
	v_mbcnt_lo_u32_b32 v112, -1, 0
	v_mbcnt_hi_u32_b32 v112, -1, v112
	s_cselect_b64 s[62:63], -1, 0
	v_and_b32_e32 v237, 15, v112
	s_cmp_eq_u32 s58, 0
	v_or_b32_e32 v231, s85, v237
	s_cselect_b32 s6, 0, 32
	v_add_u32_e32 v232, s48, v231
	s_add_u32 s16, s77, s6
	v_ashrrev_i32_e32 v233, 31, v232
	s_addc_u32 s17, s78, 0
	v_lshlrev_b64 v[114:115], 6, v[232:233]
	v_lshl_add_u64 v[118:119], s[16:17], 0, v[114:115]
	global_load_dwordx4 v[114:117], v[118:119], off
	global_load_dwordx4 v[128:131], v[118:119], off offset:16
	v_mul_f32_e32 v118, v157, v157
	v_mul_f32_e32 v119, v159, v159
	v_mul_f32_e32 v132, v153, v153
	v_mul_f32_e32 v133, v155, v155
	v_fmac_f32_e32 v118, v156, v156
	v_fmac_f32_e32 v119, v158, v158
	v_fmac_f32_e32 v132, v152, v152
	v_fmac_f32_e32 v133, v154, v154
	v_add_f32_e32 v118, v118, v119
	v_ashrrev_i32_e32 v135, 2, v112
	v_cndmask_b32_e64 v134, 0, 1, s[44:45]
	v_and_b32_e32 v208, -4, v135
	s_mov_b64 s[10:11], -1
	v_cmp_ne_u32_e64 s[6:7], 1, v134
	v_ashrrev_i32_e32 v209, 31, v208
	s_waitcnt vmcnt(1)
	v_add_f32_e32 v114, v114, v115
	v_add_f32_e32 v115, v116, v117
	s_waitcnt vmcnt(0)
	v_add_f32_e32 v116, v128, v129
	v_add_f32_e32 v117, v130, v131
	v_add_f32_e32 v114, v114, v115
	v_add_f32_e32 v115, v116, v117
	v_add_f32_e32 v114, v114, v115
	v_fmamk_f32 v114, v114, 0x3b000000, v213
	v_mul_f32_e32 v115, 0x4f800000, v114
	v_cmp_gt_f32_e32 vcc, s90, v114
	s_nop 1
	v_cndmask_b32_e32 v115, v114, v115, vcc
	v_sqrt_f32_e32 v116, v115
	v_add_f32_e32 v114, v132, v133
	v_add_f32_e32 v114, v118, v114
	v_add_u32_e32 v117, -1, v116
	v_add_u32_e32 v118, 1, v116
	v_fma_f32 v119, -v117, v116, v115
	v_fma_f32 v128, -v118, v116, v115
	v_cmp_ge_f32_e64 s[8:9], 0, v119
	s_nop 1
	v_cndmask_b32_e64 v116, v116, v117, s[8:9]
	v_cmp_lt_f32_e64 s[8:9], 0, v128
	s_nop 1
	v_cndmask_b32_e64 v116, v116, v118, s[8:9]
	v_mul_f32_e32 v117, 0x37800000, v116
	v_cndmask_b32_e32 v116, v116, v117, vcc
	v_cmp_class_f32_e32 vcc, v115, v215
	s_nop 1
	v_cndmask_b32_e32 v115, v116, v115, vcc
	v_rcp_f32_e32 v117, v115
	s_and_b64 s[8:9], exec, s[62:63]
	v_mul_f32_e32 v116, 1.0, v117
	v_mov_b32_e32 v236, v116
	v_mul_f32_e32 v115, v236, v236
	s_mov_b64 vcc, s[8:9]
	s_cbranch_vccz .LBB0_404
	s_and_b64 vcc, exec, s[6:7]
	v_mul_f32_e32 v113, v114, v115
	s_cbranch_vccnz .LBB0_403
	v_mov_b64_e32 v[116:117], s[50:51]
	v_mad_i64_i32 v[116:117], s[8:9], v232, s65, v[116:117]
	v_lshl_add_u64 v[116:117], v[208:209], 1, v[116:117]
	global_load_dwordx2 v[118:119], v[116:117], off offset:2080
	s_nop 0
	global_load_dwordx2 v[116:117], v[116:117], off offset:2048
	s_waitcnt vmcnt(1)
	v_lshlrev_b32_e32 v129, 16, v118
	v_and_b32_e32 v131, 0xffff0000, v118
	s_waitcnt vmcnt(0)
	v_and_b32_e32 v130, 0xffff0000, v116
	v_lshlrev_b32_e32 v133, 16, v119
	v_and_b32_e32 v119, 0xffff0000, v119
	v_and_b32_e32 v118, 0xffff0000, v117
	v_lshlrev_b32_e32 v128, 16, v116
	v_lshlrev_b32_e32 v132, 16, v117
	v_pk_mul_f32 v[116:117], v[130:131], v[130:131]
	v_pk_mul_f32 v[118:119], v[118:119], v[118:119]
	v_pk_fma_f32 v[116:117], v[128:129], v[128:129], v[116:117]
	v_pk_fma_f32 v[118:119], v[132:133], v[132:133], v[118:119]
	s_nop 0
	v_pk_add_f32 v[116:117], v[116:117], v[118:119]
	s_nop 0
	v_add_f32_e32 v113, v113, v116
	v_add_f32_e32 v113, v113, v117

.LBB0_410:
	s_or_b64 exec, exec, s[8:9]
	v_or_b32_e32 v238, 16, v232
	v_ashrrev_i32_e32 v239, 31, v238
	v_lshlrev_b64 v[112:113], 6, v[238:239]
	v_lshl_add_u64 v[112:113], s[16:17], 0, v[112:113]
	global_load_dwordx4 v[128:131], v[112:113], off
	global_load_dwordx4 v[132:135], v[112:113], off offset:16
	v_mul_f32_e32 v112, v109, v109
	v_mul_f32_e32 v113, v111, v111
	s_waitcnt lgkmcnt(0)
	v_mul_f32_e32 v117, v105, v105
	v_mul_f32_e32 v118, v107, v107
	v_fmac_f32_e32 v112, v108, v108
	v_fmac_f32_e32 v113, v110, v110
	v_fmac_f32_e32 v117, v104, v104
	v_fmac_f32_e32 v118, v106, v106
	v_cndmask_b32_e64 v119, 0, 1, s[62:63]
	v_add_f32_e32 v112, v112, v113
	v_add_f32_e32 v113, v117, v118
	v_cmp_ne_u32_e64 s[8:9], 1, v119
	v_add_f32_e32 v112, v112, v113
	s_mov_b64 s[26:27], -1
	s_waitcnt vmcnt(1)
	v_add_f32_e32 v128, v128, v129
	v_add_f32_e32 v129, v130, v131
	s_waitcnt vmcnt(0)
	v_add_f32_e32 v130, v132, v133
	v_add_f32_e32 v131, v134, v135
	v_add_f32_e32 v128, v128, v129
	v_add_f32_e32 v129, v130, v131
	v_add_f32_e32 v128, v128, v129
	v_fmamk_f32 v128, v128, 0x3b000000, v213
	v_mul_f32_e32 v129, 0x4f800000, v128
	v_cmp_gt_f32_e32 vcc, s90, v128
	s_nop 1
	v_cndmask_b32_e32 v128, v128, v129, vcc
	v_sqrt_f32_e32 v129, v128
	s_nop 0
	v_add_u32_e32 v117, -1, v129
	v_add_u32_e32 v118, 1, v129
	v_fma_f32 v119, -v117, v129, v128
	v_fma_f32 v130, -v118, v129, v128
	v_cmp_ge_f32_e64 s[14:15], 0, v119
	s_nop 1
	v_cndmask_b32_e64 v117, v129, v117, s[14:15]
	v_cmp_lt_f32_e64 s[14:15], 0, v130
	s_nop 1
	v_cndmask_b32_e64 v117, v117, v118, s[14:15]
	v_mul_f32_e32 v118, 0x37800000, v117
	v_cndmask_b32_e32 v117, v117, v118, vcc
	v_cmp_class_f32_e32 vcc, v128, v215
	s_nop 1
	v_cndmask_b32_e32 v117, v117, v128, vcc
	v_rcp_f32_e32 v119, v117
	s_nop 0
	v_mul_f32_e32 v113, 1.0, v119
	v_mov_b32_e32 v132, v113
	s_andn2_b64 vcc, exec, s[62:63]
	v_mul_f32_e32 v113, v132, v132
	s_cbranch_vccnz .LBB0_414
	s_and_b64 vcc, exec, s[6:7]
	v_mul_f32_e32 v117, v112, v113
	s_cbranch_vccnz .LBB0_413
	v_mov_b64_e32 v[118:119], s[50:51]
	v_mad_i64_i32 v[118:119], s[14:15], v238, s65, v[118:119]
	v_lshl_add_u64 v[118:119], v[208:209], 1, v[118:119]
	global_load_dwordx2 v[128:129], v[118:119], off offset:2080
	s_nop 0
	global_load_dwordx2 v[118:119], v[118:119], off offset:2048
	s_waitcnt vmcnt(1)
	v_lshlrev_b32_e32 v131, 16, v128
	v_and_b32_e32 v135, 0xffff0000, v128
	s_waitcnt vmcnt(0)
	v_and_b32_e32 v134, 0xffff0000, v118
	v_lshlrev_b32_e32 v137, 16, v129
	v_and_b32_e32 v129, 0xffff0000, v129
	v_and_b32_e32 v128, 0xffff0000, v119
	v_lshlrev_b32_e32 v130, 16, v118
	v_lshlrev_b32_e32 v136, 16, v119
	v_pk_mul_f32 v[118:119], v[134:135], v[134:135]
	v_pk_mul_f32 v[128:129], v[128:129], v[128:129]
	v_pk_fma_f32 v[118:119], v[130:131], v[130:131], v[118:119]
	v_pk_fma_f32 v[128:129], v[136:137], v[136:137], v[128:129]
	s_nop 0
	v_pk_add_f32 v[118:119], v[118:119], v[128:129]
	s_nop 0
	v_add_f32_e32 v117, v117, v118
	v_add_f32_e32 v117, v117, v119

.LBB0_420:
	s_or_b64 exec, exec, s[14:15]
	v_or_b32_e32 v228, 32, v232
	v_ashrrev_i32_e32 v229, 31, v228
	s_waitcnt lgkmcnt(0)
	v_lshlrev_b64 v[112:113], 6, v[228:229]
	v_lshl_add_u64 v[112:113], s[16:17], 0, v[112:113]
	global_load_dwordx4 v[128:131], v[112:113], off
	global_load_dwordx4 v[134:137], v[112:113], off offset:16
	v_mul_f32_e32 v112, v93, v93
	v_mul_f32_e32 v113, v95, v95
	v_mul_f32_e32 v117, v89, v89
	v_mul_f32_e32 v118, v91, v91
	v_fmac_f32_e32 v112, v92, v92
	v_fmac_f32_e32 v113, v94, v94
	v_fmac_f32_e32 v117, v88, v88
	v_fmac_f32_e32 v118, v90, v90
	v_add_f32_e32 v112, v112, v113
	v_add_f32_e32 v113, v117, v118
	v_add_f32_e32 v112, v112, v113
	s_mov_b64 s[26:27], -1
	s_waitcnt vmcnt(1)
	v_add_f32_e32 v119, v128, v129
	v_add_f32_e32 v128, v130, v131
	s_waitcnt vmcnt(0)
	v_add_f32_e32 v129, v134, v135
	v_add_f32_e32 v130, v136, v137
	v_add_f32_e32 v119, v119, v128
	v_add_f32_e32 v128, v129, v130
	v_add_f32_e32 v119, v119, v128
	v_fmamk_f32 v119, v119, 0x3b000000, v213
	v_mul_f32_e32 v128, 0x4f800000, v119
	v_cmp_gt_f32_e32 vcc, s90, v119
	s_nop 1
	v_cndmask_b32_e32 v119, v119, v128, vcc
	v_sqrt_f32_e32 v128, v119
	s_nop 0
	v_add_u32_e32 v117, -1, v128
	v_add_u32_e32 v118, 1, v128
	v_fma_f32 v129, -v117, v128, v119
	v_fma_f32 v130, -v118, v128, v119
	v_cmp_ge_f32_e64 s[14:15], 0, v129
	s_nop 1
	v_cndmask_b32_e64 v117, v128, v117, s[14:15]
	v_cmp_lt_f32_e64 s[14:15], 0, v130
	s_nop 1
	v_cndmask_b32_e64 v117, v117, v118, s[14:15]
	v_mul_f32_e32 v118, 0x37800000, v117
	v_cndmask_b32_e32 v117, v117, v118, vcc
	v_cmp_class_f32_e32 vcc, v119, v215
	s_nop 1
	v_cndmask_b32_e32 v117, v117, v119, vcc
	v_rcp_f32_e32 v119, v117
	s_nop 0
	v_mul_f32_e32 v113, 1.0, v119
	v_mov_b32_e32 v230, v113
	s_and_b64 vcc, exec, s[8:9]
	v_mul_f32_e32 v113, v230, v230
	s_cbranch_vccnz .LBB0_424
	s_and_b64 vcc, exec, s[6:7]
	v_mul_f32_e32 v117, v112, v113
	s_cbranch_vccnz .LBB0_423
	v_mov_b64_e32 v[118:119], s[50:51]
	v_mad_i64_i32 v[118:119], s[14:15], v228, s65, v[118:119]
	v_lshl_add_u64 v[118:119], v[208:209], 1, v[118:119]
	global_load_dwordx2 v[128:129], v[118:119], off offset:2080
	s_nop 0
	global_load_dwordx2 v[118:119], v[118:119], off offset:2048
	s_waitcnt vmcnt(1)
	v_lshlrev_b32_e32 v131, 16, v128
	v_and_b32_e32 v135, 0xffff0000, v128
	s_waitcnt vmcnt(0)
	v_and_b32_e32 v134, 0xffff0000, v118
	v_lshlrev_b32_e32 v137, 16, v129
	v_and_b32_e32 v129, 0xffff0000, v129
	v_and_b32_e32 v128, 0xffff0000, v119
	v_lshlrev_b32_e32 v130, 16, v118
	v_lshlrev_b32_e32 v136, 16, v119
	v_pk_mul_f32 v[118:119], v[134:135], v[134:135]
	v_pk_mul_f32 v[128:129], v[128:129], v[128:129]
	v_pk_fma_f32 v[118:119], v[130:131], v[130:131], v[118:119]
	v_pk_fma_f32 v[128:129], v[136:137], v[136:137], v[128:129]
	s_nop 0
	v_pk_add_f32 v[118:119], v[118:119], v[128:129]
	s_nop 0
	v_add_f32_e32 v117, v117, v118
	v_add_f32_e32 v117, v117, v119

.LBB0_430:
	s_or_b64 exec, exec, s[14:15]
	v_or_b32_e32 v234, 48, v232
	v_ashrrev_i32_e32 v235, 31, v234
	s_waitcnt lgkmcnt(0)
	v_lshlrev_b64 v[112:113], 6, v[234:235]
	v_lshl_add_u64 v[112:113], s[16:17], 0, v[112:113]
	global_load_dwordx4 v[128:131], v[112:113], off
	global_load_dwordx4 v[134:137], v[112:113], off offset:16
	v_mul_f32_e32 v112, v77, v77
	v_mul_f32_e32 v113, v79, v79
	v_mul_f32_e32 v117, v73, v73
	v_mul_f32_e32 v118, v75, v75
	v_fmac_f32_e32 v112, v76, v76
	v_fmac_f32_e32 v113, v78, v78
	v_fmac_f32_e32 v117, v72, v72
	v_fmac_f32_e32 v118, v74, v74
	v_add_f32_e32 v112, v112, v113
	v_add_f32_e32 v113, v117, v118
	v_add_f32_e32 v112, v112, v113
	s_mov_b64 s[26:27], -1
	s_waitcnt vmcnt(1)
	v_add_f32_e32 v119, v128, v129
	v_add_f32_e32 v128, v130, v131
	s_waitcnt vmcnt(0)
	v_add_f32_e32 v129, v134, v135
	v_add_f32_e32 v130, v136, v137
	v_add_f32_e32 v119, v119, v128
	v_add_f32_e32 v128, v129, v130
	v_add_f32_e32 v119, v119, v128
	v_fmamk_f32 v119, v119, 0x3b000000, v213
	v_mul_f32_e32 v128, 0x4f800000, v119
	v_cmp_gt_f32_e32 vcc, s90, v119
	s_nop 1
	v_cndmask_b32_e32 v119, v119, v128, vcc
	v_sqrt_f32_e32 v128, v119
	s_nop 0
	v_add_u32_e32 v117, -1, v128
	v_add_u32_e32 v118, 1, v128
	v_fma_f32 v129, -v117, v128, v119
	v_fma_f32 v130, -v118, v128, v119
	v_cmp_ge_f32_e64 s[14:15], 0, v129
	s_nop 1
	v_cndmask_b32_e64 v117, v128, v117, s[14:15]
	v_cmp_lt_f32_e64 s[14:15], 0, v130
	s_nop 1
	v_cndmask_b32_e64 v117, v117, v118, s[14:15]
	v_mul_f32_e32 v118, 0x37800000, v117
	v_cndmask_b32_e32 v117, v117, v118, vcc
	v_cmp_class_f32_e32 vcc, v119, v215
	s_nop 1
	v_cndmask_b32_e32 v117, v117, v119, vcc
	v_rcp_f32_e32 v119, v117
	s_nop 0
	v_mul_f32_e32 v113, 1.0, v119
	v_mov_b32_e32 v226, v113
	s_and_b64 vcc, exec, s[8:9]
	v_mul_f32_e32 v113, v226, v226
	s_cbranch_vccnz .LBB0_434
	s_and_b64 vcc, exec, s[6:7]
	v_mul_f32_e32 v117, v112, v113
	s_cbranch_vccnz .LBB0_433
	v_mov_b64_e32 v[118:119], s[50:51]
	v_mad_i64_i32 v[118:119], s[14:15], v234, s65, v[118:119]
	v_lshl_add_u64 v[118:119], v[208:209], 1, v[118:119]
	global_load_dwordx2 v[128:129], v[118:119], off offset:2080
	s_nop 0
	global_load_dwordx2 v[118:119], v[118:119], off offset:2048
	s_waitcnt vmcnt(1)
	v_lshlrev_b32_e32 v131, 16, v128
	v_and_b32_e32 v135, 0xffff0000, v128
	s_waitcnt vmcnt(0)
	v_and_b32_e32 v134, 0xffff0000, v118
	v_lshlrev_b32_e32 v137, 16, v129
	v_and_b32_e32 v129, 0xffff0000, v129
	v_and_b32_e32 v128, 0xffff0000, v119
	v_lshlrev_b32_e32 v130, 16, v118
	v_lshlrev_b32_e32 v136, 16, v119
	v_pk_mul_f32 v[118:119], v[134:135], v[134:135]
	v_pk_mul_f32 v[128:129], v[128:129], v[128:129]
	v_pk_fma_f32 v[118:119], v[130:131], v[130:131], v[118:119]
	v_pk_fma_f32 v[128:129], v[136:137], v[136:137], v[128:129]
	s_nop 0
	v_pk_add_f32 v[118:119], v[118:119], v[128:129]
	s_nop 0
	v_add_f32_e32 v117, v117, v118
	v_add_f32_e32 v117, v117, v119

.LBB0_440:
	s_or_b64 exec, exec, s[14:15]
	v_add_u32_e32 v112, 0x80, v232
	s_waitcnt lgkmcnt(0)
	v_ashrrev_i32_e32 v113, 31, v112
	v_lshlrev_b64 v[118:119], 6, v[112:113]
	v_lshl_add_u64 v[118:119], s[16:17], 0, v[118:119]
	global_load_dwordx4 v[128:131], v[118:119], off
	global_load_dwordx4 v[134:137], v[118:119], off offset:16
	v_mul_f32_e32 v113, v61, v61
	v_mul_f32_e32 v117, v63, v63
	v_mul_f32_e32 v118, v57, v57
	v_mul_f32_e32 v119, v59, v59
	v_fmac_f32_e32 v113, v60, v60
	v_fmac_f32_e32 v117, v62, v62
	v_fmac_f32_e32 v118, v56, v56
	v_fmac_f32_e32 v119, v58, v58
	v_add_f32_e32 v113, v113, v117
	v_add_f32_e32 v117, v118, v119
	v_add_f32_e32 v113, v113, v117
	s_mov_b64 s[26:27], -1
	s_waitcnt vmcnt(1)
	v_add_f32_e32 v128, v128, v129
	v_add_f32_e32 v129, v130, v131
	s_waitcnt vmcnt(0)
	v_add_f32_e32 v130, v134, v135
	v_add_f32_e32 v131, v136, v137
	v_add_f32_e32 v128, v128, v129
	v_add_f32_e32 v129, v130, v131
	v_add_f32_e32 v128, v128, v129
	v_fmamk_f32 v128, v128, 0x3b000000, v213
	v_mul_f32_e32 v129, 0x4f800000, v128
	v_cmp_gt_f32_e32 vcc, s90, v128
	s_nop 1
	v_cndmask_b32_e32 v128, v128, v129, vcc
	v_sqrt_f32_e32 v129, v128
	s_nop 0
	v_add_u32_e32 v118, -1, v129
	v_add_u32_e32 v119, 1, v129
	v_fma_f32 v130, -v118, v129, v128
	v_fma_f32 v131, -v119, v129, v128
	v_cmp_ge_f32_e64 s[14:15], 0, v130
	s_nop 1
	v_cndmask_b32_e64 v118, v129, v118, s[14:15]
	v_cmp_lt_f32_e64 s[14:15], 0, v131
	s_nop 1
	v_cndmask_b32_e64 v118, v118, v119, s[14:15]
	v_mul_f32_e32 v119, 0x37800000, v118
	v_cndmask_b32_e32 v118, v118, v119, vcc
	v_cmp_class_f32_e32 vcc, v128, v215
	s_nop 1
	v_cndmask_b32_e32 v118, v118, v128, vcc
	v_rcp_f32_e32 v128, v118
	s_nop 0
	v_mul_f32_e32 v117, 1.0, v128
	v_mov_b32_e32 v220, v117
	s_and_b64 vcc, exec, s[8:9]
	v_mul_f32_e32 v117, v220, v220
	s_cbranch_vccnz .LBB0_444
	s_and_b64 vcc, exec, s[6:7]
	v_mul_f32_e32 v118, v113, v117
	s_cbranch_vccnz .LBB0_443
	v_mov_b64_e32 v[128:129], s[50:51]
	v_mad_i64_i32 v[128:129], s[14:15], v112, s65, v[128:129]
	v_lshl_add_u64 v[128:129], v[208:209], 1, v[128:129]
	global_load_dwordx2 v[130:131], v[128:129], off offset:2080
	s_nop 0
	global_load_dwordx2 v[128:129], v[128:129], off offset:2048
	s_waitcnt vmcnt(1)
	v_lshlrev_b32_e32 v135, 16, v130
	v_and_b32_e32 v137, 0xffff0000, v130
	s_waitcnt vmcnt(0)
	v_and_b32_e32 v136, 0xffff0000, v128
	v_lshlrev_b32_e32 v139, 16, v131
	v_and_b32_e32 v131, 0xffff0000, v131
	v_and_b32_e32 v130, 0xffff0000, v129
	v_lshlrev_b32_e32 v134, 16, v128
	v_lshlrev_b32_e32 v138, 16, v129
	v_pk_mul_f32 v[128:129], v[136:137], v[136:137]
	v_pk_mul_f32 v[130:131], v[130:131], v[130:131]
	v_pk_fma_f32 v[128:129], v[134:135], v[134:135], v[128:129]
	v_pk_fma_f32 v[130:131], v[138:139], v[138:139], v[130:131]
	s_nop 0
	v_pk_add_f32 v[128:129], v[128:129], v[130:131]
	s_nop 0
	v_add_f32_e32 v112, v118, v128
	v_add_f32_e32 v118, v112, v129

.LBB0_450:
	s_or_b64 exec, exec, s[14:15]
	v_add_u32_e32 v112, 0x90, v232
	s_waitcnt lgkmcnt(0)
	v_ashrrev_i32_e32 v113, 31, v112
	v_lshlrev_b64 v[118:119], 6, v[112:113]
	v_lshl_add_u64 v[118:119], s[16:17], 0, v[118:119]
	global_load_dwordx4 v[128:131], v[118:119], off
	global_load_dwordx4 v[134:137], v[118:119], off offset:16
	v_mul_f32_e32 v113, v45, v45
	v_mul_f32_e32 v117, v47, v47
	v_mul_f32_e32 v118, v41, v41
	v_mul_f32_e32 v119, v43, v43
	v_fmac_f32_e32 v113, v44, v44
	v_fmac_f32_e32 v117, v46, v46
	v_fmac_f32_e32 v118, v40, v40
	v_fmac_f32_e32 v119, v42, v42
	v_add_f32_e32 v113, v113, v117
	v_add_f32_e32 v117, v118, v119
	v_add_f32_e32 v113, v113, v117
	s_mov_b64 s[26:27], -1
	s_waitcnt vmcnt(1)
	v_add_f32_e32 v128, v128, v129
	v_add_f32_e32 v129, v130, v131
	s_waitcnt vmcnt(0)
	v_add_f32_e32 v130, v134, v135
	v_add_f32_e32 v131, v136, v137
	v_add_f32_e32 v128, v128, v129
	v_add_f32_e32 v129, v130, v131
	v_add_f32_e32 v128, v128, v129
	v_fmamk_f32 v128, v128, 0x3b000000, v213
	v_mul_f32_e32 v129, 0x4f800000, v128
	v_cmp_gt_f32_e32 vcc, s90, v128
	s_nop 1
	v_cndmask_b32_e32 v128, v128, v129, vcc
	v_sqrt_f32_e32 v129, v128
	s_nop 0
	v_add_u32_e32 v118, -1, v129
	v_add_u32_e32 v119, 1, v129
	v_fma_f32 v130, -v118, v129, v128
	v_fma_f32 v131, -v119, v129, v128
	v_cmp_ge_f32_e64 s[14:15], 0, v130
	s_nop 1
	v_cndmask_b32_e64 v118, v129, v118, s[14:15]
	v_cmp_lt_f32_e64 s[14:15], 0, v131
	s_nop 1
	v_cndmask_b32_e64 v118, v118, v119, s[14:15]
	v_mul_f32_e32 v119, 0x37800000, v118
	v_cndmask_b32_e32 v118, v118, v119, vcc
	v_cmp_class_f32_e32 vcc, v128, v215
	s_nop 1
	v_cndmask_b32_e32 v118, v118, v128, vcc
	v_rcp_f32_e32 v128, v118
	s_nop 0
	v_mul_f32_e32 v117, 1.0, v128
	v_mov_b32_e32 v214, v117
	s_and_b64 vcc, exec, s[8:9]
	v_mul_f32_e32 v117, v214, v214
	s_cbranch_vccnz .LBB0_454
	s_and_b64 vcc, exec, s[6:7]
	v_mul_f32_e32 v118, v113, v117
	s_cbranch_vccnz .LBB0_453
	v_mov_b64_e32 v[128:129], s[50:51]
	v_mad_i64_i32 v[128:129], s[14:15], v112, s65, v[128:129]
	v_lshl_add_u64 v[128:129], v[208:209], 1, v[128:129]
	global_load_dwordx2 v[130:131], v[128:129], off offset:2080
	s_nop 0
	global_load_dwordx2 v[128:129], v[128:129], off offset:2048
	s_waitcnt vmcnt(1)
	v_lshlrev_b32_e32 v135, 16, v130
	v_and_b32_e32 v137, 0xffff0000, v130
	s_waitcnt vmcnt(0)
	v_and_b32_e32 v136, 0xffff0000, v128
	v_lshlrev_b32_e32 v139, 16, v131
	v_and_b32_e32 v131, 0xffff0000, v131
	v_and_b32_e32 v130, 0xffff0000, v129
	v_lshlrev_b32_e32 v134, 16, v128
	v_lshlrev_b32_e32 v138, 16, v129
	v_pk_mul_f32 v[128:129], v[136:137], v[136:137]
	v_pk_mul_f32 v[130:131], v[130:131], v[130:131]
	v_pk_fma_f32 v[128:129], v[134:135], v[134:135], v[128:129]
	v_pk_fma_f32 v[130:131], v[138:139], v[138:139], v[130:131]
	s_nop 0
	v_pk_add_f32 v[128:129], v[128:129], v[130:131]
	s_nop 0
	v_add_f32_e32 v112, v118, v128
	v_add_f32_e32 v118, v112, v129

.LBB0_460:
	s_or_b64 exec, exec, s[14:15]
	v_add_u32_e32 v112, 0xa0, v232
	s_waitcnt lgkmcnt(0)
	v_ashrrev_i32_e32 v113, 31, v112
	v_lshlrev_b64 v[118:119], 6, v[112:113]
	v_lshl_add_u64 v[118:119], s[16:17], 0, v[118:119]
	global_load_dwordx4 v[128:131], v[118:119], off
	global_load_dwordx4 v[134:137], v[118:119], off offset:16
	v_mul_f32_e32 v113, v29, v29
	v_mul_f32_e32 v117, v31, v31
	v_mul_f32_e32 v118, v25, v25
	v_mul_f32_e32 v119, v27, v27
	v_fmac_f32_e32 v113, v28, v28
	v_fmac_f32_e32 v117, v30, v30
	v_fmac_f32_e32 v118, v24, v24
	v_fmac_f32_e32 v119, v26, v26
	v_add_f32_e32 v113, v113, v117
	v_add_f32_e32 v117, v118, v119
	v_add_f32_e32 v113, v113, v117
	s_mov_b64 s[26:27], -1
	s_waitcnt vmcnt(1)
	v_add_f32_e32 v128, v128, v129
	v_add_f32_e32 v129, v130, v131
	s_waitcnt vmcnt(0)
	v_add_f32_e32 v130, v134, v135
	v_add_f32_e32 v131, v136, v137
	v_add_f32_e32 v128, v128, v129
	v_add_f32_e32 v129, v130, v131
	v_add_f32_e32 v128, v128, v129
	v_fmamk_f32 v128, v128, 0x3b000000, v213
	v_mul_f32_e32 v129, 0x4f800000, v128
	v_cmp_gt_f32_e32 vcc, s90, v128
	s_nop 1
	v_cndmask_b32_e32 v128, v128, v129, vcc
	v_sqrt_f32_e32 v129, v128
	s_nop 0
	v_add_u32_e32 v118, -1, v129
	v_add_u32_e32 v119, 1, v129
	v_fma_f32 v130, -v118, v129, v128
	v_fma_f32 v131, -v119, v129, v128
	v_cmp_ge_f32_e64 s[14:15], 0, v130
	s_nop 1
	v_cndmask_b32_e64 v118, v129, v118, s[14:15]
	v_cmp_lt_f32_e64 s[14:15], 0, v131
	s_nop 1
	v_cndmask_b32_e64 v118, v118, v119, s[14:15]
	v_mul_f32_e32 v119, 0x37800000, v118
	v_cndmask_b32_e32 v118, v118, v119, vcc
	v_cmp_class_f32_e32 vcc, v128, v215
	s_nop 1
	v_cndmask_b32_e32 v118, v118, v128, vcc
	v_rcp_f32_e32 v128, v118
	s_nop 0
	v_mul_f32_e32 v117, 1.0, v128
	v_mov_b32_e32 v212, v117
	s_and_b64 vcc, exec, s[8:9]
	v_mul_f32_e32 v117, v212, v212
	s_cbranch_vccnz .LBB0_464
	s_and_b64 vcc, exec, s[6:7]
	v_mul_f32_e32 v118, v113, v117
	s_cbranch_vccnz .LBB0_463
	v_mov_b64_e32 v[128:129], s[50:51]
	v_mad_i64_i32 v[128:129], s[14:15], v112, s65, v[128:129]
	v_lshl_add_u64 v[128:129], v[208:209], 1, v[128:129]
	global_load_dwordx2 v[130:131], v[128:129], off offset:2080
	s_nop 0
	global_load_dwordx2 v[128:129], v[128:129], off offset:2048
	s_waitcnt vmcnt(1)
	v_lshlrev_b32_e32 v135, 16, v130
	v_and_b32_e32 v137, 0xffff0000, v130
	s_waitcnt vmcnt(0)
	v_and_b32_e32 v136, 0xffff0000, v128
	v_lshlrev_b32_e32 v139, 16, v131
	v_and_b32_e32 v131, 0xffff0000, v131
	v_and_b32_e32 v130, 0xffff0000, v129
	v_lshlrev_b32_e32 v134, 16, v128
	v_lshlrev_b32_e32 v138, 16, v129
	v_pk_mul_f32 v[128:129], v[136:137], v[136:137]
	v_pk_mul_f32 v[130:131], v[130:131], v[130:131]
	v_pk_fma_f32 v[128:129], v[134:135], v[134:135], v[128:129]
	v_pk_fma_f32 v[130:131], v[138:139], v[138:139], v[130:131]
	s_nop 0
	v_pk_add_f32 v[128:129], v[128:129], v[130:131]
	s_nop 0
	v_add_f32_e32 v112, v118, v128
	v_add_f32_e32 v118, v112, v129

.LBB0_470:
	s_or_b64 exec, exec, s[14:15]
	v_add_u32_e32 v112, 0xb0, v232
	s_waitcnt lgkmcnt(0)
	v_ashrrev_i32_e32 v113, 31, v112
	v_lshlrev_b64 v[116:117], 6, v[112:113]
	v_lshl_add_u64 v[128:129], s[16:17], 0, v[116:117]
	global_load_dwordx4 v[116:119], v[128:129], off
	s_nop 0
	global_load_dwordx4 v[128:131], v[128:129], off offset:16
	v_mul_f32_e32 v113, v13, v13
	v_mul_f32_e32 v133, v15, v15
	v_mul_f32_e32 v134, v9, v9
	v_mul_f32_e32 v135, v11, v11
	v_fmac_f32_e32 v113, v12, v12
	v_fmac_f32_e32 v133, v14, v14
	v_fmac_f32_e32 v134, v8, v8
	v_fmac_f32_e32 v135, v10, v10
	v_add_f32_e32 v113, v113, v133
	s_mov_b64 s[14:15], -1
	s_waitcnt vmcnt(1)
	v_add_f32_e32 v116, v116, v117
	v_add_f32_e32 v117, v118, v119
	s_waitcnt vmcnt(0)
	v_add_f32_e32 v118, v128, v129
	v_add_f32_e32 v119, v130, v131
	v_add_f32_e32 v116, v116, v117
	v_add_f32_e32 v117, v118, v119
	v_add_f32_e32 v116, v116, v117
	v_fmamk_f32 v116, v116, 0x3b000000, v213
	v_mul_f32_e32 v117, 0x4f800000, v116
	v_cmp_gt_f32_e32 vcc, s90, v116
	v_add_f32_e32 v118, v134, v135
	v_add_f32_e32 v113, v113, v118
	v_cndmask_b32_e32 v116, v116, v117, vcc
	v_sqrt_f32_e32 v117, v116
	s_nop 0
	v_add_u32_e32 v119, -1, v117
	v_add_u32_e32 v128, 1, v117
	v_fma_f32 v129, -v119, v117, v116
	v_fma_f32 v130, -v128, v117, v116
	v_cmp_ge_f32_e64 s[12:13], 0, v129
	s_nop 1
	v_cndmask_b32_e64 v117, v117, v119, s[12:13]
	v_cmp_lt_f32_e64 s[12:13], 0, v130
	s_nop 1
	v_cndmask_b32_e64 v117, v117, v128, s[12:13]
	v_mul_f32_e32 v119, 0x37800000, v117
	v_cndmask_b32_e32 v117, v117, v119, vcc
	v_cmp_class_f32_e32 vcc, v116, v215
	s_nop 1
	v_cndmask_b32_e32 v116, v117, v116, vcc
	v_rcp_f32_e32 v119, v116
	s_nop 0
	v_mul_f32_e32 v117, 1.0, v119
	v_mov_b32_e32 v210, v117
	s_and_b64 vcc, exec, s[8:9]
	v_mul_f32_e32 v116, v210, v210
	s_cbranch_vccnz .LBB0_474
	s_and_b64 vcc, exec, s[6:7]
	v_mul_f32_e32 v117, v113, v116
	s_cbranch_vccnz .LBB0_473
	v_mov_b64_e32 v[118:119], s[50:51]
	v_mad_i64_i32 v[118:119], s[12:13], v112, s65, v[118:119]
	v_lshl_add_u64 v[118:119], v[208:209], 1, v[118:119]
	global_load_dwordx2 v[128:129], v[118:119], off offset:2080
	s_nop 0
	global_load_dwordx2 v[118:119], v[118:119], off offset:2048
	s_waitcnt vmcnt(1)
	v_lshlrev_b32_e32 v131, 16, v128
	v_and_b32_e32 v135, 0xffff0000, v128
	s_waitcnt vmcnt(0)
	v_and_b32_e32 v134, 0xffff0000, v118
	v_lshlrev_b32_e32 v137, 16, v129
	v_and_b32_e32 v129, 0xffff0000, v129
	v_and_b32_e32 v128, 0xffff0000, v119
	v_lshlrev_b32_e32 v130, 16, v118
	v_lshlrev_b32_e32 v136, 16, v119
	v_pk_mul_f32 v[118:119], v[134:135], v[134:135]
	v_pk_mul_f32 v[128:129], v[128:129], v[128:129]
	v_pk_fma_f32 v[118:119], v[130:131], v[130:131], v[118:119]
	v_pk_fma_f32 v[128:129], v[136:137], v[136:137], v[128:129]
	s_nop 0
	v_pk_add_f32 v[118:119], v[118:119], v[128:129]
	s_nop 0
	v_add_f32_e32 v112, v117, v118
	v_add_f32_e32 v117, v112, v119

.LBB0_494:
	s_or_b64 exec, exec, s[10:11]
	s_waitcnt lgkmcnt(7)
	v_add_f32_e32 v194, v194, v195
	v_add_f32_e32 v195, v196, v197
	v_add_f32_e32 v194, v194, v195
	v_fmamk_f32 v194, v194, 0x3baaaaab, v213
	v_mul_f32_e32 v195, 0x4f800000, v194
	v_cmp_gt_f32_e32 vcc, s90, v194
	s_mul_i32 s58, s49, 0xc0
	s_lshl_b32 s26, s49, 7
	v_cndmask_b32_e32 v194, v194, v195, vcc
	v_sqrt_f32_e32 v195, v194
	s_ashr_i32 s59, s58, 31
	s_ashr_i32 s27, s26, 31
	v_add_u32_e32 v196, -1, v195
	v_fma_f32 v197, -v196, v195, v194
	v_cmp_ge_f32_e64 s[10:11], 0, v197
	v_add_u32_e32 v197, 1, v195
	s_nop 0
	v_cndmask_b32_e64 v196, v195, v196, s[10:11]
	v_fma_f32 v195, -v197, v195, v194
	v_cmp_lt_f32_e64 s[10:11], 0, v195
	s_nop 1
	v_cndmask_b32_e64 v195, v196, v197, s[10:11]
	v_mul_f32_e32 v196, 0x37800000, v195
	v_cndmask_b32_e32 v195, v195, v196, vcc
	v_cmp_class_f32_e32 vcc, v194, v215
	s_and_b64 s[10:11], s[16:17], exec
	s_nop 0
	v_cndmask_b32_e32 v194, v195, v194, vcc
	v_rcp_f32_e32 v196, v194
	s_mov_b32 s10, 0x30680000
	s_cselect_b32 s10, s10, 0x2d380000
	s_add_u32 s60, s18, s10
	v_mul_f32_e32 v195, 1.0, v196
	v_mov_b32_e32 v206, v195
	s_addc_u32 s61, s19, 0
	v_mul_f32_e32 v196, v236, v206
	v_mov_b64_e32 v[194:195], s[60:61]
	v_mad_i64_i32 v[194:195], s[10:11], v232, s91, v[194:195]
	v_pk_mul_f32 v[152:153], v[152:153], v[196:197] op_sel_hi:[1,0]
	v_pk_mul_f32 v[154:155], v[154:155], v[196:197] op_sel_hi:[1,0]
	v_lshl_add_u64 v[194:195], s[58:59], 1, v[194:195]
	s_waitcnt vmcnt(0)
	v_pk_mul_f32 v[154:155], v[154:155], v[142:143]
	v_pk_mul_f32 v[152:153], v[152:153], v[140:141]
	v_lshl_add_u64 v[194:195], v[194:195], 0, s[34:35]
	v_pk_mul_f32 v[156:157], v[156:157], v[196:197] op_sel_hi:[1,0]
	v_cvt_pk_bf16_f32 v152, v152, v153
	v_cvt_pk_bf16_f32 v153, v154, v155
	v_cndmask_b32_e64 v154, 0, 1, s[16:17]
	v_lshl_add_u64 v[194:195], v[208:209], 1, v[194:195]
	v_pk_mul_f32 v[158:159], v[158:159], v[196:197] op_sel_hi:[1,0]
	v_pk_mul_f32 v[156:157], v[136:137], v[156:157]
	v_cmp_ne_u32_e64 s[10:11], 1, v154
	s_andn2_b64 vcc, exec, s[16:17]
	v_pk_mul_f32 v[158:159], v[138:139], v[158:159]
	v_cvt_pk_bf16_f32 v156, v156, v157
	global_store_dwordx2 v[194:195], v[152:153], off offset:32
	v_cvt_pk_bf16_f32 v157, v158, v159
	global_store_dwordx2 v[194:195], v[156:157], off
	s_cbranch_vccnz .LBB0_496
	v_lshlrev_b64 v[152:153], 11, v[232:233]
	v_lshl_add_u64 v[152:153], s[40:41], 0, v[152:153]
	v_lshl_add_u64 v[152:153], s[26:27], 1, v[152:153]
	v_lshl_add_u64 v[152:153], v[152:153], 0, s[34:35]
	v_pk_mul_f32 v[156:157], v[124:125], v[236:237] op_sel_hi:[1,0]
	v_lshl_add_u64 v[152:153], v[208:209], 1, v[152:153]
	v_pk_mul_f32 v[154:155], v[126:127], v[236:237] op_sel_hi:[1,0]
	v_cvt_pk_bf16_f32 v156, v156, v157
	s_nop 0
	v_cvt_pk_bf16_f32 v157, v154, v155
	global_store_dwordx2 v[152:153], v[156:157], off
	v_pk_mul_f32 v[156:157], v[120:121], v[236:237] op_sel_hi:[1,0]
	v_pk_mul_f32 v[154:155], v[122:123], v[236:237] op_sel_hi:[1,0]
	v_cvt_pk_bf16_f32 v156, v156, v157
	s_nop 0
	v_cvt_pk_bf16_f32 v157, v154, v155
	global_store_dwordx2 v[152:153], v[156:157], off offset:32

.LBB0_505:
	v_and_b32_e32 v120, 47, v228
	v_cndmask_b32_e64 v120, v120, v235, s[4:5]
	v_lshlrev_b32_e32 v206, 7, v120
	v_lshl_add_u64 v[120:121], s[38:39], 0, v[206:207]
	v_lshl_add_u64 v[120:121], v[208:209], 3, v[120:121]
	global_load_dwordx2 v[166:167], v[120:121], off offset:16
	global_load_dwordx2 v[160:161], v[120:121], off offset:24
	global_load_dwordx4 v[162:165], v[120:121], off
.LBB0_506:
	s_or_b64 exec, exec, s[16:17]
	s_waitcnt lgkmcnt(6)
	v_add_f32_e32 v120, v190, v191
	v_add_f32_e32 v121, v192, v193
	v_add_f32_e32 v120, v120, v121
	v_fmamk_f32 v120, v120, 0x3baaaaab, v213
	v_mul_f32_e32 v121, 0x4f800000, v120
	v_cmp_gt_f32_e32 vcc, s90, v120
	s_nop 1
	v_cndmask_b32_e32 v120, v120, v121, vcc
	v_sqrt_f32_e32 v121, v120
	s_nop 0
	v_add_u32_e32 v122, -1, v121
	v_fma_f32 v123, -v122, v121, v120
	v_cmp_ge_f32_e64 s[16:17], 0, v123
	v_add_u32_e32 v123, 1, v121
	s_nop 0
	v_cndmask_b32_e64 v122, v121, v122, s[16:17]
	v_fma_f32 v121, -v123, v121, v120
	v_cmp_lt_f32_e64 s[16:17], 0, v121
	s_nop 1
	v_cndmask_b32_e64 v121, v122, v123, s[16:17]
	v_mul_f32_e32 v122, 0x37800000, v121
	v_cndmask_b32_e32 v121, v121, v122, vcc
	v_cmp_class_f32_e32 vcc, v120, v215
	s_nop 1
	v_cndmask_b32_e32 v120, v121, v120, vcc
	v_rcp_f32_e32 v122, v120
	s_nop 0
	v_mul_f32_e32 v121, 1.0, v122
	v_mov_b32_e32 v126, v121
	v_add3_u32 v122, s48, v231, 16
	v_mov_b64_e32 v[120:121], s[60:61]
	v_mad_i64_i32 v[120:121], s[16:17], v122, s91, v[120:121]
	v_mul_f32_e32 v124, v132, v126
	v_lshl_add_u64 v[120:121], s[58:59], 1, v[120:121]
	v_lshl_add_u64 v[120:121], v[120:121], 0, s[34:35]
	v_pk_mul_f32 v[108:109], v[108:109], v[124:125] op_sel_hi:[1,0]
	v_pk_mul_f32 v[104:105], v[104:105], v[124:125] op_sel_hi:[1,0]
	v_ashrrev_i32_e32 v123, 31, v122
	v_lshl_add_u64 v[120:121], v[208:209], 1, v[120:121]
	v_pk_mul_f32 v[110:111], v[110:111], v[124:125] op_sel_hi:[1,0]
	v_pk_mul_f32 v[108:109], v[136:137], v[108:109]
	v_pk_mul_f32 v[106:107], v[106:107], v[124:125] op_sel_hi:[1,0]
	v_pk_mul_f32 v[104:105], v[104:105], v[140:141]
	s_and_b64 vcc, exec, s[10:11]
	v_pk_mul_f32 v[110:111], v[138:139], v[110:111]
	v_cvt_pk_bf16_f32 v108, v108, v109
	v_pk_mul_f32 v[106:107], v[106:107], v[142:143]
	v_cvt_pk_bf16_f32 v109, v110, v111
	global_store_dwordx2 v[120:121], v[108:109], off
	v_cvt_pk_bf16_f32 v104, v104, v105
	v_cvt_pk_bf16_f32 v105, v106, v107
	global_store_dwordx2 v[120:121], v[104:105], off offset:32
	s_cbranch_vccnz .LBB0_508
	v_lshlrev_b64 v[104:105], 11, v[122:123]
	v_lshl_add_u64 v[104:105], s[40:41], 0, v[104:105]
	v_lshl_add_u64 v[104:105], s[26:27], 1, v[104:105]
	v_lshl_add_u64 v[104:105], v[104:105], 0, s[34:35]
	v_pk_mul_f32 v[108:109], v[100:101], v[132:133] op_sel_hi:[1,0]
	v_lshl_add_u64 v[104:105], v[208:209], 1, v[104:105]
	v_pk_mul_f32 v[106:107], v[102:103], v[132:133] op_sel_hi:[1,0]
	v_cvt_pk_bf16_f32 v108, v108, v109
	s_nop 0
	v_cvt_pk_bf16_f32 v109, v106, v107
	global_store_dwordx2 v[104:105], v[108:109], off
	v_pk_mul_f32 v[108:109], v[96:97], v[132:133] op_sel_hi:[1,0]
	v_pk_mul_f32 v[106:107], v[98:99], v[132:133] op_sel_hi:[1,0]
	v_cvt_pk_bf16_f32 v108, v108, v109
	s_nop 0
	v_cvt_pk_bf16_f32 v109, v106, v107
	global_store_dwordx2 v[104:105], v[108:109], off offset:32

.LBB0_517:
	v_cndmask_b32_e64 v96, v234, v133, s[4:5]
	v_lshlrev_b32_e32 v96, 7, v96
	v_and_b32_e32 v206, 0x1f80, v96
	v_lshl_add_u64 v[96:97], s[38:39], 0, v[206:207]
	v_lshl_add_u64 v[96:97], v[208:209], 3, v[96:97]
	global_load_dwordx2 v[144:145], v[96:97], off offset:16
	global_load_dwordx2 v[134:135], v[96:97], off offset:24
	global_load_dwordx4 v[128:131], v[96:97], off
.LBB0_518:
	s_or_b64 exec, exec, s[16:17]
	s_waitcnt lgkmcnt(5)
	v_add_f32_e32 v96, v186, v187
	v_add_f32_e32 v97, v188, v189
	v_add_f32_e32 v96, v96, v97
	v_fmamk_f32 v96, v96, 0x3baaaaab, v213
	v_mul_f32_e32 v97, 0x4f800000, v96
	v_cmp_gt_f32_e32 vcc, s90, v96
	s_nop 1
	v_cndmask_b32_e32 v96, v96, v97, vcc
	v_sqrt_f32_e32 v97, v96
	s_nop 0
	v_add_u32_e32 v98, -1, v97
	v_fma_f32 v99, -v98, v97, v96
	v_cmp_ge_f32_e64 s[16:17], 0, v99
	v_add_u32_e32 v99, 1, v97
	s_nop 0
	v_cndmask_b32_e64 v98, v97, v98, s[16:17]
	v_fma_f32 v97, -v99, v97, v96
	v_cmp_lt_f32_e64 s[16:17], 0, v97
	s_nop 1
	v_cndmask_b32_e64 v97, v98, v99, s[16:17]
	v_mul_f32_e32 v98, 0x37800000, v97
	v_cndmask_b32_e32 v97, v97, v98, vcc
	v_cmp_class_f32_e32 vcc, v96, v215
	s_nop 1
	v_cndmask_b32_e32 v96, v97, v96, vcc
	v_rcp_f32_e32 v98, v96
	s_nop 0
	v_mul_f32_e32 v97, 1.0, v98
	v_mov_b32_e32 v100, v97
	v_mov_b64_e32 v[96:97], s[60:61]
	v_mad_i64_i32 v[96:97], s[16:17], v228, s91, v[96:97]
	v_mul_f32_e32 v98, v230, v100
	v_lshl_add_u64 v[96:97], s[58:59], 1, v[96:97]
	v_lshl_add_u64 v[96:97], v[96:97], 0, s[34:35]
	v_pk_mul_f32 v[92:93], v[92:93], v[98:99] op_sel_hi:[1,0]
	v_pk_mul_f32 v[88:89], v[88:89], v[98:99] op_sel_hi:[1,0]
	v_lshl_add_u64 v[96:97], v[208:209], 1, v[96:97]
	v_pk_mul_f32 v[94:95], v[94:95], v[98:99] op_sel_hi:[1,0]
	v_pk_mul_f32 v[92:93], v[136:137], v[92:93]
	v_pk_mul_f32 v[90:91], v[90:91], v[98:99] op_sel_hi:[1,0]
	v_pk_mul_f32 v[88:89], v[88:89], v[140:141]
	s_and_b64 vcc, exec, s[10:11]
	v_pk_mul_f32 v[94:95], v[138:139], v[94:95]
	v_cvt_pk_bf16_f32 v92, v92, v93
	v_pk_mul_f32 v[90:91], v[90:91], v[142:143]
	v_cvt_pk_bf16_f32 v93, v94, v95
	global_store_dwordx2 v[96:97], v[92:93], off
	v_cvt_pk_bf16_f32 v88, v88, v89
	v_cvt_pk_bf16_f32 v89, v90, v91
	global_store_dwordx2 v[96:97], v[88:89], off offset:32
	s_cbranch_vccnz .LBB0_520
	v_lshlrev_b64 v[88:89], 11, v[228:229]
	v_lshl_add_u64 v[88:89], s[40:41], 0, v[88:89]
	v_lshl_add_u64 v[88:89], s[26:27], 1, v[88:89]
	v_lshl_add_u64 v[88:89], v[88:89], 0, s[34:35]
	v_pk_mul_f32 v[92:93], v[84:85], v[230:231] op_sel_hi:[1,0]
	v_lshl_add_u64 v[88:89], v[208:209], 1, v[88:89]
	v_pk_mul_f32 v[90:91], v[86:87], v[230:231] op_sel_hi:[1,0]
	v_cvt_pk_bf16_f32 v92, v92, v93
	s_nop 0
	v_cvt_pk_bf16_f32 v93, v90, v91
	global_store_dwordx2 v[88:89], v[92:93], off
	v_pk_mul_f32 v[92:93], v[80:81], v[230:231] op_sel_hi:[1,0]
	v_pk_mul_f32 v[90:91], v[82:83], v[230:231] op_sel_hi:[1,0]
	v_cvt_pk_bf16_f32 v92, v92, v93
	s_nop 0
	v_cvt_pk_bf16_f32 v93, v90, v91
	global_store_dwordx2 v[88:89], v[92:93], off offset:32

.LBB0_525:
	v_pk_mul_f32 v[86:87], v[114:115], v[90:91]
	v_pk_mul_f32 v[80:81], v[112:113], v[88:89]
	v_pk_mul_f32 v[84:85], v[118:119], v[94:95]
	v_pk_mul_f32 v[82:83], v[116:117], v[92:93]
	s_and_saveexec_b64 s[16:17], s[14:15]
	s_cbranch_execz .LBB0_527
	s_waitcnt vmcnt(7)
	v_mul_f32_e32 v98, v167, v84
	v_mul_f32_e32 v102, v166, v84
	v_mov_b32_e32 v84, v87
	v_mov_b32_e32 v90, v163
	v_mov_b32_e32 v91, v165
	v_mul_f32_e32 v94, v166, v86
	v_mul_f32_e32 v100, v167, v86
	v_pk_mul_f32 v[104:105], v[160:161], v[84:85]
	v_mov_b32_e32 v86, v85
	v_mov_b32_e32 v88, v162
	v_mov_b32_e32 v89, v164
	v_pk_mul_f32 v[92:93], v[90:91], v[82:83]
	v_mov_b32_e32 v95, v104
	v_mov_b32_e32 v99, v105
	v_pk_mul_f32 v[84:85], v[160:161], v[86:87]
	v_pk_mul_f32 v[90:91], v[90:91], v[80:81]
	v_pk_fma_f32 v[80:81], v[88:89], v[80:81], v[92:93] neg_lo:[0,0,1] neg_hi:[0,0,1]
	v_pk_add_f32 v[92:93], v[94:95], v[98:99] neg_lo:[0,1] neg_hi:[0,1]
	v_mov_b32_e32 v103, v84
	v_mov_b32_e32 v101, v85
	v_pk_fma_f32 v[82:83], v[88:89], v[82:83], v[90:91]
	v_pk_add_f32 v[84:85], v[102:103], v[100:101]
	v_mov_b32_e32 v86, v92
	v_mov_b32_e32 v87, v93

.LBB0_530:
	v_cmp_gt_i32_e64 s[14:15], s76, v80
	s_and_b64 s[62:63], s[44:45], s[14:15]
	v_bfe_u32 v89, v80, 6, 6
	s_and_saveexec_b64 s[16:17], s[62:63]
	s_cbranch_execz .LBB0_532
	v_cndmask_b32_e64 v81, v237, v89, s[4:5]
	v_lshlrev_b32_e32 v206, 7, v81
	v_lshl_add_u64 v[82:83], s[38:39], 0, v[206:207]
	v_lshl_add_u64 v[82:83], v[208:209], 3, v[82:83]
	global_load_dwordx2 v[166:167], v[82:83], off offset:16
	global_load_dwordx2 v[160:161], v[82:83], off offset:24
	global_load_dwordx4 v[162:165], v[82:83], off
.LBB0_532:
	s_or_b64 exec, exec, s[16:17]
	s_waitcnt lgkmcnt(4)
	v_add_f32_e32 v81, v182, v183
	v_add_f32_e32 v82, v184, v185
	v_add_f32_e32 v81, v81, v82
	v_fmamk_f32 v81, v81, 0x3baaaaab, v213
	v_mul_f32_e32 v82, 0x4f800000, v81
	v_cmp_gt_f32_e32 vcc, s90, v81
	s_nop 1
	v_cndmask_b32_e32 v81, v81, v82, vcc
	v_sqrt_f32_e32 v82, v81
	s_nop 0
	v_add_u32_e32 v83, -1, v82
	v_fma_f32 v84, -v83, v82, v81
	v_cmp_ge_f32_e64 s[16:17], 0, v84
	v_add_u32_e32 v84, 1, v82
	s_nop 0
	v_cndmask_b32_e64 v83, v82, v83, s[16:17]
	v_fma_f32 v82, -v84, v82, v81
	v_cmp_lt_f32_e64 s[16:17], 0, v82
	s_nop 1
	v_cndmask_b32_e64 v82, v83, v84, s[16:17]
	v_mul_f32_e32 v83, 0x37800000, v82
	v_cndmask_b32_e32 v82, v82, v83, vcc
	v_cmp_class_f32_e32 vcc, v81, v215
	s_nop 1
	v_cndmask_b32_e32 v81, v82, v81, vcc
	v_rcp_f32_e32 v83, v81
	s_nop 0
	v_mul_f32_e32 v82, 1.0, v83
	v_mov_b32_e32 v88, v82
	v_add3_u32 v84, s48, v231, 48
	v_mov_b64_e32 v[82:83], s[60:61]
	v_mad_i64_i32 v[82:83], s[16:17], v84, s91, v[82:83]
	v_mul_f32_e32 v86, v226, v88
	v_lshl_add_u64 v[82:83], s[58:59], 1, v[82:83]
	v_lshl_add_u64 v[82:83], v[82:83], 0, s[34:35]
	v_pk_mul_f32 v[76:77], v[76:77], v[86:87] op_sel_hi:[1,0]
	v_pk_mul_f32 v[72:73], v[72:73], v[86:87] op_sel_hi:[1,0]
	v_ashrrev_i32_e32 v85, 31, v84
	v_lshl_add_u64 v[82:83], v[208:209], 1, v[82:83]
	v_pk_mul_f32 v[78:79], v[78:79], v[86:87] op_sel_hi:[1,0]
	v_pk_mul_f32 v[76:77], v[136:137], v[76:77]
	v_pk_mul_f32 v[74:75], v[74:75], v[86:87] op_sel_hi:[1,0]
	v_pk_mul_f32 v[72:73], v[72:73], v[140:141]
	s_and_b64 vcc, exec, s[10:11]
	v_pk_mul_f32 v[78:79], v[138:139], v[78:79]
	v_cvt_pk_bf16_f32 v76, v76, v77
	v_pk_mul_f32 v[74:75], v[74:75], v[142:143]
	v_cvt_pk_bf16_f32 v77, v78, v79
	global_store_dwordx2 v[82:83], v[76:77], off
	v_cvt_pk_bf16_f32 v72, v72, v73
	v_cvt_pk_bf16_f32 v73, v74, v75
	global_store_dwordx2 v[82:83], v[72:73], off offset:32
	s_cbranch_vccnz .LBB0_534
	v_lshlrev_b64 v[72:73], 11, v[84:85]
	v_lshl_add_u64 v[72:73], s[40:41], 0, v[72:73]
	v_lshl_add_u64 v[72:73], s[26:27], 1, v[72:73]
	v_lshl_add_u64 v[72:73], v[72:73], 0, s[34:35]
	v_pk_mul_f32 v[76:77], v[68:69], v[226:227] op_sel_hi:[1,0]
	v_lshl_add_u64 v[72:73], v[208:209], 1, v[72:73]
	v_pk_mul_f32 v[74:75], v[70:71], v[226:227] op_sel_hi:[1,0]
	v_cvt_pk_bf16_f32 v76, v76, v77
	s_nop 0
	v_cvt_pk_bf16_f32 v77, v74, v75
	global_store_dwordx2 v[72:73], v[76:77], off
	v_pk_mul_f32 v[76:77], v[64:65], v[226:227] op_sel_hi:[1,0]
	v_pk_mul_f32 v[74:75], v[66:67], v[226:227] op_sel_hi:[1,0]
	v_cvt_pk_bf16_f32 v76, v76, v77
	s_nop 0
	v_cvt_pk_bf16_f32 v77, v74, v75
	global_store_dwordx2 v[72:73], v[76:77], off offset:32

.LBB0_539:
	v_pk_mul_f32 v[64:65], v[118:119], v[78:79]
	v_pk_mul_f32 v[66:67], v[116:117], v[76:77]
	v_pk_mul_f32 v[70:71], v[114:115], v[74:75]
	v_pk_mul_f32 v[68:69], v[112:113], v[72:73]
	v_cmp_gt_i32_e32 vcc, s76, v84
	s_and_saveexec_b64 s[16:17], vcc
	s_cbranch_execz .LBB0_541
	s_waitcnt vmcnt(7)
	v_mul_f32_e32 v84, v145, v64
	v_mul_f32_e32 v90, v144, v64
	v_mov_b32_e32 v64, v71
	v_mov_b32_e32 v74, v129
	v_mov_b32_e32 v75, v131
	v_mul_f32_e32 v78, v144, v70
	v_mul_f32_e32 v86, v145, v70
	v_pk_mul_f32 v[92:93], v[134:135], v[64:65]
	v_mov_b32_e32 v70, v65
	v_mov_b32_e32 v72, v128
	v_mov_b32_e32 v73, v130
	v_pk_mul_f32 v[76:77], v[74:75], v[66:67]
	v_mov_b32_e32 v79, v92
	v_mov_b32_e32 v85, v93
	v_pk_mul_f32 v[64:65], v[134:135], v[70:71]
	v_pk_mul_f32 v[66:67], v[72:73], v[66:67]
	v_pk_fma_f32 v[72:73], v[72:73], v[68:69], v[76:77] neg_lo:[0,0,1] neg_hi:[0,0,1]
	v_pk_add_f32 v[76:77], v[78:79], v[84:85] neg_lo:[0,1] neg_hi:[0,1]
	v_mov_b32_e32 v87, v65
	v_mov_b32_e32 v91, v64
	v_pk_fma_f32 v[66:67], v[74:75], v[68:69], v[66:67]
	v_pk_add_f32 v[64:65], v[86:87], v[90:91]
	v_mov_b32_e32 v68, v72
	v_mov_b32_e32 v69, v73
	v_mov_b32_e32 v70, v76
	v_mov_b32_e32 v71, v77

.LBB0_544:
	v_cmp_gt_i32_e32 vcc, s76, v64
	s_and_b64 s[62:63], s[44:45], vcc
	v_lshrrev_b32_e32 v69, 6, v80
	s_and_saveexec_b64 s[16:17], s[62:63]
	s_cbranch_execz .LBB0_546
	v_cndmask_b32_e64 v64, v64, v69, s[4:5]
	v_lshlrev_b32_e32 v64, 7, v64
	v_and_b32_e32 v206, 0x1f80, v64
	v_lshl_add_u64 v[64:65], s[38:39], 0, v[206:207]
	v_lshl_add_u64 v[64:65], v[208:209], 3, v[64:65]
	global_load_dwordx2 v[144:145], v[64:65], off offset:16
	global_load_dwordx2 v[134:135], v[64:65], off offset:24
	global_load_dwordx4 v[128:131], v[64:65], off
.LBB0_546:
	s_or_b64 exec, exec, s[16:17]
	s_waitcnt lgkmcnt(3)
	v_add_f32_e32 v64, v178, v179
	v_add_f32_e32 v65, v180, v181
	v_add_f32_e32 v64, v64, v65
	v_fmamk_f32 v64, v64, 0x3baaaaab, v213
	v_mul_f32_e32 v65, 0x4f800000, v64
	v_cmp_gt_f32_e32 vcc, s90, v64
	s_nop 1
	v_cndmask_b32_e32 v64, v64, v65, vcc
	v_sqrt_f32_e32 v65, v64
	s_nop 0
	v_add_u32_e32 v66, -1, v65
	v_fma_f32 v67, -v66, v65, v64
	v_cmp_ge_f32_e64 s[16:17], 0, v67
	v_add_u32_e32 v67, 1, v65
	s_nop 0
	v_cndmask_b32_e64 v66, v65, v66, s[16:17]
	v_fma_f32 v65, -v67, v65, v64
	v_cmp_lt_f32_e64 s[16:17], 0, v65
	s_nop 1
	v_cndmask_b32_e64 v65, v66, v67, s[16:17]
	v_mul_f32_e32 v66, 0x37800000, v65
	v_cndmask_b32_e32 v65, v65, v66, vcc
	v_cmp_class_f32_e32 vcc, v64, v215
	s_nop 1
	v_cndmask_b32_e32 v64, v65, v64, vcc
	v_rcp_f32_e32 v66, v64
	s_nop 0
	v_mul_f32_e32 v65, 1.0, v66
	v_mov_b32_e32 v68, v65
	v_mov_b64_e32 v[64:65], s[60:61]
	v_mad_i64_i32 v[64:65], s[16:17], v80, s91, v[64:65]
	v_mul_f32_e32 v66, v220, v68
	v_lshl_add_u64 v[64:65], s[58:59], 1, v[64:65]
	v_lshl_add_u64 v[64:65], v[64:65], 0, s[34:35]
	v_pk_mul_f32 v[60:61], v[60:61], v[66:67] op_sel_hi:[1,0]
	v_pk_mul_f32 v[56:57], v[56:57], v[66:67] op_sel_hi:[1,0]
	v_lshl_add_u64 v[64:65], v[208:209], 1, v[64:65]
	v_pk_mul_f32 v[62:63], v[62:63], v[66:67] op_sel_hi:[1,0]
	v_pk_mul_f32 v[60:61], v[136:137], v[60:61]
	v_pk_mul_f32 v[58:59], v[58:59], v[66:67] op_sel_hi:[1,0]
	v_pk_mul_f32 v[56:57], v[56:57], v[140:141]
	s_and_b64 vcc, exec, s[10:11]
	v_pk_mul_f32 v[62:63], v[138:139], v[62:63]
	v_cvt_pk_bf16_f32 v60, v60, v61
	v_pk_mul_f32 v[58:59], v[58:59], v[142:143]
	v_cvt_pk_bf16_f32 v61, v62, v63
	global_store_dwordx2 v[64:65], v[60:61], off
	v_cvt_pk_bf16_f32 v56, v56, v57
	v_cvt_pk_bf16_f32 v57, v58, v59
	global_store_dwordx2 v[64:65], v[56:57], off offset:32
	s_cbranch_vccnz .LBB0_548
	v_ashrrev_i32_e32 v81, 31, v80
	v_lshlrev_b64 v[56:57], 11, v[80:81]
	v_lshl_add_u64 v[56:57], s[40:41], 0, v[56:57]
	v_lshl_add_u64 v[56:57], s[26:27], 1, v[56:57]
	v_lshl_add_u64 v[56:57], v[56:57], 0, s[34:35]
	v_pk_mul_f32 v[60:61], v[52:53], v[220:221] op_sel_hi:[1,0]
	v_lshl_add_u64 v[56:57], v[208:209], 1, v[56:57]
	v_pk_mul_f32 v[58:59], v[54:55], v[220:221] op_sel_hi:[1,0]
	v_cvt_pk_bf16_f32 v60, v60, v61
	s_nop 0
	v_cvt_pk_bf16_f32 v61, v58, v59
	global_store_dwordx2 v[56:57], v[60:61], off
	v_pk_mul_f32 v[60:61], v[48:49], v[220:221] op_sel_hi:[1,0]
	v_pk_mul_f32 v[58:59], v[50:51], v[220:221] op_sel_hi:[1,0]
	v_cvt_pk_bf16_f32 v60, v60, v61
	s_nop 0
	v_cvt_pk_bf16_f32 v61, v58, v59
	global_store_dwordx2 v[56:57], v[60:61], off offset:32

.LBB0_553:
	v_pk_mul_f32 v[54:55], v[114:115], v[58:59]
	v_pk_mul_f32 v[48:49], v[112:113], v[56:57]
	v_pk_mul_f32 v[52:53], v[118:119], v[62:63]
	v_pk_mul_f32 v[50:51], v[116:117], v[60:61]
	s_and_saveexec_b64 s[16:17], s[14:15]
	s_cbranch_execz .LBB0_555
	s_waitcnt vmcnt(7)
	v_mul_f32_e32 v66, v167, v52
	v_mul_f32_e32 v72, v166, v52
	v_mov_b32_e32 v52, v55
	v_mov_b32_e32 v58, v163
	v_mov_b32_e32 v59, v165
	v_mul_f32_e32 v62, v166, v54
	v_mul_f32_e32 v70, v167, v54
	v_pk_mul_f32 v[74:75], v[160:161], v[52:53]
	v_mov_b32_e32 v54, v53
	v_mov_b32_e32 v56, v162
	v_mov_b32_e32 v57, v164
	v_pk_mul_f32 v[60:61], v[58:59], v[50:51]
	v_mov_b32_e32 v63, v74
	v_mov_b32_e32 v67, v75
	v_pk_mul_f32 v[52:53], v[160:161], v[54:55]
	v_pk_mul_f32 v[58:59], v[58:59], v[48:49]
	v_pk_fma_f32 v[48:49], v[56:57], v[48:49], v[60:61] neg_lo:[0,0,1] neg_hi:[0,0,1]
	v_pk_add_f32 v[60:61], v[62:63], v[66:67] neg_lo:[0,1] neg_hi:[0,1]
	v_mov_b32_e32 v73, v52
	v_mov_b32_e32 v71, v53
	v_pk_fma_f32 v[50:51], v[56:57], v[50:51], v[58:59]
	v_pk_add_f32 v[52:53], v[72:73], v[70:71]
	v_mov_b32_e32 v54, v60
	v_mov_b32_e32 v55, v61

.LBB0_557:
	v_and_b32_e32 v49, 47, v48
	v_cndmask_b32_e64 v49, v49, v89, s[4:5]
	v_lshlrev_b32_e32 v206, 7, v49
	v_lshl_add_u64 v[50:51], s[38:39], 0, v[206:207]
	v_lshl_add_u64 v[50:51], v[208:209], 3, v[50:51]
	global_load_dwordx2 v[166:167], v[50:51], off offset:16
	global_load_dwordx2 v[160:161], v[50:51], off offset:24
	global_load_dwordx4 v[162:165], v[50:51], off
.LBB0_558:
	s_or_b64 exec, exec, s[16:17]
	s_waitcnt lgkmcnt(2)
	v_add_f32_e32 v49, v174, v175
	v_add_f32_e32 v50, v176, v177
	v_add_f32_e32 v49, v49, v50
	v_fmamk_f32 v49, v49, 0x3baaaaab, v213
	v_mul_f32_e32 v50, 0x4f800000, v49
	v_cmp_gt_f32_e32 vcc, s90, v49
	s_nop 1
	v_cndmask_b32_e32 v49, v49, v50, vcc
	v_sqrt_f32_e32 v50, v49
	s_nop 0
	v_add_u32_e32 v51, -1, v50
	v_fma_f32 v52, -v51, v50, v49
	v_cmp_ge_f32_e64 s[16:17], 0, v52
	v_add_u32_e32 v52, 1, v50
	s_nop 0
	v_cndmask_b32_e64 v51, v50, v51, s[16:17]
	v_fma_f32 v50, -v52, v50, v49
	v_cmp_lt_f32_e64 s[16:17], 0, v50
	s_nop 1
	v_cndmask_b32_e64 v50, v51, v52, s[16:17]
	v_mul_f32_e32 v51, 0x37800000, v50
	v_cndmask_b32_e32 v50, v50, v51, vcc
	v_cmp_class_f32_e32 vcc, v49, v215
	s_nop 1
	v_cndmask_b32_e32 v49, v50, v49, vcc
	v_rcp_f32_e32 v51, v49
	s_nop 0
	v_mul_f32_e32 v50, 1.0, v51
	v_mov_b32_e32 v56, v50
	v_add3_u32 v52, s48, v227, 16
	v_mov_b64_e32 v[50:51], s[60:61]
	v_mad_i64_i32 v[50:51], s[16:17], v52, s91, v[50:51]
	v_mul_f32_e32 v54, v214, v56
	v_lshl_add_u64 v[50:51], s[58:59], 1, v[50:51]
	v_lshl_add_u64 v[50:51], v[50:51], 0, s[34:35]
	v_pk_mul_f32 v[44:45], v[44:45], v[54:55] op_sel_hi:[1,0]
	v_pk_mul_f32 v[40:41], v[40:41], v[54:55] op_sel_hi:[1,0]
	v_ashrrev_i32_e32 v53, 31, v52
	v_lshl_add_u64 v[50:51], v[208:209], 1, v[50:51]
	v_pk_mul_f32 v[46:47], v[46:47], v[54:55] op_sel_hi:[1,0]
	v_pk_mul_f32 v[44:45], v[136:137], v[44:45]
	v_pk_mul_f32 v[42:43], v[42:43], v[54:55] op_sel_hi:[1,0]
	v_pk_mul_f32 v[40:41], v[40:41], v[140:141]
	s_and_b64 vcc, exec, s[10:11]
	v_pk_mul_f32 v[46:47], v[138:139], v[46:47]
	v_cvt_pk_bf16_f32 v44, v44, v45
	v_pk_mul_f32 v[42:43], v[42:43], v[142:143]
	v_cvt_pk_bf16_f32 v45, v46, v47
	global_store_dwordx2 v[50:51], v[44:45], off
	v_cvt_pk_bf16_f32 v40, v40, v41
	v_cvt_pk_bf16_f32 v41, v42, v43
	global_store_dwordx2 v[50:51], v[40:41], off offset:32
	s_cbranch_vccnz .LBB0_560
	v_lshlrev_b64 v[40:41], 11, v[52:53]
	v_lshl_add_u64 v[40:41], s[40:41], 0, v[40:41]
	v_lshl_add_u64 v[40:41], s[26:27], 1, v[40:41]
	v_lshl_add_u64 v[40:41], v[40:41], 0, s[34:35]
	v_pk_mul_f32 v[44:45], v[36:37], v[214:215] op_sel_hi:[1,0]
	v_lshl_add_u64 v[40:41], v[208:209], 1, v[40:41]
	v_pk_mul_f32 v[42:43], v[38:39], v[214:215] op_sel_hi:[1,0]
	v_cvt_pk_bf16_f32 v44, v44, v45
	s_nop 0
	v_cvt_pk_bf16_f32 v45, v42, v43
	global_store_dwordx2 v[40:41], v[44:45], off
	v_pk_mul_f32 v[44:45], v[32:33], v[214:215] op_sel_hi:[1,0]
	v_pk_mul_f32 v[42:43], v[34:35], v[214:215] op_sel_hi:[1,0]
	v_cvt_pk_bf16_f32 v44, v44, v45
	s_nop 0
	v_cvt_pk_bf16_f32 v45, v42, v43
	global_store_dwordx2 v[40:41], v[44:45], off offset:32

.LBB0_565:
	v_pk_mul_f32 v[32:33], v[118:119], v[46:47]
	v_pk_mul_f32 v[34:35], v[116:117], v[44:45]
	v_pk_mul_f32 v[38:39], v[114:115], v[42:43]
	v_pk_mul_f32 v[36:37], v[112:113], v[40:41]
	v_cmp_gt_i32_e32 vcc, s76, v52
	s_and_saveexec_b64 s[16:17], vcc
	s_cbranch_execz .LBB0_567
	s_waitcnt vmcnt(7)
	v_mul_f32_e32 v52, v145, v32
	v_mul_f32_e32 v56, v144, v32
	v_mov_b32_e32 v32, v39
	v_mov_b32_e32 v42, v129
	v_mov_b32_e32 v43, v131
	v_mul_f32_e32 v46, v144, v38
	v_mul_f32_e32 v54, v145, v38
	v_pk_mul_f32 v[58:59], v[134:135], v[32:33]
	v_mov_b32_e32 v38, v33
	v_mov_b32_e32 v40, v128
	v_mov_b32_e32 v41, v130
	v_pk_mul_f32 v[44:45], v[42:43], v[34:35]
	v_mov_b32_e32 v47, v58
	v_mov_b32_e32 v53, v59
	v_pk_mul_f32 v[32:33], v[134:135], v[38:39]
	v_pk_mul_f32 v[34:35], v[40:41], v[34:35]
	v_pk_fma_f32 v[40:41], v[40:41], v[36:37], v[44:45] neg_lo:[0,0,1] neg_hi:[0,0,1]
	v_pk_add_f32 v[44:45], v[46:47], v[52:53] neg_lo:[0,1] neg_hi:[0,1]
	v_mov_b32_e32 v55, v33
	v_mov_b32_e32 v57, v32
	v_pk_fma_f32 v[34:35], v[42:43], v[36:37], v[34:35]
	v_pk_add_f32 v[32:33], v[54:55], v[56:57]
	v_mov_b32_e32 v36, v40
	v_mov_b32_e32 v37, v41
	v_mov_b32_e32 v38, v44
	v_mov_b32_e32 v39, v45

.LBB0_569:
	v_cndmask_b32_e64 v32, v32, v69, s[4:5]
	v_lshlrev_b32_e32 v32, 7, v32
	v_and_b32_e32 v206, 0x1f80, v32
	v_lshl_add_u64 v[32:33], s[38:39], 0, v[206:207]
	v_lshl_add_u64 v[32:33], v[208:209], 3, v[32:33]
	global_load_dwordx2 v[144:145], v[32:33], off offset:16
	global_load_dwordx2 v[134:135], v[32:33], off offset:24
	global_load_dwordx4 v[128:131], v[32:33], off
.LBB0_570:
	s_or_b64 exec, exec, s[12:13]
	s_waitcnt lgkmcnt(1)
	v_add_f32_e32 v32, v170, v171
	v_add_f32_e32 v33, v172, v173
	v_add_f32_e32 v32, v32, v33
	v_fmamk_f32 v32, v32, 0x3baaaaab, v213
	v_mul_f32_e32 v33, 0x4f800000, v32
	v_cmp_gt_f32_e32 vcc, s90, v32
	s_nop 1
	v_cndmask_b32_e32 v32, v32, v33, vcc
	v_sqrt_f32_e32 v33, v32
	s_nop 0
	v_add_u32_e32 v34, -1, v33
	v_fma_f32 v35, -v34, v33, v32
	v_cmp_ge_f32_e64 s[12:13], 0, v35
	v_add_u32_e32 v35, 1, v33
	s_nop 0
	v_cndmask_b32_e64 v34, v33, v34, s[12:13]
	v_fma_f32 v33, -v35, v33, v32
	v_cmp_lt_f32_e64 s[12:13], 0, v33
	s_nop 1
	v_cndmask_b32_e64 v33, v34, v35, s[12:13]
	v_mul_f32_e32 v34, 0x37800000, v33
	v_cndmask_b32_e32 v33, v33, v34, vcc
	v_cmp_class_f32_e32 vcc, v32, v215
	s_nop 1
	v_cndmask_b32_e32 v32, v33, v32, vcc
	v_rcp_f32_e32 v34, v32
	s_nop 0
	v_mul_f32_e32 v33, 1.0, v34
	v_mov_b32_e32 v36, v33
	v_mov_b64_e32 v[32:33], s[60:61]
	v_mad_i64_i32 v[32:33], s[12:13], v48, s91, v[32:33]
	v_mul_f32_e32 v34, v212, v36
	v_lshl_add_u64 v[32:33], s[58:59], 1, v[32:33]
	v_lshl_add_u64 v[32:33], v[32:33], 0, s[34:35]
	v_pk_mul_f32 v[28:29], v[28:29], v[34:35] op_sel_hi:[1,0]
	v_pk_mul_f32 v[24:25], v[24:25], v[34:35] op_sel_hi:[1,0]
	v_lshl_add_u64 v[32:33], v[208:209], 1, v[32:33]
	v_pk_mul_f32 v[30:31], v[30:31], v[34:35] op_sel_hi:[1,0]
	v_pk_mul_f32 v[28:29], v[136:137], v[28:29]
	v_pk_mul_f32 v[26:27], v[26:27], v[34:35] op_sel_hi:[1,0]
	v_pk_mul_f32 v[24:25], v[24:25], v[140:141]
	s_and_b64 vcc, exec, s[10:11]
	v_pk_mul_f32 v[30:31], v[138:139], v[30:31]
	v_cvt_pk_bf16_f32 v28, v28, v29
	v_pk_mul_f32 v[26:27], v[26:27], v[142:143]
	v_cvt_pk_bf16_f32 v29, v30, v31
	global_store_dwordx2 v[32:33], v[28:29], off
	v_cvt_pk_bf16_f32 v24, v24, v25
	v_cvt_pk_bf16_f32 v25, v26, v27
	global_store_dwordx2 v[32:33], v[24:25], off offset:32
	s_cbranch_vccnz .LBB0_572
	v_ashrrev_i32_e32 v49, 31, v48
	v_lshlrev_b64 v[24:25], 11, v[48:49]
	v_lshl_add_u64 v[24:25], s[40:41], 0, v[24:25]
	v_lshl_add_u64 v[24:25], s[26:27], 1, v[24:25]
	v_lshl_add_u64 v[24:25], v[24:25], 0, s[34:35]
	v_pk_mul_f32 v[28:29], v[20:21], v[212:213] op_sel_hi:[1,0]
	v_lshl_add_u64 v[24:25], v[208:209], 1, v[24:25]
	v_pk_mul_f32 v[26:27], v[22:23], v[212:213] op_sel_hi:[1,0]
	v_cvt_pk_bf16_f32 v28, v28, v29
	s_nop 0
	v_cvt_pk_bf16_f32 v29, v26, v27
	global_store_dwordx2 v[24:25], v[28:29], off
	v_pk_mul_f32 v[28:29], v[16:17], v[212:213] op_sel_hi:[1,0]
	v_pk_mul_f32 v[26:27], v[18:19], v[212:213] op_sel_hi:[1,0]
	v_cvt_pk_bf16_f32 v28, v28, v29
	s_nop 0
	v_cvt_pk_bf16_f32 v29, v26, v27
	global_store_dwordx2 v[24:25], v[28:29], off offset:32

.LBB0_577:
	v_pk_mul_f32 v[22:23], v[114:115], v[26:27]
	v_pk_mul_f32 v[16:17], v[112:113], v[24:25]
	v_pk_mul_f32 v[20:21], v[118:119], v[30:31]
	v_pk_mul_f32 v[18:19], v[116:117], v[28:29]
	s_and_saveexec_b64 s[12:13], s[14:15]
	s_cbranch_execz .LBB0_579
	s_waitcnt vmcnt(7)
	v_mul_f32_e32 v34, v167, v20
	v_mul_f32_e32 v38, v166, v20
	v_mov_b32_e32 v20, v23
	v_mov_b32_e32 v25, v164
	v_mov_b32_e32 v164, v163
	v_mul_f32_e32 v30, v166, v22
	v_mul_f32_e32 v36, v167, v22
	v_pk_mul_f32 v[40:41], v[160:161], v[20:21]
	v_mov_b32_e32 v22, v21
	v_mov_b32_e32 v24, v162
	v_pk_mul_f32 v[26:27], v[164:165], v[18:19]
	v_mov_b32_e32 v31, v40
	v_mov_b32_e32 v35, v41
	v_pk_mul_f32 v[20:21], v[160:161], v[22:23]
	v_pk_mul_f32 v[28:29], v[164:165], v[16:17]
	v_pk_fma_f32 v[16:17], v[24:25], v[16:17], v[26:27] neg_lo:[0,0,1] neg_hi:[0,0,1]
	v_pk_add_f32 v[26:27], v[30:31], v[34:35] neg_lo:[0,1] neg_hi:[0,1]
	v_mov_b32_e32 v39, v20
	v_mov_b32_e32 v37, v21
	v_pk_fma_f32 v[18:19], v[24:25], v[18:19], v[28:29]
	v_pk_add_f32 v[20:21], v[38:39], v[36:37]
	v_mov_b32_e32 v22, v26
	v_mov_b32_e32 v23, v27

.LBB0_580:
	s_waitcnt lgkmcnt(0)
	v_add_f32_e32 v16, v148, v149
	v_add_f32_e32 v17, v150, v151
	v_add_f32_e32 v16, v16, v17
	v_fmamk_f32 v16, v16, 0x3baaaaab, v213
	v_mul_f32_e32 v17, 0x4f800000, v16
	v_cmp_gt_f32_e32 vcc, s90, v16
	s_nop 1
	v_cndmask_b32_e32 v16, v16, v17, vcc
	v_sqrt_f32_e32 v17, v16
	s_nop 0
	v_add_u32_e32 v18, -1, v17
	v_fma_f32 v19, -v18, v17, v16
	v_cmp_ge_f32_e64 s[12:13], 0, v19
	v_add_u32_e32 v19, 1, v17
	s_nop 0
	v_cndmask_b32_e64 v18, v17, v18, s[12:13]
	v_fma_f32 v17, -v19, v17, v16
	v_cmp_lt_f32_e64 s[12:13], 0, v17
	s_nop 1
	v_cndmask_b32_e64 v17, v18, v19, s[12:13]
	v_mul_f32_e32 v18, 0x37800000, v17
	v_cndmask_b32_e32 v17, v17, v18, vcc
	v_cmp_class_f32_e32 vcc, v16, v215
	s_nop 1
	v_cndmask_b32_e32 v16, v17, v16, vcc
	v_rcp_f32_e32 v18, v16
	s_nop 0
	v_mul_f32_e32 v17, 1.0, v18
	v_mov_b32_e32 v22, v17
	v_add3_u32 v18, s48, v227, 48
	v_mov_b64_e32 v[16:17], s[60:61]
	v_mad_i64_i32 v[16:17], s[12:13], v18, s91, v[16:17]
	v_mul_f32_e32 v20, v210, v22
	v_lshl_add_u64 v[16:17], s[58:59], 1, v[16:17]
	v_lshl_add_u64 v[16:17], v[16:17], 0, s[34:35]
	v_pk_mul_f32 v[12:13], v[12:13], v[20:21] op_sel_hi:[1,0]
	v_pk_mul_f32 v[8:9], v[8:9], v[20:21] op_sel_hi:[1,0]
	v_ashrrev_i32_e32 v19, 31, v18
	v_lshl_add_u64 v[16:17], v[208:209], 1, v[16:17]
	v_pk_mul_f32 v[14:15], v[14:15], v[20:21] op_sel_hi:[1,0]
	v_pk_mul_f32 v[12:13], v[136:137], v[12:13]
	v_pk_mul_f32 v[10:11], v[10:11], v[20:21] op_sel_hi:[1,0]
	v_pk_mul_f32 v[8:9], v[8:9], v[140:141]
	s_and_b64 vcc, exec, s[10:11]
	v_pk_mul_f32 v[14:15], v[138:139], v[14:15]
	v_cvt_pk_bf16_f32 v12, v12, v13
	v_pk_mul_f32 v[10:11], v[10:11], v[142:143]
	v_cvt_pk_bf16_f32 v13, v14, v15
	global_store_dwordx2 v[16:17], v[12:13], off
	v_cvt_pk_bf16_f32 v8, v8, v9
	v_cvt_pk_bf16_f32 v9, v10, v11
	global_store_dwordx2 v[16:17], v[8:9], off offset:32
	s_cbranch_vccnz .LBB0_582
	v_lshlrev_b64 v[8:9], 11, v[18:19]
	v_lshl_add_u64 v[8:9], s[40:41], 0, v[8:9]
	v_lshl_add_u64 v[8:9], s[26:27], 1, v[8:9]
	v_lshl_add_u64 v[8:9], v[8:9], 0, s[34:35]
	v_pk_mul_f32 v[12:13], v[4:5], v[210:211] op_sel_hi:[1,0]
	v_lshl_add_u64 v[8:9], v[208:209], 1, v[8:9]
	v_pk_mul_f32 v[10:11], v[6:7], v[210:211] op_sel_hi:[1,0]
	v_cvt_pk_bf16_f32 v12, v12, v13
	s_nop 0
	v_cvt_pk_bf16_f32 v13, v10, v11
	global_store_dwordx2 v[8:9], v[12:13], off
	v_pk_mul_f32 v[12:13], v[0:1], v[210:211] op_sel_hi:[1,0]
	v_pk_mul_f32 v[10:11], v[2:3], v[210:211] op_sel_hi:[1,0]
	v_cvt_pk_bf16_f32 v12, v12, v13
	s_nop 0
	v_cvt_pk_bf16_f32 v13, v10, v11
	global_store_dwordx2 v[8:9], v[12:13], off offset:32

.LBB0_587:
	v_pk_mul_f32 v[0:1], v[118:119], v[14:15]
	v_pk_mul_f32 v[2:3], v[116:117], v[12:13]
	v_pk_mul_f32 v[6:7], v[114:115], v[10:11]
	v_pk_mul_f32 v[4:5], v[112:113], v[8:9]
	v_cmp_gt_i32_e32 vcc, s76, v18
	s_and_saveexec_b64 s[6:7], vcc
	s_cbranch_execz .LBB0_589
	s_waitcnt vmcnt(4)
	v_mul_f32_e32 v14, v145, v0
	v_mul_f32_e32 v20, v144, v0
	v_mov_b32_e32 v0, v7
	v_mov_b32_e32 v9, v130
	v_mov_b32_e32 v130, v129
	v_mul_f32_e32 v12, v144, v6
	v_mul_f32_e32 v18, v145, v6
	v_pk_mul_f32 v[22:23], v[134:135], v[0:1]
	v_mov_b32_e32 v6, v1
	v_mov_b32_e32 v8, v128
	v_pk_mul_f32 v[10:11], v[130:131], v[2:3]
	v_mov_b32_e32 v13, v22
	v_mov_b32_e32 v15, v23
	v_pk_mul_f32 v[0:1], v[134:135], v[6:7]
	v_pk_mul_f32 v[2:3], v[8:9], v[2:3]
	v_pk_fma_f32 v[8:9], v[8:9], v[4:5], v[10:11] neg_lo:[0,0,1] neg_hi:[0,0,1]
	v_pk_add_f32 v[10:11], v[12:13], v[14:15] neg_lo:[0,1] neg_hi:[0,1]
	v_mov_b32_e32 v19, v1
	v_mov_b32_e32 v21, v0
	v_pk_fma_f32 v[2:3], v[130:131], v[4:5], v[2:3]
	v_pk_add_f32 v[0:1], v[18:19], v[20:21]
	v_mov_b32_e32 v4, v8
	v_mov_b32_e32 v5, v9
	v_mov_b32_e32 v6, v10
	v_mov_b32_e32 v7, v11

.LBB0_609:
	s_or_b64 exec, exec, s[8:9]
	s_lshl_b32 s8, s43, 5
	s_and_b32 s44, s8, 0xffffff80
	v_add_u32_e32 v0, s44, v108
	v_mov_b64_e32 v[16:17], s[16:17]
	s_waitcnt lgkmcnt(0)
	v_mad_i64_i32 v[0:1], s[8:9], v0, s40, v[16:17]
	s_lshl_b32 s24, s18, 8
	s_mov_b32 s25, s19
	v_lshl_add_u64 v[0:1], v[0:1], 0, s[24:25]
	v_mov_b32_e32 v83, v79
	v_lshl_add_u64 v[18:19], v[0:1], 0, v[82:83]
	global_load_dwordx4 v[12:15], v[18:19], off offset:3200
	global_load_dwordx4 v[8:11], v[18:19], off offset:3216
	global_load_dwordx4 v[0:3], v[18:19], off offset:3248
	global_load_dwordx4 v[4:7], v[18:19], off offset:3232
	s_lshl_b32 s18, s18, 7
	v_mov_b32_e32 v85, v79
	s_mov_b32 s23, s19
	s_waitcnt vmcnt(3)
	v_lshlrev_b32_e32 v18, 16, v12
	v_and_b32_e32 v12, 0xffff0000, v12
	v_lshlrev_b32_e32 v20, 16, v13
	v_and_b32_e32 v21, 0xffff0000, v13
	v_mul_f32_e32 v13, 0x3d372713, v18
	v_mul_f32_e32 v19, 0x3d372713, v12
	v_mul_f32_e32 v13, v13, v18
	v_mul_f32_e32 v23, 0x3d372713, v20
	v_mul_f32_e32 v19, v19, v12
	v_fma_f32 v13, v13, v18, v18
	v_mul_f32_e32 v23, v23, v20
	v_fma_f32 v19, v19, v12, v12
	v_mul_f32_e32 v13, 0x3f4c422a, v13
	v_fma_f32 v23, v23, v20, v20
	v_mul_f32_e32 v19, 0x3f4c422a, v19
	v_mul_f32_e32 v13, -2.0, v13
	v_mul_f32_e32 v23, 0x3f4c422a, v23
	v_mul_f32_e32 v19, -2.0, v19
	v_mul_f32_e32 v13, 0x3fb8aa3b, v13
	v_mul_f32_e32 v23, -2.0, v23
	v_mul_f32_e32 v19, 0x3fb8aa3b, v19
	v_exp_f32_e32 v13, v13
	v_mul_f32_e32 v23, 0x3fb8aa3b, v23
	v_exp_f32_e32 v19, v19
	v_mul_f32_e32 v24, 0x3d372713, v21
	v_exp_f32_e32 v23, v23
	v_mul_f32_e32 v24, v24, v21
	v_fma_f32 v24, v24, v21, v21
	v_add_f32_e32 v13, 1.0, v13
	v_mul_f32_e32 v24, 0x3f4c422a, v24
	v_add_f32_e32 v26, 1.0, v19
	v_mul_f32_e32 v24, -2.0, v24
	v_add_f32_e32 v23, 1.0, v23
	v_div_scale_f32 v28, s[8:9], v26, v26, v12
	v_rcp_f32_e32 v34, v13
	v_mul_f32_e32 v24, 0x3fb8aa3b, v24
	v_div_scale_f32 v30, s[10:11], v23, v23, v20
	v_rcp_f32_e32 v35, v28
	v_lshlrev_b32_e32 v22, 16, v14
	v_exp_f32_e32 v24, v24
	v_rcp_f32_e32 v36, v30
	v_mul_f32_e32 v25, 0x3d372713, v22
	v_mul_f32_e32 v25, v25, v22
	v_fma_f32 v25, v25, v22, v22
	v_fma_f32 v39, -v28, v35, 1.0
	v_mul_f32_e32 v25, 0x3f4c422a, v25
	v_add_f32_e32 v24, 1.0, v24
	v_div_scale_f32 v29, s[8:9], v12, v26, v12
	v_fma_f32 v40, -v30, v36, 1.0
	v_fmac_f32_e32 v35, v39, v35
	v_mul_f32_e32 v25, -2.0, v25
	v_div_scale_f32 v31, s[10:11], v20, v23, v20
	v_div_scale_f32 v32, s[12:13], v24, v24, v21
	v_fmac_f32_e32 v36, v40, v36
	v_mul_f32_e32 v39, v29, v35
	v_mul_f32_e32 v25, 0x3fb8aa3b, v25
	v_rcp_f32_e32 v37, v32
	v_mul_f32_e32 v40, v31, v36
	v_fma_f32 v43, -v28, v39, v29
	v_exp_f32_e32 v25, v25
	v_fma_f32 v44, -v30, v40, v31
	v_fmac_f32_e32 v39, v43, v35
	v_fmac_f32_e32 v40, v44, v36
	v_fma_f32 v27, -v28, v39, v29
	v_mul_f32_e32 v19, v18, v34
	s_mov_b64 vcc, s[8:9]
	v_fma_f32 v28, -v30, v40, v31
	v_div_fmas_f32 v13, v27, v35, v39
	s_mov_b64 vcc, s[10:11]
	v_fma_f32 v41, -v32, v37, 1.0
	v_div_fixup_f32 v13, v13, v26, v12
	v_div_fmas_f32 v12, v28, v36, v40
	v_div_scale_f32 v33, s[12:13], v21, v24, v21
	v_fmac_f32_e32 v37, v41, v37
	v_div_fixup_f32 v12, v12, v23, v20
	v_add_f32_e32 v20, 1.0, v25
	v_and_b32_e32 v26, 0xffff0000, v14
	v_mul_f32_e32 v41, v33, v37
	v_mul_f32_e32 v14, 0x3d372713, v26
	v_fma_f32 v45, -v32, v41, v33
	v_rcp_f32_e32 v25, v20
	v_mul_f32_e32 v14, v14, v26
	v_fmac_f32_e32 v41, v45, v37
	v_fma_f32 v14, v14, v26, v26
	v_fma_f32 v29, -v32, v41, v33
	s_mov_b64 vcc, s[12:13]
	v_mul_f32_e32 v14, 0x3f4c422a, v14
	v_div_fmas_f32 v18, v29, v37, v41
	v_mul_f32_e32 v14, -2.0, v14
	v_div_fixup_f32 v18, v18, v24, v21
	v_mul_f32_e32 v14, 0x3fb8aa3b, v14
	v_exp_f32_e32 v14, v14
	s_nop 0
	v_add_f32_e32 v23, 1.0, v14
	v_mul_f32_e32 v14, v22, v25
	v_rcp_f32_e32 v28, v23
	v_lshlrev_b32_e32 v22, 16, v15
	v_mul_f32_e32 v24, 0x3d372713, v22
	v_mul_f32_e32 v24, v24, v22
	v_fma_f32 v24, v24, v22, v22
	v_mul_f32_e32 v24, 0x3f4c422a, v24
	v_mul_f32_e32 v24, -2.0, v24
	v_mul_f32_e32 v24, 0x3fb8aa3b, v24
	v_exp_f32_e32 v24, v24
	v_mul_f32_e32 v20, v26, v28
	v_add_f32_e32 v24, 1.0, v24
	v_and_b32_e32 v26, 0xffff0000, v15
	v_mul_f32_e32 v15, 0x3d372713, v26
	v_rcp_f32_e32 v27, v24
	v_mul_f32_e32 v15, v15, v26
	v_fma_f32 v15, v15, v26, v26
	v_mul_f32_e32 v15, 0x3f4c422a, v15
	v_mul_f32_e32 v15, -2.0, v15
	v_mul_f32_e32 v15, 0x3fb8aa3b, v15
	v_exp_f32_e32 v15, v15
	s_nop 0
	v_add_f32_e32 v25, 1.0, v15
	v_rcp_f32_e32 v29, v25
	v_mul_f32_e32 v15, v22, v27
	s_waitcnt vmcnt(2)
	v_lshlrev_b32_e32 v23, 16, v8
	v_mul_f32_e32 v24, 0x3d372713, v23
	v_mul_f32_e32 v24, v24, v23
	v_fma_f32 v24, v24, v23, v23
	v_mul_f32_e32 v24, 0x3f4c422a, v24
	v_mul_f32_e32 v24, -2.0, v24
	v_mul_f32_e32 v24, 0x3fb8aa3b, v24
	v_exp_f32_e32 v24, v24
	v_mul_f32_e32 v21, v26, v29
	v_add_f32_e32 v24, 1.0, v24
	v_and_b32_e32 v26, 0xffff0000, v8
	v_mul_f32_e32 v8, 0x3d372713, v26
	v_rcp_f32_e32 v28, v24
	v_mul_f32_e32 v8, v8, v26
	v_fma_f32 v8, v8, v26, v26
	v_mul_f32_e32 v8, 0x3f4c422a, v8
	v_mul_f32_e32 v8, -2.0, v8
	v_mul_f32_e32 v8, 0x3fb8aa3b, v8
	v_exp_f32_e32 v8, v8
	s_nop 0
	v_add_f32_e32 v27, 1.0, v8
	v_mul_f32_e32 v8, v23, v28
	v_rcp_f32_e32 v30, v27
	v_lshlrev_b32_e32 v24, 16, v9
	v_mul_f32_e32 v25, 0x3d372713, v24
	v_mul_f32_e32 v25, v25, v24
	v_fma_f32 v25, v25, v24, v24
	v_mul_f32_e32 v25, 0x3f4c422a, v25
	v_mul_f32_e32 v25, -2.0, v25
	v_mul_f32_e32 v25, 0x3fb8aa3b, v25
	v_exp_f32_e32 v25, v25
	v_mul_f32_e32 v22, v26, v30
	v_add_f32_e32 v25, 1.0, v25
	v_and_b32_e32 v27, 0xffff0000, v9
	v_mul_f32_e32 v9, 0x3d372713, v27
	v_rcp_f32_e32 v29, v25
	v_mul_f32_e32 v9, v9, v27
	v_fma_f32 v9, v9, v27, v27
	v_mul_f32_e32 v9, 0x3f4c422a, v9
	v_mul_f32_e32 v9, -2.0, v9
	v_mul_f32_e32 v9, 0x3fb8aa3b, v9
	v_exp_f32_e32 v9, v9
	s_nop 0
	v_add_f32_e32 v28, 1.0, v9
	v_mul_f32_e32 v9, v24, v29
	v_rcp_f32_e32 v31, v28
	v_lshlrev_b32_e32 v25, 16, v10
	v_mul_f32_e32 v26, 0x3d372713, v25
	v_mul_f32_e32 v26, v26, v25
	v_fma_f32 v26, v26, v25, v25
	v_mul_f32_e32 v26, 0x3f4c422a, v26
	v_mul_f32_e32 v26, -2.0, v26
	v_mul_f32_e32 v26, 0x3fb8aa3b, v26
	v_exp_f32_e32 v26, v26
	v_mul_f32_e32 v23, v27, v31
	v_add_f32_e32 v26, 1.0, v26
	v_and_b32_e32 v28, 0xffff0000, v10
	v_mul_f32_e32 v10, 0x3d372713, v28
	v_rcp_f32_e32 v30, v26
	v_mul_f32_e32 v10, v10, v28
	v_fma_f32 v10, v10, v28, v28
	v_mul_f32_e32 v10, 0x3f4c422a, v10
	v_mul_f32_e32 v10, -2.0, v10
	v_mul_f32_e32 v10, 0x3fb8aa3b, v10
	v_exp_f32_e32 v10, v10
	s_nop 0
	v_add_f32_e32 v29, 1.0, v10
	v_mul_f32_e32 v10, v25, v30
	v_rcp_f32_e32 v32, v29
	v_lshlrev_b32_e32 v26, 16, v11
	v_mul_f32_e32 v27, 0x3d372713, v26
	v_mul_f32_e32 v27, v27, v26
	v_fma_f32 v27, v27, v26, v26
	v_mul_f32_e32 v27, 0x3f4c422a, v27
	v_mul_f32_e32 v27, -2.0, v27
	v_mul_f32_e32 v27, 0x3fb8aa3b, v27
	v_exp_f32_e32 v27, v27
	v_mul_f32_e32 v24, v28, v32
	v_add_f32_e32 v27, 1.0, v27
	v_and_b32_e32 v29, 0xffff0000, v11
	v_mul_f32_e32 v11, 0x3d372713, v29
	v_rcp_f32_e32 v31, v27
	v_mul_f32_e32 v11, v11, v29
	v_fma_f32 v11, v11, v29, v29
	v_mul_f32_e32 v11, 0x3f4c422a, v11
	v_mul_f32_e32 v11, -2.0, v11
	v_mul_f32_e32 v11, 0x3fb8aa3b, v11
	v_exp_f32_e32 v11, v11
	s_nop 0
	v_add_f32_e32 v30, 1.0, v11
	v_mul_f32_e32 v11, v26, v31
	v_rcp_f32_e32 v33, v30
	s_waitcnt vmcnt(0)
	v_lshlrev_b32_e32 v27, 16, v4
	v_mul_f32_e32 v28, 0x3d372713, v27
	v_mul_f32_e32 v28, v28, v27
	v_fma_f32 v28, v28, v27, v27
	v_mul_f32_e32 v28, 0x3f4c422a, v28
	v_mul_f32_e32 v28, -2.0, v28
	v_mul_f32_e32 v28, 0x3fb8aa3b, v28
	v_exp_f32_e32 v28, v28
	v_mul_f32_e32 v25, v29, v33
	v_add_f32_e32 v28, 1.0, v28
	v_and_b32_e32 v30, 0xffff0000, v4
	v_mul_f32_e32 v4, 0x3d372713, v30
	v_rcp_f32_e32 v32, v28
	v_mul_f32_e32 v4, v4, v30
	v_fma_f32 v4, v4, v30, v30
	v_mul_f32_e32 v4, 0x3f4c422a, v4
	v_mul_f32_e32 v4, -2.0, v4
	v_mul_f32_e32 v4, 0x3fb8aa3b, v4
	v_exp_f32_e32 v4, v4
	s_nop 0
	v_add_f32_e32 v31, 1.0, v4
	v_mul_f32_e32 v4, v27, v32
	v_rcp_f32_e32 v34, v31
	v_lshlrev_b32_e32 v28, 16, v5
	v_mul_f32_e32 v29, 0x3d372713, v28
	v_mul_f32_e32 v29, v29, v28
	v_fma_f32 v29, v29, v28, v28
	v_mul_f32_e32 v29, 0x3f4c422a, v29
	v_mul_f32_e32 v29, -2.0, v29
	v_mul_f32_e32 v29, 0x3fb8aa3b, v29
	v_exp_f32_e32 v29, v29
	v_mul_f32_e32 v26, v30, v34
	v_add_f32_e32 v29, 1.0, v29
	v_and_b32_e32 v31, 0xffff0000, v5
	v_mul_f32_e32 v5, 0x3d372713, v31
	v_rcp_f32_e32 v33, v29
	v_mul_f32_e32 v5, v5, v31
	v_fma_f32 v5, v5, v31, v31
	v_mul_f32_e32 v5, 0x3f4c422a, v5
	v_mul_f32_e32 v5, -2.0, v5
	v_mul_f32_e32 v5, 0x3fb8aa3b, v5
	v_exp_f32_e32 v5, v5
	s_nop 0
	v_add_f32_e32 v32, 1.0, v5
	v_mul_f32_e32 v5, v28, v33
	v_rcp_f32_e32 v35, v32
	v_lshlrev_b32_e32 v29, 16, v6
	v_mul_f32_e32 v30, 0x3d372713, v29
	v_mul_f32_e32 v30, v30, v29
	v_fma_f32 v30, v30, v29, v29
	v_mul_f32_e32 v30, 0x3f4c422a, v30
	v_mul_f32_e32 v30, -2.0, v30
	v_mul_f32_e32 v30, 0x3fb8aa3b, v30
	v_exp_f32_e32 v30, v30
	v_mul_f32_e32 v27, v31, v35
	v_add_f32_e32 v30, 1.0, v30
	v_and_b32_e32 v32, 0xffff0000, v6
	v_mul_f32_e32 v6, 0x3d372713, v32
	v_rcp_f32_e32 v34, v30
	v_mul_f32_e32 v6, v6, v32
	v_fma_f32 v6, v6, v32, v32
	v_mul_f32_e32 v6, 0x3f4c422a, v6
	v_mul_f32_e32 v6, -2.0, v6
	v_mul_f32_e32 v6, 0x3fb8aa3b, v6
	v_exp_f32_e32 v6, v6
	s_nop 0
	v_add_f32_e32 v33, 1.0, v6
	v_mul_f32_e32 v6, v29, v34
	v_rcp_f32_e32 v36, v33
	v_lshlrev_b32_e32 v30, 16, v7
	v_mul_f32_e32 v31, 0x3d372713, v30
	v_mul_f32_e32 v31, v31, v30
	v_fma_f32 v31, v31, v30, v30
	v_mul_f32_e32 v31, 0x3f4c422a, v31
	v_mul_f32_e32 v31, -2.0, v31
	v_mul_f32_e32 v31, 0x3fb8aa3b, v31
	v_exp_f32_e32 v31, v31
	v_mul_f32_e32 v28, v32, v36
	v_add_f32_e32 v31, 1.0, v31
	v_and_b32_e32 v33, 0xffff0000, v7
	v_mul_f32_e32 v7, 0x3d372713, v33
	v_rcp_f32_e32 v35, v31
	v_mul_f32_e32 v7, v7, v33
	v_fma_f32 v7, v7, v33, v33
	v_mul_f32_e32 v7, 0x3f4c422a, v7
	v_mul_f32_e32 v7, -2.0, v7
	v_mul_f32_e32 v7, 0x3fb8aa3b, v7
	v_exp_f32_e32 v7, v7
	s_nop 0
	v_add_f32_e32 v34, 1.0, v7
	v_mul_f32_e32 v7, v30, v35
	v_rcp_f32_e32 v37, v34
	v_lshlrev_b32_e32 v31, 16, v0
	v_mul_f32_e32 v32, 0x3d372713, v31
	v_mul_f32_e32 v32, v32, v31
	v_fma_f32 v32, v32, v31, v31
	v_mul_f32_e32 v32, 0x3f4c422a, v32
	v_mul_f32_e32 v32, -2.0, v32
	v_mul_f32_e32 v32, 0x3fb8aa3b, v32
	v_exp_f32_e32 v32, v32
	v_mul_f32_e32 v29, v33, v37
	v_add_f32_e32 v32, 1.0, v32
	v_and_b32_e32 v34, 0xffff0000, v0
	v_mul_f32_e32 v0, 0x3d372713, v34
	v_rcp_f32_e32 v36, v32
	v_mul_f32_e32 v0, v0, v34
	v_fma_f32 v0, v0, v34, v34
	v_mul_f32_e32 v0, 0x3f4c422a, v0
	v_mul_f32_e32 v0, -2.0, v0
	v_mul_f32_e32 v0, 0x3fb8aa3b, v0
	v_exp_f32_e32 v0, v0
	s_nop 0
	v_add_f32_e32 v35, 1.0, v0
	v_mul_f32_e32 v0, v31, v36
	v_rcp_f32_e32 v38, v35
	v_lshlrev_b32_e32 v32, 16, v1
	v_mul_f32_e32 v33, 0x3d372713, v32
	v_mul_f32_e32 v33, v33, v32
	v_fma_f32 v33, v33, v32, v32
	v_mul_f32_e32 v33, 0x3f4c422a, v33
	v_mul_f32_e32 v33, -2.0, v33
	v_mul_f32_e32 v33, 0x3fb8aa3b, v33
	v_exp_f32_e32 v33, v33
	v_mul_f32_e32 v30, v34, v38
	v_add_f32_e32 v33, 1.0, v33
	v_and_b32_e32 v35, 0xffff0000, v1
	v_mul_f32_e32 v1, 0x3d372713, v35
	v_rcp_f32_e32 v37, v33
	v_mul_f32_e32 v1, v1, v35
	v_fma_f32 v1, v1, v35, v35
	v_mul_f32_e32 v1, 0x3f4c422a, v1
	v_mul_f32_e32 v1, -2.0, v1
	v_mul_f32_e32 v1, 0x3fb8aa3b, v1
	v_exp_f32_e32 v1, v1
	s_nop 0
	v_add_f32_e32 v36, 1.0, v1
	v_mul_f32_e32 v1, v32, v37
	v_rcp_f32_e32 v39, v36
	v_lshlrev_b32_e32 v33, 16, v2
	v_mul_f32_e32 v34, 0x3d372713, v33
	v_mul_f32_e32 v34, v34, v33
	v_fma_f32 v34, v34, v33, v33
	v_mul_f32_e32 v34, 0x3f4c422a, v34
	v_mul_f32_e32 v34, -2.0, v34
	v_mul_f32_e32 v34, 0x3fb8aa3b, v34
	v_exp_f32_e32 v34, v34
	v_mul_f32_e32 v31, v35, v39
	v_add_f32_e32 v34, 1.0, v34
	v_and_b32_e32 v36, 0xffff0000, v2
	v_mul_f32_e32 v2, 0x3d372713, v36
	v_rcp_f32_e32 v38, v34
	v_mul_f32_e32 v2, v2, v36
	v_fma_f32 v2, v2, v36, v36
	v_mul_f32_e32 v2, 0x3f4c422a, v2
	v_mul_f32_e32 v2, -2.0, v2
	v_mul_f32_e32 v2, 0x3fb8aa3b, v2
	v_exp_f32_e32 v2, v2
	s_nop 0
	v_add_f32_e32 v37, 1.0, v2
	v_rcp_f32_e32 v40, v37
	v_mul_f32_e32 v2, v33, v38
	v_lshlrev_b32_e32 v34, 16, v3
	v_mul_f32_e32 v35, 0x3d372713, v34
	v_mul_f32_e32 v35, v35, v34
	v_fma_f32 v35, v35, v34, v34
	v_mul_f32_e32 v35, 0x3f4c422a, v35
	v_mul_f32_e32 v35, -2.0, v35
	v_mul_f32_e32 v35, 0x3fb8aa3b, v35
	v_exp_f32_e32 v35, v35
	v_mul_f32_e32 v32, v36, v40
	v_and_b32_e32 v3, 0xffff0000, v3
	v_mov_b32_e32 v56, v32
	v_mul_f32_e32 v36, 0x3d372713, v3
	v_add_f32_e32 v35, 1.0, v35
	v_mul_f32_e32 v36, v36, v3
	v_fma_f32 v36, v36, v3, v3
	v_rcp_f32_e32 v39, v35
	v_mul_f32_e32 v36, 0x3f4c422a, v36
	v_mul_f32_e32 v36, -2.0, v36
	v_mul_f32_e32 v36, 0x3fb8aa3b, v36
	v_exp_f32_e32 v36, v36
	s_nop 0
	v_add_f32_e32 v36, 1.0, v36
	v_rcp_f32_e32 v38, v36
	v_mul_f32_e32 v32, v34, v39
	v_mov_b32_e32 v57, v32
	v_mul_f32_e32 v40, v13, v13
	v_mul_f32_e32 v32, v3, v38
	v_mov_b32_e32 v3, v32
	v_or_b32_e32 v32, s18, v76
	v_lshlrev_b32_e32 v58, 2, v32
	global_load_dwordx4 v[32:35], v58, s[28:29]
	global_load_dwordx4 v[36:39], v58, s[28:29] offset:16
	v_fmac_f32_e32 v40, v19, v19
	v_fmac_f32_e32 v40, v12, v12
	v_fmac_f32_e32 v40, v18, v18
	v_fmac_f32_e32 v40, v14, v14
	v_fmac_f32_e32 v40, v20, v20
	v_fmac_f32_e32 v40, v15, v15
	v_fmac_f32_e32 v40, v21, v21
	v_fmac_f32_e32 v40, v8, v8
	v_fmac_f32_e32 v40, v22, v22
	v_fmac_f32_e32 v40, v9, v9
	v_fmac_f32_e32 v40, v23, v23
	v_fmac_f32_e32 v40, v10, v10
	v_fmac_f32_e32 v40, v24, v24
	v_fmac_f32_e32 v40, v11, v11
	v_fmac_f32_e32 v40, v25, v25
	v_fmac_f32_e32 v40, v4, v4
	v_fmac_f32_e32 v40, v26, v26
	v_fmac_f32_e32 v40, v5, v5
	v_fmac_f32_e32 v40, v27, v27
	v_fmac_f32_e32 v40, v6, v6
	v_fmac_f32_e32 v40, v28, v28
	v_fmac_f32_e32 v40, v7, v7
	v_fmac_f32_e32 v40, v29, v29
	v_fmac_f32_e32 v40, v0, v0
	v_fmac_f32_e32 v40, v30, v30
	v_fmac_f32_e32 v40, v1, v1
	v_fmac_f32_e32 v40, v31, v31
	v_fmac_f32_e32 v40, v2, v2
	v_fmac_f32_e32 v40, v56, v56
	v_cmp_lt_i32_e32 vcc, v133, v134
	v_fmac_f32_e32 v40, v57, v57
	v_fmac_f32_e32 v40, v3, v3
	v_cndmask_b32_e32 v41, v104, v133, vcc
	v_lshlrev_b32_e32 v41, 2, v41
	ds_bpermute_b32 v41, v41, v40
	v_cmp_lt_i32_e32 vcc, v135, v134
	s_and_b32 s10, s43, 0x7fffffc
	s_add_i32 s10, s10, s35
	v_lshl_or_b32 v98, s10, 5, v109
	s_waitcnt lgkmcnt(0)
	v_add_f32_e32 v44, v40, v41
	v_cndmask_b32_e32 v40, v104, v135, vcc
	v_lshlrev_b32_e32 v45, 2, v40
	ds_bpermute_b32 v45, v45, v44
	global_load_dwordx4 v[40:43], v58, s[28:29] offset:32
	v_ashrrev_i32_e32 v99, 31, v98
	s_waitcnt lgkmcnt(0)
	v_add_f32_e32 v44, v44, v45
	v_fmamk_f32 v44, v44, 0x3c000000, v136
	v_mul_f32_e32 v45, 0x4f800000, v44
	v_cmp_gt_f32_e32 vcc, s41, v44
	s_nop 1
	v_cndmask_b32_e32 v48, v44, v45, vcc
	v_sqrt_f32_e32 v49, v48
	global_load_dwordx4 v[44:47], v58, s[28:29] offset:48
	v_add_u32_e32 v50, -1, v49
	v_fma_f32 v51, -v50, v49, v48
	v_cmp_ge_f32_e64 s[8:9], 0, v51
	v_add_u32_e32 v51, 1, v49
	s_nop 0
	v_cndmask_b32_e64 v50, v49, v50, s[8:9]
	v_fma_f32 v49, -v51, v49, v48
	v_cmp_lt_f32_e64 s[8:9], 0, v49
	s_nop 1
	v_cndmask_b32_e64 v49, v50, v51, s[8:9]
	v_mul_f32_e32 v50, 0x37800000, v49
	v_cndmask_b32_e32 v49, v49, v50, vcc
	v_cmp_class_f32_e32 vcc, v48, v137
	s_nop 1
	v_cndmask_b32_e32 v52, v49, v48, vcc
	v_rcp_f32_e32 v54, v52
	global_load_dwordx4 v[48:51], v58, s[28:29] offset:64
	v_mul_f32_e32 v53, 1.0, v54
	v_mov_b32_e32 v59, v53
	v_mul_f32_e32 v12, v12, v59
	s_waitcnt vmcnt(4)
	v_mul_f32_e32 v12, v34, v12
	v_cvt_pk_bf16_f32 v12, v12, v12
	ds_write_b16 v138, v12 offset:35360
	v_mul_f32_e32 v12, v18, v59
	v_mul_f32_e32 v12, v35, v12
	v_mul_f32_e32 v19, v19, v59
	v_mul_f32_e32 v13, v13, v59
	v_cvt_pk_bf16_f32 v12, v12, v12
	v_mul_f32_e32 v19, v32, v19
	v_mul_f32_e32 v13, v33, v13
	ds_write_b16 v138, v12 offset:35632
	v_mul_f32_e32 v12, v14, v59
	global_load_dwordx4 v[32:35], v58, s[28:29] offset:96
	s_waitcnt vmcnt(4)
	v_mul_f32_e32 v12, v36, v12
	v_cvt_pk_bf16_f32 v12, v12, v12
	ds_write_b16 v138, v12 offset:35904
	v_mul_f32_e32 v12, v20, v59
	v_mul_f32_e32 v12, v37, v12
	global_load_dwordx4 v[52:55], v58, s[28:29] offset:80
	v_cvt_pk_bf16_f32 v12, v12, v12
	ds_write_b16 v138, v12 offset:36176
	v_mul_f32_e32 v12, v15, v59
	v_mul_f32_e32 v12, v38, v12
	v_cvt_pk_bf16_f32 v12, v12, v12
	ds_write_b16 v138, v12 offset:36448
	v_mul_f32_e32 v12, v21, v59
	v_mul_f32_e32 v12, v39, v12
	v_cvt_pk_bf16_f32 v13, v13, v13
	v_cvt_pk_bf16_f32 v12, v12, v12
	ds_write_b16 v138, v13 offset:35088
	ds_write_b16 v138, v12 offset:36720
	global_load_dwordx4 v[12:15], v58, s[28:29] offset:112
	v_mul_f32_e32 v4, v4, v59
	v_mul_f32_e32 v0, v0, v59
	v_mul_f32_e32 v8, v8, v59
	s_waitcnt vmcnt(5)
	v_mul_f32_e32 v8, v40, v8
	v_cvt_pk_bf16_f32 v8, v8, v8
	ds_write_b16 v138, v8 offset:36992
	v_mul_f32_e32 v8, v22, v59
	v_add_u32_e32 v20, s44, v118
	v_mul_f32_e32 v8, v41, v8
	v_mad_i64_i32 v[20:21], s[8:9], v20, s40, v[16:17]
	v_cvt_pk_bf16_f32 v8, v8, v8
	v_lshl_add_u64 v[20:21], v[20:21], 0, s[24:25]
	ds_write_b16 v138, v8 offset:37264
	v_mul_f32_e32 v8, v9, v59
	v_lshl_add_u64 v[20:21], v[20:21], 0, v[84:85]
	v_mul_f32_e32 v8, v42, v8
	v_cvt_pk_bf16_f32 v8, v8, v8
	ds_write_b16 v138, v8 offset:37536
	v_mul_f32_e32 v8, v23, v59
	v_mul_f32_e32 v8, v43, v8
	v_cvt_pk_bf16_f32 v8, v8, v8
	ds_write_b16 v138, v8 offset:37808
	v_mul_f32_e32 v8, v10, v59
	s_waitcnt vmcnt(4)
	v_mul_f32_e32 v8, v44, v8
	v_cvt_pk_bf16_f32 v8, v8, v8
	ds_write_b16 v138, v8 offset:38080
	v_mul_f32_e32 v8, v24, v59
	v_mul_f32_e32 v8, v45, v8
	v_cvt_pk_bf16_f32 v8, v8, v8
	ds_write_b16 v138, v8 offset:38352
	v_mul_f32_e32 v8, v11, v59
	v_mul_f32_e32 v8, v46, v8
	v_cvt_pk_bf16_f32 v8, v8, v8
	s_waitcnt vmcnt(3)
	v_mul_f32_e32 v4, v4, v48
	v_cvt_pk_bf16_f32 v4, v4, v4
	ds_write_b16 v138, v4 offset:39168
	v_mul_f32_e32 v4, v26, v59
	v_mul_f32_e32 v4, v4, v49
	v_cvt_pk_bf16_f32 v4, v4, v4
	ds_write_b16 v138, v4 offset:39440
	v_mul_f32_e32 v4, v5, v59
	v_mul_f32_e32 v4, v4, v50
	v_cvt_pk_bf16_f32 v4, v4, v4
	ds_write_b16 v138, v4 offset:39712
	v_mul_f32_e32 v4, v27, v59
	v_mul_f32_e32 v4, v4, v51
	v_cvt_pk_bf16_f32 v4, v4, v4
	ds_write_b16 v138, v4 offset:39984
	v_mul_f32_e32 v4, v6, v59
	v_lshl_add_u64 v[26:27], v[20:21], 0, s[22:23]
	v_add_u32_e32 v20, s44, v119
	v_mad_i64_i32 v[20:21], s[8:9], v20, s40, v[16:17]
	v_lshl_add_u64 v[20:21], v[20:21], 0, s[24:25]
	v_lshl_add_u64 v[20:21], v[20:21], 0, v[84:85]
	ds_write_b16 v138, v8 offset:38624
	v_mul_f32_e32 v8, v25, v59
	v_mul_f32_e32 v8, v8, v47
	v_cvt_pk_bf16_f32 v19, v19, v19
	s_waitcnt vmcnt(2)
	v_mul_f32_e32 v0, v0, v32
	v_cvt_pk_bf16_f32 v0, v0, v0
	ds_write_b16 v138, v0 offset:41344
	v_mul_f32_e32 v0, v30, v59
	v_mul_f32_e32 v0, v0, v33
	v_cvt_pk_bf16_f32 v0, v0, v0
	s_waitcnt vmcnt(1)
	v_mul_f32_e32 v4, v4, v52
	ds_write_b16 v138, v0 offset:41616
	v_mul_f32_e32 v0, v1, v59
	v_cvt_pk_bf16_f32 v4, v4, v4
	v_mul_f32_e32 v0, v0, v34
	ds_write_b16 v138, v4 offset:40256
	v_mul_f32_e32 v4, v28, v59
	v_cvt_pk_bf16_f32 v0, v0, v0
	v_mul_f32_e32 v4, v4, v53
	ds_write_b16 v138, v0 offset:41888
	v_mul_f32_e32 v0, v31, v59
	v_cvt_pk_bf16_f32 v4, v4, v4
	v_mul_f32_e32 v0, v0, v35
	ds_write_b16 v138, v4 offset:40528
	v_mul_f32_e32 v4, v7, v59
	v_cvt_pk_bf16_f32 v0, v0, v0
	v_mul_f32_e32 v4, v4, v54
	ds_write_b16 v138, v0 offset:42160
	v_mul_f32_e32 v0, v2, v59
	v_cvt_pk_bf16_f32 v4, v4, v4
	s_waitcnt vmcnt(0)
	v_mul_f32_e32 v0, v0, v12
	ds_write_b16 v138, v4 offset:40800
	v_mul_f32_e32 v4, v29, v59
	v_cvt_pk_bf16_f32 v0, v0, v0
	v_lshl_add_u64 v[28:29], v[20:21], 0, s[22:23]
	v_add_u32_e32 v20, s44, v120
	ds_write_b16 v138, v0 offset:42432
	v_mul_f32_e32 v0, v56, v59
	v_mad_i64_i32 v[20:21], s[8:9], v20, s40, v[16:17]
	v_mul_f32_e32 v0, v0, v13
	v_lshl_add_u64 v[20:21], v[20:21], 0, s[24:25]
	v_cvt_pk_bf16_f32 v0, v0, v0
	v_lshl_add_u64 v[20:21], v[20:21], 0, v[84:85]
	ds_write_b16 v138, v0 offset:42704
	v_mul_f32_e32 v0, v57, v59
	v_lshl_add_u64 v[30:31], v[20:21], 0, s[22:23]
	v_add_u32_e32 v20, s44, v121
	v_mul_f32_e32 v0, v0, v14
	v_mad_i64_i32 v[20:21], s[8:9], v20, s40, v[16:17]
	v_cvt_pk_bf16_f32 v0, v0, v0
	v_lshl_add_u64 v[20:21], v[20:21], 0, s[24:25]
	ds_write_b16 v138, v0 offset:42976
	v_mul_f32_e32 v0, v3, v59
	v_lshl_add_u64 v[20:21], v[20:21], 0, v[84:85]
	v_mul_f32_e32 v0, v0, v15
	v_lshl_add_u64 v[48:49], v[20:21], 0, s[22:23]
	v_add_u32_e32 v20, s44, v123
	v_cvt_pk_bf16_f32 v0, v0, v0
	v_mad_i64_i32 v[20:21], s[8:9], v20, s40, v[16:17]
	ds_write_b16 v138, v0 offset:43248
	v_add_u32_e32 v0, s18, v110
	v_lshl_add_u64 v[20:21], v[20:21], 0, s[24:25]
	v_mul_f32_e32 v4, v4, v55
	v_ashrrev_i32_e32 v1, 31, v0
	v_lshl_add_u64 v[20:21], v[20:21], 0, v[84:85]
	ds_write_b16 v138, v19 offset:34816
	v_cvt_pk_bf16_f32 v8, v8, v8
	ds_write_b16 v138, v8 offset:38896
	v_cvt_pk_bf16_f32 v4, v4, v4
	ds_write_b16 v138, v4 offset:41072
	v_lshl_add_u64 v[0:1], v[0:1], 2, s[26:27]
	v_lshl_add_u64 v[50:51], v[20:21], 0, s[22:23]
	v_add_u32_e32 v20, s44, v124
	global_load_dwordx4 v[44:47], v[0:1], off
	global_load_dwordx4 v[40:43], v[0:1], off offset:32
	v_mad_i64_i32 v[20:21], s[8:9], v20, s40, v[16:17]
	v_lshl_add_u64 v[20:21], v[20:21], 0, s[24:25]
	v_add_u32_e32 v2, s44, v110
	v_lshl_add_u64 v[20:21], v[20:21], 0, v[84:85]
	v_mad_i64_i32 v[2:3], s[8:9], v2, s40, v[16:17]
	v_add_u32_e32 v4, s44, v111
	v_add_u32_e32 v6, s44, v112
	v_add_u32_e32 v8, s44, v113
	v_add_u32_e32 v10, s44, v114
	v_add_u32_e32 v12, s44, v115
	v_add_u32_e32 v14, s44, v116
	v_add_u32_e32 v18, s44, v117
	global_load_dwordx4 v[36:39], v[0:1], off offset:64
	global_load_dwordx4 v[32:35], v[0:1], off offset:96
	v_add_u32_e32 v0, s44, v122
	v_lshl_add_u64 v[52:53], v[20:21], 0, s[22:23]
	v_add_u32_e32 v20, s44, v125
	v_lshl_add_u64 v[2:3], v[2:3], 0, s[24:25]
	v_mad_i64_i32 v[4:5], s[8:9], v4, s40, v[16:17]
	v_mad_i64_i32 v[6:7], s[8:9], v6, s40, v[16:17]
	v_mad_i64_i32 v[8:9], s[8:9], v8, s40, v[16:17]
	v_mad_i64_i32 v[10:11], s[8:9], v10, s40, v[16:17]
	v_mad_i64_i32 v[12:13], s[8:9], v12, s40, v[16:17]
	v_mad_i64_i32 v[14:15], s[8:9], v14, s40, v[16:17]
	v_mad_i64_i32 v[18:19], s[8:9], v18, s40, v[16:17]
	v_mad_i64_i32 v[0:1], s[8:9], v0, s40, v[16:17]
	v_mad_i64_i32 v[16:17], s[8:9], v20, s40, v[16:17]
	v_lshl_add_u64 v[2:3], v[2:3], 0, v[84:85]
	v_lshl_add_u64 v[4:5], v[4:5], 0, s[24:25]
	v_lshl_add_u64 v[6:7], v[6:7], 0, s[24:25]
	v_lshl_add_u64 v[8:9], v[8:9], 0, s[24:25]
	v_lshl_add_u64 v[10:11], v[10:11], 0, s[24:25]
	v_lshl_add_u64 v[12:13], v[12:13], 0, s[24:25]
	v_lshl_add_u64 v[14:15], v[14:15], 0, s[24:25]
	v_lshl_add_u64 v[18:19], v[18:19], 0, s[24:25]
	v_lshl_add_u64 v[0:1], v[0:1], 0, s[24:25]
	v_lshl_add_u64 v[16:17], v[16:17], 0, s[24:25]
	v_lshl_add_u64 v[2:3], v[2:3], 0, s[22:23]
	v_lshl_add_u64 v[4:5], v[4:5], 0, v[84:85]
	v_lshl_add_u64 v[6:7], v[6:7], 0, v[84:85]
	v_lshl_add_u64 v[8:9], v[8:9], 0, v[84:85]
	v_lshl_add_u64 v[10:11], v[10:11], 0, v[84:85]
	v_lshl_add_u64 v[12:13], v[12:13], 0, v[84:85]
	v_lshl_add_u64 v[14:15], v[14:15], 0, v[84:85]
	v_lshl_add_u64 v[18:19], v[18:19], 0, v[84:85]
	v_lshl_add_u64 v[0:1], v[0:1], 0, v[84:85]
	v_lshl_add_u64 v[16:17], v[16:17], 0, v[84:85]
	v_lshl_add_u64 v[4:5], v[4:5], 0, s[22:23]
	v_lshl_add_u64 v[6:7], v[6:7], 0, s[22:23]
	v_lshl_add_u64 v[8:9], v[8:9], 0, s[22:23]
	v_lshl_add_u64 v[10:11], v[10:11], 0, s[22:23]
	v_lshl_add_u64 v[12:13], v[12:13], 0, s[22:23]
	v_lshl_add_u64 v[14:15], v[14:15], 0, s[22:23]
	v_lshl_add_u64 v[18:19], v[18:19], 0, s[22:23]
	v_lshl_add_u64 v[0:1], v[0:1], 0, s[22:23]
	v_lshl_add_u64 v[16:17], v[16:17], 0, s[22:23]
	global_load_ushort v25, v[2:3], off offset:2176
	global_load_ushort v90, v[4:5], off offset:2176
	global_load_ushort v91, v[6:7], off offset:2176
	global_load_ushort v92, v[8:9], off offset:2176
	global_load_ushort v149, v[8:9], off offset:2240
	global_load_ushort v150, v[6:7], off offset:2240
	global_load_ushort v151, v[4:5], off offset:2240
	global_load_ushort v152, v[2:3], off offset:2240
	global_load_ushort v93, v[10:11], off offset:2176
	global_load_ushort v94, v[12:13], off offset:2176
	global_load_ushort v95, v[14:15], off offset:2176
	global_load_ushort v96, v[18:19], off offset:2176
	global_load_ushort v145, v[18:19], off offset:2240
	global_load_ushort v146, v[14:15], off offset:2240
	global_load_ushort v147, v[12:13], off offset:2240
	global_load_ushort v148, v[10:11], off offset:2240
	global_load_ushort v97, v[26:27], off offset:2176
	global_load_ushort v100, v[28:29], off offset:2176
	global_load_ushort v101, v[30:31], off offset:2176
	global_load_ushort v24, v[48:49], off offset:2176
	global_load_ushort v141, v[48:49], off offset:2240
	global_load_ushort v142, v[30:31], off offset:2240
	global_load_ushort v143, v[28:29], off offset:2240
	global_load_ushort v144, v[26:27], off offset:2240
	global_load_ushort v23, v[0:1], off offset:2176
	global_load_ushort v22, v[50:51], off offset:2176
	global_load_ushort v21, v[52:53], off offset:2176
	global_load_ushort v20, v[16:17], off offset:2176
	global_load_ushort v78, v[16:17], off offset:2240
	global_load_ushort v83, v[52:53], off offset:2240
	global_load_ushort v85, v[50:51], off offset:2240
	global_load_ushort v140, v[0:1], off offset:2240
	s_waitcnt lgkmcnt(0)
	s_barrier
	ds_read_b128 v[16:19], v126
	ds_read_b128 v[0:3], v127 offset:34816
	ds_read_b128 v[72:75], v126 offset:32
	ds_read_b128 v[26:29], v127 offset:34848
	s_waitcnt lgkmcnt(2)
	v_mfma_f32_32x32x16_bf16 v[0:15], v[16:19], v[0:3], 0
	s_waitcnt vmcnt(31)
	v_lshlrev_b32_e32 v25, 16, v25
	s_waitcnt lgkmcnt(0)
	v_mfma_f32_32x32x16_bf16 v[0:15], v[72:75], v[26:29], v[0:15]
	ds_read_b128 v[68:71], v126 offset:64
	ds_read_b128 v[26:29], v127 offset:34880
	ds_read_b128 v[64:67], v126 offset:96
	ds_read_b128 v[48:51], v127 offset:34912
	v_mul_f32_e32 v30, 0x3d372713, v25
	v_mul_f32_e32 v30, v30, v25
	v_fma_f32 v30, v30, v25, v25
	v_mul_f32_e32 v30, 0x3f4c422a, v30
	v_mul_f32_e32 v30, -2.0, v30
	v_mul_f32_e32 v30, 0x3fb8aa3b, v30
	s_waitcnt lgkmcnt(2)
	v_mfma_f32_32x32x16_bf16 v[0:15], v[68:71], v[26:29], v[0:15]
	v_exp_f32_e32 v30, v30
	s_waitcnt vmcnt(12)
	v_lshlrev_b32_e32 v24, 16, v24
	s_waitcnt lgkmcnt(0)
	v_mfma_f32_32x32x16_bf16 v[0:15], v[64:67], v[48:51], v[0:15]
	ds_read_b128 v[60:63], v126 offset:128
	ds_read_b128 v[26:29], v127 offset:34944
	ds_read_b128 v[56:59], v126 offset:160
	ds_read_b128 v[48:51], v127 offset:34976
	s_waitcnt vmcnt(7)
	v_lshlrev_b32_e32 v23, 16, v23
	s_waitcnt vmcnt(6)
	v_lshlrev_b32_e32 v22, 16, v22
	s_waitcnt vmcnt(5)
	v_lshlrev_b32_e32 v21, 16, v21
	s_waitcnt lgkmcnt(2)
	v_mfma_f32_32x32x16_bf16 v[0:15], v[60:63], v[26:29], v[0:15]
	s_waitcnt lgkmcnt(0)
	v_mfma_f32_32x32x16_bf16 v[0:15], v[56:59], v[48:51], v[0:15]
	ds_read_b128 v[26:29], v127 offset:35008
	ds_read_b128 v[52:55], v126 offset:192
	ds_read_b128 v[48:51], v126 offset:224
	ds_read_b128 v[86:89], v127 offset:35040
	ds_read_b128 v[154:157], v128 offset:34848
	s_waitcnt lgkmcnt(3)
	v_mfma_f32_32x32x16_bf16 v[0:15], v[52:55], v[26:29], v[0:15]
	v_add_f32_e32 v26, 1.0, v30
	v_rcp_f32_e32 v28, v26
	s_nop 0
	s_waitcnt lgkmcnt(1)
	v_mfma_f32_32x32x16_bf16 v[0:15], v[48:51], v[86:89], v[0:15]
	v_mul_f32_e32 v27, v25, v28
	v_lshlrev_b32_e32 v28, 16, v90
	v_mov_b32_e32 v25, v27
	v_mul_f32_e32 v26, 0x3d372713, v28
	v_mul_f32_e32 v26, v26, v28
	v_fma_f32 v26, v26, v28, v28
	v_mul_f32_e32 v26, 0x3f4c422a, v26
	v_mul_f32_e32 v26, -2.0, v26
	v_mul_f32_e32 v26, 0x3fb8aa3b, v26
	v_exp_f32_e32 v26, v26
	s_nop 1
	v_add_f32_e32 v0, v44, v0
	v_mul_f32_e32 v0, v25, v0
	v_med3_f32 v0, v0, s42, v139
	v_mov_b32_e32 v25, v79
	v_cvt_pk_fp8_f32 v25, v0, 0
	v_add_f32_e32 v0, 1.0, v26
	v_rcp_f32_e32 v30, v0
	v_lshlrev_b64 v[86:87], 11, v[98:99]
	v_lshl_add_u64 v[26:27], v[80:81], 0, v[86:87]
	v_lshl_add_u64 v[26:27], v[26:27], 0, s[18:19]
	global_store_byte v[26:27], v25, off
	v_mul_f32_e32 v25, v28, v30
	v_mov_b32_e32 v0, v25
	v_add_f32_e32 v1, v45, v1
	v_mul_f32_e32 v0, v0, v1
	v_med3_f32 v0, v0, s42, v139
	v_mov_b32_e32 v25, v79
	v_lshlrev_b32_e32 v28, 16, v91
	v_cvt_pk_fp8_f32 v25, v0, 0
	v_mul_f32_e32 v0, 0x3d372713, v28
	v_mul_f32_e32 v0, v0, v28
	v_fma_f32 v0, v0, v28, v28
	v_mul_f32_e32 v0, 0x3f4c422a, v0
	v_mul_f32_e32 v0, -2.0, v0
	v_mul_f32_e32 v0, 0x3fb8aa3b, v0
	v_exp_f32_e32 v26, v0
	v_or_b32_e32 v0, 1, v98
	v_ashrrev_i32_e32 v1, 31, v0
	v_lshlrev_b64 v[0:1], 11, v[0:1]
	v_add_f32_e32 v29, 1.0, v26
	v_rcp_f32_e32 v31, v29
	v_lshl_add_u64 v[26:27], v[80:81], 0, v[0:1]
	v_lshl_add_u64 v[26:27], v[26:27], 0, s[18:19]
	global_store_byte v[26:27], v25, off
	v_mul_f32_e32 v25, v28, v31
	v_add_f32_e32 v2, v46, v2
	v_mul_f32_e32 v2, v25, v2
	v_med3_f32 v2, v2, s42, v139
	v_mov_b32_e32 v25, v79
	v_cvt_pk_fp8_f32 v25, v2, 0
	v_lshlrev_b32_e32 v2, 16, v92
	v_mul_f32_e32 v26, 0x3d372713, v2
	v_mul_f32_e32 v26, v26, v2
	v_fma_f32 v26, v26, v2, v2
	v_mul_f32_e32 v26, 0x3f4c422a, v26
	v_mul_f32_e32 v26, -2.0, v26
	v_mul_f32_e32 v26, 0x3fb8aa3b, v26
	v_exp_f32_e32 v28, v26
	v_or_b32_e32 v26, 2, v98
	v_ashrrev_i32_e32 v27, 31, v26
	v_lshlrev_b64 v[88:89], 11, v[26:27]
	v_add_f32_e32 v28, 1.0, v28
	v_rcp_f32_e32 v30, v28
	v_lshl_add_u64 v[26:27], v[80:81], 0, v[88:89]
	v_lshl_add_u64 v[26:27], v[26:27], 0, s[18:19]
	global_store_byte v[26:27], v25, off
	v_mul_f32_e32 v25, v2, v30
	v_mov_b32_e32 v2, v25
	v_add_f32_e32 v3, v47, v3
	v_mul_f32_e32 v2, v2, v3
	v_med3_f32 v2, v2, s42, v139
	v_mov_b32_e32 v25, v79
	v_lshlrev_b32_e32 v28, 16, v93
	v_cvt_pk_fp8_f32 v25, v2, 0
	v_mul_f32_e32 v2, 0x3d372713, v28
	v_mul_f32_e32 v2, v2, v28
	v_fma_f32 v2, v2, v28, v28
	v_mul_f32_e32 v2, 0x3f4c422a, v2
	v_mul_f32_e32 v2, -2.0, v2
	v_mul_f32_e32 v2, 0x3fb8aa3b, v2
	v_exp_f32_e32 v26, v2
	v_or_b32_e32 v2, 3, v98
	v_ashrrev_i32_e32 v3, 31, v2
	v_lshlrev_b64 v[2:3], 11, v[2:3]
	v_add_f32_e32 v29, 1.0, v26
	v_rcp_f32_e32 v31, v29
	v_lshl_add_u64 v[26:27], v[80:81], 0, v[2:3]
	v_lshl_add_u64 v[26:27], v[26:27], 0, s[18:19]
	global_store_byte v[26:27], v25, off
	v_mul_f32_e32 v25, v28, v31
	v_add_f32_e32 v4, v40, v4
	v_mul_f32_e32 v4, v25, v4
	v_med3_f32 v4, v4, s42, v139
	v_mov_b32_e32 v25, v79
	v_cvt_pk_fp8_f32 v25, v4, 0
	v_lshlrev_b32_e32 v4, 16, v94
	v_mul_f32_e32 v26, 0x3d372713, v4
	v_mul_f32_e32 v26, v26, v4
	v_fma_f32 v26, v26, v4, v4
	v_mul_f32_e32 v26, 0x3f4c422a, v26
	v_mul_f32_e32 v26, -2.0, v26
	v_mul_f32_e32 v26, 0x3fb8aa3b, v26
	v_exp_f32_e32 v28, v26
	v_or_b32_e32 v26, 8, v98
	v_ashrrev_i32_e32 v27, 31, v26
	v_lshlrev_b64 v[90:91], 11, v[26:27]
	v_add_f32_e32 v28, 1.0, v28
	v_rcp_f32_e32 v30, v28
	v_lshl_add_u64 v[26:27], v[80:81], 0, v[90:91]
	v_lshl_add_u64 v[26:27], v[26:27], 0, s[18:19]
	global_store_byte v[26:27], v25, off
	v_mul_f32_e32 v25, v4, v30
	v_mov_b32_e32 v4, v25
	v_add_f32_e32 v5, v41, v5
	v_mul_f32_e32 v4, v4, v5
	v_med3_f32 v4, v4, s42, v139
	v_mov_b32_e32 v25, v79
	v_lshlrev_b32_e32 v28, 16, v95
	v_cvt_pk_fp8_f32 v25, v4, 0
	v_mul_f32_e32 v4, 0x3d372713, v28
	v_mul_f32_e32 v4, v4, v28
	v_fma_f32 v4, v4, v28, v28
	v_mul_f32_e32 v4, 0x3f4c422a, v4
	v_mul_f32_e32 v4, -2.0, v4
	v_mul_f32_e32 v4, 0x3fb8aa3b, v4
	v_exp_f32_e32 v26, v4
	v_or_b32_e32 v4, 9, v98
	v_ashrrev_i32_e32 v5, 31, v4
	v_lshlrev_b64 v[4:5], 11, v[4:5]
	v_add_f32_e32 v29, 1.0, v26
	v_rcp_f32_e32 v31, v29
	v_lshl_add_u64 v[26:27], v[80:81], 0, v[4:5]
	v_lshl_add_u64 v[26:27], v[26:27], 0, s[18:19]
	global_store_byte v[26:27], v25, off
	v_mul_f32_e32 v25, v28, v31
	v_add_f32_e32 v6, v42, v6
	v_mul_f32_e32 v6, v25, v6
	v_med3_f32 v6, v6, s42, v139
	v_mov_b32_e32 v25, v79
	v_cvt_pk_fp8_f32 v25, v6, 0
	v_lshlrev_b32_e32 v6, 16, v96
	v_mul_f32_e32 v26, 0x3d372713, v6
	v_mul_f32_e32 v26, v26, v6
	v_fma_f32 v26, v26, v6, v6
	v_mul_f32_e32 v26, 0x3f4c422a, v26
	v_mul_f32_e32 v26, -2.0, v26
	v_mul_f32_e32 v26, 0x3fb8aa3b, v26
	v_exp_f32_e32 v28, v26
	v_or_b32_e32 v26, 10, v98
	v_ashrrev_i32_e32 v27, 31, v26
	v_lshlrev_b64 v[92:93], 11, v[26:27]
	v_add_f32_e32 v28, 1.0, v28
	v_rcp_f32_e32 v30, v28
	v_lshl_add_u64 v[26:27], v[80:81], 0, v[92:93]
	v_lshl_add_u64 v[26:27], v[26:27], 0, s[18:19]
	global_store_byte v[26:27], v25, off
	v_mul_f32_e32 v25, v6, v30
	v_mov_b32_e32 v6, v25
	v_add_f32_e32 v7, v43, v7
	v_mul_f32_e32 v6, v6, v7
	v_med3_f32 v6, v6, s42, v139
	v_mov_b32_e32 v25, v79
	v_lshlrev_b32_e32 v28, 16, v97
	v_cvt_pk_fp8_f32 v25, v6, 0
	v_mul_f32_e32 v6, 0x3d372713, v28
	v_mul_f32_e32 v6, v6, v28
	v_fma_f32 v6, v6, v28, v28
	v_mul_f32_e32 v6, 0x3f4c422a, v6
	v_mul_f32_e32 v6, -2.0, v6
	v_mul_f32_e32 v6, 0x3fb8aa3b, v6
	v_exp_f32_e32 v26, v6
	v_or_b32_e32 v6, 11, v98
	v_ashrrev_i32_e32 v7, 31, v6
	v_lshlrev_b64 v[6:7], 11, v[6:7]
	v_add_f32_e32 v29, 1.0, v26
	v_rcp_f32_e32 v31, v29
	v_lshl_add_u64 v[26:27], v[80:81], 0, v[6:7]
	v_lshl_add_u64 v[26:27], v[26:27], 0, s[18:19]
	global_store_byte v[26:27], v25, off
	v_mul_f32_e32 v25, v28, v31
	v_add_f32_e32 v8, v36, v8
	v_mul_f32_e32 v8, v25, v8
	v_med3_f32 v8, v8, s42, v139
	v_mov_b32_e32 v25, v79
	v_cvt_pk_fp8_f32 v25, v8, 0
	v_lshlrev_b32_e32 v8, 16, v100
	v_mul_f32_e32 v26, 0x3d372713, v8
	v_mul_f32_e32 v26, v26, v8
	v_fma_f32 v26, v26, v8, v8
	v_mul_f32_e32 v26, 0x3f4c422a, v26
	v_mul_f32_e32 v26, -2.0, v26
	v_mul_f32_e32 v26, 0x3fb8aa3b, v26
	v_exp_f32_e32 v28, v26
	v_or_b32_e32 v26, 16, v98
	v_ashrrev_i32_e32 v27, 31, v26
	v_lshlrev_b64 v[94:95], 11, v[26:27]
	v_add_f32_e32 v28, 1.0, v28
	v_rcp_f32_e32 v30, v28
	v_lshl_add_u64 v[26:27], v[80:81], 0, v[94:95]
	v_lshl_add_u64 v[26:27], v[26:27], 0, s[18:19]
	global_store_byte v[26:27], v25, off
	v_mul_f32_e32 v25, v8, v30
	v_mov_b32_e32 v8, v25
	v_add_f32_e32 v9, v37, v9
	v_mul_f32_e32 v8, v8, v9
	v_med3_f32 v8, v8, s42, v139
	v_mov_b32_e32 v25, v79
	v_lshlrev_b32_e32 v26, 16, v101
	v_cvt_pk_fp8_f32 v25, v8, 0
	v_mul_f32_e32 v8, 0x3d372713, v26
	v_mul_f32_e32 v8, v8, v26
	v_fma_f32 v8, v8, v26, v26
	v_mul_f32_e32 v8, 0x3f4c422a, v8
	v_mul_f32_e32 v8, -2.0, v8
	v_mul_f32_e32 v8, 0x3fb8aa3b, v8
	v_exp_f32_e32 v27, v8
	v_or_b32_e32 v8, 17, v98
	v_ashrrev_i32_e32 v9, 31, v8
	v_lshlrev_b64 v[96:97], 11, v[8:9]
	v_add_f32_e32 v27, 1.0, v27
	v_rcp_f32_e32 v29, v27
	v_lshl_add_u64 v[8:9], v[80:81], 0, v[96:97]
	v_lshl_add_u64 v[8:9], v[8:9], 0, s[18:19]
	global_store_byte v[8:9], v25, off
	v_mul_f32_e32 v8, v26, v29
	v_add_f32_e32 v9, v38, v10
	v_mul_f32_e32 v8, v8, v9
	v_med3_f32 v8, v8, s42, v139
	v_mov_b32_e32 v10, v79
	v_cvt_pk_fp8_f32 v10, v8, 0
	v_mul_f32_e32 v8, 0x3d372713, v24
	v_mul_f32_e32 v8, v8, v24
	v_fma_f32 v8, v8, v24, v24
	v_mul_f32_e32 v8, 0x3f4c422a, v8
	v_mul_f32_e32 v8, -2.0, v8
	v_mul_f32_e32 v8, 0x3fb8aa3b, v8
	v_exp_f32_e32 v25, v8
	v_or_b32_e32 v8, 18, v98
	v_ashrrev_i32_e32 v9, 31, v8
	v_lshlrev_b64 v[100:101], 11, v[8:9]
	v_add_f32_e32 v25, 1.0, v25
	v_rcp_f32_e32 v27, v25
	v_lshl_add_u64 v[8:9], v[80:81], 0, v[100:101]
	v_lshl_add_u64 v[8:9], v[8:9], 0, s[18:19]
	global_store_byte v[8:9], v10, off
	v_mul_f32_e32 v8, v24, v27
	v_add_f32_e32 v9, v39, v11
	v_mul_f32_e32 v8, v8, v9
	v_med3_f32 v8, v8, s42, v139
	v_mov_b32_e32 v24, v79
	v_cvt_pk_fp8_f32 v24, v8, 0
	v_mul_f32_e32 v8, 0x3d372713, v23
	v_mul_f32_e32 v8, v8, v23
	v_fma_f32 v8, v8, v23, v23
	v_mul_f32_e32 v8, 0x3f4c422a, v8
	v_mul_f32_e32 v8, -2.0, v8
	v_mul_f32_e32 v8, 0x3fb8aa3b, v8
	v_exp_f32_e32 v25, v8
	v_or_b32_e32 v8, 19, v98
	v_ashrrev_i32_e32 v9, 31, v8
	v_lshlrev_b64 v[10:11], 11, v[8:9]
	v_add_f32_e32 v25, 1.0, v25
	v_rcp_f32_e32 v27, v25
	v_lshl_add_u64 v[8:9], v[80:81], 0, v[10:11]
	v_lshl_add_u64 v[8:9], v[8:9], 0, s[18:19]
	global_store_byte v[8:9], v24, off
	v_mul_f32_e32 v8, v23, v27
	v_add_f32_e32 v9, v32, v12
	v_mul_f32_e32 v8, v8, v9
	v_med3_f32 v8, v8, s42, v139
	v_mov_b32_e32 v12, v79
	v_cvt_pk_fp8_f32 v12, v8, 0
	v_mul_f32_e32 v8, 0x3d372713, v22
	v_mul_f32_e32 v8, v8, v22
	v_fma_f32 v8, v8, v22, v22
	v_mul_f32_e32 v8, 0x3f4c422a, v8
	v_mul_f32_e32 v8, -2.0, v8
	v_mul_f32_e32 v8, 0x3fb8aa3b, v8
	v_exp_f32_e32 v23, v8
	v_or_b32_e32 v8, 24, v98
	v_ashrrev_i32_e32 v9, 31, v8
	v_lshlrev_b64 v[102:103], 11, v[8:9]
	v_add_f32_e32 v23, 1.0, v23
	v_rcp_f32_e32 v25, v23
	v_lshl_add_u64 v[8:9], v[80:81], 0, v[102:103]
	v_lshl_add_u64 v[8:9], v[8:9], 0, s[18:19]
	global_store_byte v[8:9], v12, off
	v_mul_f32_e32 v8, v22, v25
	v_add_f32_e32 v9, v33, v13
	v_mul_f32_e32 v8, v8, v9
	v_med3_f32 v8, v8, s42, v139
	v_mov_b32_e32 v22, v79
	v_cvt_pk_fp8_f32 v22, v8, 0
	v_mul_f32_e32 v8, 0x3d372713, v21
	v_mul_f32_e32 v8, v8, v21
	v_fma_f32 v8, v8, v21, v21
	v_mul_f32_e32 v8, 0x3f4c422a, v8
	v_mul_f32_e32 v8, -2.0, v8
	v_mul_f32_e32 v8, 0x3fb8aa3b, v8
	v_exp_f32_e32 v23, v8
	v_or_b32_e32 v8, 25, v98
	v_ashrrev_i32_e32 v9, 31, v8
	v_lshlrev_b64 v[12:13], 11, v[8:9]
	v_add_f32_e32 v23, 1.0, v23
	v_rcp_f32_e32 v25, v23
	v_lshl_add_u64 v[8:9], v[80:81], 0, v[12:13]
	v_lshl_add_u64 v[8:9], v[8:9], 0, s[18:19]
	global_store_byte v[8:9], v22, off
	v_mul_f32_e32 v8, v21, v25
	ds_read_b128 v[22:25], v128 offset:34816
	s_waitcnt vmcnt(18)
	v_lshlrev_b32_e32 v99, 16, v20
	v_mul_f32_e32 v20, 0x3d372713, v99
	v_mul_f32_e32 v153, v20, v99
	s_waitcnt lgkmcnt(0)
	v_mfma_f32_32x32x16_bf16 v[16:31], v[16:19], v[22:25], 0
	v_fma_f32 v153, v153, v99, v99
	v_mul_f32_e32 v153, 0x3f4c422a, v153
	v_mul_f32_e32 v153, -2.0, v153
	v_mul_f32_e32 v153, 0x3fb8aa3b, v153
	v_exp_f32_e32 v153, v153
	v_add_f32_e32 v9, v34, v14
	v_mul_f32_e32 v8, v8, v9
	v_mfma_f32_32x32x16_bf16 v[16:31], v[72:75], v[154:157], v[16:31]
	ds_read_b128 v[72:75], v128 offset:34880
	ds_read_b128 v[154:157], v128 offset:34912
	v_med3_f32 v8, v8, s42, v139
	v_mov_b32_e32 v14, v79
	v_add_f32_e32 v153, 1.0, v153
	v_cvt_pk_fp8_f32 v14, v8, 0
	v_or_b32_e32 v8, 26, v98
	s_waitcnt lgkmcnt(1)
	v_mfma_f32_32x32x16_bf16 v[16:31], v[68:71], v[72:75], v[16:31]
	v_ashrrev_i32_e32 v9, 31, v8
	v_rcp_f32_e32 v161, v153
	v_lshlrev_b64 v[8:9], 11, v[8:9]
	v_lshl_add_u64 v[158:159], v[80:81], 0, v[8:9]
	v_lshl_add_u64 v[158:159], v[158:159], 0, s[18:19]
	s_waitcnt lgkmcnt(0)
	v_mfma_f32_32x32x16_bf16 v[16:31], v[64:67], v[154:157], v[16:31]
	global_store_byte v[158:159], v14, off
	ds_read_b128 v[64:67], v128 offset:34944
	v_mul_f32_e32 v14, v99, v161
	ds_read_b128 v[68:71], v128 offset:34976
	s_waitcnt lgkmcnt(1)
	v_mfma_f32_32x32x16_bf16 v[16:31], v[60:63], v[64:67], v[16:31]
	v_lshlrev_b32_e32 v65, 16, v152
	v_mul_f32_e32 v60, 0x3d372713, v65
	v_mul_f32_e32 v60, v60, v65
	v_fma_f32 v60, v60, v65, v65
	v_mul_f32_e32 v60, 0x3f4c422a, v60
	v_mul_f32_e32 v60, -2.0, v60
	v_mul_f32_e32 v60, 0x3fb8aa3b, v60
	s_waitcnt lgkmcnt(0)
	v_mfma_f32_32x32x16_bf16 v[16:31], v[56:59], v[68:71], v[16:31]
	ds_read_b128 v[56:59], v128 offset:35008
	v_exp_f32_e32 v66, v60
	ds_read_b128 v[60:63], v128 offset:35040
	v_add_f32_e32 v15, v35, v15
	v_mul_f32_e32 v14, v14, v15
	v_med3_f32 v14, v14, s42, v139
	s_waitcnt lgkmcnt(1)
	v_mfma_f32_32x32x16_bf16 v[16:31], v[52:55], v[56:59], v[16:31]
	v_add_f32_e32 v54, 1.0, v66
	v_rcp_f32_e32 v56, v54
	v_mov_b32_e32 v64, v79
	v_cvt_pk_fp8_f32 v64, v14, 0
	v_or_b32_e32 v14, 27, v98
	s_waitcnt lgkmcnt(0)
	v_mfma_f32_32x32x16_bf16 v[16:31], v[48:51], v[60:63], v[16:31]
	v_mul_f32_e32 v48, v65, v56
	s_nop 2
	s_nop 7
	v_add_f32_e32 v16, v44, v16
	v_lshlrev_b32_e32 v44, 16, v151
	s_nop 0
	v_mul_f32_e32 v16, v48, v16
	v_mul_f32_e32 v48, 0x3d372713, v44
	v_mul_f32_e32 v48, v48, v44
	v_fma_f32 v48, v48, v44, v44
	v_mul_f32_e32 v48, 0x3f4c422a, v48
	v_mul_f32_e32 v48, -2.0, v48
	v_mul_f32_e32 v48, 0x3fb8aa3b, v48
	v_exp_f32_e32 v48, v48
	v_ashrrev_i32_e32 v15, 31, v14
	v_lshlrev_b64 v[14:15], 11, v[14:15]
	v_lshl_add_u64 v[52:53], v[80:81], 0, v[14:15]
	v_lshl_add_u64 v[52:53], v[52:53], 0, s[18:19]
	v_add_f32_e32 v51, 1.0, v48
	global_store_byte v[52:53], v64, off
	v_med3_f32 v16, v16, s42, v139
	v_mov_b32_e32 v50, v79
	v_cvt_pk_fp8_f32 v50, v16, 0
	v_rcp_f32_e32 v53, v51
	v_or_b32_e32 v16, s18, v129
	v_or_b32_e32 v86, v86, v16
	v_lshl_add_u64 v[48:49], s[20:21], 0, v[86:87]
	global_store_byte v[48:49], v50, off
	v_mul_f32_e32 v48, v44, v53
	v_mov_b32_e32 v44, v48
	v_add_f32_e32 v17, v45, v17
	v_mul_f32_e32 v17, v44, v17
	v_lshlrev_b32_e32 v44, 16, v150
	v_mul_f32_e32 v45, 0x3d372713, v44
	v_mul_f32_e32 v45, v45, v44
	v_fma_f32 v45, v45, v44, v44
	v_mul_f32_e32 v45, 0x3f4c422a, v45
	v_mul_f32_e32 v45, -2.0, v45
	v_mul_f32_e32 v45, 0x3fb8aa3b, v45
	v_exp_f32_e32 v45, v45
	v_med3_f32 v17, v17, s42, v139
	v_mov_b32_e32 v48, v79
	v_cvt_pk_fp8_f32 v48, v17, 0
	v_add_f32_e32 v17, 1.0, v45
	v_rcp_f32_e32 v49, v17
	v_or_b32_e32 v0, v0, v16
	v_lshl_add_u64 v[0:1], s[20:21], 0, v[0:1]
	global_store_byte v[0:1], v48, off
	v_mul_f32_e32 v0, v44, v49
	v_add_f32_e32 v1, v46, v18
	v_lshlrev_b32_e32 v17, 16, v149
	v_mul_f32_e32 v0, v0, v1
	v_mul_f32_e32 v1, 0x3d372713, v17
	v_mul_f32_e32 v1, v1, v17
	v_fma_f32 v1, v1, v17, v17
	v_mul_f32_e32 v1, 0x3f4c422a, v1
	v_mul_f32_e32 v1, -2.0, v1
	v_mul_f32_e32 v1, 0x3fb8aa3b, v1
	v_exp_f32_e32 v1, v1
	v_med3_f32 v0, v0, s42, v139
	v_mov_b32_e32 v18, v79
	v_cvt_pk_fp8_f32 v18, v0, 0
	v_add_f32_e32 v44, 1.0, v1
	v_rcp_f32_e32 v46, v44
	v_or_b32_e32 v88, v88, v16
	v_lshl_add_u64 v[0:1], s[20:21], 0, v[88:89]
	global_store_byte v[0:1], v18, off
	v_mul_f32_e32 v0, v17, v46
	v_add_f32_e32 v1, v47, v19
	v_lshlrev_b32_e32 v17, 16, v148
	v_mul_f32_e32 v0, v0, v1
	v_mul_f32_e32 v1, 0x3d372713, v17
	v_mul_f32_e32 v1, v1, v17
	v_fma_f32 v1, v1, v17, v17
	v_mul_f32_e32 v1, 0x3f4c422a, v1
	v_mul_f32_e32 v1, -2.0, v1
	v_mul_f32_e32 v1, 0x3fb8aa3b, v1
	v_exp_f32_e32 v1, v1
	v_med3_f32 v0, v0, s42, v139
	v_mov_b32_e32 v18, v79
	v_cvt_pk_fp8_f32 v18, v0, 0
	v_add_f32_e32 v19, 1.0, v1
	v_rcp_f32_e32 v45, v19
	v_or_b32_e32 v2, v2, v16
	v_lshl_add_u64 v[0:1], s[20:21], 0, v[2:3]
	global_store_byte v[0:1], v18, off
	v_mul_f32_e32 v0, v17, v45
	v_add_f32_e32 v1, v40, v20
	v_lshlrev_b32_e32 v2, 16, v147
	v_mul_f32_e32 v0, v0, v1
	v_mul_f32_e32 v1, 0x3d372713, v2
	v_mul_f32_e32 v1, v1, v2
	v_fma_f32 v1, v1, v2, v2
	v_mul_f32_e32 v1, 0x3f4c422a, v1
	v_mul_f32_e32 v1, -2.0, v1
	v_mul_f32_e32 v1, 0x3fb8aa3b, v1
	v_exp_f32_e32 v1, v1
	v_med3_f32 v0, v0, s42, v139
	v_mov_b32_e32 v3, v79
	v_cvt_pk_fp8_f32 v3, v0, 0
	v_add_f32_e32 v17, 1.0, v1
	v_rcp_f32_e32 v19, v17
	v_or_b32_e32 v90, v90, v16
	v_lshl_add_u64 v[0:1], s[20:21], 0, v[90:91]
	global_store_byte v[0:1], v3, off
	v_mul_f32_e32 v0, v2, v19
	v_add_f32_e32 v1, v41, v21
	v_lshlrev_b32_e32 v2, 16, v146
	v_mul_f32_e32 v0, v0, v1
	v_mul_f32_e32 v1, 0x3d372713, v2
	v_mul_f32_e32 v1, v1, v2
	v_fma_f32 v1, v1, v2, v2
	v_mul_f32_e32 v1, 0x3f4c422a, v1
	v_mul_f32_e32 v1, -2.0, v1
	v_mul_f32_e32 v1, 0x3fb8aa3b, v1
	v_exp_f32_e32 v1, v1
	v_med3_f32 v0, v0, s42, v139
	v_mov_b32_e32 v3, v79
	v_cvt_pk_fp8_f32 v3, v0, 0
	v_add_f32_e32 v17, 1.0, v1
	v_rcp_f32_e32 v19, v17
	v_or_b32_e32 v4, v4, v16
	v_lshl_add_u64 v[0:1], s[20:21], 0, v[4:5]
	global_store_byte v[0:1], v3, off
	v_mul_f32_e32 v0, v2, v19
	v_add_f32_e32 v1, v42, v22
	v_lshlrev_b32_e32 v2, 16, v145
	v_mul_f32_e32 v0, v0, v1
	v_mul_f32_e32 v1, 0x3d372713, v2
	v_mul_f32_e32 v1, v1, v2
	v_fma_f32 v1, v1, v2, v2
	v_mul_f32_e32 v1, 0x3f4c422a, v1
	v_mul_f32_e32 v1, -2.0, v1
	v_mul_f32_e32 v1, 0x3fb8aa3b, v1
	v_exp_f32_e32 v1, v1
	v_med3_f32 v0, v0, s42, v139
	v_mov_b32_e32 v3, v79
	v_cvt_pk_fp8_f32 v3, v0, 0
	v_add_f32_e32 v4, 1.0, v1
	v_rcp_f32_e32 v17, v4
	v_or_b32_e32 v92, v92, v16
	v_lshl_add_u64 v[0:1], s[20:21], 0, v[92:93]
	global_store_byte v[0:1], v3, off
	v_mul_f32_e32 v0, v2, v17
	v_add_f32_e32 v1, v43, v23
	v_lshlrev_b32_e32 v2, 16, v144
	v_mul_f32_e32 v0, v0, v1
	v_mul_f32_e32 v1, 0x3d372713, v2
	v_mul_f32_e32 v1, v1, v2
	v_fma_f32 v1, v1, v2, v2
	v_mul_f32_e32 v1, 0x3f4c422a, v1
	v_mul_f32_e32 v1, -2.0, v1
	v_mul_f32_e32 v1, 0x3fb8aa3b, v1
	v_exp_f32_e32 v1, v1
	v_med3_f32 v0, v0, s42, v139
	v_mov_b32_e32 v3, v79
	v_cvt_pk_fp8_f32 v3, v0, 0
	v_add_f32_e32 v4, 1.0, v1
	v_rcp_f32_e32 v17, v4
	v_or_b32_e32 v6, v6, v16
	v_lshl_add_u64 v[0:1], s[20:21], 0, v[6:7]
	global_store_byte v[0:1], v3, off
	v_mul_f32_e32 v0, v2, v17
	v_add_f32_e32 v1, v36, v24
	v_lshlrev_b32_e32 v2, 16, v143
	v_mul_f32_e32 v0, v0, v1
	v_mul_f32_e32 v1, 0x3d372713, v2
	v_mul_f32_e32 v1, v1, v2
	v_fma_f32 v1, v1, v2, v2
	v_mul_f32_e32 v1, 0x3f4c422a, v1
	v_mul_f32_e32 v1, -2.0, v1
	v_mul_f32_e32 v1, 0x3fb8aa3b, v1
	v_exp_f32_e32 v1, v1
	v_med3_f32 v0, v0, s42, v139
	v_mov_b32_e32 v3, v79
	v_cvt_pk_fp8_f32 v3, v0, 0
	v_add_f32_e32 v4, 1.0, v1
	v_rcp_f32_e32 v6, v4
	v_or_b32_e32 v94, v94, v16
	v_lshl_add_u64 v[0:1], s[20:21], 0, v[94:95]
	global_store_byte v[0:1], v3, off
	v_mul_f32_e32 v0, v2, v6
	v_add_f32_e32 v1, v37, v25
	v_lshlrev_b32_e32 v2, 16, v142
	v_mul_f32_e32 v0, v0, v1
	v_mul_f32_e32 v1, 0x3d372713, v2
	v_mul_f32_e32 v1, v1, v2
	v_fma_f32 v1, v1, v2, v2
	v_mul_f32_e32 v1, 0x3f4c422a, v1
	v_mul_f32_e32 v1, -2.0, v1
	v_mul_f32_e32 v1, 0x3fb8aa3b, v1
	v_exp_f32_e32 v1, v1
	v_med3_f32 v0, v0, s42, v139
	v_mov_b32_e32 v3, v79
	v_cvt_pk_fp8_f32 v3, v0, 0
	v_add_f32_e32 v4, 1.0, v1
	v_rcp_f32_e32 v6, v4
	v_or_b32_e32 v96, v96, v16
	v_lshl_add_u64 v[0:1], s[20:21], 0, v[96:97]
	global_store_byte v[0:1], v3, off
	v_mul_f32_e32 v0, v2, v6
	v_add_f32_e32 v1, v38, v26
	v_lshlrev_b32_e32 v2, 16, v141
	v_mul_f32_e32 v0, v0, v1
	v_mul_f32_e32 v1, 0x3d372713, v2
	v_mul_f32_e32 v1, v1, v2
	v_fma_f32 v1, v1, v2, v2
	v_mul_f32_e32 v1, 0x3f4c422a, v1
	v_mul_f32_e32 v1, -2.0, v1
	v_mul_f32_e32 v1, 0x3fb8aa3b, v1
	v_exp_f32_e32 v1, v1
	v_med3_f32 v0, v0, s42, v139
	v_mov_b32_e32 v3, v79
	v_cvt_pk_fp8_f32 v3, v0, 0
	v_add_f32_e32 v4, 1.0, v1
	v_rcp_f32_e32 v6, v4
	v_or_b32_e32 v100, v100, v16
	v_lshl_add_u64 v[0:1], s[20:21], 0, v[100:101]
	global_store_byte v[0:1], v3, off
	v_mul_f32_e32 v0, v2, v6
	v_add_f32_e32 v1, v39, v27
	s_waitcnt vmcnt(27)
	v_lshlrev_b32_e32 v2, 16, v140
	v_mul_f32_e32 v0, v0, v1
	v_mul_f32_e32 v1, 0x3d372713, v2
	v_mul_f32_e32 v1, v1, v2
	v_fma_f32 v1, v1, v2, v2
	v_mul_f32_e32 v1, 0x3f4c422a, v1
	v_mul_f32_e32 v1, -2.0, v1
	v_mul_f32_e32 v1, 0x3fb8aa3b, v1
	v_exp_f32_e32 v1, v1
	v_med3_f32 v0, v0, s42, v139
	v_mov_b32_e32 v3, v79
	v_cvt_pk_fp8_f32 v3, v0, 0
	v_add_f32_e32 v4, 1.0, v1
	v_rcp_f32_e32 v6, v4
	v_or_b32_e32 v10, v10, v16
	v_lshl_add_u64 v[0:1], s[20:21], 0, v[10:11]
	global_store_byte v[0:1], v3, off
	v_mul_f32_e32 v0, v2, v6
	v_add_f32_e32 v1, v32, v28
	v_lshlrev_b32_e32 v2, 16, v85
	v_mul_f32_e32 v0, v0, v1
	v_mul_f32_e32 v1, 0x3d372713, v2
	v_mul_f32_e32 v1, v1, v2
	v_fma_f32 v1, v1, v2, v2
	v_mul_f32_e32 v1, 0x3f4c422a, v1
	v_mul_f32_e32 v1, -2.0, v1
	v_mul_f32_e32 v1, 0x3fb8aa3b, v1
	v_exp_f32_e32 v1, v1
	v_med3_f32 v0, v0, s42, v139
	v_mov_b32_e32 v3, v79
	v_cvt_pk_fp8_f32 v3, v0, 0
	v_add_f32_e32 v4, 1.0, v1
	v_rcp_f32_e32 v6, v4
	v_or_b32_e32 v102, v102, v16
	v_lshl_add_u64 v[0:1], s[20:21], 0, v[102:103]
	global_store_byte v[0:1], v3, off
	v_mul_f32_e32 v0, v2, v6
	v_add_f32_e32 v1, v33, v29
	v_lshlrev_b32_e32 v2, 16, v83
	v_mul_f32_e32 v0, v0, v1
	v_mul_f32_e32 v1, 0x3d372713, v2
	v_mul_f32_e32 v1, v1, v2
	v_fma_f32 v1, v1, v2, v2
	v_mul_f32_e32 v1, 0x3f4c422a, v1
	v_mul_f32_e32 v1, -2.0, v1
	v_mul_f32_e32 v1, 0x3fb8aa3b, v1
	v_exp_f32_e32 v1, v1
	v_med3_f32 v0, v0, s42, v139
	v_mov_b32_e32 v3, v79
	v_cvt_pk_fp8_f32 v3, v0, 0
	v_add_f32_e32 v4, 1.0, v1
	v_rcp_f32_e32 v6, v4
	v_or_b32_e32 v12, v12, v16
	v_lshl_add_u64 v[0:1], s[20:21], 0, v[12:13]
	global_store_byte v[0:1], v3, off
	v_mul_f32_e32 v0, v2, v6
	v_lshlrev_b32_e32 v2, 16, v78
	v_mul_f32_e32 v3, 0x3d372713, v2
	v_mul_f32_e32 v3, v3, v2
	v_fma_f32 v3, v3, v2, v2
	v_mul_f32_e32 v3, 0x3f4c422a, v3
	v_mul_f32_e32 v3, -2.0, v3
	v_mul_f32_e32 v3, 0x3fb8aa3b, v3
	v_exp_f32_e32 v3, v3
	v_add_f32_e32 v1, v34, v30
	v_mul_f32_e32 v0, v0, v1
	v_med3_f32 v0, v0, s42, v139
	v_add_f32_e32 v3, 1.0, v3
	v_rcp_f32_e32 v6, v3
	v_mov_b32_e32 v4, v79
	v_or_b32_e32 v8, v8, v16
	v_cvt_pk_fp8_f32 v4, v0, 0
	v_lshl_add_u64 v[0:1], s[20:21], 0, v[8:9]
	v_mul_f32_e32 v5, v2, v6
	v_mov_b32_e32 v2, v5
	v_add_f32_e32 v3, v35, v31
	v_mul_f32_e32 v2, v2, v3
	v_med3_f32 v2, v2, s42, v139
	v_mov_b32_e32 v3, v79
	v_cvt_pk_fp8_f32 v3, v2, 0
	v_or_b32_e32 v14, v14, v16
	global_store_byte v[0:1], v4, off
	v_lshl_add_u64 v[0:1], s[20:21], 0, v[14:15]
	s_mov_b64 s[8:9], 0
	global_store_byte v[0:1], v3, off

.LBB0_757:
	s_add_i32 s12, s64, -1
	s_sub_i32 s80, s11, 64
	s_cmp_lt_u32 s12, 3
	s_cselect_b32 s80, s10, s80
	s_mul_i32 s81, s80, 0xc00
	s_add_i32 s85, s82, 0x8000
	s_mov_b32 m0, s85
	s_add_i32 s85, s82, 0x10000
	buffer_load_dwordx4 v154, s[72:75], s81 offen lds
	s_mov_b32 m0, s85
	s_add_i32 s85, s82, 0xa000
	buffer_load_dwordx4 v155, s[72:75], s81 offen lds
	s_mov_b32 m0, s85
	s_add_i32 s81, s81, 0x18000
	buffer_load_dwordx4 v154, s[72:75], s81 offen lds
	s_lshl_b32 s81, s83, 11
	s_add_i32 s85, s82, 0x4000
	s_mov_b32 m0, s85
	s_add_i32 s85, s82, 0x6000
	buffer_load_dwordx4 v158, s[76:79], s81 offen lds
	s_mov_b32 m0, s85
	s_add_i32 s81, s81, 0x10000
	buffer_load_dwordx4 v158, s[76:79], s81 offen lds
	s_mov_b32 s84, s80
	s_add_i32 s6, 0, 0x12000
	v_add_u32_e32 v199, s6, v170
	v_add_u32_e32 v204, s6, v171
	v_add_u32_e32 v205, s6, v172
	ds_read_b128 v[64:67], v180 offset:49152
	ds_read_b128 v[68:71], v180 offset:57344
	ds_read_b128 v[200:203], v181 offset:49152
	ds_read_b128 v[226:229], v181 offset:57344
	ds_read_b128 v[230:233], v182 offset:49152
	ds_read_b128 v[234:237], v182 offset:57344
	ds_read_b128 v[238:241], v183 offset:49152
	ds_read_b128 v[242:245], v183 offset:57344
	s_waitcnt lgkmcnt(7)
	v_mfma_f32_32x32x16_bf16 v[80:95], v[64:67], v[124:127], 0
	v_exp_f32_e32 v216, v128
	v_add_f32_e32 v128, 0, v222
	v_add_f32_e32 v128, v224, v128
	v_add_f32_e32 v128, v220, v128
	v_add_f32_e32 v128, v223, v128
	v_add_f32_e32 v128, v219, v128
	v_add_f32_e32 v128, v221, v128
	s_waitcnt lgkmcnt(6)
	v_mfma_f32_32x32x16_bf16 v[64:79], v[68:71], v[124:127], 0
	v_add_f32_e32 v128, v217, v128
	v_add_f32_e32 v128, v218, v128
	v_add_f32_e32 v128, v212, v128
	v_add_f32_e32 v128, v214, v128
	v_add_f32_e32 v128, v211, v128
	v_add_f32_e32 v128, v213, v128
	v_exp_f32_e32 v138, v138
	s_waitcnt lgkmcnt(5)
	v_mfma_f32_32x32x16_bf16 v[80:95], v[200:203], v[120:123], v[80:95]
	v_add_f32_e32 v128, v208, v128
	v_exp_f32_e32 v139, v139
	v_add_f32_e32 v128, v210, v128
	v_exp_f32_e32 v164, v136
	v_add_f32_e32 v128, v207, v128
	v_exp_f32_e32 v137, v137
	v_add_f32_e32 v128, v209, v128
	s_waitcnt lgkmcnt(4)
	v_mfma_f32_32x32x16_bf16 v[64:79], v[226:229], v[120:123], v[64:79]
	ds_read_b128 v[200:203], v184 offset:49152
	ds_read_b128 v[226:229], v184 offset:57344
	v_exp_f32_e32 v165, v132
	v_add_f32_e32 v128, v138, v128
	v_add_f32_e32 v128, v139, v128
	v_exp_f32_e32 v206, v130
	v_add_f32_e32 v128, v164, v128
	v_exp_f32_e32 v215, v131
	s_waitcnt lgkmcnt(5)
	v_mfma_f32_32x32x16_bf16 v[80:95], v[230:233], v[116:119], v[80:95]
	v_add_f32_e32 v128, v137, v128
	v_add_f32_e32 v128, v165, v128
	v_exp_f32_e32 v225, v129
	v_exp_f32_e32 v162, v162
	v_exp_f32_e32 v163, v163
	v_exp_f32_e32 v160, v160
	v_exp_f32_e32 v161, v161
	s_waitcnt lgkmcnt(4)
	v_mfma_f32_32x32x16_bf16 v[64:79], v[234:237], v[116:119], v[64:79]
	ds_read_b128 v[230:233], v185 offset:49152
	ds_read_b128 v[234:237], v185 offset:57344
	v_cvt_pk_bf16_f32 v129, v220, v223
	v_cvt_pk_bf16_f32 v130, v219, v221
	v_cvt_pk_bf16_f32 v131, v217, v218
	v_cvt_pk_bf16_f32 v132, v212, v214
	v_cvt_pk_bf16_f32 v136, v138, v139
	v_cvt_pk_bf16_f32 v137, v164, v137
	s_waitcnt lgkmcnt(5)
	v_mfma_f32_32x32x16_bf16 v[80:95], v[238:241], v[112:115], v[80:95]
	v_cvt_pk_bf16_f32 v139, v206, v215
	v_permlane32_swap_b32_e32 v129, v131
	s_nop 0
	v_permlane32_swap_b32_e32 v137, v139
	s_waitcnt lgkmcnt(4)
	v_mfma_f32_32x32x16_bf16 v[64:79], v[242:245], v[112:115], v[64:79]
	ds_read_b128 v[238:241], v186 offset:49152
	ds_read_b128 v[242:245], v186 offset:57344
	s_waitcnt lgkmcnt(5)
	v_mfma_f32_32x32x16_bf16 v[80:95], v[200:203], v[108:111], v[80:95]
	s_waitcnt lgkmcnt(4)
	v_mfma_f32_32x32x16_bf16 v[64:79], v[226:229], v[108:111], v[64:79]
	ds_read_b128 v[200:203], v187 offset:49152
	ds_read_b128 v[226:229], v187 offset:57344
	s_waitcnt lgkmcnt(5)
	v_mfma_f32_32x32x16_bf16 v[80:95], v[230:233], v[104:107], v[80:95]
	s_waitcnt lgkmcnt(4)
	v_mfma_f32_32x32x16_bf16 v[64:79], v[234:237], v[104:107], v[64:79]
	ds_read_b128 v[230:233], v199
	ds_read_b128 v[234:237], v199 offset:4096
	ds_read_b128 v[246:249], v190
	s_waitcnt lgkmcnt(6)
	v_mfma_f32_32x32x16_bf16 v[80:95], v[238:241], v[100:103], v[80:95]
	s_waitcnt lgkmcnt(5)
	v_mfma_f32_32x32x16_bf16 v[64:79], v[242:245], v[100:103], v[64:79]
	ds_read_b128 v[238:241], v204
	ds_read_b128 v[242:245], v204 offset:4096
	ds_read_b128 v[250:253], v190 offset:1024
	v_add_u32_e32 v204, s6, v173
	s_waitcnt lgkmcnt(7)
	v_mfma_f32_32x32x16_bf16 v[80:95], v[200:203], v[96:99], v[80:95]
	s_waitcnt lgkmcnt(6)
	v_mfma_f32_32x32x16_bf16 v[64:79], v[226:229], v[96:99], v[64:79]
	ds_read_b128 v[200:203], v205
	ds_read_b128 v[226:229], v205 offset:4096
	s_waitcnt lgkmcnt(5)
	v_mfma_f32_32x32x16_bf16 v[80:95], v[230:233], v[246:249], v[80:95]
	s_waitcnt lgkmcnt(5)
	v_mfma_f32_32x32x16_bf16 v[64:79], v[234:237], v[246:249], v[64:79]
	ds_read_b128 v[230:233], v204
	ds_read_b128 v[234:237], v204 offset:4096
	ds_read_b128 v[246:249], v190 offset:2048
	s_waitcnt lgkmcnt(5)
	v_mfma_f32_32x32x16_bf16 v[80:95], v[238:241], v[250:253], v[80:95]
	s_waitcnt lgkmcnt(5)
	v_mfma_f32_32x32x16_bf16 v[64:79], v[242:245], v[250:253], v[64:79]
	ds_read_b128 v[250:253], v190 offset:3072
	s_waitcnt lgkmcnt(1)
	v_mfma_f32_32x32x16_bf16 v[80:95], v[200:203], v[246:249], v[80:95]
	v_exp_f32_e32 v205, v133
	v_cvt_pk_bf16_f32 v133, v211, v213
	v_cvt_pk_bf16_f32 v138, v165, v205
	v_add_f32_e32 v128, v205, v128
	v_add_f32_e32 v128, v206, v128
	v_add_f32_e32 v128, v215, v128
	s_waitcnt lgkmcnt(1)
	v_mfma_f32_32x32x16_bf16 v[64:79], v[226:229], v[246:249], v[64:79]
	v_add_f32_e32 v128, v216, v128
	v_add_f32_e32 v128, v225, v128
	v_add_f32_e32 v128, v162, v128
	v_add_f32_e32 v128, v163, v128
	v_add_f32_e32 v128, v160, v128
	v_add_f32_e32 v128, v161, v128
	s_waitcnt lgkmcnt(0)
	v_mfma_f32_32x32x16_bf16 v[80:95], v[230:233], v[250:253], v[80:95]
	v_exp_f32_e32 v226, v134
	v_exp_f32_e32 v227, v135
	v_cvt_pk_bf16_f32 v134, v208, v210
	v_cvt_pk_bf16_f32 v135, v207, v209
	v_add_f32_e32 v128, v226, v128
	v_add_f32_e32 v203, v227, v128
	v_mov_b32_e32 v204, v203
	s_waitcnt lgkmcnt(0)
	v_mfma_f32_32x32x16_bf16 v[64:79], v[234:237], v[250:253], v[64:79]
	s_nop 0
	v_permlane32_swap_b32_e32 v203, v204
	v_cvt_pk_bf16_f32 v128, v222, v224
	v_cvt_pk_bf16_f32 v208, v216, v225
	v_cvt_pk_bf16_f32 v209, v162, v163
	v_cvt_pk_bf16_f32 v210, v160, v161
	v_cvt_pk_bf16_f32 v211, v226, v227
	v_permlane32_swap_b32_e32 v132, v134
	v_permlane32_swap_b32_e32 v128, v130
	v_permlane32_swap_b32_e32 v133, v135
	v_permlane32_swap_b32_e32 v136, v138
	v_permlane32_swap_b32_e32 v208, v210
	v_permlane32_swap_b32_e32 v209, v211
	ds_read_b64_tr_b16 v[160:161], v167 offset:0
	ds_read_b64_tr_b16 v[162:163], v167 offset:0x800
	ds_read_b64_tr_b16 v[232:233], v167 offset:0x1000
	ds_read_b64_tr_b16 v[234:235], v167 offset:0x1800
	ds_read_b64_tr_b16 v[236:237], v167 offset:0x2000
	ds_read_b64_tr_b16 v[238:239], v167 offset:0x2800
	ds_read_b64_tr_b16 v[240:241], v167 offset:0x3000
	ds_read_b64_tr_b16 v[242:243], v167 offset:0x3800
	v_max_f32_e32 v164, v81, v81
	v_max_f32_e32 v165, v80, v80
	v_max_f32_e32 v164, v165, v164
	v_max3_f32 v164, v164, v82, v83
	v_max3_f32 v164, v164, v84, v85
	v_max3_f32 v164, v164, v86, v87
	v_max3_f32 v164, v164, v88, v89
	v_max3_f32 v164, v164, v90, v91
	v_max3_f32 v164, v164, v92, v93
	v_max3_f32 v164, v164, v94, v95
	s_waitcnt lgkmcnt(6)
	v_mfma_f32_32x32x16_bf16 v[16:31], v[128:131], v[160:163], v[16:31]
	v_max3_f32 v160, v164, v64, v65
	v_max3_f32 v160, v160, v66, v67
	v_max3_f32 v160, v160, v68, v69
	s_waitcnt lgkmcnt(4)
	v_mfma_f32_32x32x16_bf16 v[16:31], v[132:135], v[232:235], v[16:31]
	ds_read_b64_tr_b16 v[232:233], v167 offset:0x200
	ds_read_b64_tr_b16 v[234:235], v167 offset:0xa00
	v_max3_f32 v160, v160, v70, v71
	v_max3_f32 v160, v160, v72, v73
	v_max3_f32 v160, v160, v74, v75
	s_waitcnt lgkmcnt(4)
	v_mfma_f32_32x32x16_bf16 v[16:31], v[136:139], v[236:239], v[16:31]
	ds_read_b64_tr_b16 v[236:237], v167 offset:0x1200
	ds_read_b64_tr_b16 v[238:239], v167 offset:0x1a00
	ds_read_b64_tr_b16 v[244:245], v167 offset:0x2200
	ds_read_b64_tr_b16 v[246:247], v167 offset:0x2a00
	ds_read_b64_tr_b16 v[248:249], v167 offset:0x3200
	ds_read_b64_tr_b16 v[250:251], v167 offset:0x3a00
	v_max3_f32 v160, v160, v76, v77
	v_max3_f32 v160, v160, v78, v79
	v_mov_b32_e32 v161, v160
	s_waitcnt lgkmcnt(8)
	v_mfma_f32_32x32x16_bf16 v[16:31], v[208:211], v[240:243], v[16:31]
	v_max_f32_e32 v162, v198, v198
	v_permlane32_swap_b32_e32 v160, v161
	v_max_f32_e32 v161, v161, v161
	v_max_f32_e32 v160, v160, v160
	v_max_f32_e32 v160, v160, v161
	s_waitcnt lgkmcnt(6)
	v_mfma_f32_32x32x16_bf16 v[32:47], v[128:131], v[232:235], v[32:47]
	ds_read_b64_tr_b16 v[232:233], v167 offset:0x400
	ds_read_b64_tr_b16 v[234:235], v167 offset:0xc00
	v_sub_f32_e32 v161, v160, v198
	v_max_f32_e32 v160, v162, v160
	v_sub_f32_e32 v162, v198, v160
	v_mul_f32_e32 v162, 0x3dd53b94, v162
	v_exp_f32_e32 v162, v162
	s_waitcnt lgkmcnt(6)
	v_mfma_f32_32x32x16_bf16 v[32:47], v[132:135], v[236:239], v[32:47]
	ds_read_b64_tr_b16 v[236:237], v167 offset:0x1400
	ds_read_b64_tr_b16 v[238:239], v167 offset:0x1c00
	ds_read_b64_tr_b16 v[240:241], v167 offset:0x2400
	ds_read_b64_tr_b16 v[242:243], v167 offset:0x2c00
	v_cmp_ge_f32_e32 vcc, s48, v161
	s_cmp_eq_u64 vcc, exec
	s_cselect_b64 s[6:7], -1, 0
	v_cndmask_b32_e64 v206, v162, 1.0, s[6:7]
	v_cndmask_b32_e64 v160, v160, v198, s[6:7]
	v_mul_f32_e32 v205, 0xbdd53b94, v160
	v_cmp_gt_f32_e32 vcc, 1.0, v206
	s_waitcnt lgkmcnt(8)
	v_mfma_f32_32x32x16_bf16 v[32:47], v[136:139], v[244:247], v[32:47]
	ds_read_b64_tr_b16 v[244:245], v167 offset:0x3400
	ds_read_b64_tr_b16 v[246:247], v167 offset:0x3c00
	v_fmamk_f32 v87, v87, 0x3dd53b94, v205
	v_fmamk_f32 v80, v80, 0x3dd53b94, v205
	v_fmamk_f32 v81, v81, 0x3dd53b94, v205
	v_fmamk_f32 v82, v82, 0x3dd53b94, v205
	v_fmamk_f32 v83, v83, 0x3dd53b94, v205
	s_waitcnt lgkmcnt(8)
	v_mfma_f32_32x32x16_bf16 v[32:47], v[208:211], v[248:251], v[32:47]
	v_fmamk_f32 v84, v84, 0x3dd53b94, v205
	v_fmamk_f32 v85, v85, 0x3dd53b94, v205
	v_fmamk_f32 v86, v86, 0x3dd53b94, v205
	v_fmamk_f32 v88, v88, 0x3dd53b94, v205
	v_fmamk_f32 v89, v89, 0x3dd53b94, v205
	s_waitcnt lgkmcnt(6)
	v_mfma_f32_32x32x16_bf16 v[0:15], v[128:131], v[232:235], v[0:15]
	ds_read_b64_tr_b16 v[232:233], v167 offset:0x600
	ds_read_b64_tr_b16 v[234:235], v167 offset:0xe00
	v_fmamk_f32 v90, v90, 0x3dd53b94, v205
	v_fmamk_f32 v91, v91, 0x3dd53b94, v205
	v_fmamk_f32 v92, v92, 0x3dd53b94, v205
	v_fmamk_f32 v93, v93, 0x3dd53b94, v205
	v_fmamk_f32 v94, v94, 0x3dd53b94, v205
	s_waitcnt lgkmcnt(6)
	v_mfma_f32_32x32x16_bf16 v[0:15], v[132:135], v[236:239], v[0:15]
	ds_read_b64_tr_b16 v[236:237], v167 offset:0x1600
	ds_read_b64_tr_b16 v[238:239], v167 offset:0x1e00
	v_fmamk_f32 v95, v95, 0x3dd53b94, v205
	v_fmamk_f32 v215, v64, 0x3dd53b94, v205
	v_fmamk_f32 v216, v65, 0x3dd53b94, v205
	v_fmamk_f32 v217, v66, 0x3dd53b94, v205
	v_fmamk_f32 v218, v67, 0x3dd53b94, v205
	s_waitcnt lgkmcnt(6)
	v_mfma_f32_32x32x16_bf16 v[0:15], v[136:139], v[240:243], v[0:15]
	ds_read_b64_tr_b16 v[240:241], v167 offset:0x2600
	ds_read_b64_tr_b16 v[242:243], v167 offset:0x2e00
	ds_read_b64_tr_b16 v[248:249], v167 offset:0x3600
	ds_read_b64_tr_b16 v[250:251], v167 offset:0x3e00
	v_fmamk_f32 v219, v68, 0x3dd53b94, v205
	v_fmamk_f32 v212, v73, 0x3dd53b94, v205
	v_fmamk_f32 v213, v74, 0x3dd53b94, v205
	v_fmamk_f32 v214, v75, 0x3dd53b94, v205
	s_waitcnt lgkmcnt(8)
	v_mfma_f32_32x32x16_bf16 v[0:15], v[208:211], v[244:247], v[0:15]
	v_fmamk_f32 v207, v76, 0x3dd53b94, v205
	v_fmamk_f32 v220, v77, 0x3dd53b94, v205
	v_fmamk_f32 v221, v78, 0x3dd53b94, v205
	s_waitcnt lgkmcnt(6)
	v_mfma_f32_32x32x16_bf16 v[48:63], v[128:131], v[232:235], v[48:63]
	v_exp_f32_e32 v128, v80
	v_exp_f32_e32 v129, v82
	v_exp_f32_e32 v130, v84
	v_exp_f32_e32 v131, v86
	s_waitcnt lgkmcnt(4)
	v_mfma_f32_32x32x16_bf16 v[48:63], v[132:135], v[236:239], v[48:63]
	v_exp_f32_e32 v132, v88
	v_exp_f32_e32 v133, v90
	v_exp_f32_e32 v134, v92
	v_exp_f32_e32 v135, v94
	s_waitcnt lgkmcnt(2)
	v_mfma_f32_32x32x16_bf16 v[48:63], v[136:139], v[240:243], v[48:63]
	v_exp_f32_e32 v139, v89
	v_exp_f32_e32 v138, v91
	v_exp_f32_e32 v137, v93
	v_exp_f32_e32 v136, v95
	s_waitcnt lgkmcnt(0)
	v_mfma_f32_32x32x16_bf16 v[48:63], v[208:211], v[248:251], v[48:63]
	v_exp_f32_e32 v161, v87
	v_exp_f32_e32 v198, v81
	v_exp_f32_e32 v163, v83
	v_exp_f32_e32 v162, v85
	v_fmamk_f32 v208, v69, 0x3dd53b94, v205
	v_fmamk_f32 v209, v70, 0x3dd53b94, v205
	v_fmamk_f32 v210, v71, 0x3dd53b94, v205
	v_fmamk_f32 v211, v72, 0x3dd53b94, v205
	v_fmac_f32_e32 v205, 0x3dd53b94, v79
	s_cbranch_vccz .LBB0_761
	s_and_saveexec_b64 s[8:9], s[4:5]
	ds_write_b32 v189, v206 offset:128
	s_or_b64 exec, exec, s[8:9]
	s_waitcnt lgkmcnt(0)
	v_add_u32_e32 v248, s62, v169
	ds_read_b128 v[232:235], v248 offset:224
	ds_read_b128 v[236:239], v248 offset:192
	ds_read_b128 v[240:243], v248 offset:160
	ds_read_b128 v[244:247], v248 offset:128
	s_waitcnt lgkmcnt(3)
	v_pk_mul_f32 v[28:29], v[28:29], v[232:233]
	s_waitcnt lgkmcnt(2)
	v_pk_mul_f32 v[24:25], v[24:25], v[236:237]
	s_waitcnt lgkmcnt(1)
	v_pk_mul_f32 v[20:21], v[20:21], v[240:241]
	v_pk_mul_f32 v[30:31], v[30:31], v[234:235]
	v_pk_mul_f32 v[26:27], v[26:27], v[238:239]
	v_pk_mul_f32 v[22:23], v[22:23], v[242:243]
	s_waitcnt lgkmcnt(0)
	v_pk_mul_f32 v[18:19], v[18:19], v[246:247]
	v_pk_mul_f32 v[16:17], v[16:17], v[244:245]
	v_pk_mul_f32 v[44:45], v[44:45], v[232:233]
	v_pk_mul_f32 v[40:41], v[40:41], v[236:237]
	v_pk_mul_f32 v[36:37], v[36:37], v[240:241]
	v_pk_mul_f32 v[46:47], v[46:47], v[234:235]
	v_pk_mul_f32 v[42:43], v[42:43], v[238:239]
	v_pk_mul_f32 v[38:39], v[38:39], v[242:243]
	v_pk_mul_f32 v[34:35], v[34:35], v[246:247]
	v_pk_mul_f32 v[32:33], v[32:33], v[244:245]
	v_pk_mul_f32 v[12:13], v[12:13], v[232:233]
	v_pk_mul_f32 v[8:9], v[8:9], v[236:237]
	v_pk_mul_f32 v[4:5], v[4:5], v[240:241]
	v_pk_mul_f32 v[14:15], v[14:15], v[234:235]
	v_pk_mul_f32 v[10:11], v[10:11], v[238:239]
	v_pk_mul_f32 v[6:7], v[6:7], v[242:243]
	v_pk_mul_f32 v[2:3], v[2:3], v[246:247]
	v_pk_mul_f32 v[0:1], v[0:1], v[244:245]
	v_pk_mul_f32 v[60:61], v[60:61], v[232:233]
	v_pk_mul_f32 v[56:57], v[56:57], v[236:237]
	v_pk_mul_f32 v[52:53], v[52:53], v[240:241]
	v_pk_mul_f32 v[62:63], v[62:63], v[234:235]
	v_pk_mul_f32 v[58:59], v[58:59], v[238:239]
	v_pk_mul_f32 v[54:55], v[54:55], v[242:243]
	v_pk_mul_f32 v[50:51], v[50:51], v[246:247]
	v_pk_mul_f32 v[48:49], v[48:49], v[244:245]
.LBB0_761:
	s_waitcnt vmcnt(0) lgkmcnt(0)
	s_barrier
	s_add_i32 s80, s10, 64
	s_cmp_lt_u32 s12, 2
	s_cselect_b32 s80, s80, s11
	s_mul_i32 s81, s80, 0xc00
	s_add_i32 s85, s82, 0xc000
	s_mov_b32 m0, s85
	s_add_i32 s85, s82, 0x12000
	buffer_load_dwordx4 v154, s[72:75], s81 offen lds
	s_mov_b32 m0, s85
	s_add_i32 s85, s82, 0xe000
	buffer_load_dwordx4 v155, s[72:75], s81 offen lds
	s_mov_b32 m0, s85
	s_add_i32 s81, s81, 0x18000
	buffer_load_dwordx4 v154, s[72:75], s81 offen lds
	s_lshl_b32 s81, s84, 11
	s_add_i32 s85, s82, 0x0
	s_mov_b32 m0, s85
	s_add_i32 s85, s82, 0x2000
	buffer_load_dwordx4 v158, s[76:79], s81 offen lds
	s_mov_b32 m0, s85
	s_add_i32 s81, s81, 0x10000
	buffer_load_dwordx4 v158, s[76:79], s81 offen lds
	s_mov_b32 s83, s80
	ds_read_b128 v[64:67], v180 offset:32768
	ds_read_b128 v[68:71], v180 offset:40960
	ds_read_b128 v[222:225], v181 offset:32768
	ds_read_b128 v[226:229], v181 offset:40960
	ds_read_b128 v[230:233], v182 offset:32768
	ds_read_b128 v[234:237], v182 offset:40960
	ds_read_b128 v[238:241], v183 offset:32768
	ds_read_b128 v[242:245], v183 offset:40960
	v_exp_f32_e32 v164, v215
	v_add_f32_e32 v215, 0, v128
	s_waitcnt lgkmcnt(7)
	v_mfma_f32_32x32x16_bf16 v[80:95], v[64:67], v[124:127], 0
	v_add_f32_e32 v215, v198, v215
	v_add_f32_e32 v215, v129, v215
	v_add_f32_e32 v215, v163, v215
	v_add_f32_e32 v215, v130, v215
	v_add_f32_e32 v215, v162, v215
	v_add_f32_e32 v215, v131, v215
	v_add_f32_e32 v215, v161, v215
	s_waitcnt lgkmcnt(6)
	v_mfma_f32_32x32x16_bf16 v[64:79], v[68:71], v[124:127], 0
	v_add_f32_e32 v215, v132, v215
	v_add_f32_e32 v215, v139, v215
	v_add_f32_e32 v215, v133, v215
	v_add_f32_e32 v215, v138, v215
	v_add_f32_e32 v215, v134, v215
	v_exp_f32_e32 v165, v216
	v_add_f32_e32 v215, v137, v215
	s_waitcnt lgkmcnt(5)
	v_mfma_f32_32x32x16_bf16 v[80:95], v[222:225], v[120:123], v[80:95]
	v_exp_f32_e32 v217, v217
	v_add_f32_e32 v215, v135, v215
	v_exp_f32_e32 v218, v218
	v_add_f32_e32 v215, v136, v215
	v_exp_f32_e32 v219, v219
	v_add_f32_e32 v215, v164, v215
	v_exp_f32_e32 v208, v208
	s_waitcnt lgkmcnt(4)
	v_mfma_f32_32x32x16_bf16 v[64:79], v[226:229], v[120:123], v[64:79]
	ds_read_b128 v[222:225], v184 offset:32768
	ds_read_b128 v[226:229], v184 offset:40960
	v_add_f32_e32 v215, v165, v215
	v_exp_f32_e32 v209, v209
	v_add_f32_e32 v215, v217, v215
	v_exp_f32_e32 v210, v210
	v_add_f32_e32 v215, v218, v215
	v_exp_f32_e32 v211, v211
	s_waitcnt lgkmcnt(5)
	v_mfma_f32_32x32x16_bf16 v[80:95], v[230:233], v[116:119], v[80:95]
	v_add_f32_e32 v215, v219, v215
	v_exp_f32_e32 v212, v212
	v_add_f32_e32 v215, v208, v215
	v_exp_f32_e32 v213, v213
	v_add_f32_e32 v215, v209, v215
	v_exp_f32_e32 v214, v214
	v_add_f32_e32 v215, v210, v215
	s_waitcnt lgkmcnt(4)
	v_mfma_f32_32x32x16_bf16 v[64:79], v[234:237], v[116:119], v[64:79]
	ds_read_b128 v[230:233], v185 offset:32768
	ds_read_b128 v[234:237], v185 offset:40960
	v_exp_f32_e32 v207, v207
	v_add_f32_e32 v215, v211, v215
	v_exp_f32_e32 v220, v220
	v_add_f32_e32 v215, v212, v215
	v_exp_f32_e32 v221, v221
	v_add_f32_e32 v215, v213, v215
	s_waitcnt lgkmcnt(5)
	v_mfma_f32_32x32x16_bf16 v[80:95], v[238:241], v[112:115], v[80:95]
	v_exp_f32_e32 v205, v205
	v_add_f32_e32 v215, v214, v215
	v_add_f32_e32 v215, v207, v215
	v_add_f32_e32 v215, v220, v215
	v_add_f32_e32 v215, v221, v215
	v_add_f32_e32 v215, v205, v215
	v_mov_b32_e32 v216, v215
	s_waitcnt lgkmcnt(4)
	v_mfma_f32_32x32x16_bf16 v[64:79], v[242:245], v[112:115], v[64:79]
	ds_read_b128 v[238:241], v186 offset:32768
	ds_read_b128 v[242:245], v186 offset:40960
	v_permlane32_swap_b32_e32 v215, v216
	v_cvt_pk_bf16_f32 v128, v128, v198
	v_cvt_pk_bf16_f32 v129, v129, v163
	v_cvt_pk_bf16_f32 v130, v130, v162
	v_cvt_pk_bf16_f32 v131, v131, v161
	s_waitcnt lgkmcnt(5)
	v_mfma_f32_32x32x16_bf16 v[80:95], v[222:225], v[108:111], v[80:95]
	v_cvt_pk_bf16_f32 v132, v132, v139
	v_cvt_pk_bf16_f32 v133, v133, v138
	v_cvt_pk_bf16_f32 v134, v134, v137
	v_cvt_pk_bf16_f32 v135, v135, v136
	v_cvt_pk_bf16_f32 v136, v164, v165
	v_cvt_pk_bf16_f32 v137, v217, v218
	v_cvt_pk_bf16_f32 v138, v219, v208
	s_waitcnt lgkmcnt(4)
	v_mfma_f32_32x32x16_bf16 v[64:79], v[226:229], v[108:111], v[64:79]
	ds_read_b128 v[222:225], v187 offset:32768
	ds_read_b128 v[226:229], v187 offset:40960
	v_cvt_pk_bf16_f32 v139, v209, v210
	v_cvt_pk_bf16_f32 v208, v211, v212
	v_cvt_pk_bf16_f32 v209, v213, v214
	v_cvt_pk_bf16_f32 v210, v207, v220
	v_cvt_pk_bf16_f32 v211, v221, v205
	v_permlane32_swap_b32_e32 v128, v130
	s_waitcnt lgkmcnt(5)
	v_mfma_f32_32x32x16_bf16 v[80:95], v[230:233], v[104:107], v[80:95]
	v_permlane32_swap_b32_e32 v129, v131
	v_permlane32_swap_b32_e32 v132, v134
	v_permlane32_swap_b32_e32 v133, v135
	v_permlane32_swap_b32_e32 v136, v138
	s_waitcnt lgkmcnt(4)
	v_mfma_f32_32x32x16_bf16 v[64:79], v[234:237], v[104:107], v[64:79]
	ds_read_b128 v[230:233], v191
	ds_read_b128 v[234:237], v191 offset:4096
	ds_read_b128 v[246:249], v190
	v_permlane32_swap_b32_e32 v137, v139
	v_permlane32_swap_b32_e32 v208, v210
	v_permlane32_swap_b32_e32 v209, v211
	s_waitcnt lgkmcnt(6)
	v_mfma_f32_32x32x16_bf16 v[80:95], v[238:241], v[100:103], v[80:95]
	s_waitcnt lgkmcnt(5)
	v_mfma_f32_32x32x16_bf16 v[64:79], v[242:245], v[100:103], v[64:79]
	ds_read_b128 v[238:241], v192
	ds_read_b128 v[242:245], v192 offset:4096
	ds_read_b128 v[250:253], v190 offset:1024
	s_waitcnt lgkmcnt(7)
	v_mfma_f32_32x32x16_bf16 v[80:95], v[222:225], v[96:99], v[80:95]
	s_waitcnt lgkmcnt(6)
	v_mfma_f32_32x32x16_bf16 v[64:79], v[226:229], v[96:99], v[64:79]
	ds_read_b128 v[222:225], v193
	ds_read_b128 v[226:229], v193 offset:4096
	s_waitcnt lgkmcnt(5)
	v_mfma_f32_32x32x16_bf16 v[80:95], v[230:233], v[246:249], v[80:95]
	s_waitcnt lgkmcnt(5)
	v_mfma_f32_32x32x16_bf16 v[64:79], v[234:237], v[246:249], v[64:79]
	ds_read_b128 v[230:233], v194
	ds_read_b128 v[234:237], v194 offset:4096
	ds_read_b128 v[246:249], v190 offset:2048
	s_waitcnt lgkmcnt(5)
	v_mfma_f32_32x32x16_bf16 v[80:95], v[238:241], v[250:253], v[80:95]
	s_waitcnt lgkmcnt(5)
	v_mfma_f32_32x32x16_bf16 v[64:79], v[242:245], v[250:253], v[64:79]
	ds_read_b128 v[250:253], v190 offset:3072
	s_waitcnt lgkmcnt(1)
	v_mfma_f32_32x32x16_bf16 v[80:95], v[222:225], v[246:249], v[80:95]
	s_waitcnt lgkmcnt(1)
	v_mfma_f32_32x32x16_bf16 v[64:79], v[226:229], v[246:249], v[64:79]
	s_waitcnt lgkmcnt(0)
	v_mfma_f32_32x32x16_bf16 v[80:95], v[230:233], v[250:253], v[80:95]
	s_waitcnt lgkmcnt(0)
	v_mfma_f32_32x32x16_bf16 v[64:79], v[234:237], v[250:253], v[64:79]
	ds_read_b64_tr_b16 v[238:239], v174 offset:0
	ds_read_b64_tr_b16 v[240:241], v174 offset:0x800
	ds_read_b64_tr_b16 v[242:243], v174 offset:0x1000
	ds_read_b64_tr_b16 v[244:245], v174 offset:0x1800
	ds_read_b64_tr_b16 v[246:247], v174 offset:0x2000
	ds_read_b64_tr_b16 v[248:249], v174 offset:0x2800
	ds_read_b64_tr_b16 v[250:251], v174 offset:0x3000
	ds_read_b64_tr_b16 v[252:253], v174 offset:0x3800
	s_nop 3
	v_max_f32_e32 v161, v81, v81
	v_max_f32_e32 v162, v80, v80
	v_max_f32_e32 v161, v162, v161
	v_max3_f32 v161, v161, v82, v83
	v_max3_f32 v161, v161, v84, v85
	v_max3_f32 v161, v161, v86, v87
	v_max3_f32 v161, v161, v88, v89
	v_max3_f32 v161, v161, v90, v91
	v_max3_f32 v161, v161, v92, v93
	v_max3_f32 v161, v161, v94, v95
	s_waitcnt lgkmcnt(6)
	v_mfma_f32_32x32x16_bf16 v[16:31], v[128:131], v[238:241], v[16:31]
	ds_read_b64_tr_b16 v[238:239], v174 offset:0x200
	ds_read_b64_tr_b16 v[240:241], v174 offset:0xa00
	v_max3_f32 v161, v161, v64, v65
	v_max3_f32 v161, v161, v66, v67
	v_max3_f32 v161, v161, v68, v69
	s_waitcnt lgkmcnt(6)
	v_mfma_f32_32x32x16_bf16 v[16:31], v[132:135], v[242:245], v[16:31]
	ds_read_b64_tr_b16 v[242:243], v174 offset:0x1200
	ds_read_b64_tr_b16 v[244:245], v174 offset:0x1a00
	v_max3_f32 v161, v161, v70, v71
	v_max3_f32 v161, v161, v72, v73
	v_max3_f32 v161, v161, v74, v75
	s_waitcnt lgkmcnt(6)
	v_mfma_f32_32x32x16_bf16 v[16:31], v[136:139], v[246:249], v[16:31]
	ds_read_b64_tr_b16 v[246:247], v174 offset:0x2200
	ds_read_b64_tr_b16 v[248:249], v174 offset:0x2a00
	ds_read_b64_tr_b16 v[162:163], v174 offset:0x3200
	ds_read_b64_tr_b16 v[164:165], v174 offset:0x3a00
	v_max3_f32 v161, v161, v76, v77
	v_max3_f32 v161, v161, v78, v79
	v_mov_b32_e32 v198, v161
	s_waitcnt lgkmcnt(8)
	v_mfma_f32_32x32x16_bf16 v[16:31], v[208:211], v[250:253], v[16:31]
	v_max_f32_e32 v205, v160, v160
	v_permlane32_swap_b32_e32 v161, v198
	v_max_f32_e32 v198, v198, v198
	v_max_f32_e32 v161, v161, v161
	v_max_f32_e32 v161, v161, v198
	s_waitcnt lgkmcnt(6)
	v_mfma_f32_32x32x16_bf16 v[32:47], v[128:131], v[238:241], v[32:47]
	ds_read_b64_tr_b16 v[238:239], v174 offset:0x400
	ds_read_b64_tr_b16 v[240:241], v174 offset:0xc00
	v_sub_f32_e32 v198, v161, v160
	v_max_f32_e32 v161, v205, v161
	v_sub_f32_e32 v205, v160, v161
	v_mul_f32_e32 v205, 0x3dd53b94, v205
	v_exp_f32_e32 v205, v205
	s_waitcnt lgkmcnt(6)
	v_mfma_f32_32x32x16_bf16 v[32:47], v[132:135], v[242:245], v[32:47]
	ds_read_b64_tr_b16 v[242:243], v174 offset:0x1400
	ds_read_b64_tr_b16 v[244:245], v174 offset:0x1c00
	v_cmp_ge_f32_e32 vcc, s48, v198
	s_cmp_eq_u64 vcc, exec
	s_cselect_b64 s[6:7], -1, 0
	v_cndmask_b32_e64 v205, v205, 1.0, s[6:7]
	v_cndmask_b32_e64 v198, v161, v160, s[6:7]
	v_mul_f32_e32 v236, 0xbdd53b94, v198
	v_mov_b32_e32 v237, v236
	v_cmp_gt_f32_e32 vcc, 1.0, v205
	s_waitcnt lgkmcnt(6)
	v_mfma_f32_32x32x16_bf16 v[32:47], v[136:139], v[246:249], v[32:47]
	ds_read_b64_tr_b16 v[246:247], v174 offset:0x2400
	ds_read_b64_tr_b16 v[248:249], v174 offset:0x2c00
	ds_read_b64_tr_b16 v[250:251], v174 offset:0x3400
	ds_read_b64_tr_b16 v[252:253], v174 offset:0x3c00
	v_fmamk_f32 v80, v80, 0x3dd53b94, v236
	v_fmamk_f32 v81, v81, 0x3dd53b94, v236
	v_fmamk_f32 v82, v82, 0x3dd53b94, v236
	v_fmamk_f32 v83, v83, 0x3dd53b94, v236
	s_waitcnt lgkmcnt(8)
	v_mfma_f32_32x32x16_bf16 v[32:47], v[208:211], v[162:165], v[32:47]
	v_fmamk_f32 v84, v84, 0x3dd53b94, v236
	v_fmamk_f32 v85, v85, 0x3dd53b94, v236
	v_fmamk_f32 v86, v86, 0x3dd53b94, v236
	v_fmamk_f32 v87, v87, 0x3dd53b94, v236
	s_waitcnt lgkmcnt(6)
	v_mfma_f32_32x32x16_bf16 v[0:15], v[128:131], v[238:241], v[0:15]
	ds_read_b64_tr_b16 v[162:163], v174 offset:0x600
	ds_read_b64_tr_b16 v[164:165], v174 offset:0xe00
	ds_read_b64_tr_b16 v[238:239], v174 offset:0x1600
	ds_read_b64_tr_b16 v[240:241], v174 offset:0x1e00
	v_fmamk_f32 v88, v88, 0x3dd53b94, v236
	v_fmamk_f32 v89, v89, 0x3dd53b94, v236
	v_fmamk_f32 v90, v90, 0x3dd53b94, v236
	v_fmamk_f32 v91, v91, 0x3dd53b94, v236
	s_waitcnt lgkmcnt(8)
	v_mfma_f32_32x32x16_bf16 v[0:15], v[132:135], v[242:245], v[0:15]
	ds_read_b64_tr_b16 v[242:243], v174 offset:0x2600
	ds_read_b64_tr_b16 v[244:245], v174 offset:0x2e00
	v_fmamk_f32 v92, v92, 0x3dd53b94, v236
	v_fmamk_f32 v93, v93, 0x3dd53b94, v236
	v_fmamk_f32 v94, v94, 0x3dd53b94, v236
	v_fmamk_f32 v95, v95, 0x3dd53b94, v236
	s_waitcnt lgkmcnt(8)
	v_mfma_f32_32x32x16_bf16 v[0:15], v[136:139], v[246:249], v[0:15]
	ds_read_b64_tr_b16 v[246:247], v174 offset:0x3600
	ds_read_b64_tr_b16 v[248:249], v174 offset:0x3e00
	v_exp_f32_e32 v222, v80
	v_exp_f32_e32 v224, v81
	v_exp_f32_e32 v220, v82
	s_waitcnt lgkmcnt(8)
	v_mfma_f32_32x32x16_bf16 v[0:15], v[208:211], v[250:253], v[0:15]
	v_exp_f32_e32 v223, v83
	v_exp_f32_e32 v219, v84
	v_exp_f32_e32 v221, v85
	s_waitcnt lgkmcnt(6)
	v_mfma_f32_32x32x16_bf16 v[48:63], v[128:131], v[162:165], v[48:63]
	v_exp_f32_e32 v217, v86
	v_exp_f32_e32 v218, v87
	v_exp_f32_e32 v212, v88
	v_pk_fma_f32 v[130:131], v[70:71], s[28:29], v[236:237] op_sel_hi:[1,0,0]
	v_pk_fma_f32 v[128:129], v[72:73], s[28:29], v[236:237] op_sel_hi:[1,0,0]
	s_waitcnt lgkmcnt(4)
	v_mfma_f32_32x32x16_bf16 v[48:63], v[132:135], v[238:241], v[48:63]
	v_exp_f32_e32 v214, v89
	v_exp_f32_e32 v213, v91
	v_exp_f32_e32 v207, v94
	v_pk_fma_f32 v[132:133], v[68:69], s[28:29], v[236:237] op_sel_hi:[1,0,0]
	v_pk_fma_f32 v[134:135], v[78:79], s[28:29], v[236:237] op_sel_hi:[1,0,0]
	s_waitcnt lgkmcnt(2)
	v_mfma_f32_32x32x16_bf16 v[48:63], v[136:139], v[242:245], v[48:63]
	v_pk_fma_f32 v[138:139], v[64:65], s[28:29], v[236:237] op_sel_hi:[1,0,0]
	v_pk_fma_f32 v[136:137], v[66:67], s[28:29], v[236:237] op_sel_hi:[1,0,0]
	v_pk_fma_f32 v[162:163], v[74:75], s[28:29], v[236:237] op_sel_hi:[1,0,0]
	v_pk_fma_f32 v[160:161], v[76:77], s[28:29], v[236:237] op_sel_hi:[1,0,0]
	s_waitcnt lgkmcnt(0)
	v_mfma_f32_32x32x16_bf16 v[48:63], v[208:211], v[246:249], v[48:63]
	v_exp_f32_e32 v211, v90
	v_exp_f32_e32 v208, v92
	v_exp_f32_e32 v210, v93
	v_exp_f32_e32 v209, v95
	v_add_f32_e32 v64, v203, v204
	v_fmac_f32_e32 v64, v197, v140
	v_add_f32_e32 v140, v215, v216
	s_addk_i32 s10, 0x80
	s_add_i32 s64, s64, 2
	s_addk_i32 s11, 0x80
	v_fmac_f32_e32 v140, v64, v206
	s_cbranch_vccz .LBB0_765
	s_and_saveexec_b64 s[8:9], s[4:5]
	ds_write_b32 v189, v205 offset:128
	s_or_b64 exec, exec, s[8:9]
	s_waitcnt lgkmcnt(0)
	v_add_u32_e32 v164, s62, v169
	ds_read_b128 v[238:241], v164 offset:224
	ds_read_b128 v[242:245], v164 offset:192
	ds_read_b128 v[246:249], v164 offset:160
	ds_read_b128 v[250:253], v164 offset:128
	s_waitcnt lgkmcnt(3)
	v_pk_mul_f32 v[28:29], v[28:29], v[238:239]
	s_waitcnt lgkmcnt(2)
	v_pk_mul_f32 v[24:25], v[24:25], v[242:243]
	s_waitcnt lgkmcnt(1)
	v_pk_mul_f32 v[20:21], v[20:21], v[246:247]
	v_pk_mul_f32 v[30:31], v[30:31], v[240:241]
	v_pk_mul_f32 v[26:27], v[26:27], v[244:245]
	v_pk_mul_f32 v[22:23], v[22:23], v[248:249]
	s_waitcnt lgkmcnt(0)
	v_pk_mul_f32 v[18:19], v[18:19], v[252:253]
	v_pk_mul_f32 v[16:17], v[16:17], v[250:251]
	v_pk_mul_f32 v[44:45], v[44:45], v[238:239]
	v_pk_mul_f32 v[40:41], v[40:41], v[242:243]
	v_pk_mul_f32 v[36:37], v[36:37], v[246:247]
	v_pk_mul_f32 v[46:47], v[46:47], v[240:241]
	v_pk_mul_f32 v[42:43], v[42:43], v[244:245]
	v_pk_mul_f32 v[38:39], v[38:39], v[248:249]
	v_pk_mul_f32 v[34:35], v[34:35], v[252:253]
	v_pk_mul_f32 v[32:33], v[32:33], v[250:251]
	v_pk_mul_f32 v[12:13], v[12:13], v[238:239]
	v_pk_mul_f32 v[8:9], v[8:9], v[242:243]
	v_pk_mul_f32 v[4:5], v[4:5], v[246:247]
	v_pk_mul_f32 v[14:15], v[14:15], v[240:241]
	v_pk_mul_f32 v[10:11], v[10:11], v[244:245]
	v_pk_mul_f32 v[6:7], v[6:7], v[248:249]
	v_pk_mul_f32 v[2:3], v[2:3], v[252:253]
	v_pk_mul_f32 v[0:1], v[0:1], v[250:251]
	v_pk_mul_f32 v[60:61], v[60:61], v[238:239]
	v_pk_mul_f32 v[56:57], v[56:57], v[242:243]
	v_pk_mul_f32 v[52:53], v[52:53], v[246:247]
	v_pk_mul_f32 v[62:63], v[62:63], v[240:241]
	v_pk_mul_f32 v[58:59], v[58:59], v[244:245]
	v_pk_mul_f32 v[54:55], v[54:55], v[248:249]
	v_pk_mul_f32 v[50:51], v[50:51], v[252:253]
	v_pk_mul_f32 v[48:49], v[48:49], v[250:251]

.LBB0_791:
	s_waitcnt lgkmcnt(0)
	s_barrier
	ds_read_b128 v[0:3], v146
	ds_read_b128 v[4:7], v147
	ds_read_b128 v[120:123], v146 offset:32
	ds_read_b128 v[124:127], v147 offset:32
	s_waitcnt lgkmcnt(0)
	v_mfma_f32_32x32x16_bf16 v[0:15], v[0:3], v[4:7], 0
	v_add_u32_e32 v132, 0x4a00, v154
	v_mfma_f32_32x32x16_bf16 v[0:15], v[120:123], v[124:127], v[0:15]
	ds_read_b128 v[120:123], v146 offset:64
	ds_read_b128 v[124:127], v147 offset:64
	ds_read_b128 v[160:163], v146 offset:96
	ds_read_b128 v[164:167], v147 offset:96
	s_waitcnt lgkmcnt(2)
	v_mfma_f32_32x32x16_bf16 v[0:15], v[120:123], v[124:127], v[0:15]
	s_waitcnt lgkmcnt(0)
	v_mfma_f32_32x32x16_bf16 v[0:15], v[160:163], v[164:167], v[0:15]
	s_nop 11
	v_cndmask_b32_e64 v0, 0, v0, s[6:7]
	v_cndmask_b32_e64 v1, 0, v1, s[8:9]
	v_cndmask_b32_e64 v2, 0, v2, s[10:11]
	v_cndmask_b32_e64 v3, 0, v3, s[12:13]
	v_cndmask_b32_e64 v4, 0, v4, s[14:15]
	v_cndmask_b32_e64 v5, 0, v5, s[16:17]
	v_cndmask_b32_e64 v6, 0, v6, s[18:19]
	v_cndmask_b32_e64 v7, 0, v7, s[20:21]
	v_cndmask_b32_e64 v8, 0, v8, s[22:23]
	v_cndmask_b32_e64 v9, 0, v9, s[24:25]
	v_cvt_pk_bf16_f32 v0, v0, v0
	v_cvt_pk_bf16_f32 v1, v1, v1
	v_cvt_pk_bf16_f32 v2, v2, v2
	v_cvt_pk_bf16_f32 v3, v3, v3
	v_cvt_pk_bf16_f32 v4, v4, v4
	v_cvt_pk_bf16_f32 v5, v5, v5
	v_cvt_pk_bf16_f32 v6, v6, v6
	v_cvt_pk_bf16_f32 v7, v7, v7
	v_cvt_pk_bf16_f32 v8, v8, v8
	v_cvt_pk_bf16_f32 v9, v9, v9
	ds_write_b16 v151, v0
	ds_write_b16 v151, v1 offset:144
	ds_write_b16 v151, v2 offset:288
	ds_write_b16 v151, v3 offset:432
	ds_write_b16 v151, v4 offset:1152
	ds_write_b16 v151, v5 offset:1296
	ds_write_b16 v151, v6 offset:1440
	ds_write_b16 v151, v7 offset:1584
	ds_write_b16 v151, v8 offset:2304
	ds_write_b16 v151, v9 offset:2448
	v_cndmask_b32_e64 v0, 0, v10, s[26:27]
	v_cvt_pk_bf16_f32 v0, v0, v0
	ds_write_b16 v151, v0 offset:2592
	v_cndmask_b32_e64 v0, 0, v11, s[28:29]
	v_cvt_pk_bf16_f32 v0, v0, v0
	ds_write_b16 v151, v0 offset:2736
	v_cndmask_b32_e64 v0, 0, v12, s[30:31]
	v_cvt_pk_bf16_f32 v0, v0, v0
	ds_write_b16 v151, v0 offset:3456
	v_cndmask_b32_e64 v0, 0, v13, s[34:35]
	v_cvt_pk_bf16_f32 v0, v0, v0
	ds_write_b16 v151, v0 offset:3600
	v_cndmask_b32_e64 v0, 0, v14, s[36:37]
	v_cvt_pk_bf16_f32 v0, v0, v0
	ds_write_b16 v151, v0 offset:3744
	v_cndmask_b32_e64 v0, 0, v15, s[38:39]
	v_cvt_pk_bf16_f32 v0, v0, v0
	ds_write_b16 v151, v0 offset:3888
	s_waitcnt lgkmcnt(0)
	s_barrier
	ds_read_b128 v[0:3], v148
	ds_read_b128 v[120:123], v149
	ds_read_b128 v[124:127], v148 offset:32
	ds_read_b128 v[160:163], v149 offset:32
	s_waitcnt lgkmcnt(2)
	v_mfma_f32_32x32x16_bf16 v[0:15], v[0:3], v[120:123], 0
	s_waitcnt lgkmcnt(0)
	v_mfma_f32_32x32x16_bf16 v[0:15], v[124:127], v[160:163], v[0:15]
	ds_read_b128 v[124:127], v148 offset:64
	ds_read_b128 v[164:167], v149 offset:64
	ds_read_b128 v[168:171], v148 offset:96
	ds_read_b128 v[172:175], v149 offset:96
	s_waitcnt lgkmcnt(2)
	v_mfma_f32_32x32x16_bf16 v[0:15], v[124:127], v[164:167], v[0:15]
	s_waitcnt lgkmcnt(0)
	v_mfma_f32_32x32x16_bf16 v[0:15], v[168:171], v[172:175], v[0:15]
	ds_read_b128 v[124:127], v148 offset:9216
	ds_read_b128 v[168:171], v148 offset:9248
	s_waitcnt lgkmcnt(1)
	v_mfma_f32_32x32x16_bf16 v[0:15], v[124:127], v[120:123], v[0:15]
	ds_read_b128 v[120:123], v148 offset:9280
	ds_read_b128 v[124:127], v148 offset:9312
	s_waitcnt lgkmcnt(2)
	v_mfma_f32_32x32x16_bf16 v[0:15], v[168:171], v[160:163], v[0:15]
	v_add_u32_e32 v160, 0x4e00, v154
	v_add_u32_e32 v161, 0x5a00, v154
	v_add_u32_e32 v162, 0x5e00, v154
	v_add_u32_e32 v163, 0x6a00, v154
	v_lshlrev_b32_e32 v171, 2, v138
	v_and_b32_e32 v168, 64, v157
	v_xor_b32_e32 v169, 2, v157
	s_waitcnt lgkmcnt(1)
	v_mfma_f32_32x32x16_bf16 v[0:15], v[120:123], v[164:167], v[0:15]
	ds_read_b128 v[120:123], v152 offset:53760
	v_add_u32_e32 v164, 0x6e00, v154
	v_add_u32_e32 v165, 0x7a00, v154
	v_add_u32_e32 v166, 0x7e00, v154
	v_xor_b32_e32 v167, 1, v157
	v_xor_b32_e32 v170, 4, v157
	s_waitcnt lgkmcnt(1)
	v_mfma_f32_32x32x16_bf16 v[0:15], v[124:127], v[172:175], v[0:15]
	ds_read_b128 v[124:127], v152 offset:53792
	s_waitcnt vmcnt(1)
	v_lshlrev_b32_e32 v172, 16, v84
	v_and_b32_e32 v84, 0xffff0000, v84
	s_waitcnt lgkmcnt(1)
	v_mfma_f32_32x32x16_bf16 v[0:15], v[120:123], v[116:119], v[0:15]
	ds_read_b128 v[116:119], v152 offset:53824
	v_add_u32_e32 v121, 64, v168
	v_cmp_lt_i32_e32 vcc, v167, v121
	v_mul_f32_e32 v122, 0xbfb8aa3b, v172
	v_lshlrev_b32_e32 v120, 16, v85
	v_mul_f32_e32 v123, 0xbfb8aa3b, v84
	v_and_b32_e32 v85, 0xffff0000, v85
	s_waitcnt lgkmcnt(1)
	v_mfma_f32_32x32x16_bf16 v[0:15], v[124:127], v[112:115], v[0:15]
	ds_read_b128 v[112:115], v152 offset:53856
	v_cndmask_b32_e32 v126, v157, v167, vcc
	v_cmp_lt_i32_e32 vcc, v169, v121
	v_mul_f32_e32 v124, 0xbfb8aa3b, v120
	v_mul_f32_e32 v125, 0xbfb8aa3b, v85
	v_cndmask_b32_e32 v127, v157, v169, vcc
	v_cmp_lt_i32_e32 vcc, v170, v121
	s_waitcnt lgkmcnt(1)
	v_mfma_f32_32x32x16_bf16 v[0:15], v[116:119], v[108:111], v[0:15]
	ds_read_b128 v[108:111], v153
	v_exp_f32_e32 v117, v122
	v_lshlrev_b32_e32 v122, 2, v126
	v_cndmask_b32_e32 v116, v157, v170, vcc
	v_exp_f32_e32 v118, v123
	v_exp_f32_e32 v119, v124
	v_exp_f32_e32 v121, v125
	s_waitcnt lgkmcnt(1)
	v_mfma_f32_32x32x16_bf16 v[0:15], v[112:115], v[104:107], v[0:15]
	ds_read_b128 v[104:107], v153 offset:32
	v_lshlrev_b32_e32 v112, 2, v127
	v_lshlrev_b32_e32 v113, 2, v116
	v_add_f32_e32 v114, 1.0, v117
	v_add_f32_e32 v115, 1.0, v118
	v_add_f32_e32 v116, 1.0, v119
	v_add_f32_e32 v117, 1.0, v121
	s_waitcnt lgkmcnt(1)
	v_mfma_f32_32x32x16_bf16 v[0:15], v[108:111], v[100:103], v[0:15]
	ds_read_b128 v[100:103], v153 offset:64
	v_div_scale_f32 v108, s[42:43], v114, v114, v172
	v_div_scale_f32 v110, s[42:43], v115, v115, v84
	v_rcp_f32_e32 v111, v110
	v_div_scale_f32 v109, s[46:47], v172, v114, v172
	s_waitcnt lgkmcnt(1)
	v_mfma_f32_32x32x16_bf16 v[0:15], v[104:107], v[96:99], v[0:15]
	ds_read_b128 v[96:99], v153 offset:96
	v_div_scale_f32 v105, s[42:43], v116, v116, v120
	v_rcp_f32_e32 v107, v108
	v_rcp_f32_e32 v118, v105
	v_fma_f32 v123, -v110, v111, 1.0
	v_div_scale_f32 v104, s[44:45], v84, v115, v84
	s_waitcnt lgkmcnt(1)
	v_mfma_f32_32x32x16_bf16 v[0:15], v[100:103], v[92:95], v[0:15]
	v_fma_f32 v121, -v108, v107, 1.0
	v_fma_f32 v124, -v105, v118, 1.0
	v_fmac_f32_e32 v107, v121, v107
	v_div_scale_f32 v106, s[42:43], v120, v116, v120
	v_fmac_f32_e32 v111, v123, v111
	v_fmac_f32_e32 v118, v124, v118
	s_waitcnt lgkmcnt(0)
	v_mfma_f32_32x32x16_bf16 v[0:15], v[96:99], v[88:91], v[0:15]
	s_nop 11
	ds_write2_b32 v132, v0, v1 offset1:132
	ds_write2_b32 v160, v2, v3 offset0:8 offset1:140
	ds_write2_b32 v161, v4, v5 offset0:32 offset1:164
	ds_write2_b32 v162, v6, v7 offset0:40 offset1:172
	ds_write2_b32 v163, v8, v9 offset0:64 offset1:196
	ds_write2_b32 v164, v10, v11 offset0:72 offset1:204
	ds_write2_b32 v165, v12, v13 offset0:96 offset1:228
	ds_write2_b32 v166, v14, v15 offset0:104 offset1:236
	s_waitcnt lgkmcnt(0)
	s_barrier
	ds_read_b128 v[88:91], v150 offset:18944
	ds_read_b128 v[92:95], v150 offset:18960
	ds_read_b128 v[8:11], v150 offset:18976
	ds_read_b128 v[0:3], v150 offset:18992
	global_load_dwordx4 v[96:99], v171, s[68:69] offset:16
	global_load_dwordx4 v[100:103], v171, s[68:69]
	s_waitcnt lgkmcnt(3)
	v_mul_f32_e32 v4, v89, v89
	v_fmac_f32_e32 v4, v88, v88
	v_fmac_f32_e32 v4, v90, v90
	v_fmac_f32_e32 v4, v91, v91
	s_waitcnt lgkmcnt(2)
	v_fmac_f32_e32 v4, v92, v92
	v_fmac_f32_e32 v4, v93, v93
	v_fmac_f32_e32 v4, v94, v94
	v_fmac_f32_e32 v4, v95, v95
	s_waitcnt lgkmcnt(1)
	v_fmac_f32_e32 v4, v8, v8
	v_fmac_f32_e32 v4, v9, v9
	v_fmac_f32_e32 v4, v10, v10
	v_fmac_f32_e32 v4, v11, v11
	s_waitcnt lgkmcnt(0)
	v_fmac_f32_e32 v4, v0, v0
	v_fmac_f32_e32 v4, v1, v1
	v_fmac_f32_e32 v4, v2, v2
	v_fmac_f32_e32 v4, v3, v3
	ds_bpermute_b32 v5, v122, v4
	v_mul_f32_e32 v121, v109, v107
	v_mul_f32_e32 v122, v106, v118
	v_fma_f32 v6, -v108, v121, v109
	v_fma_f32 v12, -v105, v122, v106
	s_waitcnt lgkmcnt(0)
	v_add_f32_e32 v4, v4, v5
	ds_bpermute_b32 v5, v112, v4
	v_mul_f32_e32 v112, v104, v111
	v_fma_f32 v7, -v110, v112, v104
	v_fmac_f32_e32 v121, v6, v107
	s_waitcnt lgkmcnt(0)
	v_add_f32_e32 v4, v4, v5
	ds_bpermute_b32 v5, v113, v4
	v_fmac_f32_e32 v112, v7, v111
	v_fmac_f32_e32 v122, v12, v118
	v_fma_f32 v105, -v105, v122, v106
	v_fma_f32 v108, -v108, v121, v109
	s_waitcnt lgkmcnt(0)
	v_add_f32_e32 v4, v4, v5
	v_fmamk_f32 v4, v4, 0x3c000000, v155
	v_mul_f32_e32 v5, 0x4f800000, v4
	v_cmp_gt_f32_e32 vcc, s81, v4
	v_fma_f32 v104, -v110, v112, v104
	s_nop 0
	v_cndmask_b32_e32 v4, v4, v5, vcc
	v_sqrt_f32_e32 v5, v4
	s_nop 0
	v_add_u32_e32 v6, -1, v5
	v_add_u32_e32 v7, 1, v5
	v_fma_f32 v12, -v6, v5, v4
	v_fma_f32 v13, -v7, v5, v4
	v_cmp_ge_f32_e64 s[50:51], 0, v12
	s_nop 1
	v_cndmask_b32_e64 v5, v5, v6, s[50:51]
	v_cmp_lt_f32_e64 s[50:51], 0, v13
	s_nop 1
	v_cndmask_b32_e64 v5, v5, v7, s[50:51]
	v_mul_f32_e32 v6, 0x37800000, v5
	v_cndmask_b32_e32 v5, v5, v6, vcc
	v_cmp_class_f32_e32 vcc, v4, v156
	s_nop 1
	v_cndmask_b32_e32 v106, v5, v4, vcc
	v_rcp_f32_e32 v110, v106
	global_load_dwordx4 v[4:7], v171, s[68:69] offset:48
	global_load_dwordx4 v[12:15], v171, s[68:69] offset:32
	v_mul_f32_e32 v109, 1.0, v110
	s_mov_b64 vcc, s[46:47]
	v_div_fmas_f32 v107, v108, v107, v121
	s_mov_b64 vcc, s[44:45]
	v_mov_b32_e32 v106, v109
	v_div_fmas_f32 v104, v104, v111, v112
	s_mov_b64 vcc, s[42:43]
	v_mul_f32_e32 v89, v89, v106
	v_mul_f32_e32 v90, v90, v106
	v_div_fixup_f32 v84, v104, v115, v84
	v_div_fmas_f32 v104, v105, v118, v122
	v_div_fixup_f32 v104, v104, v116, v120
	s_waitcnt vmcnt(2)
	v_mul_f32_e32 v89, v101, v89
	v_mul_f32_e32 v90, v102, v90
	v_mul_f32_e32 v84, v84, v89
	v_mul_f32_e32 v89, v104, v90
	v_rcp_f32_e32 v90, v117
	v_mul_f32_e32 v88, v88, v106
	v_mul_f32_e32 v88, v100, v88
	v_mul_f32_e32 v91, v91, v106
	v_lshlrev_b32_e32 v102, 16, v86
	v_mul_f32_e32 v91, v103, v91
	v_mul_f32_e32 v103, 0xbfb8aa3b, v102
	v_exp_f32_e32 v103, v103
	v_mul_f32_e32 v90, v85, v90
	v_mov_b32_e32 v85, v90
	v_add_f32_e32 v90, 1.0, v103
	v_mul_f32_e32 v85, v85, v91
	v_rcp_f32_e32 v100, v90
	v_mul_f32_e32 v92, v92, v106
	v_mul_f32_e32 v92, v96, v92
	v_and_b32_e32 v86, 0xffff0000, v86
	v_mul_f32_e32 v96, 0xbfb8aa3b, v86
	v_exp_f32_e32 v96, v96
	v_mul_f32_e32 v91, v102, v100
	v_mov_b32_e32 v90, v91
	v_mul_f32_e32 v90, v90, v92
	v_add_f32_e32 v91, 1.0, v96
	v_rcp_f32_e32 v96, v91
	v_mul_f32_e32 v93, v93, v106
	v_mul_f32_e32 v93, v97, v93
	v_mul_f32_e32 v94, v94, v106
	v_lshlrev_b32_e32 v97, 16, v87
	v_mul_f32_e32 v101, 0xbfb8aa3b, v97
	v_exp_f32_e32 v101, v101
	v_mul_f32_e32 v92, v86, v96
	v_mov_b32_e32 v86, v92
	v_mul_f32_e32 v86, v86, v93
	v_add_f32_e32 v91, 1.0, v101
	v_rcp_f32_e32 v93, v91
	v_mul_f32_e32 v94, v94, v98
	v_and_b32_e32 v87, 0xffff0000, v87
	v_mul_f32_e32 v8, v8, v106
	v_mul_f32_e32 v96, 0xbfb8aa3b, v87
	v_exp_f32_e32 v96, v96
	v_mul_f32_e32 v92, v97, v93
	v_mov_b32_e32 v91, v92
	v_mul_f32_e32 v91, v91, v94
	v_add_f32_e32 v92, 1.0, v96
	v_rcp_f32_e32 v94, v92
	v_mul_f32_e32 v95, v95, v106
	s_waitcnt vmcnt(0)
	v_mul_f32_e32 v8, v8, v12
	v_mul_f32_e32 v95, v95, v99
	v_lshlrev_b32_e32 v96, 16, v80
	v_mul_f32_e32 v98, 0xbfb8aa3b, v96
	v_exp_f32_e32 v98, v98
	v_mul_f32_e32 v93, v87, v94
	v_mov_b32_e32 v87, v93
	v_mul_f32_e32 v87, v87, v95
	v_add_f32_e32 v92, 1.0, v98
	v_rcp_f32_e32 v94, v92
	v_and_b32_e32 v80, 0xffff0000, v80
	v_mul_f32_e32 v9, v9, v106
	v_mul_f32_e32 v9, v9, v13
	v_mul_f32_e32 v93, 0xbfb8aa3b, v80
	v_exp_f32_e32 v93, v93
	v_mul_f32_e32 v12, v96, v94
	v_mul_f32_e32 v8, v12, v8
	v_add_f32_e32 v12, 1.0, v93
	v_rcp_f32_e32 v93, v12
	v_mul_f32_e32 v10, v10, v106
	v_mul_f32_e32 v10, v10, v14
	v_mul_f32_e32 v11, v11, v106
	v_lshlrev_b32_e32 v92, 16, v81
	v_mul_f32_e32 v95, 0xbfb8aa3b, v92
	v_exp_f32_e32 v95, v95
	v_mul_f32_e32 v13, v80, v93
	v_mov_b32_e32 v12, v13
	v_mul_f32_e32 v9, v12, v9
	v_add_f32_e32 v12, 1.0, v95
	v_rcp_f32_e32 v80, v12
	v_mul_f32_e32 v11, v11, v15
	v_mul_f32_e32 v0, v0, v106
	v_mul_f32_e32 v0, v0, v4
	v_and_b32_e32 v14, 0xffff0000, v81
	v_mul_f32_e32 v81, 0xbfb8aa3b, v14
	v_exp_f32_e32 v81, v81
	v_mul_f32_e32 v13, v92, v80
	v_mov_b32_e32 v12, v13
	v_mul_f32_e32 v10, v12, v10
	v_add_f32_e32 v12, 1.0, v81
	v_rcp_f32_e32 v80, v12
	v_div_fixup_f32 v107, v107, v114, v172
	v_mul_f32_e32 v88, v107, v88
	v_med3_f32 v88, v88, s82, v158
	v_lshlrev_b32_e32 v15, 16, v82
	v_mul_f32_e32 v92, 0xbfb8aa3b, v15
	v_exp_f32_e32 v92, v92
	v_mul_f32_e32 v13, v14, v80
	v_mov_b32_e32 v12, v13
	v_mul_f32_e32 v11, v12, v11
	v_add_f32_e32 v12, 1.0, v92
	v_rcp_f32_e32 v14, v12
	v_med3_f32 v84, v84, s82, v158
	v_med3_f32 v90, v90, s82, v158
	v_med3_f32 v86, v86, s82, v158
	v_and_b32_e32 v13, 0xffff0000, v82
	v_mul_f32_e32 v81, 0xbfb8aa3b, v13
	v_exp_f32_e32 v81, v81
	v_mul_f32_e32 v4, v15, v14
	v_mul_f32_e32 v0, v4, v0
	v_add_f32_e32 v4, 1.0, v81
	v_rcp_f32_e32 v14, v4
	v_med3_f32 v15, v0, s82, v158
	v_mul_f32_e32 v0, v1, v106
	v_mul_f32_e32 v0, v0, v5
	v_lshlrev_b32_e32 v12, 16, v83
	v_mul_f32_e32 v80, 0xbfb8aa3b, v12
	v_exp_f32_e32 v80, v80
	v_mul_f32_e32 v1, v13, v14
	v_mul_f32_e32 v0, v1, v0
	v_add_f32_e32 v1, 1.0, v80
	v_rcp_f32_e32 v5, v1
	v_med3_f32 v13, v0, s82, v158
	v_mul_f32_e32 v0, v2, v106
	v_mul_f32_e32 v0, v0, v6
	v_and_b32_e32 v4, 0xffff0000, v83
	v_mul_f32_e32 v14, 0xbfb8aa3b, v4
	v_exp_f32_e32 v14, v14
	v_mul_f32_e32 v2, v12, v5
	v_mov_b32_e32 v1, v2
	v_mul_f32_e32 v0, v1, v0
	v_add_f32_e32 v1, 1.0, v14
	v_rcp_f32_e32 v5, v1
	v_med3_f32 v6, v0, s82, v158
	v_mul_f32_e32 v0, v3, v106
	v_mul_f32_e32 v0, v0, v7
	v_mul_f32_e32 v2, v4, v5
	v_mov_b32_e32 v1, v2
	v_mul_f32_e32 v0, v1, v0
	v_med3_f32 v7, v0, s82, v158
	v_add_u32_e32 v0, s67, v140
	v_ashrrev_i32_e32 v1, 31, v0
	v_lshlrev_b64 v[0:1], 11, v[0:1]
	s_lshl_b32 s42, s66, 7
	v_lshl_add_u64 v[0:1], s[58:59], 0, v[0:1]
	s_and_b32 s62, s42, 0x180
	v_lshl_add_u64 v[0:1], v[0:1], 0, s[62:63]
	v_med3_f32 v8, v8, s82, v158
	v_med3_f32 v9, v9, s82, v158
	v_lshl_add_u64 v[4:5], v[0:1], 0, v[138:139]
	v_mov_b32_e32 v0, v133
	v_mov_b32_e32 v1, v133
	v_mov_b32_e32 v2, v133
	v_mov_b32_e32 v3, v133
	v_cvt_pk_fp8_f32 v0, v88, v84
	v_cvt_pk_fp8_f32 v1, v90, v86
	v_cvt_pk_fp8_f32 v2, v8, v9
	v_cvt_pk_fp8_f32 v3, v15, v13
	v_med3_f32 v89, v89, s82, v158
	v_med3_f32 v85, v85, s82, v158
	v_med3_f32 v91, v91, s82, v158
	v_med3_f32 v87, v87, s82, v158
	v_med3_f32 v10, v10, s82, v158
	v_med3_f32 v11, v11, s82, v158
	v_cvt_pk_fp8_f32 v0, v89, v85 op_sel:[0,0,1]
	v_cvt_pk_fp8_f32 v1, v91, v87 op_sel:[0,0,1]
	v_cvt_pk_fp8_f32 v2, v10, v11 op_sel:[0,0,1]
	v_cvt_pk_fp8_f32 v3, v6, v7 op_sel:[0,0,1]
	v_add_co_u32_e32 v4, vcc, 0x35b80000, v4
	v_mov_b64_e32 v[90:91], v[70:71]
	s_nop 0
	v_addc_co_u32_e32 v5, vcc, 0, v5, vcc
	global_store_dwordx4 v[4:5], v[0:3], off offset:1536
	v_mov_b64_e32 v[94:95], v[66:67]
	v_mov_b64_e32 v[98:99], v[62:63]
	v_mov_b64_e32 v[102:103], v[58:59]
	v_mov_b64_e32 v[106:107], v[54:55]
	v_mov_b64_e32 v[110:111], v[50:51]
	v_mov_b64_e32 v[114:115], v[46:47]
	v_mov_b64_e32 v[118:119], v[42:43]
	v_mov_b64_e32 v[82:83], v[78:79]
	v_mov_b64_e32 v[86:87], v[74:75]
	v_mov_b64_e32 v[126:127], v[38:39]
	v_mov_b64_e32 v[122:123], v[34:35]
	v_mov_b64_e32 v[12:13], v[28:29]
	v_mov_b64_e32 v[8:9], v[24:25]
	v_mov_b64_e32 v[4:5], v[20:21]
	v_mov_b64_e32 v[0:1], v[16:17]
	s_mov_b64 s[42:43], 0
	v_mov_b64_e32 v[88:89], v[68:69]
	v_mov_b64_e32 v[92:93], v[64:65]
	v_mov_b64_e32 v[96:97], v[60:61]
	v_mov_b64_e32 v[100:101], v[56:57]
	v_mov_b64_e32 v[104:105], v[52:53]
	v_mov_b64_e32 v[108:109], v[48:49]
	v_mov_b64_e32 v[112:113], v[44:45]
	v_mov_b64_e32 v[116:117], v[40:41]
	v_mov_b64_e32 v[80:81], v[76:77]
	v_mov_b64_e32 v[84:85], v[72:73]
	v_mov_b64_e32 v[124:125], v[36:37]
	v_mov_b64_e32 v[120:121], v[32:33]
	v_mov_b64_e32 v[14:15], v[30:31]
	v_mov_b64_e32 v[10:11], v[26:27]
	v_mov_b64_e32 v[6:7], v[22:23]
	v_mov_b64_e32 v[2:3], v[18:19]

.LBB0_947:
	s_add_i32 s24, s46, s50
	s_ashr_i32 s25, s24, 31
	s_lshl_b64 s[20:21], s[24:25], 12
	s_waitcnt lgkmcnt(3)
	v_lshl_add_u64 v[46:47], v[26:27], 0, s[20:21]
	global_load_dwordx2 v[0:1], v[46:47], off
	global_load_dwordx2 v[2:3], v[46:47], off offset:512
	global_load_dwordx2 v[10:11], v[46:47], off offset:1024
	global_load_dwordx2 v[16:17], v[46:47], off offset:1536
	s_add_i32 s22, s24, 1
	s_ashr_i32 s23, s22, 31
	s_lshl_b64 s[20:21], s[22:23], 12
	global_load_dwordx2 v[56:57], v[46:47], off offset:3584
	s_waitcnt vmcnt(4)
	v_and_b32_e32 v7, 0xffff0000, v1
	v_lshlrev_b32_e32 v4, 16, v0
	v_and_b32_e32 v5, 0xffff0000, v0
	v_lshlrev_b32_e32 v6, 16, v1
	v_mul_f32_e32 v0, v7, v7
	v_pk_fma_f32 v[18:19], v[6:7], v[6:7], v[0:1] op_sel_hi:[1,1,0]
	s_waitcnt vmcnt(3)
	v_lshlrev_b32_e32 v1, 16, v3
	v_lshlrev_b32_e32 v0, 16, v2
	v_and_b32_e32 v3, 0xffff0000, v3
	v_and_b32_e32 v2, 0xffff0000, v2
	s_waitcnt vmcnt(1)
	v_and_b32_e32 v13, 0xffff0000, v16
	v_mul_f32_e32 v12, v5, v5
	v_pk_mul_f32 v[8:9], v[2:3], v[2:3]
	s_waitcnt lgkmcnt(2)
	v_lshlrev_b32_e32 v15, 16, v16
	v_pk_fma_f32 v[40:41], v[4:5], v[4:5], v[12:13] op_sel_hi:[1,1,0]
	v_pk_fma_f32 v[20:21], v[0:1], v[0:1], v[8:9]
	v_mov_b32_e32 v14, v40
	v_mov_b32_e32 v42, v18
	v_mov_b32_e32 v43, v15
	v_and_b32_e32 v9, 0xffff0000, v10
	v_mul_f32_e32 v22, v13, v13
	v_pk_add_f32 v[18:19], v[40:41], v[18:19]
	v_pk_mul_f32 v[40:41], v[14:15], v[42:43]
	v_pk_add_f32 v[20:21], v[20:21], v[20:21] op_sel:[0,1] op_sel_hi:[1,0]
	v_lshlrev_b32_e32 v8, 16, v10
	v_lshlrev_b32_e32 v10, 16, v11
	v_and_b32_e32 v11, 0xffff0000, v11
	v_mov_b32_e32 v19, v41
	v_mov_b32_e32 v21, v22
	v_mul_f32_e32 v12, v9, v9
	v_lshlrev_b32_e32 v16, 16, v17
	v_and_b32_e32 v17, 0xffff0000, v17
	v_pk_add_f32 v[18:19], v[18:19], v[20:21]
	v_pk_fma_f32 v[20:21], v[8:9], v[8:9], v[12:13] op_sel_hi:[1,1,0]
	v_mul_f32_e32 v12, v11, v11
	v_mul_f32_e32 v44, v16, v16
	v_mul_f32_e32 v45, v17, v17
	v_pk_fma_f32 v[40:41], v[10:11], v[10:11], v[12:13] op_sel_hi:[1,1,0]
	v_mov_b32_e32 v21, v44
	v_mov_b32_e32 v41, v45
	v_pk_add_f32 v[20:21], v[20:21], v[40:41]
	global_load_dwordx2 v[40:41], v[46:47], off offset:2560
	global_load_dwordx2 v[44:45], v[46:47], off offset:3072
	s_waitcnt lgkmcnt(1)
	v_pk_add_f32 v[50:51], v[18:19], v[20:21]
	global_load_dwordx2 v[20:21], v[46:47], off offset:2048
	v_pk_add_f32 v[50:51], v[50:51], v[50:51] op_sel:[0,1] op_sel_hi:[1,0]
	s_waitcnt vmcnt(3) lgkmcnt(0)
	v_lshlrev_b32_e32 v49, 16, v56
	v_and_b32_e32 v47, 0xffff0000, v56
	v_lshlrev_b32_e32 v86, 16, v57
	v_and_b32_e32 v87, 0xffff0000, v57
	v_mov_b32_e32 v48, v50
	v_mov_b32_e32 v57, v49
	v_mul_f32_e32 v12, v47, v47
	v_mul_f32_e32 v14, v86, v86
	v_mul_f32_e32 v22, v87, v87
	s_waitcnt vmcnt(0)
	v_and_b32_e32 v89, 0xffff0000, v21
	v_and_b32_e32 v88, 0xffff0000, v20
	v_lshlrev_b32_e32 v19, 16, v21
	v_lshlrev_b32_e32 v18, 16, v20
	v_pk_mul_f32 v[20:21], v[88:89], v[88:89]
	s_nop 0
	v_pk_fma_f32 v[20:21], v[18:19], v[18:19], v[20:21]
	s_nop 0
	v_pk_add_f32 v[52:53], v[20:21], v[20:21] op_sel:[0,1] op_sel_hi:[1,0]
	v_lshlrev_b32_e32 v21, 16, v41
	v_lshlrev_b32_e32 v20, 16, v40
	v_and_b32_e32 v41, 0xffff0000, v41
	v_and_b32_e32 v40, 0xffff0000, v40
	v_pk_mul_f32 v[42:43], v[40:41], v[40:41]
	v_mov_b32_e32 v56, v52
	v_pk_fma_f32 v[54:55], v[20:21], v[20:21], v[42:43]
	v_pk_add_f32 v[50:51], v[50:51], v[52:53]
	v_pk_mul_f32 v[52:53], v[48:49], v[56:57]
	v_and_b32_e32 v43, 0xffff0000, v44
	v_mov_b32_e32 v51, v53
	v_pk_add_f32 v[52:53], v[54:55], v[54:55] op_sel:[0,1] op_sel_hi:[1,0]
	v_lshlrev_b32_e32 v42, 16, v44
	v_lshlrev_b32_e32 v44, 16, v45
	v_and_b32_e32 v45, 0xffff0000, v45
	v_mov_b32_e32 v53, v12
	v_mul_f32_e32 v12, v43, v43
	v_pk_add_f32 v[50:51], v[50:51], v[52:53]
	v_pk_fma_f32 v[52:53], v[42:43], v[42:43], v[12:13] op_sel_hi:[1,1,0]
	v_mul_f32_e32 v12, v45, v45
	v_pk_fma_f32 v[54:55], v[44:45], v[44:45], v[12:13] op_sel_hi:[1,1,0]
	v_mov_b32_e32 v53, v14
	v_mov_b32_e32 v55, v22
	v_pk_add_f32 v[52:53], v[52:53], v[54:55]
	s_nop 0
	v_pk_add_f32 v[50:51], v[50:51], v[52:53]
	s_nop 0
	v_add_f32_e32 v12, v50, v51
	v_lshl_add_u64 v[50:51], v[26:27], 0, s[20:21]
	global_load_dwordx2 v[52:53], v[50:51], off
	global_load_dwordx2 v[54:55], v[50:51], off offset:512
	global_load_dwordx2 v[56:57], v[50:51], off offset:1024
	s_min_i32 s20, s24, 0x4000
	s_ashr_i32 s20, s20, 12
	s_mul_hi_i32 s21, s20, 0xc000
	s_mul_i32 s20, s20, 0xc000
	s_add_u32 s20, s51, s20
	s_addc_u32 s21, s56, s21
	s_add_u32 s26, s20, 0x6000
	s_addc_u32 s27, s21, 0
	s_add_u32 s28, s20, 0x8000
	s_addc_u32 s29, s21, 0
	s_waitcnt vmcnt(2)
	v_and_b32_e32 v85, 0xffff0000, v53
	v_and_b32_e32 v83, 0xffff0000, v52
	s_waitcnt vmcnt(0)
	v_lshlrev_b32_e32 v74, 16, v56
	v_and_b32_e32 v75, 0xffff0000, v56
	v_lshlrev_b32_e32 v76, 16, v57
	v_and_b32_e32 v77, 0xffff0000, v57
	global_load_dwordx2 v[56:57], v[50:51], off offset:1536
	v_lshlrev_b32_e32 v84, 16, v53
	v_mul_f32_e32 v14, v85, v85
	v_lshlrev_b32_e32 v82, 16, v52
	v_pk_fma_f32 v[52:53], v[84:85], v[84:85], v[14:15] op_sel_hi:[1,1,0]
	v_and_b32_e32 v81, 0xffff0000, v55
	v_and_b32_e32 v80, 0xffff0000, v54
	v_mul_f32_e32 v14, v83, v83
	v_lshlrev_b32_e32 v79, 16, v55
	v_lshlrev_b32_e32 v78, 16, v54
	v_pk_mul_f32 v[54:55], v[80:81], v[80:81]
	v_mov_b32_e32 v58, v52
	v_pk_fma_f32 v[54:55], v[78:79], v[78:79], v[54:55]
	s_waitcnt vmcnt(0)
	v_lshlrev_b32_e32 v71, 16, v56
	v_and_b32_e32 v69, 0xffff0000, v56
	v_lshlrev_b32_e32 v72, 16, v57
	v_and_b32_e32 v73, 0xffff0000, v57
	v_pk_fma_f32 v[56:57], v[82:83], v[82:83], v[14:15] op_sel_hi:[1,1,0]
	v_mov_b32_e32 v59, v71
	v_mov_b32_e32 v70, v56
	v_mul_f32_e32 v22, v69, v69
	v_pk_add_f32 v[52:53], v[56:57], v[52:53]
	v_pk_mul_f32 v[56:57], v[70:71], v[58:59]
	v_pk_add_f32 v[54:55], v[54:55], v[54:55] op_sel:[0,1] op_sel_hi:[1,0]
	v_mov_b32_e32 v53, v57
	v_mov_b32_e32 v55, v22
	v_mul_f32_e32 v14, v75, v75
	v_pk_add_f32 v[52:53], v[52:53], v[54:55]
	v_pk_fma_f32 v[54:55], v[74:75], v[74:75], v[14:15] op_sel_hi:[1,1,0]
	v_mul_f32_e32 v14, v77, v77
	v_mul_f32_e32 v46, v72, v72
	v_mul_f32_e32 v48, v73, v73
	v_pk_fma_f32 v[56:57], v[76:77], v[76:77], v[14:15] op_sel_hi:[1,1,0]
	v_mov_b32_e32 v55, v46
	v_mov_b32_e32 v57, v48
	v_pk_add_f32 v[54:55], v[54:55], v[56:57]
	s_nop 0
	v_pk_add_f32 v[90:91], v[52:53], v[54:55]
	global_load_dwordx2 v[52:53], v[50:51], off offset:2048
	global_load_dwordx2 v[54:55], v[50:51], off offset:3584
	v_pk_add_f32 v[90:91], v[90:91], v[90:91] op_sel:[0,1] op_sel_hi:[1,0]
	s_waitcnt vmcnt(1)
	v_and_b32_e32 v67, 0xffff0000, v53
	v_and_b32_e32 v66, 0xffff0000, v52
	v_lshlrev_b32_e32 v65, 16, v53
	v_lshlrev_b32_e32 v64, 16, v52
	v_pk_mul_f32 v[52:53], v[66:67], v[66:67]
	s_nop 0
	v_pk_fma_f32 v[52:53], v[64:65], v[64:65], v[52:53]
	s_nop 0
	v_pk_add_f32 v[114:115], v[52:53], v[52:53] op_sel:[0,1] op_sel_hi:[1,0]
	global_load_dwordx2 v[52:53], v[50:51], off offset:2560
	v_mov_b32_e32 v118, v114
	s_waitcnt vmcnt(0)
	v_and_b32_e32 v63, 0xffff0000, v53
	v_and_b32_e32 v62, 0xffff0000, v52
	v_lshlrev_b32_e32 v61, 16, v53
	v_lshlrev_b32_e32 v60, 16, v52
	v_pk_mul_f32 v[52:53], v[62:63], v[62:63]
	s_nop 0
	v_pk_fma_f32 v[116:117], v[60:61], v[60:61], v[52:53]
	global_load_dwordx2 v[52:53], v[50:51], off offset:3072
	v_and_b32_e32 v51, 0xffff0000, v54
	v_mul_f32_e32 v14, v51, v51
	s_waitcnt vmcnt(0)
	v_lshlrev_b32_e32 v58, 16, v53
	v_and_b32_e32 v59, 0xffff0000, v53
	v_lshlrev_b32_e32 v53, 16, v54
	v_lshlrev_b32_e32 v56, 16, v52
	v_and_b32_e32 v57, 0xffff0000, v52
	v_mov_b32_e32 v52, v90
	v_mov_b32_e32 v119, v53
	v_pk_add_f32 v[90:91], v[90:91], v[114:115]
	v_pk_mul_f32 v[114:115], v[52:53], v[118:119]
	v_lshlrev_b32_e32 v54, 16, v55
	v_mov_b32_e32 v91, v115
	v_pk_add_f32 v[114:115], v[116:117], v[116:117] op_sel:[0,1] op_sel_hi:[1,0]
	v_and_b32_e32 v55, 0xffff0000, v55
	v_mov_b32_e32 v115, v14
	v_mul_f32_e32 v14, v57, v57
	v_pk_add_f32 v[90:91], v[90:91], v[114:115]
	v_pk_fma_f32 v[114:115], v[56:57], v[56:57], v[14:15] op_sel_hi:[1,1,0]
	v_mul_f32_e32 v14, v59, v59
	v_mul_f32_e32 v22, v54, v54
	v_mul_f32_e32 v46, v55, v55
	v_pk_fma_f32 v[116:117], v[58:59], v[58:59], v[14:15] op_sel_hi:[1,1,0]
	v_mov_b32_e32 v115, v22
	v_mov_b32_e32 v117, v46
	v_pk_add_f32 v[114:115], v[114:115], v[116:117]
	ds_bpermute_b32 v14, v25, v12
	v_pk_add_f32 v[90:91], v[90:91], v[114:115]
	global_load_dwordx4 v[114:117], v[28:29], off
	global_load_dwordx4 v[118:121], v104, s[28:29]
	global_load_dwordx4 v[122:125], v104, s[26:27]
	v_add_f32_e32 v50, v90, v91
	s_waitcnt lgkmcnt(0)
	v_add_f32_e32 v12, v12, v14
	ds_bpermute_b32 v14, v93, v12
	s_waitcnt lgkmcnt(0)
	v_add_f32_e32 v12, v12, v14
	ds_bpermute_b32 v14, v94, v12
	s_waitcnt lgkmcnt(0)
	v_add_f32_e32 v12, v12, v14
	ds_bpermute_b32 v14, v95, v12
	s_waitcnt lgkmcnt(0)
	v_add_f32_e32 v12, v12, v14
	ds_bpermute_b32 v14, v96, v12
	s_waitcnt lgkmcnt(0)
	v_add_f32_e32 v12, v12, v14
	ds_bpermute_b32 v14, v97, v12
	s_waitcnt lgkmcnt(0)
	v_add_f32_e32 v12, v12, v14
	v_fmamk_f32 v12, v12, 0x3a000000, v102
	v_cmp_gt_f32_e32 vcc, s61, v12
	v_mul_f32_e32 v14, 0x4f800000, v12
	s_nop 0
	v_cndmask_b32_e32 v12, v12, v14, vcc
	v_sqrt_f32_e32 v14, v12
	s_nop 0
	v_add_u32_e32 v22, -1, v14
	v_fma_f32 v46, -v22, v14, v12
	v_cmp_ge_f32_e64 s[20:21], 0, v46
	v_add_u32_e32 v46, 1, v14
	s_nop 0
	v_cndmask_b32_e64 v22, v14, v22, s[20:21]
	v_fma_f32 v14, -v46, v14, v12
	v_cmp_lt_f32_e64 s[20:21], 0, v14
	s_nop 1
	v_cndmask_b32_e64 v14, v22, v46, s[20:21]
	v_mul_f32_e32 v22, 0x37800000, v14
	v_cndmask_b32_e32 v14, v14, v22, vcc
	v_cmp_class_f32_e32 vcc, v12, v103
	s_nop 1
	v_cndmask_b32_e32 v12, v14, v12, vcc
	v_rcp_f32_e32 v22, v12
	s_lshl_b64 s[20:21], s[24:25], 11
	v_mul_f32_e32 v14, 1.0, v22
	v_mov_b32_e32 v22, v14
	v_pk_mul_f32 v[6:7], v[22:23], v[6:7] op_sel_hi:[0,1]
	v_pk_mul_f32 v[4:5], v[22:23], v[4:5] op_sel_hi:[0,1]
	s_waitcnt vmcnt(2)
	v_pk_mul_f32 v[90:91], v[114:115], v[4:5]
	v_pk_mul_f32 v[4:5], v[116:117], v[6:7]
	s_waitcnt vmcnt(1)
	v_pk_add_f32 v[6:7], v[120:121], 1.0 op_sel_hi:[1,0]
	v_pk_add_f32 v[114:115], v[118:119], 1.0 op_sel_hi:[1,0]
	s_waitcnt vmcnt(0)
	v_pk_fma_f32 v[4:5], v[6:7], v[4:5], v[124:125]
	v_pk_fma_f32 v[6:7], v[114:115], v[90:91], v[122:123]
	v_mov_b32_e32 v12, 0
	v_cvt_pk_fp8_f32 v12, v6, v7
	v_lshl_add_u64 v[90:91], v[30:31], 0, s[20:21]
	v_mov_b32_e32 v118, v1
	v_mov_b32_e32 v119, v3
	v_cvt_pk_fp8_f32 v12, v4, v5 op_sel:[0,0,1]
	v_mov_b32_e32 v1, v2
	v_pk_mul_f32 v[118:119], v[22:23], v[118:119] op_sel_hi:[0,1]
	v_pk_mul_f32 v[0:1], v[22:23], v[0:1] op_sel_hi:[0,1]
	global_store_dword v[90:91], v12, off
	global_load_dwordx4 v[114:117], v[28:29], off offset:1024
	global_load_dwordx4 v[124:127], v105, s[28:29]
	global_load_dwordx4 v[128:131], v105, s[26:27]
	v_mov_b32_e32 v12, 0
	v_pk_mul_f32 v[10:11], v[22:23], v[10:11] op_sel_hi:[0,1]
	v_pk_mul_f32 v[8:9], v[22:23], v[8:9] op_sel_hi:[0,1]
	v_pk_mul_f32 v[16:17], v[16:17], v[22:23] op_sel_hi:[1,0]
	v_mov_b32_e32 v46, 0
	v_pk_mul_f32 v[44:45], v[22:23], v[44:45] op_sel_hi:[0,1]
	v_pk_mul_f32 v[42:43], v[22:23], v[42:43] op_sel_hi:[0,1]
	v_pk_mul_f32 v[86:87], v[86:87], v[22:23] op_sel_hi:[1,0]
	s_min_i32 s20, s22, 0x4000
	s_ashr_i32 s20, s20, 12
	s_mul_hi_i32 s21, s20, 0xc000
	s_mul_i32 s20, s20, 0xc000
	s_add_u32 s20, s51, s20
	s_addc_u32 s21, s56, s21
	s_add_u32 s24, s20, 0x6000
	s_addc_u32 s25, s21, 0
	v_cvt_pk_bf16_f32 v122, v6, v7
	v_cvt_pk_bf16_f32 v120, v4, v5
	s_waitcnt vmcnt(2)
	v_pk_mul_f32 v[2:3], v[0:1], v[114:115]
	v_pk_mul_f32 v[0:1], v[118:119], v[116:117]
	s_waitcnt vmcnt(1)
	v_pk_add_f32 v[116:117], v[124:125], 1.0 op_sel_hi:[1,0]
	v_pk_add_f32 v[114:115], v[126:127], 1.0 op_sel_hi:[1,0]
	s_waitcnt vmcnt(0)
	v_pk_fma_f32 v[2:3], v[2:3], v[116:117], v[128:129]
	v_pk_fma_f32 v[0:1], v[0:1], v[114:115], v[130:131]
	v_cvt_pk_fp8_f32 v12, v2, v3
	v_mov_b32_e32 v118, v21
	v_mov_b32_e32 v21, v40
	v_pk_mul_f32 v[20:21], v[22:23], v[20:21] op_sel_hi:[0,1]
	v_cvt_pk_fp8_f32 v12, v0, v1 op_sel:[0,0,1]
	v_mov_b32_e32 v119, v41
	v_pk_mul_f32 v[118:119], v[22:23], v[118:119] op_sel_hi:[0,1]
	v_cvt_pk_bf16_f32 v127, v2, v3
	global_store_dword v[90:91], v12, off offset:256
	global_load_dwordx4 v[114:117], v[28:29], off offset:2048
	global_load_dwordx4 v[128:131], v106, s[28:29]
	global_load_dwordx4 v[132:135], v106, s[26:27]
	v_mov_b32_e32 v12, 0
	v_cvt_pk_bf16_f32 v126, v0, v1
	s_waitcnt vmcnt(2)
	v_pk_mul_f32 v[114:115], v[8:9], v[114:115]
	v_pk_mul_f32 v[8:9], v[10:11], v[116:117]
	s_waitcnt vmcnt(1)
	v_pk_add_f32 v[10:11], v[130:131], 1.0 op_sel_hi:[1,0]
	v_pk_add_f32 v[116:117], v[128:129], 1.0 op_sel_hi:[1,0]
	s_waitcnt vmcnt(0)
	v_pk_fma_f32 v[8:9], v[8:9], v[10:11], v[134:135]
	v_pk_fma_f32 v[10:11], v[114:115], v[116:117], v[132:133]
	v_cvt_pk_bf16_f32 v116, v8, v9
	s_nop 0
	v_cvt_pk_fp8_f32 v12, v10, v11
	v_cvt_pk_bf16_f32 v117, v10, v11
	v_cvt_pk_fp8_f32 v12, v8, v9 op_sel:[0,0,1]
	global_store_dword v[90:91], v12, off offset:512
	global_load_dwordx4 v[128:131], v[28:29], off offset:3072
	global_load_dwordx4 v[132:135], v107, s[28:29]
	global_load_dwordx4 v[136:139], v107, s[26:27]
	v_mov_b32_e32 v12, v15
	v_pk_mul_f32 v[12:13], v[12:13], v[22:23] op_sel_hi:[1,0]
	s_waitcnt vmcnt(1)
	v_pk_add_f32 v[114:115], v[132:133], 1.0 op_sel_hi:[1,0]
	v_pk_mul_f32 v[14:15], v[12:13], v[128:129]
	v_pk_mul_f32 v[12:13], v[16:17], v[130:131]
	v_pk_add_f32 v[16:17], v[134:135], 1.0 op_sel_hi:[1,0]
	s_waitcnt vmcnt(0)
	v_pk_fma_f32 v[14:15], v[14:15], v[114:115], v[136:137]
	v_pk_fma_f32 v[12:13], v[12:13], v[16:17], v[138:139]
	v_mov_b32_e32 v16, 0
	v_cvt_pk_fp8_f32 v16, v14, v15
	v_mov_b32_e32 v17, v89
	v_cvt_pk_bf16_f32 v125, v14, v15
	v_cvt_pk_bf16_f32 v124, v12, v13
	v_cvt_pk_fp8_f32 v16, v12, v13 op_sel:[0,0,1]
	global_store_dword v[90:91], v16, off offset:768
	global_load_dwordx4 v[128:131], v[32:33], off
	global_load_dwordx4 v[132:135], v108, s[28:29]
	global_load_dwordx4 v[136:139], v108, s[26:27]
	v_mov_b32_e32 v16, v19
	v_mov_b32_e32 v19, v88
	v_pk_mul_f32 v[18:19], v[22:23], v[18:19] op_sel_hi:[0,1]
	v_pk_mul_f32 v[16:17], v[22:23], v[16:17] op_sel_hi:[0,1]
	s_waitcnt vmcnt(2)
	v_pk_mul_f32 v[18:19], v[18:19], v[128:129]
	s_waitcnt vmcnt(1)
	v_pk_add_f32 v[114:115], v[132:133], 1.0 op_sel_hi:[1,0]
	v_pk_mul_f32 v[16:17], v[16:17], v[130:131]
	s_waitcnt vmcnt(0)
	v_pk_fma_f32 v[18:19], v[18:19], v[114:115], v[136:137]
	v_pk_add_f32 v[88:89], v[134:135], 1.0 op_sel_hi:[1,0]
	v_cvt_pk_fp8_f32 v46, v18, v19
	v_pk_fma_f32 v[16:17], v[16:17], v[88:89], v[138:139]
	v_cvt_pk_bf16_f32 v114, v18, v19
	s_nop 0
	v_cvt_pk_fp8_f32 v46, v16, v17 op_sel:[0,0,1]
	v_cvt_pk_bf16_f32 v88, v16, v17
	global_store_dword v[90:91], v46, off offset:1024
	global_load_dwordx4 v[128:131], v[34:35], off
	global_load_dwordx4 v[132:135], v109, s[28:29]
	global_load_dwordx4 v[136:139], v109, s[26:27]
	v_mov_b32_e32 v46, 0
	s_waitcnt vmcnt(2)
	v_pk_mul_f32 v[40:41], v[20:21], v[128:129]
	s_waitcnt vmcnt(1)
	v_pk_add_f32 v[128:129], v[132:133], 1.0 op_sel_hi:[1,0]
	v_pk_mul_f32 v[20:21], v[118:119], v[130:131]
	s_waitcnt vmcnt(0)
	v_pk_fma_f32 v[40:41], v[40:41], v[128:129], v[136:137]
	v_pk_add_f32 v[118:119], v[134:135], 1.0 op_sel_hi:[1,0]
	v_cvt_pk_fp8_f32 v46, v40, v41
	v_pk_fma_f32 v[20:21], v[20:21], v[118:119], v[138:139]
	v_cvt_pk_bf16_f32 v123, v40, v41
	s_nop 0
	v_cvt_pk_fp8_f32 v46, v20, v21 op_sel:[0,0,1]
	v_cvt_pk_bf16_f32 v121, v20, v21
	global_store_dword v[90:91], v46, off offset:1280
	global_load_dwordx4 v[128:131], v[36:37], off
	global_load_dwordx4 v[132:135], v110, s[28:29]
	global_load_dwordx4 v[136:139], v110, s[26:27]
	v_mov_b32_e32 v46, 0
	s_waitcnt vmcnt(2)
	v_pk_mul_f32 v[118:119], v[42:43], v[128:129]
	v_pk_mul_f32 v[42:43], v[44:45], v[130:131]
	s_waitcnt vmcnt(1)
	v_pk_add_f32 v[44:45], v[134:135], 1.0 op_sel_hi:[1,0]
	v_pk_add_f32 v[128:129], v[132:133], 1.0 op_sel_hi:[1,0]
	s_waitcnt vmcnt(0)
	v_pk_fma_f32 v[42:43], v[42:43], v[44:45], v[138:139]
	v_pk_fma_f32 v[44:45], v[118:119], v[128:129], v[136:137]
	v_cvt_pk_bf16_f32 v89, v42, v43
	s_nop 0
	v_cvt_pk_fp8_f32 v46, v44, v45
	v_cvt_pk_bf16_f32 v115, v44, v45
	v_cvt_pk_fp8_f32 v46, v42, v43 op_sel:[0,0,1]
	global_store_dword v[90:91], v46, off offset:1536
	global_load_dwordx4 v[128:131], v[38:39], off
	global_load_dwordx4 v[132:135], v111, s[28:29]
	global_load_dwordx4 v[136:139], v111, s[26:27]
	v_mov_b32_e32 v46, v49
	v_pk_mul_f32 v[46:47], v[46:47], v[22:23] op_sel_hi:[1,0]
	v_mov_b32_e32 v22, 0
	s_add_u32 s26, s20, 0x8000
	s_addc_u32 s27, s21, 0
	s_waitcnt vmcnt(2)
	v_pk_mul_f32 v[48:49], v[46:47], v[128:129]
	s_waitcnt vmcnt(1)
	v_pk_add_f32 v[118:119], v[132:133], 1.0 op_sel_hi:[1,0]
	v_pk_mul_f32 v[46:47], v[86:87], v[130:131]
	s_waitcnt vmcnt(0)
	v_pk_fma_f32 v[48:49], v[48:49], v[118:119], v[136:137]
	v_pk_add_f32 v[86:87], v[134:135], 1.0 op_sel_hi:[1,0]
	v_cvt_pk_fp8_f32 v22, v48, v49
	v_pk_fma_f32 v[46:47], v[46:47], v[86:87], v[138:139]
	v_cvt_pk_bf16_f32 v119, v48, v49
	s_nop 0
	v_cvt_pk_fp8_f32 v22, v46, v47 op_sel:[0,0,1]
	v_cvt_pk_bf16_f32 v118, v46, v47
	global_store_dword v[90:91], v22, off offset:1792
	global_load_dwordx4 v[128:131], v[28:29], off
	global_load_dwordx4 v[132:135], v104, s[26:27]
	global_load_dwordx4 v[136:139], v104, s[24:25]
	ds_bpermute_b32 v22, v25, v50
	s_waitcnt lgkmcnt(0)
	v_add_f32_e32 v22, v50, v22
	ds_bpermute_b32 v50, v93, v22
	s_waitcnt lgkmcnt(0)
	v_add_f32_e32 v22, v22, v50
	ds_bpermute_b32 v50, v94, v22
	s_waitcnt lgkmcnt(0)
	v_add_f32_e32 v22, v22, v50
	ds_bpermute_b32 v50, v95, v22
	s_waitcnt lgkmcnt(0)
	v_add_f32_e32 v22, v22, v50
	ds_bpermute_b32 v50, v96, v22
	s_waitcnt lgkmcnt(0)
	v_add_f32_e32 v22, v22, v50
	ds_bpermute_b32 v50, v97, v22
	s_waitcnt lgkmcnt(0)
	v_add_f32_e32 v22, v22, v50
	v_fmamk_f32 v22, v22, 0x3a000000, v102
	v_cmp_gt_f32_e32 vcc, s61, v22
	v_mul_f32_e32 v50, 0x4f800000, v22
	s_waitcnt vmcnt(1)
	v_pk_add_f32 v[90:91], v[132:133], 1.0 op_sel_hi:[1,0]
	v_cndmask_b32_e32 v22, v22, v50, vcc
	v_sqrt_f32_e32 v50, v22
	s_nop 0
	v_add_u32_e32 v52, -1, v50
	v_fma_f32 v68, -v52, v50, v22
	v_cmp_ge_f32_e64 s[20:21], 0, v68
	v_add_u32_e32 v68, 1, v50
	s_nop 0
	v_cndmask_b32_e64 v52, v50, v52, s[20:21]
	v_fma_f32 v50, -v68, v50, v22
	v_cmp_lt_f32_e64 s[20:21], 0, v50
	s_nop 1
	v_cndmask_b32_e64 v50, v52, v68, s[20:21]
	v_mul_f32_e32 v52, 0x37800000, v50
	v_cndmask_b32_e32 v50, v50, v52, vcc
	v_cmp_class_f32_e32 vcc, v22, v103
	s_nop 1
	v_cndmask_b32_e32 v22, v50, v22, vcc
	v_rcp_f32_e32 v52, v22
	s_lshl_b64 s[20:21], s[22:23], 11
	v_mul_f32_e32 v50, 1.0, v52
	v_mov_b32_e32 v22, v50
	v_pk_mul_f32 v[84:85], v[22:23], v[84:85] op_sel_hi:[0,1]
	v_pk_mul_f32 v[82:83], v[22:23], v[82:83] op_sel_hi:[0,1]
	v_pk_mul_f32 v[86:87], v[128:129], v[82:83]
	v_pk_mul_f32 v[82:83], v[130:131], v[84:85]
	v_pk_add_f32 v[84:85], v[134:135], 1.0 op_sel_hi:[1,0]
	v_mov_b32_e32 v50, 0
	s_waitcnt vmcnt(0)
	v_pk_fma_f32 v[82:83], v[84:85], v[82:83], v[138:139]
	v_pk_fma_f32 v[84:85], v[90:91], v[86:87], v[136:137]
	v_lshl_add_u64 v[86:87], v[30:31], 0, s[20:21]
	v_cvt_pk_fp8_f32 v50, v84, v85
	v_mov_b32_e32 v90, v79
	v_mov_b32_e32 v79, v80
	v_pk_mul_f32 v[78:79], v[22:23], v[78:79] op_sel_hi:[0,1]
	v_cvt_pk_fp8_f32 v50, v82, v83 op_sel:[0,0,1]
	v_mov_b32_e32 v91, v81
	v_pk_mul_f32 v[90:91], v[22:23], v[90:91] op_sel_hi:[0,1]
	v_pk_mul_f32 v[76:77], v[22:23], v[76:77] op_sel_hi:[0,1]
	global_store_dword v[86:87], v50, off
	global_load_dwordx4 v[132:135], v[28:29], off offset:1024
	global_load_dwordx4 v[136:139], v105, s[26:27]
	global_load_dwordx4 v[140:143], v105, s[24:25]
	v_mov_b32_e32 v50, 0
	v_pk_mul_f32 v[74:75], v[22:23], v[74:75] op_sel_hi:[0,1]
	v_mov_b32_e32 v68, v71
	v_pk_mul_f32 v[68:69], v[68:69], v[22:23] op_sel_hi:[1,0]
	v_pk_mul_f32 v[72:73], v[72:73], v[22:23] op_sel_hi:[1,0]
	v_pk_mul_f32 v[58:59], v[22:23], v[58:59] op_sel_hi:[0,1]
	v_pk_mul_f32 v[56:57], v[22:23], v[56:57] op_sel_hi:[0,1]
	v_pk_mul_f32 v[54:55], v[54:55], v[22:23] op_sel_hi:[1,0]
	v_cvt_pk_bf16_f32 v130, v82, v83
	v_cvt_pk_bf16_f32 v131, v84, v85
	s_waitcnt vmcnt(2)
	v_pk_mul_f32 v[80:81], v[78:79], v[132:133]
	s_waitcnt vmcnt(1)
	v_pk_add_f32 v[128:129], v[136:137], 1.0 op_sel_hi:[1,0]
	v_pk_mul_f32 v[78:79], v[90:91], v[134:135]
	s_waitcnt vmcnt(0)
	v_pk_fma_f32 v[80:81], v[80:81], v[128:129], v[140:141]
	v_pk_add_f32 v[90:91], v[138:139], 1.0 op_sel_hi:[1,0]
	v_cvt_pk_fp8_f32 v50, v80, v81
	v_pk_fma_f32 v[78:79], v[78:79], v[90:91], v[142:143]
	v_cvt_pk_bf16_f32 v141, v80, v81
	s_nop 0
	v_cvt_pk_fp8_f32 v50, v78, v79 op_sel:[0,0,1]
	v_cvt_pk_bf16_f32 v140, v78, v79
	global_store_dword v[86:87], v50, off offset:256
	global_load_dwordx4 v[132:135], v[28:29], off offset:2048
	global_load_dwordx4 v[136:139], v106, s[26:27]
	global_load_dwordx4 v[142:145], v106, s[24:25]
	v_mov_b32_e32 v50, 0
	s_waitcnt vmcnt(2)
	v_pk_mul_f32 v[90:91], v[74:75], v[132:133]
	v_pk_mul_f32 v[74:75], v[76:77], v[134:135]
	s_waitcnt vmcnt(1)
	v_pk_add_f32 v[76:77], v[138:139], 1.0 op_sel_hi:[1,0]
	v_pk_add_f32 v[128:129], v[136:137], 1.0 op_sel_hi:[1,0]
	s_waitcnt vmcnt(0)
	v_pk_fma_f32 v[74:75], v[74:75], v[76:77], v[144:145]
	v_pk_fma_f32 v[76:77], v[90:91], v[128:129], v[142:143]
	v_cvt_pk_bf16_f32 v134, v74, v75
	s_nop 0
	v_cvt_pk_fp8_f32 v50, v76, v77
	v_cvt_pk_bf16_f32 v135, v76, v77
	v_cvt_pk_fp8_f32 v50, v74, v75 op_sel:[0,0,1]
	global_store_dword v[86:87], v50, off offset:512
	global_load_dwordx4 v[136:139], v[28:29], off offset:3072
	global_load_dwordx4 v[142:145], v107, s[26:27]
	global_load_dwordx4 v[146:149], v107, s[24:25]
	v_mov_b32_e32 v50, 0
	s_waitcnt vmcnt(2)
	v_pk_mul_f32 v[70:71], v[68:69], v[136:137]
	s_waitcnt vmcnt(1)
	v_pk_add_f32 v[90:91], v[142:143], 1.0 op_sel_hi:[1,0]
	v_pk_mul_f32 v[68:69], v[72:73], v[138:139]
	s_waitcnt vmcnt(0)
	v_pk_fma_f32 v[70:71], v[70:71], v[90:91], v[146:147]
	v_pk_add_f32 v[72:73], v[144:145], 1.0 op_sel_hi:[1,0]
	v_cvt_pk_fp8_f32 v50, v70, v71
	v_pk_fma_f32 v[68:69], v[68:69], v[72:73], v[148:149]
	v_mov_b32_e32 v72, v65
	v_mov_b32_e32 v65, v66
	v_cvt_pk_fp8_f32 v50, v68, v69 op_sel:[0,0,1]
	v_pk_mul_f32 v[64:65], v[22:23], v[64:65] op_sel_hi:[0,1]
	v_mov_b32_e32 v73, v67
	v_pk_mul_f32 v[72:73], v[22:23], v[72:73] op_sel_hi:[0,1]
	global_store_dword v[86:87], v50, off offset:768
	global_load_dwordx4 v[142:145], v[32:33], off
	global_load_dwordx4 v[146:149], v108, s[26:27]
	global_load_dwordx4 v[150:153], v108, s[24:25]
	v_mov_b32_e32 v50, 0
	v_cvt_pk_bf16_f32 v139, v70, v71
	v_cvt_pk_bf16_f32 v138, v68, v69
	s_waitcnt vmcnt(2)
	v_pk_mul_f32 v[66:67], v[64:65], v[142:143]
	s_waitcnt vmcnt(1)
	v_pk_add_f32 v[90:91], v[146:147], 1.0 op_sel_hi:[1,0]
	v_pk_mul_f32 v[64:65], v[72:73], v[144:145]
	s_waitcnt vmcnt(0)
	v_pk_fma_f32 v[66:67], v[66:67], v[90:91], v[150:151]
	v_pk_add_f32 v[72:73], v[148:149], 1.0 op_sel_hi:[1,0]
	v_cvt_pk_fp8_f32 v50, v66, v67
	v_pk_fma_f32 v[64:65], v[64:65], v[72:73], v[152:153]
	v_mov_b32_e32 v72, v61
	v_mov_b32_e32 v61, v62
	v_cvt_pk_fp8_f32 v50, v64, v65 op_sel:[0,0,1]
	v_pk_mul_f32 v[60:61], v[22:23], v[60:61] op_sel_hi:[0,1]
	v_mov_b32_e32 v73, v63
	v_pk_mul_f32 v[72:73], v[22:23], v[72:73] op_sel_hi:[0,1]
	global_store_dword v[86:87], v50, off offset:1024
	global_load_dwordx4 v[142:145], v[34:35], off
	global_load_dwordx4 v[146:149], v109, s[26:27]
	global_load_dwordx4 v[150:153], v109, s[24:25]
	v_mov_b32_e32 v50, 0
	v_cvt_pk_bf16_f32 v132, v64, v65
	v_cvt_pk_bf16_f32 v133, v66, v67
	s_waitcnt vmcnt(2)
	v_pk_mul_f32 v[62:63], v[60:61], v[142:143]
	s_waitcnt vmcnt(1)
	v_pk_add_f32 v[90:91], v[146:147], 1.0 op_sel_hi:[1,0]
	v_pk_mul_f32 v[60:61], v[72:73], v[144:145]
	s_waitcnt vmcnt(0)
	v_pk_fma_f32 v[62:63], v[62:63], v[90:91], v[150:151]
	v_pk_add_f32 v[72:73], v[148:149], 1.0 op_sel_hi:[1,0]
	v_cvt_pk_fp8_f32 v50, v62, v63
	v_pk_fma_f32 v[60:61], v[60:61], v[72:73], v[152:153]
	v_cvt_pk_bf16_f32 v137, v62, v63
	s_nop 0
	v_cvt_pk_fp8_f32 v50, v60, v61 op_sel:[0,0,1]
	v_cvt_pk_bf16_f32 v136, v60, v61
	global_store_dword v[86:87], v50, off offset:1280
	global_load_dwordx4 v[142:145], v[36:37], off
	global_load_dwordx4 v[146:149], v110, s[26:27]
	global_load_dwordx4 v[150:153], v110, s[24:25]
	v_mov_b32_e32 v50, 0
	s_waitcnt vmcnt(2)
	v_pk_mul_f32 v[72:73], v[56:57], v[142:143]
	v_pk_mul_f32 v[56:57], v[58:59], v[144:145]
	s_waitcnt vmcnt(1)
	v_pk_add_f32 v[58:59], v[148:149], 1.0 op_sel_hi:[1,0]
	v_pk_add_f32 v[90:91], v[146:147], 1.0 op_sel_hi:[1,0]
	s_waitcnt vmcnt(0)
	v_pk_fma_f32 v[56:57], v[56:57], v[58:59], v[152:153]
	v_pk_fma_f32 v[58:59], v[72:73], v[90:91], v[150:151]
	v_cvt_pk_bf16_f32 v128, v56, v57
	s_nop 0
	v_cvt_pk_fp8_f32 v50, v58, v59
	v_cvt_pk_bf16_f32 v129, v58, v59
	v_cvt_pk_fp8_f32 v50, v56, v57 op_sel:[0,0,1]
	global_store_dword v[86:87], v50, off offset:1536
	global_load_dwordx4 v[142:145], v[38:39], off
	global_load_dwordx4 v[146:149], v111, s[26:27]
	global_load_dwordx4 v[150:153], v111, s[24:25]
	v_mov_b32_e32 v50, v53
	v_pk_mul_f32 v[50:51], v[50:51], v[22:23] op_sel_hi:[1,0]
	v_mov_b32_e32 v22, 0
	s_waitcnt vmcnt(2)
	v_pk_mul_f32 v[52:53], v[50:51], v[142:143]
	s_waitcnt vmcnt(1)
	v_pk_add_f32 v[72:73], v[146:147], 1.0 op_sel_hi:[1,0]
	v_pk_mul_f32 v[50:51], v[54:55], v[144:145]
	s_waitcnt vmcnt(0)
	v_pk_fma_f32 v[52:53], v[52:53], v[72:73], v[150:151]
	v_pk_add_f32 v[54:55], v[148:149], 1.0 op_sel_hi:[1,0]
	v_cvt_pk_fp8_f32 v22, v52, v53
	v_pk_fma_f32 v[50:51], v[50:51], v[54:55], v[152:153]
	ds_read_b128 v[142:145], v98
	v_cvt_pk_bf16_f32 v90, v50, v51
	v_cvt_pk_fp8_f32 v22, v50, v51 op_sel:[0,0,1]
	v_cvt_pk_bf16_f32 v91, v52, v53
	s_waitcnt lgkmcnt(0)
	v_mul_f32_e32 v54, v5, v145
	global_store_dword v[86:87], v22, off offset:1792
	v_mul_f32_e32 v22, v7, v143
	v_fmac_f32_e32 v22, v6, v142
	v_fmac_f32_e32 v54, v4, v144
	v_add_f32_e32 v22, v22, v54
	v_mul_f32_e32 v54, v85, v143
	v_mul_f32_e32 v55, v83, v145
	v_fmac_f32_e32 v54, v84, v142
	v_fmac_f32_e32 v55, v82, v144
	ds_read_b128 v[142:145], v98 offset:1024
	v_add_f32_e32 v54, v54, v55
	v_add_f32_e32 v22, 0, v22
	v_add_f32_e32 v54, 0, v54
	s_waitcnt lgkmcnt(0)
	v_mul_f32_e32 v55, v3, v143
	v_mul_f32_e32 v72, v1, v145
	v_fmac_f32_e32 v55, v2, v142
	v_fmac_f32_e32 v72, v0, v144
	v_add_f32_e32 v55, v55, v72
	v_add_f32_e32 v22, v22, v55
	v_mul_f32_e32 v55, v81, v143
	v_mul_f32_e32 v72, v79, v145
	v_fmac_f32_e32 v55, v80, v142
	v_fmac_f32_e32 v72, v78, v144
	ds_read_b128 v[142:145], v98 offset:2048
	v_add_f32_e32 v55, v55, v72
	v_add_f32_e32 v54, v54, v55
	s_waitcnt lgkmcnt(0)
	v_mul_f32_e32 v55, v11, v143
	v_mul_f32_e32 v72, v9, v145
	v_fmac_f32_e32 v55, v10, v142
	v_fmac_f32_e32 v72, v8, v144
	v_add_f32_e32 v55, v55, v72
	v_add_f32_e32 v22, v22, v55
	v_mul_f32_e32 v55, v77, v143
	v_mul_f32_e32 v72, v75, v145
	v_fmac_f32_e32 v55, v76, v142
	v_fmac_f32_e32 v72, v74, v144
	ds_read_b128 v[142:145], v98 offset:3072
	v_add_f32_e32 v55, v55, v72
	v_add_f32_e32 v54, v54, v55
	s_waitcnt lgkmcnt(0)
	v_mul_f32_e32 v55, v15, v143
	v_mul_f32_e32 v72, v13, v145
	v_fmac_f32_e32 v55, v14, v142
	v_fmac_f32_e32 v72, v12, v144
	v_add_f32_e32 v55, v55, v72
	v_add_f32_e32 v22, v22, v55
	v_mul_f32_e32 v55, v71, v143
	v_mul_f32_e32 v72, v69, v145
	v_fmac_f32_e32 v55, v70, v142
	v_fmac_f32_e32 v72, v68, v144
	ds_read_b128 v[142:145], v98 offset:4096
	v_add_f32_e32 v55, v55, v72
	v_add_f32_e32 v54, v54, v55
	s_waitcnt lgkmcnt(0)
	v_mul_f32_e32 v55, v19, v143
	v_mul_f32_e32 v72, v17, v145
	v_fmac_f32_e32 v55, v18, v142
	v_fmac_f32_e32 v72, v16, v144
	v_add_f32_e32 v55, v55, v72
	v_add_f32_e32 v22, v22, v55
	v_mul_f32_e32 v55, v67, v143
	v_mul_f32_e32 v72, v65, v145
	v_fmac_f32_e32 v55, v66, v142
	v_fmac_f32_e32 v72, v64, v144
	ds_read_b128 v[142:145], v98 offset:5120
	v_add_f32_e32 v55, v55, v72
	v_add_f32_e32 v54, v54, v55
	s_waitcnt lgkmcnt(0)
	v_mul_f32_e32 v55, v41, v143
	v_mul_f32_e32 v72, v21, v145
	v_fmac_f32_e32 v55, v40, v142
	v_fmac_f32_e32 v72, v20, v144
	v_add_f32_e32 v55, v55, v72
	v_add_f32_e32 v22, v22, v55
	v_mul_f32_e32 v55, v63, v143
	v_mul_f32_e32 v72, v61, v145
	v_fmac_f32_e32 v55, v62, v142
	v_fmac_f32_e32 v72, v60, v144
	ds_read_b128 v[142:145], v98 offset:6144
	v_add_f32_e32 v55, v55, v72
	v_add_f32_e32 v54, v54, v55
	s_waitcnt lgkmcnt(0)
	v_mul_f32_e32 v55, v45, v143
	v_mul_f32_e32 v72, v43, v145
	v_fmac_f32_e32 v55, v44, v142
	v_fmac_f32_e32 v72, v42, v144
	v_add_f32_e32 v55, v55, v72
	v_add_f32_e32 v22, v22, v55
	v_mul_f32_e32 v55, v59, v143
	v_mul_f32_e32 v72, v57, v145
	v_fmac_f32_e32 v55, v58, v142
	v_fmac_f32_e32 v72, v56, v144
	ds_read_b128 v[142:145], v98 offset:7168
	v_add_f32_e32 v55, v55, v72
	v_add_f32_e32 v55, v54, v55
	s_waitcnt lgkmcnt(0)
	v_mul_f32_e32 v54, v49, v143
	v_mul_f32_e32 v72, v47, v145
	v_fmac_f32_e32 v54, v48, v142
	v_fmac_f32_e32 v72, v46, v144
	v_add_f32_e32 v54, v54, v72
	v_add_f32_e32 v54, v22, v54
	v_mul_f32_e32 v22, v53, v143
	v_mul_f32_e32 v72, v51, v145
	v_fmac_f32_e32 v22, v52, v142
	v_fmac_f32_e32 v72, v50, v144
	ds_read_b128 v[142:145], v98 offset:8192
	v_add_f32_e32 v22, v22, v72
	v_add_f32_e32 v22, v55, v22
	s_waitcnt lgkmcnt(0)
	v_mul_f32_e32 v55, v7, v143
	v_mul_f32_e32 v72, v5, v145
	v_fmac_f32_e32 v55, v6, v142
	v_fmac_f32_e32 v72, v4, v144
	v_add_f32_e32 v55, v55, v72
	v_mul_f32_e32 v72, v85, v143
	v_mul_f32_e32 v73, v83, v145
	v_fmac_f32_e32 v72, v84, v142
	v_fmac_f32_e32 v73, v82, v144
	ds_read_b128 v[142:145], v98 offset:9216
	v_add_f32_e32 v72, v72, v73
	v_add_f32_e32 v55, 0, v55
	v_add_f32_e32 v72, 0, v72
	s_waitcnt lgkmcnt(0)
	v_mul_f32_e32 v73, v3, v143
	v_mul_f32_e32 v86, v1, v145
	v_fmac_f32_e32 v73, v2, v142
	v_fmac_f32_e32 v86, v0, v144
	v_add_f32_e32 v73, v73, v86
	v_add_f32_e32 v55, v55, v73
	v_mul_f32_e32 v73, v81, v143
	v_mul_f32_e32 v86, v79, v145
	v_fmac_f32_e32 v73, v80, v142
	v_fmac_f32_e32 v86, v78, v144
	ds_read_b128 v[142:145], v98 offset:10240
	v_add_f32_e32 v73, v73, v86
	v_add_f32_e32 v72, v72, v73
	s_waitcnt lgkmcnt(0)
	v_mul_f32_e32 v73, v11, v143
	v_mul_f32_e32 v86, v9, v145
	v_fmac_f32_e32 v73, v10, v142
	v_fmac_f32_e32 v86, v8, v144
	v_add_f32_e32 v73, v73, v86
	v_add_f32_e32 v55, v55, v73
	v_mul_f32_e32 v73, v77, v143
	v_mul_f32_e32 v86, v75, v145
	v_fmac_f32_e32 v73, v76, v142
	v_fmac_f32_e32 v86, v74, v144
	ds_read_b128 v[142:145], v98 offset:11264
	v_add_f32_e32 v73, v73, v86
	v_add_f32_e32 v72, v72, v73
	s_waitcnt lgkmcnt(0)
	v_mul_f32_e32 v73, v15, v143
	v_mul_f32_e32 v86, v13, v145
	v_fmac_f32_e32 v73, v14, v142
	v_fmac_f32_e32 v86, v12, v144
	v_add_f32_e32 v73, v73, v86
	v_add_f32_e32 v55, v55, v73
	v_mul_f32_e32 v73, v71, v143
	v_mul_f32_e32 v86, v69, v145
	v_fmac_f32_e32 v73, v70, v142
	v_fmac_f32_e32 v86, v68, v144
	ds_read_b128 v[142:145], v98 offset:12288
	v_add_f32_e32 v73, v73, v86
	v_add_f32_e32 v72, v72, v73
	s_waitcnt lgkmcnt(0)
	v_mul_f32_e32 v73, v19, v143
	v_mul_f32_e32 v86, v17, v145
	v_fmac_f32_e32 v73, v18, v142
	v_fmac_f32_e32 v86, v16, v144
	v_add_f32_e32 v73, v73, v86
	v_add_f32_e32 v55, v55, v73
	v_mul_f32_e32 v73, v67, v143
	v_mul_f32_e32 v86, v65, v145
	v_fmac_f32_e32 v73, v66, v142
	v_fmac_f32_e32 v86, v64, v144
	ds_read_b128 v[142:145], v98 offset:13312
	v_add_f32_e32 v73, v73, v86
	v_add_f32_e32 v72, v72, v73
	s_waitcnt lgkmcnt(0)
	v_mul_f32_e32 v73, v41, v143
	v_mul_f32_e32 v86, v21, v145
	v_fmac_f32_e32 v73, v40, v142
	v_fmac_f32_e32 v86, v20, v144
	v_add_f32_e32 v73, v73, v86
	v_add_f32_e32 v55, v55, v73
	v_mul_f32_e32 v73, v63, v143
	v_mul_f32_e32 v86, v61, v145
	v_fmac_f32_e32 v73, v62, v142
	v_fmac_f32_e32 v86, v60, v144
	ds_read_b128 v[142:145], v98 offset:14336
	v_add_f32_e32 v73, v73, v86
	v_add_f32_e32 v72, v72, v73
	s_waitcnt lgkmcnt(0)
	v_mul_f32_e32 v73, v45, v143
	v_mul_f32_e32 v86, v43, v145
	v_fmac_f32_e32 v73, v44, v142
	v_fmac_f32_e32 v86, v42, v144
	v_add_f32_e32 v73, v73, v86
	v_add_f32_e32 v55, v55, v73
	v_mul_f32_e32 v73, v59, v143
	v_mul_f32_e32 v86, v57, v145
	v_fmac_f32_e32 v73, v58, v142
	v_fmac_f32_e32 v86, v56, v144
	ds_read_b128 v[142:145], v98 offset:15360
	v_add_f32_e32 v73, v73, v86
	v_add_f32_e32 v73, v72, v73
	s_waitcnt lgkmcnt(0)
	v_mul_f32_e32 v72, v49, v143
	v_mul_f32_e32 v86, v47, v145
	v_fmac_f32_e32 v72, v48, v142
	v_fmac_f32_e32 v86, v46, v144
	v_add_f32_e32 v72, v72, v86
	v_add_f32_e32 v72, v55, v72
	v_mul_f32_e32 v55, v53, v143
	v_mul_f32_e32 v86, v51, v145
	v_fmac_f32_e32 v55, v52, v142
	v_fmac_f32_e32 v86, v50, v144
	ds_read_b128 v[142:145], v98 offset:16384
	v_add_f32_e32 v55, v55, v86
	v_add_f32_e32 v55, v73, v55
	s_waitcnt lgkmcnt(0)
	v_mul_f32_e32 v73, v7, v143
	v_mul_f32_e32 v86, v5, v145
	v_fmac_f32_e32 v73, v6, v142
	v_fmac_f32_e32 v86, v4, v144
	v_add_f32_e32 v73, v73, v86
	v_mul_f32_e32 v86, v85, v143
	v_mul_f32_e32 v87, v83, v145
	v_fmac_f32_e32 v86, v84, v142
	v_fmac_f32_e32 v87, v82, v144
	ds_read_b128 v[142:145], v98 offset:17408
	v_add_f32_e32 v86, v86, v87
	v_add_f32_e32 v73, 0, v73
	v_add_f32_e32 v86, 0, v86
	s_waitcnt lgkmcnt(0)
	v_mul_f32_e32 v87, v3, v143
	v_mul_f32_e32 v146, v1, v145
	v_fmac_f32_e32 v87, v2, v142
	v_fmac_f32_e32 v146, v0, v144
	v_add_f32_e32 v87, v87, v146
	v_add_f32_e32 v73, v73, v87
	v_mul_f32_e32 v87, v81, v143
	v_fmac_f32_e32 v87, v80, v142
	v_mul_f32_e32 v142, v79, v145
	v_fmac_f32_e32 v142, v78, v144
	v_add_f32_e32 v87, v87, v142
	ds_read_b128 v[142:145], v98 offset:18432
	v_add_f32_e32 v86, v86, v87
	s_waitcnt lgkmcnt(0)
	v_mul_f32_e32 v87, v11, v143
	v_mul_f32_e32 v146, v9, v145
	v_fmac_f32_e32 v87, v10, v142
	v_fmac_f32_e32 v146, v8, v144
	v_add_f32_e32 v87, v87, v146
	v_add_f32_e32 v73, v73, v87
	v_mul_f32_e32 v87, v77, v143
	v_fmac_f32_e32 v87, v76, v142
	v_mul_f32_e32 v142, v75, v145
	v_fmac_f32_e32 v142, v74, v144
	v_add_f32_e32 v87, v87, v142
	ds_read_b128 v[142:145], v98 offset:19456
	v_add_f32_e32 v86, v86, v87
	s_waitcnt lgkmcnt(0)
	v_mul_f32_e32 v87, v15, v143
	v_mul_f32_e32 v146, v13, v145
	v_fmac_f32_e32 v87, v14, v142
	v_fmac_f32_e32 v146, v12, v144
	v_add_f32_e32 v87, v87, v146
	v_add_f32_e32 v73, v73, v87
	v_mul_f32_e32 v87, v71, v143
	v_fmac_f32_e32 v87, v70, v142
	v_mul_f32_e32 v142, v69, v145
	v_fmac_f32_e32 v142, v68, v144
	v_add_f32_e32 v87, v87, v142
	ds_read_b128 v[142:145], v98 offset:20480
	v_add_f32_e32 v86, v86, v87
	s_waitcnt lgkmcnt(0)
	v_mul_f32_e32 v87, v19, v143
	v_mul_f32_e32 v146, v17, v145
	v_fmac_f32_e32 v87, v18, v142
	v_fmac_f32_e32 v146, v16, v144
	v_add_f32_e32 v87, v87, v146
	v_add_f32_e32 v73, v73, v87
	v_mul_f32_e32 v87, v67, v143
	v_fmac_f32_e32 v87, v66, v142
	v_mul_f32_e32 v142, v65, v145
	v_fmac_f32_e32 v142, v64, v144
	v_add_f32_e32 v87, v87, v142
	ds_read_b128 v[142:145], v98 offset:21504
	v_add_f32_e32 v86, v86, v87
	s_waitcnt lgkmcnt(0)
	v_mul_f32_e32 v87, v41, v143
	v_mul_f32_e32 v146, v21, v145
	v_fmac_f32_e32 v87, v40, v142
	v_fmac_f32_e32 v146, v20, v144
	v_add_f32_e32 v87, v87, v146
	v_add_f32_e32 v73, v73, v87
	v_mul_f32_e32 v87, v63, v143
	v_fmac_f32_e32 v87, v62, v142
	v_mul_f32_e32 v142, v61, v145
	v_fmac_f32_e32 v142, v60, v144
	v_add_f32_e32 v87, v87, v142
	ds_read_b128 v[142:145], v98 offset:22528
	v_add_f32_e32 v86, v86, v87
	s_waitcnt lgkmcnt(0)
	v_mul_f32_e32 v87, v45, v143
	v_mul_f32_e32 v146, v43, v145
	v_fmac_f32_e32 v87, v44, v142
	v_fmac_f32_e32 v146, v42, v144
	v_add_f32_e32 v87, v87, v146
	v_add_f32_e32 v73, v73, v87
	v_mul_f32_e32 v87, v59, v143
	v_fmac_f32_e32 v87, v58, v142
	v_mul_f32_e32 v142, v57, v145
	v_fmac_f32_e32 v142, v56, v144
	v_add_f32_e32 v87, v87, v142
	ds_read_b128 v[142:145], v98 offset:23552
	v_add_f32_e32 v87, v86, v87
	s_waitcnt lgkmcnt(0)
	v_mul_f32_e32 v86, v49, v143
	v_mul_f32_e32 v146, v47, v145
	v_fmac_f32_e32 v86, v48, v142
	v_fmac_f32_e32 v146, v46, v144
	v_add_f32_e32 v86, v86, v146
	v_add_f32_e32 v86, v73, v86
	v_mul_f32_e32 v73, v53, v143
	v_fmac_f32_e32 v73, v52, v142
	v_mul_f32_e32 v142, v51, v145
	v_fmac_f32_e32 v142, v50, v144
	v_add_f32_e32 v73, v73, v142
	ds_read_b128 v[142:145], v98 offset:24576
	v_add_f32_e32 v73, v87, v73
	s_waitcnt lgkmcnt(0)
	v_mul_f32_e32 v7, v7, v143
	v_mul_f32_e32 v5, v5, v145
	v_fmac_f32_e32 v7, v6, v142
	v_fmac_f32_e32 v5, v4, v144
	v_add_f32_e32 v4, v7, v5
	v_add_f32_e32 v87, 0, v4
	v_mul_f32_e32 v4, v85, v143
	v_mul_f32_e32 v5, v83, v145
	v_fmac_f32_e32 v4, v84, v142
	v_fmac_f32_e32 v5, v82, v144
	v_add_f32_e32 v4, v4, v5
	v_add_f32_e32 v82, 0, v4
	ds_read_b128 v[4:7], v98 offset:25600
	s_waitcnt lgkmcnt(0)
	v_mul_f32_e32 v3, v3, v5
	v_mul_f32_e32 v1, v1, v7
	v_fmac_f32_e32 v3, v2, v4
	v_fmac_f32_e32 v1, v0, v6
	v_add_f32_e32 v0, v3, v1
	v_add_f32_e32 v83, v87, v0
	v_mul_f32_e32 v0, v81, v5
	v_mul_f32_e32 v1, v79, v7
	v_fmac_f32_e32 v0, v80, v4
	v_fmac_f32_e32 v1, v78, v6
	v_add_f32_e32 v0, v0, v1
	v_add_f32_e32 v4, v82, v0
	ds_read_b128 v[0:3], v98 offset:26624
	v_and_b32_e32 v81, 0xffff0000, v136
	v_and_b32_e32 v78, 0xffff0000, v89
	v_and_b32_e32 v87, 0xffff0000, v118
	s_waitcnt lgkmcnt(0)
	v_mul_f32_e32 v5, v11, v1
	v_mul_f32_e32 v1, v77, v1
	v_fmac_f32_e32 v5, v10, v0
	v_fmac_f32_e32 v1, v76, v0
	v_mul_f32_e32 v0, v75, v3
	v_fmac_f32_e32 v0, v74, v2
	v_mul_f32_e32 v6, v9, v3
	v_add_f32_e32 v0, v1, v0
	v_fmac_f32_e32 v6, v8, v2
	v_add_f32_e32 v4, v4, v0
	ds_read_b128 v[0:3], v98 offset:27648
	v_add_f32_e32 v5, v5, v6
	v_add_f32_e32 v5, v83, v5
	v_and_b32_e32 v11, 0xffff0000, v130
	v_and_b32_e32 v76, 0xffff0000, v137
	s_waitcnt lgkmcnt(0)
	v_mul_f32_e32 v6, v15, v1
	v_mul_f32_e32 v1, v71, v1
	v_fmac_f32_e32 v6, v14, v0
	v_fmac_f32_e32 v1, v70, v0
	v_mul_f32_e32 v0, v69, v3
	v_fmac_f32_e32 v0, v68, v2
	v_mul_f32_e32 v7, v13, v3
	v_add_f32_e32 v0, v1, v0
	v_fmac_f32_e32 v7, v12, v2
	v_add_f32_e32 v4, v4, v0
	ds_read_b128 v[0:3], v98 offset:28672
	v_add_f32_e32 v6, v6, v7
	v_add_f32_e32 v5, v5, v6
	ds_read2st64_b64 v[12:15], v99 offset0:64 offset1:65
	ds_read2st64_b64 v[68:71], v99 offset0:68 offset1:69
	s_waitcnt lgkmcnt(2)
	v_mul_f32_e32 v6, v19, v1
	v_mul_f32_e32 v1, v67, v1
	v_fmac_f32_e32 v6, v18, v0
	v_fmac_f32_e32 v1, v66, v0
	v_mul_f32_e32 v0, v65, v3
	v_fmac_f32_e32 v0, v64, v2
	v_mul_f32_e32 v7, v17, v3
	v_add_f32_e32 v0, v1, v0
	v_fmac_f32_e32 v7, v16, v2
	v_add_f32_e32 v4, v4, v0
	ds_read_b128 v[0:3], v98 offset:29696
	v_add_f32_e32 v6, v6, v7
	v_add_f32_e32 v5, v5, v6
	s_waitcnt lgkmcnt(1)
	v_and_b32_e32 v65, 0xffff0000, v69
	v_lshlrev_b32_e32 v74, 16, v71
	s_waitcnt lgkmcnt(0)
	v_mul_f32_e32 v6, v41, v1
	v_mul_f32_e32 v1, v63, v1
	v_fmac_f32_e32 v6, v40, v0
	v_fmac_f32_e32 v1, v62, v0
	v_mul_f32_e32 v0, v61, v3
	v_fmac_f32_e32 v0, v60, v2
	v_mul_f32_e32 v7, v21, v3
	v_add_f32_e32 v0, v1, v0
	v_fmac_f32_e32 v7, v20, v2
	v_add_f32_e32 v4, v4, v0
	ds_read_b128 v[0:3], v98 offset:30720
	v_add_f32_e32 v6, v6, v7
	v_add_f32_e32 v5, v5, v6
	v_and_b32_e32 v41, 0xffff0000, v140
	v_and_b32_e32 v62, 0xffff0000, v68
	s_waitcnt lgkmcnt(0)
	v_mul_f32_e32 v6, v45, v1
	v_mul_f32_e32 v1, v59, v1
	v_fmac_f32_e32 v6, v44, v0
	v_mul_f32_e32 v7, v43, v3
	v_fmac_f32_e32 v1, v58, v0
	v_mul_f32_e32 v0, v57, v3
	v_fmac_f32_e32 v7, v42, v2
	v_fmac_f32_e32 v0, v56, v2
	v_add_f32_e32 v6, v6, v7
	v_add_f32_e32 v0, v1, v0
	v_add_f32_e32 v6, v5, v6
	v_add_f32_e32 v0, v4, v0
	ds_read_b128 v[2:5], v98 offset:31744
	v_and_b32_e32 v42, 0xffff0000, v116
	v_and_b32_e32 v59, 0xffff0000, v88
	v_lshlrev_b32_e32 v63, 16, v69
	v_mul_f32_e32 v64, v59, v65
	s_waitcnt lgkmcnt(0)
	v_mul_f32_e32 v1, v49, v3
	v_mul_f32_e32 v3, v53, v3
	v_fmac_f32_e32 v1, v48, v2
	v_mul_f32_e32 v7, v47, v5
	v_fmac_f32_e32 v3, v52, v2
	v_mul_f32_e32 v2, v51, v5
	v_fmac_f32_e32 v7, v46, v4
	v_fmac_f32_e32 v2, v50, v4
	v_add_f32_e32 v1, v1, v7
	v_add_f32_e32 v2, v3, v2
	v_add_f32_e32 v1, v6, v1
	v_add_f32_e32 v0, v0, v2
	v_and_b32_e32 v5, 0xffff0000, v122
	v_and_b32_e32 v6, 0xffff0000, v120
	ds_read2st64_b64 v[48:51], v99 offset0:66 offset1:67
	v_lshlrev_b32_e32 v2, 16, v12
	v_and_b32_e32 v9, 0xffff0000, v12
	v_and_b32_e32 v12, 0xffff0000, v13
	v_lshlrev_b32_e32 v3, 16, v122
	v_mul_f32_e32 v7, v5, v9
	v_lshlrev_b32_e32 v4, 16, v120
	v_lshlrev_b32_e32 v10, 16, v13
	v_mul_f32_e32 v8, v6, v12
	v_fmac_f32_e32 v7, v3, v2
	v_fmac_f32_e32 v8, v4, v10
	v_add_f32_e32 v7, v7, v8
	v_and_b32_e32 v8, 0xffff0000, v131
	v_add_f32_e32 v16, 0, v7
	v_lshlrev_b32_e32 v7, 16, v131
	v_mul_f32_e32 v13, v8, v9
	v_fmac_f32_e32 v13, v7, v2
	v_lshlrev_b32_e32 v9, 16, v130
	v_mul_f32_e32 v2, v11, v12
	v_fmac_f32_e32 v2, v9, v10
	v_add_f32_e32 v2, v13, v2
	v_lshlrev_b32_e32 v17, 16, v14
	v_and_b32_e32 v13, 0xffff0000, v127
	v_and_b32_e32 v19, 0xffff0000, v14
	v_lshlrev_b32_e32 v20, 16, v15
	v_and_b32_e32 v14, 0xffff0000, v126
	v_and_b32_e32 v15, 0xffff0000, v15
	v_lshlrev_b32_e32 v10, 16, v127
	v_mul_f32_e32 v18, v13, v19
	v_lshlrev_b32_e32 v12, 16, v126
	v_mul_f32_e32 v21, v14, v15
	v_fmac_f32_e32 v18, v10, v17
	v_fmac_f32_e32 v21, v12, v20
	v_add_f32_e32 v18, v18, v21
	v_add_f32_e32 v21, v16, v18
	v_and_b32_e32 v18, 0xffff0000, v141
	v_lshlrev_b32_e32 v16, 16, v141
	v_mul_f32_e32 v40, v18, v19
	v_lshlrev_b32_e32 v19, 16, v140
	v_mul_f32_e32 v15, v41, v15
	v_fmac_f32_e32 v40, v16, v17
	v_fmac_f32_e32 v15, v19, v20
	v_add_f32_e32 v2, 0, v2
	v_add_f32_e32 v15, v40, v15
	s_waitcnt lgkmcnt(0)
	v_lshlrev_b32_e32 v40, 16, v48
	v_and_b32_e32 v20, 0xffff0000, v117
	v_and_b32_e32 v43, 0xffff0000, v48
	v_and_b32_e32 v48, 0xffff0000, v49
	v_add_f32_e32 v2, v2, v15
	v_lshlrev_b32_e32 v15, 16, v117
	v_mul_f32_e32 v44, v20, v43
	v_lshlrev_b32_e32 v17, 16, v116
	v_lshlrev_b32_e32 v47, 16, v49
	v_mul_f32_e32 v45, v42, v48
	v_fmac_f32_e32 v44, v15, v40
	v_fmac_f32_e32 v45, v17, v47
	v_add_f32_e32 v44, v44, v45
	v_and_b32_e32 v45, 0xffff0000, v135
	v_add_f32_e32 v52, v21, v44
	v_lshlrev_b32_e32 v21, 16, v135
	v_mul_f32_e32 v44, v45, v43
	v_and_b32_e32 v46, 0xffff0000, v134
	v_fmac_f32_e32 v44, v21, v40
	v_lshlrev_b32_e32 v43, 16, v134
	v_mul_f32_e32 v40, v46, v48
	v_fmac_f32_e32 v40, v43, v47
	v_add_f32_e32 v40, v44, v40
	v_lshlrev_b32_e32 v53, 16, v50
	v_and_b32_e32 v47, 0xffff0000, v125
	v_and_b32_e32 v50, 0xffff0000, v50
	v_and_b32_e32 v49, 0xffff0000, v124
	v_and_b32_e32 v57, 0xffff0000, v51
	v_add_f32_e32 v2, v2, v40
	v_lshlrev_b32_e32 v40, 16, v125
	v_mul_f32_e32 v48, v47, v50
	v_lshlrev_b32_e32 v44, 16, v124
	v_lshlrev_b32_e32 v56, 16, v51
	v_mul_f32_e32 v51, v49, v57
	v_fmac_f32_e32 v48, v40, v53
	v_fmac_f32_e32 v51, v44, v56
	v_add_f32_e32 v48, v48, v51
	v_and_b32_e32 v51, 0xffff0000, v139
	v_add_f32_e32 v60, v52, v48
	v_lshlrev_b32_e32 v48, 16, v139
	v_mul_f32_e32 v58, v51, v50
	v_and_b32_e32 v52, 0xffff0000, v138
	v_fmac_f32_e32 v58, v48, v53
	v_lshlrev_b32_e32 v50, 16, v138
	v_mul_f32_e32 v53, v52, v57
	v_fmac_f32_e32 v53, v50, v56
	v_add_f32_e32 v53, v58, v53
	v_and_b32_e32 v58, 0xffff0000, v114
	v_add_f32_e32 v2, v2, v53
	v_lshlrev_b32_e32 v56, 16, v114
	v_lshlrev_b32_e32 v53, 16, v68
	v_mul_f32_e32 v61, v58, v62
	v_lshlrev_b32_e32 v57, 16, v88
	v_fmac_f32_e32 v61, v56, v53
	v_fmac_f32_e32 v64, v57, v63
	v_add_f32_e32 v61, v61, v64
	v_add_f32_e32 v67, v60, v61
	v_and_b32_e32 v61, 0xffff0000, v133
	v_lshlrev_b32_e32 v60, 16, v133
	v_mul_f32_e32 v66, v61, v62
	v_and_b32_e32 v64, 0xffff0000, v132
	v_fmac_f32_e32 v66, v60, v53
	v_lshlrev_b32_e32 v62, 16, v132
	v_mul_f32_e32 v53, v64, v65
	v_fmac_f32_e32 v53, v62, v63
	v_add_f32_e32 v53, v66, v53
	v_and_b32_e32 v66, 0xffff0000, v123
	v_and_b32_e32 v68, 0xffff0000, v70
	v_and_b32_e32 v69, 0xffff0000, v121
	v_and_b32_e32 v71, 0xffff0000, v71
	v_add_f32_e32 v2, v2, v53
	v_lshlrev_b32_e32 v63, 16, v123
	v_lshlrev_b32_e32 v53, 16, v70
	v_mul_f32_e32 v70, v66, v68
	v_lshlrev_b32_e32 v65, 16, v121
	v_mul_f32_e32 v75, v69, v71
	v_fmac_f32_e32 v70, v63, v53
	v_fmac_f32_e32 v75, v65, v74
	ds_read2st64_b64 v[120:123], v99 offset0:70 offset1:71
	v_add_f32_e32 v70, v70, v75
	v_add_f32_e32 v75, v67, v70
	v_lshlrev_b32_e32 v70, 16, v137
	v_mul_f32_e32 v67, v76, v68
	v_fmac_f32_e32 v67, v70, v53
	v_lshlrev_b32_e32 v77, 16, v136
	v_mul_f32_e32 v53, v81, v71
	v_fmac_f32_e32 v53, v77, v74
	v_add_f32_e32 v53, v67, v53
	v_and_b32_e32 v71, 0xffff0000, v115
	s_waitcnt lgkmcnt(0)
	v_and_b32_e32 v79, 0xffff0000, v120
	v_and_b32_e32 v84, 0xffff0000, v121
	v_add_f32_e32 v2, v2, v53
	v_lshlrev_b32_e32 v67, 16, v115
	v_lshlrev_b32_e32 v53, 16, v120
	v_mul_f32_e32 v74, v71, v79
	v_lshlrev_b32_e32 v68, 16, v89
	v_lshlrev_b32_e32 v80, 16, v121
	v_mul_f32_e32 v82, v78, v84
	v_fmac_f32_e32 v74, v67, v53
	v_fmac_f32_e32 v82, v68, v80
	v_add_f32_e32 v74, v74, v82
	v_and_b32_e32 v82, 0xffff0000, v129
	v_add_f32_e32 v85, v75, v74
	v_lshlrev_b32_e32 v74, 16, v129
	v_mul_f32_e32 v75, v82, v79
	v_and_b32_e32 v83, 0xffff0000, v128
	v_fmac_f32_e32 v75, v74, v53
	v_lshlrev_b32_e32 v79, 16, v128
	v_mul_f32_e32 v53, v83, v84
	v_fmac_f32_e32 v53, v79, v80
	v_add_f32_e32 v53, v75, v53
	v_and_b32_e32 v84, 0xffff0000, v119
	v_and_b32_e32 v114, 0xffff0000, v122
	v_and_b32_e32 v116, 0xffff0000, v123
	v_add_f32_e32 v2, v2, v53
	v_lshlrev_b32_e32 v75, 16, v119
	v_lshlrev_b32_e32 v88, 16, v122
	v_mul_f32_e32 v53, v84, v114
	v_lshlrev_b32_e32 v80, 16, v118
	v_lshlrev_b32_e32 v115, 16, v123
	v_mul_f32_e32 v89, v87, v116
	v_fmac_f32_e32 v53, v75, v88
	v_fmac_f32_e32 v89, v80, v115
	v_add_f32_e32 v53, v53, v89
	v_and_b32_e32 v89, 0xffff0000, v91
	v_add_f32_e32 v53, v85, v53
	v_lshlrev_b32_e32 v85, 16, v91
	v_mul_f32_e32 v91, v89, v114
	v_fmac_f32_e32 v91, v85, v88
	v_lshlrev_b32_e32 v88, 16, v90
	v_and_b32_e32 v90, 0xffff0000, v90
	v_mul_f32_e32 v114, v90, v116
	v_fmac_f32_e32 v114, v88, v115
	v_add_f32_e32 v91, v91, v114
	ds_read2st64_b64 v[114:117], v99 offset0:72 offset1:73
	v_add_f32_e32 v2, v2, v91
	s_waitcnt lgkmcnt(0)
	v_lshlrev_b32_e32 v91, 16, v114
	v_and_b32_e32 v114, 0xffff0000, v114
	v_mul_f32_e32 v118, v5, v114
	v_lshlrev_b32_e32 v119, 16, v115
	v_and_b32_e32 v115, 0xffff0000, v115
	v_mul_f32_e32 v114, v8, v114
	v_fmac_f32_e32 v118, v3, v91
	v_fmac_f32_e32 v114, v7, v91
	v_mul_f32_e32 v91, v11, v115
	v_mul_f32_e32 v120, v6, v115
	v_fmac_f32_e32 v91, v9, v119
	v_and_b32_e32 v115, 0xffff0000, v116
	v_fmac_f32_e32 v120, v4, v119
	v_add_f32_e32 v91, v114, v91
	v_lshlrev_b32_e32 v114, 16, v116
	v_mul_f32_e32 v116, v13, v115
	v_lshlrev_b32_e32 v119, 16, v117
	v_and_b32_e32 v117, 0xffff0000, v117
	v_mul_f32_e32 v115, v18, v115
	v_add_f32_e32 v118, v118, v120
	v_fmac_f32_e32 v116, v10, v114
	v_mul_f32_e32 v120, v14, v117
	v_fmac_f32_e32 v115, v16, v114
	v_mul_f32_e32 v114, v41, v117
	v_fmac_f32_e32 v120, v12, v119
	v_fmac_f32_e32 v114, v19, v119
	v_add_f32_e32 v118, 0, v118
	v_add_f32_e32 v91, 0, v91
	v_add_f32_e32 v116, v116, v120
	v_add_f32_e32 v114, v115, v114
	v_add_f32_e32 v118, v118, v116
	v_add_f32_e32 v91, v91, v114
	ds_read2st64_b64 v[114:117], v99 offset0:74 offset1:75
	s_waitcnt lgkmcnt(0)
	v_lshlrev_b32_e32 v119, 16, v114
	v_and_b32_e32 v114, 0xffff0000, v114
	v_lshlrev_b32_e32 v121, 16, v115
	v_and_b32_e32 v115, 0xffff0000, v115
	v_mul_f32_e32 v120, v20, v114
	v_mul_f32_e32 v122, v42, v115
	v_mul_f32_e32 v114, v45, v114
	v_mul_f32_e32 v115, v46, v115
	v_fmac_f32_e32 v114, v21, v119
	v_fmac_f32_e32 v115, v43, v121
	v_fmac_f32_e32 v120, v15, v119
	v_fmac_f32_e32 v122, v17, v121
	v_add_f32_e32 v114, v114, v115
	v_and_b32_e32 v115, 0xffff0000, v116
	v_add_f32_e32 v120, v120, v122
	v_add_f32_e32 v91, v91, v114
	v_lshlrev_b32_e32 v114, 16, v116
	v_mul_f32_e32 v116, v47, v115
	v_lshlrev_b32_e32 v119, 16, v117
	v_and_b32_e32 v117, 0xffff0000, v117
	v_mul_f32_e32 v115, v51, v115
	v_add_f32_e32 v118, v118, v120
	v_fmac_f32_e32 v116, v40, v114
	v_mul_f32_e32 v120, v49, v117
	v_fmac_f32_e32 v115, v48, v114
	v_mul_f32_e32 v114, v52, v117
	v_fmac_f32_e32 v120, v44, v119
	v_fmac_f32_e32 v114, v50, v119
	v_add_f32_e32 v116, v116, v120
	v_add_f32_e32 v114, v115, v114
	v_add_f32_e32 v118, v118, v116
	v_add_f32_e32 v91, v91, v114
	ds_read2st64_b64 v[114:117], v99 offset0:76 offset1:77
	s_waitcnt lgkmcnt(0)
	v_lshlrev_b32_e32 v119, 16, v114
	v_and_b32_e32 v114, 0xffff0000, v114
	v_lshlrev_b32_e32 v121, 16, v115
	v_and_b32_e32 v115, 0xffff0000, v115
	v_mul_f32_e32 v120, v58, v114
	v_mul_f32_e32 v122, v59, v115
	v_mul_f32_e32 v114, v61, v114
	v_mul_f32_e32 v115, v64, v115
	v_fmac_f32_e32 v114, v60, v119
	v_fmac_f32_e32 v115, v62, v121
	v_fmac_f32_e32 v120, v56, v119
	v_fmac_f32_e32 v122, v57, v121
	v_add_f32_e32 v114, v114, v115
	v_and_b32_e32 v115, 0xffff0000, v116
	v_add_f32_e32 v120, v120, v122
	v_add_f32_e32 v91, v91, v114
	v_lshlrev_b32_e32 v114, 16, v116
	v_mul_f32_e32 v116, v66, v115
	v_lshlrev_b32_e32 v119, 16, v117
	v_and_b32_e32 v117, 0xffff0000, v117
	v_mul_f32_e32 v115, v76, v115
	v_add_f32_e32 v118, v118, v120
	v_fmac_f32_e32 v116, v63, v114
	v_mul_f32_e32 v120, v69, v117
	v_fmac_f32_e32 v115, v70, v114
	v_mul_f32_e32 v114, v81, v117
	v_fmac_f32_e32 v120, v65, v119
	v_fmac_f32_e32 v114, v77, v119
	v_add_f32_e32 v116, v116, v120
	v_add_f32_e32 v114, v115, v114
	v_add_f32_e32 v118, v118, v116
	v_add_f32_e32 v91, v91, v114
	ds_read2st64_b64 v[114:117], v99 offset0:78 offset1:79
	s_waitcnt lgkmcnt(0)
	v_lshlrev_b32_e32 v119, 16, v114
	v_and_b32_e32 v114, 0xffff0000, v114
	v_lshlrev_b32_e32 v121, 16, v115
	v_and_b32_e32 v115, 0xffff0000, v115
	v_mul_f32_e32 v120, v71, v114
	v_mul_f32_e32 v122, v78, v115
	v_mul_f32_e32 v114, v82, v114
	v_mul_f32_e32 v115, v83, v115
	v_fmac_f32_e32 v120, v67, v119
	v_fmac_f32_e32 v122, v68, v121
	v_fmac_f32_e32 v114, v74, v119
	v_fmac_f32_e32 v115, v79, v121
	v_add_f32_e32 v120, v120, v122
	v_add_f32_e32 v114, v114, v115
	v_lshlrev_b32_e32 v115, 16, v116
	v_and_b32_e32 v116, 0xffff0000, v116
	v_lshlrev_b32_e32 v119, 16, v117
	v_and_b32_e32 v117, 0xffff0000, v117
	v_add_f32_e32 v118, v118, v120
	v_add_f32_e32 v91, v91, v114
	v_mul_f32_e32 v114, v84, v116
	v_mul_f32_e32 v120, v87, v117
	v_mul_f32_e32 v116, v89, v116
	v_fmac_f32_e32 v114, v75, v115
	v_fmac_f32_e32 v120, v80, v119
	v_fmac_f32_e32 v116, v85, v115
	v_mul_f32_e32 v115, v90, v117
	v_add_f32_e32 v114, v114, v120
	v_fmac_f32_e32 v115, v88, v119
	v_add_f32_e32 v114, v118, v114
	v_add_f32_e32 v115, v116, v115
	ds_read2st64_b64 v[116:119], v99 offset0:80 offset1:81
	v_add_f32_e32 v91, v91, v115
	s_waitcnt lgkmcnt(0)
	v_lshlrev_b32_e32 v115, 16, v116
	v_and_b32_e32 v116, 0xffff0000, v116
	v_mul_f32_e32 v120, v5, v116
	v_lshlrev_b32_e32 v121, 16, v117
	v_and_b32_e32 v117, 0xffff0000, v117
	v_mul_f32_e32 v116, v8, v116
	v_fmac_f32_e32 v120, v3, v115
	v_fmac_f32_e32 v116, v7, v115
	v_mul_f32_e32 v115, v11, v117
	v_mul_f32_e32 v122, v6, v117
	v_fmac_f32_e32 v115, v9, v121
	v_and_b32_e32 v117, 0xffff0000, v118
	v_fmac_f32_e32 v122, v4, v121
	v_add_f32_e32 v115, v116, v115
	v_lshlrev_b32_e32 v116, 16, v118
	v_mul_f32_e32 v118, v13, v117
	v_lshlrev_b32_e32 v121, 16, v119
	v_and_b32_e32 v119, 0xffff0000, v119
	v_mul_f32_e32 v117, v18, v117
	v_add_f32_e32 v120, v120, v122
	v_fmac_f32_e32 v118, v10, v116
	v_mul_f32_e32 v122, v14, v119
	v_fmac_f32_e32 v117, v16, v116
	v_mul_f32_e32 v116, v41, v119
	v_fmac_f32_e32 v122, v12, v121
	v_fmac_f32_e32 v116, v19, v121
	v_add_f32_e32 v120, 0, v120
	v_add_f32_e32 v115, 0, v115
	v_add_f32_e32 v118, v118, v122
	v_add_f32_e32 v116, v117, v116
	v_add_f32_e32 v120, v120, v118
	v_add_f32_e32 v115, v115, v116
	ds_read2st64_b64 v[116:119], v99 offset0:82 offset1:83
	s_waitcnt lgkmcnt(0)
	v_lshlrev_b32_e32 v121, 16, v116
	v_and_b32_e32 v116, 0xffff0000, v116
	v_lshlrev_b32_e32 v123, 16, v117
	v_and_b32_e32 v117, 0xffff0000, v117
	v_mul_f32_e32 v122, v20, v116
	v_mul_f32_e32 v124, v42, v117
	v_mul_f32_e32 v116, v45, v116
	v_mul_f32_e32 v117, v46, v117
	v_fmac_f32_e32 v116, v21, v121
	v_fmac_f32_e32 v117, v43, v123
	v_fmac_f32_e32 v122, v15, v121
	v_fmac_f32_e32 v124, v17, v123
	v_add_f32_e32 v116, v116, v117
	v_and_b32_e32 v117, 0xffff0000, v118
	v_add_f32_e32 v122, v122, v124
	v_add_f32_e32 v115, v115, v116
	v_lshlrev_b32_e32 v116, 16, v118
	v_mul_f32_e32 v118, v47, v117
	v_lshlrev_b32_e32 v121, 16, v119
	v_and_b32_e32 v119, 0xffff0000, v119
	v_mul_f32_e32 v117, v51, v117
	v_add_f32_e32 v120, v120, v122
	v_fmac_f32_e32 v118, v40, v116
	v_mul_f32_e32 v122, v49, v119
	v_fmac_f32_e32 v117, v48, v116
	v_mul_f32_e32 v116, v52, v119
	v_fmac_f32_e32 v122, v44, v121
	v_fmac_f32_e32 v116, v50, v121
	v_add_f32_e32 v118, v118, v122
	v_add_f32_e32 v116, v117, v116
	v_add_f32_e32 v120, v120, v118
	v_add_f32_e32 v115, v115, v116
	ds_read2st64_b64 v[116:119], v99 offset0:84 offset1:85
	s_waitcnt lgkmcnt(0)
	v_lshlrev_b32_e32 v121, 16, v116
	v_and_b32_e32 v116, 0xffff0000, v116
	v_lshlrev_b32_e32 v123, 16, v117
	v_and_b32_e32 v117, 0xffff0000, v117
	v_mul_f32_e32 v122, v58, v116
	v_mul_f32_e32 v124, v59, v117
	v_mul_f32_e32 v116, v61, v116
	v_mul_f32_e32 v117, v64, v117
	v_fmac_f32_e32 v116, v60, v121
	v_fmac_f32_e32 v117, v62, v123
	v_fmac_f32_e32 v122, v56, v121
	v_fmac_f32_e32 v124, v57, v123
	v_add_f32_e32 v116, v116, v117
	v_and_b32_e32 v117, 0xffff0000, v118
	v_add_f32_e32 v122, v122, v124
	v_add_f32_e32 v115, v115, v116
	v_lshlrev_b32_e32 v116, 16, v118
	v_mul_f32_e32 v118, v66, v117
	v_lshlrev_b32_e32 v121, 16, v119
	v_and_b32_e32 v119, 0xffff0000, v119
	v_mul_f32_e32 v117, v76, v117
	v_add_f32_e32 v120, v120, v122
	v_fmac_f32_e32 v118, v63, v116
	v_mul_f32_e32 v122, v69, v119
	v_fmac_f32_e32 v117, v70, v116
	v_mul_f32_e32 v116, v81, v119
	v_fmac_f32_e32 v122, v65, v121
	v_fmac_f32_e32 v116, v77, v121
	v_add_f32_e32 v118, v118, v122
	v_add_f32_e32 v116, v117, v116
	v_add_f32_e32 v120, v120, v118
	v_add_f32_e32 v115, v115, v116
	ds_read2st64_b64 v[116:119], v99 offset0:86 offset1:87
	s_waitcnt lgkmcnt(0)
	v_lshlrev_b32_e32 v121, 16, v116
	v_and_b32_e32 v116, 0xffff0000, v116
	v_lshlrev_b32_e32 v123, 16, v117
	v_and_b32_e32 v117, 0xffff0000, v117
	v_mul_f32_e32 v122, v71, v116
	v_mul_f32_e32 v124, v78, v117
	v_mul_f32_e32 v116, v82, v116
	v_mul_f32_e32 v117, v83, v117
	v_fmac_f32_e32 v122, v67, v121
	v_fmac_f32_e32 v124, v68, v123
	v_fmac_f32_e32 v116, v74, v121
	v_fmac_f32_e32 v117, v79, v123
	v_add_f32_e32 v122, v122, v124
	v_add_f32_e32 v116, v116, v117
	v_lshlrev_b32_e32 v117, 16, v118
	v_and_b32_e32 v118, 0xffff0000, v118
	v_lshlrev_b32_e32 v121, 16, v119
	v_and_b32_e32 v119, 0xffff0000, v119
	v_add_f32_e32 v120, v120, v122
	v_add_f32_e32 v115, v115, v116
	v_mul_f32_e32 v116, v84, v118
	v_mul_f32_e32 v122, v87, v119
	v_mul_f32_e32 v118, v89, v118
	v_fmac_f32_e32 v116, v75, v117
	v_fmac_f32_e32 v122, v80, v121
	v_fmac_f32_e32 v118, v85, v117
	v_mul_f32_e32 v117, v90, v119
	v_add_f32_e32 v116, v116, v122
	v_fmac_f32_e32 v117, v88, v121
	v_add_f32_e32 v116, v120, v116
	v_add_f32_e32 v117, v118, v117
	ds_read2st64_b64 v[118:121], v99 offset0:88 offset1:89
	v_add_f32_e32 v115, v115, v117
	s_waitcnt lgkmcnt(0)
	v_lshlrev_b32_e32 v117, 16, v118
	v_and_b32_e32 v118, 0xffff0000, v118
	v_mul_f32_e32 v122, v5, v118
	v_lshlrev_b32_e32 v123, 16, v119
	v_and_b32_e32 v119, 0xffff0000, v119
	v_mul_f32_e32 v118, v8, v118
	v_fmac_f32_e32 v122, v3, v117
	v_fmac_f32_e32 v118, v7, v117
	v_mul_f32_e32 v117, v11, v119
	v_mul_f32_e32 v124, v6, v119
	v_fmac_f32_e32 v117, v9, v123
	v_and_b32_e32 v119, 0xffff0000, v120
	v_fmac_f32_e32 v124, v4, v123
	v_add_f32_e32 v117, v118, v117
	v_lshlrev_b32_e32 v118, 16, v120
	v_mul_f32_e32 v120, v13, v119
	v_lshlrev_b32_e32 v123, 16, v121
	v_and_b32_e32 v121, 0xffff0000, v121
	v_mul_f32_e32 v119, v18, v119
	v_add_f32_e32 v122, v122, v124
	v_fmac_f32_e32 v120, v10, v118
	v_mul_f32_e32 v124, v14, v121
	v_fmac_f32_e32 v119, v16, v118
	v_mul_f32_e32 v118, v41, v121
	v_fmac_f32_e32 v124, v12, v123
	v_fmac_f32_e32 v118, v19, v123
	v_add_f32_e32 v122, 0, v122
	v_add_f32_e32 v117, 0, v117
	v_add_f32_e32 v120, v120, v124
	v_add_f32_e32 v118, v119, v118
	v_add_f32_e32 v122, v122, v120
	v_add_f32_e32 v117, v117, v118
	ds_read2st64_b64 v[118:121], v99 offset0:90 offset1:91
	s_waitcnt lgkmcnt(0)
	v_lshlrev_b32_e32 v123, 16, v118
	v_and_b32_e32 v118, 0xffff0000, v118
	v_lshlrev_b32_e32 v125, 16, v119
	v_and_b32_e32 v119, 0xffff0000, v119
	v_mul_f32_e32 v124, v20, v118
	v_mul_f32_e32 v126, v42, v119
	v_mul_f32_e32 v118, v45, v118
	v_mul_f32_e32 v119, v46, v119
	v_fmac_f32_e32 v118, v21, v123
	v_fmac_f32_e32 v119, v43, v125
	v_add_f32_e32 v118, v118, v119
	v_and_b32_e32 v119, 0xffff0000, v120
	v_fmac_f32_e32 v124, v15, v123
	v_add_f32_e32 v117, v117, v118
	v_lshlrev_b32_e32 v118, 16, v120
	v_mul_f32_e32 v123, v47, v119
	v_lshlrev_b32_e32 v120, 16, v121
	v_and_b32_e32 v121, 0xffff0000, v121
	v_mul_f32_e32 v119, v51, v119
	v_fmac_f32_e32 v126, v17, v125
	v_fmac_f32_e32 v123, v40, v118
	v_fmac_f32_e32 v119, v48, v118
	v_mul_f32_e32 v118, v52, v121
	v_add_f32_e32 v124, v124, v126
	v_fmac_f32_e32 v118, v50, v120
	v_add_f32_e32 v122, v122, v124
	v_mul_f32_e32 v124, v49, v121
	v_add_f32_e32 v118, v119, v118
	v_fmac_f32_e32 v124, v44, v120
	v_add_f32_e32 v117, v117, v118
	ds_read2st64_b64 v[118:121], v99 offset0:92 offset1:93
	v_add_f32_e32 v123, v123, v124
	v_add_f32_e32 v122, v122, v123
	s_waitcnt lgkmcnt(0)
	v_lshlrev_b32_e32 v123, 16, v118
	v_and_b32_e32 v118, 0xffff0000, v118
	v_lshlrev_b32_e32 v125, 16, v119
	v_and_b32_e32 v119, 0xffff0000, v119
	v_mul_f32_e32 v124, v58, v118
	v_mul_f32_e32 v126, v59, v119
	v_mul_f32_e32 v118, v61, v118
	v_mul_f32_e32 v119, v64, v119
	v_fmac_f32_e32 v118, v60, v123
	v_fmac_f32_e32 v119, v62, v125
	v_fmac_f32_e32 v124, v56, v123
	v_fmac_f32_e32 v126, v57, v125
	v_add_f32_e32 v118, v118, v119
	v_and_b32_e32 v119, 0xffff0000, v120
	v_add_f32_e32 v124, v124, v126
	v_add_f32_e32 v117, v117, v118
	v_lshlrev_b32_e32 v118, 16, v120
	v_mul_f32_e32 v120, v66, v119
	v_lshlrev_b32_e32 v123, 16, v121
	v_and_b32_e32 v121, 0xffff0000, v121
	v_mul_f32_e32 v119, v76, v119
	v_add_f32_e32 v122, v122, v124
	v_fmac_f32_e32 v120, v63, v118
	v_mul_f32_e32 v124, v69, v121
	v_fmac_f32_e32 v119, v70, v118
	v_mul_f32_e32 v118, v81, v121
	v_fmac_f32_e32 v124, v65, v123
	v_fmac_f32_e32 v118, v77, v123
	v_add_f32_e32 v120, v120, v124
	v_add_f32_e32 v118, v119, v118
	v_add_f32_e32 v122, v122, v120
	v_add_f32_e32 v117, v117, v118
	ds_read2st64_b64 v[118:121], v99 offset0:94 offset1:95
	s_waitcnt lgkmcnt(0)
	v_lshlrev_b32_e32 v123, 16, v118
	v_and_b32_e32 v118, 0xffff0000, v118
	v_lshlrev_b32_e32 v125, 16, v119
	v_and_b32_e32 v119, 0xffff0000, v119
	v_mul_f32_e32 v124, v71, v118
	v_mul_f32_e32 v126, v78, v119
	v_mul_f32_e32 v118, v82, v118
	v_mul_f32_e32 v119, v83, v119
	v_fmac_f32_e32 v124, v67, v123
	v_fmac_f32_e32 v126, v68, v125
	v_fmac_f32_e32 v118, v74, v123
	v_fmac_f32_e32 v119, v79, v125
	v_add_f32_e32 v124, v124, v126
	v_add_f32_e32 v118, v118, v119
	v_lshlrev_b32_e32 v119, 16, v120
	v_and_b32_e32 v120, 0xffff0000, v120
	v_lshlrev_b32_e32 v123, 16, v121
	v_and_b32_e32 v121, 0xffff0000, v121
	v_add_f32_e32 v122, v122, v124
	v_add_f32_e32 v117, v117, v118
	v_mul_f32_e32 v118, v84, v120
	v_mul_f32_e32 v124, v87, v121
	v_mul_f32_e32 v120, v89, v120
	v_fmac_f32_e32 v118, v75, v119
	v_fmac_f32_e32 v124, v80, v123
	v_fmac_f32_e32 v120, v85, v119
	v_mul_f32_e32 v119, v90, v121
	v_add_f32_e32 v118, v118, v124
	v_fmac_f32_e32 v119, v88, v123
	v_add_f32_e32 v118, v122, v118
	v_add_f32_e32 v119, v120, v119
	ds_read2st64_b64 v[120:123], v99 offset0:96 offset1:97
	v_add_f32_e32 v117, v117, v119
	s_waitcnt lgkmcnt(0)
	v_lshlrev_b32_e32 v119, 16, v120
	v_and_b32_e32 v120, 0xffff0000, v120
	v_mul_f32_e32 v124, v5, v120
	v_lshlrev_b32_e32 v125, 16, v121
	v_and_b32_e32 v121, 0xffff0000, v121
	v_mul_f32_e32 v120, v8, v120
	v_fmac_f32_e32 v124, v3, v119
	v_fmac_f32_e32 v120, v7, v119
	v_mul_f32_e32 v119, v11, v121
	v_mul_f32_e32 v126, v6, v121
	v_fmac_f32_e32 v119, v9, v125
	v_and_b32_e32 v121, 0xffff0000, v122
	v_fmac_f32_e32 v126, v4, v125
	v_add_f32_e32 v119, v120, v119
	v_lshlrev_b32_e32 v120, 16, v122
	v_mul_f32_e32 v122, v13, v121
	v_lshlrev_b32_e32 v125, 16, v123
	v_and_b32_e32 v123, 0xffff0000, v123
	v_mul_f32_e32 v121, v18, v121
	v_add_f32_e32 v124, v124, v126
	v_fmac_f32_e32 v122, v10, v120
	v_mul_f32_e32 v126, v14, v123
	v_fmac_f32_e32 v121, v16, v120
	v_mul_f32_e32 v120, v41, v123
	v_fmac_f32_e32 v126, v12, v125
	v_fmac_f32_e32 v120, v19, v125
	v_add_f32_e32 v124, 0, v124
	v_add_f32_e32 v119, 0, v119
	v_add_f32_e32 v122, v122, v126
	v_add_f32_e32 v120, v121, v120
	v_add_f32_e32 v124, v124, v122
	v_add_f32_e32 v119, v119, v120
	ds_read2st64_b64 v[120:123], v99 offset0:98 offset1:99
	s_waitcnt lgkmcnt(0)
	v_lshlrev_b32_e32 v125, 16, v120
	v_and_b32_e32 v120, 0xffff0000, v120
	v_lshlrev_b32_e32 v127, 16, v121
	v_and_b32_e32 v121, 0xffff0000, v121
	v_mul_f32_e32 v126, v20, v120
	v_mul_f32_e32 v128, v42, v121
	v_mul_f32_e32 v120, v45, v120
	v_mul_f32_e32 v121, v46, v121
	v_fmac_f32_e32 v120, v21, v125
	v_fmac_f32_e32 v121, v43, v127
	v_fmac_f32_e32 v126, v15, v125
	v_fmac_f32_e32 v128, v17, v127
	v_add_f32_e32 v120, v120, v121
	v_and_b32_e32 v121, 0xffff0000, v122
	v_add_f32_e32 v126, v126, v128
	v_add_f32_e32 v119, v119, v120
	v_lshlrev_b32_e32 v120, 16, v122
	v_mul_f32_e32 v122, v47, v121
	v_lshlrev_b32_e32 v125, 16, v123
	v_and_b32_e32 v123, 0xffff0000, v123
	v_mul_f32_e32 v121, v51, v121
	v_add_f32_e32 v124, v124, v126
	v_fmac_f32_e32 v122, v40, v120
	v_mul_f32_e32 v126, v49, v123
	v_fmac_f32_e32 v121, v48, v120
	v_mul_f32_e32 v120, v52, v123
	v_fmac_f32_e32 v126, v44, v125
	v_fmac_f32_e32 v120, v50, v125
	v_add_f32_e32 v122, v122, v126
	v_add_f32_e32 v120, v121, v120
	v_add_f32_e32 v124, v124, v122
	v_add_f32_e32 v119, v119, v120
	ds_read2st64_b64 v[120:123], v99 offset0:100 offset1:101
	s_waitcnt lgkmcnt(0)
	v_lshlrev_b32_e32 v125, 16, v120
	v_and_b32_e32 v120, 0xffff0000, v120
	v_lshlrev_b32_e32 v127, 16, v121
	v_and_b32_e32 v121, 0xffff0000, v121
	v_mul_f32_e32 v126, v58, v120
	v_mul_f32_e32 v128, v59, v121
	v_mul_f32_e32 v120, v61, v120
	v_mul_f32_e32 v121, v64, v121
	v_fmac_f32_e32 v120, v60, v125
	v_fmac_f32_e32 v121, v62, v127
	v_fmac_f32_e32 v126, v56, v125
	v_fmac_f32_e32 v128, v57, v127
	v_add_f32_e32 v120, v120, v121
	v_and_b32_e32 v121, 0xffff0000, v122
	v_add_f32_e32 v126, v126, v128
	v_add_f32_e32 v119, v119, v120
	v_lshlrev_b32_e32 v120, 16, v122
	v_mul_f32_e32 v122, v66, v121
	v_lshlrev_b32_e32 v125, 16, v123
	v_and_b32_e32 v123, 0xffff0000, v123
	v_mul_f32_e32 v121, v76, v121
	v_add_f32_e32 v124, v124, v126
	v_fmac_f32_e32 v122, v63, v120
	v_mul_f32_e32 v126, v69, v123
	v_fmac_f32_e32 v121, v70, v120
	v_mul_f32_e32 v120, v81, v123
	v_fmac_f32_e32 v126, v65, v125
	v_fmac_f32_e32 v120, v77, v125
	v_add_f32_e32 v122, v122, v126
	v_add_f32_e32 v120, v121, v120
	v_add_f32_e32 v124, v124, v122
	v_add_f32_e32 v119, v119, v120
	ds_read2st64_b64 v[120:123], v99 offset0:102 offset1:103
	s_waitcnt lgkmcnt(0)
	v_lshlrev_b32_e32 v125, 16, v120
	v_and_b32_e32 v120, 0xffff0000, v120
	v_lshlrev_b32_e32 v127, 16, v121
	v_and_b32_e32 v121, 0xffff0000, v121
	v_mul_f32_e32 v126, v71, v120
	v_mul_f32_e32 v128, v78, v121
	v_mul_f32_e32 v120, v82, v120
	v_mul_f32_e32 v121, v83, v121
	v_fmac_f32_e32 v126, v67, v125
	v_fmac_f32_e32 v128, v68, v127
	v_fmac_f32_e32 v120, v74, v125
	v_fmac_f32_e32 v121, v79, v127
	v_add_f32_e32 v126, v126, v128
	v_add_f32_e32 v120, v120, v121
	v_lshlrev_b32_e32 v121, 16, v122
	v_and_b32_e32 v122, 0xffff0000, v122
	v_lshlrev_b32_e32 v125, 16, v123
	v_and_b32_e32 v123, 0xffff0000, v123
	v_add_f32_e32 v124, v124, v126
	v_add_f32_e32 v119, v119, v120
	v_mul_f32_e32 v120, v84, v122
	v_mul_f32_e32 v126, v87, v123
	v_mul_f32_e32 v122, v89, v122
	v_fmac_f32_e32 v120, v75, v121
	v_fmac_f32_e32 v126, v80, v125
	v_fmac_f32_e32 v122, v85, v121
	v_mul_f32_e32 v121, v90, v123
	v_add_f32_e32 v120, v120, v126
	v_fmac_f32_e32 v121, v88, v125
	v_add_f32_e32 v120, v124, v120
	v_add_f32_e32 v121, v122, v121
	ds_read2st64_b64 v[122:125], v99 offset0:104 offset1:105
	v_add_f32_e32 v119, v119, v121
	s_waitcnt lgkmcnt(0)
	v_lshlrev_b32_e32 v121, 16, v122
	v_and_b32_e32 v122, 0xffff0000, v122
	v_mul_f32_e32 v126, v5, v122
	v_lshlrev_b32_e32 v127, 16, v123
	v_and_b32_e32 v123, 0xffff0000, v123
	v_mul_f32_e32 v122, v8, v122
	v_fmac_f32_e32 v126, v3, v121
	v_fmac_f32_e32 v122, v7, v121
	v_mul_f32_e32 v121, v11, v123
	v_mul_f32_e32 v128, v6, v123
	v_fmac_f32_e32 v121, v9, v127
	v_and_b32_e32 v123, 0xffff0000, v124
	v_fmac_f32_e32 v128, v4, v127
	v_add_f32_e32 v121, v122, v121
	v_lshlrev_b32_e32 v122, 16, v124
	v_mul_f32_e32 v124, v13, v123
	v_lshlrev_b32_e32 v127, 16, v125
	v_and_b32_e32 v125, 0xffff0000, v125
	v_mul_f32_e32 v123, v18, v123
	v_add_f32_e32 v126, v126, v128
	v_fmac_f32_e32 v124, v10, v122
	v_mul_f32_e32 v128, v14, v125
	v_fmac_f32_e32 v123, v16, v122
	v_mul_f32_e32 v122, v41, v125
	v_fmac_f32_e32 v128, v12, v127
	v_fmac_f32_e32 v122, v19, v127
	v_add_f32_e32 v126, 0, v126
	v_add_f32_e32 v121, 0, v121
	v_add_f32_e32 v124, v124, v128
	v_add_f32_e32 v122, v123, v122
	v_add_f32_e32 v126, v126, v124
	v_add_f32_e32 v121, v121, v122
	ds_read2st64_b64 v[122:125], v99 offset0:106 offset1:107
	s_waitcnt lgkmcnt(0)
	v_lshlrev_b32_e32 v127, 16, v122
	v_and_b32_e32 v122, 0xffff0000, v122
	v_lshlrev_b32_e32 v129, 16, v123
	v_and_b32_e32 v123, 0xffff0000, v123
	v_mul_f32_e32 v128, v20, v122
	v_mul_f32_e32 v130, v42, v123
	v_mul_f32_e32 v122, v45, v122
	v_mul_f32_e32 v123, v46, v123
	v_fmac_f32_e32 v122, v21, v127
	v_fmac_f32_e32 v123, v43, v129
	v_fmac_f32_e32 v128, v15, v127
	v_fmac_f32_e32 v130, v17, v129
	v_add_f32_e32 v122, v122, v123
	v_and_b32_e32 v123, 0xffff0000, v124
	v_add_f32_e32 v128, v128, v130
	v_add_f32_e32 v121, v121, v122
	v_lshlrev_b32_e32 v122, 16, v124
	v_mul_f32_e32 v124, v47, v123
	v_lshlrev_b32_e32 v127, 16, v125
	v_and_b32_e32 v125, 0xffff0000, v125
	v_mul_f32_e32 v123, v51, v123
	v_add_f32_e32 v126, v126, v128
	v_fmac_f32_e32 v124, v40, v122
	v_mul_f32_e32 v128, v49, v125
	v_fmac_f32_e32 v123, v48, v122
	v_mul_f32_e32 v122, v52, v125
	v_fmac_f32_e32 v128, v44, v127
	v_fmac_f32_e32 v122, v50, v127
	v_add_f32_e32 v124, v124, v128
	v_add_f32_e32 v122, v123, v122
	v_add_f32_e32 v126, v126, v124
	v_add_f32_e32 v121, v121, v122
	ds_read2st64_b64 v[122:125], v99 offset0:108 offset1:109
	s_waitcnt lgkmcnt(0)
	v_lshlrev_b32_e32 v127, 16, v122
	v_and_b32_e32 v122, 0xffff0000, v122
	v_lshlrev_b32_e32 v129, 16, v123
	v_and_b32_e32 v123, 0xffff0000, v123
	v_mul_f32_e32 v128, v58, v122
	v_mul_f32_e32 v130, v59, v123
	v_mul_f32_e32 v122, v61, v122
	v_mul_f32_e32 v123, v64, v123
	v_fmac_f32_e32 v122, v60, v127
	v_fmac_f32_e32 v123, v62, v129
	v_fmac_f32_e32 v128, v56, v127
	v_fmac_f32_e32 v130, v57, v129
	v_add_f32_e32 v122, v122, v123
	v_and_b32_e32 v123, 0xffff0000, v124
	v_add_f32_e32 v128, v128, v130
	v_add_f32_e32 v121, v121, v122
	v_lshlrev_b32_e32 v122, 16, v124
	v_mul_f32_e32 v124, v66, v123
	v_lshlrev_b32_e32 v127, 16, v125
	v_and_b32_e32 v125, 0xffff0000, v125
	v_mul_f32_e32 v123, v76, v123
	v_add_f32_e32 v126, v126, v128
	v_fmac_f32_e32 v124, v63, v122
	v_mul_f32_e32 v128, v69, v125
	v_fmac_f32_e32 v123, v70, v122
	v_mul_f32_e32 v122, v81, v125
	v_fmac_f32_e32 v128, v65, v127
	v_fmac_f32_e32 v122, v77, v127
	v_add_f32_e32 v124, v124, v128
	v_add_f32_e32 v122, v123, v122
	v_add_f32_e32 v126, v126, v124
	v_add_f32_e32 v121, v121, v122
	ds_read2st64_b64 v[122:125], v99 offset0:110 offset1:111
	s_waitcnt lgkmcnt(0)
	v_lshlrev_b32_e32 v127, 16, v122
	v_and_b32_e32 v122, 0xffff0000, v122
	v_lshlrev_b32_e32 v129, 16, v123
	v_and_b32_e32 v123, 0xffff0000, v123
	v_mul_f32_e32 v128, v71, v122
	v_mul_f32_e32 v130, v78, v123
	v_mul_f32_e32 v122, v82, v122
	v_mul_f32_e32 v123, v83, v123
	v_fmac_f32_e32 v128, v67, v127
	v_fmac_f32_e32 v130, v68, v129
	v_fmac_f32_e32 v122, v74, v127
	v_fmac_f32_e32 v123, v79, v129
	v_add_f32_e32 v128, v128, v130
	v_add_f32_e32 v122, v122, v123
	v_lshlrev_b32_e32 v123, 16, v124
	v_and_b32_e32 v124, 0xffff0000, v124
	v_lshlrev_b32_e32 v127, 16, v125
	v_and_b32_e32 v125, 0xffff0000, v125
	v_add_f32_e32 v126, v126, v128
	v_add_f32_e32 v121, v121, v122
	v_mul_f32_e32 v122, v84, v124
	v_mul_f32_e32 v128, v87, v125
	v_mul_f32_e32 v124, v89, v124
	v_fmac_f32_e32 v122, v75, v123
	v_fmac_f32_e32 v128, v80, v127
	v_fmac_f32_e32 v124, v85, v123
	v_mul_f32_e32 v123, v90, v125
	v_add_f32_e32 v122, v122, v128
	v_fmac_f32_e32 v123, v88, v127
	v_add_f32_e32 v122, v126, v122
	v_add_f32_e32 v123, v124, v123
	ds_read2st64_b64 v[124:127], v99 offset0:112 offset1:113
	v_add_f32_e32 v121, v121, v123
	s_waitcnt lgkmcnt(0)
	v_lshlrev_b32_e32 v123, 16, v124
	v_and_b32_e32 v124, 0xffff0000, v124
	v_mul_f32_e32 v128, v5, v124
	v_lshlrev_b32_e32 v129, 16, v125
	v_and_b32_e32 v125, 0xffff0000, v125
	v_mul_f32_e32 v124, v8, v124
	v_fmac_f32_e32 v128, v3, v123
	v_fmac_f32_e32 v124, v7, v123
	v_mul_f32_e32 v123, v11, v125
	v_mul_f32_e32 v130, v6, v125
	v_fmac_f32_e32 v123, v9, v129
	v_and_b32_e32 v125, 0xffff0000, v126
	v_fmac_f32_e32 v130, v4, v129
	v_add_f32_e32 v123, v124, v123
	v_lshlrev_b32_e32 v124, 16, v126
	v_mul_f32_e32 v126, v13, v125
	v_lshlrev_b32_e32 v129, 16, v127
	v_and_b32_e32 v127, 0xffff0000, v127
	v_mul_f32_e32 v125, v18, v125
	v_add_f32_e32 v128, v128, v130
	v_fmac_f32_e32 v126, v10, v124
	v_mul_f32_e32 v130, v14, v127
	v_fmac_f32_e32 v125, v16, v124
	v_mul_f32_e32 v124, v41, v127
	v_fmac_f32_e32 v130, v12, v129
	v_fmac_f32_e32 v124, v19, v129
	v_add_f32_e32 v128, 0, v128
	v_add_f32_e32 v123, 0, v123
	v_add_f32_e32 v126, v126, v130
	v_add_f32_e32 v124, v125, v124
	v_add_f32_e32 v128, v128, v126
	v_add_f32_e32 v123, v123, v124
	ds_read2st64_b64 v[124:127], v99 offset0:114 offset1:115
	s_waitcnt lgkmcnt(0)
	v_lshlrev_b32_e32 v129, 16, v124
	v_and_b32_e32 v124, 0xffff0000, v124
	v_lshlrev_b32_e32 v131, 16, v125
	v_and_b32_e32 v125, 0xffff0000, v125
	v_mul_f32_e32 v130, v20, v124
	v_mul_f32_e32 v132, v42, v125
	v_mul_f32_e32 v124, v45, v124
	v_mul_f32_e32 v125, v46, v125
	v_fmac_f32_e32 v124, v21, v129
	v_fmac_f32_e32 v125, v43, v131
	v_fmac_f32_e32 v130, v15, v129
	v_fmac_f32_e32 v132, v17, v131
	v_add_f32_e32 v124, v124, v125
	v_and_b32_e32 v125, 0xffff0000, v126
	v_add_f32_e32 v130, v130, v132
	v_add_f32_e32 v123, v123, v124
	v_lshlrev_b32_e32 v124, 16, v126
	v_mul_f32_e32 v126, v47, v125
	v_lshlrev_b32_e32 v129, 16, v127
	v_and_b32_e32 v127, 0xffff0000, v127
	v_mul_f32_e32 v125, v51, v125
	v_add_f32_e32 v128, v128, v130
	v_fmac_f32_e32 v126, v40, v124
	v_mul_f32_e32 v130, v49, v127
	v_fmac_f32_e32 v125, v48, v124
	v_mul_f32_e32 v124, v52, v127
	v_fmac_f32_e32 v130, v44, v129
	v_fmac_f32_e32 v124, v50, v129
	v_add_f32_e32 v126, v126, v130
	v_add_f32_e32 v124, v125, v124
	v_add_f32_e32 v128, v128, v126
	v_add_f32_e32 v123, v123, v124
	ds_read2st64_b64 v[124:127], v99 offset0:116 offset1:117
	s_waitcnt lgkmcnt(0)
	v_lshlrev_b32_e32 v129, 16, v124
	v_and_b32_e32 v124, 0xffff0000, v124
	v_lshlrev_b32_e32 v131, 16, v125
	v_and_b32_e32 v125, 0xffff0000, v125
	v_mul_f32_e32 v130, v58, v124
	v_mul_f32_e32 v132, v59, v125
	v_mul_f32_e32 v124, v61, v124
	v_mul_f32_e32 v125, v64, v125
	v_fmac_f32_e32 v124, v60, v129
	v_fmac_f32_e32 v125, v62, v131
	v_fmac_f32_e32 v130, v56, v129
	v_fmac_f32_e32 v132, v57, v131
	v_add_f32_e32 v124, v124, v125
	v_and_b32_e32 v125, 0xffff0000, v126
	v_add_f32_e32 v130, v130, v132
	v_add_f32_e32 v123, v123, v124
	v_lshlrev_b32_e32 v124, 16, v126
	v_mul_f32_e32 v126, v66, v125
	v_lshlrev_b32_e32 v129, 16, v127
	v_and_b32_e32 v127, 0xffff0000, v127
	v_mul_f32_e32 v125, v76, v125
	v_add_f32_e32 v128, v128, v130
	v_fmac_f32_e32 v126, v63, v124
	v_mul_f32_e32 v130, v69, v127
	v_fmac_f32_e32 v125, v70, v124
	v_mul_f32_e32 v124, v81, v127
	v_fmac_f32_e32 v130, v65, v129
	v_fmac_f32_e32 v124, v77, v129
	v_add_f32_e32 v126, v126, v130
	v_add_f32_e32 v124, v125, v124
	v_add_f32_e32 v128, v128, v126
	v_add_f32_e32 v123, v123, v124
	ds_read2st64_b64 v[124:127], v99 offset0:118 offset1:119
	s_waitcnt lgkmcnt(0)
	v_lshlrev_b32_e32 v129, 16, v124
	v_and_b32_e32 v124, 0xffff0000, v124
	v_lshlrev_b32_e32 v131, 16, v125
	v_and_b32_e32 v125, 0xffff0000, v125
	v_mul_f32_e32 v130, v71, v124
	v_mul_f32_e32 v132, v78, v125
	v_mul_f32_e32 v124, v82, v124
	v_mul_f32_e32 v125, v83, v125
	v_fmac_f32_e32 v130, v67, v129
	v_fmac_f32_e32 v132, v68, v131
	v_fmac_f32_e32 v124, v74, v129
	v_fmac_f32_e32 v125, v79, v131
	v_add_f32_e32 v130, v130, v132
	v_add_f32_e32 v124, v124, v125
	v_lshlrev_b32_e32 v125, 16, v126
	v_and_b32_e32 v126, 0xffff0000, v126
	v_lshlrev_b32_e32 v129, 16, v127
	v_and_b32_e32 v127, 0xffff0000, v127
	v_add_f32_e32 v128, v128, v130
	v_add_f32_e32 v123, v123, v124
	v_mul_f32_e32 v124, v84, v126
	v_mul_f32_e32 v130, v87, v127
	v_mul_f32_e32 v126, v89, v126
	v_fmac_f32_e32 v124, v75, v125
	v_fmac_f32_e32 v130, v80, v129
	v_fmac_f32_e32 v126, v85, v125
	v_mul_f32_e32 v125, v90, v127
	v_add_f32_e32 v124, v124, v130
	v_fmac_f32_e32 v125, v88, v129
	v_add_f32_e32 v124, v128, v124
	v_add_f32_e32 v125, v126, v125
	ds_read2st64_b64 v[126:129], v99 offset0:120 offset1:121
	v_add_f32_e32 v123, v123, v125
	s_waitcnt lgkmcnt(0)
	v_lshlrev_b32_e32 v125, 16, v126
	v_and_b32_e32 v126, 0xffff0000, v126
	v_mul_f32_e32 v130, v5, v126
	v_lshlrev_b32_e32 v131, 16, v127
	v_and_b32_e32 v127, 0xffff0000, v127
	v_mul_f32_e32 v126, v8, v126
	v_fmac_f32_e32 v130, v3, v125
	v_fmac_f32_e32 v126, v7, v125
	v_mul_f32_e32 v125, v11, v127
	v_mul_f32_e32 v132, v6, v127
	v_fmac_f32_e32 v125, v9, v131
	v_and_b32_e32 v127, 0xffff0000, v128
	v_fmac_f32_e32 v132, v4, v131
	v_add_f32_e32 v125, v126, v125
	v_lshlrev_b32_e32 v126, 16, v128
	v_mul_f32_e32 v128, v13, v127
	v_lshlrev_b32_e32 v131, 16, v129
	v_and_b32_e32 v129, 0xffff0000, v129
	v_mul_f32_e32 v127, v18, v127
	v_add_f32_e32 v130, v130, v132
	v_fmac_f32_e32 v128, v10, v126
	v_mul_f32_e32 v132, v14, v129
	v_fmac_f32_e32 v127, v16, v126
	v_mul_f32_e32 v126, v41, v129
	v_fmac_f32_e32 v132, v12, v131
	v_fmac_f32_e32 v126, v19, v131
	v_add_f32_e32 v130, 0, v130
	v_add_f32_e32 v125, 0, v125
	v_add_f32_e32 v128, v128, v132
	v_add_f32_e32 v126, v127, v126
	v_add_f32_e32 v130, v130, v128
	v_add_f32_e32 v125, v125, v126
	ds_read2st64_b64 v[126:129], v99 offset0:122 offset1:123
	s_waitcnt lgkmcnt(0)
	v_lshlrev_b32_e32 v131, 16, v126
	v_and_b32_e32 v126, 0xffff0000, v126
	v_lshlrev_b32_e32 v133, 16, v127
	v_and_b32_e32 v127, 0xffff0000, v127
	v_mul_f32_e32 v132, v20, v126
	v_mul_f32_e32 v134, v42, v127
	v_mul_f32_e32 v126, v45, v126
	v_mul_f32_e32 v127, v46, v127
	v_fmac_f32_e32 v126, v21, v131
	v_fmac_f32_e32 v127, v43, v133
	v_fmac_f32_e32 v132, v15, v131
	v_fmac_f32_e32 v134, v17, v133
	v_add_f32_e32 v126, v126, v127
	v_and_b32_e32 v127, 0xffff0000, v128
	v_add_f32_e32 v132, v132, v134
	v_add_f32_e32 v125, v125, v126
	v_lshlrev_b32_e32 v126, 16, v128
	v_mul_f32_e32 v128, v47, v127
	v_lshlrev_b32_e32 v131, 16, v129
	v_and_b32_e32 v129, 0xffff0000, v129
	v_mul_f32_e32 v127, v51, v127
	v_add_f32_e32 v130, v130, v132
	v_fmac_f32_e32 v128, v40, v126
	v_mul_f32_e32 v132, v49, v129
	v_fmac_f32_e32 v127, v48, v126
	v_mul_f32_e32 v126, v52, v129
	v_fmac_f32_e32 v132, v44, v131
	v_fmac_f32_e32 v126, v50, v131
	v_add_f32_e32 v128, v128, v132
	v_add_f32_e32 v126, v127, v126
	v_add_f32_e32 v130, v130, v128
	v_add_f32_e32 v125, v125, v126
	ds_read2st64_b64 v[126:129], v99 offset0:124 offset1:125
	s_waitcnt lgkmcnt(0)
	v_lshlrev_b32_e32 v131, 16, v126
	v_and_b32_e32 v126, 0xffff0000, v126
	v_lshlrev_b32_e32 v133, 16, v127
	v_and_b32_e32 v127, 0xffff0000, v127
	v_mul_f32_e32 v132, v58, v126
	v_mul_f32_e32 v134, v59, v127
	v_mul_f32_e32 v126, v61, v126
	v_mul_f32_e32 v127, v64, v127
	v_fmac_f32_e32 v126, v60, v131
	v_fmac_f32_e32 v127, v62, v133
	v_fmac_f32_e32 v132, v56, v131
	v_fmac_f32_e32 v134, v57, v133
	v_add_f32_e32 v126, v126, v127
	v_and_b32_e32 v127, 0xffff0000, v128
	v_add_f32_e32 v132, v132, v134
	v_add_f32_e32 v125, v125, v126
	v_lshlrev_b32_e32 v126, 16, v128
	v_mul_f32_e32 v128, v66, v127
	v_lshlrev_b32_e32 v131, 16, v129
	v_and_b32_e32 v129, 0xffff0000, v129
	v_mul_f32_e32 v127, v76, v127
	v_add_f32_e32 v130, v130, v132
	v_fmac_f32_e32 v128, v63, v126
	v_mul_f32_e32 v132, v69, v129
	v_fmac_f32_e32 v127, v70, v126
	v_mul_f32_e32 v126, v81, v129
	v_fmac_f32_e32 v132, v65, v131
	v_fmac_f32_e32 v126, v77, v131
	v_add_f32_e32 v128, v128, v132
	v_add_f32_e32 v126, v127, v126
	v_add_f32_e32 v130, v130, v128
	v_add_f32_e32 v125, v125, v126
	ds_read2st64_b64 v[126:129], v99 offset0:126 offset1:127
	s_waitcnt lgkmcnt(0)
	v_lshlrev_b32_e32 v131, 16, v126
	v_and_b32_e32 v126, 0xffff0000, v126
	v_lshlrev_b32_e32 v133, 16, v127
	v_and_b32_e32 v127, 0xffff0000, v127
	v_mul_f32_e32 v132, v71, v126
	v_mul_f32_e32 v134, v78, v127
	v_mul_f32_e32 v126, v82, v126
	v_mul_f32_e32 v127, v83, v127
	v_fmac_f32_e32 v132, v67, v131
	v_fmac_f32_e32 v134, v68, v133
	v_fmac_f32_e32 v126, v74, v131
	v_fmac_f32_e32 v127, v79, v133
	v_add_f32_e32 v132, v132, v134
	v_add_f32_e32 v126, v126, v127
	v_lshlrev_b32_e32 v127, 16, v128
	v_and_b32_e32 v128, 0xffff0000, v128
	v_lshlrev_b32_e32 v131, 16, v129
	v_and_b32_e32 v129, 0xffff0000, v129
	v_add_f32_e32 v130, v130, v132
	v_add_f32_e32 v125, v125, v126
	v_mul_f32_e32 v126, v84, v128
	v_mul_f32_e32 v132, v87, v129
	v_mul_f32_e32 v128, v89, v128
	v_fmac_f32_e32 v126, v75, v127
	v_fmac_f32_e32 v132, v80, v131
	v_fmac_f32_e32 v128, v85, v127
	v_mul_f32_e32 v127, v90, v129
	v_add_f32_e32 v126, v126, v132
	v_fmac_f32_e32 v127, v88, v131
	v_add_f32_e32 v126, v130, v126
	v_add_f32_e32 v127, v128, v127
	ds_read2st64_b64 v[128:131], v100 offset0:64 offset1:65
	v_add_f32_e32 v125, v125, v127
	s_waitcnt lgkmcnt(0)
	v_lshlrev_b32_e32 v127, 16, v128
	v_and_b32_e32 v128, 0xffff0000, v128
	v_mul_f32_e32 v132, v5, v128
	v_lshlrev_b32_e32 v133, 16, v129
	v_and_b32_e32 v129, 0xffff0000, v129
	v_mul_f32_e32 v128, v8, v128
	v_fmac_f32_e32 v132, v3, v127
	v_fmac_f32_e32 v128, v7, v127
	v_mul_f32_e32 v127, v11, v129
	v_mul_f32_e32 v134, v6, v129
	v_fmac_f32_e32 v127, v9, v133
	v_and_b32_e32 v129, 0xffff0000, v130
	v_fmac_f32_e32 v134, v4, v133
	v_add_f32_e32 v127, v128, v127
	v_lshlrev_b32_e32 v128, 16, v130
	v_mul_f32_e32 v130, v13, v129
	v_lshlrev_b32_e32 v133, 16, v131
	v_and_b32_e32 v131, 0xffff0000, v131
	v_mul_f32_e32 v129, v18, v129
	v_add_f32_e32 v132, v132, v134
	v_fmac_f32_e32 v130, v10, v128
	v_mul_f32_e32 v134, v14, v131
	v_fmac_f32_e32 v129, v16, v128
	v_mul_f32_e32 v128, v41, v131
	v_fmac_f32_e32 v134, v12, v133
	v_fmac_f32_e32 v128, v19, v133
	v_add_f32_e32 v132, 0, v132
	v_add_f32_e32 v127, 0, v127
	v_add_f32_e32 v130, v130, v134
	v_add_f32_e32 v128, v129, v128
	v_add_f32_e32 v132, v132, v130
	v_add_f32_e32 v127, v127, v128
	ds_read2st64_b64 v[128:131], v100 offset0:66 offset1:67
	s_waitcnt lgkmcnt(0)
	v_lshlrev_b32_e32 v133, 16, v128
	v_and_b32_e32 v128, 0xffff0000, v128
	v_lshlrev_b32_e32 v135, 16, v129
	v_and_b32_e32 v129, 0xffff0000, v129
	v_mul_f32_e32 v134, v20, v128
	v_mul_f32_e32 v136, v42, v129
	v_mul_f32_e32 v128, v45, v128
	v_mul_f32_e32 v129, v46, v129
	v_fmac_f32_e32 v128, v21, v133
	v_fmac_f32_e32 v129, v43, v135
	v_fmac_f32_e32 v134, v15, v133
	v_fmac_f32_e32 v136, v17, v135
	v_add_f32_e32 v128, v128, v129
	v_and_b32_e32 v129, 0xffff0000, v130
	v_add_f32_e32 v134, v134, v136
	v_add_f32_e32 v127, v127, v128
	v_lshlrev_b32_e32 v128, 16, v130
	v_mul_f32_e32 v130, v47, v129
	v_lshlrev_b32_e32 v133, 16, v131
	v_and_b32_e32 v131, 0xffff0000, v131
	v_mul_f32_e32 v129, v51, v129
	v_add_f32_e32 v132, v132, v134
	v_fmac_f32_e32 v130, v40, v128
	v_mul_f32_e32 v134, v49, v131
	v_fmac_f32_e32 v129, v48, v128
	v_mul_f32_e32 v128, v52, v131
	v_fmac_f32_e32 v134, v44, v133
	v_fmac_f32_e32 v128, v50, v133
	v_add_f32_e32 v130, v130, v134
	v_add_f32_e32 v128, v129, v128
	v_add_f32_e32 v132, v132, v130
	v_add_f32_e32 v127, v127, v128
	ds_read2st64_b64 v[128:131], v100 offset0:68 offset1:69
	s_waitcnt lgkmcnt(0)
	v_lshlrev_b32_e32 v133, 16, v128
	v_and_b32_e32 v128, 0xffff0000, v128
	v_lshlrev_b32_e32 v135, 16, v129
	v_and_b32_e32 v129, 0xffff0000, v129
	v_mul_f32_e32 v134, v58, v128
	v_mul_f32_e32 v136, v59, v129
	v_mul_f32_e32 v128, v61, v128
	v_mul_f32_e32 v129, v64, v129
	v_fmac_f32_e32 v128, v60, v133
	v_fmac_f32_e32 v129, v62, v135
	v_fmac_f32_e32 v134, v56, v133
	v_fmac_f32_e32 v136, v57, v135
	v_add_f32_e32 v128, v128, v129
	v_and_b32_e32 v129, 0xffff0000, v130
	v_add_f32_e32 v134, v134, v136
	v_add_f32_e32 v127, v127, v128
	v_lshlrev_b32_e32 v128, 16, v130
	v_mul_f32_e32 v130, v66, v129
	v_lshlrev_b32_e32 v133, 16, v131
	v_and_b32_e32 v131, 0xffff0000, v131
	v_mul_f32_e32 v129, v76, v129
	v_add_f32_e32 v132, v132, v134
	v_fmac_f32_e32 v130, v63, v128
	v_mul_f32_e32 v134, v69, v131
	v_fmac_f32_e32 v129, v70, v128
	v_mul_f32_e32 v128, v81, v131
	v_fmac_f32_e32 v134, v65, v133
	v_fmac_f32_e32 v128, v77, v133
	v_add_f32_e32 v130, v130, v134
	v_add_f32_e32 v128, v129, v128
	v_add_f32_e32 v132, v132, v130
	v_add_f32_e32 v127, v127, v128
	ds_read2st64_b64 v[128:131], v100 offset0:70 offset1:71
	s_waitcnt lgkmcnt(0)
	v_lshlrev_b32_e32 v133, 16, v128
	v_and_b32_e32 v128, 0xffff0000, v128
	v_lshlrev_b32_e32 v135, 16, v129
	v_and_b32_e32 v129, 0xffff0000, v129
	v_mul_f32_e32 v134, v71, v128
	v_mul_f32_e32 v136, v78, v129
	v_mul_f32_e32 v128, v82, v128
	v_mul_f32_e32 v129, v83, v129
	v_fmac_f32_e32 v134, v67, v133
	v_fmac_f32_e32 v136, v68, v135
	v_fmac_f32_e32 v128, v74, v133
	v_fmac_f32_e32 v129, v79, v135
	v_add_f32_e32 v134, v134, v136
	v_add_f32_e32 v128, v128, v129
	v_lshlrev_b32_e32 v129, 16, v130
	v_and_b32_e32 v130, 0xffff0000, v130
	v_lshlrev_b32_e32 v133, 16, v131
	v_and_b32_e32 v131, 0xffff0000, v131
	v_add_f32_e32 v132, v132, v134
	v_add_f32_e32 v127, v127, v128
	v_mul_f32_e32 v128, v84, v130
	v_mul_f32_e32 v134, v87, v131
	v_mul_f32_e32 v130, v89, v130
	v_fmac_f32_e32 v128, v75, v129
	v_fmac_f32_e32 v134, v80, v133
	v_fmac_f32_e32 v130, v85, v129
	v_mul_f32_e32 v129, v90, v131
	v_add_f32_e32 v128, v128, v134
	v_fmac_f32_e32 v129, v88, v133
	v_add_f32_e32 v128, v132, v128
	v_add_f32_e32 v129, v130, v129
	ds_read2st64_b64 v[130:133], v100 offset0:72 offset1:73
	v_add_f32_e32 v127, v127, v129
	s_waitcnt lgkmcnt(0)
	v_lshlrev_b32_e32 v129, 16, v130
	v_and_b32_e32 v130, 0xffff0000, v130
	v_mul_f32_e32 v134, v5, v130
	v_lshlrev_b32_e32 v135, 16, v131
	v_and_b32_e32 v131, 0xffff0000, v131
	v_mul_f32_e32 v130, v8, v130
	v_fmac_f32_e32 v134, v3, v129
	v_fmac_f32_e32 v130, v7, v129
	v_mul_f32_e32 v129, v11, v131
	v_mul_f32_e32 v136, v6, v131
	v_fmac_f32_e32 v129, v9, v135
	v_and_b32_e32 v131, 0xffff0000, v132
	v_fmac_f32_e32 v136, v4, v135
	v_add_f32_e32 v129, v130, v129
	v_lshlrev_b32_e32 v130, 16, v132
	v_mul_f32_e32 v132, v13, v131
	v_lshlrev_b32_e32 v135, 16, v133
	v_and_b32_e32 v133, 0xffff0000, v133
	v_mul_f32_e32 v131, v18, v131
	v_add_f32_e32 v134, v134, v136
	v_fmac_f32_e32 v132, v10, v130
	v_mul_f32_e32 v136, v14, v133
	v_fmac_f32_e32 v131, v16, v130
	v_mul_f32_e32 v130, v41, v133
	v_fmac_f32_e32 v136, v12, v135
	v_fmac_f32_e32 v130, v19, v135
	v_add_f32_e32 v134, 0, v134
	v_add_f32_e32 v129, 0, v129
	v_add_f32_e32 v132, v132, v136
	v_add_f32_e32 v130, v131, v130
	v_add_f32_e32 v134, v134, v132
	v_add_f32_e32 v129, v129, v130
	ds_read2st64_b64 v[130:133], v100 offset0:74 offset1:75
	s_waitcnt lgkmcnt(0)
	v_lshlrev_b32_e32 v135, 16, v130
	v_and_b32_e32 v130, 0xffff0000, v130
	v_lshlrev_b32_e32 v137, 16, v131
	v_and_b32_e32 v131, 0xffff0000, v131
	v_mul_f32_e32 v136, v20, v130
	v_mul_f32_e32 v138, v42, v131
	v_mul_f32_e32 v130, v45, v130
	v_mul_f32_e32 v131, v46, v131
	v_fmac_f32_e32 v130, v21, v135
	v_fmac_f32_e32 v131, v43, v137
	v_fmac_f32_e32 v136, v15, v135
	v_fmac_f32_e32 v138, v17, v137
	v_add_f32_e32 v130, v130, v131
	v_and_b32_e32 v131, 0xffff0000, v132
	v_add_f32_e32 v136, v136, v138
	v_add_f32_e32 v129, v129, v130
	v_lshlrev_b32_e32 v130, 16, v132
	v_mul_f32_e32 v132, v47, v131
	v_lshlrev_b32_e32 v135, 16, v133
	v_and_b32_e32 v133, 0xffff0000, v133
	v_mul_f32_e32 v131, v51, v131
	v_add_f32_e32 v134, v134, v136
	v_fmac_f32_e32 v132, v40, v130
	v_mul_f32_e32 v136, v49, v133
	v_fmac_f32_e32 v131, v48, v130
	v_mul_f32_e32 v130, v52, v133
	v_fmac_f32_e32 v136, v44, v135
	v_fmac_f32_e32 v130, v50, v135
	v_add_f32_e32 v132, v132, v136
	v_add_f32_e32 v130, v131, v130
	v_add_f32_e32 v134, v134, v132
	v_add_f32_e32 v129, v129, v130
	ds_read2st64_b64 v[130:133], v100 offset0:76 offset1:77
	s_waitcnt lgkmcnt(0)
	v_lshlrev_b32_e32 v135, 16, v130
	v_and_b32_e32 v130, 0xffff0000, v130
	v_lshlrev_b32_e32 v137, 16, v131
	v_and_b32_e32 v131, 0xffff0000, v131
	v_mul_f32_e32 v136, v58, v130
	v_mul_f32_e32 v138, v59, v131
	v_mul_f32_e32 v130, v61, v130
	v_mul_f32_e32 v131, v64, v131
	v_fmac_f32_e32 v130, v60, v135
	v_fmac_f32_e32 v131, v62, v137
	v_fmac_f32_e32 v136, v56, v135
	v_fmac_f32_e32 v138, v57, v137
	v_add_f32_e32 v130, v130, v131
	v_and_b32_e32 v131, 0xffff0000, v132
	v_add_f32_e32 v136, v136, v138
	v_add_f32_e32 v129, v129, v130
	v_lshlrev_b32_e32 v130, 16, v132
	v_mul_f32_e32 v132, v66, v131
	v_lshlrev_b32_e32 v135, 16, v133
	v_and_b32_e32 v133, 0xffff0000, v133
	v_mul_f32_e32 v131, v76, v131
	v_add_f32_e32 v134, v134, v136
	v_fmac_f32_e32 v132, v63, v130
	v_mul_f32_e32 v136, v69, v133
	v_fmac_f32_e32 v131, v70, v130
	v_mul_f32_e32 v130, v81, v133
	v_fmac_f32_e32 v136, v65, v135
	v_fmac_f32_e32 v130, v77, v135
	v_add_f32_e32 v132, v132, v136
	v_add_f32_e32 v130, v131, v130
	v_add_f32_e32 v134, v134, v132
	v_add_f32_e32 v129, v129, v130
	ds_read2st64_b64 v[130:133], v100 offset0:78 offset1:79
	s_waitcnt lgkmcnt(0)
	v_lshlrev_b32_e32 v135, 16, v130
	v_and_b32_e32 v130, 0xffff0000, v130
	v_lshlrev_b32_e32 v137, 16, v131
	v_and_b32_e32 v131, 0xffff0000, v131
	v_mul_f32_e32 v136, v71, v130
	v_mul_f32_e32 v138, v78, v131
	v_mul_f32_e32 v130, v82, v130
	v_mul_f32_e32 v131, v83, v131
	v_fmac_f32_e32 v136, v67, v135
	v_fmac_f32_e32 v138, v68, v137
	v_fmac_f32_e32 v130, v74, v135
	v_fmac_f32_e32 v131, v79, v137
	v_add_f32_e32 v136, v136, v138
	v_add_f32_e32 v130, v130, v131
	v_lshlrev_b32_e32 v131, 16, v132
	v_and_b32_e32 v132, 0xffff0000, v132
	v_lshlrev_b32_e32 v135, 16, v133
	v_and_b32_e32 v133, 0xffff0000, v133
	v_add_f32_e32 v134, v134, v136
	v_add_f32_e32 v129, v129, v130
	v_mul_f32_e32 v130, v84, v132
	v_mul_f32_e32 v136, v87, v133
	v_mul_f32_e32 v132, v89, v132
	v_fmac_f32_e32 v130, v75, v131
	v_fmac_f32_e32 v136, v80, v135
	v_fmac_f32_e32 v132, v85, v131
	v_mul_f32_e32 v131, v90, v133
	v_add_f32_e32 v130, v130, v136
	v_fmac_f32_e32 v131, v88, v135
	v_add_f32_e32 v130, v134, v130
	v_add_f32_e32 v131, v132, v131
	ds_read2st64_b64 v[132:135], v100 offset0:80 offset1:81
	v_add_f32_e32 v129, v129, v131
	s_waitcnt lgkmcnt(0)
	v_lshlrev_b32_e32 v131, 16, v132
	v_and_b32_e32 v132, 0xffff0000, v132
	v_mul_f32_e32 v136, v5, v132
	v_lshlrev_b32_e32 v137, 16, v133
	v_and_b32_e32 v133, 0xffff0000, v133
	v_mul_f32_e32 v132, v8, v132
	v_fmac_f32_e32 v136, v3, v131
	v_fmac_f32_e32 v132, v7, v131
	v_mul_f32_e32 v131, v11, v133
	v_mul_f32_e32 v138, v6, v133
	v_fmac_f32_e32 v131, v9, v137
	v_and_b32_e32 v133, 0xffff0000, v134
	v_fmac_f32_e32 v138, v4, v137
	v_add_f32_e32 v131, v132, v131
	v_lshlrev_b32_e32 v132, 16, v134
	v_mul_f32_e32 v134, v13, v133
	v_lshlrev_b32_e32 v137, 16, v135
	v_and_b32_e32 v135, 0xffff0000, v135
	v_mul_f32_e32 v133, v18, v133
	v_add_f32_e32 v136, v136, v138
	v_fmac_f32_e32 v134, v10, v132
	v_mul_f32_e32 v138, v14, v135
	v_fmac_f32_e32 v133, v16, v132
	v_mul_f32_e32 v132, v41, v135
	v_fmac_f32_e32 v138, v12, v137
	v_fmac_f32_e32 v132, v19, v137
	v_add_f32_e32 v136, 0, v136
	v_add_f32_e32 v131, 0, v131
	v_add_f32_e32 v134, v134, v138
	v_add_f32_e32 v132, v133, v132
	v_add_f32_e32 v136, v136, v134
	v_add_f32_e32 v131, v131, v132
	ds_read2st64_b64 v[132:135], v100 offset0:82 offset1:83
	s_waitcnt lgkmcnt(0)
	v_lshlrev_b32_e32 v137, 16, v132
	v_and_b32_e32 v132, 0xffff0000, v132
	v_lshlrev_b32_e32 v139, 16, v133
	v_and_b32_e32 v133, 0xffff0000, v133
	v_mul_f32_e32 v138, v20, v132
	v_mul_f32_e32 v140, v42, v133
	v_mul_f32_e32 v132, v45, v132
	v_mul_f32_e32 v133, v46, v133
	v_fmac_f32_e32 v132, v21, v137
	v_fmac_f32_e32 v133, v43, v139
	v_fmac_f32_e32 v138, v15, v137
	v_fmac_f32_e32 v140, v17, v139
	v_add_f32_e32 v132, v132, v133
	v_and_b32_e32 v133, 0xffff0000, v134
	v_add_f32_e32 v138, v138, v140
	v_add_f32_e32 v131, v131, v132
	v_lshlrev_b32_e32 v132, 16, v134
	v_mul_f32_e32 v134, v47, v133
	v_lshlrev_b32_e32 v137, 16, v135
	v_and_b32_e32 v135, 0xffff0000, v135
	v_mul_f32_e32 v133, v51, v133
	v_add_f32_e32 v136, v136, v138
	v_fmac_f32_e32 v134, v40, v132
	v_mul_f32_e32 v138, v49, v135
	v_fmac_f32_e32 v133, v48, v132
	v_mul_f32_e32 v132, v52, v135
	v_fmac_f32_e32 v138, v44, v137
	v_fmac_f32_e32 v132, v50, v137
	v_add_f32_e32 v134, v134, v138
	v_add_f32_e32 v132, v133, v132
	v_add_f32_e32 v136, v136, v134
	v_add_f32_e32 v131, v131, v132
	ds_read2st64_b64 v[132:135], v100 offset0:84 offset1:85
	s_waitcnt lgkmcnt(0)
	v_lshlrev_b32_e32 v137, 16, v132
	v_and_b32_e32 v132, 0xffff0000, v132
	v_lshlrev_b32_e32 v139, 16, v133
	v_and_b32_e32 v133, 0xffff0000, v133
	v_mul_f32_e32 v138, v58, v132
	v_mul_f32_e32 v140, v59, v133
	v_mul_f32_e32 v132, v61, v132
	v_mul_f32_e32 v133, v64, v133
	v_fmac_f32_e32 v132, v60, v137
	v_fmac_f32_e32 v133, v62, v139
	v_fmac_f32_e32 v138, v56, v137
	v_fmac_f32_e32 v140, v57, v139
	v_add_f32_e32 v132, v132, v133
	v_and_b32_e32 v133, 0xffff0000, v134
	v_add_f32_e32 v138, v138, v140
	v_add_f32_e32 v131, v131, v132
	v_lshlrev_b32_e32 v132, 16, v134
	v_mul_f32_e32 v134, v66, v133
	v_lshlrev_b32_e32 v137, 16, v135
	v_and_b32_e32 v135, 0xffff0000, v135
	v_mul_f32_e32 v133, v76, v133
	v_add_f32_e32 v136, v136, v138
	v_fmac_f32_e32 v134, v63, v132
	v_mul_f32_e32 v138, v69, v135
	v_fmac_f32_e32 v133, v70, v132
	v_mul_f32_e32 v132, v81, v135
	v_fmac_f32_e32 v138, v65, v137
	v_fmac_f32_e32 v132, v77, v137
	v_add_f32_e32 v134, v134, v138
	v_add_f32_e32 v132, v133, v132
	v_add_f32_e32 v136, v136, v134
	v_add_f32_e32 v131, v131, v132
	ds_read2st64_b64 v[132:135], v100 offset0:86 offset1:87
	s_waitcnt lgkmcnt(0)
	v_lshlrev_b32_e32 v137, 16, v132
	v_and_b32_e32 v132, 0xffff0000, v132
	v_lshlrev_b32_e32 v139, 16, v133
	v_and_b32_e32 v133, 0xffff0000, v133
	v_mul_f32_e32 v138, v71, v132
	v_mul_f32_e32 v140, v78, v133
	v_mul_f32_e32 v132, v82, v132
	v_mul_f32_e32 v133, v83, v133
	v_fmac_f32_e32 v138, v67, v137
	v_fmac_f32_e32 v140, v68, v139
	v_fmac_f32_e32 v132, v74, v137
	v_fmac_f32_e32 v133, v79, v139
	v_add_f32_e32 v138, v138, v140
	v_add_f32_e32 v132, v132, v133
	v_lshlrev_b32_e32 v133, 16, v134
	v_and_b32_e32 v134, 0xffff0000, v134
	v_lshlrev_b32_e32 v137, 16, v135
	v_and_b32_e32 v135, 0xffff0000, v135
	v_add_f32_e32 v136, v136, v138
	v_add_f32_e32 v131, v131, v132
	v_mul_f32_e32 v132, v84, v134
	v_mul_f32_e32 v138, v87, v135
	v_mul_f32_e32 v134, v89, v134
	v_fmac_f32_e32 v132, v75, v133
	v_fmac_f32_e32 v138, v80, v137
	v_fmac_f32_e32 v134, v85, v133
	v_mul_f32_e32 v133, v90, v135
	v_add_f32_e32 v132, v132, v138
	v_fmac_f32_e32 v133, v88, v137
	v_add_f32_e32 v132, v136, v132
	v_add_f32_e32 v133, v134, v133
	ds_read2st64_b64 v[134:137], v100 offset0:88 offset1:89
	v_add_f32_e32 v131, v131, v133
	s_waitcnt lgkmcnt(0)
	v_lshlrev_b32_e32 v133, 16, v134
	v_and_b32_e32 v134, 0xffff0000, v134
	v_mul_f32_e32 v138, v5, v134
	v_lshlrev_b32_e32 v139, 16, v135
	v_and_b32_e32 v135, 0xffff0000, v135
	v_mul_f32_e32 v134, v8, v134
	v_fmac_f32_e32 v138, v3, v133
	v_fmac_f32_e32 v134, v7, v133
	v_mul_f32_e32 v133, v11, v135
	v_mul_f32_e32 v140, v6, v135
	v_fmac_f32_e32 v133, v9, v139
	v_and_b32_e32 v135, 0xffff0000, v136
	v_fmac_f32_e32 v140, v4, v139
	v_add_f32_e32 v133, v134, v133
	v_lshlrev_b32_e32 v134, 16, v136
	v_mul_f32_e32 v136, v13, v135
	v_lshlrev_b32_e32 v139, 16, v137
	v_and_b32_e32 v137, 0xffff0000, v137
	v_mul_f32_e32 v135, v18, v135
	v_add_f32_e32 v138, v138, v140
	v_fmac_f32_e32 v136, v10, v134
	v_mul_f32_e32 v140, v14, v137
	v_fmac_f32_e32 v135, v16, v134
	v_mul_f32_e32 v134, v41, v137
	v_fmac_f32_e32 v140, v12, v139
	v_fmac_f32_e32 v134, v19, v139
	v_add_f32_e32 v138, 0, v138
	v_add_f32_e32 v133, 0, v133
	v_add_f32_e32 v136, v136, v140
	v_add_f32_e32 v134, v135, v134
	v_add_f32_e32 v138, v138, v136
	v_add_f32_e32 v133, v133, v134
	ds_read2st64_b64 v[134:137], v100 offset0:90 offset1:91
	s_waitcnt lgkmcnt(0)
	v_lshlrev_b32_e32 v139, 16, v134
	v_and_b32_e32 v134, 0xffff0000, v134
	v_lshlrev_b32_e32 v141, 16, v135
	v_and_b32_e32 v135, 0xffff0000, v135
	v_mul_f32_e32 v140, v20, v134
	v_mul_f32_e32 v142, v42, v135
	v_mul_f32_e32 v134, v45, v134
	v_mul_f32_e32 v135, v46, v135
	v_fmac_f32_e32 v134, v21, v139
	v_fmac_f32_e32 v135, v43, v141
	v_fmac_f32_e32 v140, v15, v139
	v_fmac_f32_e32 v142, v17, v141
	v_add_f32_e32 v134, v134, v135
	v_and_b32_e32 v135, 0xffff0000, v136
	v_add_f32_e32 v140, v140, v142
	v_add_f32_e32 v133, v133, v134
	v_lshlrev_b32_e32 v134, 16, v136
	v_mul_f32_e32 v136, v47, v135
	v_lshlrev_b32_e32 v139, 16, v137
	v_and_b32_e32 v137, 0xffff0000, v137
	v_mul_f32_e32 v135, v51, v135
	v_add_f32_e32 v138, v138, v140
	v_fmac_f32_e32 v136, v40, v134
	v_mul_f32_e32 v140, v49, v137
	v_fmac_f32_e32 v135, v48, v134
	v_mul_f32_e32 v134, v52, v137
	v_fmac_f32_e32 v140, v44, v139
	v_fmac_f32_e32 v134, v50, v139
	v_add_f32_e32 v136, v136, v140
	v_add_f32_e32 v134, v135, v134
	v_add_f32_e32 v138, v138, v136
	v_add_f32_e32 v133, v133, v134
	ds_read2st64_b64 v[134:137], v100 offset0:92 offset1:93
	s_waitcnt lgkmcnt(0)
	v_lshlrev_b32_e32 v139, 16, v134
	v_and_b32_e32 v134, 0xffff0000, v134
	v_lshlrev_b32_e32 v141, 16, v135
	v_and_b32_e32 v135, 0xffff0000, v135
	v_mul_f32_e32 v140, v58, v134
	v_mul_f32_e32 v142, v59, v135
	v_mul_f32_e32 v134, v61, v134
	v_mul_f32_e32 v135, v64, v135
	v_fmac_f32_e32 v134, v60, v139
	v_fmac_f32_e32 v135, v62, v141
	v_fmac_f32_e32 v140, v56, v139
	v_fmac_f32_e32 v142, v57, v141
	v_add_f32_e32 v134, v134, v135
	v_and_b32_e32 v135, 0xffff0000, v136
	v_add_f32_e32 v140, v140, v142
	v_add_f32_e32 v133, v133, v134
	v_lshlrev_b32_e32 v134, 16, v136
	v_mul_f32_e32 v136, v66, v135
	v_lshlrev_b32_e32 v139, 16, v137
	v_and_b32_e32 v137, 0xffff0000, v137
	v_mul_f32_e32 v135, v76, v135
	v_add_f32_e32 v138, v138, v140
	v_fmac_f32_e32 v136, v63, v134
	v_mul_f32_e32 v140, v69, v137
	v_fmac_f32_e32 v135, v70, v134
	v_mul_f32_e32 v134, v81, v137
	v_fmac_f32_e32 v140, v65, v139
	v_fmac_f32_e32 v134, v77, v139
	v_add_f32_e32 v136, v136, v140
	v_add_f32_e32 v134, v135, v134
	v_add_f32_e32 v138, v138, v136
	v_add_f32_e32 v133, v133, v134
	ds_read2st64_b64 v[134:137], v100 offset0:94 offset1:95
	s_waitcnt lgkmcnt(0)
	v_lshlrev_b32_e32 v139, 16, v134
	v_and_b32_e32 v134, 0xffff0000, v134
	v_lshlrev_b32_e32 v141, 16, v135
	v_and_b32_e32 v135, 0xffff0000, v135
	v_mul_f32_e32 v140, v71, v134
	v_mul_f32_e32 v142, v78, v135
	v_mul_f32_e32 v134, v82, v134
	v_mul_f32_e32 v135, v83, v135
	v_fmac_f32_e32 v140, v67, v139
	v_fmac_f32_e32 v142, v68, v141
	v_fmac_f32_e32 v134, v74, v139
	v_fmac_f32_e32 v135, v79, v141
	v_add_f32_e32 v140, v140, v142
	v_add_f32_e32 v134, v134, v135
	v_lshlrev_b32_e32 v135, 16, v136
	v_and_b32_e32 v136, 0xffff0000, v136
	v_lshlrev_b32_e32 v139, 16, v137
	v_and_b32_e32 v137, 0xffff0000, v137
	v_add_f32_e32 v138, v138, v140
	v_add_f32_e32 v133, v133, v134
	v_mul_f32_e32 v134, v84, v136
	v_mul_f32_e32 v140, v87, v137
	v_mul_f32_e32 v136, v89, v136
	v_fmac_f32_e32 v134, v75, v135
	v_fmac_f32_e32 v140, v80, v139
	v_fmac_f32_e32 v136, v85, v135
	v_mul_f32_e32 v135, v90, v137
	v_add_f32_e32 v134, v134, v140
	v_fmac_f32_e32 v135, v88, v139
	v_add_f32_e32 v134, v138, v134
	v_add_f32_e32 v135, v136, v135
	ds_read2st64_b64 v[136:139], v100 offset0:96 offset1:97
	v_add_f32_e32 v133, v133, v135
	s_waitcnt lgkmcnt(0)
	v_lshlrev_b32_e32 v135, 16, v136
	v_and_b32_e32 v136, 0xffff0000, v136
	v_mul_f32_e32 v140, v5, v136
	v_lshlrev_b32_e32 v141, 16, v137
	v_and_b32_e32 v137, 0xffff0000, v137
	v_mul_f32_e32 v136, v8, v136
	v_fmac_f32_e32 v140, v3, v135
	v_fmac_f32_e32 v136, v7, v135
	v_mul_f32_e32 v135, v11, v137
	v_mul_f32_e32 v142, v6, v137
	v_fmac_f32_e32 v135, v9, v141
	v_and_b32_e32 v137, 0xffff0000, v138
	v_fmac_f32_e32 v142, v4, v141
	v_add_f32_e32 v135, v136, v135
	v_lshlrev_b32_e32 v136, 16, v138
	v_mul_f32_e32 v138, v13, v137
	v_lshlrev_b32_e32 v141, 16, v139
	v_and_b32_e32 v139, 0xffff0000, v139
	v_mul_f32_e32 v137, v18, v137
	v_add_f32_e32 v140, v140, v142
	v_fmac_f32_e32 v138, v10, v136
	v_mul_f32_e32 v142, v14, v139
	v_fmac_f32_e32 v137, v16, v136
	v_mul_f32_e32 v136, v41, v139
	v_fmac_f32_e32 v142, v12, v141
	v_fmac_f32_e32 v136, v19, v141
	v_add_f32_e32 v140, 0, v140
	v_add_f32_e32 v135, 0, v135
	v_add_f32_e32 v138, v138, v142
	v_add_f32_e32 v136, v137, v136
	v_add_f32_e32 v140, v140, v138
	v_add_f32_e32 v135, v135, v136
	ds_read2st64_b64 v[136:139], v100 offset0:98 offset1:99
	s_waitcnt lgkmcnt(0)
	v_lshlrev_b32_e32 v141, 16, v136
	v_and_b32_e32 v136, 0xffff0000, v136
	v_lshlrev_b32_e32 v143, 16, v137
	v_and_b32_e32 v137, 0xffff0000, v137
	v_mul_f32_e32 v142, v20, v136
	v_mul_f32_e32 v144, v42, v137
	v_mul_f32_e32 v136, v45, v136
	v_mul_f32_e32 v137, v46, v137
	v_fmac_f32_e32 v136, v21, v141
	v_fmac_f32_e32 v137, v43, v143
	v_fmac_f32_e32 v142, v15, v141
	v_fmac_f32_e32 v144, v17, v143
	v_add_f32_e32 v136, v136, v137
	v_and_b32_e32 v137, 0xffff0000, v138
	v_add_f32_e32 v142, v142, v144
	v_add_f32_e32 v135, v135, v136
	v_lshlrev_b32_e32 v136, 16, v138
	v_mul_f32_e32 v138, v47, v137
	v_lshlrev_b32_e32 v141, 16, v139
	v_and_b32_e32 v139, 0xffff0000, v139
	v_mul_f32_e32 v137, v51, v137
	v_add_f32_e32 v140, v140, v142
	v_fmac_f32_e32 v138, v40, v136
	v_mul_f32_e32 v142, v49, v139
	v_fmac_f32_e32 v137, v48, v136
	v_mul_f32_e32 v136, v52, v139
	v_fmac_f32_e32 v142, v44, v141
	v_fmac_f32_e32 v136, v50, v141
	v_add_f32_e32 v138, v138, v142
	v_add_f32_e32 v136, v137, v136
	v_add_f32_e32 v140, v140, v138
	v_add_f32_e32 v135, v135, v136
	ds_read2st64_b64 v[136:139], v100 offset0:100 offset1:101
	s_waitcnt lgkmcnt(0)
	v_lshlrev_b32_e32 v141, 16, v136
	v_and_b32_e32 v136, 0xffff0000, v136
	v_lshlrev_b32_e32 v143, 16, v137
	v_and_b32_e32 v137, 0xffff0000, v137
	v_mul_f32_e32 v142, v58, v136
	v_mul_f32_e32 v144, v59, v137
	v_mul_f32_e32 v136, v61, v136
	v_mul_f32_e32 v137, v64, v137
	v_fmac_f32_e32 v136, v60, v141
	v_fmac_f32_e32 v137, v62, v143
	v_fmac_f32_e32 v142, v56, v141
	v_fmac_f32_e32 v144, v57, v143
	v_add_f32_e32 v136, v136, v137
	v_and_b32_e32 v137, 0xffff0000, v138
	v_add_f32_e32 v142, v142, v144
	v_add_f32_e32 v135, v135, v136
	v_lshlrev_b32_e32 v136, 16, v138
	v_mul_f32_e32 v138, v66, v137
	v_lshlrev_b32_e32 v141, 16, v139
	v_and_b32_e32 v139, 0xffff0000, v139
	v_mul_f32_e32 v137, v76, v137
	v_add_f32_e32 v140, v140, v142
	v_fmac_f32_e32 v138, v63, v136
	v_mul_f32_e32 v142, v69, v139
	v_fmac_f32_e32 v137, v70, v136
	v_mul_f32_e32 v136, v81, v139
	v_fmac_f32_e32 v142, v65, v141
	v_fmac_f32_e32 v136, v77, v141
	v_add_f32_e32 v138, v138, v142
	v_add_f32_e32 v136, v137, v136
	v_add_f32_e32 v140, v140, v138
	v_add_f32_e32 v135, v135, v136
	ds_read2st64_b64 v[136:139], v100 offset0:102 offset1:103
	s_waitcnt lgkmcnt(0)
	v_lshlrev_b32_e32 v141, 16, v136
	v_and_b32_e32 v136, 0xffff0000, v136
	v_lshlrev_b32_e32 v143, 16, v137
	v_and_b32_e32 v137, 0xffff0000, v137
	v_mul_f32_e32 v142, v71, v136
	v_mul_f32_e32 v144, v78, v137
	v_mul_f32_e32 v136, v82, v136
	v_mul_f32_e32 v137, v83, v137
	v_fmac_f32_e32 v142, v67, v141
	v_fmac_f32_e32 v144, v68, v143
	v_fmac_f32_e32 v136, v74, v141
	v_fmac_f32_e32 v137, v79, v143
	v_add_f32_e32 v142, v142, v144
	v_add_f32_e32 v136, v136, v137
	v_lshlrev_b32_e32 v137, 16, v138
	v_and_b32_e32 v138, 0xffff0000, v138
	v_lshlrev_b32_e32 v141, 16, v139
	v_and_b32_e32 v139, 0xffff0000, v139
	v_add_f32_e32 v140, v140, v142
	v_add_f32_e32 v135, v135, v136
	v_mul_f32_e32 v136, v84, v138
	v_mul_f32_e32 v142, v87, v139
	v_mul_f32_e32 v138, v89, v138
	v_fmac_f32_e32 v136, v75, v137
	v_fmac_f32_e32 v142, v80, v141
	v_fmac_f32_e32 v138, v85, v137
	v_mul_f32_e32 v137, v90, v139
	v_add_f32_e32 v136, v136, v142
	v_fmac_f32_e32 v137, v88, v141
	v_add_f32_e32 v136, v140, v136
	v_add_f32_e32 v137, v138, v137
	ds_read2st64_b64 v[138:141], v100 offset0:104 offset1:105
	v_add_f32_e32 v135, v135, v137
	s_waitcnt lgkmcnt(0)
	v_lshlrev_b32_e32 v137, 16, v138
	v_and_b32_e32 v138, 0xffff0000, v138
	v_mul_f32_e32 v142, v5, v138
	v_lshlrev_b32_e32 v143, 16, v139
	v_and_b32_e32 v139, 0xffff0000, v139
	v_mul_f32_e32 v138, v8, v138
	v_fmac_f32_e32 v142, v3, v137
	v_fmac_f32_e32 v138, v7, v137
	v_mul_f32_e32 v137, v11, v139
	v_mul_f32_e32 v144, v6, v139
	v_fmac_f32_e32 v137, v9, v143
	v_and_b32_e32 v139, 0xffff0000, v140
	v_fmac_f32_e32 v144, v4, v143
	v_add_f32_e32 v137, v138, v137
	v_lshlrev_b32_e32 v138, 16, v140
	v_mul_f32_e32 v140, v13, v139
	v_lshlrev_b32_e32 v143, 16, v141
	v_and_b32_e32 v141, 0xffff0000, v141
	v_mul_f32_e32 v139, v18, v139
	v_add_f32_e32 v142, v142, v144
	v_fmac_f32_e32 v140, v10, v138
	v_mul_f32_e32 v144, v14, v141
	v_fmac_f32_e32 v139, v16, v138
	v_mul_f32_e32 v138, v41, v141
	v_fmac_f32_e32 v144, v12, v143
	v_fmac_f32_e32 v138, v19, v143
	v_add_f32_e32 v142, 0, v142
	v_add_f32_e32 v137, 0, v137
	v_add_f32_e32 v140, v140, v144
	v_add_f32_e32 v138, v139, v138
	v_add_f32_e32 v142, v142, v140
	v_add_f32_e32 v137, v137, v138
	ds_read2st64_b64 v[138:141], v100 offset0:106 offset1:107
	s_waitcnt lgkmcnt(0)
	v_lshlrev_b32_e32 v143, 16, v138
	v_and_b32_e32 v138, 0xffff0000, v138
	v_lshlrev_b32_e32 v145, 16, v139
	v_and_b32_e32 v139, 0xffff0000, v139
	v_mul_f32_e32 v144, v20, v138
	v_mul_f32_e32 v146, v42, v139
	v_mul_f32_e32 v138, v45, v138
	v_mul_f32_e32 v139, v46, v139
	v_fmac_f32_e32 v138, v21, v143
	v_fmac_f32_e32 v139, v43, v145
	v_fmac_f32_e32 v144, v15, v143
	v_fmac_f32_e32 v146, v17, v145
	v_add_f32_e32 v138, v138, v139
	v_and_b32_e32 v139, 0xffff0000, v140
	v_add_f32_e32 v144, v144, v146
	v_add_f32_e32 v137, v137, v138
	v_lshlrev_b32_e32 v138, 16, v140
	v_mul_f32_e32 v140, v47, v139
	v_lshlrev_b32_e32 v143, 16, v141
	v_and_b32_e32 v141, 0xffff0000, v141
	v_mul_f32_e32 v139, v51, v139
	v_add_f32_e32 v142, v142, v144
	v_fmac_f32_e32 v140, v40, v138
	v_mul_f32_e32 v144, v49, v141
	v_fmac_f32_e32 v139, v48, v138
	v_mul_f32_e32 v138, v52, v141
	v_fmac_f32_e32 v144, v44, v143
	v_fmac_f32_e32 v138, v50, v143
	v_add_f32_e32 v140, v140, v144
	v_add_f32_e32 v138, v139, v138
	v_add_f32_e32 v142, v142, v140
	v_add_f32_e32 v137, v137, v138
	ds_read2st64_b64 v[138:141], v100 offset0:108 offset1:109
	s_waitcnt lgkmcnt(0)
	v_lshlrev_b32_e32 v143, 16, v138
	v_and_b32_e32 v138, 0xffff0000, v138
	v_lshlrev_b32_e32 v145, 16, v139
	v_and_b32_e32 v139, 0xffff0000, v139
	v_mul_f32_e32 v144, v58, v138
	v_mul_f32_e32 v146, v59, v139
	v_mul_f32_e32 v138, v61, v138
	v_mul_f32_e32 v139, v64, v139
	v_fmac_f32_e32 v138, v60, v143
	v_fmac_f32_e32 v139, v62, v145
	v_fmac_f32_e32 v144, v56, v143
	v_fmac_f32_e32 v146, v57, v145
	v_add_f32_e32 v138, v138, v139
	v_and_b32_e32 v139, 0xffff0000, v140
	v_add_f32_e32 v144, v144, v146
	v_add_f32_e32 v137, v137, v138
	v_lshlrev_b32_e32 v138, 16, v140
	v_mul_f32_e32 v140, v66, v139
	v_lshlrev_b32_e32 v143, 16, v141
	v_and_b32_e32 v141, 0xffff0000, v141
	v_mul_f32_e32 v139, v76, v139
	v_add_f32_e32 v142, v142, v144
	v_fmac_f32_e32 v140, v63, v138
	v_mul_f32_e32 v144, v69, v141
	v_fmac_f32_e32 v139, v70, v138
	v_mul_f32_e32 v138, v81, v141
	v_fmac_f32_e32 v144, v65, v143
	v_fmac_f32_e32 v138, v77, v143
	v_add_f32_e32 v140, v140, v144
	v_add_f32_e32 v138, v139, v138
	v_add_f32_e32 v142, v142, v140
	v_add_f32_e32 v137, v137, v138
	ds_read2st64_b64 v[138:141], v100 offset0:110 offset1:111
	s_waitcnt lgkmcnt(0)
	v_lshlrev_b32_e32 v143, 16, v138
	v_and_b32_e32 v138, 0xffff0000, v138
	v_lshlrev_b32_e32 v145, 16, v139
	v_and_b32_e32 v139, 0xffff0000, v139
	v_mul_f32_e32 v144, v71, v138
	v_mul_f32_e32 v146, v78, v139
	v_mul_f32_e32 v138, v82, v138
	v_mul_f32_e32 v139, v83, v139
	v_fmac_f32_e32 v144, v67, v143
	v_fmac_f32_e32 v146, v68, v145
	v_fmac_f32_e32 v138, v74, v143
	v_fmac_f32_e32 v139, v79, v145
	v_add_f32_e32 v144, v144, v146
	v_add_f32_e32 v138, v138, v139
	v_lshlrev_b32_e32 v139, 16, v140
	v_and_b32_e32 v140, 0xffff0000, v140
	v_lshlrev_b32_e32 v143, 16, v141
	v_and_b32_e32 v141, 0xffff0000, v141
	v_add_f32_e32 v142, v142, v144
	v_add_f32_e32 v137, v137, v138
	v_mul_f32_e32 v138, v84, v140
	v_mul_f32_e32 v144, v87, v141
	v_mul_f32_e32 v140, v89, v140
	v_fmac_f32_e32 v138, v75, v139
	v_fmac_f32_e32 v144, v80, v143
	v_fmac_f32_e32 v140, v85, v139
	v_mul_f32_e32 v139, v90, v141
	v_add_f32_e32 v138, v138, v144
	v_fmac_f32_e32 v139, v88, v143
	v_add_f32_e32 v138, v142, v138
	v_add_f32_e32 v139, v140, v139
	ds_read2st64_b64 v[140:143], v100 offset0:112 offset1:113
	v_add_f32_e32 v137, v137, v139
	s_waitcnt lgkmcnt(0)
	v_lshlrev_b32_e32 v139, 16, v140
	v_and_b32_e32 v140, 0xffff0000, v140
	v_mul_f32_e32 v144, v5, v140
	v_lshlrev_b32_e32 v145, 16, v141
	v_and_b32_e32 v141, 0xffff0000, v141
	v_mul_f32_e32 v140, v8, v140
	v_fmac_f32_e32 v144, v3, v139
	v_fmac_f32_e32 v140, v7, v139
	v_mul_f32_e32 v139, v11, v141
	v_mul_f32_e32 v146, v6, v141
	v_fmac_f32_e32 v139, v9, v145
	v_and_b32_e32 v141, 0xffff0000, v142
	v_fmac_f32_e32 v146, v4, v145
	v_add_f32_e32 v139, v140, v139
	v_lshlrev_b32_e32 v140, 16, v142
	v_mul_f32_e32 v142, v13, v141
	v_lshlrev_b32_e32 v145, 16, v143
	v_and_b32_e32 v143, 0xffff0000, v143
	v_mul_f32_e32 v141, v18, v141
	v_add_f32_e32 v144, v144, v146
	v_fmac_f32_e32 v142, v10, v140
	v_mul_f32_e32 v146, v14, v143
	v_fmac_f32_e32 v141, v16, v140
	v_mul_f32_e32 v140, v41, v143
	v_fmac_f32_e32 v146, v12, v145
	v_fmac_f32_e32 v140, v19, v145
	v_add_f32_e32 v144, 0, v144
	v_add_f32_e32 v139, 0, v139
	v_add_f32_e32 v142, v142, v146
	v_add_f32_e32 v140, v141, v140
	v_add_f32_e32 v144, v144, v142
	v_add_f32_e32 v139, v139, v140
	ds_read2st64_b64 v[140:143], v100 offset0:114 offset1:115
	s_waitcnt lgkmcnt(0)
	v_lshlrev_b32_e32 v145, 16, v140
	v_and_b32_e32 v140, 0xffff0000, v140
	v_lshlrev_b32_e32 v147, 16, v141
	v_and_b32_e32 v141, 0xffff0000, v141
	v_mul_f32_e32 v146, v20, v140
	v_mul_f32_e32 v148, v42, v141
	v_mul_f32_e32 v140, v45, v140
	v_mul_f32_e32 v141, v46, v141
	v_fmac_f32_e32 v140, v21, v145
	v_fmac_f32_e32 v141, v43, v147
	v_fmac_f32_e32 v146, v15, v145
	v_fmac_f32_e32 v148, v17, v147
	v_add_f32_e32 v140, v140, v141
	v_and_b32_e32 v141, 0xffff0000, v142
	v_add_f32_e32 v146, v146, v148
	v_add_f32_e32 v139, v139, v140
	v_lshlrev_b32_e32 v140, 16, v142
	v_mul_f32_e32 v142, v47, v141
	v_lshlrev_b32_e32 v145, 16, v143
	v_and_b32_e32 v143, 0xffff0000, v143
	v_mul_f32_e32 v141, v51, v141
	v_add_f32_e32 v144, v144, v146
	v_fmac_f32_e32 v142, v40, v140
	v_mul_f32_e32 v146, v49, v143
	v_fmac_f32_e32 v141, v48, v140
	v_mul_f32_e32 v140, v52, v143
	v_fmac_f32_e32 v146, v44, v145
	v_fmac_f32_e32 v140, v50, v145
	v_add_f32_e32 v142, v142, v146
	v_add_f32_e32 v140, v141, v140
	v_add_f32_e32 v144, v144, v142
	v_add_f32_e32 v139, v139, v140
	ds_read2st64_b64 v[140:143], v100 offset0:116 offset1:117
	s_waitcnt lgkmcnt(0)
	v_lshlrev_b32_e32 v145, 16, v140
	v_and_b32_e32 v140, 0xffff0000, v140
	v_lshlrev_b32_e32 v147, 16, v141
	v_and_b32_e32 v141, 0xffff0000, v141
	v_mul_f32_e32 v146, v58, v140
	v_mul_f32_e32 v148, v59, v141
	v_mul_f32_e32 v140, v61, v140
	v_mul_f32_e32 v141, v64, v141
	v_fmac_f32_e32 v140, v60, v145
	v_fmac_f32_e32 v141, v62, v147
	v_fmac_f32_e32 v146, v56, v145
	v_fmac_f32_e32 v148, v57, v147
	v_add_f32_e32 v140, v140, v141
	v_and_b32_e32 v141, 0xffff0000, v142
	v_add_f32_e32 v146, v146, v148
	v_add_f32_e32 v139, v139, v140
	v_lshlrev_b32_e32 v140, 16, v142
	v_mul_f32_e32 v142, v66, v141
	v_lshlrev_b32_e32 v145, 16, v143
	v_and_b32_e32 v143, 0xffff0000, v143
	v_mul_f32_e32 v141, v76, v141
	v_add_f32_e32 v144, v144, v146
	v_fmac_f32_e32 v142, v63, v140
	v_mul_f32_e32 v146, v69, v143
	v_fmac_f32_e32 v141, v70, v140
	v_mul_f32_e32 v140, v81, v143
	v_fmac_f32_e32 v146, v65, v145
	v_fmac_f32_e32 v140, v77, v145
	v_add_f32_e32 v142, v142, v146
	v_add_f32_e32 v140, v141, v140
	v_add_f32_e32 v144, v144, v142
	v_add_f32_e32 v139, v139, v140
	ds_read2st64_b64 v[140:143], v100 offset0:118 offset1:119
	s_waitcnt lgkmcnt(0)
	v_lshlrev_b32_e32 v145, 16, v140
	v_and_b32_e32 v140, 0xffff0000, v140
	v_lshlrev_b32_e32 v147, 16, v141
	v_and_b32_e32 v141, 0xffff0000, v141
	v_mul_f32_e32 v146, v71, v140
	v_mul_f32_e32 v148, v78, v141
	v_mul_f32_e32 v140, v82, v140
	v_mul_f32_e32 v141, v83, v141
	v_fmac_f32_e32 v146, v67, v145
	v_fmac_f32_e32 v148, v68, v147
	v_fmac_f32_e32 v140, v74, v145
	v_fmac_f32_e32 v141, v79, v147
	v_add_f32_e32 v146, v146, v148
	v_add_f32_e32 v140, v140, v141
	v_lshlrev_b32_e32 v141, 16, v142
	v_and_b32_e32 v142, 0xffff0000, v142
	v_lshlrev_b32_e32 v145, 16, v143
	v_and_b32_e32 v143, 0xffff0000, v143
	v_add_f32_e32 v144, v144, v146
	v_add_f32_e32 v139, v139, v140
	v_mul_f32_e32 v140, v84, v142
	v_mul_f32_e32 v146, v87, v143
	v_mul_f32_e32 v142, v89, v142
	v_fmac_f32_e32 v140, v75, v141
	v_fmac_f32_e32 v146, v80, v145
	v_fmac_f32_e32 v142, v85, v141
	v_mul_f32_e32 v141, v90, v143
	v_add_f32_e32 v140, v140, v146
	v_fmac_f32_e32 v141, v88, v145
	v_add_f32_e32 v140, v144, v140
	v_add_f32_e32 v141, v142, v141
	ds_read2st64_b64 v[142:145], v100 offset0:120 offset1:121
	v_add_f32_e32 v139, v139, v141
	s_waitcnt lgkmcnt(0)
	v_lshlrev_b32_e32 v141, 16, v142
	v_and_b32_e32 v142, 0xffff0000, v142
	v_mul_f32_e32 v5, v5, v142
	v_fmac_f32_e32 v5, v3, v141
	v_lshlrev_b32_e32 v3, 16, v143
	v_and_b32_e32 v143, 0xffff0000, v143
	v_mul_f32_e32 v6, v6, v143
	v_fmac_f32_e32 v6, v4, v3
	v_add_f32_e32 v4, v5, v6
	v_mul_f32_e32 v5, v8, v142
	v_mul_f32_e32 v6, v11, v143
	v_fmac_f32_e32 v5, v7, v141
	v_fmac_f32_e32 v6, v9, v3
	v_add_f32_e32 v3, v5, v6
	v_and_b32_e32 v6, 0xffff0000, v144
	v_lshlrev_b32_e32 v5, 16, v144
	v_mul_f32_e32 v7, v13, v6
	v_and_b32_e32 v9, 0xffff0000, v145
	v_fmac_f32_e32 v7, v10, v5
	v_lshlrev_b32_e32 v8, 16, v145
	v_mul_f32_e32 v10, v14, v9
	v_fmac_f32_e32 v10, v12, v8
	v_add_f32_e32 v4, 0, v4
	v_add_f32_e32 v7, v7, v10
	v_add_f32_e32 v10, v4, v7
	v_mul_f32_e32 v4, v18, v6
	v_fmac_f32_e32 v4, v16, v5
	v_mul_f32_e32 v5, v41, v9
	v_fmac_f32_e32 v5, v19, v8
	v_add_f32_e32 v3, 0, v3
	v_add_f32_e32 v4, v4, v5
	v_add_f32_e32 v3, v3, v4
	ds_read2st64_b64 v[4:7], v100 offset0:122 offset1:123
	v_cndmask_b32_e64 v13, v122, 0, s[6:7]
	ds_bpermute_b32 v13, v97, v13
	v_cndmask_b32_e64 v14, v124, 0, s[6:7]
	ds_bpermute_b32 v14, v97, v14
	s_waitcnt lgkmcnt(2)
	v_lshlrev_b32_e32 v8, 16, v4
	v_and_b32_e32 v4, 0xffff0000, v4
	v_lshlrev_b32_e32 v11, 16, v5
	v_and_b32_e32 v5, 0xffff0000, v5
	v_mul_f32_e32 v9, v20, v4
	v_mul_f32_e32 v12, v42, v5
	v_mul_f32_e32 v4, v45, v4
	v_mul_f32_e32 v5, v46, v5
	v_fmac_f32_e32 v4, v21, v8
	v_fmac_f32_e32 v5, v43, v11
	v_fmac_f32_e32 v9, v15, v8
	v_fmac_f32_e32 v12, v17, v11
	v_add_f32_e32 v4, v4, v5
	v_and_b32_e32 v5, 0xffff0000, v6
	v_add_f32_e32 v9, v9, v12
	v_add_f32_e32 v3, v3, v4
	v_lshlrev_b32_e32 v4, 16, v6
	v_mul_f32_e32 v6, v47, v5
	v_lshlrev_b32_e32 v8, 16, v7
	v_and_b32_e32 v7, 0xffff0000, v7
	v_mul_f32_e32 v5, v51, v5
	v_add_f32_e32 v9, v10, v9
	v_fmac_f32_e32 v6, v40, v4
	v_mul_f32_e32 v10, v49, v7
	v_fmac_f32_e32 v5, v48, v4
	v_mul_f32_e32 v4, v52, v7
	v_fmac_f32_e32 v10, v44, v8
	v_fmac_f32_e32 v4, v50, v8
	v_add_f32_e32 v6, v6, v10
	v_add_f32_e32 v4, v5, v4
	v_add_f32_e32 v9, v9, v6
	v_add_f32_e32 v3, v3, v4
	ds_read2st64_b64 v[4:7], v100 offset0:124 offset1:125
	v_cndmask_b32_e64 v15, v126, 0, s[6:7]
	ds_bpermute_b32 v15, v97, v15
	v_cndmask_b32_e64 v16, v128, 0, s[6:7]
	ds_bpermute_b32 v16, v97, v16
	s_waitcnt lgkmcnt(2)
	v_lshlrev_b32_e32 v8, 16, v4
	v_and_b32_e32 v4, 0xffff0000, v4
	v_lshlrev_b32_e32 v11, 16, v5
	v_and_b32_e32 v5, 0xffff0000, v5
	v_mul_f32_e32 v10, v58, v4
	v_mul_f32_e32 v12, v59, v5
	v_mul_f32_e32 v4, v61, v4
	v_mul_f32_e32 v5, v64, v5
	v_fmac_f32_e32 v4, v60, v8
	v_fmac_f32_e32 v5, v62, v11
	v_fmac_f32_e32 v10, v56, v8
	v_fmac_f32_e32 v12, v57, v11
	v_add_f32_e32 v4, v4, v5
	v_and_b32_e32 v5, 0xffff0000, v6
	v_add_f32_e32 v10, v10, v12
	v_add_f32_e32 v3, v3, v4
	v_lshlrev_b32_e32 v4, 16, v6
	v_mul_f32_e32 v6, v66, v5
	v_lshlrev_b32_e32 v8, 16, v7
	v_and_b32_e32 v7, 0xffff0000, v7
	v_mul_f32_e32 v5, v76, v5
	v_add_f32_e32 v9, v9, v10
	v_fmac_f32_e32 v6, v63, v4
	v_mul_f32_e32 v10, v69, v7
	v_fmac_f32_e32 v5, v70, v4
	v_mul_f32_e32 v4, v81, v7
	v_fmac_f32_e32 v10, v65, v8
	v_fmac_f32_e32 v4, v77, v8
	v_add_f32_e32 v6, v6, v10
	v_add_f32_e32 v4, v5, v4
	v_add_f32_e32 v9, v9, v6
	v_add_f32_e32 v3, v3, v4
	ds_read2st64_b64 v[4:7], v100 offset0:126 offset1:127
	v_cndmask_b32_e64 v17, v130, 0, s[6:7]
	ds_bpermute_b32 v17, v97, v17
	v_cndmask_b32_e64 v18, v132, 0, s[6:7]
	ds_bpermute_b32 v18, v97, v18
	s_waitcnt lgkmcnt(2)
	v_lshlrev_b32_e32 v8, 16, v4
	v_and_b32_e32 v4, 0xffff0000, v4
	v_lshlrev_b32_e32 v11, 16, v5
	v_and_b32_e32 v5, 0xffff0000, v5
	v_mul_f32_e32 v10, v71, v4
	v_mul_f32_e32 v12, v78, v5
	v_mul_f32_e32 v4, v82, v4
	v_mul_f32_e32 v5, v83, v5
	v_fmac_f32_e32 v4, v74, v8
	v_fmac_f32_e32 v5, v79, v11
	v_add_f32_e32 v4, v4, v5
	v_and_b32_e32 v5, 0xffff0000, v6
	v_fmac_f32_e32 v10, v67, v8
	v_add_f32_e32 v3, v3, v4
	v_lshlrev_b32_e32 v4, 16, v6
	v_mul_f32_e32 v6, v84, v5
	v_lshlrev_b32_e32 v8, 16, v7
	v_and_b32_e32 v7, 0xffff0000, v7
	v_mul_f32_e32 v5, v89, v5
	v_fmac_f32_e32 v6, v75, v4
	v_fmac_f32_e32 v5, v85, v4
	v_mul_f32_e32 v4, v90, v7
	v_fmac_f32_e32 v4, v88, v8
	v_add_f32_e32 v4, v5, v4
	v_add_f32_e32 v3, v3, v4
	v_cndmask_b32_e64 v4, v54, v136, s[6:7]
	ds_bpermute_b32 v4, v97, v4
	v_cndmask_b32_e64 v5, v136, v54, s[6:7]
	v_fmac_f32_e32 v12, v68, v11
	v_add_f32_e32 v10, v10, v12
	v_add_f32_e32 v9, v9, v10
	s_waitcnt lgkmcnt(0)
	v_add_f32_e32 v4, v5, v4
	v_cndmask_b32_e64 v5, v72, v138, s[6:7]
	ds_bpermute_b32 v5, v97, v5
	v_mul_f32_e32 v10, v87, v7
	v_cndmask_b32_e64 v7, v138, v72, s[6:7]
	v_fmac_f32_e32 v10, v80, v8
	v_add_f32_e32 v6, v6, v10
	s_waitcnt lgkmcnt(0)
	v_add_f32_e32 v5, v7, v5
	v_cndmask_b32_e64 v7, v86, v140, s[6:7]
	ds_bpermute_b32 v7, v97, v7
	v_add_f32_e32 v6, v9, v6
	v_cndmask_b32_e64 v8, v140, v86, s[6:7]
	v_cndmask_b32_e64 v9, v114, 0, s[6:7]
	ds_bpermute_b32 v9, v97, v9
	s_waitcnt lgkmcnt(1)
	v_add_f32_e32 v7, v8, v7
	v_cndmask_b32_e64 v8, v1, v6, s[6:7]
	v_cndmask_b32_e64 v1, v6, v1, s[6:7]
	ds_bpermute_b32 v6, v97, v8
	v_cndmask_b32_e64 v8, v53, 0, s[6:7]
	ds_bpermute_b32 v8, v97, v8
	v_cndmask_b32_e64 v10, v116, 0, s[6:7]
	ds_bpermute_b32 v10, v97, v10
	v_cndmask_b32_e64 v11, v118, 0, s[6:7]
	ds_bpermute_b32 v11, v97, v11
	v_cndmask_b32_e64 v12, v120, 0, s[6:7]
	s_waitcnt lgkmcnt(3)
	v_add_f32_e32 v1, v1, v6
	v_cndmask_b32_e64 v6, 0, v53, s[6:7]
	ds_bpermute_b32 v12, v97, v12
	s_waitcnt lgkmcnt(3)
	v_add_f32_e32 v6, v6, v8
	v_cndmask_b32_e64 v8, 0, v114, s[6:7]
	v_add_f32_e32 v8, v8, v9
	v_cndmask_b32_e64 v9, 0, v116, s[6:7]
	s_waitcnt lgkmcnt(2)
	v_add_f32_e32 v9, v9, v10
	v_cndmask_b32_e64 v10, 0, v118, s[6:7]
	s_waitcnt lgkmcnt(1)
	v_add_f32_e32 v10, v10, v11
	v_cndmask_b32_e64 v11, 0, v120, s[6:7]
	s_waitcnt lgkmcnt(0)
	v_add_f32_e32 v11, v11, v12
	v_cndmask_b32_e64 v12, 0, v122, s[6:7]
	v_add_f32_e32 v12, v12, v13
	v_cndmask_b32_e64 v13, 0, v124, s[6:7]
	v_cndmask_b32_e64 v19, v134, 0, s[6:7]
	v_add_f32_e32 v13, v13, v14
	v_cndmask_b32_e64 v14, 0, v126, s[6:7]
	ds_bpermute_b32 v19, v97, v19
	v_add_f32_e32 v14, v14, v15
	v_cndmask_b32_e64 v15, 0, v128, s[6:7]
	v_add_f32_e32 v15, v15, v16
	v_cndmask_b32_e64 v16, 0, v130, s[6:7]
	v_add_f32_e32 v16, v16, v17
	v_cndmask_b32_e64 v17, 0, v132, s[6:7]
	v_add_f32_e32 v17, v17, v18
	v_cndmask_b32_e64 v18, 0, v134, s[6:7]
	s_waitcnt lgkmcnt(0)
	v_add_f32_e32 v18, v18, v19
	v_cndmask_b32_e64 v19, v22, v135, s[6:7]
	ds_bpermute_b32 v19, v97, v19
	v_cndmask_b32_e64 v20, v135, v22, s[6:7]
	v_cndmask_b32_e64 v21, v137, v55, s[6:7]
	v_cndmask_b32_e64 v22, v139, v73, s[6:7]
	v_cndmask_b32_e64 v40, v115, 0, s[6:7]
	s_waitcnt lgkmcnt(0)
	v_add_f32_e32 v19, v20, v19
	v_cndmask_b32_e64 v20, v55, v137, s[6:7]
	ds_bpermute_b32 v20, v97, v20
	ds_bpermute_b32 v40, v97, v40
	v_cndmask_b32_e64 v41, v117, 0, s[6:7]
	ds_bpermute_b32 v41, v97, v41
	v_cndmask_b32_e64 v42, v119, 0, s[6:7]
	s_waitcnt lgkmcnt(2)
	v_add_f32_e32 v20, v21, v20
	v_cndmask_b32_e64 v21, v73, v139, s[6:7]
	ds_bpermute_b32 v21, v97, v21
	ds_bpermute_b32 v42, v97, v42
	v_cndmask_b32_e64 v43, v121, 0, s[6:7]
	ds_bpermute_b32 v43, v97, v43
	v_cndmask_b32_e64 v44, v123, 0, s[6:7]
	s_waitcnt lgkmcnt(2)
	v_add_f32_e32 v21, v22, v21
	v_cndmask_b32_e64 v22, v0, v3, s[6:7]
	v_cndmask_b32_e64 v0, v3, v0, s[6:7]
	ds_bpermute_b32 v3, v97, v22
	v_cndmask_b32_e64 v22, v91, 0, s[6:7]
	ds_bpermute_b32 v22, v97, v22
	ds_bpermute_b32 v44, v97, v44
	v_cndmask_b32_e64 v45, v125, 0, s[6:7]
	s_waitcnt lgkmcnt(2)
	v_add_f32_e32 v0, v0, v3
	v_cndmask_b32_e64 v3, 0, v2, s[6:7]
	v_cndmask_b32_e64 v2, v2, 0, s[6:7]
	ds_bpermute_b32 v2, v97, v2
	ds_bpermute_b32 v45, v97, v45
	v_cndmask_b32_e64 v46, v127, 0, s[6:7]
	ds_bpermute_b32 v46, v97, v46
	v_cndmask_b32_e64 v47, v129, 0, s[6:7]
	s_waitcnt lgkmcnt(2)
	v_add_f32_e32 v2, v3, v2
	v_cndmask_b32_e64 v3, 0, v91, s[6:7]
	v_add_f32_e32 v3, v3, v22
	v_cndmask_b32_e64 v22, 0, v115, s[6:7]
	v_add_f32_e32 v22, v22, v40
	v_cndmask_b32_e64 v40, 0, v117, s[6:7]
	v_add_f32_e32 v40, v40, v41
	v_cndmask_b32_e64 v41, 0, v119, s[6:7]
	v_add_f32_e32 v41, v41, v42
	v_cndmask_b32_e64 v42, 0, v121, s[6:7]
	ds_bpermute_b32 v47, v97, v47
	v_cndmask_b32_e64 v48, v131, 0, s[6:7]
	v_add_f32_e32 v42, v42, v43
	v_cndmask_b32_e64 v43, 0, v123, s[6:7]
	ds_bpermute_b32 v48, v97, v48
	v_cndmask_b32_e64 v49, v133, 0, s[6:7]
	v_add_f32_e32 v43, v43, v44
	v_cndmask_b32_e64 v44, 0, v125, s[6:7]
	ds_bpermute_b32 v49, v97, v49
	s_waitcnt lgkmcnt(4)
	v_add_f32_e32 v44, v44, v45
	v_cndmask_b32_e64 v45, 0, v127, s[6:7]
	s_waitcnt lgkmcnt(3)
	v_add_f32_e32 v45, v45, v46
	v_cndmask_b32_e64 v46, 0, v129, s[6:7]
	s_waitcnt lgkmcnt(2)
	v_add_f32_e32 v46, v46, v47
	v_cndmask_b32_e64 v47, 0, v131, s[6:7]
	s_waitcnt lgkmcnt(1)
	v_add_f32_e32 v47, v47, v48
	v_cndmask_b32_e64 v48, 0, v133, s[6:7]
	s_waitcnt lgkmcnt(0)
	v_add_f32_e32 v48, v48, v49
	v_cndmask_b32_e64 v49, v4, v11, s[8:9]
	v_cndmask_b32_e64 v4, v11, v4, s[8:9]
	ds_bpermute_b32 v11, v96, v49
	s_waitcnt lgkmcnt(0)
	v_add_f32_e32 v4, v4, v11
	v_cndmask_b32_e64 v11, v5, v12, s[8:9]
	ds_bpermute_b32 v11, v96, v11
	v_cndmask_b32_e64 v5, v12, v5, s[8:9]
	v_cndmask_b32_e64 v12, v41, v19, s[8:9]
	s_waitcnt lgkmcnt(0)
	v_add_f32_e32 v5, v5, v11
	v_cndmask_b32_e64 v11, v7, v13, s[8:9]
	ds_bpermute_b32 v11, v96, v11
	v_cndmask_b32_e64 v7, v13, v7, s[8:9]
	v_cndmask_b32_e64 v13, v42, v20, s[8:9]
	s_waitcnt lgkmcnt(0)
	v_add_f32_e32 v7, v7, v11
	v_cndmask_b32_e64 v11, v1, v14, s[8:9]
	ds_bpermute_b32 v11, v96, v11
	v_cndmask_b32_e64 v1, v14, v1, s[8:9]
	v_cndmask_b32_e64 v14, v43, v21, s[8:9]
	s_waitcnt lgkmcnt(0)
	v_add_f32_e32 v1, v1, v11
	v_cndmask_b32_e64 v11, v6, v15, s[8:9]
	ds_bpermute_b32 v11, v96, v11
	v_cndmask_b32_e64 v6, v15, v6, s[8:9]
	v_cndmask_b32_e64 v15, v47, v22, s[8:9]
	s_waitcnt lgkmcnt(0)
	v_add_f32_e32 v6, v6, v11
	v_cndmask_b32_e64 v11, v8, v16, s[8:9]
	ds_bpermute_b32 v11, v96, v11
	v_cndmask_b32_e64 v8, v16, v8, s[8:9]
	v_cndmask_b32_e64 v16, v48, v40, s[8:9]
	s_waitcnt lgkmcnt(0)
	v_add_f32_e32 v8, v8, v11
	v_cndmask_b32_e64 v11, v9, v17, s[8:9]
	ds_bpermute_b32 v11, v96, v11
	v_cndmask_b32_e64 v9, v17, v9, s[8:9]
	s_waitcnt lgkmcnt(0)
	v_add_f32_e32 v9, v9, v11
	v_cndmask_b32_e64 v11, v10, v18, s[8:9]
	ds_bpermute_b32 v11, v96, v11
	v_cndmask_b32_e64 v10, v18, v10, s[8:9]
	s_waitcnt lgkmcnt(0)
	v_add_f32_e32 v10, v10, v11
	v_cndmask_b32_e64 v11, v19, v41, s[8:9]
	ds_bpermute_b32 v11, v96, v11
	s_waitcnt lgkmcnt(0)
	v_add_f32_e32 v11, v12, v11
	v_cndmask_b32_e64 v12, v20, v42, s[8:9]
	ds_bpermute_b32 v12, v96, v12
	s_waitcnt lgkmcnt(0)
	v_add_f32_e32 v12, v13, v12
	v_cndmask_b32_e64 v13, v21, v43, s[8:9]
	ds_bpermute_b32 v13, v96, v13
	s_waitcnt lgkmcnt(0)
	v_add_f32_e32 v13, v14, v13
	v_cndmask_b32_e64 v14, v0, v44, s[8:9]
	ds_bpermute_b32 v14, v96, v14
	v_cndmask_b32_e64 v0, v44, v0, s[8:9]
	s_waitcnt lgkmcnt(0)
	v_add_f32_e32 v0, v0, v14
	v_cndmask_b32_e64 v14, v2, v45, s[8:9]
	ds_bpermute_b32 v14, v96, v14
	v_cndmask_b32_e64 v2, v45, v2, s[8:9]
	s_waitcnt lgkmcnt(0)
	v_add_f32_e32 v2, v2, v14
	v_cndmask_b32_e64 v14, v3, v46, s[8:9]
	ds_bpermute_b32 v14, v96, v14
	v_cndmask_b32_e64 v3, v46, v3, s[8:9]
	s_waitcnt lgkmcnt(0)
	v_add_f32_e32 v3, v3, v14
	v_cndmask_b32_e64 v14, v22, v47, s[8:9]
	ds_bpermute_b32 v14, v96, v14
	s_waitcnt lgkmcnt(0)
	v_add_f32_e32 v14, v15, v14
	v_cndmask_b32_e64 v15, v40, v48, s[8:9]
	ds_bpermute_b32 v15, v96, v15
	s_waitcnt lgkmcnt(0)
	v_add_f32_e32 v15, v16, v15
	v_cndmask_b32_e64 v16, v4, v6, s[10:11]
	v_cndmask_b32_e64 v4, v6, v4, s[10:11]
	ds_bpermute_b32 v6, v95, v16
	s_waitcnt lgkmcnt(0)
	v_add_f32_e32 v4, v4, v6
	v_cndmask_b32_e64 v6, v5, v8, s[10:11]
	ds_bpermute_b32 v6, v95, v6
	v_cndmask_b32_e64 v5, v8, v5, s[10:11]
	v_cndmask_b32_e64 v8, v14, v13, s[10:11]
	s_waitcnt lgkmcnt(0)
	v_add_f32_e32 v5, v5, v6
	v_cndmask_b32_e64 v6, v7, v9, s[10:11]
	ds_bpermute_b32 v6, v95, v6
	v_cndmask_b32_e64 v7, v9, v7, s[10:11]
	s_waitcnt lgkmcnt(0)
	v_add_f32_e32 v6, v7, v6
	v_cndmask_b32_e64 v7, v1, v10, s[10:11]
	ds_bpermute_b32 v7, v95, v7
	v_cndmask_b32_e64 v1, v10, v1, s[10:11]
	s_waitcnt lgkmcnt(0)
	v_add_f32_e32 v1, v1, v7
	v_cndmask_b32_e64 v7, v11, v2, s[10:11]
	ds_bpermute_b32 v7, v95, v7
	v_cndmask_b32_e64 v2, v2, v11, s[10:11]
	s_waitcnt lgkmcnt(0)
	v_add_f32_e32 v2, v2, v7
	v_cndmask_b32_e64 v7, v12, v3, s[10:11]
	ds_bpermute_b32 v7, v95, v7
	v_cndmask_b32_e64 v3, v3, v12, s[10:11]
	s_waitcnt lgkmcnt(0)
	v_add_f32_e32 v3, v3, v7
	v_cndmask_b32_e64 v7, v13, v14, s[10:11]
	ds_bpermute_b32 v7, v95, v7
	s_waitcnt lgkmcnt(0)
	v_add_f32_e32 v7, v8, v7
	v_cndmask_b32_e64 v8, v0, v15, s[10:11]
	ds_bpermute_b32 v8, v95, v8
	v_cndmask_b32_e64 v0, v15, v0, s[10:11]
	s_waitcnt lgkmcnt(0)
	v_add_f32_e32 v8, v0, v8
	v_cndmask_b32_e64 v0, v4, v6, s[12:13]
	ds_bpermute_b32 v0, v94, v0
	v_cndmask_b32_e64 v4, v6, v4, s[12:13]
	s_waitcnt lgkmcnt(0)
	v_add_f32_e32 v4, v4, v0
	v_cndmask_b32_e64 v0, v5, v1, s[12:13]
	ds_bpermute_b32 v0, v94, v0
	v_cndmask_b32_e64 v1, v1, v5, s[12:13]
	s_waitcnt lgkmcnt(0)
	v_add_f32_e32 v5, v1, v0
	v_cndmask_b32_e64 v0, v2, v7, s[12:13]
	ds_bpermute_b32 v0, v94, v0
	v_cndmask_b32_e64 v1, v7, v2, s[12:13]
	v_cndmask_b32_e64 v2, v8, v3, s[12:13]
	s_waitcnt lgkmcnt(0)
	v_add_f32_e32 v0, v1, v0
	v_cndmask_b32_e64 v1, v3, v8, s[12:13]
	ds_bpermute_b32 v1, v94, v1
	v_cndmask_b32_e64 v3, v5, v4, s[14:15]
	s_waitcnt lgkmcnt(0)
	v_add_f32_e32 v1, v2, v1
	v_cndmask_b32_e64 v2, v4, v5, s[14:15]
	ds_bpermute_b32 v2, v93, v2
	s_waitcnt lgkmcnt(0)
	v_add_f32_e32 v3, v3, v2
	v_cndmask_b32_e64 v2, v0, v1, s[14:15]
	ds_bpermute_b32 v2, v93, v2
	ds_bpermute_b32 v4, v25, v3
	s_and_saveexec_b64 s[20:21], s[16:17]
	s_cbranch_execz .LBB0_949
	s_waitcnt lgkmcnt(0)
	v_add_f32_e32 v3, v3, v4
	ds_write_b32 v101, v3

.LBB0_994:
	s_or_b64 exec, exec, s[26:27]
	v_cndmask_b32_e64 v2, v56, v41, s[20:21]
	v_sub_f32_e32 v3, v18, v2
	v_mul_f32_e32 v3, 0x3fb8aa3b, v3
	v_sub_f32_e32 v4, v19, v2
	v_exp_f32_e32 v3, v3
	v_mul_f32_e32 v4, 0x3fb8aa3b, v4
	v_sub_f32_e32 v5, v43, v2
	v_exp_f32_e32 v4, v4
	v_mul_f32_e32 v5, 0x3fb8aa3b, v5
	v_sub_f32_e32 v2, v41, v2
	v_exp_f32_e32 v5, v5
	v_mul_f32_e32 v2, 0x3fb8aa3b, v2
	v_exp_f32_e32 v2, v2
	v_add_f32_e32 v3, 0, v3
	v_add_f32_e32 v3, v4, v3
	v_add_f32_e32 v3, v5, v3
	v_add_f32_e32 v2, v2, v3
	v_rcp_f32_e32 v4, v2
	v_cndmask_b32_e64 v1, v1, v46, s[22:23]
	v_cndmask_b32_e32 v0, v46, v0, vcc
	v_sub_f32_e32 v0, v1, v0
	v_mul_f32_e32 v0, 0x3fb8aa3b, v0
	v_exp_f32_e32 v1, v0
	v_mul_f32_e32 v0, 1.0, v4
	v_add_f32_e32 v2, 1.0, v1
	v_rcp_f32_e32 v4, v2
	s_ashr_i32 s41, s40, 31
	s_lshl_b64 s[20:21], s[40:41], 2
	s_add_u32 s20, s57, s20
	v_rcp_f32_e32 v7, v2
	v_mul_f32_e32 v3, v1, v4
	s_addc_u32 s21, s58, s21
	v_mul_f32_e32 v1, 1.0, v7
	v_mov_b32_e32 v2, v1
	v_pk_mul_f32 v[0:1], v[0:1], v[2:3] op_sel_hi:[0,1]
	global_store_dwordx2 v23, v[0:1], s[20:21]
	global_load_dwordx3 v[20:22], v23, s[38:39] offset:52
	global_load_dwordx4 v[4:7], v23, s[38:39] offset:4
	s_nop 0
	global_load_dwordx4 v[0:3], v23, s[38:39] offset:20
	global_load_dwordx4 v[8:11], v23, s[38:39] offset:36
	global_load_dwordx4 v[12:15], v23, s[36:37]
	s_waitcnt lgkmcnt(0)
	v_readfirstlane_b32 s20, v42
	v_add_u32_e32 v18, s28, v16
	v_mov_b32_e32 v16, s48
	v_mov_b32_e32 v41, s60
	v_add_u32_e32 v19, s20, v40
	ds_write_b128 v41, v[16:19]
	s_waitcnt vmcnt(3)
	v_mov_b32_e32 v42, v7
	s_waitcnt vmcnt(2)
	v_mov_b32_e32 v16, v3
	s_waitcnt vmcnt(1)
	v_mov_b32_e32 v40, v11

.LBB0_1038:
	v_cndmask_b32_e32 v2, v52, v7, vcc
	v_cmp_gt_f32_e32 vcc, v16, v41
	v_sub_f32_e32 v4, v12, v2
	v_sub_f32_e32 v5, v13, v2
	v_sub_f32_e32 v6, v11, v2
	v_sub_f32_e32 v2, v7, v2
	v_cndmask_b32_e32 v7, v41, v16, vcc
	v_cmp_gt_f32_e64 s[20:21], v0, v7
	v_cndmask_b32_e64 v8, 0, 1, vcc
	v_mul_f32_e32 v4, 0x3fb8aa3b, v4
	v_cndmask_b32_e64 v7, v7, v0, s[20:21]
	v_cndmask_b32_e64 v8, v8, 2, s[20:21]
	v_cmp_ngt_f32_e32 vcc, v1, v7
	v_cmp_nlt_f32_e64 s[24:25], s62, v41
	v_exp_f32_e32 v4, v4
	v_cndmask_b32_e32 v8, 3, v8, vcc
	v_cmp_eq_u32_e64 s[22:23], 0, v8
	v_mul_f32_e32 v5, 0x3fb8aa3b, v5
	s_or_b64 s[22:23], s[22:23], s[24:25]
	v_exp_f32_e32 v5, v5
	v_mul_f32_e32 v6, 0x3fb8aa3b, v6
	v_cndmask_b32_e64 v9, v41, v113, s[22:23]
	v_exp_f32_e32 v6, v6
	v_mul_f32_e32 v2, 0x3fb8aa3b, v2
	s_and_b64 s[26:27], s[20:21], vcc
	v_cmp_ne_u32_e64 s[20:21], 1, v8
	v_cmp_gt_f32_e64 s[24:25], v16, v9
	v_exp_f32_e32 v2, v2
	s_and_b64 s[20:21], s[20:21], s[24:25]
	v_cndmask_b32_e64 v9, v9, v16, s[20:21]
	v_add_f32_e32 v4, 0, v4
	v_cmp_ngt_f32_e64 s[24:25], v0, v9
	v_add_f32_e32 v4, v5, v4
	s_or_b64 s[24:25], s[26:27], s[24:25]
	v_add_f32_e32 v4, v6, v4
	v_cndmask_b32_e64 v0, v0, v9, s[24:25]
	v_cndmask_b32_e64 v9, 0, -1, s[22:23]
	v_add_f32_e32 v4, v2, v4
	v_cndmask_b32_e64 v9, v9, 1, s[20:21]
	v_rcp_f32_e32 v5, v4
	v_cmp_gt_f32_e64 s[26:27], v1, v0
	s_and_b64 s[26:27], vcc, s[26:27]
	v_cndmask_b32_e64 v6, 2, v9, s[24:25]
	v_cndmask_b32_e64 v0, v0, v1, s[26:27]
	v_cndmask_b32_e32 v1, v1, v7, vcc
	v_sub_f32_e32 v0, v0, v1
	v_mul_f32_e32 v0, 0x3fb8aa3b, v0
	v_lshlrev_b32_e32 v1, 2, v3
	v_cndmask_b32_e64 v6, v6, 3, s[26:27]
	v_exp_f32_e32 v10, v0
	v_or_b32_e32 v0, v8, v1
	s_add_i32 s20, 0, 0x20000
	v_add_u32_e32 v1, v6, v1
	v_lshl_add_u32 v2, v0, 2, s20
	ds_add_rtn_u32 v2, v2, v112
	v_lshl_add_u32 v3, v1, 2, s20
	ds_add_rtn_u32 v3, v3, v112
	v_mul_f32_e32 v5, 1.0, v5
	v_mov_b32_e32 v4, v5
	v_add_f32_e32 v5, 1.0, v10
	v_mov_b32_e32 v6, s60
	s_waitcnt lgkmcnt(0)
	ds_write_b128 v6, v[0:3] offset:16
	v_rcp_f32_e32 v1, v5
	s_add_i32 s20, s40, 2
	s_ashr_i32 s21, s20, 31
	s_lshl_b64 s[20:21], s[20:21], 2
	v_rcp_f32_e32 v6, v5
	v_mul_f32_e32 v0, v10, v1
	v_mov_b32_e32 v1, v0
	s_add_u32 s20, s57, s20
	v_mul_f32_e32 v0, 1.0, v6
	s_addc_u32 s21, s58, s21
	v_pk_mul_f32 v[0:1], v[4:5], v[0:1] op_sel_hi:[0,1]
	global_store_dwordx2 v23, v[0:1], s[20:21]
	s_branch .LBB0_946

.LBB0_1869:
	s_or_b64 exec, exec, s[8:9]
	s_lshl_b32 s8, s43, 5
	s_and_b32 s44, s8, 0xffffff80
	v_add_u32_e32 v0, s44, v108
	v_mov_b64_e32 v[16:17], s[16:17]
	s_waitcnt lgkmcnt(0)
	v_mad_i64_i32 v[0:1], s[8:9], v0, s40, v[16:17]
	s_lshl_b32 s24, s18, 8
	s_mov_b32 s25, s19
	v_lshl_add_u64 v[0:1], v[0:1], 0, s[24:25]
	v_mov_b32_e32 v83, v79
	v_lshl_add_u64 v[18:19], v[0:1], 0, v[82:83]
	global_load_dwordx4 v[12:15], v[18:19], off offset:3200
	global_load_dwordx4 v[8:11], v[18:19], off offset:3216
	global_load_dwordx4 v[0:3], v[18:19], off offset:3248
	global_load_dwordx4 v[4:7], v[18:19], off offset:3232
	s_lshl_b32 s18, s18, 7
	v_mov_b32_e32 v85, v79
	s_mov_b32 s23, s19
	s_waitcnt vmcnt(3)
	v_lshlrev_b32_e32 v18, 16, v12
	v_and_b32_e32 v12, 0xffff0000, v12
	v_lshlrev_b32_e32 v20, 16, v13
	v_and_b32_e32 v21, 0xffff0000, v13
	v_mul_f32_e32 v13, 0x3d372713, v18
	v_mul_f32_e32 v19, 0x3d372713, v12
	v_mul_f32_e32 v13, v13, v18
	v_mul_f32_e32 v23, 0x3d372713, v20
	v_mul_f32_e32 v19, v19, v12
	v_fma_f32 v13, v13, v18, v18
	v_mul_f32_e32 v23, v23, v20
	v_fma_f32 v19, v19, v12, v12
	v_mul_f32_e32 v13, 0x3f4c422a, v13
	v_fma_f32 v23, v23, v20, v20
	v_mul_f32_e32 v19, 0x3f4c422a, v19
	v_mul_f32_e32 v13, -2.0, v13
	v_mul_f32_e32 v23, 0x3f4c422a, v23
	v_mul_f32_e32 v19, -2.0, v19
	v_mul_f32_e32 v13, 0x3fb8aa3b, v13
	v_mul_f32_e32 v23, -2.0, v23
	v_mul_f32_e32 v19, 0x3fb8aa3b, v19
	v_exp_f32_e32 v13, v13
	v_mul_f32_e32 v23, 0x3fb8aa3b, v23
	v_exp_f32_e32 v19, v19
	v_mul_f32_e32 v24, 0x3d372713, v21
	v_exp_f32_e32 v23, v23
	v_mul_f32_e32 v24, v24, v21
	v_fma_f32 v24, v24, v21, v21
	v_add_f32_e32 v13, 1.0, v13
	v_mul_f32_e32 v24, 0x3f4c422a, v24
	v_add_f32_e32 v26, 1.0, v19
	v_mul_f32_e32 v24, -2.0, v24
	v_add_f32_e32 v23, 1.0, v23
	v_div_scale_f32 v28, s[8:9], v26, v26, v12
	v_rcp_f32_e32 v34, v13
	v_mul_f32_e32 v24, 0x3fb8aa3b, v24
	v_div_scale_f32 v30, s[10:11], v23, v23, v20
	v_rcp_f32_e32 v35, v28
	v_lshlrev_b32_e32 v22, 16, v14
	v_exp_f32_e32 v24, v24
	v_rcp_f32_e32 v36, v30
	v_mul_f32_e32 v25, 0x3d372713, v22
	v_mul_f32_e32 v25, v25, v22
	v_fma_f32 v25, v25, v22, v22
	v_fma_f32 v39, -v28, v35, 1.0
	v_mul_f32_e32 v25, 0x3f4c422a, v25
	v_add_f32_e32 v24, 1.0, v24
	v_div_scale_f32 v29, s[8:9], v12, v26, v12
	v_fma_f32 v40, -v30, v36, 1.0
	v_fmac_f32_e32 v35, v39, v35
	v_mul_f32_e32 v25, -2.0, v25
	v_div_scale_f32 v31, s[10:11], v20, v23, v20
	v_div_scale_f32 v32, s[12:13], v24, v24, v21
	v_fmac_f32_e32 v36, v40, v36
	v_mul_f32_e32 v39, v29, v35
	v_mul_f32_e32 v25, 0x3fb8aa3b, v25
	v_rcp_f32_e32 v37, v32
	v_mul_f32_e32 v40, v31, v36
	v_fma_f32 v43, -v28, v39, v29
	v_exp_f32_e32 v25, v25
	v_fma_f32 v44, -v30, v40, v31
	v_fmac_f32_e32 v39, v43, v35
	v_fmac_f32_e32 v40, v44, v36
	v_fma_f32 v27, -v28, v39, v29
	v_mul_f32_e32 v19, v18, v34
	s_mov_b64 vcc, s[8:9]
	v_fma_f32 v28, -v30, v40, v31
	v_div_fmas_f32 v13, v27, v35, v39
	s_mov_b64 vcc, s[10:11]
	v_fma_f32 v41, -v32, v37, 1.0
	v_div_fixup_f32 v13, v13, v26, v12
	v_div_fmas_f32 v12, v28, v36, v40
	v_div_scale_f32 v33, s[12:13], v21, v24, v21
	v_fmac_f32_e32 v37, v41, v37
	v_div_fixup_f32 v12, v12, v23, v20
	v_add_f32_e32 v20, 1.0, v25
	v_and_b32_e32 v26, 0xffff0000, v14
	v_mul_f32_e32 v41, v33, v37
	v_mul_f32_e32 v14, 0x3d372713, v26
	v_fma_f32 v45, -v32, v41, v33
	v_rcp_f32_e32 v25, v20
	v_mul_f32_e32 v14, v14, v26
	v_fmac_f32_e32 v41, v45, v37
	v_fma_f32 v14, v14, v26, v26
	v_fma_f32 v29, -v32, v41, v33
	s_mov_b64 vcc, s[12:13]
	v_mul_f32_e32 v14, 0x3f4c422a, v14
	v_div_fmas_f32 v18, v29, v37, v41
	v_mul_f32_e32 v14, -2.0, v14
	v_div_fixup_f32 v18, v18, v24, v21
	v_mul_f32_e32 v14, 0x3fb8aa3b, v14
	v_exp_f32_e32 v14, v14
	s_nop 0
	v_add_f32_e32 v23, 1.0, v14
	v_mul_f32_e32 v14, v22, v25
	v_rcp_f32_e32 v28, v23
	v_lshlrev_b32_e32 v22, 16, v15
	v_mul_f32_e32 v24, 0x3d372713, v22
	v_mul_f32_e32 v24, v24, v22
	v_fma_f32 v24, v24, v22, v22
	v_mul_f32_e32 v24, 0x3f4c422a, v24
	v_mul_f32_e32 v24, -2.0, v24
	v_mul_f32_e32 v24, 0x3fb8aa3b, v24
	v_exp_f32_e32 v24, v24
	v_mul_f32_e32 v20, v26, v28
	v_add_f32_e32 v24, 1.0, v24
	v_and_b32_e32 v26, 0xffff0000, v15
	v_mul_f32_e32 v15, 0x3d372713, v26
	v_rcp_f32_e32 v27, v24
	v_mul_f32_e32 v15, v15, v26
	v_fma_f32 v15, v15, v26, v26
	v_mul_f32_e32 v15, 0x3f4c422a, v15
	v_mul_f32_e32 v15, -2.0, v15
	v_mul_f32_e32 v15, 0x3fb8aa3b, v15
	v_exp_f32_e32 v15, v15
	s_nop 0
	v_add_f32_e32 v25, 1.0, v15
	v_rcp_f32_e32 v29, v25
	v_mul_f32_e32 v15, v22, v27
	s_waitcnt vmcnt(2)
	v_lshlrev_b32_e32 v23, 16, v8
	v_mul_f32_e32 v24, 0x3d372713, v23
	v_mul_f32_e32 v24, v24, v23
	v_fma_f32 v24, v24, v23, v23
	v_mul_f32_e32 v24, 0x3f4c422a, v24
	v_mul_f32_e32 v24, -2.0, v24
	v_mul_f32_e32 v24, 0x3fb8aa3b, v24
	v_exp_f32_e32 v24, v24
	v_mul_f32_e32 v21, v26, v29
	v_add_f32_e32 v24, 1.0, v24
	v_and_b32_e32 v26, 0xffff0000, v8
	v_mul_f32_e32 v8, 0x3d372713, v26
	v_rcp_f32_e32 v28, v24
	v_mul_f32_e32 v8, v8, v26
	v_fma_f32 v8, v8, v26, v26
	v_mul_f32_e32 v8, 0x3f4c422a, v8
	v_mul_f32_e32 v8, -2.0, v8
	v_mul_f32_e32 v8, 0x3fb8aa3b, v8
	v_exp_f32_e32 v8, v8
	s_nop 0
	v_add_f32_e32 v27, 1.0, v8
	v_mul_f32_e32 v8, v23, v28
	v_rcp_f32_e32 v30, v27
	v_lshlrev_b32_e32 v24, 16, v9
	v_mul_f32_e32 v25, 0x3d372713, v24
	v_mul_f32_e32 v25, v25, v24
	v_fma_f32 v25, v25, v24, v24
	v_mul_f32_e32 v25, 0x3f4c422a, v25
	v_mul_f32_e32 v25, -2.0, v25
	v_mul_f32_e32 v25, 0x3fb8aa3b, v25
	v_exp_f32_e32 v25, v25
	v_mul_f32_e32 v22, v26, v30
	v_add_f32_e32 v25, 1.0, v25
	v_and_b32_e32 v27, 0xffff0000, v9
	v_mul_f32_e32 v9, 0x3d372713, v27
	v_rcp_f32_e32 v29, v25
	v_mul_f32_e32 v9, v9, v27
	v_fma_f32 v9, v9, v27, v27
	v_mul_f32_e32 v9, 0x3f4c422a, v9
	v_mul_f32_e32 v9, -2.0, v9
	v_mul_f32_e32 v9, 0x3fb8aa3b, v9
	v_exp_f32_e32 v9, v9
	s_nop 0
	v_add_f32_e32 v28, 1.0, v9
	v_mul_f32_e32 v9, v24, v29
	v_rcp_f32_e32 v31, v28
	v_lshlrev_b32_e32 v25, 16, v10
	v_mul_f32_e32 v26, 0x3d372713, v25
	v_mul_f32_e32 v26, v26, v25
	v_fma_f32 v26, v26, v25, v25
	v_mul_f32_e32 v26, 0x3f4c422a, v26
	v_mul_f32_e32 v26, -2.0, v26
	v_mul_f32_e32 v26, 0x3fb8aa3b, v26
	v_exp_f32_e32 v26, v26
	v_mul_f32_e32 v23, v27, v31
	v_add_f32_e32 v26, 1.0, v26
	v_and_b32_e32 v28, 0xffff0000, v10
	v_mul_f32_e32 v10, 0x3d372713, v28
	v_rcp_f32_e32 v30, v26
	v_mul_f32_e32 v10, v10, v28
	v_fma_f32 v10, v10, v28, v28
	v_mul_f32_e32 v10, 0x3f4c422a, v10
	v_mul_f32_e32 v10, -2.0, v10
	v_mul_f32_e32 v10, 0x3fb8aa3b, v10
	v_exp_f32_e32 v10, v10
	s_nop 0
	v_add_f32_e32 v29, 1.0, v10
	v_mul_f32_e32 v10, v25, v30
	v_rcp_f32_e32 v32, v29
	v_lshlrev_b32_e32 v26, 16, v11
	v_mul_f32_e32 v27, 0x3d372713, v26
	v_mul_f32_e32 v27, v27, v26
	v_fma_f32 v27, v27, v26, v26
	v_mul_f32_e32 v27, 0x3f4c422a, v27
	v_mul_f32_e32 v27, -2.0, v27
	v_mul_f32_e32 v27, 0x3fb8aa3b, v27
	v_exp_f32_e32 v27, v27
	v_mul_f32_e32 v24, v28, v32
	v_add_f32_e32 v27, 1.0, v27
	v_and_b32_e32 v29, 0xffff0000, v11
	v_mul_f32_e32 v11, 0x3d372713, v29
	v_rcp_f32_e32 v31, v27
	v_mul_f32_e32 v11, v11, v29
	v_fma_f32 v11, v11, v29, v29
	v_mul_f32_e32 v11, 0x3f4c422a, v11
	v_mul_f32_e32 v11, -2.0, v11
	v_mul_f32_e32 v11, 0x3fb8aa3b, v11
	v_exp_f32_e32 v11, v11
	s_nop 0
	v_add_f32_e32 v30, 1.0, v11
	v_mul_f32_e32 v11, v26, v31
	v_rcp_f32_e32 v33, v30
	s_waitcnt vmcnt(0)
	v_lshlrev_b32_e32 v27, 16, v4
	v_mul_f32_e32 v28, 0x3d372713, v27
	v_mul_f32_e32 v28, v28, v27
	v_fma_f32 v28, v28, v27, v27
	v_mul_f32_e32 v28, 0x3f4c422a, v28
	v_mul_f32_e32 v28, -2.0, v28
	v_mul_f32_e32 v28, 0x3fb8aa3b, v28
	v_exp_f32_e32 v28, v28
	v_mul_f32_e32 v25, v29, v33
	v_add_f32_e32 v28, 1.0, v28
	v_and_b32_e32 v30, 0xffff0000, v4
	v_mul_f32_e32 v4, 0x3d372713, v30
	v_rcp_f32_e32 v32, v28
	v_mul_f32_e32 v4, v4, v30
	v_fma_f32 v4, v4, v30, v30
	v_mul_f32_e32 v4, 0x3f4c422a, v4
	v_mul_f32_e32 v4, -2.0, v4
	v_mul_f32_e32 v4, 0x3fb8aa3b, v4
	v_exp_f32_e32 v4, v4
	s_nop 0
	v_add_f32_e32 v31, 1.0, v4
	v_mul_f32_e32 v4, v27, v32
	v_rcp_f32_e32 v34, v31
	v_lshlrev_b32_e32 v28, 16, v5
	v_mul_f32_e32 v29, 0x3d372713, v28
	v_mul_f32_e32 v29, v29, v28
	v_fma_f32 v29, v29, v28, v28
	v_mul_f32_e32 v29, 0x3f4c422a, v29
	v_mul_f32_e32 v29, -2.0, v29
	v_mul_f32_e32 v29, 0x3fb8aa3b, v29
	v_exp_f32_e32 v29, v29
	v_mul_f32_e32 v26, v30, v34
	v_add_f32_e32 v29, 1.0, v29
	v_and_b32_e32 v31, 0xffff0000, v5
	v_mul_f32_e32 v5, 0x3d372713, v31
	v_rcp_f32_e32 v33, v29
	v_mul_f32_e32 v5, v5, v31
	v_fma_f32 v5, v5, v31, v31
	v_mul_f32_e32 v5, 0x3f4c422a, v5
	v_mul_f32_e32 v5, -2.0, v5
	v_mul_f32_e32 v5, 0x3fb8aa3b, v5
	v_exp_f32_e32 v5, v5
	s_nop 0
	v_add_f32_e32 v32, 1.0, v5
	v_mul_f32_e32 v5, v28, v33
	v_rcp_f32_e32 v35, v32
	v_lshlrev_b32_e32 v29, 16, v6
	v_mul_f32_e32 v30, 0x3d372713, v29
	v_mul_f32_e32 v30, v30, v29
	v_fma_f32 v30, v30, v29, v29
	v_mul_f32_e32 v30, 0x3f4c422a, v30
	v_mul_f32_e32 v30, -2.0, v30
	v_mul_f32_e32 v30, 0x3fb8aa3b, v30
	v_exp_f32_e32 v30, v30
	v_mul_f32_e32 v27, v31, v35
	v_add_f32_e32 v30, 1.0, v30
	v_and_b32_e32 v32, 0xffff0000, v6
	v_mul_f32_e32 v6, 0x3d372713, v32
	v_rcp_f32_e32 v34, v30
	v_mul_f32_e32 v6, v6, v32
	v_fma_f32 v6, v6, v32, v32
	v_mul_f32_e32 v6, 0x3f4c422a, v6
	v_mul_f32_e32 v6, -2.0, v6
	v_mul_f32_e32 v6, 0x3fb8aa3b, v6
	v_exp_f32_e32 v6, v6
	s_nop 0
	v_add_f32_e32 v33, 1.0, v6
	v_mul_f32_e32 v6, v29, v34
	v_rcp_f32_e32 v36, v33
	v_lshlrev_b32_e32 v30, 16, v7
	v_mul_f32_e32 v31, 0x3d372713, v30
	v_mul_f32_e32 v31, v31, v30
	v_fma_f32 v31, v31, v30, v30
	v_mul_f32_e32 v31, 0x3f4c422a, v31
	v_mul_f32_e32 v31, -2.0, v31
	v_mul_f32_e32 v31, 0x3fb8aa3b, v31
	v_exp_f32_e32 v31, v31
	v_mul_f32_e32 v28, v32, v36
	v_add_f32_e32 v31, 1.0, v31
	v_and_b32_e32 v33, 0xffff0000, v7
	v_mul_f32_e32 v7, 0x3d372713, v33
	v_rcp_f32_e32 v35, v31
	v_mul_f32_e32 v7, v7, v33
	v_fma_f32 v7, v7, v33, v33
	v_mul_f32_e32 v7, 0x3f4c422a, v7
	v_mul_f32_e32 v7, -2.0, v7
	v_mul_f32_e32 v7, 0x3fb8aa3b, v7
	v_exp_f32_e32 v7, v7
	s_nop 0
	v_add_f32_e32 v34, 1.0, v7
	v_mul_f32_e32 v7, v30, v35
	v_rcp_f32_e32 v37, v34
	v_lshlrev_b32_e32 v31, 16, v0
	v_mul_f32_e32 v32, 0x3d372713, v31
	v_mul_f32_e32 v32, v32, v31
	v_fma_f32 v32, v32, v31, v31
	v_mul_f32_e32 v32, 0x3f4c422a, v32
	v_mul_f32_e32 v32, -2.0, v32
	v_mul_f32_e32 v32, 0x3fb8aa3b, v32
	v_exp_f32_e32 v32, v32
	v_mul_f32_e32 v29, v33, v37
	v_add_f32_e32 v32, 1.0, v32
	v_and_b32_e32 v34, 0xffff0000, v0
	v_mul_f32_e32 v0, 0x3d372713, v34
	v_rcp_f32_e32 v36, v32
	v_mul_f32_e32 v0, v0, v34
	v_fma_f32 v0, v0, v34, v34
	v_mul_f32_e32 v0, 0x3f4c422a, v0
	v_mul_f32_e32 v0, -2.0, v0
	v_mul_f32_e32 v0, 0x3fb8aa3b, v0
	v_exp_f32_e32 v0, v0
	s_nop 0
	v_add_f32_e32 v35, 1.0, v0
	v_mul_f32_e32 v0, v31, v36
	v_rcp_f32_e32 v38, v35
	v_lshlrev_b32_e32 v32, 16, v1
	v_mul_f32_e32 v33, 0x3d372713, v32
	v_mul_f32_e32 v33, v33, v32
	v_fma_f32 v33, v33, v32, v32
	v_mul_f32_e32 v33, 0x3f4c422a, v33
	v_mul_f32_e32 v33, -2.0, v33
	v_mul_f32_e32 v33, 0x3fb8aa3b, v33
	v_exp_f32_e32 v33, v33
	v_mul_f32_e32 v30, v34, v38
	v_add_f32_e32 v33, 1.0, v33
	v_and_b32_e32 v35, 0xffff0000, v1
	v_mul_f32_e32 v1, 0x3d372713, v35
	v_rcp_f32_e32 v37, v33
	v_mul_f32_e32 v1, v1, v35
	v_fma_f32 v1, v1, v35, v35
	v_mul_f32_e32 v1, 0x3f4c422a, v1
	v_mul_f32_e32 v1, -2.0, v1
	v_mul_f32_e32 v1, 0x3fb8aa3b, v1
	v_exp_f32_e32 v1, v1
	s_nop 0
	v_add_f32_e32 v36, 1.0, v1
	v_mul_f32_e32 v1, v32, v37
	v_rcp_f32_e32 v39, v36
	v_lshlrev_b32_e32 v33, 16, v2
	v_mul_f32_e32 v34, 0x3d372713, v33
	v_mul_f32_e32 v34, v34, v33
	v_fma_f32 v34, v34, v33, v33
	v_mul_f32_e32 v34, 0x3f4c422a, v34
	v_mul_f32_e32 v34, -2.0, v34
	v_mul_f32_e32 v34, 0x3fb8aa3b, v34
	v_exp_f32_e32 v34, v34
	v_mul_f32_e32 v31, v35, v39
	v_add_f32_e32 v34, 1.0, v34
	v_and_b32_e32 v36, 0xffff0000, v2
	v_mul_f32_e32 v2, 0x3d372713, v36
	v_rcp_f32_e32 v38, v34
	v_mul_f32_e32 v2, v2, v36
	v_fma_f32 v2, v2, v36, v36
	v_mul_f32_e32 v2, 0x3f4c422a, v2
	v_mul_f32_e32 v2, -2.0, v2
	v_mul_f32_e32 v2, 0x3fb8aa3b, v2
	v_exp_f32_e32 v2, v2
	s_nop 0
	v_add_f32_e32 v37, 1.0, v2
	v_rcp_f32_e32 v40, v37
	v_mul_f32_e32 v2, v33, v38
	v_lshlrev_b32_e32 v34, 16, v3
	v_mul_f32_e32 v35, 0x3d372713, v34
	v_mul_f32_e32 v35, v35, v34
	v_fma_f32 v35, v35, v34, v34
	v_mul_f32_e32 v35, 0x3f4c422a, v35
	v_mul_f32_e32 v35, -2.0, v35
	v_mul_f32_e32 v35, 0x3fb8aa3b, v35
	v_exp_f32_e32 v35, v35
	v_mul_f32_e32 v32, v36, v40
	v_and_b32_e32 v3, 0xffff0000, v3
	v_mov_b32_e32 v56, v32
	v_mul_f32_e32 v36, 0x3d372713, v3
	v_add_f32_e32 v35, 1.0, v35
	v_mul_f32_e32 v36, v36, v3
	v_fma_f32 v36, v36, v3, v3
	v_rcp_f32_e32 v39, v35
	v_mul_f32_e32 v36, 0x3f4c422a, v36
	v_mul_f32_e32 v36, -2.0, v36
	v_mul_f32_e32 v36, 0x3fb8aa3b, v36
	v_exp_f32_e32 v36, v36
	s_nop 0
	v_add_f32_e32 v36, 1.0, v36
	v_rcp_f32_e32 v38, v36
	v_mul_f32_e32 v32, v34, v39
	v_mov_b32_e32 v57, v32
	v_mul_f32_e32 v40, v13, v13
	v_mul_f32_e32 v32, v3, v38
	v_mov_b32_e32 v3, v32
	v_or_b32_e32 v32, s18, v76
	v_lshlrev_b32_e32 v58, 2, v32
	global_load_dwordx4 v[32:35], v58, s[28:29] offset:2048
	global_load_dwordx4 v[36:39], v58, s[28:29] offset:2064
	v_fmac_f32_e32 v40, v19, v19
	v_fmac_f32_e32 v40, v12, v12
	v_fmac_f32_e32 v40, v18, v18
	v_fmac_f32_e32 v40, v14, v14
	v_fmac_f32_e32 v40, v20, v20
	v_fmac_f32_e32 v40, v15, v15
	v_fmac_f32_e32 v40, v21, v21
	v_fmac_f32_e32 v40, v8, v8
	v_fmac_f32_e32 v40, v22, v22
	v_fmac_f32_e32 v40, v9, v9
	v_fmac_f32_e32 v40, v23, v23
	v_fmac_f32_e32 v40, v10, v10
	v_fmac_f32_e32 v40, v24, v24
	v_fmac_f32_e32 v40, v11, v11
	v_fmac_f32_e32 v40, v25, v25
	v_fmac_f32_e32 v40, v4, v4
	v_fmac_f32_e32 v40, v26, v26
	v_fmac_f32_e32 v40, v5, v5
	v_fmac_f32_e32 v40, v27, v27
	v_fmac_f32_e32 v40, v6, v6
	v_fmac_f32_e32 v40, v28, v28
	v_fmac_f32_e32 v40, v7, v7
	v_fmac_f32_e32 v40, v29, v29
	v_fmac_f32_e32 v40, v0, v0
	v_fmac_f32_e32 v40, v30, v30
	v_fmac_f32_e32 v40, v1, v1
	v_fmac_f32_e32 v40, v31, v31
	v_fmac_f32_e32 v40, v2, v2
	v_fmac_f32_e32 v40, v56, v56
	v_cmp_lt_i32_e32 vcc, v133, v134
	v_fmac_f32_e32 v40, v57, v57
	v_fmac_f32_e32 v40, v3, v3
	v_cndmask_b32_e32 v41, v104, v133, vcc
	v_lshlrev_b32_e32 v41, 2, v41
	ds_bpermute_b32 v41, v41, v40
	v_cmp_lt_i32_e32 vcc, v135, v134
	s_and_b32 s10, s43, 0x7fffffc
	s_add_i32 s10, s10, s35
	v_lshl_or_b32 v98, s10, 5, v109
	s_waitcnt lgkmcnt(0)
	v_add_f32_e32 v44, v40, v41
	v_cndmask_b32_e32 v40, v104, v135, vcc
	v_lshlrev_b32_e32 v45, 2, v40
	ds_bpermute_b32 v45, v45, v44
	global_load_dwordx4 v[40:43], v58, s[28:29] offset:2080
	v_ashrrev_i32_e32 v99, 31, v98
	s_waitcnt lgkmcnt(0)
	v_add_f32_e32 v44, v44, v45
	v_fmamk_f32 v44, v44, 0x3c000000, v136
	v_mul_f32_e32 v45, 0x4f800000, v44
	v_cmp_gt_f32_e32 vcc, s41, v44
	s_nop 1
	v_cndmask_b32_e32 v48, v44, v45, vcc
	v_sqrt_f32_e32 v49, v48
	global_load_dwordx4 v[44:47], v58, s[28:29] offset:2096
	v_add_u32_e32 v50, -1, v49
	v_fma_f32 v51, -v50, v49, v48
	v_cmp_ge_f32_e64 s[8:9], 0, v51
	v_add_u32_e32 v51, 1, v49
	s_nop 0
	v_cndmask_b32_e64 v50, v49, v50, s[8:9]
	v_fma_f32 v49, -v51, v49, v48
	v_cmp_lt_f32_e64 s[8:9], 0, v49
	s_nop 1
	v_cndmask_b32_e64 v49, v50, v51, s[8:9]
	v_mul_f32_e32 v50, 0x37800000, v49
	v_cndmask_b32_e32 v49, v49, v50, vcc
	v_cmp_class_f32_e32 vcc, v48, v137
	s_nop 1
	v_cndmask_b32_e32 v52, v49, v48, vcc
	v_rcp_f32_e32 v54, v52
	global_load_dwordx4 v[48:51], v58, s[28:29] offset:2112
	v_mul_f32_e32 v53, 1.0, v54
	v_mov_b32_e32 v59, v53
	v_mul_f32_e32 v12, v12, v59
	s_waitcnt vmcnt(4)
	v_mul_f32_e32 v12, v34, v12
	v_cvt_pk_bf16_f32 v12, v12, v12
	ds_write_b16 v138, v12 offset:35360
	v_mul_f32_e32 v12, v18, v59
	v_mul_f32_e32 v12, v35, v12
	v_mul_f32_e32 v19, v19, v59
	v_mul_f32_e32 v13, v13, v59
	v_cvt_pk_bf16_f32 v12, v12, v12
	v_mul_f32_e32 v19, v32, v19
	v_mul_f32_e32 v13, v33, v13
	ds_write_b16 v138, v12 offset:35632
	v_mul_f32_e32 v12, v14, v59
	global_load_dwordx4 v[32:35], v58, s[28:29] offset:2144
	s_waitcnt vmcnt(4)
	v_mul_f32_e32 v12, v36, v12
	v_cvt_pk_bf16_f32 v12, v12, v12
	ds_write_b16 v138, v12 offset:35904
	v_mul_f32_e32 v12, v20, v59
	v_mul_f32_e32 v12, v37, v12
	global_load_dwordx4 v[52:55], v58, s[28:29] offset:2128
	v_cvt_pk_bf16_f32 v12, v12, v12
	ds_write_b16 v138, v12 offset:36176
	v_mul_f32_e32 v12, v15, v59
	v_mul_f32_e32 v12, v38, v12
	v_cvt_pk_bf16_f32 v12, v12, v12
	ds_write_b16 v138, v12 offset:36448
	v_mul_f32_e32 v12, v21, v59
	v_mul_f32_e32 v12, v39, v12
	v_cvt_pk_bf16_f32 v13, v13, v13
	v_cvt_pk_bf16_f32 v12, v12, v12
	ds_write_b16 v138, v13 offset:35088
	ds_write_b16 v138, v12 offset:36720
	global_load_dwordx4 v[12:15], v58, s[28:29] offset:2160
	v_mul_f32_e32 v4, v4, v59
	v_mul_f32_e32 v0, v0, v59
	v_mul_f32_e32 v8, v8, v59
	s_waitcnt vmcnt(5)
	v_mul_f32_e32 v8, v40, v8
	v_cvt_pk_bf16_f32 v8, v8, v8
	ds_write_b16 v138, v8 offset:36992
	v_mul_f32_e32 v8, v22, v59
	v_add_u32_e32 v20, s44, v118
	v_mul_f32_e32 v8, v41, v8
	v_mad_i64_i32 v[20:21], s[8:9], v20, s40, v[16:17]
	v_cvt_pk_bf16_f32 v8, v8, v8
	v_lshl_add_u64 v[20:21], v[20:21], 0, s[24:25]
	ds_write_b16 v138, v8 offset:37264
	v_mul_f32_e32 v8, v9, v59
	v_lshl_add_u64 v[20:21], v[20:21], 0, v[84:85]
	v_mul_f32_e32 v8, v42, v8
	v_cvt_pk_bf16_f32 v8, v8, v8
	ds_write_b16 v138, v8 offset:37536
	v_mul_f32_e32 v8, v23, v59
	v_mul_f32_e32 v8, v43, v8
	v_cvt_pk_bf16_f32 v8, v8, v8
	ds_write_b16 v138, v8 offset:37808
	v_mul_f32_e32 v8, v10, v59
	s_waitcnt vmcnt(4)
	v_mul_f32_e32 v8, v44, v8
	v_cvt_pk_bf16_f32 v8, v8, v8
	ds_write_b16 v138, v8 offset:38080
	v_mul_f32_e32 v8, v24, v59
	v_mul_f32_e32 v8, v45, v8
	v_cvt_pk_bf16_f32 v8, v8, v8
	ds_write_b16 v138, v8 offset:38352
	v_mul_f32_e32 v8, v11, v59
	v_mul_f32_e32 v8, v46, v8
	v_cvt_pk_bf16_f32 v8, v8, v8
	s_waitcnt vmcnt(3)
	v_mul_f32_e32 v4, v4, v48
	v_cvt_pk_bf16_f32 v4, v4, v4
	ds_write_b16 v138, v4 offset:39168
	v_mul_f32_e32 v4, v26, v59
	v_mul_f32_e32 v4, v4, v49
	v_cvt_pk_bf16_f32 v4, v4, v4
	ds_write_b16 v138, v4 offset:39440
	v_mul_f32_e32 v4, v5, v59
	v_mul_f32_e32 v4, v4, v50
	v_cvt_pk_bf16_f32 v4, v4, v4
	ds_write_b16 v138, v4 offset:39712
	v_mul_f32_e32 v4, v27, v59
	v_mul_f32_e32 v4, v4, v51
	v_cvt_pk_bf16_f32 v4, v4, v4
	ds_write_b16 v138, v4 offset:39984
	v_mul_f32_e32 v4, v6, v59
	v_lshl_add_u64 v[26:27], v[20:21], 0, s[22:23]
	v_add_u32_e32 v20, s44, v119
	v_mad_i64_i32 v[20:21], s[8:9], v20, s40, v[16:17]
	v_lshl_add_u64 v[20:21], v[20:21], 0, s[24:25]
	v_lshl_add_u64 v[20:21], v[20:21], 0, v[84:85]
	ds_write_b16 v138, v8 offset:38624
	v_mul_f32_e32 v8, v25, v59
	v_mul_f32_e32 v8, v8, v47
	v_cvt_pk_bf16_f32 v19, v19, v19
	s_waitcnt vmcnt(2)
	v_mul_f32_e32 v0, v0, v32
	v_cvt_pk_bf16_f32 v0, v0, v0
	ds_write_b16 v138, v0 offset:41344
	v_mul_f32_e32 v0, v30, v59
	v_mul_f32_e32 v0, v0, v33
	v_cvt_pk_bf16_f32 v0, v0, v0
	s_waitcnt vmcnt(1)
	v_mul_f32_e32 v4, v4, v52
	ds_write_b16 v138, v0 offset:41616
	v_mul_f32_e32 v0, v1, v59
	v_cvt_pk_bf16_f32 v4, v4, v4
	v_mul_f32_e32 v0, v0, v34
	ds_write_b16 v138, v4 offset:40256
	v_mul_f32_e32 v4, v28, v59
	v_cvt_pk_bf16_f32 v0, v0, v0
	v_mul_f32_e32 v4, v4, v53
	ds_write_b16 v138, v0 offset:41888
	v_mul_f32_e32 v0, v31, v59
	v_cvt_pk_bf16_f32 v4, v4, v4
	v_mul_f32_e32 v0, v0, v35
	ds_write_b16 v138, v4 offset:40528
	v_mul_f32_e32 v4, v7, v59
	v_cvt_pk_bf16_f32 v0, v0, v0
	v_mul_f32_e32 v4, v4, v54
	ds_write_b16 v138, v0 offset:42160
	v_mul_f32_e32 v0, v2, v59
	v_cvt_pk_bf16_f32 v4, v4, v4
	s_waitcnt vmcnt(0)
	v_mul_f32_e32 v0, v0, v12
	ds_write_b16 v138, v4 offset:40800
	v_mul_f32_e32 v4, v29, v59
	v_cvt_pk_bf16_f32 v0, v0, v0
	v_lshl_add_u64 v[28:29], v[20:21], 0, s[22:23]
	v_add_u32_e32 v20, s44, v120
	ds_write_b16 v138, v0 offset:42432
	v_mul_f32_e32 v0, v56, v59
	v_mad_i64_i32 v[20:21], s[8:9], v20, s40, v[16:17]
	v_mul_f32_e32 v0, v0, v13
	v_lshl_add_u64 v[20:21], v[20:21], 0, s[24:25]
	v_cvt_pk_bf16_f32 v0, v0, v0
	v_lshl_add_u64 v[20:21], v[20:21], 0, v[84:85]
	ds_write_b16 v138, v0 offset:42704
	v_mul_f32_e32 v0, v57, v59
	v_lshl_add_u64 v[30:31], v[20:21], 0, s[22:23]
	v_add_u32_e32 v20, s44, v121
	v_mul_f32_e32 v0, v0, v14
	v_mad_i64_i32 v[20:21], s[8:9], v20, s40, v[16:17]
	v_cvt_pk_bf16_f32 v0, v0, v0
	v_lshl_add_u64 v[20:21], v[20:21], 0, s[24:25]
	ds_write_b16 v138, v0 offset:42976
	v_mul_f32_e32 v0, v3, v59
	v_lshl_add_u64 v[20:21], v[20:21], 0, v[84:85]
	v_mul_f32_e32 v0, v0, v15
	v_lshl_add_u64 v[48:49], v[20:21], 0, s[22:23]
	v_add_u32_e32 v20, s44, v123
	v_cvt_pk_bf16_f32 v0, v0, v0
	v_mad_i64_i32 v[20:21], s[8:9], v20, s40, v[16:17]
	ds_write_b16 v138, v0 offset:43248
	v_add_u32_e32 v0, s18, v110
	v_lshl_add_u64 v[20:21], v[20:21], 0, s[24:25]
	v_mul_f32_e32 v4, v4, v55
	v_ashrrev_i32_e32 v1, 31, v0
	v_lshl_add_u64 v[20:21], v[20:21], 0, v[84:85]
	ds_write_b16 v138, v19 offset:34816
	v_cvt_pk_bf16_f32 v8, v8, v8
	ds_write_b16 v138, v8 offset:38896
	v_cvt_pk_bf16_f32 v4, v4, v4
	ds_write_b16 v138, v4 offset:41072
	v_lshl_add_u64 v[0:1], v[0:1], 2, s[26:27]
	v_lshl_add_u64 v[50:51], v[20:21], 0, s[22:23]
	v_add_u32_e32 v20, s44, v124
	global_load_dwordx4 v[44:47], v[0:1], off offset:2048
	global_load_dwordx4 v[40:43], v[0:1], off offset:2080
	v_mad_i64_i32 v[20:21], s[8:9], v20, s40, v[16:17]
	v_lshl_add_u64 v[20:21], v[20:21], 0, s[24:25]
	v_add_u32_e32 v2, s44, v110
	v_lshl_add_u64 v[20:21], v[20:21], 0, v[84:85]
	v_mad_i64_i32 v[2:3], s[8:9], v2, s40, v[16:17]
	v_add_u32_e32 v4, s44, v111
	v_add_u32_e32 v6, s44, v112
	v_add_u32_e32 v8, s44, v113
	v_add_u32_e32 v10, s44, v114
	v_add_u32_e32 v12, s44, v115
	v_add_u32_e32 v14, s44, v116
	v_add_u32_e32 v18, s44, v117
	global_load_dwordx4 v[36:39], v[0:1], off offset:2112
	global_load_dwordx4 v[32:35], v[0:1], off offset:2144
	v_add_u32_e32 v0, s44, v122
	v_lshl_add_u64 v[52:53], v[20:21], 0, s[22:23]
	v_add_u32_e32 v20, s44, v125
	v_lshl_add_u64 v[2:3], v[2:3], 0, s[24:25]
	v_mad_i64_i32 v[4:5], s[8:9], v4, s40, v[16:17]
	v_mad_i64_i32 v[6:7], s[8:9], v6, s40, v[16:17]
	v_mad_i64_i32 v[8:9], s[8:9], v8, s40, v[16:17]
	v_mad_i64_i32 v[10:11], s[8:9], v10, s40, v[16:17]
	v_mad_i64_i32 v[12:13], s[8:9], v12, s40, v[16:17]
	v_mad_i64_i32 v[14:15], s[8:9], v14, s40, v[16:17]
	v_mad_i64_i32 v[18:19], s[8:9], v18, s40, v[16:17]
	v_mad_i64_i32 v[0:1], s[8:9], v0, s40, v[16:17]
	v_mad_i64_i32 v[16:17], s[8:9], v20, s40, v[16:17]
	v_lshl_add_u64 v[2:3], v[2:3], 0, v[84:85]
	v_lshl_add_u64 v[4:5], v[4:5], 0, s[24:25]
	v_lshl_add_u64 v[6:7], v[6:7], 0, s[24:25]
	v_lshl_add_u64 v[8:9], v[8:9], 0, s[24:25]
	v_lshl_add_u64 v[10:11], v[10:11], 0, s[24:25]
	v_lshl_add_u64 v[12:13], v[12:13], 0, s[24:25]
	v_lshl_add_u64 v[14:15], v[14:15], 0, s[24:25]
	v_lshl_add_u64 v[18:19], v[18:19], 0, s[24:25]
	v_lshl_add_u64 v[0:1], v[0:1], 0, s[24:25]
	v_lshl_add_u64 v[16:17], v[16:17], 0, s[24:25]
	v_lshl_add_u64 v[2:3], v[2:3], 0, s[22:23]
	v_lshl_add_u64 v[4:5], v[4:5], 0, v[84:85]
	v_lshl_add_u64 v[6:7], v[6:7], 0, v[84:85]
	v_lshl_add_u64 v[8:9], v[8:9], 0, v[84:85]
	v_lshl_add_u64 v[10:11], v[10:11], 0, v[84:85]
	v_lshl_add_u64 v[12:13], v[12:13], 0, v[84:85]
	v_lshl_add_u64 v[14:15], v[14:15], 0, v[84:85]
	v_lshl_add_u64 v[18:19], v[18:19], 0, v[84:85]
	v_lshl_add_u64 v[0:1], v[0:1], 0, v[84:85]
	v_lshl_add_u64 v[16:17], v[16:17], 0, v[84:85]
	v_lshl_add_u64 v[4:5], v[4:5], 0, s[22:23]
	v_lshl_add_u64 v[6:7], v[6:7], 0, s[22:23]
	v_lshl_add_u64 v[8:9], v[8:9], 0, s[22:23]
	v_lshl_add_u64 v[10:11], v[10:11], 0, s[22:23]
	v_lshl_add_u64 v[12:13], v[12:13], 0, s[22:23]
	v_lshl_add_u64 v[14:15], v[14:15], 0, s[22:23]
	v_lshl_add_u64 v[18:19], v[18:19], 0, s[22:23]
	v_lshl_add_u64 v[0:1], v[0:1], 0, s[22:23]
	v_lshl_add_u64 v[16:17], v[16:17], 0, s[22:23]
	global_load_ushort v25, v[2:3], off offset:2176
	global_load_ushort v90, v[4:5], off offset:2176
	global_load_ushort v91, v[6:7], off offset:2176
	global_load_ushort v92, v[8:9], off offset:2176
	global_load_ushort v149, v[8:9], off offset:2240
	global_load_ushort v150, v[6:7], off offset:2240
	global_load_ushort v151, v[4:5], off offset:2240
	global_load_ushort v152, v[2:3], off offset:2240
	global_load_ushort v93, v[10:11], off offset:2176
	global_load_ushort v94, v[12:13], off offset:2176
	global_load_ushort v95, v[14:15], off offset:2176
	global_load_ushort v96, v[18:19], off offset:2176
	global_load_ushort v145, v[18:19], off offset:2240
	global_load_ushort v146, v[14:15], off offset:2240
	global_load_ushort v147, v[12:13], off offset:2240
	global_load_ushort v148, v[10:11], off offset:2240
	global_load_ushort v97, v[26:27], off offset:2176
	global_load_ushort v100, v[28:29], off offset:2176
	global_load_ushort v101, v[30:31], off offset:2176
	global_load_ushort v24, v[48:49], off offset:2176
	global_load_ushort v141, v[48:49], off offset:2240
	global_load_ushort v142, v[30:31], off offset:2240
	global_load_ushort v143, v[28:29], off offset:2240
	global_load_ushort v144, v[26:27], off offset:2240
	global_load_ushort v23, v[0:1], off offset:2176
	global_load_ushort v22, v[50:51], off offset:2176
	global_load_ushort v21, v[52:53], off offset:2176
	global_load_ushort v20, v[16:17], off offset:2176
	global_load_ushort v78, v[16:17], off offset:2240
	global_load_ushort v83, v[52:53], off offset:2240
	global_load_ushort v85, v[50:51], off offset:2240
	global_load_ushort v140, v[0:1], off offset:2240
	s_waitcnt lgkmcnt(0)
	s_barrier
	ds_read_b128 v[16:19], v126
	ds_read_b128 v[0:3], v127 offset:34816
	ds_read_b128 v[72:75], v126 offset:32
	ds_read_b128 v[26:29], v127 offset:34848
	s_waitcnt lgkmcnt(2)
	v_mfma_f32_32x32x16_bf16 v[0:15], v[16:19], v[0:3], 0
	s_waitcnt vmcnt(31)
	v_lshlrev_b32_e32 v25, 16, v25
	s_waitcnt lgkmcnt(0)
	v_mfma_f32_32x32x16_bf16 v[0:15], v[72:75], v[26:29], v[0:15]
	ds_read_b128 v[68:71], v126 offset:64
	ds_read_b128 v[26:29], v127 offset:34880
	ds_read_b128 v[64:67], v126 offset:96
	ds_read_b128 v[48:51], v127 offset:34912
	v_mul_f32_e32 v30, 0x3d372713, v25
	v_mul_f32_e32 v30, v30, v25
	v_fma_f32 v30, v30, v25, v25
	v_mul_f32_e32 v30, 0x3f4c422a, v30
	v_mul_f32_e32 v30, -2.0, v30
	v_mul_f32_e32 v30, 0x3fb8aa3b, v30
	s_waitcnt lgkmcnt(2)
	v_mfma_f32_32x32x16_bf16 v[0:15], v[68:71], v[26:29], v[0:15]
	v_exp_f32_e32 v30, v30
	s_waitcnt vmcnt(12)
	v_lshlrev_b32_e32 v24, 16, v24
	s_waitcnt lgkmcnt(0)
	v_mfma_f32_32x32x16_bf16 v[0:15], v[64:67], v[48:51], v[0:15]
	ds_read_b128 v[60:63], v126 offset:128
	ds_read_b128 v[26:29], v127 offset:34944
	ds_read_b128 v[56:59], v126 offset:160
	ds_read_b128 v[48:51], v127 offset:34976
	s_waitcnt vmcnt(7)
	v_lshlrev_b32_e32 v23, 16, v23
	s_waitcnt vmcnt(6)
	v_lshlrev_b32_e32 v22, 16, v22
	s_waitcnt vmcnt(5)
	v_lshlrev_b32_e32 v21, 16, v21
	s_waitcnt lgkmcnt(2)
	v_mfma_f32_32x32x16_bf16 v[0:15], v[60:63], v[26:29], v[0:15]
	s_waitcnt lgkmcnt(0)
	v_mfma_f32_32x32x16_bf16 v[0:15], v[56:59], v[48:51], v[0:15]
	ds_read_b128 v[26:29], v127 offset:35008
	ds_read_b128 v[52:55], v126 offset:192
	ds_read_b128 v[48:51], v126 offset:224
	ds_read_b128 v[86:89], v127 offset:35040
	ds_read_b128 v[154:157], v128 offset:34848
	s_waitcnt lgkmcnt(3)
	v_mfma_f32_32x32x16_bf16 v[0:15], v[52:55], v[26:29], v[0:15]
	v_add_f32_e32 v26, 1.0, v30
	v_rcp_f32_e32 v28, v26
	s_nop 0
	s_waitcnt lgkmcnt(1)
	v_mfma_f32_32x32x16_bf16 v[0:15], v[48:51], v[86:89], v[0:15]
	v_mul_f32_e32 v27, v25, v28
	v_lshlrev_b32_e32 v28, 16, v90
	v_mov_b32_e32 v25, v27
	v_mul_f32_e32 v26, 0x3d372713, v28
	v_mul_f32_e32 v26, v26, v28
	v_fma_f32 v26, v26, v28, v28
	v_mul_f32_e32 v26, 0x3f4c422a, v26
	v_mul_f32_e32 v26, -2.0, v26
	v_mul_f32_e32 v26, 0x3fb8aa3b, v26
	v_exp_f32_e32 v26, v26
	s_nop 1
	v_add_f32_e32 v0, v44, v0
	v_mul_f32_e32 v0, v25, v0
	v_med3_f32 v0, v0, s42, v139
	v_mov_b32_e32 v25, v79
	v_cvt_pk_fp8_f32 v25, v0, 0
	v_add_f32_e32 v0, 1.0, v26
	v_rcp_f32_e32 v30, v0
	v_lshlrev_b64 v[86:87], 11, v[98:99]
	v_lshl_add_u64 v[26:27], v[80:81], 0, v[86:87]
	v_lshl_add_u64 v[26:27], v[26:27], 0, s[18:19]
	global_store_byte v[26:27], v25, off
	v_mul_f32_e32 v25, v28, v30
	v_mov_b32_e32 v0, v25
	v_add_f32_e32 v1, v45, v1
	v_mul_f32_e32 v0, v0, v1
	v_med3_f32 v0, v0, s42, v139
	v_mov_b32_e32 v25, v79
	v_lshlrev_b32_e32 v28, 16, v91
	v_cvt_pk_fp8_f32 v25, v0, 0
	v_mul_f32_e32 v0, 0x3d372713, v28
	v_mul_f32_e32 v0, v0, v28
	v_fma_f32 v0, v0, v28, v28
	v_mul_f32_e32 v0, 0x3f4c422a, v0
	v_mul_f32_e32 v0, -2.0, v0
	v_mul_f32_e32 v0, 0x3fb8aa3b, v0
	v_exp_f32_e32 v26, v0
	v_or_b32_e32 v0, 1, v98
	v_ashrrev_i32_e32 v1, 31, v0
	v_lshlrev_b64 v[0:1], 11, v[0:1]
	v_add_f32_e32 v29, 1.0, v26
	v_rcp_f32_e32 v31, v29
	v_lshl_add_u64 v[26:27], v[80:81], 0, v[0:1]
	v_lshl_add_u64 v[26:27], v[26:27], 0, s[18:19]
	global_store_byte v[26:27], v25, off
	v_mul_f32_e32 v25, v28, v31
	v_add_f32_e32 v2, v46, v2
	v_mul_f32_e32 v2, v25, v2
	v_med3_f32 v2, v2, s42, v139
	v_mov_b32_e32 v25, v79
	v_cvt_pk_fp8_f32 v25, v2, 0
	v_lshlrev_b32_e32 v2, 16, v92
	v_mul_f32_e32 v26, 0x3d372713, v2
	v_mul_f32_e32 v26, v26, v2
	v_fma_f32 v26, v26, v2, v2
	v_mul_f32_e32 v26, 0x3f4c422a, v26
	v_mul_f32_e32 v26, -2.0, v26
	v_mul_f32_e32 v26, 0x3fb8aa3b, v26
	v_exp_f32_e32 v28, v26
	v_or_b32_e32 v26, 2, v98
	v_ashrrev_i32_e32 v27, 31, v26
	v_lshlrev_b64 v[88:89], 11, v[26:27]
	v_add_f32_e32 v28, 1.0, v28
	v_rcp_f32_e32 v30, v28
	v_lshl_add_u64 v[26:27], v[80:81], 0, v[88:89]
	v_lshl_add_u64 v[26:27], v[26:27], 0, s[18:19]
	global_store_byte v[26:27], v25, off
	v_mul_f32_e32 v25, v2, v30
	v_mov_b32_e32 v2, v25
	v_add_f32_e32 v3, v47, v3
	v_mul_f32_e32 v2, v2, v3
	v_med3_f32 v2, v2, s42, v139
	v_mov_b32_e32 v25, v79
	v_lshlrev_b32_e32 v28, 16, v93
	v_cvt_pk_fp8_f32 v25, v2, 0
	v_mul_f32_e32 v2, 0x3d372713, v28
	v_mul_f32_e32 v2, v2, v28
	v_fma_f32 v2, v2, v28, v28
	v_mul_f32_e32 v2, 0x3f4c422a, v2
	v_mul_f32_e32 v2, -2.0, v2
	v_mul_f32_e32 v2, 0x3fb8aa3b, v2
	v_exp_f32_e32 v26, v2
	v_or_b32_e32 v2, 3, v98
	v_ashrrev_i32_e32 v3, 31, v2
	v_lshlrev_b64 v[2:3], 11, v[2:3]
	v_add_f32_e32 v29, 1.0, v26
	v_rcp_f32_e32 v31, v29
	v_lshl_add_u64 v[26:27], v[80:81], 0, v[2:3]
	v_lshl_add_u64 v[26:27], v[26:27], 0, s[18:19]
	global_store_byte v[26:27], v25, off
	v_mul_f32_e32 v25, v28, v31
	v_add_f32_e32 v4, v40, v4
	v_mul_f32_e32 v4, v25, v4
	v_med3_f32 v4, v4, s42, v139
	v_mov_b32_e32 v25, v79
	v_cvt_pk_fp8_f32 v25, v4, 0
	v_lshlrev_b32_e32 v4, 16, v94
	v_mul_f32_e32 v26, 0x3d372713, v4
	v_mul_f32_e32 v26, v26, v4
	v_fma_f32 v26, v26, v4, v4
	v_mul_f32_e32 v26, 0x3f4c422a, v26
	v_mul_f32_e32 v26, -2.0, v26
	v_mul_f32_e32 v26, 0x3fb8aa3b, v26
	v_exp_f32_e32 v28, v26
	v_or_b32_e32 v26, 8, v98
	v_ashrrev_i32_e32 v27, 31, v26
	v_lshlrev_b64 v[90:91], 11, v[26:27]
	v_add_f32_e32 v28, 1.0, v28
	v_rcp_f32_e32 v30, v28
	v_lshl_add_u64 v[26:27], v[80:81], 0, v[90:91]
	v_lshl_add_u64 v[26:27], v[26:27], 0, s[18:19]
	global_store_byte v[26:27], v25, off
	v_mul_f32_e32 v25, v4, v30
	v_mov_b32_e32 v4, v25
	v_add_f32_e32 v5, v41, v5
	v_mul_f32_e32 v4, v4, v5
	v_med3_f32 v4, v4, s42, v139
	v_mov_b32_e32 v25, v79
	v_lshlrev_b32_e32 v28, 16, v95
	v_cvt_pk_fp8_f32 v25, v4, 0
	v_mul_f32_e32 v4, 0x3d372713, v28
	v_mul_f32_e32 v4, v4, v28
	v_fma_f32 v4, v4, v28, v28
	v_mul_f32_e32 v4, 0x3f4c422a, v4
	v_mul_f32_e32 v4, -2.0, v4
	v_mul_f32_e32 v4, 0x3fb8aa3b, v4
	v_exp_f32_e32 v26, v4
	v_or_b32_e32 v4, 9, v98
	v_ashrrev_i32_e32 v5, 31, v4
	v_lshlrev_b64 v[4:5], 11, v[4:5]
	v_add_f32_e32 v29, 1.0, v26
	v_rcp_f32_e32 v31, v29
	v_lshl_add_u64 v[26:27], v[80:81], 0, v[4:5]
	v_lshl_add_u64 v[26:27], v[26:27], 0, s[18:19]
	global_store_byte v[26:27], v25, off
	v_mul_f32_e32 v25, v28, v31
	v_add_f32_e32 v6, v42, v6
	v_mul_f32_e32 v6, v25, v6
	v_med3_f32 v6, v6, s42, v139
	v_mov_b32_e32 v25, v79
	v_cvt_pk_fp8_f32 v25, v6, 0
	v_lshlrev_b32_e32 v6, 16, v96
	v_mul_f32_e32 v26, 0x3d372713, v6
	v_mul_f32_e32 v26, v26, v6
	v_fma_f32 v26, v26, v6, v6
	v_mul_f32_e32 v26, 0x3f4c422a, v26
	v_mul_f32_e32 v26, -2.0, v26
	v_mul_f32_e32 v26, 0x3fb8aa3b, v26
	v_exp_f32_e32 v28, v26
	v_or_b32_e32 v26, 10, v98
	v_ashrrev_i32_e32 v27, 31, v26
	v_lshlrev_b64 v[92:93], 11, v[26:27]
	v_add_f32_e32 v28, 1.0, v28
	v_rcp_f32_e32 v30, v28
	v_lshl_add_u64 v[26:27], v[80:81], 0, v[92:93]
	v_lshl_add_u64 v[26:27], v[26:27], 0, s[18:19]
	global_store_byte v[26:27], v25, off
	v_mul_f32_e32 v25, v6, v30
	v_mov_b32_e32 v6, v25
	v_add_f32_e32 v7, v43, v7
	v_mul_f32_e32 v6, v6, v7
	v_med3_f32 v6, v6, s42, v139
	v_mov_b32_e32 v25, v79
	v_lshlrev_b32_e32 v28, 16, v97
	v_cvt_pk_fp8_f32 v25, v6, 0
	v_mul_f32_e32 v6, 0x3d372713, v28
	v_mul_f32_e32 v6, v6, v28
	v_fma_f32 v6, v6, v28, v28
	v_mul_f32_e32 v6, 0x3f4c422a, v6
	v_mul_f32_e32 v6, -2.0, v6
	v_mul_f32_e32 v6, 0x3fb8aa3b, v6
	v_exp_f32_e32 v26, v6
	v_or_b32_e32 v6, 11, v98
	v_ashrrev_i32_e32 v7, 31, v6
	v_lshlrev_b64 v[6:7], 11, v[6:7]
	v_add_f32_e32 v29, 1.0, v26
	v_rcp_f32_e32 v31, v29
	v_lshl_add_u64 v[26:27], v[80:81], 0, v[6:7]
	v_lshl_add_u64 v[26:27], v[26:27], 0, s[18:19]
	global_store_byte v[26:27], v25, off
	v_mul_f32_e32 v25, v28, v31
	v_add_f32_e32 v8, v36, v8
	v_mul_f32_e32 v8, v25, v8
	v_med3_f32 v8, v8, s42, v139
	v_mov_b32_e32 v25, v79
	v_cvt_pk_fp8_f32 v25, v8, 0
	v_lshlrev_b32_e32 v8, 16, v100
	v_mul_f32_e32 v26, 0x3d372713, v8
	v_mul_f32_e32 v26, v26, v8
	v_fma_f32 v26, v26, v8, v8
	v_mul_f32_e32 v26, 0x3f4c422a, v26
	v_mul_f32_e32 v26, -2.0, v26
	v_mul_f32_e32 v26, 0x3fb8aa3b, v26
	v_exp_f32_e32 v28, v26
	v_or_b32_e32 v26, 16, v98
	v_ashrrev_i32_e32 v27, 31, v26
	v_lshlrev_b64 v[94:95], 11, v[26:27]
	v_add_f32_e32 v28, 1.0, v28
	v_rcp_f32_e32 v30, v28
	v_lshl_add_u64 v[26:27], v[80:81], 0, v[94:95]
	v_lshl_add_u64 v[26:27], v[26:27], 0, s[18:19]
	global_store_byte v[26:27], v25, off
	v_mul_f32_e32 v25, v8, v30
	v_mov_b32_e32 v8, v25
	v_add_f32_e32 v9, v37, v9
	v_mul_f32_e32 v8, v8, v9
	v_med3_f32 v8, v8, s42, v139
	v_mov_b32_e32 v25, v79
	v_lshlrev_b32_e32 v26, 16, v101
	v_cvt_pk_fp8_f32 v25, v8, 0
	v_mul_f32_e32 v8, 0x3d372713, v26
	v_mul_f32_e32 v8, v8, v26
	v_fma_f32 v8, v8, v26, v26
	v_mul_f32_e32 v8, 0x3f4c422a, v8
	v_mul_f32_e32 v8, -2.0, v8
	v_mul_f32_e32 v8, 0x3fb8aa3b, v8
	v_exp_f32_e32 v27, v8
	v_or_b32_e32 v8, 17, v98
	v_ashrrev_i32_e32 v9, 31, v8
	v_lshlrev_b64 v[96:97], 11, v[8:9]
	v_add_f32_e32 v27, 1.0, v27
	v_rcp_f32_e32 v29, v27
	v_lshl_add_u64 v[8:9], v[80:81], 0, v[96:97]
	v_lshl_add_u64 v[8:9], v[8:9], 0, s[18:19]
	global_store_byte v[8:9], v25, off
	v_mul_f32_e32 v8, v26, v29
	v_add_f32_e32 v9, v38, v10
	v_mul_f32_e32 v8, v8, v9
	v_med3_f32 v8, v8, s42, v139
	v_mov_b32_e32 v10, v79
	v_cvt_pk_fp8_f32 v10, v8, 0
	v_mul_f32_e32 v8, 0x3d372713, v24
	v_mul_f32_e32 v8, v8, v24
	v_fma_f32 v8, v8, v24, v24
	v_mul_f32_e32 v8, 0x3f4c422a, v8
	v_mul_f32_e32 v8, -2.0, v8
	v_mul_f32_e32 v8, 0x3fb8aa3b, v8
	v_exp_f32_e32 v25, v8
	v_or_b32_e32 v8, 18, v98
	v_ashrrev_i32_e32 v9, 31, v8
	v_lshlrev_b64 v[100:101], 11, v[8:9]
	v_add_f32_e32 v25, 1.0, v25
	v_rcp_f32_e32 v27, v25
	v_lshl_add_u64 v[8:9], v[80:81], 0, v[100:101]
	v_lshl_add_u64 v[8:9], v[8:9], 0, s[18:19]
	global_store_byte v[8:9], v10, off
	v_mul_f32_e32 v8, v24, v27
	v_add_f32_e32 v9, v39, v11
	v_mul_f32_e32 v8, v8, v9
	v_med3_f32 v8, v8, s42, v139
	v_mov_b32_e32 v24, v79
	v_cvt_pk_fp8_f32 v24, v8, 0
	v_mul_f32_e32 v8, 0x3d372713, v23
	v_mul_f32_e32 v8, v8, v23
	v_fma_f32 v8, v8, v23, v23
	v_mul_f32_e32 v8, 0x3f4c422a, v8
	v_mul_f32_e32 v8, -2.0, v8
	v_mul_f32_e32 v8, 0x3fb8aa3b, v8
	v_exp_f32_e32 v25, v8
	v_or_b32_e32 v8, 19, v98
	v_ashrrev_i32_e32 v9, 31, v8
	v_lshlrev_b64 v[10:11], 11, v[8:9]
	v_add_f32_e32 v25, 1.0, v25
	v_rcp_f32_e32 v27, v25
	v_lshl_add_u64 v[8:9], v[80:81], 0, v[10:11]
	v_lshl_add_u64 v[8:9], v[8:9], 0, s[18:19]
	global_store_byte v[8:9], v24, off
	v_mul_f32_e32 v8, v23, v27
	v_add_f32_e32 v9, v32, v12
	v_mul_f32_e32 v8, v8, v9
	v_med3_f32 v8, v8, s42, v139
	v_mov_b32_e32 v12, v79
	v_cvt_pk_fp8_f32 v12, v8, 0
	v_mul_f32_e32 v8, 0x3d372713, v22
	v_mul_f32_e32 v8, v8, v22
	v_fma_f32 v8, v8, v22, v22
	v_mul_f32_e32 v8, 0x3f4c422a, v8
	v_mul_f32_e32 v8, -2.0, v8
	v_mul_f32_e32 v8, 0x3fb8aa3b, v8
	v_exp_f32_e32 v23, v8
	v_or_b32_e32 v8, 24, v98
	v_ashrrev_i32_e32 v9, 31, v8
	v_lshlrev_b64 v[102:103], 11, v[8:9]
	v_add_f32_e32 v23, 1.0, v23
	v_rcp_f32_e32 v25, v23
	v_lshl_add_u64 v[8:9], v[80:81], 0, v[102:103]
	v_lshl_add_u64 v[8:9], v[8:9], 0, s[18:19]
	global_store_byte v[8:9], v12, off
	v_mul_f32_e32 v8, v22, v25
	v_add_f32_e32 v9, v33, v13
	v_mul_f32_e32 v8, v8, v9
	v_med3_f32 v8, v8, s42, v139
	v_mov_b32_e32 v22, v79
	v_cvt_pk_fp8_f32 v22, v8, 0
	v_mul_f32_e32 v8, 0x3d372713, v21
	v_mul_f32_e32 v8, v8, v21
	v_fma_f32 v8, v8, v21, v21
	v_mul_f32_e32 v8, 0x3f4c422a, v8
	v_mul_f32_e32 v8, -2.0, v8
	v_mul_f32_e32 v8, 0x3fb8aa3b, v8
	v_exp_f32_e32 v23, v8
	v_or_b32_e32 v8, 25, v98
	v_ashrrev_i32_e32 v9, 31, v8
	v_lshlrev_b64 v[12:13], 11, v[8:9]
	v_add_f32_e32 v23, 1.0, v23
	v_rcp_f32_e32 v25, v23
	v_lshl_add_u64 v[8:9], v[80:81], 0, v[12:13]
	v_lshl_add_u64 v[8:9], v[8:9], 0, s[18:19]
	global_store_byte v[8:9], v22, off
	v_mul_f32_e32 v8, v21, v25
	ds_read_b128 v[22:25], v128 offset:34816
	s_waitcnt vmcnt(18)
	v_lshlrev_b32_e32 v99, 16, v20
	v_mul_f32_e32 v20, 0x3d372713, v99
	v_mul_f32_e32 v153, v20, v99
	s_waitcnt lgkmcnt(0)
	v_mfma_f32_32x32x16_bf16 v[16:31], v[16:19], v[22:25], 0
	v_fma_f32 v153, v153, v99, v99
	v_mul_f32_e32 v153, 0x3f4c422a, v153
	v_mul_f32_e32 v153, -2.0, v153
	v_mul_f32_e32 v153, 0x3fb8aa3b, v153
	v_exp_f32_e32 v153, v153
	v_add_f32_e32 v9, v34, v14
	v_mul_f32_e32 v8, v8, v9
	v_mfma_f32_32x32x16_bf16 v[16:31], v[72:75], v[154:157], v[16:31]
	ds_read_b128 v[72:75], v128 offset:34880
	ds_read_b128 v[154:157], v128 offset:34912
	v_med3_f32 v8, v8, s42, v139
	v_mov_b32_e32 v14, v79
	v_add_f32_e32 v153, 1.0, v153
	v_cvt_pk_fp8_f32 v14, v8, 0
	v_or_b32_e32 v8, 26, v98
	s_waitcnt lgkmcnt(1)
	v_mfma_f32_32x32x16_bf16 v[16:31], v[68:71], v[72:75], v[16:31]
	v_ashrrev_i32_e32 v9, 31, v8
	v_rcp_f32_e32 v161, v153
	v_lshlrev_b64 v[8:9], 11, v[8:9]
	v_lshl_add_u64 v[158:159], v[80:81], 0, v[8:9]
	v_lshl_add_u64 v[158:159], v[158:159], 0, s[18:19]
	s_waitcnt lgkmcnt(0)
	v_mfma_f32_32x32x16_bf16 v[16:31], v[64:67], v[154:157], v[16:31]
	global_store_byte v[158:159], v14, off
	ds_read_b128 v[64:67], v128 offset:34944
	v_mul_f32_e32 v14, v99, v161
	ds_read_b128 v[68:71], v128 offset:34976
	s_waitcnt lgkmcnt(1)
	v_mfma_f32_32x32x16_bf16 v[16:31], v[60:63], v[64:67], v[16:31]
	v_lshlrev_b32_e32 v65, 16, v152
	v_mul_f32_e32 v60, 0x3d372713, v65
	v_mul_f32_e32 v60, v60, v65
	v_fma_f32 v60, v60, v65, v65
	v_mul_f32_e32 v60, 0x3f4c422a, v60
	v_mul_f32_e32 v60, -2.0, v60
	v_mul_f32_e32 v60, 0x3fb8aa3b, v60
	s_waitcnt lgkmcnt(0)
	v_mfma_f32_32x32x16_bf16 v[16:31], v[56:59], v[68:71], v[16:31]
	ds_read_b128 v[56:59], v128 offset:35008
	v_exp_f32_e32 v66, v60
	ds_read_b128 v[60:63], v128 offset:35040
	v_add_f32_e32 v15, v35, v15
	v_mul_f32_e32 v14, v14, v15
	v_med3_f32 v14, v14, s42, v139
	s_waitcnt lgkmcnt(1)
	v_mfma_f32_32x32x16_bf16 v[16:31], v[52:55], v[56:59], v[16:31]
	v_add_f32_e32 v54, 1.0, v66
	v_rcp_f32_e32 v56, v54
	v_mov_b32_e32 v64, v79
	v_cvt_pk_fp8_f32 v64, v14, 0
	v_or_b32_e32 v14, 27, v98
	s_waitcnt lgkmcnt(0)
	v_mfma_f32_32x32x16_bf16 v[16:31], v[48:51], v[60:63], v[16:31]
	v_mul_f32_e32 v48, v65, v56
	s_nop 2
	s_nop 7
	v_add_f32_e32 v16, v44, v16
	v_lshlrev_b32_e32 v44, 16, v151
	s_nop 0
	v_mul_f32_e32 v16, v48, v16
	v_mul_f32_e32 v48, 0x3d372713, v44
	v_mul_f32_e32 v48, v48, v44
	v_fma_f32 v48, v48, v44, v44
	v_mul_f32_e32 v48, 0x3f4c422a, v48
	v_mul_f32_e32 v48, -2.0, v48
	v_mul_f32_e32 v48, 0x3fb8aa3b, v48
	v_exp_f32_e32 v48, v48
	v_ashrrev_i32_e32 v15, 31, v14
	v_lshlrev_b64 v[14:15], 11, v[14:15]
	v_lshl_add_u64 v[52:53], v[80:81], 0, v[14:15]
	v_lshl_add_u64 v[52:53], v[52:53], 0, s[18:19]
	v_add_f32_e32 v51, 1.0, v48
	global_store_byte v[52:53], v64, off
	v_med3_f32 v16, v16, s42, v139
	v_mov_b32_e32 v50, v79
	v_cvt_pk_fp8_f32 v50, v16, 0
	v_rcp_f32_e32 v53, v51
	v_or_b32_e32 v16, s18, v129
	v_or_b32_e32 v86, v86, v16
	v_lshl_add_u64 v[48:49], s[20:21], 0, v[86:87]
	global_store_byte v[48:49], v50, off
	v_mul_f32_e32 v48, v44, v53
	v_mov_b32_e32 v44, v48
	v_add_f32_e32 v17, v45, v17
	v_mul_f32_e32 v17, v44, v17
	v_lshlrev_b32_e32 v44, 16, v150
	v_mul_f32_e32 v45, 0x3d372713, v44
	v_mul_f32_e32 v45, v45, v44
	v_fma_f32 v45, v45, v44, v44
	v_mul_f32_e32 v45, 0x3f4c422a, v45
	v_mul_f32_e32 v45, -2.0, v45
	v_mul_f32_e32 v45, 0x3fb8aa3b, v45
	v_exp_f32_e32 v45, v45
	v_med3_f32 v17, v17, s42, v139
	v_mov_b32_e32 v48, v79
	v_cvt_pk_fp8_f32 v48, v17, 0
	v_add_f32_e32 v17, 1.0, v45
	v_rcp_f32_e32 v49, v17
	v_or_b32_e32 v0, v0, v16
	v_lshl_add_u64 v[0:1], s[20:21], 0, v[0:1]
	global_store_byte v[0:1], v48, off
	v_mul_f32_e32 v0, v44, v49
	v_add_f32_e32 v1, v46, v18
	v_lshlrev_b32_e32 v17, 16, v149
	v_mul_f32_e32 v0, v0, v1
	v_mul_f32_e32 v1, 0x3d372713, v17
	v_mul_f32_e32 v1, v1, v17
	v_fma_f32 v1, v1, v17, v17
	v_mul_f32_e32 v1, 0x3f4c422a, v1
	v_mul_f32_e32 v1, -2.0, v1
	v_mul_f32_e32 v1, 0x3fb8aa3b, v1
	v_exp_f32_e32 v1, v1
	v_med3_f32 v0, v0, s42, v139
	v_mov_b32_e32 v18, v79
	v_cvt_pk_fp8_f32 v18, v0, 0
	v_add_f32_e32 v44, 1.0, v1
	v_rcp_f32_e32 v46, v44
	v_or_b32_e32 v88, v88, v16
	v_lshl_add_u64 v[0:1], s[20:21], 0, v[88:89]
	global_store_byte v[0:1], v18, off
	v_mul_f32_e32 v0, v17, v46
	v_add_f32_e32 v1, v47, v19
	v_lshlrev_b32_e32 v17, 16, v148
	v_mul_f32_e32 v0, v0, v1
	v_mul_f32_e32 v1, 0x3d372713, v17
	v_mul_f32_e32 v1, v1, v17
	v_fma_f32 v1, v1, v17, v17
	v_mul_f32_e32 v1, 0x3f4c422a, v1
	v_mul_f32_e32 v1, -2.0, v1
	v_mul_f32_e32 v1, 0x3fb8aa3b, v1
	v_exp_f32_e32 v1, v1
	v_med3_f32 v0, v0, s42, v139
	v_mov_b32_e32 v18, v79
	v_cvt_pk_fp8_f32 v18, v0, 0
	v_add_f32_e32 v19, 1.0, v1
	v_rcp_f32_e32 v45, v19
	v_or_b32_e32 v2, v2, v16
	v_lshl_add_u64 v[0:1], s[20:21], 0, v[2:3]
	global_store_byte v[0:1], v18, off
	v_mul_f32_e32 v0, v17, v45
	v_add_f32_e32 v1, v40, v20
	v_lshlrev_b32_e32 v2, 16, v147
	v_mul_f32_e32 v0, v0, v1
	v_mul_f32_e32 v1, 0x3d372713, v2
	v_mul_f32_e32 v1, v1, v2
	v_fma_f32 v1, v1, v2, v2
	v_mul_f32_e32 v1, 0x3f4c422a, v1
	v_mul_f32_e32 v1, -2.0, v1
	v_mul_f32_e32 v1, 0x3fb8aa3b, v1
	v_exp_f32_e32 v1, v1
	v_med3_f32 v0, v0, s42, v139
	v_mov_b32_e32 v3, v79
	v_cvt_pk_fp8_f32 v3, v0, 0
	v_add_f32_e32 v17, 1.0, v1
	v_rcp_f32_e32 v19, v17
	v_or_b32_e32 v90, v90, v16
	v_lshl_add_u64 v[0:1], s[20:21], 0, v[90:91]
	global_store_byte v[0:1], v3, off
	v_mul_f32_e32 v0, v2, v19
	v_add_f32_e32 v1, v41, v21
	v_lshlrev_b32_e32 v2, 16, v146
	v_mul_f32_e32 v0, v0, v1
	v_mul_f32_e32 v1, 0x3d372713, v2
	v_mul_f32_e32 v1, v1, v2
	v_fma_f32 v1, v1, v2, v2
	v_mul_f32_e32 v1, 0x3f4c422a, v1
	v_mul_f32_e32 v1, -2.0, v1
	v_mul_f32_e32 v1, 0x3fb8aa3b, v1
	v_exp_f32_e32 v1, v1
	v_med3_f32 v0, v0, s42, v139
	v_mov_b32_e32 v3, v79
	v_cvt_pk_fp8_f32 v3, v0, 0
	v_add_f32_e32 v17, 1.0, v1
	v_rcp_f32_e32 v19, v17
	v_or_b32_e32 v4, v4, v16
	v_lshl_add_u64 v[0:1], s[20:21], 0, v[4:5]
	global_store_byte v[0:1], v3, off
	v_mul_f32_e32 v0, v2, v19
	v_add_f32_e32 v1, v42, v22
	v_lshlrev_b32_e32 v2, 16, v145
	v_mul_f32_e32 v0, v0, v1
	v_mul_f32_e32 v1, 0x3d372713, v2
	v_mul_f32_e32 v1, v1, v2
	v_fma_f32 v1, v1, v2, v2
	v_mul_f32_e32 v1, 0x3f4c422a, v1
	v_mul_f32_e32 v1, -2.0, v1
	v_mul_f32_e32 v1, 0x3fb8aa3b, v1
	v_exp_f32_e32 v1, v1
	v_med3_f32 v0, v0, s42, v139
	v_mov_b32_e32 v3, v79
	v_cvt_pk_fp8_f32 v3, v0, 0
	v_add_f32_e32 v4, 1.0, v1
	v_rcp_f32_e32 v17, v4
	v_or_b32_e32 v92, v92, v16
	v_lshl_add_u64 v[0:1], s[20:21], 0, v[92:93]
	global_store_byte v[0:1], v3, off
	v_mul_f32_e32 v0, v2, v17
	v_add_f32_e32 v1, v43, v23
	v_lshlrev_b32_e32 v2, 16, v144
	v_mul_f32_e32 v0, v0, v1
	v_mul_f32_e32 v1, 0x3d372713, v2
	v_mul_f32_e32 v1, v1, v2
	v_fma_f32 v1, v1, v2, v2
	v_mul_f32_e32 v1, 0x3f4c422a, v1
	v_mul_f32_e32 v1, -2.0, v1
	v_mul_f32_e32 v1, 0x3fb8aa3b, v1
	v_exp_f32_e32 v1, v1
	v_med3_f32 v0, v0, s42, v139
	v_mov_b32_e32 v3, v79
	v_cvt_pk_fp8_f32 v3, v0, 0
	v_add_f32_e32 v4, 1.0, v1
	v_rcp_f32_e32 v17, v4
	v_or_b32_e32 v6, v6, v16
	v_lshl_add_u64 v[0:1], s[20:21], 0, v[6:7]
	global_store_byte v[0:1], v3, off
	v_mul_f32_e32 v0, v2, v17
	v_add_f32_e32 v1, v36, v24
	v_lshlrev_b32_e32 v2, 16, v143
	v_mul_f32_e32 v0, v0, v1
	v_mul_f32_e32 v1, 0x3d372713, v2
	v_mul_f32_e32 v1, v1, v2
	v_fma_f32 v1, v1, v2, v2
	v_mul_f32_e32 v1, 0x3f4c422a, v1
	v_mul_f32_e32 v1, -2.0, v1
	v_mul_f32_e32 v1, 0x3fb8aa3b, v1
	v_exp_f32_e32 v1, v1
	v_med3_f32 v0, v0, s42, v139
	v_mov_b32_e32 v3, v79
	v_cvt_pk_fp8_f32 v3, v0, 0
	v_add_f32_e32 v4, 1.0, v1
	v_rcp_f32_e32 v6, v4
	v_or_b32_e32 v94, v94, v16
	v_lshl_add_u64 v[0:1], s[20:21], 0, v[94:95]
	global_store_byte v[0:1], v3, off
	v_mul_f32_e32 v0, v2, v6
	v_add_f32_e32 v1, v37, v25
	v_lshlrev_b32_e32 v2, 16, v142
	v_mul_f32_e32 v0, v0, v1
	v_mul_f32_e32 v1, 0x3d372713, v2
	v_mul_f32_e32 v1, v1, v2
	v_fma_f32 v1, v1, v2, v2
	v_mul_f32_e32 v1, 0x3f4c422a, v1
	v_mul_f32_e32 v1, -2.0, v1
	v_mul_f32_e32 v1, 0x3fb8aa3b, v1
	v_exp_f32_e32 v1, v1
	v_med3_f32 v0, v0, s42, v139
	v_mov_b32_e32 v3, v79
	v_cvt_pk_fp8_f32 v3, v0, 0
	v_add_f32_e32 v4, 1.0, v1
	v_rcp_f32_e32 v6, v4
	v_or_b32_e32 v96, v96, v16
	v_lshl_add_u64 v[0:1], s[20:21], 0, v[96:97]
	global_store_byte v[0:1], v3, off
	v_mul_f32_e32 v0, v2, v6
	v_add_f32_e32 v1, v38, v26
	v_lshlrev_b32_e32 v2, 16, v141
	v_mul_f32_e32 v0, v0, v1
	v_mul_f32_e32 v1, 0x3d372713, v2
	v_mul_f32_e32 v1, v1, v2
	v_fma_f32 v1, v1, v2, v2
	v_mul_f32_e32 v1, 0x3f4c422a, v1
	v_mul_f32_e32 v1, -2.0, v1
	v_mul_f32_e32 v1, 0x3fb8aa3b, v1
	v_exp_f32_e32 v1, v1
	v_med3_f32 v0, v0, s42, v139
	v_mov_b32_e32 v3, v79
	v_cvt_pk_fp8_f32 v3, v0, 0
	v_add_f32_e32 v4, 1.0, v1
	v_rcp_f32_e32 v6, v4
	v_or_b32_e32 v100, v100, v16
	v_lshl_add_u64 v[0:1], s[20:21], 0, v[100:101]
	global_store_byte v[0:1], v3, off
	v_mul_f32_e32 v0, v2, v6
	v_add_f32_e32 v1, v39, v27
	s_waitcnt vmcnt(27)
	v_lshlrev_b32_e32 v2, 16, v140
	v_mul_f32_e32 v0, v0, v1
	v_mul_f32_e32 v1, 0x3d372713, v2
	v_mul_f32_e32 v1, v1, v2
	v_fma_f32 v1, v1, v2, v2
	v_mul_f32_e32 v1, 0x3f4c422a, v1
	v_mul_f32_e32 v1, -2.0, v1
	v_mul_f32_e32 v1, 0x3fb8aa3b, v1
	v_exp_f32_e32 v1, v1
	v_med3_f32 v0, v0, s42, v139
	v_mov_b32_e32 v3, v79
	v_cvt_pk_fp8_f32 v3, v0, 0
	v_add_f32_e32 v4, 1.0, v1
	v_rcp_f32_e32 v6, v4
	v_or_b32_e32 v10, v10, v16
	v_lshl_add_u64 v[0:1], s[20:21], 0, v[10:11]
	global_store_byte v[0:1], v3, off
	v_mul_f32_e32 v0, v2, v6
	v_add_f32_e32 v1, v32, v28
	v_lshlrev_b32_e32 v2, 16, v85
	v_mul_f32_e32 v0, v0, v1
	v_mul_f32_e32 v1, 0x3d372713, v2
	v_mul_f32_e32 v1, v1, v2
	v_fma_f32 v1, v1, v2, v2
	v_mul_f32_e32 v1, 0x3f4c422a, v1
	v_mul_f32_e32 v1, -2.0, v1
	v_mul_f32_e32 v1, 0x3fb8aa3b, v1
	v_exp_f32_e32 v1, v1
	v_med3_f32 v0, v0, s42, v139
	v_mov_b32_e32 v3, v79
	v_cvt_pk_fp8_f32 v3, v0, 0
	v_add_f32_e32 v4, 1.0, v1
	v_rcp_f32_e32 v6, v4
	v_or_b32_e32 v102, v102, v16
	v_lshl_add_u64 v[0:1], s[20:21], 0, v[102:103]
	global_store_byte v[0:1], v3, off
	v_mul_f32_e32 v0, v2, v6
	v_add_f32_e32 v1, v33, v29
	v_lshlrev_b32_e32 v2, 16, v83
	v_mul_f32_e32 v0, v0, v1
	v_mul_f32_e32 v1, 0x3d372713, v2
	v_mul_f32_e32 v1, v1, v2
	v_fma_f32 v1, v1, v2, v2
	v_mul_f32_e32 v1, 0x3f4c422a, v1
	v_mul_f32_e32 v1, -2.0, v1
	v_mul_f32_e32 v1, 0x3fb8aa3b, v1
	v_exp_f32_e32 v1, v1
	v_med3_f32 v0, v0, s42, v139
	v_mov_b32_e32 v3, v79
	v_cvt_pk_fp8_f32 v3, v0, 0
	v_add_f32_e32 v4, 1.0, v1
	v_rcp_f32_e32 v6, v4
	v_or_b32_e32 v12, v12, v16
	v_lshl_add_u64 v[0:1], s[20:21], 0, v[12:13]
	global_store_byte v[0:1], v3, off
	v_mul_f32_e32 v0, v2, v6
	v_lshlrev_b32_e32 v2, 16, v78
	v_mul_f32_e32 v3, 0x3d372713, v2
	v_mul_f32_e32 v3, v3, v2
	v_fma_f32 v3, v3, v2, v2
	v_mul_f32_e32 v3, 0x3f4c422a, v3
	v_mul_f32_e32 v3, -2.0, v3
	v_mul_f32_e32 v3, 0x3fb8aa3b, v3
	v_exp_f32_e32 v3, v3
	v_add_f32_e32 v1, v34, v30
	v_mul_f32_e32 v0, v0, v1
	v_med3_f32 v0, v0, s42, v139
	v_add_f32_e32 v3, 1.0, v3
	v_rcp_f32_e32 v6, v3
	v_mov_b32_e32 v4, v79
	v_or_b32_e32 v8, v8, v16
	v_cvt_pk_fp8_f32 v4, v0, 0
	v_lshl_add_u64 v[0:1], s[20:21], 0, v[8:9]
	v_mul_f32_e32 v5, v2, v6
	v_mov_b32_e32 v2, v5
	v_add_f32_e32 v3, v35, v31
	v_mul_f32_e32 v2, v2, v3
	v_med3_f32 v2, v2, s42, v139
	v_mov_b32_e32 v3, v79
	v_cvt_pk_fp8_f32 v3, v2, 0
	v_or_b32_e32 v14, v14, v16
	global_store_byte v[0:1], v4, off
	v_lshl_add_u64 v[0:1], s[20:21], 0, v[14:15]
	s_mov_b64 s[8:9], 0
	global_store_byte v[0:1], v3, off

.LBB0_2012:
	s_add_i32 s8, s8, 2
	s_sub_i32 s80, s14, 64
	s_cmp_lt_u32 s8, 3
	s_cselect_b32 s80, s13, s80
	s_mul_i32 s81, s80, 0xc00
	s_add_i32 s85, s82, 0x8000
	s_mov_b32 m0, s85
	s_add_i32 s85, s82, 0x10000
	buffer_load_dwordx4 v154, s[72:75], s81 offen lds
	s_mov_b32 m0, s85
	s_add_i32 s85, s82, 0xa000
	buffer_load_dwordx4 v155, s[72:75], s81 offen lds
	s_mov_b32 m0, s85
	s_add_i32 s81, s81, 0x18000
	buffer_load_dwordx4 v154, s[72:75], s81 offen lds
	s_lshl_b32 s81, s83, 11
	s_add_i32 s85, s82, 0x4000
	s_mov_b32 m0, s85
	s_add_i32 s85, s82, 0x6000
	buffer_load_dwordx4 v158, s[76:79], s81 offen lds
	s_mov_b32 m0, s85
	s_add_i32 s81, s81, 0x10000
	buffer_load_dwordx4 v158, s[76:79], s81 offen lds
	s_mov_b32 s84, s80
	s_add_i32 s6, 0, 0x12000
	v_add_u32_e32 v199, s6, v170
	v_add_u32_e32 v204, s6, v171
	v_add_u32_e32 v205, s6, v172
	ds_read_b128 v[64:67], v180 offset:49152
	ds_read_b128 v[68:71], v180 offset:57344
	ds_read_b128 v[200:203], v181 offset:49152
	ds_read_b128 v[226:229], v181 offset:57344
	ds_read_b128 v[230:233], v182 offset:49152
	ds_read_b128 v[234:237], v182 offset:57344
	ds_read_b128 v[238:241], v183 offset:49152
	ds_read_b128 v[242:245], v183 offset:57344
	s_waitcnt lgkmcnt(7)
	v_mfma_f32_32x32x16_bf16 v[80:95], v[64:67], v[124:127], 0
	v_exp_f32_e32 v216, v128
	v_add_f32_e32 v128, 0, v222
	v_add_f32_e32 v128, v224, v128
	v_add_f32_e32 v128, v220, v128
	v_add_f32_e32 v128, v223, v128
	v_add_f32_e32 v128, v219, v128
	v_add_f32_e32 v128, v221, v128
	s_waitcnt lgkmcnt(6)
	v_mfma_f32_32x32x16_bf16 v[64:79], v[68:71], v[124:127], 0
	v_add_f32_e32 v128, v217, v128
	v_add_f32_e32 v128, v218, v128
	v_add_f32_e32 v128, v212, v128
	v_add_f32_e32 v128, v214, v128
	v_add_f32_e32 v128, v211, v128
	v_add_f32_e32 v128, v213, v128
	v_exp_f32_e32 v138, v138
	s_waitcnt lgkmcnt(5)
	v_mfma_f32_32x32x16_bf16 v[80:95], v[200:203], v[120:123], v[80:95]
	v_add_f32_e32 v128, v208, v128
	v_exp_f32_e32 v139, v139
	v_add_f32_e32 v128, v210, v128
	v_exp_f32_e32 v164, v136
	v_add_f32_e32 v128, v207, v128
	v_exp_f32_e32 v137, v137
	v_add_f32_e32 v128, v209, v128
	s_waitcnt lgkmcnt(4)
	v_mfma_f32_32x32x16_bf16 v[64:79], v[226:229], v[120:123], v[64:79]
	ds_read_b128 v[200:203], v184 offset:49152
	ds_read_b128 v[226:229], v184 offset:57344
	v_exp_f32_e32 v165, v132
	v_add_f32_e32 v128, v138, v128
	v_add_f32_e32 v128, v139, v128
	v_exp_f32_e32 v206, v130
	v_add_f32_e32 v128, v164, v128
	v_exp_f32_e32 v215, v131
	s_waitcnt lgkmcnt(5)
	v_mfma_f32_32x32x16_bf16 v[80:95], v[230:233], v[116:119], v[80:95]
	v_add_f32_e32 v128, v137, v128
	v_add_f32_e32 v128, v165, v128
	v_exp_f32_e32 v225, v129
	v_exp_f32_e32 v162, v162
	v_exp_f32_e32 v163, v163
	v_exp_f32_e32 v160, v160
	v_exp_f32_e32 v161, v161
	s_waitcnt lgkmcnt(4)
	v_mfma_f32_32x32x16_bf16 v[64:79], v[234:237], v[116:119], v[64:79]
	ds_read_b128 v[230:233], v185 offset:49152
	ds_read_b128 v[234:237], v185 offset:57344
	v_cvt_pk_bf16_f32 v129, v220, v223
	v_cvt_pk_bf16_f32 v130, v219, v221
	v_cvt_pk_bf16_f32 v131, v217, v218
	v_cvt_pk_bf16_f32 v132, v212, v214
	v_cvt_pk_bf16_f32 v136, v138, v139
	v_cvt_pk_bf16_f32 v137, v164, v137
	s_waitcnt lgkmcnt(5)
	v_mfma_f32_32x32x16_bf16 v[80:95], v[238:241], v[112:115], v[80:95]
	v_cvt_pk_bf16_f32 v139, v206, v215
	v_permlane32_swap_b32_e32 v129, v131
	s_nop 0
	v_permlane32_swap_b32_e32 v137, v139
	s_waitcnt lgkmcnt(4)
	v_mfma_f32_32x32x16_bf16 v[64:79], v[242:245], v[112:115], v[64:79]
	ds_read_b128 v[238:241], v186 offset:49152
	ds_read_b128 v[242:245], v186 offset:57344
	s_waitcnt lgkmcnt(5)
	v_mfma_f32_32x32x16_bf16 v[80:95], v[200:203], v[108:111], v[80:95]
	s_waitcnt lgkmcnt(4)
	v_mfma_f32_32x32x16_bf16 v[64:79], v[226:229], v[108:111], v[64:79]
	ds_read_b128 v[200:203], v187 offset:49152
	ds_read_b128 v[226:229], v187 offset:57344
	s_waitcnt lgkmcnt(5)
	v_mfma_f32_32x32x16_bf16 v[80:95], v[230:233], v[104:107], v[80:95]
	s_waitcnt lgkmcnt(4)
	v_mfma_f32_32x32x16_bf16 v[64:79], v[234:237], v[104:107], v[64:79]
	ds_read_b128 v[230:233], v199
	ds_read_b128 v[234:237], v199 offset:4096
	ds_read_b128 v[246:249], v190
	s_waitcnt lgkmcnt(6)
	v_mfma_f32_32x32x16_bf16 v[80:95], v[238:241], v[100:103], v[80:95]
	s_waitcnt lgkmcnt(5)
	v_mfma_f32_32x32x16_bf16 v[64:79], v[242:245], v[100:103], v[64:79]
	ds_read_b128 v[238:241], v204
	ds_read_b128 v[242:245], v204 offset:4096
	ds_read_b128 v[250:253], v190 offset:1024
	v_add_u32_e32 v204, s6, v173
	s_waitcnt lgkmcnt(7)
	v_mfma_f32_32x32x16_bf16 v[80:95], v[200:203], v[96:99], v[80:95]
	s_waitcnt lgkmcnt(6)
	v_mfma_f32_32x32x16_bf16 v[64:79], v[226:229], v[96:99], v[64:79]
	ds_read_b128 v[200:203], v205
	ds_read_b128 v[226:229], v205 offset:4096
	s_waitcnt lgkmcnt(5)
	v_mfma_f32_32x32x16_bf16 v[80:95], v[230:233], v[246:249], v[80:95]
	s_waitcnt lgkmcnt(5)
	v_mfma_f32_32x32x16_bf16 v[64:79], v[234:237], v[246:249], v[64:79]
	ds_read_b128 v[230:233], v204
	ds_read_b128 v[234:237], v204 offset:4096
	ds_read_b128 v[246:249], v190 offset:2048
	s_waitcnt lgkmcnt(5)
	v_mfma_f32_32x32x16_bf16 v[80:95], v[238:241], v[250:253], v[80:95]
	s_waitcnt lgkmcnt(5)
	v_mfma_f32_32x32x16_bf16 v[64:79], v[242:245], v[250:253], v[64:79]
	ds_read_b128 v[250:253], v190 offset:3072
	s_waitcnt lgkmcnt(1)
	v_mfma_f32_32x32x16_bf16 v[80:95], v[200:203], v[246:249], v[80:95]
	v_exp_f32_e32 v205, v133
	v_cvt_pk_bf16_f32 v133, v211, v213
	v_cvt_pk_bf16_f32 v138, v165, v205
	v_add_f32_e32 v128, v205, v128
	v_add_f32_e32 v128, v206, v128
	v_add_f32_e32 v128, v215, v128
	s_waitcnt lgkmcnt(1)
	v_mfma_f32_32x32x16_bf16 v[64:79], v[226:229], v[246:249], v[64:79]
	v_add_f32_e32 v128, v216, v128
	v_add_f32_e32 v128, v225, v128
	v_add_f32_e32 v128, v162, v128
	v_add_f32_e32 v128, v163, v128
	v_add_f32_e32 v128, v160, v128
	v_add_f32_e32 v128, v161, v128
	s_waitcnt lgkmcnt(0)
	v_mfma_f32_32x32x16_bf16 v[80:95], v[230:233], v[250:253], v[80:95]
	v_exp_f32_e32 v226, v134
	v_exp_f32_e32 v227, v135
	v_cvt_pk_bf16_f32 v134, v208, v210
	v_cvt_pk_bf16_f32 v135, v207, v209
	v_add_f32_e32 v128, v226, v128
	v_add_f32_e32 v203, v227, v128
	v_mov_b32_e32 v204, v203
	s_waitcnt lgkmcnt(0)
	v_mfma_f32_32x32x16_bf16 v[64:79], v[234:237], v[250:253], v[64:79]
	s_nop 0
	v_permlane32_swap_b32_e32 v203, v204
	v_cvt_pk_bf16_f32 v128, v222, v224
	v_cvt_pk_bf16_f32 v208, v216, v225
	v_cvt_pk_bf16_f32 v209, v162, v163
	v_cvt_pk_bf16_f32 v210, v160, v161
	v_cvt_pk_bf16_f32 v211, v226, v227
	v_permlane32_swap_b32_e32 v132, v134
	v_permlane32_swap_b32_e32 v128, v130
	v_permlane32_swap_b32_e32 v133, v135
	v_permlane32_swap_b32_e32 v136, v138
	v_permlane32_swap_b32_e32 v208, v210
	v_permlane32_swap_b32_e32 v209, v211
	ds_read_b64_tr_b16 v[160:161], v167 offset:0
	ds_read_b64_tr_b16 v[162:163], v167 offset:0x800
	ds_read_b64_tr_b16 v[232:233], v167 offset:0x1000
	ds_read_b64_tr_b16 v[234:235], v167 offset:0x1800
	ds_read_b64_tr_b16 v[236:237], v167 offset:0x2000
	ds_read_b64_tr_b16 v[238:239], v167 offset:0x2800
	ds_read_b64_tr_b16 v[240:241], v167 offset:0x3000
	ds_read_b64_tr_b16 v[242:243], v167 offset:0x3800
	v_max_f32_e32 v164, v81, v81
	v_max_f32_e32 v165, v80, v80
	v_max_f32_e32 v164, v165, v164
	v_max3_f32 v164, v164, v82, v83
	v_max3_f32 v164, v164, v84, v85
	v_max3_f32 v164, v164, v86, v87
	v_max3_f32 v164, v164, v88, v89
	v_max3_f32 v164, v164, v90, v91
	v_max3_f32 v164, v164, v92, v93
	v_max3_f32 v164, v164, v94, v95
	s_waitcnt lgkmcnt(6)
	v_mfma_f32_32x32x16_bf16 v[0:15], v[128:131], v[160:163], v[0:15]
	v_max3_f32 v160, v164, v64, v65
	v_max3_f32 v160, v160, v66, v67
	v_max3_f32 v160, v160, v68, v69
	s_waitcnt lgkmcnt(4)
	v_mfma_f32_32x32x16_bf16 v[0:15], v[132:135], v[232:235], v[0:15]
	ds_read_b64_tr_b16 v[232:233], v167 offset:0x200
	ds_read_b64_tr_b16 v[234:235], v167 offset:0xa00
	v_max3_f32 v160, v160, v70, v71
	v_max3_f32 v160, v160, v72, v73
	v_max3_f32 v160, v160, v74, v75
	s_waitcnt lgkmcnt(4)
	v_mfma_f32_32x32x16_bf16 v[0:15], v[136:139], v[236:239], v[0:15]
	ds_read_b64_tr_b16 v[236:237], v167 offset:0x1200
	ds_read_b64_tr_b16 v[238:239], v167 offset:0x1a00
	ds_read_b64_tr_b16 v[244:245], v167 offset:0x2200
	ds_read_b64_tr_b16 v[246:247], v167 offset:0x2a00
	ds_read_b64_tr_b16 v[248:249], v167 offset:0x3200
	ds_read_b64_tr_b16 v[250:251], v167 offset:0x3a00
	v_max3_f32 v160, v160, v76, v77
	v_max3_f32 v160, v160, v78, v79
	v_mov_b32_e32 v161, v160
	s_waitcnt lgkmcnt(8)
	v_mfma_f32_32x32x16_bf16 v[0:15], v[208:211], v[240:243], v[0:15]
	v_max_f32_e32 v162, v198, v198
	v_permlane32_swap_b32_e32 v160, v161
	v_max_f32_e32 v161, v161, v161
	v_max_f32_e32 v160, v160, v160
	v_max_f32_e32 v160, v160, v161
	s_waitcnt lgkmcnt(6)
	v_mfma_f32_32x32x16_bf16 v[32:47], v[128:131], v[232:235], v[32:47]
	ds_read_b64_tr_b16 v[232:233], v167 offset:0x400
	ds_read_b64_tr_b16 v[234:235], v167 offset:0xc00
	v_sub_f32_e32 v161, v160, v198
	v_max_f32_e32 v160, v162, v160
	v_sub_f32_e32 v162, v198, v160
	v_mul_f32_e32 v162, 0x3dd53b94, v162
	v_exp_f32_e32 v162, v162
	s_waitcnt lgkmcnt(6)
	v_mfma_f32_32x32x16_bf16 v[32:47], v[132:135], v[236:239], v[32:47]
	ds_read_b64_tr_b16 v[236:237], v167 offset:0x1400
	ds_read_b64_tr_b16 v[238:239], v167 offset:0x1c00
	ds_read_b64_tr_b16 v[240:241], v167 offset:0x2400
	ds_read_b64_tr_b16 v[242:243], v167 offset:0x2c00
	v_cmp_ge_f32_e32 vcc, s46, v161
	s_cmp_eq_u64 vcc, exec
	s_cselect_b64 s[6:7], -1, 0
	v_cndmask_b32_e64 v206, v162, 1.0, s[6:7]
	v_cndmask_b32_e64 v160, v160, v198, s[6:7]
	v_mul_f32_e32 v205, 0xbdd53b94, v160
	v_cmp_gt_f32_e32 vcc, 1.0, v206
	s_waitcnt lgkmcnt(8)
	v_mfma_f32_32x32x16_bf16 v[32:47], v[136:139], v[244:247], v[32:47]
	ds_read_b64_tr_b16 v[244:245], v167 offset:0x3400
	ds_read_b64_tr_b16 v[246:247], v167 offset:0x3c00
	v_fmamk_f32 v87, v87, 0x3dd53b94, v205
	v_fmamk_f32 v80, v80, 0x3dd53b94, v205
	v_fmamk_f32 v81, v81, 0x3dd53b94, v205
	v_fmamk_f32 v82, v82, 0x3dd53b94, v205
	v_fmamk_f32 v83, v83, 0x3dd53b94, v205
	s_waitcnt lgkmcnt(8)
	v_mfma_f32_32x32x16_bf16 v[32:47], v[208:211], v[248:251], v[32:47]
	v_fmamk_f32 v84, v84, 0x3dd53b94, v205
	v_fmamk_f32 v85, v85, 0x3dd53b94, v205
	v_fmamk_f32 v86, v86, 0x3dd53b94, v205
	v_fmamk_f32 v88, v88, 0x3dd53b94, v205
	v_fmamk_f32 v89, v89, 0x3dd53b94, v205
	s_waitcnt lgkmcnt(6)
	v_mfma_f32_32x32x16_bf16 v[16:31], v[128:131], v[232:235], v[16:31]
	ds_read_b64_tr_b16 v[232:233], v167 offset:0x600
	ds_read_b64_tr_b16 v[234:235], v167 offset:0xe00
	v_fmamk_f32 v90, v90, 0x3dd53b94, v205
	v_fmamk_f32 v91, v91, 0x3dd53b94, v205
	v_fmamk_f32 v92, v92, 0x3dd53b94, v205
	v_fmamk_f32 v93, v93, 0x3dd53b94, v205
	v_fmamk_f32 v94, v94, 0x3dd53b94, v205
	s_waitcnt lgkmcnt(6)
	v_mfma_f32_32x32x16_bf16 v[16:31], v[132:135], v[236:239], v[16:31]
	ds_read_b64_tr_b16 v[236:237], v167 offset:0x1600
	ds_read_b64_tr_b16 v[238:239], v167 offset:0x1e00
	v_fmamk_f32 v95, v95, 0x3dd53b94, v205
	v_fmamk_f32 v215, v64, 0x3dd53b94, v205
	v_fmamk_f32 v216, v65, 0x3dd53b94, v205
	v_fmamk_f32 v217, v66, 0x3dd53b94, v205
	v_fmamk_f32 v218, v67, 0x3dd53b94, v205
	s_waitcnt lgkmcnt(6)
	v_mfma_f32_32x32x16_bf16 v[16:31], v[136:139], v[240:243], v[16:31]
	ds_read_b64_tr_b16 v[240:241], v167 offset:0x2600
	ds_read_b64_tr_b16 v[242:243], v167 offset:0x2e00
	ds_read_b64_tr_b16 v[248:249], v167 offset:0x3600
	ds_read_b64_tr_b16 v[250:251], v167 offset:0x3e00
	v_fmamk_f32 v219, v68, 0x3dd53b94, v205
	v_fmamk_f32 v212, v73, 0x3dd53b94, v205
	v_fmamk_f32 v213, v74, 0x3dd53b94, v205
	v_fmamk_f32 v214, v75, 0x3dd53b94, v205
	s_waitcnt lgkmcnt(8)
	v_mfma_f32_32x32x16_bf16 v[16:31], v[208:211], v[244:247], v[16:31]
	v_fmamk_f32 v207, v76, 0x3dd53b94, v205
	v_fmamk_f32 v220, v77, 0x3dd53b94, v205
	v_fmamk_f32 v221, v78, 0x3dd53b94, v205
	s_waitcnt lgkmcnt(6)
	v_mfma_f32_32x32x16_bf16 v[48:63], v[128:131], v[232:235], v[48:63]
	v_exp_f32_e32 v128, v80
	v_exp_f32_e32 v129, v82
	v_exp_f32_e32 v130, v84
	v_exp_f32_e32 v131, v86
	s_waitcnt lgkmcnt(4)
	v_mfma_f32_32x32x16_bf16 v[48:63], v[132:135], v[236:239], v[48:63]
	v_exp_f32_e32 v132, v88
	v_exp_f32_e32 v133, v90
	v_exp_f32_e32 v134, v92
	v_exp_f32_e32 v135, v94
	s_waitcnt lgkmcnt(2)
	v_mfma_f32_32x32x16_bf16 v[48:63], v[136:139], v[240:243], v[48:63]
	v_exp_f32_e32 v139, v89
	v_exp_f32_e32 v138, v91
	v_exp_f32_e32 v137, v93
	v_exp_f32_e32 v136, v95
	s_waitcnt lgkmcnt(0)
	v_mfma_f32_32x32x16_bf16 v[48:63], v[208:211], v[248:251], v[48:63]
	v_exp_f32_e32 v161, v87
	v_exp_f32_e32 v198, v81
	v_exp_f32_e32 v163, v83
	v_exp_f32_e32 v162, v85
	v_fmamk_f32 v208, v69, 0x3dd53b94, v205
	v_fmamk_f32 v209, v70, 0x3dd53b94, v205
	v_fmamk_f32 v210, v71, 0x3dd53b94, v205
	v_fmamk_f32 v211, v72, 0x3dd53b94, v205
	v_fmac_f32_e32 v205, 0x3dd53b94, v79
	s_cbranch_vccz .LBB0_2016
	s_and_saveexec_b64 s[10:11], s[4:5]
	ds_write_b32 v189, v206 offset:128
	s_or_b64 exec, exec, s[10:11]
	s_waitcnt lgkmcnt(0)
	v_add_u32_e32 v248, s12, v169
	ds_read_b128 v[232:235], v248 offset:224
	ds_read_b128 v[236:239], v248 offset:192
	ds_read_b128 v[240:243], v248 offset:160
	ds_read_b128 v[244:247], v248 offset:128
	s_waitcnt lgkmcnt(3)
	v_pk_mul_f32 v[12:13], v[12:13], v[232:233]
	s_waitcnt lgkmcnt(2)
	v_pk_mul_f32 v[8:9], v[8:9], v[236:237]
	s_waitcnt lgkmcnt(1)
	v_pk_mul_f32 v[4:5], v[4:5], v[240:241]
	v_pk_mul_f32 v[14:15], v[14:15], v[234:235]
	v_pk_mul_f32 v[10:11], v[10:11], v[238:239]
	v_pk_mul_f32 v[6:7], v[6:7], v[242:243]
	s_waitcnt lgkmcnt(0)
	v_pk_mul_f32 v[2:3], v[2:3], v[246:247]
	v_pk_mul_f32 v[0:1], v[0:1], v[244:245]
	v_pk_mul_f32 v[44:45], v[44:45], v[232:233]
	v_pk_mul_f32 v[40:41], v[40:41], v[236:237]
	v_pk_mul_f32 v[36:37], v[36:37], v[240:241]
	v_pk_mul_f32 v[46:47], v[46:47], v[234:235]
	v_pk_mul_f32 v[42:43], v[42:43], v[238:239]
	v_pk_mul_f32 v[38:39], v[38:39], v[242:243]
	v_pk_mul_f32 v[34:35], v[34:35], v[246:247]
	v_pk_mul_f32 v[32:33], v[32:33], v[244:245]
	v_pk_mul_f32 v[28:29], v[28:29], v[232:233]
	v_pk_mul_f32 v[24:25], v[24:25], v[236:237]
	v_pk_mul_f32 v[20:21], v[20:21], v[240:241]
	v_pk_mul_f32 v[30:31], v[30:31], v[234:235]
	v_pk_mul_f32 v[26:27], v[26:27], v[238:239]
	v_pk_mul_f32 v[22:23], v[22:23], v[242:243]
	v_pk_mul_f32 v[18:19], v[18:19], v[246:247]
	v_pk_mul_f32 v[16:17], v[16:17], v[244:245]
	v_pk_mul_f32 v[60:61], v[60:61], v[232:233]
	v_pk_mul_f32 v[56:57], v[56:57], v[236:237]
	v_pk_mul_f32 v[52:53], v[52:53], v[240:241]
	v_pk_mul_f32 v[62:63], v[62:63], v[234:235]
	v_pk_mul_f32 v[58:59], v[58:59], v[238:239]
	v_pk_mul_f32 v[54:55], v[54:55], v[242:243]
	v_pk_mul_f32 v[50:51], v[50:51], v[246:247]
	v_pk_mul_f32 v[48:49], v[48:49], v[244:245]
.LBB0_2016:
	s_waitcnt vmcnt(0) lgkmcnt(0)
	s_barrier
	s_add_i32 s80, s13, 64
	s_cmp_lt_u32 s8, 2
	s_cselect_b32 s80, s80, s14
	s_mul_i32 s81, s80, 0xc00
	s_add_i32 s85, s82, 0xc000
	s_mov_b32 m0, s85
	s_add_i32 s85, s82, 0x12000
	buffer_load_dwordx4 v154, s[72:75], s81 offen lds
	s_mov_b32 m0, s85
	s_add_i32 s85, s82, 0xe000
	buffer_load_dwordx4 v155, s[72:75], s81 offen lds
	s_mov_b32 m0, s85
	s_add_i32 s81, s81, 0x18000
	buffer_load_dwordx4 v154, s[72:75], s81 offen lds
	s_lshl_b32 s81, s84, 11
	s_add_i32 s85, s82, 0x0
	s_mov_b32 m0, s85
	s_add_i32 s85, s82, 0x2000
	buffer_load_dwordx4 v158, s[76:79], s81 offen lds
	s_mov_b32 m0, s85
	s_add_i32 s81, s81, 0x10000
	buffer_load_dwordx4 v158, s[76:79], s81 offen lds
	s_mov_b32 s83, s80
	ds_read_b128 v[64:67], v180 offset:32768
	ds_read_b128 v[68:71], v180 offset:40960
	ds_read_b128 v[222:225], v181 offset:32768
	ds_read_b128 v[226:229], v181 offset:40960
	ds_read_b128 v[230:233], v182 offset:32768
	ds_read_b128 v[234:237], v182 offset:40960
	ds_read_b128 v[238:241], v183 offset:32768
	ds_read_b128 v[242:245], v183 offset:40960
	v_exp_f32_e32 v164, v215
	v_add_f32_e32 v215, 0, v128
	s_waitcnt lgkmcnt(7)
	v_mfma_f32_32x32x16_bf16 v[80:95], v[64:67], v[124:127], 0
	v_add_f32_e32 v215, v198, v215
	v_add_f32_e32 v215, v129, v215
	v_add_f32_e32 v215, v163, v215
	v_add_f32_e32 v215, v130, v215
	v_add_f32_e32 v215, v162, v215
	v_add_f32_e32 v215, v131, v215
	v_add_f32_e32 v215, v161, v215
	s_waitcnt lgkmcnt(6)
	v_mfma_f32_32x32x16_bf16 v[64:79], v[68:71], v[124:127], 0
	v_add_f32_e32 v215, v132, v215
	v_add_f32_e32 v215, v139, v215
	v_add_f32_e32 v215, v133, v215
	v_add_f32_e32 v215, v138, v215
	v_add_f32_e32 v215, v134, v215
	v_exp_f32_e32 v165, v216
	v_add_f32_e32 v215, v137, v215
	s_waitcnt lgkmcnt(5)
	v_mfma_f32_32x32x16_bf16 v[80:95], v[222:225], v[120:123], v[80:95]
	v_exp_f32_e32 v217, v217
	v_add_f32_e32 v215, v135, v215
	v_exp_f32_e32 v218, v218
	v_add_f32_e32 v215, v136, v215
	v_exp_f32_e32 v219, v219
	v_add_f32_e32 v215, v164, v215
	v_exp_f32_e32 v208, v208
	s_waitcnt lgkmcnt(4)
	v_mfma_f32_32x32x16_bf16 v[64:79], v[226:229], v[120:123], v[64:79]
	ds_read_b128 v[222:225], v184 offset:32768
	ds_read_b128 v[226:229], v184 offset:40960
	v_add_f32_e32 v215, v165, v215
	v_exp_f32_e32 v209, v209
	v_add_f32_e32 v215, v217, v215
	v_exp_f32_e32 v210, v210
	v_add_f32_e32 v215, v218, v215
	v_exp_f32_e32 v211, v211
	s_waitcnt lgkmcnt(5)
	v_mfma_f32_32x32x16_bf16 v[80:95], v[230:233], v[116:119], v[80:95]
	v_add_f32_e32 v215, v219, v215
	v_exp_f32_e32 v212, v212
	v_add_f32_e32 v215, v208, v215
	v_exp_f32_e32 v213, v213
	v_add_f32_e32 v215, v209, v215
	v_exp_f32_e32 v214, v214
	v_add_f32_e32 v215, v210, v215
	s_waitcnt lgkmcnt(4)
	v_mfma_f32_32x32x16_bf16 v[64:79], v[234:237], v[116:119], v[64:79]
	ds_read_b128 v[230:233], v185 offset:32768
	ds_read_b128 v[234:237], v185 offset:40960
	v_exp_f32_e32 v207, v207
	v_add_f32_e32 v215, v211, v215
	v_exp_f32_e32 v220, v220
	v_add_f32_e32 v215, v212, v215
	v_exp_f32_e32 v221, v221
	v_add_f32_e32 v215, v213, v215
	s_waitcnt lgkmcnt(5)
	v_mfma_f32_32x32x16_bf16 v[80:95], v[238:241], v[112:115], v[80:95]
	v_exp_f32_e32 v205, v205
	v_add_f32_e32 v215, v214, v215
	v_add_f32_e32 v215, v207, v215
	v_add_f32_e32 v215, v220, v215
	v_add_f32_e32 v215, v221, v215
	v_add_f32_e32 v215, v205, v215
	v_mov_b32_e32 v216, v215
	s_waitcnt lgkmcnt(4)
	v_mfma_f32_32x32x16_bf16 v[64:79], v[242:245], v[112:115], v[64:79]
	ds_read_b128 v[238:241], v186 offset:32768
	ds_read_b128 v[242:245], v186 offset:40960
	v_permlane32_swap_b32_e32 v215, v216
	v_cvt_pk_bf16_f32 v128, v128, v198
	v_cvt_pk_bf16_f32 v129, v129, v163
	v_cvt_pk_bf16_f32 v130, v130, v162
	v_cvt_pk_bf16_f32 v131, v131, v161
	s_waitcnt lgkmcnt(5)
	v_mfma_f32_32x32x16_bf16 v[80:95], v[222:225], v[108:111], v[80:95]
	v_cvt_pk_bf16_f32 v132, v132, v139
	v_cvt_pk_bf16_f32 v133, v133, v138
	v_cvt_pk_bf16_f32 v134, v134, v137
	v_cvt_pk_bf16_f32 v135, v135, v136
	v_cvt_pk_bf16_f32 v136, v164, v165
	v_cvt_pk_bf16_f32 v137, v217, v218
	v_cvt_pk_bf16_f32 v138, v219, v208
	s_waitcnt lgkmcnt(4)
	v_mfma_f32_32x32x16_bf16 v[64:79], v[226:229], v[108:111], v[64:79]
	ds_read_b128 v[222:225], v187 offset:32768
	ds_read_b128 v[226:229], v187 offset:40960
	v_cvt_pk_bf16_f32 v139, v209, v210
	v_cvt_pk_bf16_f32 v208, v211, v212
	v_cvt_pk_bf16_f32 v209, v213, v214
	v_cvt_pk_bf16_f32 v210, v207, v220
	v_cvt_pk_bf16_f32 v211, v221, v205
	v_permlane32_swap_b32_e32 v128, v130
	s_waitcnt lgkmcnt(5)
	v_mfma_f32_32x32x16_bf16 v[80:95], v[230:233], v[104:107], v[80:95]
	v_permlane32_swap_b32_e32 v129, v131
	v_permlane32_swap_b32_e32 v132, v134
	v_permlane32_swap_b32_e32 v133, v135
	v_permlane32_swap_b32_e32 v136, v138
	s_waitcnt lgkmcnt(4)
	v_mfma_f32_32x32x16_bf16 v[64:79], v[234:237], v[104:107], v[64:79]
	ds_read_b128 v[230:233], v191
	ds_read_b128 v[234:237], v191 offset:4096
	ds_read_b128 v[246:249], v190
	v_permlane32_swap_b32_e32 v137, v139
	v_permlane32_swap_b32_e32 v208, v210
	v_permlane32_swap_b32_e32 v209, v211
	s_waitcnt lgkmcnt(6)
	v_mfma_f32_32x32x16_bf16 v[80:95], v[238:241], v[100:103], v[80:95]
	s_waitcnt lgkmcnt(5)
	v_mfma_f32_32x32x16_bf16 v[64:79], v[242:245], v[100:103], v[64:79]
	ds_read_b128 v[238:241], v192
	ds_read_b128 v[242:245], v192 offset:4096
	ds_read_b128 v[250:253], v190 offset:1024
	s_waitcnt lgkmcnt(7)
	v_mfma_f32_32x32x16_bf16 v[80:95], v[222:225], v[96:99], v[80:95]
	s_waitcnt lgkmcnt(6)
	v_mfma_f32_32x32x16_bf16 v[64:79], v[226:229], v[96:99], v[64:79]
	ds_read_b128 v[222:225], v193
	ds_read_b128 v[226:229], v193 offset:4096
	s_waitcnt lgkmcnt(5)
	v_mfma_f32_32x32x16_bf16 v[80:95], v[230:233], v[246:249], v[80:95]
	s_waitcnt lgkmcnt(5)
	v_mfma_f32_32x32x16_bf16 v[64:79], v[234:237], v[246:249], v[64:79]
	ds_read_b128 v[230:233], v194
	ds_read_b128 v[234:237], v194 offset:4096
	ds_read_b128 v[246:249], v190 offset:2048
	s_waitcnt lgkmcnt(5)
	v_mfma_f32_32x32x16_bf16 v[80:95], v[238:241], v[250:253], v[80:95]
	s_waitcnt lgkmcnt(5)
	v_mfma_f32_32x32x16_bf16 v[64:79], v[242:245], v[250:253], v[64:79]
	ds_read_b128 v[250:253], v190 offset:3072
	s_waitcnt lgkmcnt(1)
	v_mfma_f32_32x32x16_bf16 v[80:95], v[222:225], v[246:249], v[80:95]
	s_waitcnt lgkmcnt(1)
	v_mfma_f32_32x32x16_bf16 v[64:79], v[226:229], v[246:249], v[64:79]
	s_waitcnt lgkmcnt(0)
	v_mfma_f32_32x32x16_bf16 v[80:95], v[230:233], v[250:253], v[80:95]
	s_waitcnt lgkmcnt(0)
	v_mfma_f32_32x32x16_bf16 v[64:79], v[234:237], v[250:253], v[64:79]
	ds_read_b64_tr_b16 v[238:239], v174 offset:0
	ds_read_b64_tr_b16 v[240:241], v174 offset:0x800
	ds_read_b64_tr_b16 v[242:243], v174 offset:0x1000
	ds_read_b64_tr_b16 v[244:245], v174 offset:0x1800
	ds_read_b64_tr_b16 v[246:247], v174 offset:0x2000
	ds_read_b64_tr_b16 v[248:249], v174 offset:0x2800
	ds_read_b64_tr_b16 v[250:251], v174 offset:0x3000
	ds_read_b64_tr_b16 v[252:253], v174 offset:0x3800
	s_nop 3
	v_max_f32_e32 v161, v81, v81
	v_max_f32_e32 v162, v80, v80
	v_max_f32_e32 v161, v162, v161
	v_max3_f32 v161, v161, v82, v83
	v_max3_f32 v161, v161, v84, v85
	v_max3_f32 v161, v161, v86, v87
	v_max3_f32 v161, v161, v88, v89
	v_max3_f32 v161, v161, v90, v91
	v_max3_f32 v161, v161, v92, v93
	v_max3_f32 v161, v161, v94, v95
	s_waitcnt lgkmcnt(6)
	v_mfma_f32_32x32x16_bf16 v[0:15], v[128:131], v[238:241], v[0:15]
	ds_read_b64_tr_b16 v[238:239], v174 offset:0x200
	ds_read_b64_tr_b16 v[240:241], v174 offset:0xa00
	v_max3_f32 v161, v161, v64, v65
	v_max3_f32 v161, v161, v66, v67
	v_max3_f32 v161, v161, v68, v69
	s_waitcnt lgkmcnt(6)
	v_mfma_f32_32x32x16_bf16 v[0:15], v[132:135], v[242:245], v[0:15]
	ds_read_b64_tr_b16 v[242:243], v174 offset:0x1200
	ds_read_b64_tr_b16 v[244:245], v174 offset:0x1a00
	v_max3_f32 v161, v161, v70, v71
	v_max3_f32 v161, v161, v72, v73
	v_max3_f32 v161, v161, v74, v75
	s_waitcnt lgkmcnt(6)
	v_mfma_f32_32x32x16_bf16 v[0:15], v[136:139], v[246:249], v[0:15]
	ds_read_b64_tr_b16 v[246:247], v174 offset:0x2200
	ds_read_b64_tr_b16 v[248:249], v174 offset:0x2a00
	ds_read_b64_tr_b16 v[162:163], v174 offset:0x3200
	ds_read_b64_tr_b16 v[164:165], v174 offset:0x3a00
	v_max3_f32 v161, v161, v76, v77
	v_max3_f32 v161, v161, v78, v79
	v_mov_b32_e32 v198, v161
	s_waitcnt lgkmcnt(8)
	v_mfma_f32_32x32x16_bf16 v[0:15], v[208:211], v[250:253], v[0:15]
	v_max_f32_e32 v205, v160, v160
	v_permlane32_swap_b32_e32 v161, v198
	v_max_f32_e32 v198, v198, v198
	v_max_f32_e32 v161, v161, v161
	v_max_f32_e32 v161, v161, v198
	s_waitcnt lgkmcnt(6)
	v_mfma_f32_32x32x16_bf16 v[32:47], v[128:131], v[238:241], v[32:47]
	ds_read_b64_tr_b16 v[238:239], v174 offset:0x400
	ds_read_b64_tr_b16 v[240:241], v174 offset:0xc00
	v_sub_f32_e32 v198, v161, v160
	v_max_f32_e32 v161, v205, v161
	v_sub_f32_e32 v205, v160, v161
	v_mul_f32_e32 v205, 0x3dd53b94, v205
	v_exp_f32_e32 v205, v205
	s_waitcnt lgkmcnt(6)
	v_mfma_f32_32x32x16_bf16 v[32:47], v[132:135], v[242:245], v[32:47]
	ds_read_b64_tr_b16 v[242:243], v174 offset:0x1400
	ds_read_b64_tr_b16 v[244:245], v174 offset:0x1c00
	v_cmp_ge_f32_e32 vcc, s46, v198
	s_cmp_eq_u64 vcc, exec
	s_cselect_b64 s[6:7], -1, 0
	v_cndmask_b32_e64 v205, v205, 1.0, s[6:7]
	v_cndmask_b32_e64 v198, v161, v160, s[6:7]
	v_mul_f32_e32 v236, 0xbdd53b94, v198
	v_mov_b32_e32 v237, v236
	v_cmp_gt_f32_e32 vcc, 1.0, v205
	s_waitcnt lgkmcnt(6)
	v_mfma_f32_32x32x16_bf16 v[32:47], v[136:139], v[246:249], v[32:47]
	ds_read_b64_tr_b16 v[246:247], v174 offset:0x2400
	ds_read_b64_tr_b16 v[248:249], v174 offset:0x2c00
	ds_read_b64_tr_b16 v[250:251], v174 offset:0x3400
	ds_read_b64_tr_b16 v[252:253], v174 offset:0x3c00
	v_fmamk_f32 v80, v80, 0x3dd53b94, v236
	v_fmamk_f32 v81, v81, 0x3dd53b94, v236
	v_fmamk_f32 v82, v82, 0x3dd53b94, v236
	v_fmamk_f32 v83, v83, 0x3dd53b94, v236
	s_waitcnt lgkmcnt(8)
	v_mfma_f32_32x32x16_bf16 v[32:47], v[208:211], v[162:165], v[32:47]
	v_fmamk_f32 v84, v84, 0x3dd53b94, v236
	v_fmamk_f32 v85, v85, 0x3dd53b94, v236
	v_fmamk_f32 v86, v86, 0x3dd53b94, v236
	v_fmamk_f32 v87, v87, 0x3dd53b94, v236
	s_waitcnt lgkmcnt(6)
	v_mfma_f32_32x32x16_bf16 v[16:31], v[128:131], v[238:241], v[16:31]
	ds_read_b64_tr_b16 v[162:163], v174 offset:0x600
	ds_read_b64_tr_b16 v[164:165], v174 offset:0xe00
	ds_read_b64_tr_b16 v[238:239], v174 offset:0x1600
	ds_read_b64_tr_b16 v[240:241], v174 offset:0x1e00
	v_fmamk_f32 v88, v88, 0x3dd53b94, v236
	v_fmamk_f32 v89, v89, 0x3dd53b94, v236
	v_fmamk_f32 v90, v90, 0x3dd53b94, v236
	v_fmamk_f32 v91, v91, 0x3dd53b94, v236
	s_waitcnt lgkmcnt(8)
	v_mfma_f32_32x32x16_bf16 v[16:31], v[132:135], v[242:245], v[16:31]
	ds_read_b64_tr_b16 v[242:243], v174 offset:0x2600
	ds_read_b64_tr_b16 v[244:245], v174 offset:0x2e00
	v_fmamk_f32 v92, v92, 0x3dd53b94, v236
	v_fmamk_f32 v93, v93, 0x3dd53b94, v236
	v_fmamk_f32 v94, v94, 0x3dd53b94, v236
	v_fmamk_f32 v95, v95, 0x3dd53b94, v236
	s_waitcnt lgkmcnt(8)
	v_mfma_f32_32x32x16_bf16 v[16:31], v[136:139], v[246:249], v[16:31]
	ds_read_b64_tr_b16 v[246:247], v174 offset:0x3600
	ds_read_b64_tr_b16 v[248:249], v174 offset:0x3e00
	v_exp_f32_e32 v222, v80
	v_exp_f32_e32 v224, v81
	v_exp_f32_e32 v220, v82
	s_waitcnt lgkmcnt(8)
	v_mfma_f32_32x32x16_bf16 v[16:31], v[208:211], v[250:253], v[16:31]
	v_exp_f32_e32 v223, v83
	v_exp_f32_e32 v219, v84
	v_exp_f32_e32 v221, v85
	s_waitcnt lgkmcnt(6)
	v_mfma_f32_32x32x16_bf16 v[48:63], v[128:131], v[162:165], v[48:63]
	v_exp_f32_e32 v217, v86
	v_exp_f32_e32 v218, v87
	v_exp_f32_e32 v212, v88
	v_pk_fma_f32 v[130:131], v[70:71], s[26:27], v[236:237] op_sel_hi:[1,0,0]
	v_pk_fma_f32 v[128:129], v[72:73], s[26:27], v[236:237] op_sel_hi:[1,0,0]
	s_waitcnt lgkmcnt(4)
	v_mfma_f32_32x32x16_bf16 v[48:63], v[132:135], v[238:241], v[48:63]
	v_exp_f32_e32 v214, v89
	v_exp_f32_e32 v213, v91
	v_exp_f32_e32 v207, v94
	v_pk_fma_f32 v[132:133], v[68:69], s[26:27], v[236:237] op_sel_hi:[1,0,0]
	v_pk_fma_f32 v[134:135], v[78:79], s[26:27], v[236:237] op_sel_hi:[1,0,0]
	s_waitcnt lgkmcnt(2)
	v_mfma_f32_32x32x16_bf16 v[48:63], v[136:139], v[242:245], v[48:63]
	v_pk_fma_f32 v[138:139], v[64:65], s[26:27], v[236:237] op_sel_hi:[1,0,0]
	v_pk_fma_f32 v[136:137], v[66:67], s[26:27], v[236:237] op_sel_hi:[1,0,0]
	v_pk_fma_f32 v[162:163], v[74:75], s[26:27], v[236:237] op_sel_hi:[1,0,0]
	v_pk_fma_f32 v[160:161], v[76:77], s[26:27], v[236:237] op_sel_hi:[1,0,0]
	s_waitcnt lgkmcnt(0)
	v_mfma_f32_32x32x16_bf16 v[48:63], v[208:211], v[246:249], v[48:63]
	v_exp_f32_e32 v211, v90
	v_exp_f32_e32 v208, v92
	v_exp_f32_e32 v210, v93
	v_exp_f32_e32 v209, v95
	v_add_f32_e32 v64, v203, v204
	v_fmac_f32_e32 v64, v197, v140
	v_add_f32_e32 v140, v215, v216
	s_addk_i32 s13, 0x80
	s_addk_i32 s14, 0x80
	v_fmac_f32_e32 v140, v64, v206
	s_cbranch_vccz .LBB0_2020
	s_and_saveexec_b64 s[10:11], s[4:5]
	ds_write_b32 v189, v205 offset:128
	s_or_b64 exec, exec, s[10:11]
	s_waitcnt lgkmcnt(0)
	v_add_u32_e32 v164, s12, v169
	ds_read_b128 v[238:241], v164 offset:224
	ds_read_b128 v[242:245], v164 offset:192
	ds_read_b128 v[246:249], v164 offset:160
	ds_read_b128 v[250:253], v164 offset:128
	s_waitcnt lgkmcnt(3)
	v_pk_mul_f32 v[12:13], v[12:13], v[238:239]
	s_waitcnt lgkmcnt(2)
	v_pk_mul_f32 v[8:9], v[8:9], v[242:243]
	s_waitcnt lgkmcnt(1)
	v_pk_mul_f32 v[4:5], v[4:5], v[246:247]
	v_pk_mul_f32 v[14:15], v[14:15], v[240:241]
	v_pk_mul_f32 v[10:11], v[10:11], v[244:245]
	v_pk_mul_f32 v[6:7], v[6:7], v[248:249]
	s_waitcnt lgkmcnt(0)
	v_pk_mul_f32 v[2:3], v[2:3], v[252:253]
	v_pk_mul_f32 v[0:1], v[0:1], v[250:251]
	v_pk_mul_f32 v[44:45], v[44:45], v[238:239]
	v_pk_mul_f32 v[40:41], v[40:41], v[242:243]
	v_pk_mul_f32 v[36:37], v[36:37], v[246:247]
	v_pk_mul_f32 v[46:47], v[46:47], v[240:241]
	v_pk_mul_f32 v[42:43], v[42:43], v[244:245]
	v_pk_mul_f32 v[38:39], v[38:39], v[248:249]
	v_pk_mul_f32 v[34:35], v[34:35], v[252:253]
	v_pk_mul_f32 v[32:33], v[32:33], v[250:251]
	v_pk_mul_f32 v[28:29], v[28:29], v[238:239]
	v_pk_mul_f32 v[24:25], v[24:25], v[242:243]
	v_pk_mul_f32 v[20:21], v[20:21], v[246:247]
	v_pk_mul_f32 v[30:31], v[30:31], v[240:241]
	v_pk_mul_f32 v[26:27], v[26:27], v[244:245]
	v_pk_mul_f32 v[22:23], v[22:23], v[248:249]
	v_pk_mul_f32 v[18:19], v[18:19], v[252:253]
	v_pk_mul_f32 v[16:17], v[16:17], v[250:251]
	v_pk_mul_f32 v[60:61], v[60:61], v[238:239]
	v_pk_mul_f32 v[56:57], v[56:57], v[242:243]
	v_pk_mul_f32 v[52:53], v[52:53], v[246:247]
	v_pk_mul_f32 v[62:63], v[62:63], v[240:241]
	v_pk_mul_f32 v[58:59], v[58:59], v[244:245]
	v_pk_mul_f32 v[54:55], v[54:55], v[248:249]
	v_pk_mul_f32 v[50:51], v[50:51], v[252:253]
	v_pk_mul_f32 v[48:49], v[48:49], v[250:251]

.LBB0_2046:
	s_waitcnt lgkmcnt(0)
	s_barrier
	ds_read_b128 v[0:3], v146
	ds_read_b128 v[4:7], v147
	ds_read_b128 v[120:123], v146 offset:32
	ds_read_b128 v[124:127], v147 offset:32
	s_waitcnt lgkmcnt(0)
	v_mfma_f32_32x32x16_bf16 v[0:15], v[0:3], v[4:7], 0
	v_add_u32_e32 v132, 0x4a00, v154
	v_mfma_f32_32x32x16_bf16 v[0:15], v[120:123], v[124:127], v[0:15]
	ds_read_b128 v[120:123], v146 offset:64
	ds_read_b128 v[124:127], v147 offset:64
	ds_read_b128 v[160:163], v146 offset:96
	ds_read_b128 v[164:167], v147 offset:96
	s_waitcnt lgkmcnt(2)
	v_mfma_f32_32x32x16_bf16 v[0:15], v[120:123], v[124:127], v[0:15]
	s_waitcnt lgkmcnt(0)
	v_mfma_f32_32x32x16_bf16 v[0:15], v[160:163], v[164:167], v[0:15]
	s_nop 11
	v_cndmask_b32_e64 v0, 0, v0, s[6:7]
	v_cndmask_b32_e64 v1, 0, v1, s[8:9]
	v_cndmask_b32_e64 v2, 0, v2, s[10:11]
	v_cndmask_b32_e64 v3, 0, v3, s[12:13]
	v_cndmask_b32_e64 v4, 0, v4, s[14:15]
	v_cndmask_b32_e64 v5, 0, v5, s[16:17]
	v_cndmask_b32_e64 v6, 0, v6, s[18:19]
	v_cndmask_b32_e64 v7, 0, v7, s[20:21]
	v_cndmask_b32_e64 v8, 0, v8, s[22:23]
	v_cndmask_b32_e64 v9, 0, v9, s[24:25]
	v_cvt_pk_bf16_f32 v0, v0, v0
	v_cvt_pk_bf16_f32 v1, v1, v1
	v_cvt_pk_bf16_f32 v2, v2, v2
	v_cvt_pk_bf16_f32 v3, v3, v3
	v_cvt_pk_bf16_f32 v4, v4, v4
	v_cvt_pk_bf16_f32 v5, v5, v5
	v_cvt_pk_bf16_f32 v6, v6, v6
	v_cvt_pk_bf16_f32 v7, v7, v7
	v_cvt_pk_bf16_f32 v8, v8, v8
	v_cvt_pk_bf16_f32 v9, v9, v9
	ds_write_b16 v151, v0
	ds_write_b16 v151, v1 offset:144
	ds_write_b16 v151, v2 offset:288
	ds_write_b16 v151, v3 offset:432
	ds_write_b16 v151, v4 offset:1152
	ds_write_b16 v151, v5 offset:1296
	ds_write_b16 v151, v6 offset:1440
	ds_write_b16 v151, v7 offset:1584
	ds_write_b16 v151, v8 offset:2304
	ds_write_b16 v151, v9 offset:2448
	v_cndmask_b32_e64 v0, 0, v10, s[26:27]
	v_cvt_pk_bf16_f32 v0, v0, v0
	ds_write_b16 v151, v0 offset:2592
	v_cndmask_b32_e64 v0, 0, v11, s[28:29]
	v_cvt_pk_bf16_f32 v0, v0, v0
	ds_write_b16 v151, v0 offset:2736
	v_cndmask_b32_e64 v0, 0, v12, s[30:31]
	v_cvt_pk_bf16_f32 v0, v0, v0
	ds_write_b16 v151, v0 offset:3456
	v_cndmask_b32_e64 v0, 0, v13, s[34:35]
	v_cvt_pk_bf16_f32 v0, v0, v0
	ds_write_b16 v151, v0 offset:3600
	v_cndmask_b32_e64 v0, 0, v14, s[36:37]
	v_cvt_pk_bf16_f32 v0, v0, v0
	ds_write_b16 v151, v0 offset:3744
	v_cndmask_b32_e64 v0, 0, v15, s[38:39]
	v_cvt_pk_bf16_f32 v0, v0, v0
	ds_write_b16 v151, v0 offset:3888
	s_waitcnt lgkmcnt(0)
	s_barrier
	ds_read_b128 v[0:3], v148
	ds_read_b128 v[120:123], v149
	ds_read_b128 v[124:127], v148 offset:32
	ds_read_b128 v[160:163], v149 offset:32
	s_waitcnt lgkmcnt(2)
	v_mfma_f32_32x32x16_bf16 v[0:15], v[0:3], v[120:123], 0
	s_waitcnt lgkmcnt(0)
	v_mfma_f32_32x32x16_bf16 v[0:15], v[124:127], v[160:163], v[0:15]
	ds_read_b128 v[124:127], v148 offset:64
	ds_read_b128 v[164:167], v149 offset:64
	ds_read_b128 v[168:171], v148 offset:96
	ds_read_b128 v[172:175], v149 offset:96
	s_waitcnt lgkmcnt(2)
	v_mfma_f32_32x32x16_bf16 v[0:15], v[124:127], v[164:167], v[0:15]
	s_waitcnt lgkmcnt(0)
	v_mfma_f32_32x32x16_bf16 v[0:15], v[168:171], v[172:175], v[0:15]
	ds_read_b128 v[124:127], v148 offset:9216
	ds_read_b128 v[168:171], v148 offset:9248
	s_waitcnt lgkmcnt(1)
	v_mfma_f32_32x32x16_bf16 v[0:15], v[124:127], v[120:123], v[0:15]
	ds_read_b128 v[120:123], v148 offset:9280
	ds_read_b128 v[124:127], v148 offset:9312
	s_waitcnt lgkmcnt(2)
	v_mfma_f32_32x32x16_bf16 v[0:15], v[168:171], v[160:163], v[0:15]
	v_add_u32_e32 v160, 0x4e00, v154
	v_add_u32_e32 v161, 0x5a00, v154
	v_add_u32_e32 v162, 0x5e00, v154
	v_add_u32_e32 v163, 0x6a00, v154
	v_lshlrev_b32_e32 v171, 2, v138
	v_and_b32_e32 v168, 64, v157
	v_xor_b32_e32 v169, 2, v157
	s_waitcnt lgkmcnt(1)
	v_mfma_f32_32x32x16_bf16 v[0:15], v[120:123], v[164:167], v[0:15]
	ds_read_b128 v[120:123], v152 offset:53760
	v_add_u32_e32 v164, 0x6e00, v154
	v_add_u32_e32 v165, 0x7a00, v154
	v_add_u32_e32 v166, 0x7e00, v154
	v_xor_b32_e32 v167, 1, v157
	v_xor_b32_e32 v170, 4, v157
	s_waitcnt lgkmcnt(1)
	v_mfma_f32_32x32x16_bf16 v[0:15], v[124:127], v[172:175], v[0:15]
	ds_read_b128 v[124:127], v152 offset:53792
	s_waitcnt vmcnt(1)
	v_lshlrev_b32_e32 v172, 16, v84
	v_and_b32_e32 v84, 0xffff0000, v84
	s_waitcnt lgkmcnt(1)
	v_mfma_f32_32x32x16_bf16 v[0:15], v[120:123], v[116:119], v[0:15]
	ds_read_b128 v[116:119], v152 offset:53824
	v_add_u32_e32 v121, 64, v168
	v_cmp_lt_i32_e32 vcc, v167, v121
	v_mul_f32_e32 v122, 0xbfb8aa3b, v172
	v_lshlrev_b32_e32 v120, 16, v85
	v_mul_f32_e32 v123, 0xbfb8aa3b, v84
	v_and_b32_e32 v85, 0xffff0000, v85
	s_waitcnt lgkmcnt(1)
	v_mfma_f32_32x32x16_bf16 v[0:15], v[124:127], v[112:115], v[0:15]
	ds_read_b128 v[112:115], v152 offset:53856
	v_cndmask_b32_e32 v126, v157, v167, vcc
	v_cmp_lt_i32_e32 vcc, v169, v121
	v_mul_f32_e32 v124, 0xbfb8aa3b, v120
	v_mul_f32_e32 v125, 0xbfb8aa3b, v85
	v_cndmask_b32_e32 v127, v157, v169, vcc
	v_cmp_lt_i32_e32 vcc, v170, v121
	s_waitcnt lgkmcnt(1)
	v_mfma_f32_32x32x16_bf16 v[0:15], v[116:119], v[108:111], v[0:15]
	ds_read_b128 v[108:111], v153
	v_exp_f32_e32 v117, v122
	v_lshlrev_b32_e32 v122, 2, v126
	v_cndmask_b32_e32 v116, v157, v170, vcc
	v_exp_f32_e32 v118, v123
	v_exp_f32_e32 v119, v124
	v_exp_f32_e32 v121, v125
	s_waitcnt lgkmcnt(1)
	v_mfma_f32_32x32x16_bf16 v[0:15], v[112:115], v[104:107], v[0:15]
	ds_read_b128 v[104:107], v153 offset:32
	v_lshlrev_b32_e32 v112, 2, v127
	v_lshlrev_b32_e32 v113, 2, v116
	v_add_f32_e32 v114, 1.0, v117
	v_add_f32_e32 v115, 1.0, v118
	v_add_f32_e32 v116, 1.0, v119
	v_add_f32_e32 v117, 1.0, v121
	s_waitcnt lgkmcnt(1)
	v_mfma_f32_32x32x16_bf16 v[0:15], v[108:111], v[100:103], v[0:15]
	ds_read_b128 v[100:103], v153 offset:64
	v_div_scale_f32 v108, s[42:43], v114, v114, v172
	v_div_scale_f32 v110, s[42:43], v115, v115, v84
	v_rcp_f32_e32 v111, v110
	v_div_scale_f32 v109, s[46:47], v172, v114, v172
	s_waitcnt lgkmcnt(1)
	v_mfma_f32_32x32x16_bf16 v[0:15], v[104:107], v[96:99], v[0:15]
	ds_read_b128 v[96:99], v153 offset:96
	v_div_scale_f32 v105, s[42:43], v116, v116, v120
	v_rcp_f32_e32 v107, v108
	v_rcp_f32_e32 v118, v105
	v_fma_f32 v123, -v110, v111, 1.0
	v_div_scale_f32 v104, s[44:45], v84, v115, v84
	s_waitcnt lgkmcnt(1)
	v_mfma_f32_32x32x16_bf16 v[0:15], v[100:103], v[92:95], v[0:15]
	v_fma_f32 v121, -v108, v107, 1.0
	v_fma_f32 v124, -v105, v118, 1.0
	v_fmac_f32_e32 v107, v121, v107
	v_div_scale_f32 v106, s[42:43], v120, v116, v120
	v_fmac_f32_e32 v111, v123, v111
	v_fmac_f32_e32 v118, v124, v118
	s_waitcnt lgkmcnt(0)
	v_mfma_f32_32x32x16_bf16 v[0:15], v[96:99], v[88:91], v[0:15]
	s_nop 11
	ds_write2_b32 v132, v0, v1 offset1:132
	ds_write2_b32 v160, v2, v3 offset0:8 offset1:140
	ds_write2_b32 v161, v4, v5 offset0:32 offset1:164
	ds_write2_b32 v162, v6, v7 offset0:40 offset1:172
	ds_write2_b32 v163, v8, v9 offset0:64 offset1:196
	ds_write2_b32 v164, v10, v11 offset0:72 offset1:204
	ds_write2_b32 v165, v12, v13 offset0:96 offset1:228
	ds_write2_b32 v166, v14, v15 offset0:104 offset1:236
	s_waitcnt lgkmcnt(0)
	s_barrier
	ds_read_b128 v[88:91], v150 offset:18944
	ds_read_b128 v[92:95], v150 offset:18960
	ds_read_b128 v[8:11], v150 offset:18976
	ds_read_b128 v[0:3], v150 offset:18992
	global_load_dwordx4 v[96:99], v171, s[68:69] offset:528
	global_load_dwordx4 v[100:103], v171, s[68:69] offset:512
	s_waitcnt lgkmcnt(3)
	v_mul_f32_e32 v4, v89, v89
	v_fmac_f32_e32 v4, v88, v88
	v_fmac_f32_e32 v4, v90, v90
	v_fmac_f32_e32 v4, v91, v91
	s_waitcnt lgkmcnt(2)
	v_fmac_f32_e32 v4, v92, v92
	v_fmac_f32_e32 v4, v93, v93
	v_fmac_f32_e32 v4, v94, v94
	v_fmac_f32_e32 v4, v95, v95
	s_waitcnt lgkmcnt(1)
	v_fmac_f32_e32 v4, v8, v8
	v_fmac_f32_e32 v4, v9, v9
	v_fmac_f32_e32 v4, v10, v10
	v_fmac_f32_e32 v4, v11, v11
	s_waitcnt lgkmcnt(0)
	v_fmac_f32_e32 v4, v0, v0
	v_fmac_f32_e32 v4, v1, v1
	v_fmac_f32_e32 v4, v2, v2
	v_fmac_f32_e32 v4, v3, v3
	ds_bpermute_b32 v5, v122, v4
	v_mul_f32_e32 v121, v109, v107
	v_mul_f32_e32 v122, v106, v118
	v_fma_f32 v6, -v108, v121, v109
	v_fma_f32 v12, -v105, v122, v106
	s_waitcnt lgkmcnt(0)
	v_add_f32_e32 v4, v4, v5
	ds_bpermute_b32 v5, v112, v4
	v_mul_f32_e32 v112, v104, v111
	v_fma_f32 v7, -v110, v112, v104
	v_fmac_f32_e32 v121, v6, v107
	s_waitcnt lgkmcnt(0)
	v_add_f32_e32 v4, v4, v5
	ds_bpermute_b32 v5, v113, v4
	v_fmac_f32_e32 v112, v7, v111
	v_fmac_f32_e32 v122, v12, v118
	v_fma_f32 v105, -v105, v122, v106
	v_fma_f32 v108, -v108, v121, v109
	s_waitcnt lgkmcnt(0)
	v_add_f32_e32 v4, v4, v5
	v_fmamk_f32 v4, v4, 0x3c000000, v155
	v_mul_f32_e32 v5, 0x4f800000, v4
	v_cmp_gt_f32_e32 vcc, s81, v4
	v_fma_f32 v104, -v110, v112, v104
	s_nop 0
	v_cndmask_b32_e32 v4, v4, v5, vcc
	v_sqrt_f32_e32 v5, v4
	s_nop 0
	v_add_u32_e32 v6, -1, v5
	v_add_u32_e32 v7, 1, v5
	v_fma_f32 v12, -v6, v5, v4
	v_fma_f32 v13, -v7, v5, v4
	v_cmp_ge_f32_e64 s[50:51], 0, v12
	s_nop 1
	v_cndmask_b32_e64 v5, v5, v6, s[50:51]
	v_cmp_lt_f32_e64 s[50:51], 0, v13
	s_nop 1
	v_cndmask_b32_e64 v5, v5, v7, s[50:51]
	v_mul_f32_e32 v6, 0x37800000, v5
	v_cndmask_b32_e32 v5, v5, v6, vcc
	v_cmp_class_f32_e32 vcc, v4, v156
	s_nop 1
	v_cndmask_b32_e32 v106, v5, v4, vcc
	v_rcp_f32_e32 v110, v106
	global_load_dwordx4 v[4:7], v171, s[68:69] offset:560
	global_load_dwordx4 v[12:15], v171, s[68:69] offset:544
	v_mul_f32_e32 v109, 1.0, v110
	s_mov_b64 vcc, s[46:47]
	v_div_fmas_f32 v107, v108, v107, v121
	s_mov_b64 vcc, s[44:45]
	v_mov_b32_e32 v106, v109
	v_div_fmas_f32 v104, v104, v111, v112
	s_mov_b64 vcc, s[42:43]
	v_mul_f32_e32 v89, v89, v106
	v_mul_f32_e32 v90, v90, v106
	v_div_fixup_f32 v84, v104, v115, v84
	v_div_fmas_f32 v104, v105, v118, v122
	v_div_fixup_f32 v104, v104, v116, v120
	s_waitcnt vmcnt(2)
	v_mul_f32_e32 v89, v101, v89
	v_mul_f32_e32 v90, v102, v90
	v_mul_f32_e32 v84, v84, v89
	v_mul_f32_e32 v89, v104, v90
	v_rcp_f32_e32 v90, v117
	v_mul_f32_e32 v88, v88, v106
	v_mul_f32_e32 v88, v100, v88
	v_mul_f32_e32 v91, v91, v106
	v_lshlrev_b32_e32 v102, 16, v86
	v_mul_f32_e32 v91, v103, v91
	v_mul_f32_e32 v103, 0xbfb8aa3b, v102
	v_exp_f32_e32 v103, v103
	v_mul_f32_e32 v90, v85, v90
	v_mov_b32_e32 v85, v90
	v_add_f32_e32 v90, 1.0, v103
	v_mul_f32_e32 v85, v85, v91
	v_rcp_f32_e32 v100, v90
	v_mul_f32_e32 v92, v92, v106
	v_mul_f32_e32 v92, v96, v92
	v_and_b32_e32 v86, 0xffff0000, v86
	v_mul_f32_e32 v96, 0xbfb8aa3b, v86
	v_exp_f32_e32 v96, v96
	v_mul_f32_e32 v91, v102, v100
	v_mov_b32_e32 v90, v91
	v_mul_f32_e32 v90, v90, v92
	v_add_f32_e32 v91, 1.0, v96
	v_rcp_f32_e32 v96, v91
	v_mul_f32_e32 v93, v93, v106
	v_mul_f32_e32 v93, v97, v93
	v_mul_f32_e32 v94, v94, v106
	v_lshlrev_b32_e32 v97, 16, v87
	v_mul_f32_e32 v101, 0xbfb8aa3b, v97
	v_exp_f32_e32 v101, v101
	v_mul_f32_e32 v92, v86, v96
	v_mov_b32_e32 v86, v92
	v_mul_f32_e32 v86, v86, v93
	v_add_f32_e32 v91, 1.0, v101
	v_rcp_f32_e32 v93, v91
	v_mul_f32_e32 v94, v94, v98
	v_and_b32_e32 v87, 0xffff0000, v87
	v_mul_f32_e32 v8, v8, v106
	v_mul_f32_e32 v96, 0xbfb8aa3b, v87
	v_exp_f32_e32 v96, v96
	v_mul_f32_e32 v92, v97, v93
	v_mov_b32_e32 v91, v92
	v_mul_f32_e32 v91, v91, v94
	v_add_f32_e32 v92, 1.0, v96
	v_rcp_f32_e32 v94, v92
	v_mul_f32_e32 v95, v95, v106
	s_waitcnt vmcnt(0)
	v_mul_f32_e32 v8, v8, v12
	v_mul_f32_e32 v95, v95, v99
	v_lshlrev_b32_e32 v96, 16, v80
	v_mul_f32_e32 v98, 0xbfb8aa3b, v96
	v_exp_f32_e32 v98, v98
	v_mul_f32_e32 v93, v87, v94
	v_mov_b32_e32 v87, v93
	v_mul_f32_e32 v87, v87, v95
	v_add_f32_e32 v92, 1.0, v98
	v_rcp_f32_e32 v94, v92
	v_and_b32_e32 v80, 0xffff0000, v80
	v_mul_f32_e32 v9, v9, v106
	v_mul_f32_e32 v9, v9, v13
	v_mul_f32_e32 v93, 0xbfb8aa3b, v80
	v_exp_f32_e32 v93, v93
	v_mul_f32_e32 v12, v96, v94
	v_mul_f32_e32 v8, v12, v8
	v_add_f32_e32 v12, 1.0, v93
	v_rcp_f32_e32 v93, v12
	v_mul_f32_e32 v10, v10, v106
	v_mul_f32_e32 v10, v10, v14
	v_mul_f32_e32 v11, v11, v106
	v_lshlrev_b32_e32 v92, 16, v81
	v_mul_f32_e32 v95, 0xbfb8aa3b, v92
	v_exp_f32_e32 v95, v95
	v_mul_f32_e32 v13, v80, v93
	v_mov_b32_e32 v12, v13
	v_mul_f32_e32 v9, v12, v9
	v_add_f32_e32 v12, 1.0, v95
	v_rcp_f32_e32 v80, v12
	v_mul_f32_e32 v11, v11, v15
	v_mul_f32_e32 v0, v0, v106
	v_mul_f32_e32 v0, v0, v4
	v_and_b32_e32 v14, 0xffff0000, v81
	v_mul_f32_e32 v81, 0xbfb8aa3b, v14
	v_exp_f32_e32 v81, v81
	v_mul_f32_e32 v13, v92, v80
	v_mov_b32_e32 v12, v13
	v_mul_f32_e32 v10, v12, v10
	v_add_f32_e32 v12, 1.0, v81
	v_rcp_f32_e32 v80, v12
	v_div_fixup_f32 v107, v107, v114, v172
	v_mul_f32_e32 v88, v107, v88
	v_med3_f32 v88, v88, s82, v158
	v_lshlrev_b32_e32 v15, 16, v82
	v_mul_f32_e32 v92, 0xbfb8aa3b, v15
	v_exp_f32_e32 v92, v92
	v_mul_f32_e32 v13, v14, v80
	v_mov_b32_e32 v12, v13
	v_mul_f32_e32 v11, v12, v11
	v_add_f32_e32 v12, 1.0, v92
	v_rcp_f32_e32 v14, v12
	v_med3_f32 v84, v84, s82, v158
	v_med3_f32 v90, v90, s82, v158
	v_med3_f32 v86, v86, s82, v158
	v_and_b32_e32 v13, 0xffff0000, v82
	v_mul_f32_e32 v81, 0xbfb8aa3b, v13
	v_exp_f32_e32 v81, v81
	v_mul_f32_e32 v4, v15, v14
	v_mul_f32_e32 v0, v4, v0
	v_add_f32_e32 v4, 1.0, v81
	v_rcp_f32_e32 v14, v4
	v_med3_f32 v15, v0, s82, v158
	v_mul_f32_e32 v0, v1, v106
	v_mul_f32_e32 v0, v0, v5
	v_lshlrev_b32_e32 v12, 16, v83
	v_mul_f32_e32 v80, 0xbfb8aa3b, v12
	v_exp_f32_e32 v80, v80
	v_mul_f32_e32 v1, v13, v14
	v_mul_f32_e32 v0, v1, v0
	v_add_f32_e32 v1, 1.0, v80
	v_rcp_f32_e32 v5, v1
	v_med3_f32 v13, v0, s82, v158
	v_mul_f32_e32 v0, v2, v106
	v_mul_f32_e32 v0, v0, v6
	v_and_b32_e32 v4, 0xffff0000, v83
	v_mul_f32_e32 v14, 0xbfb8aa3b, v4
	v_exp_f32_e32 v14, v14
	v_mul_f32_e32 v2, v12, v5
	v_mov_b32_e32 v1, v2
	v_mul_f32_e32 v0, v1, v0
	v_add_f32_e32 v1, 1.0, v14
	v_rcp_f32_e32 v5, v1
	v_med3_f32 v6, v0, s82, v158
	v_mul_f32_e32 v0, v3, v106
	v_mul_f32_e32 v0, v0, v7
	v_mul_f32_e32 v2, v4, v5
	v_mov_b32_e32 v1, v2
	v_mul_f32_e32 v0, v1, v0
	v_med3_f32 v7, v0, s82, v158
	v_add_u32_e32 v0, s67, v140
	v_ashrrev_i32_e32 v1, 31, v0
	v_lshlrev_b64 v[0:1], 11, v[0:1]
	s_lshl_b32 s42, s66, 7
	v_lshl_add_u64 v[0:1], s[58:59], 0, v[0:1]
	s_and_b32 s62, s42, 0x180
	v_lshl_add_u64 v[0:1], v[0:1], 0, s[62:63]
	v_med3_f32 v8, v8, s82, v158
	v_med3_f32 v9, v9, s82, v158
	v_lshl_add_u64 v[4:5], v[0:1], 0, v[138:139]
	v_mov_b32_e32 v0, v133
	v_mov_b32_e32 v1, v133
	v_mov_b32_e32 v2, v133
	v_mov_b32_e32 v3, v133
	v_cvt_pk_fp8_f32 v0, v88, v84
	v_cvt_pk_fp8_f32 v1, v90, v86
	v_cvt_pk_fp8_f32 v2, v8, v9
	v_cvt_pk_fp8_f32 v3, v15, v13
	v_med3_f32 v89, v89, s82, v158
	v_med3_f32 v85, v85, s82, v158
	v_med3_f32 v91, v91, s82, v158
	v_med3_f32 v87, v87, s82, v158
	v_med3_f32 v10, v10, s82, v158
	v_med3_f32 v11, v11, s82, v158
	v_cvt_pk_fp8_f32 v0, v89, v85 op_sel:[0,0,1]
	v_cvt_pk_fp8_f32 v1, v91, v87 op_sel:[0,0,1]
	v_cvt_pk_fp8_f32 v2, v10, v11 op_sel:[0,0,1]
	v_cvt_pk_fp8_f32 v3, v6, v7 op_sel:[0,0,1]
	v_add_co_u32_e32 v4, vcc, 0x35b80000, v4
	v_mov_b64_e32 v[90:91], v[70:71]
	s_nop 0
	v_addc_co_u32_e32 v5, vcc, 0, v5, vcc
	global_store_dwordx4 v[4:5], v[0:3], off offset:1536
	v_mov_b64_e32 v[94:95], v[66:67]
	v_mov_b64_e32 v[98:99], v[62:63]
	v_mov_b64_e32 v[102:103], v[58:59]
	v_mov_b64_e32 v[106:107], v[54:55]
	v_mov_b64_e32 v[110:111], v[50:51]
	v_mov_b64_e32 v[114:115], v[46:47]
	v_mov_b64_e32 v[118:119], v[42:43]
	v_mov_b64_e32 v[82:83], v[78:79]
	v_mov_b64_e32 v[86:87], v[74:75]
	v_mov_b64_e32 v[126:127], v[38:39]
	v_mov_b64_e32 v[122:123], v[34:35]
	v_mov_b64_e32 v[12:13], v[28:29]
	v_mov_b64_e32 v[8:9], v[24:25]
	v_mov_b64_e32 v[4:5], v[20:21]
	v_mov_b64_e32 v[0:1], v[16:17]
	s_mov_b64 s[42:43], 0
	v_mov_b64_e32 v[88:89], v[68:69]
	v_mov_b64_e32 v[92:93], v[64:65]
	v_mov_b64_e32 v[96:97], v[60:61]
	v_mov_b64_e32 v[100:101], v[56:57]
	v_mov_b64_e32 v[104:105], v[52:53]
	v_mov_b64_e32 v[108:109], v[48:49]
	v_mov_b64_e32 v[112:113], v[44:45]
	v_mov_b64_e32 v[116:117], v[40:41]
	v_mov_b64_e32 v[80:81], v[76:77]
	v_mov_b64_e32 v[84:85], v[72:73]
	v_mov_b64_e32 v[124:125], v[36:37]
	v_mov_b64_e32 v[120:121], v[32:33]
	v_mov_b64_e32 v[14:15], v[30:31]
	v_mov_b64_e32 v[10:11], v[26:27]
	v_mov_b64_e32 v[6:7], v[22:23]
	v_mov_b64_e32 v[2:3], v[18:19]

.LBB0_2210:
	s_add_i32 s24, s46, s50
	s_ashr_i32 s25, s24, 31
	s_lshl_b64 s[20:21], s[24:25], 12
	s_waitcnt lgkmcnt(3)
	v_lshl_add_u64 v[52:53], v[26:27], 0, s[20:21]
	global_load_dwordx2 v[2:3], v[52:53], off
	global_load_dwordx2 v[6:7], v[52:53], off offset:512
	global_load_dwordx2 v[10:11], v[52:53], off offset:1024
	global_load_dwordx2 v[16:17], v[52:53], off offset:1536
	s_add_i32 s22, s24, 1
	s_ashr_i32 s23, s22, 31
	s_lshl_b64 s[20:21], s[22:23], 12
	global_load_dwordx2 v[62:63], v[52:53], off offset:3584
	s_waitcnt vmcnt(4)
	v_and_b32_e32 v5, 0xffff0000, v3
	v_lshlrev_b32_e32 v0, 16, v2
	v_and_b32_e32 v1, 0xffff0000, v2
	v_lshlrev_b32_e32 v4, 16, v3
	v_mul_f32_e32 v2, v5, v5
	v_pk_fma_f32 v[18:19], v[4:5], v[4:5], v[2:3] op_sel_hi:[1,1,0]
	s_waitcnt vmcnt(3)
	v_lshlrev_b32_e32 v3, 16, v7
	v_lshlrev_b32_e32 v2, 16, v6
	v_and_b32_e32 v7, 0xffff0000, v7
	v_and_b32_e32 v6, 0xffff0000, v6
	s_waitcnt vmcnt(1)
	v_and_b32_e32 v13, 0xffff0000, v16
	v_mul_f32_e32 v12, v1, v1
	v_pk_mul_f32 v[8:9], v[6:7], v[6:7]
	s_waitcnt lgkmcnt(2)
	v_lshlrev_b32_e32 v15, 16, v16
	v_pk_fma_f32 v[46:47], v[0:1], v[0:1], v[12:13] op_sel_hi:[1,1,0]
	v_pk_fma_f32 v[20:21], v[2:3], v[2:3], v[8:9]
	v_mov_b32_e32 v14, v46
	v_mov_b32_e32 v48, v18
	v_mov_b32_e32 v49, v15
	v_and_b32_e32 v9, 0xffff0000, v10
	v_mul_f32_e32 v22, v13, v13
	v_pk_add_f32 v[18:19], v[46:47], v[18:19]
	v_pk_mul_f32 v[46:47], v[14:15], v[48:49]
	v_pk_add_f32 v[20:21], v[20:21], v[20:21] op_sel:[0,1] op_sel_hi:[1,0]
	v_lshlrev_b32_e32 v8, 16, v10
	v_lshlrev_b32_e32 v10, 16, v11
	v_and_b32_e32 v11, 0xffff0000, v11
	v_mov_b32_e32 v19, v47
	v_mov_b32_e32 v21, v22
	v_mul_f32_e32 v12, v9, v9
	v_lshlrev_b32_e32 v16, 16, v17
	v_and_b32_e32 v17, 0xffff0000, v17
	v_pk_add_f32 v[18:19], v[18:19], v[20:21]
	v_pk_fma_f32 v[20:21], v[8:9], v[8:9], v[12:13] op_sel_hi:[1,1,0]
	v_mul_f32_e32 v12, v11, v11
	v_mul_f32_e32 v50, v16, v16
	v_mul_f32_e32 v51, v17, v17
	v_pk_fma_f32 v[46:47], v[10:11], v[10:11], v[12:13] op_sel_hi:[1,1,0]
	v_mov_b32_e32 v21, v50
	v_mov_b32_e32 v47, v51
	v_pk_add_f32 v[20:21], v[20:21], v[46:47]
	global_load_dwordx2 v[46:47], v[52:53], off offset:2560
	global_load_dwordx2 v[50:51], v[52:53], off offset:3072
	s_waitcnt lgkmcnt(1)
	v_pk_add_f32 v[56:57], v[18:19], v[20:21]
	global_load_dwordx2 v[20:21], v[52:53], off offset:2048
	v_pk_add_f32 v[56:57], v[56:57], v[56:57] op_sel:[0,1] op_sel_hi:[1,0]
	s_waitcnt vmcnt(3) lgkmcnt(0)
	v_lshlrev_b32_e32 v55, 16, v62
	v_and_b32_e32 v53, 0xffff0000, v62
	v_lshlrev_b32_e32 v92, 16, v63
	v_and_b32_e32 v93, 0xffff0000, v63
	v_mov_b32_e32 v54, v56
	v_mov_b32_e32 v63, v55
	v_mul_f32_e32 v12, v53, v53
	v_mul_f32_e32 v14, v92, v92
	v_mul_f32_e32 v22, v93, v93
	s_waitcnt vmcnt(0)
	v_and_b32_e32 v95, 0xffff0000, v21
	v_and_b32_e32 v94, 0xffff0000, v20
	v_lshlrev_b32_e32 v19, 16, v21
	v_lshlrev_b32_e32 v18, 16, v20
	v_pk_mul_f32 v[20:21], v[94:95], v[94:95]
	s_nop 0
	v_pk_fma_f32 v[20:21], v[18:19], v[18:19], v[20:21]
	s_nop 0
	v_pk_add_f32 v[58:59], v[20:21], v[20:21] op_sel:[0,1] op_sel_hi:[1,0]
	v_lshlrev_b32_e32 v21, 16, v47
	v_lshlrev_b32_e32 v20, 16, v46
	v_and_b32_e32 v47, 0xffff0000, v47
	v_and_b32_e32 v46, 0xffff0000, v46
	v_pk_mul_f32 v[48:49], v[46:47], v[46:47]
	v_mov_b32_e32 v62, v58
	v_pk_fma_f32 v[60:61], v[20:21], v[20:21], v[48:49]
	v_pk_add_f32 v[56:57], v[56:57], v[58:59]
	v_pk_mul_f32 v[58:59], v[54:55], v[62:63]
	v_and_b32_e32 v49, 0xffff0000, v50
	v_mov_b32_e32 v57, v59
	v_pk_add_f32 v[58:59], v[60:61], v[60:61] op_sel:[0,1] op_sel_hi:[1,0]
	v_lshlrev_b32_e32 v48, 16, v50
	v_lshlrev_b32_e32 v50, 16, v51
	v_and_b32_e32 v51, 0xffff0000, v51
	v_mov_b32_e32 v59, v12
	v_mul_f32_e32 v12, v49, v49
	v_pk_add_f32 v[56:57], v[56:57], v[58:59]
	v_pk_fma_f32 v[58:59], v[48:49], v[48:49], v[12:13] op_sel_hi:[1,1,0]
	v_mul_f32_e32 v12, v51, v51
	v_pk_fma_f32 v[60:61], v[50:51], v[50:51], v[12:13] op_sel_hi:[1,1,0]
	v_mov_b32_e32 v59, v14
	v_mov_b32_e32 v61, v22
	v_pk_add_f32 v[58:59], v[58:59], v[60:61]
	s_nop 0
	v_pk_add_f32 v[56:57], v[56:57], v[58:59]
	s_nop 0
	v_add_f32_e32 v12, v56, v57
	v_lshl_add_u64 v[56:57], v[26:27], 0, s[20:21]
	global_load_dwordx2 v[58:59], v[56:57], off
	global_load_dwordx2 v[60:61], v[56:57], off offset:512
	global_load_dwordx2 v[62:63], v[56:57], off offset:1024
	s_min_i32 s20, s24, 0x4000
	s_ashr_i32 s20, s20, 12
	s_mul_hi_i32 s21, s20, 0xc000
	s_mul_i32 s20, s20, 0xc000
	s_add_u32 s20, s51, s20
	s_addc_u32 s21, s56, s21
	s_add_u32 s26, s20, 0x6000
	s_addc_u32 s27, s21, 0
	s_add_u32 s28, s20, 0x8000
	s_addc_u32 s29, s21, 0
	s_waitcnt vmcnt(2)
	v_and_b32_e32 v91, 0xffff0000, v59
	v_and_b32_e32 v89, 0xffff0000, v58
	s_waitcnt vmcnt(0)
	v_lshlrev_b32_e32 v80, 16, v62
	v_and_b32_e32 v81, 0xffff0000, v62
	v_lshlrev_b32_e32 v82, 16, v63
	v_and_b32_e32 v83, 0xffff0000, v63
	global_load_dwordx2 v[62:63], v[56:57], off offset:1536
	v_lshlrev_b32_e32 v90, 16, v59
	v_mul_f32_e32 v14, v91, v91
	v_lshlrev_b32_e32 v88, 16, v58
	v_pk_fma_f32 v[58:59], v[90:91], v[90:91], v[14:15] op_sel_hi:[1,1,0]
	v_and_b32_e32 v87, 0xffff0000, v61
	v_and_b32_e32 v86, 0xffff0000, v60
	v_mul_f32_e32 v14, v89, v89
	v_lshlrev_b32_e32 v85, 16, v61
	v_lshlrev_b32_e32 v84, 16, v60
	v_pk_mul_f32 v[60:61], v[86:87], v[86:87]
	v_mov_b32_e32 v64, v58
	v_pk_fma_f32 v[60:61], v[84:85], v[84:85], v[60:61]
	s_waitcnt vmcnt(0)
	v_lshlrev_b32_e32 v77, 16, v62
	v_and_b32_e32 v75, 0xffff0000, v62
	v_lshlrev_b32_e32 v78, 16, v63
	v_and_b32_e32 v79, 0xffff0000, v63
	v_pk_fma_f32 v[62:63], v[88:89], v[88:89], v[14:15] op_sel_hi:[1,1,0]
	v_mov_b32_e32 v65, v77
	v_mov_b32_e32 v76, v62
	v_mul_f32_e32 v22, v75, v75
	v_pk_add_f32 v[58:59], v[62:63], v[58:59]
	v_pk_mul_f32 v[62:63], v[76:77], v[64:65]
	v_pk_add_f32 v[60:61], v[60:61], v[60:61] op_sel:[0,1] op_sel_hi:[1,0]
	v_mov_b32_e32 v59, v63
	v_mov_b32_e32 v61, v22
	v_mul_f32_e32 v14, v81, v81
	v_pk_add_f32 v[58:59], v[58:59], v[60:61]
	v_pk_fma_f32 v[60:61], v[80:81], v[80:81], v[14:15] op_sel_hi:[1,1,0]
	v_mul_f32_e32 v14, v83, v83
	v_mul_f32_e32 v52, v78, v78
	v_mul_f32_e32 v54, v79, v79
	v_pk_fma_f32 v[62:63], v[82:83], v[82:83], v[14:15] op_sel_hi:[1,1,0]
	v_mov_b32_e32 v61, v52
	v_mov_b32_e32 v63, v54
	v_pk_add_f32 v[60:61], v[60:61], v[62:63]
	s_nop 0
	v_pk_add_f32 v[96:97], v[58:59], v[60:61]
	global_load_dwordx2 v[58:59], v[56:57], off offset:2048
	global_load_dwordx2 v[60:61], v[56:57], off offset:3584
	v_pk_add_f32 v[96:97], v[96:97], v[96:97] op_sel:[0,1] op_sel_hi:[1,0]
	s_waitcnt vmcnt(1)
	v_and_b32_e32 v73, 0xffff0000, v59
	v_and_b32_e32 v72, 0xffff0000, v58
	v_lshlrev_b32_e32 v71, 16, v59
	v_lshlrev_b32_e32 v70, 16, v58
	v_pk_mul_f32 v[58:59], v[72:73], v[72:73]
	s_nop 0
	v_pk_fma_f32 v[58:59], v[70:71], v[70:71], v[58:59]
	s_nop 0
	v_pk_add_f32 v[120:121], v[58:59], v[58:59] op_sel:[0,1] op_sel_hi:[1,0]
	global_load_dwordx2 v[58:59], v[56:57], off offset:2560
	v_mov_b32_e32 v124, v120
	s_waitcnt vmcnt(0)
	v_and_b32_e32 v69, 0xffff0000, v59
	v_and_b32_e32 v68, 0xffff0000, v58
	v_lshlrev_b32_e32 v67, 16, v59
	v_lshlrev_b32_e32 v66, 16, v58
	v_pk_mul_f32 v[58:59], v[68:69], v[68:69]
	s_nop 0
	v_pk_fma_f32 v[122:123], v[66:67], v[66:67], v[58:59]
	global_load_dwordx2 v[58:59], v[56:57], off offset:3072
	v_and_b32_e32 v57, 0xffff0000, v60
	v_mul_f32_e32 v14, v57, v57
	s_waitcnt vmcnt(0)
	v_lshlrev_b32_e32 v64, 16, v59
	v_and_b32_e32 v65, 0xffff0000, v59
	v_lshlrev_b32_e32 v59, 16, v60
	v_lshlrev_b32_e32 v62, 16, v58
	v_and_b32_e32 v63, 0xffff0000, v58
	v_mov_b32_e32 v58, v96
	v_mov_b32_e32 v125, v59
	v_pk_add_f32 v[96:97], v[96:97], v[120:121]
	v_pk_mul_f32 v[120:121], v[58:59], v[124:125]
	v_lshlrev_b32_e32 v60, 16, v61
	v_mov_b32_e32 v97, v121
	v_pk_add_f32 v[120:121], v[122:123], v[122:123] op_sel:[0,1] op_sel_hi:[1,0]
	v_and_b32_e32 v61, 0xffff0000, v61
	v_mov_b32_e32 v121, v14
	v_mul_f32_e32 v14, v63, v63
	v_pk_add_f32 v[96:97], v[96:97], v[120:121]
	v_pk_fma_f32 v[120:121], v[62:63], v[62:63], v[14:15] op_sel_hi:[1,1,0]
	v_mul_f32_e32 v14, v65, v65
	v_mul_f32_e32 v22, v60, v60
	v_mul_f32_e32 v52, v61, v61
	v_pk_fma_f32 v[122:123], v[64:65], v[64:65], v[14:15] op_sel_hi:[1,1,0]
	v_mov_b32_e32 v121, v22
	v_mov_b32_e32 v123, v52
	v_pk_add_f32 v[120:121], v[120:121], v[122:123]
	ds_bpermute_b32 v14, v25, v12
	v_pk_add_f32 v[96:97], v[96:97], v[120:121]
	global_load_dwordx4 v[120:123], v[28:29], off
	global_load_dwordx4 v[124:127], v110, s[28:29]
	global_load_dwordx4 v[128:131], v110, s[26:27]
	v_add_f32_e32 v56, v96, v97
	s_waitcnt lgkmcnt(0)
	v_add_f32_e32 v12, v12, v14
	ds_bpermute_b32 v14, v99, v12
	s_waitcnt lgkmcnt(0)
	v_add_f32_e32 v12, v12, v14
	ds_bpermute_b32 v14, v100, v12
	s_waitcnt lgkmcnt(0)
	v_add_f32_e32 v12, v12, v14
	ds_bpermute_b32 v14, v101, v12
	s_waitcnt lgkmcnt(0)
	v_add_f32_e32 v12, v12, v14
	ds_bpermute_b32 v14, v102, v12
	s_waitcnt lgkmcnt(0)
	v_add_f32_e32 v12, v12, v14
	ds_bpermute_b32 v14, v103, v12
	s_waitcnt lgkmcnt(0)
	v_add_f32_e32 v12, v12, v14
	v_fmamk_f32 v12, v12, 0x3a000000, v108
	v_cmp_gt_f32_e32 vcc, s61, v12
	v_mul_f32_e32 v14, 0x4f800000, v12
	s_nop 0
	v_cndmask_b32_e32 v12, v12, v14, vcc
	v_sqrt_f32_e32 v14, v12
	s_nop 0
	v_add_u32_e32 v22, -1, v14
	v_fma_f32 v52, -v22, v14, v12
	v_cmp_ge_f32_e64 s[20:21], 0, v52
	v_add_u32_e32 v52, 1, v14
	s_nop 0
	v_cndmask_b32_e64 v22, v14, v22, s[20:21]
	v_fma_f32 v14, -v52, v14, v12
	v_cmp_lt_f32_e64 s[20:21], 0, v14
	s_nop 1
	v_cndmask_b32_e64 v14, v22, v52, s[20:21]
	v_mul_f32_e32 v22, 0x37800000, v14
	v_cndmask_b32_e32 v14, v14, v22, vcc
	v_cmp_class_f32_e32 vcc, v12, v109
	s_nop 1
	v_cndmask_b32_e32 v12, v14, v12, vcc
	v_rcp_f32_e32 v22, v12
	s_lshl_b64 s[20:21], s[24:25], 11
	v_mul_f32_e32 v14, 1.0, v22
	v_mov_b32_e32 v22, v14
	v_pk_mul_f32 v[4:5], v[22:23], v[4:5] op_sel_hi:[0,1]
	v_pk_mul_f32 v[0:1], v[22:23], v[0:1] op_sel_hi:[0,1]
	s_waitcnt vmcnt(2)
	v_pk_mul_f32 v[96:97], v[120:121], v[0:1]
	v_pk_mul_f32 v[0:1], v[122:123], v[4:5]
	s_waitcnt vmcnt(1)
	v_pk_add_f32 v[4:5], v[126:127], 1.0 op_sel_hi:[1,0]
	v_pk_add_f32 v[120:121], v[124:125], 1.0 op_sel_hi:[1,0]
	s_waitcnt vmcnt(0)
	v_pk_fma_f32 v[0:1], v[4:5], v[0:1], v[130:131]
	v_pk_fma_f32 v[4:5], v[120:121], v[96:97], v[128:129]
	v_mov_b32_e32 v12, 0
	v_cvt_pk_fp8_f32 v12, v4, v5
	v_lshl_add_u64 v[96:97], v[30:31], 0, s[20:21]
	v_mov_b32_e32 v124, v3
	v_mov_b32_e32 v125, v7
	v_cvt_pk_fp8_f32 v12, v0, v1 op_sel:[0,0,1]
	v_mov_b32_e32 v3, v6
	v_pk_mul_f32 v[124:125], v[22:23], v[124:125] op_sel_hi:[0,1]
	v_pk_mul_f32 v[2:3], v[22:23], v[2:3] op_sel_hi:[0,1]
	global_store_dword v[96:97], v12, off
	global_load_dwordx4 v[120:123], v[32:33], off
	global_load_dwordx4 v[128:131], v111, s[28:29]
	global_load_dwordx4 v[132:135], v111, s[26:27]
	v_mov_b32_e32 v12, 0
	v_pk_mul_f32 v[10:11], v[22:23], v[10:11] op_sel_hi:[0,1]
	v_pk_mul_f32 v[8:9], v[22:23], v[8:9] op_sel_hi:[0,1]
	v_pk_mul_f32 v[16:17], v[16:17], v[22:23] op_sel_hi:[1,0]
	v_mov_b32_e32 v52, 0
	v_pk_mul_f32 v[50:51], v[22:23], v[50:51] op_sel_hi:[0,1]
	v_pk_mul_f32 v[48:49], v[22:23], v[48:49] op_sel_hi:[0,1]
	v_pk_mul_f32 v[92:93], v[92:93], v[22:23] op_sel_hi:[1,0]
	s_min_i32 s20, s22, 0x4000
	s_ashr_i32 s20, s20, 12
	s_mul_hi_i32 s21, s20, 0xc000
	s_mul_i32 s20, s20, 0xc000
	s_add_u32 s20, s51, s20
	s_addc_u32 s21, s56, s21
	s_add_u32 s24, s20, 0x6000
	s_addc_u32 s25, s21, 0
	v_cvt_pk_bf16_f32 v127, v4, v5
	v_cvt_pk_bf16_f32 v126, v0, v1
	s_waitcnt vmcnt(2)
	v_pk_mul_f32 v[6:7], v[2:3], v[120:121]
	v_pk_mul_f32 v[2:3], v[124:125], v[122:123]
	s_waitcnt vmcnt(1)
	v_pk_add_f32 v[122:123], v[128:129], 1.0 op_sel_hi:[1,0]
	v_pk_add_f32 v[120:121], v[130:131], 1.0 op_sel_hi:[1,0]
	s_waitcnt vmcnt(0)
	v_pk_fma_f32 v[6:7], v[6:7], v[122:123], v[132:133]
	v_pk_fma_f32 v[2:3], v[2:3], v[120:121], v[134:135]
	v_cvt_pk_fp8_f32 v12, v6, v7
	v_mov_b32_e32 v124, v21
	v_mov_b32_e32 v21, v46
	v_pk_mul_f32 v[20:21], v[22:23], v[20:21] op_sel_hi:[0,1]
	v_cvt_pk_fp8_f32 v12, v2, v3 op_sel:[0,0,1]
	v_mov_b32_e32 v125, v47
	v_pk_mul_f32 v[124:125], v[22:23], v[124:125] op_sel_hi:[0,1]
	v_cvt_pk_bf16_f32 v132, v2, v3
	global_store_dword v[96:97], v12, off offset:256
	global_load_dwordx4 v[120:123], v[34:35], off
	global_load_dwordx4 v[128:131], v112, s[28:29]
	global_load_dwordx4 v[134:137], v112, s[26:27]
	v_mov_b32_e32 v12, 0
	v_cvt_pk_bf16_f32 v133, v6, v7
	s_waitcnt vmcnt(2)
	v_pk_mul_f32 v[120:121], v[8:9], v[120:121]
	v_pk_mul_f32 v[8:9], v[10:11], v[122:123]
	s_waitcnt vmcnt(1)
	v_pk_add_f32 v[10:11], v[130:131], 1.0 op_sel_hi:[1,0]
	v_pk_add_f32 v[122:123], v[128:129], 1.0 op_sel_hi:[1,0]
	s_waitcnt vmcnt(0)
	v_pk_fma_f32 v[8:9], v[8:9], v[10:11], v[136:137]
	v_pk_fma_f32 v[10:11], v[120:121], v[122:123], v[134:135]
	v_cvt_pk_bf16_f32 v122, v8, v9
	s_nop 0
	v_cvt_pk_fp8_f32 v12, v10, v11
	v_cvt_pk_bf16_f32 v123, v10, v11
	v_cvt_pk_fp8_f32 v12, v8, v9 op_sel:[0,0,1]
	global_store_dword v[96:97], v12, off offset:512
	global_load_dwordx4 v[128:131], v[36:37], off
	global_load_dwordx4 v[134:137], v113, s[28:29]
	global_load_dwordx4 v[138:141], v113, s[26:27]
	v_mov_b32_e32 v12, v15
	v_pk_mul_f32 v[12:13], v[12:13], v[22:23] op_sel_hi:[1,0]
	s_waitcnt vmcnt(1)
	v_pk_add_f32 v[120:121], v[134:135], 1.0 op_sel_hi:[1,0]
	v_pk_mul_f32 v[14:15], v[12:13], v[128:129]
	v_pk_mul_f32 v[12:13], v[16:17], v[130:131]
	v_pk_add_f32 v[16:17], v[136:137], 1.0 op_sel_hi:[1,0]
	s_waitcnt vmcnt(0)
	v_pk_fma_f32 v[14:15], v[14:15], v[120:121], v[138:139]
	v_pk_fma_f32 v[12:13], v[12:13], v[16:17], v[140:141]
	v_mov_b32_e32 v16, 0
	v_cvt_pk_fp8_f32 v16, v14, v15
	v_mov_b32_e32 v17, v95
	v_cvt_pk_bf16_f32 v131, v14, v15
	v_cvt_pk_bf16_f32 v129, v12, v13
	v_cvt_pk_fp8_f32 v16, v12, v13 op_sel:[0,0,1]
	global_store_dword v[96:97], v16, off offset:768
	global_load_dwordx4 v[134:137], v[38:39], off
	global_load_dwordx4 v[138:141], v114, s[28:29]
	global_load_dwordx4 v[142:145], v114, s[26:27]
	v_mov_b32_e32 v16, v19
	v_mov_b32_e32 v19, v94
	v_pk_mul_f32 v[18:19], v[22:23], v[18:19] op_sel_hi:[0,1]
	v_pk_mul_f32 v[16:17], v[22:23], v[16:17] op_sel_hi:[0,1]
	s_waitcnt vmcnt(2)
	v_pk_mul_f32 v[18:19], v[18:19], v[134:135]
	s_waitcnt vmcnt(1)
	v_pk_add_f32 v[120:121], v[138:139], 1.0 op_sel_hi:[1,0]
	v_pk_mul_f32 v[16:17], v[16:17], v[136:137]
	s_waitcnt vmcnt(0)
	v_pk_fma_f32 v[18:19], v[18:19], v[120:121], v[142:143]
	v_pk_add_f32 v[94:95], v[140:141], 1.0 op_sel_hi:[1,0]
	v_cvt_pk_fp8_f32 v52, v18, v19
	v_pk_fma_f32 v[16:17], v[16:17], v[94:95], v[144:145]
	v_cvt_pk_bf16_f32 v120, v18, v19
	s_nop 0
	v_cvt_pk_fp8_f32 v52, v16, v17 op_sel:[0,0,1]
	v_cvt_pk_bf16_f32 v94, v16, v17
	global_store_dword v[96:97], v52, off offset:1024
	global_load_dwordx4 v[134:137], v[40:41], off
	global_load_dwordx4 v[138:141], v115, s[28:29]
	global_load_dwordx4 v[142:145], v115, s[26:27]
	v_mov_b32_e32 v52, 0
	s_waitcnt vmcnt(2)
	v_pk_mul_f32 v[46:47], v[20:21], v[134:135]
	s_waitcnt vmcnt(1)
	v_pk_add_f32 v[134:135], v[138:139], 1.0 op_sel_hi:[1,0]
	v_pk_mul_f32 v[20:21], v[124:125], v[136:137]
	s_waitcnt vmcnt(0)
	v_pk_fma_f32 v[46:47], v[46:47], v[134:135], v[142:143]
	v_pk_add_f32 v[124:125], v[140:141], 1.0 op_sel_hi:[1,0]
	v_cvt_pk_fp8_f32 v52, v46, v47
	v_pk_fma_f32 v[20:21], v[20:21], v[124:125], v[144:145]
	v_cvt_pk_bf16_f32 v130, v46, v47
	s_nop 0
	v_cvt_pk_fp8_f32 v52, v20, v21 op_sel:[0,0,1]
	v_cvt_pk_bf16_f32 v128, v20, v21
	global_store_dword v[96:97], v52, off offset:1280
	global_load_dwordx4 v[134:137], v[42:43], off
	global_load_dwordx4 v[138:141], v116, s[28:29]
	global_load_dwordx4 v[142:145], v116, s[26:27]
	v_mov_b32_e32 v52, 0
	s_waitcnt vmcnt(2)
	v_pk_mul_f32 v[124:125], v[48:49], v[134:135]
	v_pk_mul_f32 v[48:49], v[50:51], v[136:137]
	s_waitcnt vmcnt(1)
	v_pk_add_f32 v[50:51], v[140:141], 1.0 op_sel_hi:[1,0]
	v_pk_add_f32 v[134:135], v[138:139], 1.0 op_sel_hi:[1,0]
	s_waitcnt vmcnt(0)
	v_pk_fma_f32 v[48:49], v[48:49], v[50:51], v[144:145]
	v_pk_fma_f32 v[50:51], v[124:125], v[134:135], v[142:143]
	v_cvt_pk_bf16_f32 v95, v48, v49
	s_nop 0
	v_cvt_pk_fp8_f32 v52, v50, v51
	v_cvt_pk_bf16_f32 v121, v50, v51
	v_cvt_pk_fp8_f32 v52, v48, v49 op_sel:[0,0,1]
	global_store_dword v[96:97], v52, off offset:1536
	global_load_dwordx4 v[134:137], v[44:45], off
	global_load_dwordx4 v[138:141], v117, s[28:29]
	global_load_dwordx4 v[142:145], v117, s[26:27]
	v_mov_b32_e32 v52, v55
	v_pk_mul_f32 v[52:53], v[52:53], v[22:23] op_sel_hi:[1,0]
	v_mov_b32_e32 v22, 0
	s_add_u32 s26, s20, 0x8000
	s_addc_u32 s27, s21, 0
	s_waitcnt vmcnt(2)
	v_pk_mul_f32 v[54:55], v[52:53], v[134:135]
	s_waitcnt vmcnt(1)
	v_pk_add_f32 v[124:125], v[138:139], 1.0 op_sel_hi:[1,0]
	v_pk_mul_f32 v[52:53], v[92:93], v[136:137]
	s_waitcnt vmcnt(0)
	v_pk_fma_f32 v[54:55], v[54:55], v[124:125], v[142:143]
	v_pk_add_f32 v[92:93], v[140:141], 1.0 op_sel_hi:[1,0]
	v_cvt_pk_fp8_f32 v22, v54, v55
	v_pk_fma_f32 v[52:53], v[52:53], v[92:93], v[144:145]
	v_cvt_pk_bf16_f32 v125, v54, v55
	s_nop 0
	v_cvt_pk_fp8_f32 v22, v52, v53 op_sel:[0,0,1]
	v_cvt_pk_bf16_f32 v124, v52, v53
	global_store_dword v[96:97], v22, off offset:1792
	global_load_dwordx4 v[134:137], v[28:29], off
	global_load_dwordx4 v[138:141], v110, s[26:27]
	global_load_dwordx4 v[142:145], v110, s[24:25]
	ds_bpermute_b32 v22, v25, v56
	s_waitcnt lgkmcnt(0)
	v_add_f32_e32 v22, v56, v22
	ds_bpermute_b32 v56, v99, v22
	s_waitcnt lgkmcnt(0)
	v_add_f32_e32 v22, v22, v56
	ds_bpermute_b32 v56, v100, v22
	s_waitcnt lgkmcnt(0)
	v_add_f32_e32 v22, v22, v56
	ds_bpermute_b32 v56, v101, v22
	s_waitcnt lgkmcnt(0)
	v_add_f32_e32 v22, v22, v56
	ds_bpermute_b32 v56, v102, v22
	s_waitcnt lgkmcnt(0)
	v_add_f32_e32 v22, v22, v56
	ds_bpermute_b32 v56, v103, v22
	s_waitcnt lgkmcnt(0)
	v_add_f32_e32 v22, v22, v56
	v_fmamk_f32 v22, v22, 0x3a000000, v108
	v_cmp_gt_f32_e32 vcc, s61, v22
	v_mul_f32_e32 v56, 0x4f800000, v22
	s_waitcnt vmcnt(1)
	v_pk_add_f32 v[96:97], v[138:139], 1.0 op_sel_hi:[1,0]
	v_cndmask_b32_e32 v22, v22, v56, vcc
	v_sqrt_f32_e32 v56, v22
	s_nop 0
	v_add_u32_e32 v58, -1, v56
	v_fma_f32 v74, -v58, v56, v22
	v_cmp_ge_f32_e64 s[20:21], 0, v74
	v_add_u32_e32 v74, 1, v56
	s_nop 0
	v_cndmask_b32_e64 v58, v56, v58, s[20:21]
	v_fma_f32 v56, -v74, v56, v22
	v_cmp_lt_f32_e64 s[20:21], 0, v56
	s_nop 1
	v_cndmask_b32_e64 v56, v58, v74, s[20:21]
	v_mul_f32_e32 v58, 0x37800000, v56
	v_cndmask_b32_e32 v56, v56, v58, vcc
	v_cmp_class_f32_e32 vcc, v22, v109
	s_nop 1
	v_cndmask_b32_e32 v22, v56, v22, vcc
	v_rcp_f32_e32 v58, v22
	s_lshl_b64 s[20:21], s[22:23], 11
	v_mul_f32_e32 v56, 1.0, v58
	v_mov_b32_e32 v22, v56
	v_pk_mul_f32 v[90:91], v[22:23], v[90:91] op_sel_hi:[0,1]
	v_pk_mul_f32 v[88:89], v[22:23], v[88:89] op_sel_hi:[0,1]
	v_pk_mul_f32 v[92:93], v[134:135], v[88:89]
	v_pk_mul_f32 v[88:89], v[136:137], v[90:91]
	v_pk_add_f32 v[90:91], v[140:141], 1.0 op_sel_hi:[1,0]
	v_mov_b32_e32 v56, 0
	s_waitcnt vmcnt(0)
	v_pk_fma_f32 v[88:89], v[90:91], v[88:89], v[144:145]
	v_pk_fma_f32 v[90:91], v[96:97], v[92:93], v[142:143]
	v_lshl_add_u64 v[92:93], v[30:31], 0, s[20:21]
	v_cvt_pk_fp8_f32 v56, v90, v91
	v_mov_b32_e32 v96, v85
	v_mov_b32_e32 v85, v86
	v_pk_mul_f32 v[84:85], v[22:23], v[84:85] op_sel_hi:[0,1]
	v_cvt_pk_fp8_f32 v56, v88, v89 op_sel:[0,0,1]
	v_mov_b32_e32 v97, v87
	v_pk_mul_f32 v[96:97], v[22:23], v[96:97] op_sel_hi:[0,1]
	v_pk_mul_f32 v[82:83], v[22:23], v[82:83] op_sel_hi:[0,1]
	global_store_dword v[92:93], v56, off
	global_load_dwordx4 v[138:141], v[32:33], off
	global_load_dwordx4 v[142:145], v111, s[26:27]
	global_load_dwordx4 v[146:149], v111, s[24:25]
	v_mov_b32_e32 v56, 0
	v_pk_mul_f32 v[80:81], v[22:23], v[80:81] op_sel_hi:[0,1]
	v_mov_b32_e32 v74, v77
	v_pk_mul_f32 v[74:75], v[74:75], v[22:23] op_sel_hi:[1,0]
	v_pk_mul_f32 v[78:79], v[78:79], v[22:23] op_sel_hi:[1,0]
	v_pk_mul_f32 v[64:65], v[22:23], v[64:65] op_sel_hi:[0,1]
	v_pk_mul_f32 v[62:63], v[22:23], v[62:63] op_sel_hi:[0,1]
	v_pk_mul_f32 v[60:61], v[60:61], v[22:23] op_sel_hi:[1,0]
	v_cvt_pk_bf16_f32 v137, v90, v91
	v_cvt_pk_bf16_f32 v136, v88, v89
	s_waitcnt vmcnt(2)
	v_pk_mul_f32 v[86:87], v[84:85], v[138:139]
	s_waitcnt vmcnt(1)
	v_pk_add_f32 v[134:135], v[142:143], 1.0 op_sel_hi:[1,0]
	v_pk_mul_f32 v[84:85], v[96:97], v[140:141]
	s_waitcnt vmcnt(0)
	v_pk_fma_f32 v[86:87], v[86:87], v[134:135], v[146:147]
	v_pk_add_f32 v[96:97], v[144:145], 1.0 op_sel_hi:[1,0]
	v_cvt_pk_fp8_f32 v56, v86, v87
	v_pk_fma_f32 v[84:85], v[84:85], v[96:97], v[148:149]
	v_cvt_pk_bf16_f32 v147, v86, v87
	s_nop 0
	v_cvt_pk_fp8_f32 v56, v84, v85 op_sel:[0,0,1]
	v_cvt_pk_bf16_f32 v146, v84, v85
	global_store_dword v[92:93], v56, off offset:256
	global_load_dwordx4 v[138:141], v[34:35], off
	global_load_dwordx4 v[142:145], v112, s[26:27]
	global_load_dwordx4 v[148:151], v112, s[24:25]
	v_mov_b32_e32 v56, 0
	s_waitcnt vmcnt(2)
	v_pk_mul_f32 v[96:97], v[80:81], v[138:139]
	v_pk_mul_f32 v[80:81], v[82:83], v[140:141]
	s_waitcnt vmcnt(1)
	v_pk_add_f32 v[82:83], v[144:145], 1.0 op_sel_hi:[1,0]
	v_pk_add_f32 v[134:135], v[142:143], 1.0 op_sel_hi:[1,0]
	s_waitcnt vmcnt(0)
	v_pk_fma_f32 v[80:81], v[80:81], v[82:83], v[150:151]
	v_pk_fma_f32 v[82:83], v[96:97], v[134:135], v[148:149]
	v_cvt_pk_bf16_f32 v140, v80, v81
	s_nop 0
	v_cvt_pk_fp8_f32 v56, v82, v83
	v_cvt_pk_bf16_f32 v141, v82, v83
	v_cvt_pk_fp8_f32 v56, v80, v81 op_sel:[0,0,1]
	global_store_dword v[92:93], v56, off offset:512
	global_load_dwordx4 v[142:145], v[36:37], off
	global_load_dwordx4 v[148:151], v113, s[26:27]
	global_load_dwordx4 v[152:155], v113, s[24:25]
	v_mov_b32_e32 v56, 0
	s_waitcnt vmcnt(2)
	v_pk_mul_f32 v[76:77], v[74:75], v[142:143]
	s_waitcnt vmcnt(1)
	v_pk_add_f32 v[96:97], v[148:149], 1.0 op_sel_hi:[1,0]
	v_pk_mul_f32 v[74:75], v[78:79], v[144:145]
	s_waitcnt vmcnt(0)
	v_pk_fma_f32 v[76:77], v[76:77], v[96:97], v[152:153]
	v_pk_add_f32 v[78:79], v[150:151], 1.0 op_sel_hi:[1,0]
	v_cvt_pk_fp8_f32 v56, v76, v77
	v_pk_fma_f32 v[74:75], v[74:75], v[78:79], v[154:155]
	v_mov_b32_e32 v78, v71
	v_mov_b32_e32 v71, v72
	v_cvt_pk_fp8_f32 v56, v74, v75 op_sel:[0,0,1]
	v_pk_mul_f32 v[70:71], v[22:23], v[70:71] op_sel_hi:[0,1]
	v_mov_b32_e32 v79, v73
	v_pk_mul_f32 v[78:79], v[22:23], v[78:79] op_sel_hi:[0,1]
	global_store_dword v[92:93], v56, off offset:768
	global_load_dwordx4 v[148:151], v[38:39], off
	global_load_dwordx4 v[152:155], v114, s[26:27]
	global_load_dwordx4 v[156:159], v114, s[24:25]
	v_mov_b32_e32 v56, 0
	v_cvt_pk_bf16_f32 v145, v76, v77
	v_cvt_pk_bf16_f32 v144, v74, v75
	s_waitcnt vmcnt(2)
	v_pk_mul_f32 v[72:73], v[70:71], v[148:149]
	s_waitcnt vmcnt(1)
	v_pk_add_f32 v[96:97], v[152:153], 1.0 op_sel_hi:[1,0]
	v_pk_mul_f32 v[70:71], v[78:79], v[150:151]
	s_waitcnt vmcnt(0)
	v_pk_fma_f32 v[72:73], v[72:73], v[96:97], v[156:157]
	v_pk_add_f32 v[78:79], v[154:155], 1.0 op_sel_hi:[1,0]
	v_cvt_pk_fp8_f32 v56, v72, v73
	v_pk_fma_f32 v[70:71], v[70:71], v[78:79], v[158:159]
	v_mov_b32_e32 v78, v67
	v_mov_b32_e32 v67, v68
	v_cvt_pk_fp8_f32 v56, v70, v71 op_sel:[0,0,1]
	v_pk_mul_f32 v[66:67], v[22:23], v[66:67] op_sel_hi:[0,1]
	v_mov_b32_e32 v79, v69
	v_pk_mul_f32 v[78:79], v[22:23], v[78:79] op_sel_hi:[0,1]
	global_store_dword v[92:93], v56, off offset:1024
	global_load_dwordx4 v[148:151], v[40:41], off
	global_load_dwordx4 v[152:155], v115, s[26:27]
	global_load_dwordx4 v[156:159], v115, s[24:25]
	v_mov_b32_e32 v56, 0
	v_cvt_pk_bf16_f32 v139, v72, v73
	v_cvt_pk_bf16_f32 v138, v70, v71
	s_waitcnt vmcnt(2)
	v_pk_mul_f32 v[68:69], v[66:67], v[148:149]
	s_waitcnt vmcnt(1)
	v_pk_add_f32 v[96:97], v[152:153], 1.0 op_sel_hi:[1,0]
	v_pk_mul_f32 v[66:67], v[78:79], v[150:151]
	s_waitcnt vmcnt(0)
	v_pk_fma_f32 v[68:69], v[68:69], v[96:97], v[156:157]
	v_pk_add_f32 v[78:79], v[154:155], 1.0 op_sel_hi:[1,0]
	v_cvt_pk_fp8_f32 v56, v68, v69
	v_pk_fma_f32 v[66:67], v[66:67], v[78:79], v[158:159]
	v_cvt_pk_bf16_f32 v143, v68, v69
	s_nop 0
	v_cvt_pk_fp8_f32 v56, v66, v67 op_sel:[0,0,1]
	v_cvt_pk_bf16_f32 v142, v66, v67
	global_store_dword v[92:93], v56, off offset:1280
	global_load_dwordx4 v[148:151], v[42:43], off
	global_load_dwordx4 v[152:155], v116, s[26:27]
	global_load_dwordx4 v[156:159], v116, s[24:25]
	v_mov_b32_e32 v56, 0
	s_waitcnt vmcnt(2)
	v_pk_mul_f32 v[78:79], v[62:63], v[148:149]
	v_pk_mul_f32 v[62:63], v[64:65], v[150:151]
	s_waitcnt vmcnt(1)
	v_pk_add_f32 v[64:65], v[154:155], 1.0 op_sel_hi:[1,0]
	v_pk_add_f32 v[96:97], v[152:153], 1.0 op_sel_hi:[1,0]
	s_waitcnt vmcnt(0)
	v_pk_fma_f32 v[62:63], v[62:63], v[64:65], v[158:159]
	v_pk_fma_f32 v[64:65], v[78:79], v[96:97], v[156:157]
	v_cvt_pk_bf16_f32 v96, v62, v63
	s_nop 0
	v_cvt_pk_fp8_f32 v56, v64, v65
	v_cvt_pk_bf16_f32 v97, v64, v65
	v_cvt_pk_fp8_f32 v56, v62, v63 op_sel:[0,0,1]
	global_store_dword v[92:93], v56, off offset:1536
	global_load_dwordx4 v[148:151], v[44:45], off
	global_load_dwordx4 v[152:155], v117, s[26:27]
	global_load_dwordx4 v[156:159], v117, s[24:25]
	v_mov_b32_e32 v56, v59
	v_pk_mul_f32 v[56:57], v[56:57], v[22:23] op_sel_hi:[1,0]
	v_mov_b32_e32 v22, 0
	s_waitcnt vmcnt(2)
	v_pk_mul_f32 v[58:59], v[56:57], v[148:149]
	s_waitcnt vmcnt(1)
	v_pk_add_f32 v[78:79], v[152:153], 1.0 op_sel_hi:[1,0]
	v_pk_mul_f32 v[56:57], v[60:61], v[150:151]
	s_waitcnt vmcnt(0)
	v_pk_fma_f32 v[58:59], v[58:59], v[78:79], v[156:157]
	v_pk_add_f32 v[60:61], v[154:155], 1.0 op_sel_hi:[1,0]
	v_cvt_pk_fp8_f32 v22, v58, v59
	v_pk_fma_f32 v[56:57], v[56:57], v[60:61], v[158:159]
	ds_read_b128 v[148:151], v104
	v_cvt_pk_bf16_f32 v134, v56, v57
	v_cvt_pk_fp8_f32 v22, v56, v57 op_sel:[0,0,1]
	v_cvt_pk_bf16_f32 v135, v58, v59
	s_waitcnt lgkmcnt(0)
	v_mul_f32_e32 v60, v1, v151
	global_store_dword v[92:93], v22, off offset:1792
	v_mul_f32_e32 v22, v5, v149
	v_fmac_f32_e32 v22, v4, v148
	v_fmac_f32_e32 v60, v0, v150
	v_add_f32_e32 v22, v22, v60
	v_mul_f32_e32 v60, v91, v149
	v_mul_f32_e32 v61, v89, v151
	v_fmac_f32_e32 v60, v90, v148
	v_fmac_f32_e32 v61, v88, v150
	ds_read_b128 v[148:151], v104 offset:1024
	v_add_f32_e32 v60, v60, v61
	v_add_f32_e32 v22, 0, v22
	v_add_f32_e32 v60, 0, v60
	s_waitcnt lgkmcnt(0)
	v_mul_f32_e32 v61, v7, v149
	v_mul_f32_e32 v78, v3, v151
	v_fmac_f32_e32 v61, v6, v148
	v_fmac_f32_e32 v78, v2, v150
	v_add_f32_e32 v61, v61, v78
	v_add_f32_e32 v22, v22, v61
	v_mul_f32_e32 v61, v87, v149
	v_mul_f32_e32 v78, v85, v151
	v_fmac_f32_e32 v61, v86, v148
	v_fmac_f32_e32 v78, v84, v150
	ds_read_b128 v[148:151], v104 offset:2048
	v_add_f32_e32 v61, v61, v78
	v_add_f32_e32 v60, v60, v61
	s_waitcnt lgkmcnt(0)
	v_mul_f32_e32 v61, v11, v149
	v_mul_f32_e32 v78, v9, v151
	v_fmac_f32_e32 v61, v10, v148
	v_fmac_f32_e32 v78, v8, v150
	v_add_f32_e32 v61, v61, v78
	v_add_f32_e32 v22, v22, v61
	v_mul_f32_e32 v61, v83, v149
	v_mul_f32_e32 v78, v81, v151
	v_fmac_f32_e32 v61, v82, v148
	v_fmac_f32_e32 v78, v80, v150
	ds_read_b128 v[148:151], v104 offset:3072
	v_add_f32_e32 v61, v61, v78
	v_add_f32_e32 v60, v60, v61
	s_waitcnt lgkmcnt(0)
	v_mul_f32_e32 v61, v15, v149
	v_mul_f32_e32 v78, v13, v151
	v_fmac_f32_e32 v61, v14, v148
	v_fmac_f32_e32 v78, v12, v150
	v_add_f32_e32 v61, v61, v78
	v_add_f32_e32 v22, v22, v61
	v_mul_f32_e32 v61, v77, v149
	v_mul_f32_e32 v78, v75, v151
	v_fmac_f32_e32 v61, v76, v148
	v_fmac_f32_e32 v78, v74, v150
	ds_read_b128 v[148:151], v104 offset:4096
	v_add_f32_e32 v61, v61, v78
	v_add_f32_e32 v60, v60, v61
	s_waitcnt lgkmcnt(0)
	v_mul_f32_e32 v61, v19, v149
	v_mul_f32_e32 v78, v17, v151
	v_fmac_f32_e32 v61, v18, v148
	v_fmac_f32_e32 v78, v16, v150
	v_add_f32_e32 v61, v61, v78
	v_add_f32_e32 v22, v22, v61
	v_mul_f32_e32 v61, v73, v149
	v_mul_f32_e32 v78, v71, v151
	v_fmac_f32_e32 v61, v72, v148
	v_fmac_f32_e32 v78, v70, v150
	ds_read_b128 v[148:151], v104 offset:5120
	v_add_f32_e32 v61, v61, v78
	v_add_f32_e32 v60, v60, v61
	s_waitcnt lgkmcnt(0)
	v_mul_f32_e32 v61, v47, v149
	v_mul_f32_e32 v78, v21, v151
	v_fmac_f32_e32 v61, v46, v148
	v_fmac_f32_e32 v78, v20, v150
	v_add_f32_e32 v61, v61, v78
	v_add_f32_e32 v22, v22, v61
	v_mul_f32_e32 v61, v69, v149
	v_mul_f32_e32 v78, v67, v151
	v_fmac_f32_e32 v61, v68, v148
	v_fmac_f32_e32 v78, v66, v150
	ds_read_b128 v[148:151], v104 offset:6144
	v_add_f32_e32 v61, v61, v78
	v_add_f32_e32 v60, v60, v61
	s_waitcnt lgkmcnt(0)
	v_mul_f32_e32 v61, v51, v149
	v_mul_f32_e32 v78, v49, v151
	v_fmac_f32_e32 v61, v50, v148
	v_fmac_f32_e32 v78, v48, v150
	v_add_f32_e32 v61, v61, v78
	v_add_f32_e32 v22, v22, v61
	v_mul_f32_e32 v61, v65, v149
	v_mul_f32_e32 v78, v63, v151
	v_fmac_f32_e32 v61, v64, v148
	v_fmac_f32_e32 v78, v62, v150
	ds_read_b128 v[148:151], v104 offset:7168
	v_add_f32_e32 v61, v61, v78
	v_add_f32_e32 v61, v60, v61
	s_waitcnt lgkmcnt(0)
	v_mul_f32_e32 v60, v55, v149
	v_mul_f32_e32 v78, v53, v151
	v_fmac_f32_e32 v60, v54, v148
	v_fmac_f32_e32 v78, v52, v150
	v_add_f32_e32 v60, v60, v78
	v_add_f32_e32 v60, v22, v60
	v_mul_f32_e32 v22, v59, v149
	v_mul_f32_e32 v78, v57, v151
	v_fmac_f32_e32 v22, v58, v148
	v_fmac_f32_e32 v78, v56, v150
	ds_read_b128 v[148:151], v104 offset:8192
	v_add_f32_e32 v22, v22, v78
	v_add_f32_e32 v22, v61, v22
	s_waitcnt lgkmcnt(0)
	v_mul_f32_e32 v61, v5, v149
	v_mul_f32_e32 v78, v1, v151
	v_fmac_f32_e32 v61, v4, v148
	v_fmac_f32_e32 v78, v0, v150
	v_add_f32_e32 v61, v61, v78
	v_mul_f32_e32 v78, v91, v149
	v_mul_f32_e32 v79, v89, v151
	v_fmac_f32_e32 v78, v90, v148
	v_fmac_f32_e32 v79, v88, v150
	ds_read_b128 v[148:151], v104 offset:9216
	v_add_f32_e32 v78, v78, v79
	v_add_f32_e32 v61, 0, v61
	v_add_f32_e32 v78, 0, v78
	s_waitcnt lgkmcnt(0)
	v_mul_f32_e32 v79, v7, v149
	v_mul_f32_e32 v92, v3, v151
	v_fmac_f32_e32 v79, v6, v148
	v_fmac_f32_e32 v92, v2, v150
	v_add_f32_e32 v79, v79, v92
	v_add_f32_e32 v61, v61, v79
	v_mul_f32_e32 v79, v87, v149
	v_mul_f32_e32 v92, v85, v151
	v_fmac_f32_e32 v79, v86, v148
	v_fmac_f32_e32 v92, v84, v150
	ds_read_b128 v[148:151], v104 offset:10240
	v_add_f32_e32 v79, v79, v92
	v_add_f32_e32 v78, v78, v79
	s_waitcnt lgkmcnt(0)
	v_mul_f32_e32 v79, v11, v149
	v_mul_f32_e32 v92, v9, v151
	v_fmac_f32_e32 v79, v10, v148
	v_fmac_f32_e32 v92, v8, v150
	v_add_f32_e32 v79, v79, v92
	v_add_f32_e32 v61, v61, v79
	v_mul_f32_e32 v79, v83, v149
	v_mul_f32_e32 v92, v81, v151
	v_fmac_f32_e32 v79, v82, v148
	v_fmac_f32_e32 v92, v80, v150
	ds_read_b128 v[148:151], v104 offset:11264
	v_add_f32_e32 v79, v79, v92
	v_add_f32_e32 v78, v78, v79
	s_waitcnt lgkmcnt(0)
	v_mul_f32_e32 v79, v15, v149
	v_mul_f32_e32 v92, v13, v151
	v_fmac_f32_e32 v79, v14, v148
	v_fmac_f32_e32 v92, v12, v150
	v_add_f32_e32 v79, v79, v92
	v_add_f32_e32 v61, v61, v79
	v_mul_f32_e32 v79, v77, v149
	v_mul_f32_e32 v92, v75, v151
	v_fmac_f32_e32 v79, v76, v148
	v_fmac_f32_e32 v92, v74, v150
	ds_read_b128 v[148:151], v104 offset:12288
	v_add_f32_e32 v79, v79, v92
	v_add_f32_e32 v78, v78, v79
	s_waitcnt lgkmcnt(0)
	v_mul_f32_e32 v79, v19, v149
	v_mul_f32_e32 v92, v17, v151
	v_fmac_f32_e32 v79, v18, v148
	v_fmac_f32_e32 v92, v16, v150
	v_add_f32_e32 v79, v79, v92
	v_add_f32_e32 v61, v61, v79
	v_mul_f32_e32 v79, v73, v149
	v_mul_f32_e32 v92, v71, v151
	v_fmac_f32_e32 v79, v72, v148
	v_fmac_f32_e32 v92, v70, v150
	ds_read_b128 v[148:151], v104 offset:13312
	v_add_f32_e32 v79, v79, v92
	v_add_f32_e32 v78, v78, v79
	s_waitcnt lgkmcnt(0)
	v_mul_f32_e32 v79, v47, v149
	v_mul_f32_e32 v92, v21, v151
	v_fmac_f32_e32 v79, v46, v148
	v_fmac_f32_e32 v92, v20, v150
	v_add_f32_e32 v79, v79, v92
	v_add_f32_e32 v61, v61, v79
	v_mul_f32_e32 v79, v69, v149
	v_mul_f32_e32 v92, v67, v151
	v_fmac_f32_e32 v79, v68, v148
	v_fmac_f32_e32 v92, v66, v150
	ds_read_b128 v[148:151], v104 offset:14336
	v_add_f32_e32 v79, v79, v92
	v_add_f32_e32 v78, v78, v79
	s_waitcnt lgkmcnt(0)
	v_mul_f32_e32 v79, v51, v149
	v_mul_f32_e32 v92, v49, v151
	v_fmac_f32_e32 v79, v50, v148
	v_fmac_f32_e32 v92, v48, v150
	v_add_f32_e32 v79, v79, v92
	v_add_f32_e32 v61, v61, v79
	v_mul_f32_e32 v79, v65, v149
	v_mul_f32_e32 v92, v63, v151
	v_fmac_f32_e32 v79, v64, v148
	v_fmac_f32_e32 v92, v62, v150
	ds_read_b128 v[148:151], v104 offset:15360
	v_add_f32_e32 v79, v79, v92
	v_add_f32_e32 v79, v78, v79
	s_waitcnt lgkmcnt(0)
	v_mul_f32_e32 v78, v55, v149
	v_mul_f32_e32 v92, v53, v151
	v_fmac_f32_e32 v78, v54, v148
	v_fmac_f32_e32 v92, v52, v150
	v_add_f32_e32 v78, v78, v92
	v_add_f32_e32 v78, v61, v78
	v_mul_f32_e32 v61, v59, v149
	v_mul_f32_e32 v92, v57, v151
	v_fmac_f32_e32 v61, v58, v148
	v_fmac_f32_e32 v92, v56, v150
	ds_read_b128 v[148:151], v104 offset:16384
	v_add_f32_e32 v61, v61, v92
	v_add_f32_e32 v61, v79, v61
	s_waitcnt lgkmcnt(0)
	v_mul_f32_e32 v79, v5, v149
	v_mul_f32_e32 v92, v1, v151
	v_fmac_f32_e32 v79, v4, v148
	v_fmac_f32_e32 v92, v0, v150
	v_add_f32_e32 v79, v79, v92
	v_mul_f32_e32 v92, v91, v149
	v_mul_f32_e32 v93, v89, v151
	v_fmac_f32_e32 v92, v90, v148
	v_fmac_f32_e32 v93, v88, v150
	ds_read_b128 v[148:151], v104 offset:17408
	v_add_f32_e32 v92, v92, v93
	v_add_f32_e32 v79, 0, v79
	v_add_f32_e32 v92, 0, v92
	s_waitcnt lgkmcnt(0)
	v_mul_f32_e32 v93, v7, v149
	v_mul_f32_e32 v152, v3, v151
	v_fmac_f32_e32 v93, v6, v148
	v_fmac_f32_e32 v152, v2, v150
	v_add_f32_e32 v93, v93, v152
	v_add_f32_e32 v79, v79, v93
	v_mul_f32_e32 v93, v87, v149
	v_fmac_f32_e32 v93, v86, v148
	v_mul_f32_e32 v148, v85, v151
	v_fmac_f32_e32 v148, v84, v150
	v_add_f32_e32 v93, v93, v148
	ds_read_b128 v[148:151], v104 offset:18432
	v_add_f32_e32 v92, v92, v93
	s_waitcnt lgkmcnt(0)
	v_mul_f32_e32 v93, v11, v149
	v_mul_f32_e32 v152, v9, v151
	v_fmac_f32_e32 v93, v10, v148
	v_fmac_f32_e32 v152, v8, v150
	v_add_f32_e32 v93, v93, v152
	v_add_f32_e32 v79, v79, v93
	v_mul_f32_e32 v93, v83, v149
	v_fmac_f32_e32 v93, v82, v148
	v_mul_f32_e32 v148, v81, v151
	v_fmac_f32_e32 v148, v80, v150
	v_add_f32_e32 v93, v93, v148
	ds_read_b128 v[148:151], v104 offset:19456
	v_add_f32_e32 v92, v92, v93
	s_waitcnt lgkmcnt(0)
	v_mul_f32_e32 v93, v15, v149
	v_mul_f32_e32 v152, v13, v151
	v_fmac_f32_e32 v93, v14, v148
	v_fmac_f32_e32 v152, v12, v150
	v_add_f32_e32 v93, v93, v152
	v_add_f32_e32 v79, v79, v93
	v_mul_f32_e32 v93, v77, v149
	v_fmac_f32_e32 v93, v76, v148
	v_mul_f32_e32 v148, v75, v151
	v_fmac_f32_e32 v148, v74, v150
	v_add_f32_e32 v93, v93, v148
	ds_read_b128 v[148:151], v104 offset:20480
	v_add_f32_e32 v92, v92, v93
	s_waitcnt lgkmcnt(0)
	v_mul_f32_e32 v93, v19, v149
	v_mul_f32_e32 v152, v17, v151
	v_fmac_f32_e32 v93, v18, v148
	v_fmac_f32_e32 v152, v16, v150
	v_add_f32_e32 v93, v93, v152
	v_add_f32_e32 v79, v79, v93
	v_mul_f32_e32 v93, v73, v149
	v_fmac_f32_e32 v93, v72, v148
	v_mul_f32_e32 v148, v71, v151
	v_fmac_f32_e32 v148, v70, v150
	v_add_f32_e32 v93, v93, v148
	ds_read_b128 v[148:151], v104 offset:21504
	v_add_f32_e32 v92, v92, v93
	s_waitcnt lgkmcnt(0)
	v_mul_f32_e32 v93, v47, v149
	v_mul_f32_e32 v152, v21, v151
	v_fmac_f32_e32 v93, v46, v148
	v_fmac_f32_e32 v152, v20, v150
	v_add_f32_e32 v93, v93, v152
	v_add_f32_e32 v79, v79, v93
	v_mul_f32_e32 v93, v69, v149
	v_fmac_f32_e32 v93, v68, v148
	v_mul_f32_e32 v148, v67, v151
	v_fmac_f32_e32 v148, v66, v150
	v_add_f32_e32 v93, v93, v148
	ds_read_b128 v[148:151], v104 offset:22528
	v_add_f32_e32 v92, v92, v93
	s_waitcnt lgkmcnt(0)
	v_mul_f32_e32 v93, v51, v149
	v_mul_f32_e32 v152, v49, v151
	v_fmac_f32_e32 v93, v50, v148
	v_fmac_f32_e32 v152, v48, v150
	v_add_f32_e32 v93, v93, v152
	v_add_f32_e32 v79, v79, v93
	v_mul_f32_e32 v93, v65, v149
	v_fmac_f32_e32 v93, v64, v148
	v_mul_f32_e32 v148, v63, v151
	v_fmac_f32_e32 v148, v62, v150
	v_add_f32_e32 v93, v93, v148
	ds_read_b128 v[148:151], v104 offset:23552
	v_add_f32_e32 v93, v92, v93
	s_waitcnt lgkmcnt(0)
	v_mul_f32_e32 v92, v55, v149
	v_mul_f32_e32 v152, v53, v151
	v_fmac_f32_e32 v92, v54, v148
	v_fmac_f32_e32 v152, v52, v150
	v_add_f32_e32 v92, v92, v152
	v_add_f32_e32 v92, v79, v92
	v_mul_f32_e32 v79, v59, v149
	v_fmac_f32_e32 v79, v58, v148
	v_mul_f32_e32 v148, v57, v151
	v_fmac_f32_e32 v148, v56, v150
	v_add_f32_e32 v79, v79, v148
	ds_read_b128 v[148:151], v104 offset:24576
	v_add_f32_e32 v79, v93, v79
	v_and_b32_e32 v93, 0xffff0000, v97
	s_waitcnt lgkmcnt(0)
	v_mul_f32_e32 v5, v5, v149
	v_mul_f32_e32 v1, v1, v151
	v_fmac_f32_e32 v5, v4, v148
	v_fmac_f32_e32 v1, v0, v150
	v_add_f32_e32 v0, v5, v1
	v_mul_f32_e32 v1, v91, v149
	v_mul_f32_e32 v4, v89, v151
	v_fmac_f32_e32 v1, v90, v148
	v_fmac_f32_e32 v4, v88, v150
	ds_read_b128 v[88:91], v104 offset:25600
	v_add_f32_e32 v1, v1, v4
	v_add_f32_e32 v0, 0, v0
	v_add_f32_e32 v1, 0, v1
	s_waitcnt lgkmcnt(0)
	v_mul_f32_e32 v4, v7, v89
	v_mul_f32_e32 v3, v3, v91
	v_fmac_f32_e32 v4, v6, v88
	v_fmac_f32_e32 v3, v2, v90
	v_add_f32_e32 v2, v4, v3
	v_add_f32_e32 v4, v0, v2
	v_mul_f32_e32 v0, v87, v89
	v_mul_f32_e32 v2, v85, v91
	v_fmac_f32_e32 v0, v86, v88
	v_fmac_f32_e32 v2, v84, v90
	v_add_f32_e32 v0, v0, v2
	v_add_f32_e32 v5, v1, v0
	ds_read_b128 v[0:3], v104 offset:26624
	v_and_b32_e32 v86, 0xffff0000, v143
	v_and_b32_e32 v91, 0xffff0000, v142
	v_lshlrev_b32_e32 v87, 16, v142
	v_and_b32_e32 v88, 0xffff0000, v95
	s_waitcnt lgkmcnt(0)
	v_mul_f32_e32 v6, v11, v1
	v_mul_f32_e32 v1, v83, v1
	v_fmac_f32_e32 v6, v10, v0
	v_fmac_f32_e32 v1, v82, v0
	v_mul_f32_e32 v0, v81, v3
	v_fmac_f32_e32 v0, v80, v2
	v_mul_f32_e32 v7, v9, v3
	v_add_f32_e32 v0, v1, v0
	v_fmac_f32_e32 v7, v8, v2
	v_add_f32_e32 v5, v5, v0
	ds_read_b128 v[0:3], v104 offset:27648
	v_add_f32_e32 v6, v6, v7
	v_add_f32_e32 v4, v4, v6
	v_and_b32_e32 v9, 0xffff0000, v127
	v_and_b32_e32 v10, 0xffff0000, v126
	s_waitcnt lgkmcnt(0)
	v_mul_f32_e32 v6, v15, v1
	v_mul_f32_e32 v1, v77, v1
	v_fmac_f32_e32 v6, v14, v0
	v_fmac_f32_e32 v1, v76, v0
	v_mul_f32_e32 v0, v75, v3
	v_fmac_f32_e32 v0, v74, v2
	v_mul_f32_e32 v7, v13, v3
	v_add_f32_e32 v0, v1, v0
	v_fmac_f32_e32 v7, v12, v2
	v_add_f32_e32 v5, v5, v0
	ds_read_b128 v[0:3], v104 offset:28672
	v_add_f32_e32 v6, v6, v7
	v_add_f32_e32 v4, v4, v6
	v_lshlrev_b32_e32 v8, 16, v126
	v_and_b32_e32 v15, 0xffff0000, v136
	s_waitcnt lgkmcnt(0)
	v_mul_f32_e32 v6, v19, v1
	v_mul_f32_e32 v1, v73, v1
	v_fmac_f32_e32 v6, v18, v0
	v_fmac_f32_e32 v1, v72, v0
	v_mul_f32_e32 v0, v71, v3
	v_fmac_f32_e32 v0, v70, v2
	v_mul_f32_e32 v7, v17, v3
	v_add_f32_e32 v0, v1, v0
	v_fmac_f32_e32 v7, v16, v2
	v_add_f32_e32 v5, v5, v0
	ds_read_b128 v[0:3], v104 offset:29696
	v_add_f32_e32 v6, v6, v7
	v_add_f32_e32 v4, v4, v6
	v_lshlrev_b32_e32 v13, 16, v136
	v_and_b32_e32 v17, 0xffff0000, v133
	s_waitcnt lgkmcnt(0)
	v_mul_f32_e32 v6, v47, v1
	v_mul_f32_e32 v1, v69, v1
	v_fmac_f32_e32 v6, v46, v0
	v_fmac_f32_e32 v1, v68, v0
	v_mul_f32_e32 v0, v67, v3
	v_fmac_f32_e32 v0, v66, v2
	v_mul_f32_e32 v7, v21, v3
	v_add_f32_e32 v0, v1, v0
	v_fmac_f32_e32 v7, v20, v2
	v_add_f32_e32 v5, v5, v0
	ds_read_b128 v[0:3], v104 offset:30720
	v_add_f32_e32 v6, v6, v7
	v_add_f32_e32 v4, v4, v6
	v_and_b32_e32 v20, 0xffff0000, v132
	v_lshlrev_b32_e32 v16, 16, v132
	s_waitcnt lgkmcnt(0)
	v_mul_f32_e32 v6, v51, v1
	v_mul_f32_e32 v1, v65, v1
	v_fmac_f32_e32 v6, v50, v0
	v_mul_f32_e32 v7, v49, v3
	v_fmac_f32_e32 v1, v64, v0
	v_mul_f32_e32 v0, v63, v3
	v_fmac_f32_e32 v7, v48, v2
	v_fmac_f32_e32 v0, v62, v2
	v_add_f32_e32 v6, v6, v7
	v_add_f32_e32 v0, v1, v0
	v_add_f32_e32 v4, v4, v6
	v_add_f32_e32 v6, v5, v0
	ds_read_b128 v[0:3], v104 offset:31744
	v_and_b32_e32 v49, 0xffff0000, v147
	v_lshlrev_b32_e32 v50, 16, v146
	v_and_b32_e32 v46, 0xffff0000, v123
	v_and_b32_e32 v51, 0xffff0000, v122
	s_waitcnt lgkmcnt(0)
	v_mul_f32_e32 v5, v55, v1
	v_mul_f32_e32 v1, v59, v1
	v_fmac_f32_e32 v5, v54, v0
	v_mul_f32_e32 v7, v53, v3
	v_fmac_f32_e32 v1, v58, v0
	v_mul_f32_e32 v0, v57, v3
	v_fmac_f32_e32 v7, v52, v2
	v_fmac_f32_e32 v0, v56, v2
	v_add_f32_e32 v5, v5, v7
	v_add_f32_e32 v0, v1, v0
	v_add_f32_e32 v5, v4, v5
	v_add_f32_e32 v4, v6, v0
	ds_read2st64_b64 v[0:3], v105 offset0:64 offset1:65
	v_lshlrev_b32_e32 v7, 16, v127
	v_and_b32_e32 v54, 0xffff0000, v146
	v_and_b32_e32 v56, 0xffff0000, v140
	v_and_b32_e32 v57, 0xffff0000, v131
	s_waitcnt lgkmcnt(0)
	v_lshlrev_b32_e32 v6, 16, v0
	v_and_b32_e32 v0, 0xffff0000, v0
	v_lshlrev_b32_e32 v14, 16, v1
	v_and_b32_e32 v1, 0xffff0000, v1
	v_mul_f32_e32 v11, v9, v0
	v_mul_f32_e32 v12, v10, v1
	v_fmac_f32_e32 v11, v7, v6
	v_fmac_f32_e32 v12, v8, v14
	v_add_f32_e32 v11, v11, v12
	v_and_b32_e32 v12, 0xffff0000, v137
	v_add_f32_e32 v18, 0, v11
	v_lshlrev_b32_e32 v11, 16, v137
	v_mul_f32_e32 v0, v12, v0
	v_mul_f32_e32 v1, v15, v1
	v_fmac_f32_e32 v0, v11, v6
	v_fmac_f32_e32 v1, v13, v14
	v_add_f32_e32 v0, v0, v1
	v_lshlrev_b32_e32 v1, 16, v2
	v_and_b32_e32 v2, 0xffff0000, v2
	v_lshlrev_b32_e32 v19, 16, v3
	v_and_b32_e32 v3, 0xffff0000, v3
	v_lshlrev_b32_e32 v14, 16, v133
	v_mul_f32_e32 v6, v17, v2
	v_mul_f32_e32 v21, v20, v3
	v_fmac_f32_e32 v6, v14, v1
	v_fmac_f32_e32 v21, v16, v19
	v_add_f32_e32 v6, v6, v21
	v_lshlrev_b32_e32 v21, 16, v147
	v_mul_f32_e32 v2, v49, v2
	v_fmac_f32_e32 v2, v21, v1
	v_mul_f32_e32 v1, v54, v3
	v_fmac_f32_e32 v1, v50, v19
	v_add_f32_e32 v0, 0, v0
	v_add_f32_e32 v1, v2, v1
	v_add_f32_e32 v48, v0, v1
	ds_read2st64_b64 v[0:3], v105 offset0:66 offset1:67
	v_add_f32_e32 v6, v18, v6
	v_lshlrev_b32_e32 v18, 16, v123
	v_lshlrev_b32_e32 v19, 16, v122
	v_and_b32_e32 v59, 0xffff0000, v129
	s_waitcnt lgkmcnt(0)
	v_lshlrev_b32_e32 v52, 16, v0
	v_and_b32_e32 v0, 0xffff0000, v0
	v_lshlrev_b32_e32 v53, 16, v1
	v_and_b32_e32 v1, 0xffff0000, v1
	v_mul_f32_e32 v47, v46, v0
	v_mul_f32_e32 v55, v51, v1
	v_fmac_f32_e32 v47, v18, v52
	v_fmac_f32_e32 v55, v19, v53
	v_add_f32_e32 v47, v47, v55
	v_and_b32_e32 v55, 0xffff0000, v141
	v_add_f32_e32 v6, v6, v47
	v_lshlrev_b32_e32 v47, 16, v141
	v_mul_f32_e32 v0, v55, v0
	v_fmac_f32_e32 v0, v47, v52
	v_lshlrev_b32_e32 v52, 16, v140
	v_mul_f32_e32 v1, v56, v1
	v_fmac_f32_e32 v1, v52, v53
	v_add_f32_e32 v0, v0, v1
	v_lshlrev_b32_e32 v1, 16, v2
	v_and_b32_e32 v2, 0xffff0000, v2
	v_lshlrev_b32_e32 v65, 16, v3
	v_and_b32_e32 v3, 0xffff0000, v3
	v_add_f32_e32 v0, v48, v0
	v_lshlrev_b32_e32 v48, 16, v131
	v_mul_f32_e32 v58, v57, v2
	v_lshlrev_b32_e32 v53, 16, v129
	v_mul_f32_e32 v62, v59, v3
	v_fmac_f32_e32 v58, v48, v1
	v_fmac_f32_e32 v62, v53, v65
	v_add_f32_e32 v58, v58, v62
	v_and_b32_e32 v63, 0xffff0000, v145
	v_add_f32_e32 v6, v6, v58
	v_lshlrev_b32_e32 v58, 16, v145
	v_mul_f32_e32 v2, v63, v2
	v_and_b32_e32 v64, 0xffff0000, v144
	v_fmac_f32_e32 v2, v58, v1
	v_lshlrev_b32_e32 v62, 16, v144
	v_mul_f32_e32 v1, v64, v3
	v_fmac_f32_e32 v1, v62, v65
	v_add_f32_e32 v1, v2, v1
	v_add_f32_e32 v65, v0, v1
	ds_read2st64_b64 v[0:3], v105 offset0:68 offset1:69
	v_and_b32_e32 v68, 0xffff0000, v120
	v_and_b32_e32 v69, 0xffff0000, v94
	v_lshlrev_b32_e32 v66, 16, v120
	v_lshlrev_b32_e32 v67, 16, v94
	s_waitcnt lgkmcnt(0)
	v_lshlrev_b32_e32 v72, 16, v0
	v_and_b32_e32 v0, 0xffff0000, v0
	v_lshlrev_b32_e32 v73, 16, v1
	v_and_b32_e32 v1, 0xffff0000, v1
	v_mul_f32_e32 v70, v68, v0
	v_mul_f32_e32 v71, v69, v1
	v_fmac_f32_e32 v70, v66, v72
	v_fmac_f32_e32 v71, v67, v73
	v_add_f32_e32 v70, v70, v71
	v_and_b32_e32 v71, 0xffff0000, v139
	v_add_f32_e32 v6, v6, v70
	v_lshlrev_b32_e32 v70, 16, v139
	v_mul_f32_e32 v0, v71, v0
	v_and_b32_e32 v74, 0xffff0000, v138
	v_fmac_f32_e32 v0, v70, v72
	v_lshlrev_b32_e32 v72, 16, v138
	v_mul_f32_e32 v1, v74, v1
	v_fmac_f32_e32 v1, v72, v73
	v_add_f32_e32 v0, v0, v1
	v_lshlrev_b32_e32 v1, 16, v2
	v_and_b32_e32 v76, 0xffff0000, v130
	v_and_b32_e32 v2, 0xffff0000, v2
	v_add_f32_e32 v0, v65, v0
	v_lshlrev_b32_e32 v73, 16, v130
	v_mul_f32_e32 v65, v76, v2
	v_lshlrev_b32_e32 v77, 16, v3
	v_and_b32_e32 v81, 0xffff0000, v128
	v_and_b32_e32 v3, 0xffff0000, v3
	v_lshlrev_b32_e32 v82, 16, v143
	v_mul_f32_e32 v2, v86, v2
	v_fmac_f32_e32 v65, v73, v1
	v_lshlrev_b32_e32 v75, 16, v128
	v_mul_f32_e32 v80, v81, v3
	v_fmac_f32_e32 v2, v82, v1
	v_mul_f32_e32 v1, v91, v3
	v_fmac_f32_e32 v80, v75, v77
	v_fmac_f32_e32 v1, v87, v77
	v_add_f32_e32 v65, v65, v80
	v_add_f32_e32 v1, v2, v1
	v_add_f32_e32 v6, v6, v65
	v_add_f32_e32 v65, v0, v1
	ds_read2st64_b64 v[0:3], v105 offset0:70 offset1:71
	v_and_b32_e32 v83, 0xffff0000, v121
	v_lshlrev_b32_e32 v77, 16, v121
	v_lshlrev_b32_e32 v80, 16, v95
	v_and_b32_e32 v94, 0xffff0000, v96
	s_waitcnt lgkmcnt(0)
	v_lshlrev_b32_e32 v85, 16, v0
	v_and_b32_e32 v0, 0xffff0000, v0
	v_lshlrev_b32_e32 v90, 16, v1
	v_and_b32_e32 v1, 0xffff0000, v1
	v_mul_f32_e32 v84, v83, v0
	v_mul_f32_e32 v89, v88, v1
	v_fmac_f32_e32 v84, v77, v85
	v_fmac_f32_e32 v89, v80, v90
	v_add_f32_e32 v84, v84, v89
	v_add_f32_e32 v6, v6, v84
	v_lshlrev_b32_e32 v84, 16, v97
	v_mul_f32_e32 v0, v93, v0
	v_lshlrev_b32_e32 v89, 16, v96
	v_mul_f32_e32 v1, v94, v1
	v_fmac_f32_e32 v0, v84, v85
	v_fmac_f32_e32 v1, v89, v90
	v_add_f32_e32 v0, v0, v1
	v_lshlrev_b32_e32 v1, 16, v2
	v_and_b32_e32 v95, 0xffff0000, v125
	v_and_b32_e32 v2, 0xffff0000, v2
	v_lshlrev_b32_e32 v123, 16, v3
	v_and_b32_e32 v97, 0xffff0000, v124
	v_and_b32_e32 v3, 0xffff0000, v3
	v_add_f32_e32 v0, v65, v0
	v_lshlrev_b32_e32 v85, 16, v125
	v_mul_f32_e32 v65, v95, v2
	v_lshlrev_b32_e32 v90, 16, v124
	v_mul_f32_e32 v96, v97, v3
	v_fmac_f32_e32 v65, v85, v1
	v_fmac_f32_e32 v96, v90, v123
	v_and_b32_e32 v121, 0xffff0000, v135
	v_add_f32_e32 v65, v65, v96
	v_lshlrev_b32_e32 v96, 16, v135
	v_mul_f32_e32 v2, v121, v2
	v_and_b32_e32 v122, 0xffff0000, v134
	v_fmac_f32_e32 v2, v96, v1
	v_lshlrev_b32_e32 v120, 16, v134
	v_mul_f32_e32 v1, v122, v3
	v_fmac_f32_e32 v1, v120, v123
	v_add_f32_e32 v1, v2, v1
	v_add_f32_e32 v65, v6, v65
	v_add_f32_e32 v6, v0, v1
	ds_read2st64_b64 v[0:3], v105 offset0:72 offset1:73
	s_waitcnt lgkmcnt(0)
	v_lshlrev_b32_e32 v123, 16, v0
	v_and_b32_e32 v0, 0xffff0000, v0
	v_lshlrev_b32_e32 v125, 16, v1
	v_and_b32_e32 v1, 0xffff0000, v1
	v_mul_f32_e32 v124, v9, v0
	v_mul_f32_e32 v126, v10, v1
	v_mul_f32_e32 v0, v12, v0
	v_mul_f32_e32 v1, v15, v1
	v_fmac_f32_e32 v0, v11, v123
	v_fmac_f32_e32 v1, v13, v125
	v_add_f32_e32 v0, v0, v1
	v_lshlrev_b32_e32 v1, 16, v2
	v_and_b32_e32 v2, 0xffff0000, v2
	v_fmac_f32_e32 v124, v7, v123
	v_fmac_f32_e32 v126, v8, v125
	v_mul_f32_e32 v123, v17, v2
	v_lshlrev_b32_e32 v125, 16, v3
	v_and_b32_e32 v3, 0xffff0000, v3
	v_mul_f32_e32 v2, v49, v2
	v_add_f32_e32 v124, v124, v126
	v_fmac_f32_e32 v123, v14, v1
	v_mul_f32_e32 v126, v20, v3
	v_fmac_f32_e32 v2, v21, v1
	v_mul_f32_e32 v1, v54, v3
	v_fmac_f32_e32 v126, v16, v125
	v_fmac_f32_e32 v1, v50, v125
	v_add_f32_e32 v124, 0, v124
	v_add_f32_e32 v0, 0, v0
	v_add_f32_e32 v123, v123, v126
	v_add_f32_e32 v1, v2, v1
	v_add_f32_e32 v123, v124, v123
	v_add_f32_e32 v124, v0, v1
	ds_read2st64_b64 v[0:3], v105 offset0:74 offset1:75
	s_waitcnt lgkmcnt(0)
	v_lshlrev_b32_e32 v125, 16, v0
	v_and_b32_e32 v0, 0xffff0000, v0
	v_lshlrev_b32_e32 v127, 16, v1
	v_and_b32_e32 v1, 0xffff0000, v1
	v_mul_f32_e32 v126, v46, v0
	v_mul_f32_e32 v128, v51, v1
	v_mul_f32_e32 v0, v55, v0
	v_mul_f32_e32 v1, v56, v1
	v_fmac_f32_e32 v0, v47, v125
	v_fmac_f32_e32 v1, v52, v127
	v_fmac_f32_e32 v126, v18, v125
	v_fmac_f32_e32 v128, v19, v127
	v_add_f32_e32 v0, v0, v1
	v_lshlrev_b32_e32 v1, 16, v2
	v_and_b32_e32 v2, 0xffff0000, v2
	v_add_f32_e32 v126, v126, v128
	v_add_f32_e32 v0, v124, v0
	v_mul_f32_e32 v124, v57, v2
	v_lshlrev_b32_e32 v125, 16, v3
	v_and_b32_e32 v3, 0xffff0000, v3
	v_mul_f32_e32 v2, v63, v2
	v_add_f32_e32 v123, v123, v126
	v_fmac_f32_e32 v124, v48, v1
	v_mul_f32_e32 v126, v59, v3
	v_fmac_f32_e32 v2, v58, v1
	v_mul_f32_e32 v1, v64, v3
	v_fmac_f32_e32 v126, v53, v125
	v_fmac_f32_e32 v1, v62, v125
	v_add_f32_e32 v124, v124, v126
	v_add_f32_e32 v1, v2, v1
	v_add_f32_e32 v123, v123, v124
	v_add_f32_e32 v124, v0, v1
	ds_read2st64_b64 v[0:3], v105 offset0:76 offset1:77
	s_waitcnt lgkmcnt(0)
	v_lshlrev_b32_e32 v125, 16, v0
	v_and_b32_e32 v0, 0xffff0000, v0
	v_lshlrev_b32_e32 v127, 16, v1
	v_and_b32_e32 v1, 0xffff0000, v1
	v_mul_f32_e32 v126, v68, v0
	v_mul_f32_e32 v128, v69, v1
	v_mul_f32_e32 v0, v71, v0
	v_mul_f32_e32 v1, v74, v1
	v_fmac_f32_e32 v0, v70, v125
	v_fmac_f32_e32 v1, v72, v127
	v_fmac_f32_e32 v126, v66, v125
	v_fmac_f32_e32 v128, v67, v127
	v_add_f32_e32 v0, v0, v1
	v_lshlrev_b32_e32 v1, 16, v2
	v_and_b32_e32 v2, 0xffff0000, v2
	v_add_f32_e32 v126, v126, v128
	v_add_f32_e32 v0, v124, v0
	v_mul_f32_e32 v124, v76, v2
	v_lshlrev_b32_e32 v125, 16, v3
	v_and_b32_e32 v3, 0xffff0000, v3
	v_mul_f32_e32 v2, v86, v2
	v_add_f32_e32 v123, v123, v126
	v_fmac_f32_e32 v124, v73, v1
	v_mul_f32_e32 v126, v81, v3
	v_fmac_f32_e32 v2, v82, v1
	v_mul_f32_e32 v1, v91, v3
	v_fmac_f32_e32 v126, v75, v125
	v_fmac_f32_e32 v1, v87, v125
	v_add_f32_e32 v124, v124, v126
	v_add_f32_e32 v1, v2, v1
	v_add_f32_e32 v123, v123, v124
	v_add_f32_e32 v124, v0, v1
	ds_read2st64_b64 v[0:3], v105 offset0:78 offset1:79
	s_waitcnt lgkmcnt(0)
	v_lshlrev_b32_e32 v125, 16, v0
	v_and_b32_e32 v0, 0xffff0000, v0
	v_lshlrev_b32_e32 v127, 16, v1
	v_and_b32_e32 v1, 0xffff0000, v1
	v_mul_f32_e32 v126, v83, v0
	v_mul_f32_e32 v128, v88, v1
	v_mul_f32_e32 v0, v93, v0
	v_mul_f32_e32 v1, v94, v1
	v_fmac_f32_e32 v0, v84, v125
	v_fmac_f32_e32 v1, v89, v127
	v_fmac_f32_e32 v126, v77, v125
	v_fmac_f32_e32 v128, v80, v127
	v_add_f32_e32 v0, v0, v1
	v_lshlrev_b32_e32 v1, 16, v2
	v_and_b32_e32 v2, 0xffff0000, v2
	v_add_f32_e32 v126, v126, v128
	v_add_f32_e32 v0, v124, v0
	v_mul_f32_e32 v124, v95, v2
	v_lshlrev_b32_e32 v125, 16, v3
	v_and_b32_e32 v3, 0xffff0000, v3
	v_mul_f32_e32 v2, v121, v2
	v_add_f32_e32 v123, v123, v126
	v_fmac_f32_e32 v124, v85, v1
	v_mul_f32_e32 v126, v97, v3
	v_fmac_f32_e32 v2, v96, v1
	v_mul_f32_e32 v1, v122, v3
	v_fmac_f32_e32 v126, v90, v125
	v_fmac_f32_e32 v1, v120, v125
	v_add_f32_e32 v124, v124, v126
	v_add_f32_e32 v1, v2, v1
	v_add_f32_e32 v124, v123, v124
	v_add_f32_e32 v123, v0, v1
	ds_read2st64_b64 v[0:3], v105 offset0:80 offset1:81
	s_waitcnt lgkmcnt(0)
	v_lshlrev_b32_e32 v125, 16, v0
	v_and_b32_e32 v0, 0xffff0000, v0
	v_lshlrev_b32_e32 v127, 16, v1
	v_and_b32_e32 v1, 0xffff0000, v1
	v_mul_f32_e32 v126, v9, v0
	v_mul_f32_e32 v128, v10, v1
	v_mul_f32_e32 v0, v12, v0
	v_mul_f32_e32 v1, v15, v1
	v_fmac_f32_e32 v0, v11, v125
	v_fmac_f32_e32 v1, v13, v127
	v_add_f32_e32 v0, v0, v1
	v_lshlrev_b32_e32 v1, 16, v2
	v_and_b32_e32 v2, 0xffff0000, v2
	v_fmac_f32_e32 v126, v7, v125
	v_fmac_f32_e32 v128, v8, v127
	v_mul_f32_e32 v125, v17, v2
	v_lshlrev_b32_e32 v127, 16, v3
	v_and_b32_e32 v3, 0xffff0000, v3
	v_mul_f32_e32 v2, v49, v2
	v_add_f32_e32 v126, v126, v128
	v_fmac_f32_e32 v125, v14, v1
	v_mul_f32_e32 v128, v20, v3
	v_fmac_f32_e32 v2, v21, v1
	v_mul_f32_e32 v1, v54, v3
	v_fmac_f32_e32 v128, v16, v127
	v_fmac_f32_e32 v1, v50, v127
	v_add_f32_e32 v126, 0, v126
	v_add_f32_e32 v0, 0, v0
	v_add_f32_e32 v125, v125, v128
	v_add_f32_e32 v1, v2, v1
	v_add_f32_e32 v125, v126, v125
	v_add_f32_e32 v126, v0, v1
	ds_read2st64_b64 v[0:3], v105 offset0:82 offset1:83
	s_waitcnt lgkmcnt(0)
	v_lshlrev_b32_e32 v127, 16, v0
	v_and_b32_e32 v0, 0xffff0000, v0
	v_lshlrev_b32_e32 v129, 16, v1
	v_and_b32_e32 v1, 0xffff0000, v1
	v_mul_f32_e32 v128, v46, v0
	v_mul_f32_e32 v130, v51, v1
	v_mul_f32_e32 v0, v55, v0
	v_mul_f32_e32 v1, v56, v1
	v_fmac_f32_e32 v0, v47, v127
	v_fmac_f32_e32 v1, v52, v129
	v_fmac_f32_e32 v128, v18, v127
	v_fmac_f32_e32 v130, v19, v129
	v_add_f32_e32 v0, v0, v1
	v_lshlrev_b32_e32 v1, 16, v2
	v_and_b32_e32 v2, 0xffff0000, v2
	v_add_f32_e32 v128, v128, v130
	v_add_f32_e32 v0, v126, v0
	v_mul_f32_e32 v126, v57, v2
	v_lshlrev_b32_e32 v127, 16, v3
	v_and_b32_e32 v3, 0xffff0000, v3
	v_mul_f32_e32 v2, v63, v2
	v_add_f32_e32 v125, v125, v128
	v_fmac_f32_e32 v126, v48, v1
	v_mul_f32_e32 v128, v59, v3
	v_fmac_f32_e32 v2, v58, v1
	v_mul_f32_e32 v1, v64, v3
	v_fmac_f32_e32 v128, v53, v127
	v_fmac_f32_e32 v1, v62, v127
	v_add_f32_e32 v126, v126, v128
	v_add_f32_e32 v1, v2, v1
	v_add_f32_e32 v125, v125, v126
	v_add_f32_e32 v126, v0, v1
	ds_read2st64_b64 v[0:3], v105 offset0:84 offset1:85
	s_waitcnt lgkmcnt(0)
	v_lshlrev_b32_e32 v127, 16, v0
	v_and_b32_e32 v0, 0xffff0000, v0
	v_lshlrev_b32_e32 v129, 16, v1
	v_and_b32_e32 v1, 0xffff0000, v1
	v_mul_f32_e32 v128, v68, v0
	v_mul_f32_e32 v130, v69, v1
	v_mul_f32_e32 v0, v71, v0
	v_mul_f32_e32 v1, v74, v1
	v_fmac_f32_e32 v0, v70, v127
	v_fmac_f32_e32 v1, v72, v129
	v_fmac_f32_e32 v128, v66, v127
	v_fmac_f32_e32 v130, v67, v129
	v_add_f32_e32 v0, v0, v1
	v_lshlrev_b32_e32 v1, 16, v2
	v_and_b32_e32 v2, 0xffff0000, v2
	v_add_f32_e32 v128, v128, v130
	v_add_f32_e32 v0, v126, v0
	v_mul_f32_e32 v126, v76, v2
	v_lshlrev_b32_e32 v127, 16, v3
	v_and_b32_e32 v3, 0xffff0000, v3
	v_mul_f32_e32 v2, v86, v2
	v_add_f32_e32 v125, v125, v128
	v_fmac_f32_e32 v126, v73, v1
	v_mul_f32_e32 v128, v81, v3
	v_fmac_f32_e32 v2, v82, v1
	v_mul_f32_e32 v1, v91, v3
	v_fmac_f32_e32 v128, v75, v127
	v_fmac_f32_e32 v1, v87, v127
	v_add_f32_e32 v126, v126, v128
	v_add_f32_e32 v1, v2, v1
	v_add_f32_e32 v125, v125, v126
	v_add_f32_e32 v126, v0, v1
	ds_read2st64_b64 v[0:3], v105 offset0:86 offset1:87
	s_waitcnt lgkmcnt(0)
	v_lshlrev_b32_e32 v127, 16, v0
	v_and_b32_e32 v0, 0xffff0000, v0
	v_lshlrev_b32_e32 v129, 16, v1
	v_and_b32_e32 v1, 0xffff0000, v1
	v_mul_f32_e32 v128, v83, v0
	v_mul_f32_e32 v130, v88, v1
	v_mul_f32_e32 v0, v93, v0
	v_mul_f32_e32 v1, v94, v1
	v_fmac_f32_e32 v0, v84, v127
	v_fmac_f32_e32 v1, v89, v129
	v_fmac_f32_e32 v128, v77, v127
	v_fmac_f32_e32 v130, v80, v129
	v_add_f32_e32 v0, v0, v1
	v_add_f32_e32 v128, v128, v130
	v_add_f32_e32 v0, v126, v0
	v_lshlrev_b32_e32 v126, 16, v2
	v_and_b32_e32 v2, 0xffff0000, v2
	v_lshlrev_b32_e32 v127, 16, v3
	v_and_b32_e32 v3, 0xffff0000, v3
	v_add_f32_e32 v125, v125, v128
	v_mul_f32_e32 v1, v95, v2
	v_mul_f32_e32 v128, v97, v3
	v_fmac_f32_e32 v1, v85, v126
	v_fmac_f32_e32 v128, v90, v127
	v_mul_f32_e32 v2, v121, v2
	v_mul_f32_e32 v3, v122, v3
	v_add_f32_e32 v1, v1, v128
	v_fmac_f32_e32 v2, v96, v126
	v_fmac_f32_e32 v3, v120, v127
	ds_read2st64_b64 v[126:129], v105 offset0:88 offset1:89
	v_add_f32_e32 v2, v2, v3
	v_add_f32_e32 v1, v125, v1
	v_add_f32_e32 v0, v0, v2
	s_waitcnt lgkmcnt(0)
	v_and_b32_e32 v3, 0xffff0000, v126
	v_lshlrev_b32_e32 v2, 16, v126
	v_mul_f32_e32 v125, v9, v3
	v_lshlrev_b32_e32 v126, 16, v127
	v_and_b32_e32 v127, 0xffff0000, v127
	v_mul_f32_e32 v3, v12, v3
	v_fmac_f32_e32 v125, v7, v2
	v_fmac_f32_e32 v3, v11, v2
	v_mul_f32_e32 v2, v15, v127
	v_mul_f32_e32 v130, v10, v127
	v_fmac_f32_e32 v2, v13, v126
	v_fmac_f32_e32 v130, v8, v126
	v_add_f32_e32 v2, v3, v2
	v_lshlrev_b32_e32 v3, 16, v128
	v_and_b32_e32 v126, 0xffff0000, v128
	v_lshlrev_b32_e32 v128, 16, v129
	v_and_b32_e32 v129, 0xffff0000, v129
	v_add_f32_e32 v125, v125, v130
	v_mul_f32_e32 v127, v17, v126
	v_mul_f32_e32 v130, v20, v129
	v_mul_f32_e32 v126, v49, v126
	v_fmac_f32_e32 v127, v14, v3
	v_fmac_f32_e32 v130, v16, v128
	v_fmac_f32_e32 v126, v21, v3
	v_mul_f32_e32 v3, v54, v129
	v_add_f32_e32 v125, 0, v125
	v_add_f32_e32 v127, v127, v130
	v_fmac_f32_e32 v3, v50, v128
	v_add_f32_e32 v125, v125, v127
	v_add_f32_e32 v3, v126, v3
	ds_read2st64_b64 v[126:129], v105 offset0:90 offset1:91
	v_add_f32_e32 v2, 0, v2
	v_add_f32_e32 v2, v2, v3
	s_waitcnt lgkmcnt(0)
	v_lshlrev_b32_e32 v130, 16, v126
	v_and_b32_e32 v126, 0xffff0000, v126
	v_lshlrev_b32_e32 v131, 16, v127
	v_and_b32_e32 v127, 0xffff0000, v127
	v_mul_f32_e32 v3, v46, v126
	v_mul_f32_e32 v132, v51, v127
	v_fmac_f32_e32 v3, v18, v130
	v_fmac_f32_e32 v132, v19, v131
	v_add_f32_e32 v3, v3, v132
	v_add_f32_e32 v3, v125, v3
	v_mul_f32_e32 v125, v55, v126
	v_mul_f32_e32 v126, v56, v127
	v_fmac_f32_e32 v125, v47, v130
	v_fmac_f32_e32 v126, v52, v131
	v_add_f32_e32 v125, v125, v126
	v_lshlrev_b32_e32 v126, 16, v128
	v_and_b32_e32 v128, 0xffff0000, v128
	v_and_b32_e32 v127, 0xffff0000, v129
	v_add_f32_e32 v2, v2, v125
	v_mul_f32_e32 v130, v57, v128
	v_lshlrev_b32_e32 v125, 16, v129
	v_mul_f32_e32 v129, v59, v127
	v_mul_f32_e32 v128, v63, v128
	v_fmac_f32_e32 v130, v48, v126
	v_fmac_f32_e32 v129, v53, v125
	v_fmac_f32_e32 v128, v58, v126
	v_mul_f32_e32 v126, v64, v127
	v_add_f32_e32 v129, v130, v129
	v_fmac_f32_e32 v126, v62, v125
	v_add_f32_e32 v3, v3, v129
	v_add_f32_e32 v125, v128, v126
	ds_read2st64_b64 v[126:129], v105 offset0:92 offset1:93
	v_add_f32_e32 v2, v2, v125
	s_waitcnt lgkmcnt(0)
	v_lshlrev_b32_e32 v125, 16, v126
	v_and_b32_e32 v126, 0xffff0000, v126
	v_mul_f32_e32 v130, v68, v126
	v_lshlrev_b32_e32 v131, 16, v127
	v_and_b32_e32 v127, 0xffff0000, v127
	v_mul_f32_e32 v126, v71, v126
	v_fmac_f32_e32 v130, v66, v125
	v_fmac_f32_e32 v126, v70, v125
	v_mul_f32_e32 v125, v74, v127
	v_mul_f32_e32 v132, v69, v127
	v_fmac_f32_e32 v125, v72, v131
	v_fmac_f32_e32 v132, v67, v131
	v_add_f32_e32 v125, v126, v125
	v_add_f32_e32 v130, v130, v132
	v_add_f32_e32 v2, v2, v125
	v_lshlrev_b32_e32 v125, 16, v128
	v_and_b32_e32 v126, 0xffff0000, v128
	v_lshlrev_b32_e32 v128, 16, v129
	v_and_b32_e32 v129, 0xffff0000, v129
	v_add_f32_e32 v3, v3, v130
	v_mul_f32_e32 v127, v76, v126
	v_mul_f32_e32 v130, v81, v129
	v_mul_f32_e32 v126, v86, v126
	v_fmac_f32_e32 v127, v73, v125
	v_fmac_f32_e32 v130, v75, v128
	v_fmac_f32_e32 v126, v82, v125
	v_mul_f32_e32 v125, v91, v129
	v_add_f32_e32 v127, v127, v130
	v_fmac_f32_e32 v125, v87, v128
	v_add_f32_e32 v3, v3, v127
	v_add_f32_e32 v125, v126, v125
	ds_read2st64_b64 v[126:129], v105 offset0:94 offset1:95
	v_add_f32_e32 v2, v2, v125
	s_waitcnt lgkmcnt(0)
	v_lshlrev_b32_e32 v125, 16, v126
	v_and_b32_e32 v126, 0xffff0000, v126
	v_mul_f32_e32 v130, v83, v126
	v_lshlrev_b32_e32 v131, 16, v127
	v_and_b32_e32 v127, 0xffff0000, v127
	v_mul_f32_e32 v126, v93, v126
	v_fmac_f32_e32 v130, v77, v125
	v_fmac_f32_e32 v126, v84, v125
	v_mul_f32_e32 v125, v94, v127
	v_mul_f32_e32 v132, v88, v127
	v_fmac_f32_e32 v125, v89, v131
	v_fmac_f32_e32 v132, v80, v131
	v_add_f32_e32 v125, v126, v125
	v_add_f32_e32 v130, v130, v132
	v_add_f32_e32 v2, v2, v125
	v_lshlrev_b32_e32 v125, 16, v128
	v_and_b32_e32 v126, 0xffff0000, v128
	v_lshlrev_b32_e32 v128, 16, v129
	v_and_b32_e32 v129, 0xffff0000, v129
	v_add_f32_e32 v3, v3, v130
	v_mul_f32_e32 v127, v95, v126
	v_mul_f32_e32 v130, v97, v129
	v_mul_f32_e32 v126, v121, v126
	v_fmac_f32_e32 v127, v85, v125
	v_fmac_f32_e32 v130, v90, v128
	v_fmac_f32_e32 v126, v96, v125
	v_mul_f32_e32 v125, v122, v129
	v_add_f32_e32 v127, v127, v130
	v_fmac_f32_e32 v125, v120, v128
	v_add_f32_e32 v3, v3, v127
	v_add_f32_e32 v125, v126, v125
	ds_read2st64_b64 v[126:129], v105 offset0:96 offset1:97
	v_add_f32_e32 v2, v2, v125
	s_waitcnt lgkmcnt(0)
	v_lshlrev_b32_e32 v125, 16, v126
	v_and_b32_e32 v126, 0xffff0000, v126
	v_mul_f32_e32 v130, v9, v126
	v_lshlrev_b32_e32 v131, 16, v127
	v_and_b32_e32 v127, 0xffff0000, v127
	v_mul_f32_e32 v126, v12, v126
	v_fmac_f32_e32 v130, v7, v125
	v_fmac_f32_e32 v126, v11, v125
	v_mul_f32_e32 v125, v15, v127
	v_mul_f32_e32 v132, v10, v127
	v_fmac_f32_e32 v125, v13, v131
	v_and_b32_e32 v127, 0xffff0000, v128
	v_fmac_f32_e32 v132, v8, v131
	v_add_f32_e32 v125, v126, v125
	v_lshlrev_b32_e32 v126, 16, v128
	v_mul_f32_e32 v128, v17, v127
	v_lshlrev_b32_e32 v131, 16, v129
	v_and_b32_e32 v129, 0xffff0000, v129
	v_mul_f32_e32 v127, v49, v127
	v_add_f32_e32 v130, v130, v132
	v_fmac_f32_e32 v128, v14, v126
	v_mul_f32_e32 v132, v20, v129
	v_fmac_f32_e32 v127, v21, v126
	v_mul_f32_e32 v126, v54, v129
	v_fmac_f32_e32 v132, v16, v131
	v_fmac_f32_e32 v126, v50, v131
	v_add_f32_e32 v130, 0, v130
	v_add_f32_e32 v125, 0, v125
	v_add_f32_e32 v128, v128, v132
	v_add_f32_e32 v126, v127, v126
	v_add_f32_e32 v130, v130, v128
	v_add_f32_e32 v125, v125, v126
	ds_read2st64_b64 v[126:129], v105 offset0:98 offset1:99
	s_waitcnt lgkmcnt(0)
	v_lshlrev_b32_e32 v131, 16, v126
	v_and_b32_e32 v126, 0xffff0000, v126
	v_lshlrev_b32_e32 v133, 16, v127
	v_and_b32_e32 v127, 0xffff0000, v127
	v_mul_f32_e32 v132, v46, v126
	v_mul_f32_e32 v134, v51, v127
	v_mul_f32_e32 v126, v55, v126
	v_mul_f32_e32 v127, v56, v127
	v_fmac_f32_e32 v126, v47, v131
	v_fmac_f32_e32 v127, v52, v133
	v_fmac_f32_e32 v132, v18, v131
	v_fmac_f32_e32 v134, v19, v133
	v_add_f32_e32 v126, v126, v127
	v_and_b32_e32 v127, 0xffff0000, v128
	v_add_f32_e32 v132, v132, v134
	v_add_f32_e32 v125, v125, v126
	v_lshlrev_b32_e32 v126, 16, v128
	v_mul_f32_e32 v128, v57, v127
	v_lshlrev_b32_e32 v131, 16, v129
	v_and_b32_e32 v129, 0xffff0000, v129
	v_mul_f32_e32 v127, v63, v127
	v_add_f32_e32 v130, v130, v132
	v_fmac_f32_e32 v128, v48, v126
	v_mul_f32_e32 v132, v59, v129
	v_fmac_f32_e32 v127, v58, v126
	v_mul_f32_e32 v126, v64, v129
	v_fmac_f32_e32 v132, v53, v131
	v_fmac_f32_e32 v126, v62, v131
	v_add_f32_e32 v128, v128, v132
	v_add_f32_e32 v126, v127, v126
	v_add_f32_e32 v130, v130, v128
	v_add_f32_e32 v125, v125, v126
	ds_read2st64_b64 v[126:129], v105 offset0:100 offset1:101
	s_waitcnt lgkmcnt(0)
	v_lshlrev_b32_e32 v131, 16, v126
	v_and_b32_e32 v126, 0xffff0000, v126
	v_lshlrev_b32_e32 v133, 16, v127
	v_and_b32_e32 v127, 0xffff0000, v127
	v_mul_f32_e32 v132, v68, v126
	v_mul_f32_e32 v134, v69, v127
	v_mul_f32_e32 v126, v71, v126
	v_mul_f32_e32 v127, v74, v127
	v_fmac_f32_e32 v126, v70, v131
	v_fmac_f32_e32 v127, v72, v133
	v_fmac_f32_e32 v132, v66, v131
	v_fmac_f32_e32 v134, v67, v133
	v_add_f32_e32 v126, v126, v127
	v_and_b32_e32 v127, 0xffff0000, v128
	v_add_f32_e32 v132, v132, v134
	v_add_f32_e32 v125, v125, v126
	v_lshlrev_b32_e32 v126, 16, v128
	v_mul_f32_e32 v128, v76, v127
	v_lshlrev_b32_e32 v131, 16, v129
	v_and_b32_e32 v129, 0xffff0000, v129
	v_mul_f32_e32 v127, v86, v127
	v_add_f32_e32 v130, v130, v132
	v_fmac_f32_e32 v128, v73, v126
	v_mul_f32_e32 v132, v81, v129
	v_fmac_f32_e32 v127, v82, v126
	v_mul_f32_e32 v126, v91, v129
	v_fmac_f32_e32 v132, v75, v131
	v_fmac_f32_e32 v126, v87, v131
	v_add_f32_e32 v128, v128, v132
	v_add_f32_e32 v126, v127, v126
	v_add_f32_e32 v130, v130, v128
	v_add_f32_e32 v125, v125, v126
	ds_read2st64_b64 v[126:129], v105 offset0:102 offset1:103
	s_waitcnt lgkmcnt(0)
	v_lshlrev_b32_e32 v131, 16, v126
	v_and_b32_e32 v126, 0xffff0000, v126
	v_lshlrev_b32_e32 v133, 16, v127
	v_and_b32_e32 v127, 0xffff0000, v127
	v_mul_f32_e32 v132, v83, v126
	v_mul_f32_e32 v134, v88, v127
	v_mul_f32_e32 v126, v93, v126
	v_mul_f32_e32 v127, v94, v127
	v_fmac_f32_e32 v132, v77, v131
	v_fmac_f32_e32 v134, v80, v133
	v_fmac_f32_e32 v126, v84, v131
	v_fmac_f32_e32 v127, v89, v133
	v_add_f32_e32 v132, v132, v134
	v_add_f32_e32 v126, v126, v127
	v_lshlrev_b32_e32 v127, 16, v128
	v_and_b32_e32 v128, 0xffff0000, v128
	v_lshlrev_b32_e32 v131, 16, v129
	v_and_b32_e32 v129, 0xffff0000, v129
	v_add_f32_e32 v130, v130, v132
	v_add_f32_e32 v125, v125, v126
	v_mul_f32_e32 v126, v95, v128
	v_mul_f32_e32 v132, v97, v129
	v_mul_f32_e32 v128, v121, v128
	v_fmac_f32_e32 v126, v85, v127
	v_fmac_f32_e32 v132, v90, v131
	v_fmac_f32_e32 v128, v96, v127
	v_mul_f32_e32 v127, v122, v129
	v_add_f32_e32 v126, v126, v132
	v_fmac_f32_e32 v127, v120, v131
	v_add_f32_e32 v126, v130, v126
	v_add_f32_e32 v127, v128, v127
	ds_read2st64_b64 v[128:131], v105 offset0:104 offset1:105
	v_add_f32_e32 v125, v125, v127
	s_waitcnt lgkmcnt(0)
	v_lshlrev_b32_e32 v127, 16, v128
	v_and_b32_e32 v128, 0xffff0000, v128
	v_mul_f32_e32 v132, v9, v128
	v_lshlrev_b32_e32 v133, 16, v129
	v_and_b32_e32 v129, 0xffff0000, v129
	v_mul_f32_e32 v128, v12, v128
	v_fmac_f32_e32 v132, v7, v127
	v_fmac_f32_e32 v128, v11, v127
	v_mul_f32_e32 v127, v15, v129
	v_mul_f32_e32 v134, v10, v129
	v_fmac_f32_e32 v127, v13, v133
	v_and_b32_e32 v129, 0xffff0000, v130
	v_fmac_f32_e32 v134, v8, v133
	v_add_f32_e32 v127, v128, v127
	v_lshlrev_b32_e32 v128, 16, v130
	v_mul_f32_e32 v130, v17, v129
	v_lshlrev_b32_e32 v133, 16, v131
	v_and_b32_e32 v131, 0xffff0000, v131
	v_mul_f32_e32 v129, v49, v129
	v_add_f32_e32 v132, v132, v134
	v_fmac_f32_e32 v130, v14, v128
	v_mul_f32_e32 v134, v20, v131
	v_fmac_f32_e32 v129, v21, v128
	v_mul_f32_e32 v128, v54, v131
	v_fmac_f32_e32 v134, v16, v133
	v_fmac_f32_e32 v128, v50, v133
	v_add_f32_e32 v132, 0, v132
	v_add_f32_e32 v127, 0, v127
	v_add_f32_e32 v130, v130, v134
	v_add_f32_e32 v128, v129, v128
	v_add_f32_e32 v132, v132, v130
	v_add_f32_e32 v127, v127, v128
	ds_read2st64_b64 v[128:131], v105 offset0:106 offset1:107
	s_waitcnt lgkmcnt(0)
	v_lshlrev_b32_e32 v133, 16, v128
	v_and_b32_e32 v128, 0xffff0000, v128
	v_lshlrev_b32_e32 v135, 16, v129
	v_and_b32_e32 v129, 0xffff0000, v129
	v_mul_f32_e32 v134, v46, v128
	v_mul_f32_e32 v136, v51, v129
	v_mul_f32_e32 v128, v55, v128
	v_mul_f32_e32 v129, v56, v129
	v_fmac_f32_e32 v128, v47, v133
	v_fmac_f32_e32 v129, v52, v135
	v_fmac_f32_e32 v134, v18, v133
	v_fmac_f32_e32 v136, v19, v135
	v_add_f32_e32 v128, v128, v129
	v_and_b32_e32 v129, 0xffff0000, v130
	v_add_f32_e32 v134, v134, v136
	v_add_f32_e32 v127, v127, v128
	v_lshlrev_b32_e32 v128, 16, v130
	v_mul_f32_e32 v130, v57, v129
	v_lshlrev_b32_e32 v133, 16, v131
	v_and_b32_e32 v131, 0xffff0000, v131
	v_mul_f32_e32 v129, v63, v129
	v_add_f32_e32 v132, v132, v134
	v_fmac_f32_e32 v130, v48, v128
	v_mul_f32_e32 v134, v59, v131
	v_fmac_f32_e32 v129, v58, v128
	v_mul_f32_e32 v128, v64, v131
	v_fmac_f32_e32 v134, v53, v133
	v_fmac_f32_e32 v128, v62, v133
	v_add_f32_e32 v130, v130, v134
	v_add_f32_e32 v128, v129, v128
	v_add_f32_e32 v132, v132, v130
	v_add_f32_e32 v127, v127, v128
	ds_read2st64_b64 v[128:131], v105 offset0:108 offset1:109
	s_waitcnt lgkmcnt(0)
	v_lshlrev_b32_e32 v133, 16, v128
	v_and_b32_e32 v128, 0xffff0000, v128
	v_lshlrev_b32_e32 v135, 16, v129
	v_and_b32_e32 v129, 0xffff0000, v129
	v_mul_f32_e32 v134, v68, v128
	v_mul_f32_e32 v136, v69, v129
	v_mul_f32_e32 v128, v71, v128
	v_mul_f32_e32 v129, v74, v129
	v_fmac_f32_e32 v128, v70, v133
	v_fmac_f32_e32 v129, v72, v135
	v_fmac_f32_e32 v134, v66, v133
	v_fmac_f32_e32 v136, v67, v135
	v_add_f32_e32 v128, v128, v129
	v_and_b32_e32 v129, 0xffff0000, v130
	v_add_f32_e32 v134, v134, v136
	v_add_f32_e32 v127, v127, v128
	v_lshlrev_b32_e32 v128, 16, v130
	v_mul_f32_e32 v130, v76, v129
	v_lshlrev_b32_e32 v133, 16, v131
	v_and_b32_e32 v131, 0xffff0000, v131
	v_mul_f32_e32 v129, v86, v129
	v_add_f32_e32 v132, v132, v134
	v_fmac_f32_e32 v130, v73, v128
	v_mul_f32_e32 v134, v81, v131
	v_fmac_f32_e32 v129, v82, v128
	v_mul_f32_e32 v128, v91, v131
	v_fmac_f32_e32 v134, v75, v133
	v_fmac_f32_e32 v128, v87, v133
	v_add_f32_e32 v130, v130, v134
	v_add_f32_e32 v128, v129, v128
	v_add_f32_e32 v132, v132, v130
	v_add_f32_e32 v127, v127, v128
	ds_read2st64_b64 v[128:131], v105 offset0:110 offset1:111
	s_waitcnt lgkmcnt(0)
	v_lshlrev_b32_e32 v133, 16, v128
	v_and_b32_e32 v128, 0xffff0000, v128
	v_lshlrev_b32_e32 v135, 16, v129
	v_and_b32_e32 v129, 0xffff0000, v129
	v_mul_f32_e32 v134, v83, v128
	v_mul_f32_e32 v136, v88, v129
	v_mul_f32_e32 v128, v93, v128
	v_mul_f32_e32 v129, v94, v129
	v_fmac_f32_e32 v134, v77, v133
	v_fmac_f32_e32 v136, v80, v135
	v_fmac_f32_e32 v128, v84, v133
	v_fmac_f32_e32 v129, v89, v135
	v_add_f32_e32 v134, v134, v136
	v_add_f32_e32 v128, v128, v129
	v_lshlrev_b32_e32 v129, 16, v130
	v_and_b32_e32 v130, 0xffff0000, v130
	v_lshlrev_b32_e32 v133, 16, v131
	v_and_b32_e32 v131, 0xffff0000, v131
	v_add_f32_e32 v132, v132, v134
	v_add_f32_e32 v127, v127, v128
	v_mul_f32_e32 v128, v95, v130
	v_mul_f32_e32 v134, v97, v131
	v_mul_f32_e32 v130, v121, v130
	v_fmac_f32_e32 v128, v85, v129
	v_fmac_f32_e32 v134, v90, v133
	v_fmac_f32_e32 v130, v96, v129
	v_mul_f32_e32 v129, v122, v131
	v_add_f32_e32 v128, v128, v134
	v_fmac_f32_e32 v129, v120, v133
	v_add_f32_e32 v128, v132, v128
	v_add_f32_e32 v129, v130, v129
	ds_read2st64_b64 v[130:133], v105 offset0:112 offset1:113
	v_add_f32_e32 v127, v127, v129
	s_waitcnt lgkmcnt(0)
	v_lshlrev_b32_e32 v129, 16, v130
	v_and_b32_e32 v130, 0xffff0000, v130
	v_mul_f32_e32 v134, v9, v130
	v_lshlrev_b32_e32 v135, 16, v131
	v_and_b32_e32 v131, 0xffff0000, v131
	v_mul_f32_e32 v130, v12, v130
	v_fmac_f32_e32 v134, v7, v129
	v_fmac_f32_e32 v130, v11, v129
	v_mul_f32_e32 v129, v15, v131
	v_mul_f32_e32 v136, v10, v131
	v_fmac_f32_e32 v129, v13, v135
	v_and_b32_e32 v131, 0xffff0000, v132
	v_fmac_f32_e32 v136, v8, v135
	v_add_f32_e32 v129, v130, v129
	v_lshlrev_b32_e32 v130, 16, v132
	v_mul_f32_e32 v132, v17, v131
	v_lshlrev_b32_e32 v135, 16, v133
	v_and_b32_e32 v133, 0xffff0000, v133
	v_mul_f32_e32 v131, v49, v131
	v_add_f32_e32 v134, v134, v136
	v_fmac_f32_e32 v132, v14, v130
	v_mul_f32_e32 v136, v20, v133
	v_fmac_f32_e32 v131, v21, v130
	v_mul_f32_e32 v130, v54, v133
	v_fmac_f32_e32 v136, v16, v135
	v_fmac_f32_e32 v130, v50, v135
	v_add_f32_e32 v134, 0, v134
	v_add_f32_e32 v129, 0, v129
	v_add_f32_e32 v132, v132, v136
	v_add_f32_e32 v130, v131, v130
	v_add_f32_e32 v134, v134, v132
	v_add_f32_e32 v129, v129, v130
	ds_read2st64_b64 v[130:133], v105 offset0:114 offset1:115
	s_waitcnt lgkmcnt(0)
	v_lshlrev_b32_e32 v135, 16, v130
	v_and_b32_e32 v130, 0xffff0000, v130
	v_lshlrev_b32_e32 v137, 16, v131
	v_and_b32_e32 v131, 0xffff0000, v131
	v_mul_f32_e32 v136, v46, v130
	v_mul_f32_e32 v138, v51, v131
	v_mul_f32_e32 v130, v55, v130
	v_mul_f32_e32 v131, v56, v131
	v_fmac_f32_e32 v130, v47, v135
	v_fmac_f32_e32 v131, v52, v137
	v_fmac_f32_e32 v136, v18, v135
	v_fmac_f32_e32 v138, v19, v137
	v_add_f32_e32 v130, v130, v131
	v_and_b32_e32 v131, 0xffff0000, v132
	v_add_f32_e32 v136, v136, v138
	v_add_f32_e32 v129, v129, v130
	v_lshlrev_b32_e32 v130, 16, v132
	v_mul_f32_e32 v132, v57, v131
	v_lshlrev_b32_e32 v135, 16, v133
	v_and_b32_e32 v133, 0xffff0000, v133
	v_mul_f32_e32 v131, v63, v131
	v_add_f32_e32 v134, v134, v136
	v_fmac_f32_e32 v132, v48, v130
	v_mul_f32_e32 v136, v59, v133
	v_fmac_f32_e32 v131, v58, v130
	v_mul_f32_e32 v130, v64, v133
	v_fmac_f32_e32 v136, v53, v135
	v_fmac_f32_e32 v130, v62, v135
	v_add_f32_e32 v132, v132, v136
	v_add_f32_e32 v130, v131, v130
	v_add_f32_e32 v134, v134, v132
	v_add_f32_e32 v129, v129, v130
	ds_read2st64_b64 v[130:133], v105 offset0:116 offset1:117
	s_waitcnt lgkmcnt(0)
	v_lshlrev_b32_e32 v135, 16, v130
	v_and_b32_e32 v130, 0xffff0000, v130
	v_lshlrev_b32_e32 v137, 16, v131
	v_and_b32_e32 v131, 0xffff0000, v131
	v_mul_f32_e32 v136, v68, v130
	v_mul_f32_e32 v138, v69, v131
	v_mul_f32_e32 v130, v71, v130
	v_mul_f32_e32 v131, v74, v131
	v_fmac_f32_e32 v130, v70, v135
	v_fmac_f32_e32 v131, v72, v137
	v_fmac_f32_e32 v136, v66, v135
	v_fmac_f32_e32 v138, v67, v137
	v_add_f32_e32 v130, v130, v131
	v_and_b32_e32 v131, 0xffff0000, v132
	v_add_f32_e32 v136, v136, v138
	v_add_f32_e32 v129, v129, v130
	v_lshlrev_b32_e32 v130, 16, v132
	v_mul_f32_e32 v132, v76, v131
	v_lshlrev_b32_e32 v135, 16, v133
	v_and_b32_e32 v133, 0xffff0000, v133
	v_mul_f32_e32 v131, v86, v131
	v_add_f32_e32 v134, v134, v136
	v_fmac_f32_e32 v132, v73, v130
	v_mul_f32_e32 v136, v81, v133
	v_fmac_f32_e32 v131, v82, v130
	v_mul_f32_e32 v130, v91, v133
	v_fmac_f32_e32 v136, v75, v135
	v_fmac_f32_e32 v130, v87, v135
	v_add_f32_e32 v132, v132, v136
	v_add_f32_e32 v130, v131, v130
	v_add_f32_e32 v134, v134, v132
	v_add_f32_e32 v129, v129, v130
	ds_read2st64_b64 v[130:133], v105 offset0:118 offset1:119
	s_waitcnt lgkmcnt(0)
	v_lshlrev_b32_e32 v135, 16, v130
	v_and_b32_e32 v130, 0xffff0000, v130
	v_lshlrev_b32_e32 v137, 16, v131
	v_and_b32_e32 v131, 0xffff0000, v131
	v_mul_f32_e32 v136, v83, v130
	v_mul_f32_e32 v138, v88, v131
	v_mul_f32_e32 v130, v93, v130
	v_mul_f32_e32 v131, v94, v131
	v_fmac_f32_e32 v136, v77, v135
	v_fmac_f32_e32 v138, v80, v137
	v_fmac_f32_e32 v130, v84, v135
	v_fmac_f32_e32 v131, v89, v137
	v_add_f32_e32 v136, v136, v138
	v_add_f32_e32 v130, v130, v131
	v_lshlrev_b32_e32 v131, 16, v132
	v_and_b32_e32 v132, 0xffff0000, v132
	v_lshlrev_b32_e32 v135, 16, v133
	v_and_b32_e32 v133, 0xffff0000, v133
	v_add_f32_e32 v134, v134, v136
	v_add_f32_e32 v129, v129, v130
	v_mul_f32_e32 v130, v95, v132
	v_mul_f32_e32 v136, v97, v133
	v_mul_f32_e32 v132, v121, v132
	v_fmac_f32_e32 v130, v85, v131
	v_fmac_f32_e32 v136, v90, v135
	v_fmac_f32_e32 v132, v96, v131
	v_mul_f32_e32 v131, v122, v133
	v_add_f32_e32 v130, v130, v136
	v_fmac_f32_e32 v131, v120, v135
	v_add_f32_e32 v130, v134, v130
	v_add_f32_e32 v131, v132, v131
	ds_read2st64_b64 v[132:135], v105 offset0:120 offset1:121
	v_add_f32_e32 v129, v129, v131
	s_waitcnt lgkmcnt(0)
	v_lshlrev_b32_e32 v131, 16, v132
	v_and_b32_e32 v132, 0xffff0000, v132
	v_mul_f32_e32 v136, v9, v132
	v_lshlrev_b32_e32 v137, 16, v133
	v_and_b32_e32 v133, 0xffff0000, v133
	v_mul_f32_e32 v132, v12, v132
	v_fmac_f32_e32 v136, v7, v131
	v_fmac_f32_e32 v132, v11, v131
	v_mul_f32_e32 v131, v15, v133
	v_mul_f32_e32 v138, v10, v133
	v_fmac_f32_e32 v131, v13, v137
	v_and_b32_e32 v133, 0xffff0000, v134
	v_fmac_f32_e32 v138, v8, v137
	v_add_f32_e32 v131, v132, v131
	v_lshlrev_b32_e32 v132, 16, v134
	v_mul_f32_e32 v134, v17, v133
	v_lshlrev_b32_e32 v137, 16, v135
	v_and_b32_e32 v135, 0xffff0000, v135
	v_mul_f32_e32 v133, v49, v133
	v_add_f32_e32 v136, v136, v138
	v_fmac_f32_e32 v134, v14, v132
	v_mul_f32_e32 v138, v20, v135
	v_fmac_f32_e32 v133, v21, v132
	v_mul_f32_e32 v132, v54, v135
	v_fmac_f32_e32 v138, v16, v137
	v_fmac_f32_e32 v132, v50, v137
	v_add_f32_e32 v136, 0, v136
	v_add_f32_e32 v131, 0, v131
	v_add_f32_e32 v134, v134, v138
	v_add_f32_e32 v132, v133, v132
	v_add_f32_e32 v136, v136, v134
	v_add_f32_e32 v131, v131, v132
	ds_read2st64_b64 v[132:135], v105 offset0:122 offset1:123
	s_waitcnt lgkmcnt(0)
	v_lshlrev_b32_e32 v137, 16, v132
	v_and_b32_e32 v132, 0xffff0000, v132
	v_lshlrev_b32_e32 v139, 16, v133
	v_and_b32_e32 v133, 0xffff0000, v133
	v_mul_f32_e32 v138, v46, v132
	v_mul_f32_e32 v140, v51, v133
	v_mul_f32_e32 v132, v55, v132
	v_mul_f32_e32 v133, v56, v133
	v_fmac_f32_e32 v132, v47, v137
	v_fmac_f32_e32 v133, v52, v139
	v_fmac_f32_e32 v138, v18, v137
	v_fmac_f32_e32 v140, v19, v139
	v_add_f32_e32 v132, v132, v133
	v_and_b32_e32 v133, 0xffff0000, v134
	v_add_f32_e32 v138, v138, v140
	v_add_f32_e32 v131, v131, v132
	v_lshlrev_b32_e32 v132, 16, v134
	v_mul_f32_e32 v134, v57, v133
	v_lshlrev_b32_e32 v137, 16, v135
	v_and_b32_e32 v135, 0xffff0000, v135
	v_mul_f32_e32 v133, v63, v133
	v_add_f32_e32 v136, v136, v138
	v_fmac_f32_e32 v134, v48, v132
	v_mul_f32_e32 v138, v59, v135
	v_fmac_f32_e32 v133, v58, v132
	v_mul_f32_e32 v132, v64, v135
	v_fmac_f32_e32 v138, v53, v137
	v_fmac_f32_e32 v132, v62, v137
	v_add_f32_e32 v134, v134, v138
	v_add_f32_e32 v132, v133, v132
	v_add_f32_e32 v136, v136, v134
	v_add_f32_e32 v131, v131, v132
	ds_read2st64_b64 v[132:135], v105 offset0:124 offset1:125
	s_waitcnt lgkmcnt(0)
	v_lshlrev_b32_e32 v137, 16, v132
	v_and_b32_e32 v132, 0xffff0000, v132
	v_lshlrev_b32_e32 v139, 16, v133
	v_and_b32_e32 v133, 0xffff0000, v133
	v_mul_f32_e32 v138, v68, v132
	v_mul_f32_e32 v140, v69, v133
	v_mul_f32_e32 v132, v71, v132
	v_mul_f32_e32 v133, v74, v133
	v_fmac_f32_e32 v132, v70, v137
	v_fmac_f32_e32 v133, v72, v139
	v_fmac_f32_e32 v138, v66, v137
	v_fmac_f32_e32 v140, v67, v139
	v_add_f32_e32 v132, v132, v133
	v_and_b32_e32 v133, 0xffff0000, v134
	v_add_f32_e32 v138, v138, v140
	v_add_f32_e32 v131, v131, v132
	v_lshlrev_b32_e32 v132, 16, v134
	v_mul_f32_e32 v134, v76, v133
	v_lshlrev_b32_e32 v137, 16, v135
	v_and_b32_e32 v135, 0xffff0000, v135
	v_mul_f32_e32 v133, v86, v133
	v_add_f32_e32 v136, v136, v138
	v_fmac_f32_e32 v134, v73, v132
	v_mul_f32_e32 v138, v81, v135
	v_fmac_f32_e32 v133, v82, v132
	v_mul_f32_e32 v132, v91, v135
	v_fmac_f32_e32 v138, v75, v137
	v_fmac_f32_e32 v132, v87, v137
	v_add_f32_e32 v134, v134, v138
	v_add_f32_e32 v132, v133, v132
	v_add_f32_e32 v136, v136, v134
	v_add_f32_e32 v131, v131, v132
	ds_read2st64_b64 v[132:135], v105 offset0:126 offset1:127
	s_waitcnt lgkmcnt(0)
	v_lshlrev_b32_e32 v137, 16, v132
	v_and_b32_e32 v132, 0xffff0000, v132
	v_lshlrev_b32_e32 v139, 16, v133
	v_and_b32_e32 v133, 0xffff0000, v133
	v_mul_f32_e32 v138, v83, v132
	v_mul_f32_e32 v140, v88, v133
	v_mul_f32_e32 v132, v93, v132
	v_mul_f32_e32 v133, v94, v133
	v_fmac_f32_e32 v138, v77, v137
	v_fmac_f32_e32 v140, v80, v139
	v_fmac_f32_e32 v132, v84, v137
	v_fmac_f32_e32 v133, v89, v139
	v_add_f32_e32 v138, v138, v140
	v_add_f32_e32 v132, v132, v133
	v_lshlrev_b32_e32 v133, 16, v134
	v_and_b32_e32 v134, 0xffff0000, v134
	v_lshlrev_b32_e32 v137, 16, v135
	v_and_b32_e32 v135, 0xffff0000, v135
	v_add_f32_e32 v136, v136, v138
	v_add_f32_e32 v131, v131, v132
	v_mul_f32_e32 v132, v95, v134
	v_mul_f32_e32 v138, v97, v135
	v_mul_f32_e32 v134, v121, v134
	v_fmac_f32_e32 v132, v85, v133
	v_fmac_f32_e32 v138, v90, v137
	v_fmac_f32_e32 v134, v96, v133
	v_mul_f32_e32 v133, v122, v135
	v_add_f32_e32 v132, v132, v138
	v_fmac_f32_e32 v133, v120, v137
	v_add_f32_e32 v132, v136, v132
	v_add_f32_e32 v133, v134, v133
	ds_read2st64_b64 v[134:137], v106 offset0:64 offset1:65
	v_add_f32_e32 v131, v131, v133
	s_waitcnt lgkmcnt(0)
	v_lshlrev_b32_e32 v133, 16, v134
	v_and_b32_e32 v134, 0xffff0000, v134
	v_mul_f32_e32 v138, v9, v134
	v_lshlrev_b32_e32 v139, 16, v135
	v_and_b32_e32 v135, 0xffff0000, v135
	v_mul_f32_e32 v134, v12, v134
	v_fmac_f32_e32 v138, v7, v133
	v_fmac_f32_e32 v134, v11, v133
	v_mul_f32_e32 v133, v15, v135
	v_mul_f32_e32 v140, v10, v135
	v_fmac_f32_e32 v133, v13, v139
	v_and_b32_e32 v135, 0xffff0000, v136
	v_fmac_f32_e32 v140, v8, v139
	v_add_f32_e32 v133, v134, v133
	v_lshlrev_b32_e32 v134, 16, v136
	v_mul_f32_e32 v136, v17, v135
	v_lshlrev_b32_e32 v139, 16, v137
	v_and_b32_e32 v137, 0xffff0000, v137
	v_mul_f32_e32 v135, v49, v135
	v_add_f32_e32 v138, v138, v140
	v_fmac_f32_e32 v136, v14, v134
	v_mul_f32_e32 v140, v20, v137
	v_fmac_f32_e32 v135, v21, v134
	v_mul_f32_e32 v134, v54, v137
	v_fmac_f32_e32 v140, v16, v139
	v_fmac_f32_e32 v134, v50, v139
	v_add_f32_e32 v138, 0, v138
	v_add_f32_e32 v133, 0, v133
	v_add_f32_e32 v136, v136, v140
	v_add_f32_e32 v134, v135, v134
	v_add_f32_e32 v138, v138, v136
	v_add_f32_e32 v133, v133, v134
	ds_read2st64_b64 v[134:137], v106 offset0:66 offset1:67
	s_waitcnt lgkmcnt(0)
	v_lshlrev_b32_e32 v139, 16, v134
	v_and_b32_e32 v134, 0xffff0000, v134
	v_lshlrev_b32_e32 v141, 16, v135
	v_and_b32_e32 v135, 0xffff0000, v135
	v_mul_f32_e32 v140, v46, v134
	v_mul_f32_e32 v142, v51, v135
	v_mul_f32_e32 v134, v55, v134
	v_mul_f32_e32 v135, v56, v135
	v_fmac_f32_e32 v134, v47, v139
	v_fmac_f32_e32 v135, v52, v141
	v_fmac_f32_e32 v140, v18, v139
	v_fmac_f32_e32 v142, v19, v141
	v_add_f32_e32 v134, v134, v135
	v_and_b32_e32 v135, 0xffff0000, v136
	v_add_f32_e32 v140, v140, v142
	v_add_f32_e32 v133, v133, v134
	v_lshlrev_b32_e32 v134, 16, v136
	v_mul_f32_e32 v136, v57, v135
	v_lshlrev_b32_e32 v139, 16, v137
	v_and_b32_e32 v137, 0xffff0000, v137
	v_mul_f32_e32 v135, v63, v135
	v_add_f32_e32 v138, v138, v140
	v_fmac_f32_e32 v136, v48, v134
	v_mul_f32_e32 v140, v59, v137
	v_fmac_f32_e32 v135, v58, v134
	v_mul_f32_e32 v134, v64, v137
	v_fmac_f32_e32 v140, v53, v139
	v_fmac_f32_e32 v134, v62, v139
	v_add_f32_e32 v136, v136, v140
	v_add_f32_e32 v134, v135, v134
	v_add_f32_e32 v138, v138, v136
	v_add_f32_e32 v133, v133, v134
	ds_read2st64_b64 v[134:137], v106 offset0:68 offset1:69
	s_waitcnt lgkmcnt(0)
	v_lshlrev_b32_e32 v139, 16, v134
	v_and_b32_e32 v134, 0xffff0000, v134
	v_lshlrev_b32_e32 v141, 16, v135
	v_and_b32_e32 v135, 0xffff0000, v135
	v_mul_f32_e32 v140, v68, v134
	v_mul_f32_e32 v142, v69, v135
	v_mul_f32_e32 v134, v71, v134
	v_mul_f32_e32 v135, v74, v135
	v_fmac_f32_e32 v134, v70, v139
	v_fmac_f32_e32 v135, v72, v141
	v_fmac_f32_e32 v140, v66, v139
	v_fmac_f32_e32 v142, v67, v141
	v_add_f32_e32 v134, v134, v135
	v_and_b32_e32 v135, 0xffff0000, v136
	v_add_f32_e32 v140, v140, v142
	v_add_f32_e32 v133, v133, v134
	v_lshlrev_b32_e32 v134, 16, v136
	v_mul_f32_e32 v136, v76, v135
	v_lshlrev_b32_e32 v139, 16, v137
	v_and_b32_e32 v137, 0xffff0000, v137
	v_mul_f32_e32 v135, v86, v135
	v_add_f32_e32 v138, v138, v140
	v_fmac_f32_e32 v136, v73, v134
	v_mul_f32_e32 v140, v81, v137
	v_fmac_f32_e32 v135, v82, v134
	v_mul_f32_e32 v134, v91, v137
	v_fmac_f32_e32 v140, v75, v139
	v_fmac_f32_e32 v134, v87, v139
	v_add_f32_e32 v136, v136, v140
	v_add_f32_e32 v134, v135, v134
	v_add_f32_e32 v138, v138, v136
	v_add_f32_e32 v133, v133, v134
	ds_read2st64_b64 v[134:137], v106 offset0:70 offset1:71
	s_waitcnt lgkmcnt(0)
	v_lshlrev_b32_e32 v139, 16, v134
	v_and_b32_e32 v134, 0xffff0000, v134
	v_lshlrev_b32_e32 v141, 16, v135
	v_and_b32_e32 v135, 0xffff0000, v135
	v_mul_f32_e32 v140, v83, v134
	v_mul_f32_e32 v142, v88, v135
	v_mul_f32_e32 v134, v93, v134
	v_mul_f32_e32 v135, v94, v135
	v_fmac_f32_e32 v140, v77, v139
	v_fmac_f32_e32 v142, v80, v141
	v_fmac_f32_e32 v134, v84, v139
	v_fmac_f32_e32 v135, v89, v141
	v_add_f32_e32 v140, v140, v142
	v_add_f32_e32 v134, v134, v135
	v_lshlrev_b32_e32 v135, 16, v136
	v_and_b32_e32 v136, 0xffff0000, v136
	v_lshlrev_b32_e32 v139, 16, v137
	v_and_b32_e32 v137, 0xffff0000, v137
	v_add_f32_e32 v138, v138, v140
	v_add_f32_e32 v133, v133, v134
	v_mul_f32_e32 v134, v95, v136
	v_mul_f32_e32 v140, v97, v137
	v_mul_f32_e32 v136, v121, v136
	v_fmac_f32_e32 v134, v85, v135
	v_fmac_f32_e32 v140, v90, v139
	v_fmac_f32_e32 v136, v96, v135
	v_mul_f32_e32 v135, v122, v137
	v_add_f32_e32 v134, v134, v140
	v_fmac_f32_e32 v135, v120, v139
	v_add_f32_e32 v134, v138, v134
	v_add_f32_e32 v135, v136, v135
	ds_read2st64_b64 v[136:139], v106 offset0:72 offset1:73
	v_add_f32_e32 v133, v133, v135
	s_waitcnt lgkmcnt(0)
	v_lshlrev_b32_e32 v135, 16, v136
	v_and_b32_e32 v136, 0xffff0000, v136
	v_mul_f32_e32 v140, v9, v136
	v_lshlrev_b32_e32 v141, 16, v137
	v_and_b32_e32 v137, 0xffff0000, v137
	v_mul_f32_e32 v136, v12, v136
	v_fmac_f32_e32 v140, v7, v135
	v_fmac_f32_e32 v136, v11, v135
	v_mul_f32_e32 v135, v15, v137
	v_mul_f32_e32 v142, v10, v137
	v_fmac_f32_e32 v135, v13, v141
	v_and_b32_e32 v137, 0xffff0000, v138
	v_fmac_f32_e32 v142, v8, v141
	v_add_f32_e32 v135, v136, v135
	v_lshlrev_b32_e32 v136, 16, v138
	v_mul_f32_e32 v138, v17, v137
	v_lshlrev_b32_e32 v141, 16, v139
	v_and_b32_e32 v139, 0xffff0000, v139
	v_mul_f32_e32 v137, v49, v137
	v_add_f32_e32 v140, v140, v142
	v_fmac_f32_e32 v138, v14, v136
	v_mul_f32_e32 v142, v20, v139
	v_fmac_f32_e32 v137, v21, v136
	v_mul_f32_e32 v136, v54, v139
	v_fmac_f32_e32 v142, v16, v141
	v_fmac_f32_e32 v136, v50, v141
	v_add_f32_e32 v140, 0, v140
	v_add_f32_e32 v135, 0, v135
	v_add_f32_e32 v138, v138, v142
	v_add_f32_e32 v136, v137, v136
	v_add_f32_e32 v140, v140, v138
	v_add_f32_e32 v135, v135, v136
	ds_read2st64_b64 v[136:139], v106 offset0:74 offset1:75
	s_waitcnt lgkmcnt(0)
	v_lshlrev_b32_e32 v141, 16, v136
	v_and_b32_e32 v136, 0xffff0000, v136
	v_lshlrev_b32_e32 v143, 16, v137
	v_and_b32_e32 v137, 0xffff0000, v137
	v_mul_f32_e32 v142, v46, v136
	v_mul_f32_e32 v144, v51, v137
	v_mul_f32_e32 v136, v55, v136
	v_mul_f32_e32 v137, v56, v137
	v_fmac_f32_e32 v136, v47, v141
	v_fmac_f32_e32 v137, v52, v143
	v_fmac_f32_e32 v142, v18, v141
	v_fmac_f32_e32 v144, v19, v143
	v_add_f32_e32 v136, v136, v137
	v_and_b32_e32 v137, 0xffff0000, v138
	v_add_f32_e32 v142, v142, v144
	v_add_f32_e32 v135, v135, v136
	v_lshlrev_b32_e32 v136, 16, v138
	v_mul_f32_e32 v138, v57, v137
	v_lshlrev_b32_e32 v141, 16, v139
	v_and_b32_e32 v139, 0xffff0000, v139
	v_mul_f32_e32 v137, v63, v137
	v_add_f32_e32 v140, v140, v142
	v_fmac_f32_e32 v138, v48, v136
	v_mul_f32_e32 v142, v59, v139
	v_fmac_f32_e32 v137, v58, v136
	v_mul_f32_e32 v136, v64, v139
	v_fmac_f32_e32 v142, v53, v141
	v_fmac_f32_e32 v136, v62, v141
	v_add_f32_e32 v138, v138, v142
	v_add_f32_e32 v136, v137, v136
	v_add_f32_e32 v140, v140, v138
	v_add_f32_e32 v135, v135, v136
	ds_read2st64_b64 v[136:139], v106 offset0:76 offset1:77
	s_waitcnt lgkmcnt(0)
	v_lshlrev_b32_e32 v141, 16, v136
	v_and_b32_e32 v136, 0xffff0000, v136
	v_lshlrev_b32_e32 v143, 16, v137
	v_and_b32_e32 v137, 0xffff0000, v137
	v_mul_f32_e32 v142, v68, v136
	v_mul_f32_e32 v144, v69, v137
	v_mul_f32_e32 v136, v71, v136
	v_mul_f32_e32 v137, v74, v137
	v_fmac_f32_e32 v136, v70, v141
	v_fmac_f32_e32 v137, v72, v143
	v_fmac_f32_e32 v142, v66, v141
	v_fmac_f32_e32 v144, v67, v143
	v_add_f32_e32 v136, v136, v137
	v_and_b32_e32 v137, 0xffff0000, v138
	v_add_f32_e32 v142, v142, v144
	v_add_f32_e32 v135, v135, v136
	v_lshlrev_b32_e32 v136, 16, v138
	v_mul_f32_e32 v138, v76, v137
	v_lshlrev_b32_e32 v141, 16, v139
	v_and_b32_e32 v139, 0xffff0000, v139
	v_mul_f32_e32 v137, v86, v137
	v_add_f32_e32 v140, v140, v142
	v_fmac_f32_e32 v138, v73, v136
	v_mul_f32_e32 v142, v81, v139
	v_fmac_f32_e32 v137, v82, v136
	v_mul_f32_e32 v136, v91, v139
	v_fmac_f32_e32 v142, v75, v141
	v_fmac_f32_e32 v136, v87, v141
	v_add_f32_e32 v138, v138, v142
	v_add_f32_e32 v136, v137, v136
	v_add_f32_e32 v140, v140, v138
	v_add_f32_e32 v135, v135, v136
	ds_read2st64_b64 v[136:139], v106 offset0:78 offset1:79
	s_waitcnt lgkmcnt(0)
	v_lshlrev_b32_e32 v141, 16, v136
	v_and_b32_e32 v136, 0xffff0000, v136
	v_lshlrev_b32_e32 v143, 16, v137
	v_and_b32_e32 v137, 0xffff0000, v137
	v_mul_f32_e32 v142, v83, v136
	v_mul_f32_e32 v144, v88, v137
	v_mul_f32_e32 v136, v93, v136
	v_mul_f32_e32 v137, v94, v137
	v_fmac_f32_e32 v142, v77, v141
	v_fmac_f32_e32 v144, v80, v143
	v_fmac_f32_e32 v136, v84, v141
	v_fmac_f32_e32 v137, v89, v143
	v_add_f32_e32 v142, v142, v144
	v_add_f32_e32 v136, v136, v137
	v_lshlrev_b32_e32 v137, 16, v138
	v_and_b32_e32 v138, 0xffff0000, v138
	v_lshlrev_b32_e32 v141, 16, v139
	v_and_b32_e32 v139, 0xffff0000, v139
	v_add_f32_e32 v140, v140, v142
	v_add_f32_e32 v135, v135, v136
	v_mul_f32_e32 v136, v95, v138
	v_mul_f32_e32 v142, v97, v139
	v_mul_f32_e32 v138, v121, v138
	v_fmac_f32_e32 v136, v85, v137
	v_fmac_f32_e32 v142, v90, v141
	v_fmac_f32_e32 v138, v96, v137
	v_mul_f32_e32 v137, v122, v139
	v_add_f32_e32 v136, v136, v142
	v_fmac_f32_e32 v137, v120, v141
	v_add_f32_e32 v136, v140, v136
	v_add_f32_e32 v137, v138, v137
	ds_read2st64_b64 v[138:141], v106 offset0:80 offset1:81
	v_add_f32_e32 v135, v135, v137
	s_waitcnt lgkmcnt(0)
	v_lshlrev_b32_e32 v137, 16, v138
	v_and_b32_e32 v138, 0xffff0000, v138
	v_mul_f32_e32 v142, v9, v138
	v_lshlrev_b32_e32 v143, 16, v139
	v_and_b32_e32 v139, 0xffff0000, v139
	v_mul_f32_e32 v138, v12, v138
	v_fmac_f32_e32 v142, v7, v137
	v_fmac_f32_e32 v138, v11, v137
	v_mul_f32_e32 v137, v15, v139
	v_mul_f32_e32 v144, v10, v139
	v_fmac_f32_e32 v137, v13, v143
	v_and_b32_e32 v139, 0xffff0000, v140
	v_fmac_f32_e32 v144, v8, v143
	v_add_f32_e32 v137, v138, v137
	v_lshlrev_b32_e32 v138, 16, v140
	v_mul_f32_e32 v140, v17, v139
	v_lshlrev_b32_e32 v143, 16, v141
	v_and_b32_e32 v141, 0xffff0000, v141
	v_mul_f32_e32 v139, v49, v139
	v_add_f32_e32 v142, v142, v144
	v_fmac_f32_e32 v140, v14, v138
	v_mul_f32_e32 v144, v20, v141
	v_fmac_f32_e32 v139, v21, v138
	v_mul_f32_e32 v138, v54, v141
	v_fmac_f32_e32 v144, v16, v143
	v_fmac_f32_e32 v138, v50, v143
	v_add_f32_e32 v142, 0, v142
	v_add_f32_e32 v137, 0, v137
	v_add_f32_e32 v140, v140, v144
	v_add_f32_e32 v138, v139, v138
	v_add_f32_e32 v142, v142, v140
	v_add_f32_e32 v137, v137, v138
	ds_read2st64_b64 v[138:141], v106 offset0:82 offset1:83
	s_waitcnt lgkmcnt(0)
	v_lshlrev_b32_e32 v143, 16, v138
	v_and_b32_e32 v138, 0xffff0000, v138
	v_lshlrev_b32_e32 v145, 16, v139
	v_and_b32_e32 v139, 0xffff0000, v139
	v_mul_f32_e32 v144, v46, v138
	v_mul_f32_e32 v146, v51, v139
	v_mul_f32_e32 v138, v55, v138
	v_mul_f32_e32 v139, v56, v139
	v_fmac_f32_e32 v138, v47, v143
	v_fmac_f32_e32 v139, v52, v145
	v_fmac_f32_e32 v144, v18, v143
	v_fmac_f32_e32 v146, v19, v145
	v_add_f32_e32 v138, v138, v139
	v_and_b32_e32 v139, 0xffff0000, v140
	v_add_f32_e32 v144, v144, v146
	v_add_f32_e32 v137, v137, v138
	v_lshlrev_b32_e32 v138, 16, v140
	v_mul_f32_e32 v140, v57, v139
	v_lshlrev_b32_e32 v143, 16, v141
	v_and_b32_e32 v141, 0xffff0000, v141
	v_mul_f32_e32 v139, v63, v139
	v_add_f32_e32 v142, v142, v144
	v_fmac_f32_e32 v140, v48, v138
	v_mul_f32_e32 v144, v59, v141
	v_fmac_f32_e32 v139, v58, v138
	v_mul_f32_e32 v138, v64, v141
	v_fmac_f32_e32 v144, v53, v143
	v_fmac_f32_e32 v138, v62, v143
	v_add_f32_e32 v140, v140, v144
	v_add_f32_e32 v138, v139, v138
	v_add_f32_e32 v142, v142, v140
	v_add_f32_e32 v137, v137, v138
	ds_read2st64_b64 v[138:141], v106 offset0:84 offset1:85
	s_waitcnt lgkmcnt(0)
	v_lshlrev_b32_e32 v143, 16, v138
	v_and_b32_e32 v138, 0xffff0000, v138
	v_lshlrev_b32_e32 v145, 16, v139
	v_and_b32_e32 v139, 0xffff0000, v139
	v_mul_f32_e32 v144, v68, v138
	v_mul_f32_e32 v146, v69, v139
	v_mul_f32_e32 v138, v71, v138
	v_mul_f32_e32 v139, v74, v139
	v_fmac_f32_e32 v138, v70, v143
	v_fmac_f32_e32 v139, v72, v145
	v_fmac_f32_e32 v144, v66, v143
	v_fmac_f32_e32 v146, v67, v145
	v_add_f32_e32 v138, v138, v139
	v_and_b32_e32 v139, 0xffff0000, v140
	v_add_f32_e32 v144, v144, v146
	v_add_f32_e32 v137, v137, v138
	v_lshlrev_b32_e32 v138, 16, v140
	v_mul_f32_e32 v140, v76, v139
	v_lshlrev_b32_e32 v143, 16, v141
	v_and_b32_e32 v141, 0xffff0000, v141
	v_mul_f32_e32 v139, v86, v139
	v_add_f32_e32 v142, v142, v144
	v_fmac_f32_e32 v140, v73, v138
	v_mul_f32_e32 v144, v81, v141
	v_fmac_f32_e32 v139, v82, v138
	v_mul_f32_e32 v138, v91, v141
	v_fmac_f32_e32 v144, v75, v143
	v_fmac_f32_e32 v138, v87, v143
	v_add_f32_e32 v140, v140, v144
	v_add_f32_e32 v138, v139, v138
	v_add_f32_e32 v142, v142, v140
	v_add_f32_e32 v137, v137, v138
	ds_read2st64_b64 v[138:141], v106 offset0:86 offset1:87
	s_waitcnt lgkmcnt(0)
	v_lshlrev_b32_e32 v143, 16, v138
	v_and_b32_e32 v138, 0xffff0000, v138
	v_lshlrev_b32_e32 v145, 16, v139
	v_and_b32_e32 v139, 0xffff0000, v139
	v_mul_f32_e32 v144, v83, v138
	v_mul_f32_e32 v146, v88, v139
	v_mul_f32_e32 v138, v93, v138
	v_mul_f32_e32 v139, v94, v139
	v_fmac_f32_e32 v144, v77, v143
	v_fmac_f32_e32 v146, v80, v145
	v_fmac_f32_e32 v138, v84, v143
	v_fmac_f32_e32 v139, v89, v145
	v_add_f32_e32 v144, v144, v146
	v_add_f32_e32 v138, v138, v139
	v_lshlrev_b32_e32 v139, 16, v140
	v_and_b32_e32 v140, 0xffff0000, v140
	v_lshlrev_b32_e32 v143, 16, v141
	v_and_b32_e32 v141, 0xffff0000, v141
	v_add_f32_e32 v142, v142, v144
	v_add_f32_e32 v137, v137, v138
	v_mul_f32_e32 v138, v95, v140
	v_mul_f32_e32 v144, v97, v141
	v_mul_f32_e32 v140, v121, v140
	v_fmac_f32_e32 v138, v85, v139
	v_fmac_f32_e32 v144, v90, v143
	v_fmac_f32_e32 v140, v96, v139
	v_mul_f32_e32 v139, v122, v141
	v_add_f32_e32 v138, v138, v144
	v_fmac_f32_e32 v139, v120, v143
	v_add_f32_e32 v138, v142, v138
	v_add_f32_e32 v139, v140, v139
	ds_read2st64_b64 v[140:143], v106 offset0:88 offset1:89
	v_add_f32_e32 v137, v137, v139
	s_waitcnt lgkmcnt(0)
	v_lshlrev_b32_e32 v139, 16, v140
	v_and_b32_e32 v140, 0xffff0000, v140
	v_mul_f32_e32 v144, v9, v140
	v_lshlrev_b32_e32 v145, 16, v141
	v_and_b32_e32 v141, 0xffff0000, v141
	v_mul_f32_e32 v140, v12, v140
	v_fmac_f32_e32 v144, v7, v139
	v_fmac_f32_e32 v140, v11, v139
	v_mul_f32_e32 v139, v15, v141
	v_mul_f32_e32 v146, v10, v141
	v_fmac_f32_e32 v139, v13, v145
	v_and_b32_e32 v141, 0xffff0000, v142
	v_fmac_f32_e32 v146, v8, v145
	v_add_f32_e32 v139, v140, v139
	v_lshlrev_b32_e32 v140, 16, v142
	v_mul_f32_e32 v142, v17, v141
	v_lshlrev_b32_e32 v145, 16, v143
	v_and_b32_e32 v143, 0xffff0000, v143
	v_mul_f32_e32 v141, v49, v141
	v_add_f32_e32 v144, v144, v146
	v_fmac_f32_e32 v142, v14, v140
	v_mul_f32_e32 v146, v20, v143
	v_fmac_f32_e32 v141, v21, v140
	v_mul_f32_e32 v140, v54, v143
	v_fmac_f32_e32 v146, v16, v145
	v_fmac_f32_e32 v140, v50, v145
	v_add_f32_e32 v144, 0, v144
	v_add_f32_e32 v139, 0, v139
	v_add_f32_e32 v142, v142, v146
	v_add_f32_e32 v140, v141, v140
	v_add_f32_e32 v144, v144, v142
	v_add_f32_e32 v139, v139, v140
	ds_read2st64_b64 v[140:143], v106 offset0:90 offset1:91
	s_waitcnt lgkmcnt(0)
	v_lshlrev_b32_e32 v145, 16, v140
	v_and_b32_e32 v140, 0xffff0000, v140
	v_lshlrev_b32_e32 v147, 16, v141
	v_and_b32_e32 v141, 0xffff0000, v141
	v_mul_f32_e32 v146, v46, v140
	v_mul_f32_e32 v148, v51, v141
	v_mul_f32_e32 v140, v55, v140
	v_mul_f32_e32 v141, v56, v141
	v_fmac_f32_e32 v140, v47, v145
	v_fmac_f32_e32 v141, v52, v147
	v_fmac_f32_e32 v146, v18, v145
	v_fmac_f32_e32 v148, v19, v147
	v_add_f32_e32 v140, v140, v141
	v_and_b32_e32 v141, 0xffff0000, v142
	v_add_f32_e32 v146, v146, v148
	v_add_f32_e32 v139, v139, v140
	v_lshlrev_b32_e32 v140, 16, v142
	v_mul_f32_e32 v142, v57, v141
	v_lshlrev_b32_e32 v145, 16, v143
	v_and_b32_e32 v143, 0xffff0000, v143
	v_mul_f32_e32 v141, v63, v141
	v_add_f32_e32 v144, v144, v146
	v_fmac_f32_e32 v142, v48, v140
	v_mul_f32_e32 v146, v59, v143
	v_fmac_f32_e32 v141, v58, v140
	v_mul_f32_e32 v140, v64, v143
	v_fmac_f32_e32 v146, v53, v145
	v_fmac_f32_e32 v140, v62, v145
	v_add_f32_e32 v142, v142, v146
	v_add_f32_e32 v140, v141, v140
	v_add_f32_e32 v144, v144, v142
	v_add_f32_e32 v139, v139, v140
	ds_read2st64_b64 v[140:143], v106 offset0:92 offset1:93
	s_waitcnt lgkmcnt(0)
	v_lshlrev_b32_e32 v145, 16, v140
	v_and_b32_e32 v140, 0xffff0000, v140
	v_lshlrev_b32_e32 v147, 16, v141
	v_and_b32_e32 v141, 0xffff0000, v141
	v_mul_f32_e32 v146, v68, v140
	v_mul_f32_e32 v148, v69, v141
	v_mul_f32_e32 v140, v71, v140
	v_mul_f32_e32 v141, v74, v141
	v_fmac_f32_e32 v140, v70, v145
	v_fmac_f32_e32 v141, v72, v147
	v_fmac_f32_e32 v146, v66, v145
	v_fmac_f32_e32 v148, v67, v147
	v_add_f32_e32 v140, v140, v141
	v_and_b32_e32 v141, 0xffff0000, v142
	v_add_f32_e32 v146, v146, v148
	v_add_f32_e32 v139, v139, v140
	v_lshlrev_b32_e32 v140, 16, v142
	v_mul_f32_e32 v142, v76, v141
	v_lshlrev_b32_e32 v145, 16, v143
	v_and_b32_e32 v143, 0xffff0000, v143
	v_mul_f32_e32 v141, v86, v141
	v_add_f32_e32 v144, v144, v146
	v_fmac_f32_e32 v142, v73, v140
	v_mul_f32_e32 v146, v81, v143
	v_fmac_f32_e32 v141, v82, v140
	v_mul_f32_e32 v140, v91, v143
	v_fmac_f32_e32 v146, v75, v145
	v_fmac_f32_e32 v140, v87, v145
	v_add_f32_e32 v142, v142, v146
	v_add_f32_e32 v140, v141, v140
	v_add_f32_e32 v144, v144, v142
	v_add_f32_e32 v139, v139, v140
	ds_read2st64_b64 v[140:143], v106 offset0:94 offset1:95
	s_waitcnt lgkmcnt(0)
	v_lshlrev_b32_e32 v145, 16, v140
	v_and_b32_e32 v140, 0xffff0000, v140
	v_lshlrev_b32_e32 v147, 16, v141
	v_and_b32_e32 v141, 0xffff0000, v141
	v_mul_f32_e32 v146, v83, v140
	v_mul_f32_e32 v148, v88, v141
	v_mul_f32_e32 v140, v93, v140
	v_mul_f32_e32 v141, v94, v141
	v_fmac_f32_e32 v146, v77, v145
	v_fmac_f32_e32 v148, v80, v147
	v_fmac_f32_e32 v140, v84, v145
	v_fmac_f32_e32 v141, v89, v147
	v_add_f32_e32 v146, v146, v148
	v_add_f32_e32 v140, v140, v141
	v_lshlrev_b32_e32 v141, 16, v142
	v_and_b32_e32 v142, 0xffff0000, v142
	v_lshlrev_b32_e32 v145, 16, v143
	v_and_b32_e32 v143, 0xffff0000, v143
	v_add_f32_e32 v144, v144, v146
	v_add_f32_e32 v139, v139, v140
	v_mul_f32_e32 v140, v95, v142
	v_mul_f32_e32 v146, v97, v143
	v_mul_f32_e32 v142, v121, v142
	v_fmac_f32_e32 v140, v85, v141
	v_fmac_f32_e32 v146, v90, v145
	v_fmac_f32_e32 v142, v96, v141
	v_mul_f32_e32 v141, v122, v143
	v_add_f32_e32 v140, v140, v146
	v_fmac_f32_e32 v141, v120, v145
	v_add_f32_e32 v140, v144, v140
	v_add_f32_e32 v141, v142, v141
	ds_read2st64_b64 v[142:145], v106 offset0:96 offset1:97
	v_add_f32_e32 v139, v139, v141
	s_waitcnt lgkmcnt(0)
	v_lshlrev_b32_e32 v141, 16, v142
	v_and_b32_e32 v142, 0xffff0000, v142
	v_mul_f32_e32 v146, v9, v142
	v_lshlrev_b32_e32 v147, 16, v143
	v_and_b32_e32 v143, 0xffff0000, v143
	v_mul_f32_e32 v142, v12, v142
	v_fmac_f32_e32 v146, v7, v141
	v_fmac_f32_e32 v142, v11, v141
	v_mul_f32_e32 v141, v15, v143
	v_mul_f32_e32 v148, v10, v143
	v_fmac_f32_e32 v141, v13, v147
	v_and_b32_e32 v143, 0xffff0000, v144
	v_fmac_f32_e32 v148, v8, v147
	v_add_f32_e32 v141, v142, v141
	v_lshlrev_b32_e32 v142, 16, v144
	v_mul_f32_e32 v144, v17, v143
	v_lshlrev_b32_e32 v147, 16, v145
	v_and_b32_e32 v145, 0xffff0000, v145
	v_mul_f32_e32 v143, v49, v143
	v_add_f32_e32 v146, v146, v148
	v_fmac_f32_e32 v144, v14, v142
	v_mul_f32_e32 v148, v20, v145
	v_fmac_f32_e32 v143, v21, v142
	v_mul_f32_e32 v142, v54, v145
	v_fmac_f32_e32 v148, v16, v147
	v_fmac_f32_e32 v142, v50, v147
	v_add_f32_e32 v146, 0, v146
	v_add_f32_e32 v141, 0, v141
	v_add_f32_e32 v144, v144, v148
	v_add_f32_e32 v142, v143, v142
	v_add_f32_e32 v146, v146, v144
	v_add_f32_e32 v141, v141, v142
	ds_read2st64_b64 v[142:145], v106 offset0:98 offset1:99
	s_waitcnt lgkmcnt(0)
	v_lshlrev_b32_e32 v147, 16, v142
	v_and_b32_e32 v142, 0xffff0000, v142
	v_lshlrev_b32_e32 v149, 16, v143
	v_and_b32_e32 v143, 0xffff0000, v143
	v_mul_f32_e32 v148, v46, v142
	v_mul_f32_e32 v150, v51, v143
	v_mul_f32_e32 v142, v55, v142
	v_mul_f32_e32 v143, v56, v143
	v_fmac_f32_e32 v142, v47, v147
	v_fmac_f32_e32 v143, v52, v149
	v_fmac_f32_e32 v148, v18, v147
	v_fmac_f32_e32 v150, v19, v149
	v_add_f32_e32 v142, v142, v143
	v_and_b32_e32 v143, 0xffff0000, v144
	v_add_f32_e32 v148, v148, v150
	v_add_f32_e32 v141, v141, v142
	v_lshlrev_b32_e32 v142, 16, v144
	v_mul_f32_e32 v144, v57, v143
	v_lshlrev_b32_e32 v147, 16, v145
	v_and_b32_e32 v145, 0xffff0000, v145
	v_mul_f32_e32 v143, v63, v143
	v_add_f32_e32 v146, v146, v148
	v_fmac_f32_e32 v144, v48, v142
	v_mul_f32_e32 v148, v59, v145
	v_fmac_f32_e32 v143, v58, v142
	v_mul_f32_e32 v142, v64, v145
	v_fmac_f32_e32 v148, v53, v147
	v_fmac_f32_e32 v142, v62, v147
	v_add_f32_e32 v144, v144, v148
	v_add_f32_e32 v142, v143, v142
	v_add_f32_e32 v146, v146, v144
	v_add_f32_e32 v141, v141, v142
	ds_read2st64_b64 v[142:145], v106 offset0:100 offset1:101
	s_waitcnt lgkmcnt(0)
	v_lshlrev_b32_e32 v147, 16, v142
	v_and_b32_e32 v142, 0xffff0000, v142
	v_lshlrev_b32_e32 v149, 16, v143
	v_and_b32_e32 v143, 0xffff0000, v143
	v_mul_f32_e32 v148, v68, v142
	v_mul_f32_e32 v150, v69, v143
	v_mul_f32_e32 v142, v71, v142
	v_mul_f32_e32 v143, v74, v143
	v_fmac_f32_e32 v142, v70, v147
	v_fmac_f32_e32 v143, v72, v149
	v_fmac_f32_e32 v148, v66, v147
	v_fmac_f32_e32 v150, v67, v149
	v_add_f32_e32 v142, v142, v143
	v_and_b32_e32 v143, 0xffff0000, v144
	v_add_f32_e32 v148, v148, v150
	v_add_f32_e32 v141, v141, v142
	v_lshlrev_b32_e32 v142, 16, v144
	v_mul_f32_e32 v144, v76, v143
	v_lshlrev_b32_e32 v147, 16, v145
	v_and_b32_e32 v145, 0xffff0000, v145
	v_mul_f32_e32 v143, v86, v143
	v_add_f32_e32 v146, v146, v148
	v_fmac_f32_e32 v144, v73, v142
	v_mul_f32_e32 v148, v81, v145
	v_fmac_f32_e32 v143, v82, v142
	v_mul_f32_e32 v142, v91, v145
	v_fmac_f32_e32 v148, v75, v147
	v_fmac_f32_e32 v142, v87, v147
	v_add_f32_e32 v144, v144, v148
	v_add_f32_e32 v142, v143, v142
	v_add_f32_e32 v146, v146, v144
	v_add_f32_e32 v141, v141, v142
	ds_read2st64_b64 v[142:145], v106 offset0:102 offset1:103
	s_waitcnt lgkmcnt(0)
	v_lshlrev_b32_e32 v147, 16, v142
	v_and_b32_e32 v142, 0xffff0000, v142
	v_lshlrev_b32_e32 v149, 16, v143
	v_and_b32_e32 v143, 0xffff0000, v143
	v_mul_f32_e32 v148, v83, v142
	v_mul_f32_e32 v150, v88, v143
	v_mul_f32_e32 v142, v93, v142
	v_mul_f32_e32 v143, v94, v143
	v_fmac_f32_e32 v148, v77, v147
	v_fmac_f32_e32 v150, v80, v149
	v_fmac_f32_e32 v142, v84, v147
	v_fmac_f32_e32 v143, v89, v149
	v_add_f32_e32 v148, v148, v150
	v_add_f32_e32 v142, v142, v143
	v_lshlrev_b32_e32 v143, 16, v144
	v_and_b32_e32 v144, 0xffff0000, v144
	v_lshlrev_b32_e32 v147, 16, v145
	v_and_b32_e32 v145, 0xffff0000, v145
	v_add_f32_e32 v146, v146, v148
	v_add_f32_e32 v141, v141, v142
	v_mul_f32_e32 v142, v95, v144
	v_mul_f32_e32 v148, v97, v145
	v_mul_f32_e32 v144, v121, v144
	v_fmac_f32_e32 v142, v85, v143
	v_fmac_f32_e32 v148, v90, v147
	v_fmac_f32_e32 v144, v96, v143
	v_mul_f32_e32 v143, v122, v145
	v_add_f32_e32 v142, v142, v148
	v_fmac_f32_e32 v143, v120, v147
	v_add_f32_e32 v142, v146, v142
	v_add_f32_e32 v143, v144, v143
	ds_read2st64_b64 v[144:147], v106 offset0:104 offset1:105
	v_add_f32_e32 v141, v141, v143
	s_waitcnt lgkmcnt(0)
	v_lshlrev_b32_e32 v143, 16, v144
	v_and_b32_e32 v144, 0xffff0000, v144
	v_mul_f32_e32 v148, v9, v144
	v_lshlrev_b32_e32 v149, 16, v145
	v_and_b32_e32 v145, 0xffff0000, v145
	v_mul_f32_e32 v144, v12, v144
	v_fmac_f32_e32 v148, v7, v143
	v_fmac_f32_e32 v144, v11, v143
	v_mul_f32_e32 v143, v15, v145
	v_mul_f32_e32 v150, v10, v145
	v_fmac_f32_e32 v143, v13, v149
	v_and_b32_e32 v145, 0xffff0000, v146
	v_fmac_f32_e32 v150, v8, v149
	v_add_f32_e32 v143, v144, v143
	v_lshlrev_b32_e32 v144, 16, v146
	v_mul_f32_e32 v146, v17, v145
	v_lshlrev_b32_e32 v149, 16, v147
	v_and_b32_e32 v147, 0xffff0000, v147
	v_mul_f32_e32 v145, v49, v145
	v_add_f32_e32 v148, v148, v150
	v_fmac_f32_e32 v146, v14, v144
	v_mul_f32_e32 v150, v20, v147
	v_fmac_f32_e32 v145, v21, v144
	v_mul_f32_e32 v144, v54, v147
	v_fmac_f32_e32 v150, v16, v149
	v_fmac_f32_e32 v144, v50, v149
	v_add_f32_e32 v148, 0, v148
	v_add_f32_e32 v143, 0, v143
	v_add_f32_e32 v146, v146, v150
	v_add_f32_e32 v144, v145, v144
	v_add_f32_e32 v148, v148, v146
	v_add_f32_e32 v143, v143, v144
	ds_read2st64_b64 v[144:147], v106 offset0:106 offset1:107
	s_waitcnt lgkmcnt(0)
	v_lshlrev_b32_e32 v149, 16, v144
	v_and_b32_e32 v144, 0xffff0000, v144
	v_lshlrev_b32_e32 v151, 16, v145
	v_and_b32_e32 v145, 0xffff0000, v145
	v_mul_f32_e32 v150, v46, v144
	v_mul_f32_e32 v152, v51, v145
	v_mul_f32_e32 v144, v55, v144
	v_mul_f32_e32 v145, v56, v145
	v_fmac_f32_e32 v144, v47, v149
	v_fmac_f32_e32 v145, v52, v151
	v_fmac_f32_e32 v150, v18, v149
	v_fmac_f32_e32 v152, v19, v151
	v_add_f32_e32 v144, v144, v145
	v_and_b32_e32 v145, 0xffff0000, v146
	v_add_f32_e32 v150, v150, v152
	v_add_f32_e32 v143, v143, v144
	v_lshlrev_b32_e32 v144, 16, v146
	v_mul_f32_e32 v146, v57, v145
	v_lshlrev_b32_e32 v149, 16, v147
	v_and_b32_e32 v147, 0xffff0000, v147
	v_mul_f32_e32 v145, v63, v145
	v_add_f32_e32 v148, v148, v150
	v_fmac_f32_e32 v146, v48, v144
	v_mul_f32_e32 v150, v59, v147
	v_fmac_f32_e32 v145, v58, v144
	v_mul_f32_e32 v144, v64, v147
	v_fmac_f32_e32 v150, v53, v149
	v_fmac_f32_e32 v144, v62, v149
	v_add_f32_e32 v146, v146, v150
	v_add_f32_e32 v144, v145, v144
	v_add_f32_e32 v148, v148, v146
	v_add_f32_e32 v143, v143, v144
	ds_read2st64_b64 v[144:147], v106 offset0:108 offset1:109
	s_waitcnt lgkmcnt(0)
	v_lshlrev_b32_e32 v149, 16, v144
	v_and_b32_e32 v144, 0xffff0000, v144
	v_lshlrev_b32_e32 v151, 16, v145
	v_and_b32_e32 v145, 0xffff0000, v145
	v_mul_f32_e32 v150, v68, v144
	v_mul_f32_e32 v152, v69, v145
	v_mul_f32_e32 v144, v71, v144
	v_mul_f32_e32 v145, v74, v145
	v_fmac_f32_e32 v144, v70, v149
	v_fmac_f32_e32 v145, v72, v151
	v_fmac_f32_e32 v150, v66, v149
	v_fmac_f32_e32 v152, v67, v151
	v_add_f32_e32 v144, v144, v145
	v_and_b32_e32 v145, 0xffff0000, v146
	v_add_f32_e32 v150, v150, v152
	v_add_f32_e32 v143, v143, v144
	v_lshlrev_b32_e32 v144, 16, v146
	v_mul_f32_e32 v146, v76, v145
	v_lshlrev_b32_e32 v149, 16, v147
	v_and_b32_e32 v147, 0xffff0000, v147
	v_mul_f32_e32 v145, v86, v145
	v_add_f32_e32 v148, v148, v150
	v_fmac_f32_e32 v146, v73, v144
	v_mul_f32_e32 v150, v81, v147
	v_fmac_f32_e32 v145, v82, v144
	v_mul_f32_e32 v144, v91, v147
	v_fmac_f32_e32 v150, v75, v149
	v_fmac_f32_e32 v144, v87, v149
	v_add_f32_e32 v146, v146, v150
	v_add_f32_e32 v144, v145, v144
	v_add_f32_e32 v148, v148, v146
	v_add_f32_e32 v143, v143, v144
	ds_read2st64_b64 v[144:147], v106 offset0:110 offset1:111
	s_waitcnt lgkmcnt(0)
	v_lshlrev_b32_e32 v149, 16, v144
	v_and_b32_e32 v144, 0xffff0000, v144
	v_lshlrev_b32_e32 v151, 16, v145
	v_and_b32_e32 v145, 0xffff0000, v145
	v_mul_f32_e32 v150, v83, v144
	v_mul_f32_e32 v152, v88, v145
	v_mul_f32_e32 v144, v93, v144
	v_mul_f32_e32 v145, v94, v145
	v_fmac_f32_e32 v150, v77, v149
	v_fmac_f32_e32 v152, v80, v151
	v_fmac_f32_e32 v144, v84, v149
	v_fmac_f32_e32 v145, v89, v151
	v_add_f32_e32 v150, v150, v152
	v_add_f32_e32 v144, v144, v145
	v_lshlrev_b32_e32 v145, 16, v146
	v_and_b32_e32 v146, 0xffff0000, v146
	v_lshlrev_b32_e32 v149, 16, v147
	v_and_b32_e32 v147, 0xffff0000, v147
	v_add_f32_e32 v148, v148, v150
	v_add_f32_e32 v143, v143, v144
	v_mul_f32_e32 v144, v95, v146
	v_mul_f32_e32 v150, v97, v147
	v_mul_f32_e32 v146, v121, v146
	v_fmac_f32_e32 v144, v85, v145
	v_fmac_f32_e32 v150, v90, v149
	v_fmac_f32_e32 v146, v96, v145
	v_mul_f32_e32 v145, v122, v147
	v_add_f32_e32 v144, v144, v150
	v_fmac_f32_e32 v145, v120, v149
	v_add_f32_e32 v144, v148, v144
	v_add_f32_e32 v145, v146, v145
	ds_read2st64_b64 v[146:149], v106 offset0:112 offset1:113
	v_add_f32_e32 v143, v143, v145
	s_waitcnt lgkmcnt(0)
	v_lshlrev_b32_e32 v145, 16, v146
	v_and_b32_e32 v146, 0xffff0000, v146
	v_mul_f32_e32 v150, v9, v146
	v_lshlrev_b32_e32 v151, 16, v147
	v_and_b32_e32 v147, 0xffff0000, v147
	v_mul_f32_e32 v146, v12, v146
	v_fmac_f32_e32 v150, v7, v145
	v_fmac_f32_e32 v146, v11, v145
	v_mul_f32_e32 v145, v15, v147
	v_mul_f32_e32 v152, v10, v147
	v_fmac_f32_e32 v145, v13, v151
	v_and_b32_e32 v147, 0xffff0000, v148
	v_fmac_f32_e32 v152, v8, v151
	v_add_f32_e32 v145, v146, v145
	v_lshlrev_b32_e32 v146, 16, v148
	v_mul_f32_e32 v148, v17, v147
	v_lshlrev_b32_e32 v151, 16, v149
	v_and_b32_e32 v149, 0xffff0000, v149
	v_mul_f32_e32 v147, v49, v147
	v_add_f32_e32 v150, v150, v152
	v_fmac_f32_e32 v148, v14, v146
	v_mul_f32_e32 v152, v20, v149
	v_fmac_f32_e32 v147, v21, v146
	v_mul_f32_e32 v146, v54, v149
	v_fmac_f32_e32 v152, v16, v151
	v_fmac_f32_e32 v146, v50, v151
	v_add_f32_e32 v150, 0, v150
	v_add_f32_e32 v145, 0, v145
	v_add_f32_e32 v148, v148, v152
	v_add_f32_e32 v146, v147, v146
	v_add_f32_e32 v150, v150, v148
	v_add_f32_e32 v145, v145, v146
	ds_read2st64_b64 v[146:149], v106 offset0:114 offset1:115
	s_waitcnt lgkmcnt(0)
	v_lshlrev_b32_e32 v151, 16, v146
	v_and_b32_e32 v146, 0xffff0000, v146
	v_lshlrev_b32_e32 v153, 16, v147
	v_and_b32_e32 v147, 0xffff0000, v147
	v_mul_f32_e32 v152, v46, v146
	v_mul_f32_e32 v154, v51, v147
	v_mul_f32_e32 v146, v55, v146
	v_mul_f32_e32 v147, v56, v147
	v_fmac_f32_e32 v146, v47, v151
	v_fmac_f32_e32 v147, v52, v153
	v_fmac_f32_e32 v152, v18, v151
	v_fmac_f32_e32 v154, v19, v153
	v_add_f32_e32 v146, v146, v147
	v_and_b32_e32 v147, 0xffff0000, v148
	v_add_f32_e32 v152, v152, v154
	v_add_f32_e32 v145, v145, v146
	v_lshlrev_b32_e32 v146, 16, v148
	v_mul_f32_e32 v148, v57, v147
	v_lshlrev_b32_e32 v151, 16, v149
	v_and_b32_e32 v149, 0xffff0000, v149
	v_mul_f32_e32 v147, v63, v147
	v_add_f32_e32 v150, v150, v152
	v_fmac_f32_e32 v148, v48, v146
	v_mul_f32_e32 v152, v59, v149
	v_fmac_f32_e32 v147, v58, v146
	v_mul_f32_e32 v146, v64, v149
	v_fmac_f32_e32 v152, v53, v151
	v_fmac_f32_e32 v146, v62, v151
	v_add_f32_e32 v148, v148, v152
	v_add_f32_e32 v146, v147, v146
	v_add_f32_e32 v150, v150, v148
	v_add_f32_e32 v145, v145, v146
	ds_read2st64_b64 v[146:149], v106 offset0:116 offset1:117
	s_waitcnt lgkmcnt(0)
	v_lshlrev_b32_e32 v151, 16, v146
	v_and_b32_e32 v146, 0xffff0000, v146
	v_lshlrev_b32_e32 v153, 16, v147
	v_and_b32_e32 v147, 0xffff0000, v147
	v_mul_f32_e32 v152, v68, v146
	v_mul_f32_e32 v154, v69, v147
	v_mul_f32_e32 v146, v71, v146
	v_mul_f32_e32 v147, v74, v147
	v_fmac_f32_e32 v146, v70, v151
	v_fmac_f32_e32 v147, v72, v153
	v_fmac_f32_e32 v152, v66, v151
	v_fmac_f32_e32 v154, v67, v153
	v_add_f32_e32 v146, v146, v147
	v_and_b32_e32 v147, 0xffff0000, v148
	v_add_f32_e32 v152, v152, v154
	v_add_f32_e32 v145, v145, v146
	v_lshlrev_b32_e32 v146, 16, v148
	v_mul_f32_e32 v148, v76, v147
	v_lshlrev_b32_e32 v151, 16, v149
	v_and_b32_e32 v149, 0xffff0000, v149
	v_mul_f32_e32 v147, v86, v147
	v_add_f32_e32 v150, v150, v152
	v_fmac_f32_e32 v148, v73, v146
	v_mul_f32_e32 v152, v81, v149
	v_fmac_f32_e32 v147, v82, v146
	v_mul_f32_e32 v146, v91, v149
	v_fmac_f32_e32 v152, v75, v151
	v_fmac_f32_e32 v146, v87, v151
	v_add_f32_e32 v148, v148, v152
	v_add_f32_e32 v146, v147, v146
	v_add_f32_e32 v150, v150, v148
	v_add_f32_e32 v145, v145, v146
	ds_read2st64_b64 v[146:149], v106 offset0:118 offset1:119
	s_waitcnt lgkmcnt(0)
	v_lshlrev_b32_e32 v151, 16, v146
	v_and_b32_e32 v146, 0xffff0000, v146
	v_lshlrev_b32_e32 v153, 16, v147
	v_and_b32_e32 v147, 0xffff0000, v147
	v_mul_f32_e32 v152, v83, v146
	v_mul_f32_e32 v154, v88, v147
	v_mul_f32_e32 v146, v93, v146
	v_mul_f32_e32 v147, v94, v147
	v_fmac_f32_e32 v152, v77, v151
	v_fmac_f32_e32 v154, v80, v153
	v_fmac_f32_e32 v146, v84, v151
	v_fmac_f32_e32 v147, v89, v153
	v_add_f32_e32 v152, v152, v154
	v_add_f32_e32 v146, v146, v147
	v_lshlrev_b32_e32 v147, 16, v148
	v_and_b32_e32 v148, 0xffff0000, v148
	v_lshlrev_b32_e32 v151, 16, v149
	v_and_b32_e32 v149, 0xffff0000, v149
	v_add_f32_e32 v150, v150, v152
	v_add_f32_e32 v145, v145, v146
	v_mul_f32_e32 v146, v95, v148
	v_mul_f32_e32 v152, v97, v149
	v_mul_f32_e32 v148, v121, v148
	v_fmac_f32_e32 v146, v85, v147
	v_fmac_f32_e32 v152, v90, v151
	v_fmac_f32_e32 v148, v96, v147
	v_mul_f32_e32 v147, v122, v149
	v_add_f32_e32 v146, v146, v152
	v_fmac_f32_e32 v147, v120, v151
	v_add_f32_e32 v146, v150, v146
	v_add_f32_e32 v147, v148, v147
	ds_read2st64_b64 v[148:151], v106 offset0:120 offset1:121
	v_add_f32_e32 v145, v145, v147
	s_waitcnt lgkmcnt(0)
	v_lshlrev_b32_e32 v147, 16, v148
	v_and_b32_e32 v148, 0xffff0000, v148
	v_mul_f32_e32 v9, v9, v148
	v_fmac_f32_e32 v9, v7, v147
	v_lshlrev_b32_e32 v7, 16, v149
	v_and_b32_e32 v149, 0xffff0000, v149
	v_mul_f32_e32 v10, v10, v149
	v_fmac_f32_e32 v10, v8, v7
	v_add_f32_e32 v8, v9, v10
	v_mul_f32_e32 v9, v12, v148
	v_mul_f32_e32 v10, v15, v149
	v_fmac_f32_e32 v9, v11, v147
	v_fmac_f32_e32 v10, v13, v7
	v_add_f32_e32 v7, v9, v10
	v_and_b32_e32 v10, 0xffff0000, v150
	v_lshlrev_b32_e32 v9, 16, v150
	v_mul_f32_e32 v11, v17, v10
	v_and_b32_e32 v13, 0xffff0000, v151
	v_fmac_f32_e32 v11, v14, v9
	v_lshlrev_b32_e32 v12, 16, v151
	v_mul_f32_e32 v14, v20, v13
	v_fmac_f32_e32 v14, v16, v12
	v_add_f32_e32 v8, 0, v8
	v_add_f32_e32 v11, v11, v14
	v_add_f32_e32 v14, v8, v11
	v_mul_f32_e32 v8, v49, v10
	v_fmac_f32_e32 v8, v21, v9
	v_mul_f32_e32 v9, v54, v13
	v_fmac_f32_e32 v9, v50, v12
	v_add_f32_e32 v7, 0, v7
	v_add_f32_e32 v8, v8, v9
	v_add_f32_e32 v7, v7, v8
	ds_read2st64_b64 v[8:11], v106 offset0:122 offset1:123
	v_cndmask_b32_e64 v17, v132, 0, s[6:7]
	ds_bpermute_b32 v17, v103, v17
	v_cndmask_b32_e64 v20, v138, 0, s[6:7]
	ds_bpermute_b32 v20, v103, v20
	s_waitcnt lgkmcnt(2)
	v_lshlrev_b32_e32 v12, 16, v8
	v_and_b32_e32 v8, 0xffff0000, v8
	v_lshlrev_b32_e32 v15, 16, v9
	v_and_b32_e32 v9, 0xffff0000, v9
	v_mul_f32_e32 v13, v46, v8
	v_mul_f32_e32 v16, v51, v9
	v_mul_f32_e32 v8, v55, v8
	v_mul_f32_e32 v9, v56, v9
	v_fmac_f32_e32 v8, v47, v12
	v_fmac_f32_e32 v9, v52, v15
	v_fmac_f32_e32 v13, v18, v12
	v_fmac_f32_e32 v16, v19, v15
	v_add_f32_e32 v8, v8, v9
	v_and_b32_e32 v9, 0xffff0000, v10
	v_add_f32_e32 v13, v13, v16
	v_add_f32_e32 v7, v7, v8
	v_lshlrev_b32_e32 v8, 16, v10
	v_mul_f32_e32 v10, v57, v9
	v_lshlrev_b32_e32 v12, 16, v11
	v_and_b32_e32 v11, 0xffff0000, v11
	v_mul_f32_e32 v9, v63, v9
	v_add_f32_e32 v13, v14, v13
	v_fmac_f32_e32 v10, v48, v8
	v_mul_f32_e32 v14, v59, v11
	v_fmac_f32_e32 v9, v58, v8
	v_mul_f32_e32 v8, v64, v11
	v_fmac_f32_e32 v14, v53, v12
	v_fmac_f32_e32 v8, v62, v12
	v_add_f32_e32 v10, v10, v14
	v_add_f32_e32 v8, v9, v8
	v_add_f32_e32 v13, v13, v10
	v_add_f32_e32 v7, v7, v8
	ds_read2st64_b64 v[8:11], v106 offset0:124 offset1:125
	v_cndmask_b32_e64 v18, v134, 0, s[6:7]
	ds_bpermute_b32 v18, v103, v18
	v_cndmask_b32_e64 v19, v136, 0, s[6:7]
	ds_bpermute_b32 v19, v103, v19
	s_waitcnt lgkmcnt(2)
	v_lshlrev_b32_e32 v12, 16, v8
	v_and_b32_e32 v8, 0xffff0000, v8
	v_lshlrev_b32_e32 v15, 16, v9
	v_and_b32_e32 v9, 0xffff0000, v9
	v_mul_f32_e32 v14, v68, v8
	v_mul_f32_e32 v16, v69, v9
	v_mul_f32_e32 v8, v71, v8
	v_mul_f32_e32 v9, v74, v9
	v_fmac_f32_e32 v8, v70, v12
	v_fmac_f32_e32 v9, v72, v15
	v_fmac_f32_e32 v14, v66, v12
	v_fmac_f32_e32 v16, v67, v15
	v_add_f32_e32 v8, v8, v9
	v_and_b32_e32 v9, 0xffff0000, v10
	v_add_f32_e32 v14, v14, v16
	v_add_f32_e32 v7, v7, v8
	v_lshlrev_b32_e32 v8, 16, v10
	v_mul_f32_e32 v10, v76, v9
	v_lshlrev_b32_e32 v12, 16, v11
	v_and_b32_e32 v11, 0xffff0000, v11
	v_mul_f32_e32 v9, v86, v9
	v_add_f32_e32 v13, v13, v14
	v_fmac_f32_e32 v10, v73, v8
	v_mul_f32_e32 v14, v81, v11
	v_fmac_f32_e32 v9, v82, v8
	v_mul_f32_e32 v8, v91, v11
	v_fmac_f32_e32 v14, v75, v12
	v_fmac_f32_e32 v8, v87, v12
	v_add_f32_e32 v10, v10, v14
	v_add_f32_e32 v8, v9, v8
	v_add_f32_e32 v13, v13, v10
	v_add_f32_e32 v7, v7, v8
	ds_read2st64_b64 v[8:11], v106 offset0:126 offset1:127
	v_cndmask_b32_e64 v21, v140, 0, s[6:7]
	ds_bpermute_b32 v21, v103, v21
	v_cndmask_b32_e64 v46, v143, v61, s[6:7]
	v_cndmask_b32_e64 v47, v145, v79, s[6:7]
	s_waitcnt lgkmcnt(1)
	v_lshlrev_b32_e32 v12, 16, v8
	v_and_b32_e32 v8, 0xffff0000, v8
	v_lshlrev_b32_e32 v15, 16, v9
	v_and_b32_e32 v9, 0xffff0000, v9
	v_mul_f32_e32 v14, v83, v8
	v_mul_f32_e32 v16, v88, v9
	v_mul_f32_e32 v8, v93, v8
	v_mul_f32_e32 v9, v94, v9
	v_fmac_f32_e32 v8, v84, v12
	v_fmac_f32_e32 v9, v89, v15
	v_add_f32_e32 v8, v8, v9
	v_and_b32_e32 v9, 0xffff0000, v10
	v_fmac_f32_e32 v14, v77, v12
	v_add_f32_e32 v7, v7, v8
	v_lshlrev_b32_e32 v8, 16, v10
	v_mul_f32_e32 v10, v95, v9
	v_lshlrev_b32_e32 v12, 16, v11
	v_and_b32_e32 v11, 0xffff0000, v11
	v_mul_f32_e32 v9, v121, v9
	v_fmac_f32_e32 v10, v85, v8
	v_fmac_f32_e32 v9, v96, v8
	v_mul_f32_e32 v8, v122, v11
	v_fmac_f32_e32 v8, v120, v12
	v_add_f32_e32 v8, v9, v8
	v_add_f32_e32 v7, v7, v8
	v_cndmask_b32_e64 v8, v60, v142, s[6:7]
	ds_bpermute_b32 v8, v103, v8
	v_cndmask_b32_e64 v9, v142, v60, s[6:7]
	v_fmac_f32_e32 v16, v80, v15
	v_add_f32_e32 v14, v14, v16
	v_add_f32_e32 v13, v13, v14
	s_waitcnt lgkmcnt(0)
	v_add_f32_e32 v8, v9, v8
	v_cndmask_b32_e64 v9, v78, v144, s[6:7]
	ds_bpermute_b32 v9, v103, v9
	v_mul_f32_e32 v14, v97, v11
	v_cndmask_b32_e64 v11, v144, v78, s[6:7]
	v_fmac_f32_e32 v14, v90, v12
	v_add_f32_e32 v10, v10, v14
	s_waitcnt lgkmcnt(0)
	v_add_f32_e32 v9, v11, v9
	v_cndmask_b32_e64 v11, v92, v146, s[6:7]
	ds_bpermute_b32 v11, v103, v11
	v_add_f32_e32 v10, v13, v10
	v_cndmask_b32_e64 v12, v146, v92, s[6:7]
	v_cndmask_b32_e64 v13, v124, 0, s[6:7]
	ds_bpermute_b32 v13, v103, v13
	s_waitcnt lgkmcnt(1)
	v_add_f32_e32 v11, v12, v11
	v_cndmask_b32_e64 v12, v5, v10, s[6:7]
	v_cndmask_b32_e64 v5, v10, v5, s[6:7]
	ds_bpermute_b32 v10, v103, v12
	v_cndmask_b32_e64 v12, v65, 0, s[6:7]
	ds_bpermute_b32 v12, v103, v12
	v_cndmask_b32_e64 v14, v126, 0, s[6:7]
	ds_bpermute_b32 v14, v103, v14
	s_waitcnt lgkmcnt(2)
	v_add_f32_e32 v5, v5, v10
	v_cndmask_b32_e64 v10, 0, v65, s[6:7]
	s_waitcnt lgkmcnt(1)
	v_add_f32_e32 v10, v10, v12
	v_cndmask_b32_e64 v12, 0, v124, s[6:7]
	v_add_f32_e32 v12, v12, v13
	v_cndmask_b32_e64 v13, 0, v1, s[6:7]
	v_cndmask_b32_e64 v1, v1, 0, s[6:7]
	ds_bpermute_b32 v1, v103, v1
	v_cndmask_b32_e64 v15, v128, 0, s[6:7]
	ds_bpermute_b32 v15, v103, v15
	v_cndmask_b32_e64 v16, v130, 0, s[6:7]
	ds_bpermute_b32 v16, v103, v16
	s_waitcnt lgkmcnt(2)
	v_add_f32_e32 v1, v13, v1
	v_cndmask_b32_e64 v13, 0, v3, s[6:7]
	v_cndmask_b32_e64 v3, v3, 0, s[6:7]
	ds_bpermute_b32 v3, v103, v3
	v_cndmask_b32_e64 v48, v125, 0, s[6:7]
	ds_bpermute_b32 v48, v103, v48
	v_cndmask_b32_e64 v49, v127, 0, s[6:7]
	ds_bpermute_b32 v49, v103, v49
	s_waitcnt lgkmcnt(2)
	v_add_f32_e32 v3, v13, v3
	v_cndmask_b32_e64 v13, 0, v126, s[6:7]
	v_add_f32_e32 v13, v13, v14
	v_cndmask_b32_e64 v14, 0, v128, s[6:7]
	v_add_f32_e32 v14, v14, v15
	v_cndmask_b32_e64 v15, 0, v130, s[6:7]
	v_add_f32_e32 v15, v15, v16
	v_cndmask_b32_e64 v16, 0, v132, s[6:7]
	v_add_f32_e32 v16, v16, v17
	v_cndmask_b32_e64 v17, 0, v134, s[6:7]
	v_add_f32_e32 v17, v17, v18
	v_cndmask_b32_e64 v18, 0, v136, s[6:7]
	v_add_f32_e32 v18, v18, v19
	v_cndmask_b32_e64 v19, 0, v138, s[6:7]
	v_add_f32_e32 v19, v19, v20
	v_cndmask_b32_e64 v20, 0, v140, s[6:7]
	v_add_f32_e32 v20, v20, v21
	v_cndmask_b32_e64 v21, v22, v141, s[6:7]
	ds_bpermute_b32 v21, v103, v21
	v_cndmask_b32_e64 v22, v141, v22, s[6:7]
	v_cndmask_b32_e64 v50, v129, 0, s[6:7]
	ds_bpermute_b32 v50, v103, v50
	v_cndmask_b32_e64 v51, v131, 0, s[6:7]
	s_waitcnt lgkmcnt(1)
	v_add_f32_e32 v21, v22, v21
	v_cndmask_b32_e64 v22, v61, v143, s[6:7]
	ds_bpermute_b32 v22, v103, v22
	ds_bpermute_b32 v51, v103, v51
	v_cndmask_b32_e64 v52, v133, 0, s[6:7]
	ds_bpermute_b32 v52, v103, v52
	v_cndmask_b32_e64 v53, v135, 0, s[6:7]
	s_waitcnt lgkmcnt(2)
	v_add_f32_e32 v22, v46, v22
	v_cndmask_b32_e64 v46, v79, v145, s[6:7]
	ds_bpermute_b32 v46, v103, v46
	ds_bpermute_b32 v53, v103, v53
	v_cndmask_b32_e64 v54, v137, 0, s[6:7]
	ds_bpermute_b32 v54, v103, v54
	v_cndmask_b32_e64 v55, v139, 0, s[6:7]
	s_waitcnt lgkmcnt(2)
	v_add_f32_e32 v46, v47, v46
	v_cndmask_b32_e64 v47, v4, v7, s[6:7]
	v_cndmask_b32_e64 v4, v7, v4, s[6:7]
	ds_bpermute_b32 v7, v103, v47
	v_cndmask_b32_e64 v47, v123, 0, s[6:7]
	ds_bpermute_b32 v47, v103, v47
	ds_bpermute_b32 v55, v103, v55
	s_waitcnt lgkmcnt(2)
	v_add_f32_e32 v4, v4, v7
	v_cndmask_b32_e64 v7, 0, v6, s[6:7]
	v_cndmask_b32_e64 v6, v6, 0, s[6:7]
	ds_bpermute_b32 v6, v103, v6
	s_waitcnt lgkmcnt(0)
	v_add_f32_e32 v6, v7, v6
	v_cndmask_b32_e64 v7, 0, v123, s[6:7]
	v_add_f32_e32 v7, v7, v47
	v_cndmask_b32_e64 v47, 0, v0, s[6:7]
	v_cndmask_b32_e64 v0, v0, 0, s[6:7]
	ds_bpermute_b32 v0, v103, v0
	s_waitcnt lgkmcnt(0)
	v_add_f32_e32 v0, v47, v0
	v_cndmask_b32_e64 v47, 0, v2, s[6:7]
	v_cndmask_b32_e64 v2, v2, 0, s[6:7]
	ds_bpermute_b32 v2, v103, v2
	s_waitcnt lgkmcnt(0)
	v_add_f32_e32 v2, v47, v2
	v_cndmask_b32_e64 v47, 0, v125, s[6:7]
	v_add_f32_e32 v47, v47, v48
	v_cndmask_b32_e64 v48, 0, v127, s[6:7]
	v_add_f32_e32 v48, v48, v49
	v_cndmask_b32_e64 v49, 0, v129, s[6:7]
	v_add_f32_e32 v49, v49, v50
	v_cndmask_b32_e64 v50, 0, v131, s[6:7]
	v_add_f32_e32 v50, v50, v51
	v_cndmask_b32_e64 v51, 0, v133, s[6:7]
	v_add_f32_e32 v51, v51, v52
	v_cndmask_b32_e64 v52, 0, v135, s[6:7]
	v_add_f32_e32 v52, v52, v53
	v_cndmask_b32_e64 v53, 0, v137, s[6:7]
	v_add_f32_e32 v53, v53, v54
	v_cndmask_b32_e64 v54, 0, v139, s[6:7]
	v_add_f32_e32 v54, v54, v55
	v_cndmask_b32_e64 v55, v8, v13, s[8:9]
	v_cndmask_b32_e64 v8, v13, v8, s[8:9]
	ds_bpermute_b32 v13, v102, v55
	s_waitcnt lgkmcnt(0)
	v_add_f32_e32 v8, v8, v13
	v_cndmask_b32_e64 v13, v9, v14, s[8:9]
	ds_bpermute_b32 v13, v102, v13
	v_cndmask_b32_e64 v9, v14, v9, s[8:9]
	v_cndmask_b32_e64 v14, v47, v21, s[8:9]
	s_waitcnt lgkmcnt(0)
	v_add_f32_e32 v9, v9, v13
	v_cndmask_b32_e64 v13, v11, v15, s[8:9]
	ds_bpermute_b32 v13, v102, v13
	v_cndmask_b32_e64 v11, v15, v11, s[8:9]
	v_cndmask_b32_e64 v15, v48, v22, s[8:9]
	s_waitcnt lgkmcnt(0)
	v_add_f32_e32 v11, v11, v13
	v_cndmask_b32_e64 v13, v5, v16, s[8:9]
	ds_bpermute_b32 v13, v102, v13
	v_cndmask_b32_e64 v5, v16, v5, s[8:9]
	v_cndmask_b32_e64 v16, v49, v46, s[8:9]
	s_waitcnt lgkmcnt(0)
	v_add_f32_e32 v5, v5, v13
	v_cndmask_b32_e64 v13, v10, v17, s[8:9]
	ds_bpermute_b32 v13, v102, v13
	v_cndmask_b32_e64 v10, v17, v10, s[8:9]
	s_waitcnt lgkmcnt(0)
	v_add_f32_e32 v10, v10, v13
	v_cndmask_b32_e64 v13, v12, v18, s[8:9]
	ds_bpermute_b32 v13, v102, v13
	v_cndmask_b32_e64 v12, v18, v12, s[8:9]
	s_waitcnt lgkmcnt(0)
	v_add_f32_e32 v12, v12, v13
	v_cndmask_b32_e64 v13, v1, v19, s[8:9]
	ds_bpermute_b32 v13, v102, v13
	v_cndmask_b32_e64 v1, v19, v1, s[8:9]
	s_waitcnt lgkmcnt(0)
	v_add_f32_e32 v1, v1, v13
	v_cndmask_b32_e64 v13, v3, v20, s[8:9]
	ds_bpermute_b32 v13, v102, v13
	v_cndmask_b32_e64 v3, v20, v3, s[8:9]
	s_waitcnt lgkmcnt(0)
	v_add_f32_e32 v3, v3, v13
	v_cndmask_b32_e64 v13, v21, v47, s[8:9]
	ds_bpermute_b32 v13, v102, v13
	s_waitcnt lgkmcnt(0)
	v_add_f32_e32 v13, v14, v13
	v_cndmask_b32_e64 v14, v22, v48, s[8:9]
	ds_bpermute_b32 v14, v102, v14
	s_waitcnt lgkmcnt(0)
	v_add_f32_e32 v14, v15, v14
	v_cndmask_b32_e64 v15, v46, v49, s[8:9]
	ds_bpermute_b32 v15, v102, v15
	s_waitcnt lgkmcnt(0)
	v_add_f32_e32 v15, v16, v15
	v_cndmask_b32_e64 v16, v4, v50, s[8:9]
	ds_bpermute_b32 v16, v102, v16
	v_cndmask_b32_e64 v4, v50, v4, s[8:9]
	s_waitcnt lgkmcnt(0)
	v_add_f32_e32 v4, v4, v16
	v_cndmask_b32_e64 v16, v6, v51, s[8:9]
	ds_bpermute_b32 v16, v102, v16
	v_cndmask_b32_e64 v6, v51, v6, s[8:9]
	s_waitcnt lgkmcnt(0)
	v_add_f32_e32 v6, v6, v16
	v_cndmask_b32_e64 v16, v7, v52, s[8:9]
	ds_bpermute_b32 v16, v102, v16
	v_cndmask_b32_e64 v7, v52, v7, s[8:9]
	s_waitcnt lgkmcnt(0)
	v_add_f32_e32 v7, v7, v16
	v_cndmask_b32_e64 v16, v0, v53, s[8:9]
	ds_bpermute_b32 v16, v102, v16
	v_cndmask_b32_e64 v0, v53, v0, s[8:9]
	s_waitcnt lgkmcnt(0)
	v_add_f32_e32 v0, v0, v16
	v_cndmask_b32_e64 v16, v2, v54, s[8:9]
	ds_bpermute_b32 v16, v102, v16
	v_cndmask_b32_e64 v2, v54, v2, s[8:9]
	s_waitcnt lgkmcnt(0)
	v_add_f32_e32 v2, v2, v16
	v_cndmask_b32_e64 v16, v8, v10, s[10:11]
	v_cndmask_b32_e64 v8, v10, v8, s[10:11]
	ds_bpermute_b32 v10, v101, v16
	s_waitcnt lgkmcnt(0)
	v_add_f32_e32 v8, v8, v10
	v_cndmask_b32_e64 v10, v9, v12, s[10:11]
	ds_bpermute_b32 v10, v101, v10
	v_cndmask_b32_e64 v9, v12, v9, s[10:11]
	s_waitcnt lgkmcnt(0)
	v_add_f32_e32 v9, v9, v10
	v_cndmask_b32_e64 v10, v11, v1, s[10:11]
	ds_bpermute_b32 v10, v101, v10
	v_cndmask_b32_e64 v1, v1, v11, s[10:11]
	s_waitcnt lgkmcnt(0)
	v_add_f32_e32 v1, v1, v10
	v_cndmask_b32_e64 v10, v5, v3, s[10:11]
	v_cndmask_b32_e64 v3, v3, v5, s[10:11]
	ds_bpermute_b32 v5, v101, v10
	s_waitcnt lgkmcnt(0)
	v_add_f32_e32 v3, v3, v5
	v_cndmask_b32_e64 v5, v13, v6, s[10:11]
	ds_bpermute_b32 v5, v101, v5
	v_cndmask_b32_e64 v6, v6, v13, s[10:11]
	s_waitcnt lgkmcnt(0)
	v_add_f32_e32 v5, v6, v5
	v_cndmask_b32_e64 v6, v14, v7, s[10:11]
	ds_bpermute_b32 v6, v101, v6
	v_cndmask_b32_e64 v7, v7, v14, s[10:11]
	s_waitcnt lgkmcnt(0)
	v_add_f32_e32 v6, v7, v6
	v_cndmask_b32_e64 v7, v15, v0, s[10:11]
	ds_bpermute_b32 v7, v101, v7
	v_cndmask_b32_e64 v0, v0, v15, s[10:11]
	s_waitcnt lgkmcnt(0)
	v_add_f32_e32 v0, v0, v7
	v_cndmask_b32_e64 v7, v4, v2, s[10:11]
	v_cndmask_b32_e64 v2, v2, v4, s[10:11]
	ds_bpermute_b32 v4, v101, v7
	s_waitcnt lgkmcnt(0)
	v_add_f32_e32 v2, v2, v4
	v_cndmask_b32_e64 v4, v8, v1, s[12:13]
	ds_bpermute_b32 v4, v100, v4
	v_cndmask_b32_e64 v1, v1, v8, s[12:13]
	s_waitcnt lgkmcnt(0)
	v_add_f32_e32 v4, v1, v4
	v_cndmask_b32_e64 v1, v9, v3, s[12:13]
	ds_bpermute_b32 v1, v100, v1
	v_cndmask_b32_e64 v3, v3, v9, s[12:13]
	s_waitcnt lgkmcnt(0)
	v_add_f32_e32 v3, v3, v1
	v_cndmask_b32_e64 v1, v5, v0, s[12:13]
	ds_bpermute_b32 v1, v100, v1
	v_cndmask_b32_e64 v0, v0, v5, s[12:13]
	s_waitcnt lgkmcnt(0)
	v_add_f32_e32 v0, v0, v1
	v_cndmask_b32_e64 v1, v6, v2, s[12:13]
	ds_bpermute_b32 v1, v100, v1
	v_cndmask_b32_e64 v2, v2, v6, s[12:13]
	s_waitcnt lgkmcnt(0)
	v_add_f32_e32 v1, v2, v1
	v_cndmask_b32_e64 v2, v4, v3, s[14:15]
	ds_bpermute_b32 v2, v99, v2
	v_cndmask_b32_e64 v3, v3, v4, s[14:15]
	s_waitcnt lgkmcnt(0)
	v_add_f32_e32 v3, v3, v2
	v_cndmask_b32_e64 v2, v0, v1, s[14:15]
	ds_bpermute_b32 v2, v99, v2
	ds_bpermute_b32 v4, v25, v3
	s_and_saveexec_b64 s[20:21], s[16:17]
	s_cbranch_execz .LBB0_2212
	s_waitcnt lgkmcnt(0)
	v_add_f32_e32 v3, v3, v4
	ds_write_b32 v107, v3

.LBB0_2257:
	s_or_b64 exec, exec, s[26:27]
	v_cndmask_b32_e64 v2, v62, v47, s[20:21]
	v_sub_f32_e32 v3, v18, v2
	v_mul_f32_e32 v3, 0x3fb8aa3b, v3
	v_sub_f32_e32 v4, v19, v2
	v_exp_f32_e32 v3, v3
	v_mul_f32_e32 v4, 0x3fb8aa3b, v4
	v_sub_f32_e32 v5, v49, v2
	v_exp_f32_e32 v4, v4
	v_mul_f32_e32 v5, 0x3fb8aa3b, v5
	v_sub_f32_e32 v2, v47, v2
	v_exp_f32_e32 v5, v5
	v_mul_f32_e32 v2, 0x3fb8aa3b, v2
	v_exp_f32_e32 v2, v2
	v_add_f32_e32 v3, 0, v3
	v_add_f32_e32 v3, v4, v3
	v_add_f32_e32 v3, v5, v3
	v_add_f32_e32 v2, v2, v3
	v_rcp_f32_e32 v4, v2
	v_cndmask_b32_e64 v1, v1, v52, s[22:23]
	v_cndmask_b32_e32 v0, v52, v0, vcc
	v_sub_f32_e32 v0, v1, v0
	v_mul_f32_e32 v0, 0x3fb8aa3b, v0
	v_exp_f32_e32 v1, v0
	v_mul_f32_e32 v0, 1.0, v4
	v_add_f32_e32 v2, 1.0, v1
	v_rcp_f32_e32 v4, v2
	s_ashr_i32 s41, s40, 31
	s_lshl_b64 s[20:21], s[40:41], 2
	s_add_u32 s20, s57, s20
	v_rcp_f32_e32 v7, v2
	v_mul_f32_e32 v3, v1, v4
	s_addc_u32 s21, s58, s21
	v_mul_f32_e32 v1, 1.0, v7
	v_mov_b32_e32 v2, v1
	v_pk_mul_f32 v[0:1], v[0:1], v[2:3] op_sel_hi:[0,1]
	global_store_dwordx2 v23, v[0:1], s[20:21]
	global_load_dwordx3 v[20:22], v23, s[38:39] offset:116
	global_load_dwordx4 v[4:7], v23, s[38:39] offset:68
	s_nop 0
	global_load_dwordx4 v[0:3], v23, s[38:39] offset:84
	global_load_dwordx4 v[8:11], v23, s[38:39] offset:100
	global_load_dwordx4 v[12:15], v23, s[36:37] offset:16
	s_waitcnt lgkmcnt(0)
	v_readfirstlane_b32 s20, v48
	v_add_u32_e32 v18, s28, v16
	v_mov_b32_e32 v16, s48
	v_mov_b32_e32 v47, s60
	v_add_u32_e32 v19, s20, v46
	ds_write_b128 v47, v[16:19]
	s_waitcnt vmcnt(3)
	v_mov_b32_e32 v48, v7
	s_waitcnt vmcnt(2)
	v_mov_b32_e32 v16, v3
	s_waitcnt vmcnt(1)
	v_mov_b32_e32 v46, v11

.LBB0_2301:
	v_cndmask_b32_e32 v2, v58, v7, vcc
	v_cmp_gt_f32_e32 vcc, v16, v47
	v_sub_f32_e32 v4, v12, v2
	v_sub_f32_e32 v5, v13, v2
	v_sub_f32_e32 v6, v11, v2
	v_sub_f32_e32 v2, v7, v2
	v_cndmask_b32_e32 v7, v47, v16, vcc
	v_cmp_gt_f32_e64 s[20:21], v0, v7
	v_cndmask_b32_e64 v8, 0, 1, vcc
	v_mul_f32_e32 v4, 0x3fb8aa3b, v4
	v_cndmask_b32_e64 v7, v7, v0, s[20:21]
	v_cndmask_b32_e64 v8, v8, 2, s[20:21]
	v_cmp_ngt_f32_e32 vcc, v1, v7
	v_cmp_nlt_f32_e64 s[24:25], s62, v47
	v_exp_f32_e32 v4, v4
	v_cndmask_b32_e32 v8, 3, v8, vcc
	v_cmp_eq_u32_e64 s[22:23], 0, v8
	v_mul_f32_e32 v5, 0x3fb8aa3b, v5
	s_or_b64 s[22:23], s[22:23], s[24:25]
	v_exp_f32_e32 v5, v5
	v_mul_f32_e32 v6, 0x3fb8aa3b, v6
	v_cndmask_b32_e64 v9, v47, v119, s[22:23]
	v_exp_f32_e32 v6, v6
	v_mul_f32_e32 v2, 0x3fb8aa3b, v2
	s_and_b64 s[26:27], s[20:21], vcc
	v_cmp_ne_u32_e64 s[20:21], 1, v8
	v_cmp_gt_f32_e64 s[24:25], v16, v9
	v_exp_f32_e32 v2, v2
	s_and_b64 s[20:21], s[20:21], s[24:25]
	v_cndmask_b32_e64 v9, v9, v16, s[20:21]
	v_add_f32_e32 v4, 0, v4
	v_cmp_ngt_f32_e64 s[24:25], v0, v9
	v_add_f32_e32 v4, v5, v4
	s_or_b64 s[24:25], s[26:27], s[24:25]
	v_add_f32_e32 v4, v6, v4
	v_cndmask_b32_e64 v0, v0, v9, s[24:25]
	v_cndmask_b32_e64 v9, 0, -1, s[22:23]
	v_add_f32_e32 v4, v2, v4
	v_cndmask_b32_e64 v9, v9, 1, s[20:21]
	v_rcp_f32_e32 v5, v4
	v_cmp_gt_f32_e64 s[26:27], v1, v0
	s_and_b64 s[26:27], vcc, s[26:27]
	v_cndmask_b32_e64 v6, 2, v9, s[24:25]
	v_cndmask_b32_e64 v0, v0, v1, s[26:27]
	v_cndmask_b32_e32 v1, v1, v7, vcc
	v_sub_f32_e32 v0, v0, v1
	v_mul_f32_e32 v0, 0x3fb8aa3b, v0
	v_lshlrev_b32_e32 v1, 2, v3
	v_cndmask_b32_e64 v6, v6, 3, s[26:27]
	v_exp_f32_e32 v10, v0
	v_or_b32_e32 v0, v8, v1
	s_add_i32 s20, 0, 0x20000
	v_add_u32_e32 v1, v6, v1
	v_lshl_add_u32 v2, v0, 2, s20
	ds_add_rtn_u32 v2, v2, v118
	v_lshl_add_u32 v3, v1, 2, s20
	ds_add_rtn_u32 v3, v3, v118
	v_mul_f32_e32 v5, 1.0, v5
	v_mov_b32_e32 v4, v5
	v_add_f32_e32 v5, 1.0, v10
	v_mov_b32_e32 v6, s60
	s_waitcnt lgkmcnt(0)
	ds_write_b128 v6, v[0:3] offset:16
	v_rcp_f32_e32 v1, v5
	s_add_i32 s20, s40, 2
	s_ashr_i32 s21, s20, 31
	s_lshl_b64 s[20:21], s[20:21], 2
	v_rcp_f32_e32 v6, v5
	v_mul_f32_e32 v0, v10, v1
	v_mov_b32_e32 v1, v0
	s_add_u32 s20, s57, s20
	v_mul_f32_e32 v0, 1.0, v6
	s_addc_u32 s21, s58, s21
	v_pk_mul_f32 v[0:1], v[4:5], v[0:1] op_sel_hi:[0,1]
	global_store_dwordx2 v23, v[0:1], s[20:21]
	s_branch .LBB0_2209
